# speedup vs baseline: 1.0066x; 1.0066x over previous
.LBB3_5:
	s_waitcnt lgkmcnt(0)
	v_cvt_f16_f32_e32 v180, s7
	v_cvt_f16_f32_e32 v182, s6
	v_cvt_f16_f32_e32 v181, s28
	s_waitcnt vmcnt(12)
	v_pk_mul_f16 v183, v182, v184 op_sel_hi:[0,1]
	v_pk_mul_f16 v190, v182, v187 op_sel_hi:[0,1]
	v_pk_mul_f16 v194, v180, v187 op_sel_hi:[0,1]
	v_pk_mul_f16 v198, v181, v187 op_sel_hi:[0,1]
	v_pk_mul_f16 v188, v182, v185 op_sel_hi:[0,1]
	v_pk_mul_f16 v189, v182, v186 op_sel_hi:[0,1]
	v_pk_mul_f16 v191, v180, v184 op_sel_hi:[0,1]
	v_pk_mul_f16 v192, v180, v185 op_sel_hi:[0,1]
	v_pk_mul_f16 v193, v180, v186 op_sel_hi:[0,1]
	v_pk_mul_f16 v195, v181, v184 op_sel_hi:[0,1]
	v_pk_mul_f16 v196, v181, v185 op_sel_hi:[0,1]
	v_pk_mul_f16 v197, v181, v186 op_sel_hi:[0,1]
	v_pk_fma_f16 v113, v113, v187, v190
	v_pk_fma_f16 v110, v110, v184, v183
	v_pk_fma_f16 v129, v129, v187, v190
	v_pk_fma_f16 v126, v126, v184, v183
	v_pk_fma_f16 v141, v141, v187, v190
	v_pk_fma_f16 v138, v138, v184, v183
	v_pk_fma_f16 v183, v89, v187, v194
	v_pk_fma_f16 v199, v109, v187, v194
	v_pk_fma_f16 v194, v125, v187, v194
	v_pk_fma_f16 v203, v53, v187, v198
	v_pk_fma_f16 v207, v69, v187, v198
	v_pk_fma_f16 v187, v97, v187, v198
	v_pk_maximum3_f16 v198, v113, v129, v141
	v_pk_fma_f16 v112, v112, v186, v189
	v_pk_fma_f16 v111, v111, v185, v188
	v_pk_fma_f16 v128, v128, v186, v189
	v_pk_fma_f16 v127, v127, v185, v188
	v_pk_fma_f16 v140, v140, v186, v189
	v_pk_fma_f16 v139, v139, v185, v188
	v_pk_fma_f16 v188, v88, v186, v193
	v_pk_fma_f16 v189, v87, v185, v192
	v_pk_fma_f16 v190, v86, v184, v191
	v_pk_fma_f16 v200, v108, v186, v193
	v_pk_fma_f16 v201, v107, v185, v192
	v_pk_fma_f16 v202, v106, v184, v191
	v_pk_fma_f16 v193, v124, v186, v193
	v_pk_fma_f16 v192, v123, v185, v192
	v_pk_fma_f16 v191, v122, v184, v191
	v_pk_fma_f16 v204, v52, v186, v197
	v_pk_fma_f16 v205, v51, v185, v196
	v_pk_fma_f16 v206, v50, v184, v195
	v_pk_fma_f16 v208, v68, v186, v197
	v_pk_fma_f16 v209, v67, v185, v196
	v_pk_fma_f16 v210, v66, v184, v195
	v_pk_fma_f16 v186, v96, v186, v197
	v_pk_fma_f16 v185, v95, v185, v196
	v_pk_fma_f16 v184, v94, v184, v195
	v_pk_maximum3_f16 v195, v110, v126, v138
	v_pk_maximum3_f16 v196, v111, v127, v139
	v_pk_maximum3_f16 v197, v112, v128, v140
	v_pk_maximum3_f16 v214, v183, v199, v194
	v_pk_maximum3_f16 v218, v203, v207, v187
	v_pk_maximum3_f16 v211, v190, v202, v191
	v_pk_maximum3_f16 v212, v189, v201, v192
	v_pk_maximum3_f16 v213, v188, v200, v193
	v_pk_maximum3_f16 v215, v206, v210, v184
	v_pk_maximum3_f16 v216, v205, v209, v185
	v_pk_maximum3_f16 v198, v198, v214, v218
	v_pk_maximum3_f16 v217, v204, v208, v186
	v_pk_maximum3_f16 v195, v195, v211, v215
	v_pk_maximum3_f16 v196, v196, v212, v216
	v_pk_maximum3_f16 v197, v197, v213, v217
	v_pk_add_f16 v113, v113, v198 neg_lo:[0,1] neg_hi:[0,1]
	v_pk_add_f16 v110, v110, v195 neg_lo:[0,1] neg_hi:[0,1]
	v_pk_add_f16 v111, v111, v196 neg_lo:[0,1] neg_hi:[0,1]
	v_pk_add_f16 v112, v112, v197 neg_lo:[0,1] neg_hi:[0,1]
	v_pk_add_f16 v126, v126, v195 neg_lo:[0,1] neg_hi:[0,1]
	v_exp_f16_sdwa v211, v110 dst_sel:WORD_0 dst_unused:UNUSED_PAD src0_sel:WORD_0
	v_exp_f16_sdwa v212, v111 dst_sel:WORD_0 dst_unused:UNUSED_PAD src0_sel:WORD_0
	v_exp_f16_sdwa v213, v112 dst_sel:WORD_0 dst_unused:UNUSED_PAD src0_sel:WORD_0
	v_exp_f16_sdwa v214, v113 dst_sel:WORD_0 dst_unused:UNUSED_PAD src0_sel:WORD_0
	v_exp_f16_sdwa v211, v110 dst_sel:WORD_1 dst_unused:UNUSED_PRESERVE src0_sel:WORD_1
	v_exp_f16_sdwa v212, v111 dst_sel:WORD_1 dst_unused:UNUSED_PRESERVE src0_sel:WORD_1
	v_exp_f16_sdwa v213, v112 dst_sel:WORD_1 dst_unused:UNUSED_PRESERVE src0_sel:WORD_1
	v_exp_f16_sdwa v214, v113 dst_sel:WORD_1 dst_unused:UNUSED_PRESERVE src0_sel:WORD_1
	v_pk_add_f16 v127, v127, v196 neg_lo:[0,1] neg_hi:[0,1]
	v_pk_add_f16 v113, v211, 0
	s_waitcnt vmcnt(3)
	v_pk_fma_f16 v81, v81, v214, 0
	v_pk_add_f16 v110, v214, 0
	v_pk_add_f16 v111, v213, 0
	v_pk_add_f16 v112, v212, 0
	v_pk_fma_f16 v80, v80, v213, 0
	v_pk_fma_f16 v79, v79, v212, 0
	s_mov_b64 exec, s[64:65]
	buffer_load_dwordx4 v[18:21], v249, s[16:19], 0 offen
	buffer_load_dwordx4 v[6:9], v249, s[16:19], 0 offen offset:512
	s_mov_b64 exec, -1
	v_pk_fma_f16 v78, v78, v211, 0
	v_pk_add_f16 v128, v128, v197 neg_lo:[0,1] neg_hi:[0,1]
	v_pk_add_f16 v129, v129, v198 neg_lo:[0,1] neg_hi:[0,1]
	v_exp_f16_sdwa v211, v126 dst_sel:WORD_0 dst_unused:UNUSED_PAD src0_sel:WORD_0
	v_exp_f16_sdwa v212, v127 dst_sel:WORD_0 dst_unused:UNUSED_PAD src0_sel:WORD_0
	v_exp_f16_sdwa v213, v128 dst_sel:WORD_0 dst_unused:UNUSED_PAD src0_sel:WORD_0
	v_exp_f16_sdwa v214, v129 dst_sel:WORD_0 dst_unused:UNUSED_PAD src0_sel:WORD_0
	v_exp_f16_sdwa v211, v126 dst_sel:WORD_1 dst_unused:UNUSED_PRESERVE src0_sel:WORD_1
	v_exp_f16_sdwa v212, v127 dst_sel:WORD_1 dst_unused:UNUSED_PRESERVE src0_sel:WORD_1
	v_exp_f16_sdwa v213, v128 dst_sel:WORD_1 dst_unused:UNUSED_PRESERVE src0_sel:WORD_1
	v_exp_f16_sdwa v214, v129 dst_sel:WORD_1 dst_unused:UNUSED_PRESERVE src0_sel:WORD_1
	v_pk_add_f16 v113, v113, v211
	v_pk_fma_f16 v81, v105, v214, v81
	v_pk_add_f16 v105, v141, v198 neg_lo:[0,1] neg_hi:[0,1]
	v_pk_add_f16 v112, v112, v212
	v_pk_add_f16 v111, v111, v213
	v_pk_add_f16 v110, v110, v214
	buffer_load_dwordx4 v[30:33], v250, s[16:19], 0 offen offset:512
	buffer_load_dwordx4 v[10:13], v250, s[16:19], 0 offen offset:1024
	v_pk_fma_f16 v78, v102, v211, v78
	v_pk_fma_f16 v79, v103, v212, v79
	v_pk_fma_f16 v80, v104, v213, v80
	v_pk_add_f16 v102, v138, v195 neg_lo:[0,1] neg_hi:[0,1]
	v_pk_add_f16 v103, v139, v196 neg_lo:[0,1] neg_hi:[0,1]
	v_pk_add_f16 v104, v140, v197 neg_lo:[0,1] neg_hi:[0,1]
	v_exp_f16_sdwa v126, v102 dst_sel:WORD_0 dst_unused:UNUSED_PAD src0_sel:WORD_0
	v_exp_f16_sdwa v127, v103 dst_sel:WORD_0 dst_unused:UNUSED_PAD src0_sel:WORD_0
	v_exp_f16_sdwa v128, v104 dst_sel:WORD_0 dst_unused:UNUSED_PAD src0_sel:WORD_0
	v_exp_f16_sdwa v129, v105 dst_sel:WORD_0 dst_unused:UNUSED_PAD src0_sel:WORD_0
	v_exp_f16_sdwa v126, v102 dst_sel:WORD_1 dst_unused:UNUSED_PRESERVE src0_sel:WORD_1
	v_exp_f16_sdwa v127, v103 dst_sel:WORD_1 dst_unused:UNUSED_PRESERVE src0_sel:WORD_1
	v_exp_f16_sdwa v128, v104 dst_sel:WORD_1 dst_unused:UNUSED_PRESERVE src0_sel:WORD_1
	v_exp_f16_sdwa v129, v105 dst_sel:WORD_1 dst_unused:UNUSED_PRESERVE src0_sel:WORD_1
	v_pk_add_f16 v105, v113, v126
	v_pk_add_f16 v102, v110, v129
	v_pk_add_f16 v103, v111, v128
	s_mov_b64 exec, s[66:67]
	buffer_load_dwordx4 v[54:57], v250, s[16:19], 0 offen offset:2048
	buffer_load_dwordx4 v[14:17], v250, s[16:19], 0 offen offset:2560
	s_mov_b64 exec, -1
	v_pk_add_f16 v104, v112, v127
	v_pk_fma_f16 v81, v121, v129, v81
	v_pk_fma_f16 v80, v120, v128, v80
	v_pk_fma_f16 v79, v119, v127, v79
	v_pk_fma_f16 v78, v118, v126, v78
	v_pk_add_f16 v110, v190, v195 neg_lo:[0,1] neg_hi:[0,1]
	v_pk_add_f16 v111, v189, v196 neg_lo:[0,1] neg_hi:[0,1]
	v_pk_add_f16 v112, v188, v197 neg_lo:[0,1] neg_hi:[0,1]
	s_mov_b64 exec, s[64:65]
	buffer_load_dwordx4 v[74:77], v251, s[16:19], 0 offen
	buffer_load_dwordx4 v[26:29], v251, s[16:19], 0 offen offset:512
	s_mov_b64 exec, -1
	v_pk_add_f16 v113, v183, v198 neg_lo:[0,1] neg_hi:[0,1]
	v_exp_f16_sdwa v118, v110 dst_sel:WORD_0 dst_unused:UNUSED_PAD src0_sel:WORD_0
	v_exp_f16_sdwa v119, v111 dst_sel:WORD_0 dst_unused:UNUSED_PAD src0_sel:WORD_0
	v_exp_f16_sdwa v120, v112 dst_sel:WORD_0 dst_unused:UNUSED_PAD src0_sel:WORD_0
	v_exp_f16_sdwa v121, v113 dst_sel:WORD_0 dst_unused:UNUSED_PAD src0_sel:WORD_0
	v_exp_f16_sdwa v118, v110 dst_sel:WORD_1 dst_unused:UNUSED_PRESERVE src0_sel:WORD_1
	v_exp_f16_sdwa v119, v111 dst_sel:WORD_1 dst_unused:UNUSED_PRESERVE src0_sel:WORD_1
	v_exp_f16_sdwa v120, v112 dst_sel:WORD_1 dst_unused:UNUSED_PRESERVE src0_sel:WORD_1
	v_exp_f16_sdwa v121, v113 dst_sel:WORD_1 dst_unused:UNUSED_PRESERVE src0_sel:WORD_1
	v_pk_add_f16 v110, v202, v195 neg_lo:[0,1] neg_hi:[0,1]
	v_pk_add_f16 v105, v105, v118
	v_pk_add_f16 v104, v104, v119
	v_pk_add_f16 v103, v103, v120
	v_pk_add_f16 v102, v102, v121
	v_pk_fma_f16 v78, v46, v118, v78
	v_pk_fma_f16 v79, v47, v119, v79
	v_pk_fma_f16 v80, v48, v120, v80
	v_pk_fma_f16 v81, v49, v121, v81
	buffer_load_dwordx4 v[98:101], v252, s[16:19], 0 offen offset:512
	buffer_load_dwordx4 v[38:41], v252, s[16:19], 0 offen offset:1024
	v_pk_add_f16 v111, v201, v196 neg_lo:[0,1] neg_hi:[0,1]
	v_pk_add_f16 v112, v200, v197 neg_lo:[0,1] neg_hi:[0,1]
	v_pk_add_f16 v113, v199, v198 neg_lo:[0,1] neg_hi:[0,1]
	v_exp_f16_sdwa v118, v110 dst_sel:WORD_0 dst_unused:UNUSED_PAD src0_sel:WORD_0
	v_exp_f16_sdwa v119, v111 dst_sel:WORD_0 dst_unused:UNUSED_PAD src0_sel:WORD_0
	v_exp_f16_sdwa v120, v112 dst_sel:WORD_0 dst_unused:UNUSED_PAD src0_sel:WORD_0
	v_exp_f16_sdwa v121, v113 dst_sel:WORD_0 dst_unused:UNUSED_PAD src0_sel:WORD_0
	v_exp_f16_sdwa v118, v110 dst_sel:WORD_1 dst_unused:UNUSED_PRESERVE src0_sel:WORD_1
	v_exp_f16_sdwa v119, v111 dst_sel:WORD_1 dst_unused:UNUSED_PRESERVE src0_sel:WORD_1
	v_exp_f16_sdwa v120, v112 dst_sel:WORD_1 dst_unused:UNUSED_PRESERVE src0_sel:WORD_1
	v_exp_f16_sdwa v121, v113 dst_sel:WORD_1 dst_unused:UNUSED_PRESERVE src0_sel:WORD_1
	v_pk_add_f16 v110, v191, v195 neg_lo:[0,1] neg_hi:[0,1]
	v_pk_add_f16 v105, v105, v118
	v_pk_add_f16 v102, v102, v121
	v_pk_add_f16 v103, v103, v120
	v_pk_add_f16 v104, v104, v119
	v_pk_fma_f16 v81, v65, v121, v81
	s_mov_b64 exec, s[66:67]
	buffer_load_dwordx4 v[114:117], v252, s[16:19], 0 offen offset:2048
	buffer_load_dwordx4 v[58:61], v252, s[16:19], 0 offen offset:2560
	s_mov_b64 exec, -1
	v_pk_fma_f16 v80, v64, v120, v80
	v_pk_fma_f16 v79, v63, v119, v79
	v_pk_fma_f16 v78, v62, v118, v78
	v_pk_add_f16 v111, v192, v196 neg_lo:[0,1] neg_hi:[0,1]
	v_pk_add_f16 v112, v193, v197 neg_lo:[0,1] neg_hi:[0,1]
	v_pk_add_f16 v113, v194, v198 neg_lo:[0,1] neg_hi:[0,1]
	v_exp_f16_sdwa v118, v110 dst_sel:WORD_0 dst_unused:UNUSED_PAD src0_sel:WORD_0
	v_exp_f16_sdwa v119, v111 dst_sel:WORD_0 dst_unused:UNUSED_PAD src0_sel:WORD_0
	v_exp_f16_sdwa v120, v112 dst_sel:WORD_0 dst_unused:UNUSED_PAD src0_sel:WORD_0
	v_exp_f16_sdwa v121, v113 dst_sel:WORD_0 dst_unused:UNUSED_PAD src0_sel:WORD_0
	v_exp_f16_sdwa v118, v110 dst_sel:WORD_1 dst_unused:UNUSED_PRESERVE src0_sel:WORD_1
	v_exp_f16_sdwa v119, v111 dst_sel:WORD_1 dst_unused:UNUSED_PRESERVE src0_sel:WORD_1
	v_exp_f16_sdwa v120, v112 dst_sel:WORD_1 dst_unused:UNUSED_PRESERVE src0_sel:WORD_1
	v_exp_f16_sdwa v121, v113 dst_sel:WORD_1 dst_unused:UNUSED_PRESERVE src0_sel:WORD_1
	v_pk_add_f16 v110, v206, v195 neg_lo:[0,1] neg_hi:[0,1]
	v_pk_add_f16 v105, v105, v118
	v_pk_add_f16 v104, v104, v119
	s_mov_b64 exec, s[76:77]
	buffer_load_dwordx4 v[130:133], v253, s[16:19], 0 offen
	buffer_load_dwordx4 v[70:73], v253, s[16:19], 0 offen offset:512
	s_mov_b64 exec, -1
	v_pk_add_f16 v103, v103, v120
	v_pk_add_f16 v102, v102, v121
	v_pk_fma_f16 v78, v82, v118, v78
	v_pk_fma_f16 v79, v83, v119, v79
	v_pk_fma_f16 v80, v84, v120, v80
	v_pk_fma_f16 v81, v85, v121, v81
	v_pk_add_f16 v111, v205, v196 neg_lo:[0,1] neg_hi:[0,1]
	v_pk_add_f16 v112, v204, v197 neg_lo:[0,1] neg_hi:[0,1]
	s_mov_b64 exec, s[70:71]
	buffer_load_dwordx4 v[134:137], v254, s[16:19], 0 offen offset:512
	buffer_load_dwordx4 v[90:93], v254, s[16:19], 0 offen offset:1024
	s_mov_b64 exec, -1
	v_pk_add_f16 v113, v203, v198 neg_lo:[0,1] neg_hi:[0,1]
	v_exp_f16_sdwa v118, v110 dst_sel:WORD_0 dst_unused:UNUSED_PAD src0_sel:WORD_0
	v_exp_f16_sdwa v119, v111 dst_sel:WORD_0 dst_unused:UNUSED_PAD src0_sel:WORD_0
	v_exp_f16_sdwa v120, v112 dst_sel:WORD_0 dst_unused:UNUSED_PAD src0_sel:WORD_0
	v_exp_f16_sdwa v121, v113 dst_sel:WORD_0 dst_unused:UNUSED_PAD src0_sel:WORD_0
	v_exp_f16_sdwa v118, v110 dst_sel:WORD_1 dst_unused:UNUSED_PRESERVE src0_sel:WORD_1
	v_exp_f16_sdwa v119, v111 dst_sel:WORD_1 dst_unused:UNUSED_PRESERVE src0_sel:WORD_1
	v_exp_f16_sdwa v120, v112 dst_sel:WORD_1 dst_unused:UNUSED_PRESERVE src0_sel:WORD_1
	v_exp_f16_sdwa v121, v113 dst_sel:WORD_1 dst_unused:UNUSED_PRESERVE src0_sel:WORD_1
	v_pk_add_f16 v110, v210, v195 neg_lo:[0,1] neg_hi:[0,1]
	v_pk_add_f16 v105, v105, v118
	v_pk_add_f16 v102, v102, v121
	v_pk_add_f16 v103, v103, v120
	v_pk_add_f16 v104, v104, v119
	v_pk_fma_f16 v81, v25, v121, v81
	v_pk_fma_f16 v80, v24, v120, v80
	v_pk_fma_f16 v79, v23, v119, v79
	s_mov_b64 exec, s[78:79]
	buffer_load_dwordx4 v[142:145], v254, s[16:19], 0 offen offset:2048
	buffer_load_dwordx4 v[2:5], v254, s[16:19], 0 offen offset:2560
	s_mov_b64 exec, -1
	v_pk_fma_f16 v78, v22, v118, v78
	v_pk_add_f16 v111, v209, v196 neg_lo:[0,1] neg_hi:[0,1]
	v_pk_add_f16 v112, v208, v197 neg_lo:[0,1] neg_hi:[0,1]
	v_pk_add_f16 v113, v207, v198 neg_lo:[0,1] neg_hi:[0,1]
	v_exp_f16_sdwa v118, v110 dst_sel:WORD_0 dst_unused:UNUSED_PAD src0_sel:WORD_0
	v_exp_f16_sdwa v119, v111 dst_sel:WORD_0 dst_unused:UNUSED_PAD src0_sel:WORD_0
	v_exp_f16_sdwa v120, v112 dst_sel:WORD_0 dst_unused:UNUSED_PAD src0_sel:WORD_0
	v_exp_f16_sdwa v121, v113 dst_sel:WORD_0 dst_unused:UNUSED_PAD src0_sel:WORD_0
	v_exp_f16_sdwa v118, v110 dst_sel:WORD_1 dst_unused:UNUSED_PRESERVE src0_sel:WORD_1
	v_exp_f16_sdwa v119, v111 dst_sel:WORD_1 dst_unused:UNUSED_PRESERVE src0_sel:WORD_1
	v_exp_f16_sdwa v120, v112 dst_sel:WORD_1 dst_unused:UNUSED_PRESERVE src0_sel:WORD_1
	v_exp_f16_sdwa v121, v113 dst_sel:WORD_1 dst_unused:UNUSED_PRESERVE src0_sel:WORD_1
	v_pk_add_f16 v110, v184, v195 neg_lo:[0,1] neg_hi:[0,1]
	v_pk_add_f16 v105, v105, v118
	v_pk_add_f16 v104, v104, v119
	v_pk_add_f16 v103, v103, v120
	v_pk_add_f16 v102, v102, v121
	v_pk_fma_f16 v78, v34, v118, v78
	v_pk_fma_f16 v79, v35, v119, v79
	v_pk_fma_f16 v80, v36, v120, v80
	v_pk_fma_f16 v81, v37, v121, v81
	v_pk_add_f16 v111, v185, v196 neg_lo:[0,1] neg_hi:[0,1]
	v_pk_add_f16 v112, v186, v197 neg_lo:[0,1] neg_hi:[0,1]
	v_pk_add_f16 v113, v187, v198 neg_lo:[0,1] neg_hi:[0,1]
	v_exp_f16_sdwa v118, v110 dst_sel:WORD_0 dst_unused:UNUSED_PAD src0_sel:WORD_0
	v_exp_f16_sdwa v119, v111 dst_sel:WORD_0 dst_unused:UNUSED_PAD src0_sel:WORD_0
	v_exp_f16_sdwa v120, v112 dst_sel:WORD_0 dst_unused:UNUSED_PAD src0_sel:WORD_0
	v_exp_f16_sdwa v121, v113 dst_sel:WORD_0 dst_unused:UNUSED_PAD src0_sel:WORD_0
	v_exp_f16_sdwa v118, v110 dst_sel:WORD_1 dst_unused:UNUSED_PRESERVE src0_sel:WORD_1
	v_exp_f16_sdwa v119, v111 dst_sel:WORD_1 dst_unused:UNUSED_PRESERVE src0_sel:WORD_1
	v_exp_f16_sdwa v120, v112 dst_sel:WORD_1 dst_unused:UNUSED_PRESERVE src0_sel:WORD_1
	v_exp_f16_sdwa v121, v113 dst_sel:WORD_1 dst_unused:UNUSED_PRESERVE src0_sel:WORD_1
	v_pk_add_f16 v105, v105, v118
	v_pk_add_f16 v104, v104, v119
	v_rcp_f16_e32 v110, v105
	v_rcp_f16_sdwa v105, v105 dst_sel:DWORD dst_unused:UNUSED_PAD src0_sel:WORD_1
	v_pk_add_f16 v103, v103, v120
	v_rcp_f16_e32 v111, v104
	v_rcp_f16_sdwa v104, v104 dst_sel:DWORD dst_unused:UNUSED_PAD src0_sel:WORD_1
	v_pk_add_f16 v102, v102, v121
	v_rcp_f16_e32 v112, v103
	v_rcp_f16_sdwa v103, v103 dst_sel:DWORD dst_unused:UNUSED_PAD src0_sel:WORD_1
	v_rcp_f16_e32 v113, v102
	v_rcp_f16_sdwa v102, v102 dst_sel:DWORD dst_unused:UNUSED_PAD src0_sel:WORD_1
	v_pk_fma_f16 v78, v42, v118, v78
	v_pack_b32_f16 v105, v110, v105
	v_pk_fma_f16 v79, v43, v119, v79
	v_pk_mul_f16 v110, v78, v105
	v_pack_b32_f16 v78, v111, v104
	v_pk_fma_f16 v80, v44, v120, v80
	v_pk_mul_f16 v111, v79, v78
	v_pack_b32_f16 v78, v112, v103
	v_pk_fma_f16 v81, v45, v121, v81
	v_pk_mul_f16 v112, v80, v78
	v_pack_b32_f16 v78, v113, v102
	v_pk_mul_f16 v113, v81, v78
	s_waitcnt vmcnt(12)
	v_pk_mul_f16 v78, v182, v154 op_sel_hi:[0,1]
	v_pk_mul_f16 v81, v182, v157 op_sel_hi:[0,1]
	v_pk_mul_f16 v105, v180, v157 op_sel_hi:[0,1]
	v_pk_mul_f16 v121, v181, v157 op_sel_hi:[0,1]
	v_pk_mul_f16 v79, v182, v155 op_sel_hi:[0,1]
	v_pk_mul_f16 v80, v182, v156 op_sel_hi:[0,1]
	v_pk_mul_f16 v102, v180, v154 op_sel_hi:[0,1]
	v_pk_mul_f16 v103, v180, v155 op_sel_hi:[0,1]
	v_pk_mul_f16 v104, v180, v156 op_sel_hi:[0,1]
	v_pk_mul_f16 v118, v181, v154 op_sel_hi:[0,1]
	v_pk_mul_f16 v119, v181, v155 op_sel_hi:[0,1]
	v_pk_mul_f16 v120, v181, v156 op_sel_hi:[0,1]
	v_pk_fma_f16 v89, v89, v157, v81
	v_pk_fma_f16 v86, v86, v154, v78
	v_pk_fma_f16 v109, v109, v157, v81
	v_pk_fma_f16 v106, v106, v154, v78
	v_pk_fma_f16 v81, v125, v157, v81
	v_pk_fma_f16 v78, v122, v154, v78
	v_pk_fma_f16 v122, v53, v157, v105
	v_pk_fma_f16 v126, v69, v157, v105
	v_pk_fma_f16 v105, v97, v157, v105
	v_pk_fma_f16 v138, v21, v157, v121
	v_pk_fma_f16 v183, v33, v157, v121
	v_pk_fma_f16 v121, v57, v157, v121
	v_pk_maximum3_f16 v157, v89, v109, v81
	v_pk_fma_f16 v88, v88, v156, v80
	v_pk_fma_f16 v87, v87, v155, v79
	v_pk_fma_f16 v108, v108, v156, v80
	v_pk_fma_f16 v107, v107, v155, v79
	v_pk_fma_f16 v80, v124, v156, v80
	v_pk_fma_f16 v79, v123, v155, v79
	v_pk_fma_f16 v123, v52, v156, v104
	v_pk_fma_f16 v124, v51, v155, v103
	v_pk_fma_f16 v125, v50, v154, v102
	v_pk_fma_f16 v127, v68, v156, v104
	v_pk_fma_f16 v128, v67, v155, v103
	v_pk_fma_f16 v129, v66, v154, v102
	v_pk_fma_f16 v104, v96, v156, v104
	v_pk_fma_f16 v103, v95, v155, v103
	v_pk_fma_f16 v102, v94, v154, v102
	v_pk_fma_f16 v139, v20, v156, v120
	v_pk_fma_f16 v140, v19, v155, v119
	v_pk_fma_f16 v141, v18, v154, v118
	v_pk_fma_f16 v184, v32, v156, v120
	v_pk_fma_f16 v185, v31, v155, v119
	v_pk_fma_f16 v186, v30, v154, v118
	v_pk_fma_f16 v120, v56, v156, v120
	v_pk_fma_f16 v119, v55, v155, v119
	v_pk_fma_f16 v118, v54, v154, v118
	v_pk_maximum3_f16 v154, v86, v106, v78
	v_pk_maximum3_f16 v155, v87, v107, v79
	v_pk_maximum3_f16 v156, v88, v108, v80
	v_pk_maximum3_f16 v190, v122, v126, v105
	v_pk_maximum3_f16 v194, v138, v183, v121
	v_pk_maximum3_f16 v187, v125, v129, v102
	v_pk_maximum3_f16 v188, v124, v128, v103
	v_pk_maximum3_f16 v189, v123, v127, v104
	v_pk_maximum3_f16 v191, v141, v186, v118
	v_pk_maximum3_f16 v192, v140, v185, v119
	v_pk_maximum3_f16 v157, v157, v190, v194
	v_pk_maximum3_f16 v193, v139, v184, v120
	v_pk_maximum3_f16 v154, v154, v187, v191
	v_pk_maximum3_f16 v155, v155, v188, v192
	v_pk_maximum3_f16 v156, v156, v189, v193
	v_pk_add_f16 v89, v89, v157 neg_lo:[0,1] neg_hi:[0,1]
	v_pk_add_f16 v86, v86, v154 neg_lo:[0,1] neg_hi:[0,1]
	v_pk_add_f16 v87, v87, v155 neg_lo:[0,1] neg_hi:[0,1]
	v_pk_add_f16 v88, v88, v156 neg_lo:[0,1] neg_hi:[0,1]
	v_pk_add_f16 v106, v106, v154 neg_lo:[0,1] neg_hi:[0,1]
	v_exp_f16_sdwa v187, v86 dst_sel:WORD_0 dst_unused:UNUSED_PAD src0_sel:WORD_0
	v_exp_f16_sdwa v188, v87 dst_sel:WORD_0 dst_unused:UNUSED_PAD src0_sel:WORD_0
	v_exp_f16_sdwa v189, v88 dst_sel:WORD_0 dst_unused:UNUSED_PAD src0_sel:WORD_0
	v_exp_f16_sdwa v190, v89 dst_sel:WORD_0 dst_unused:UNUSED_PAD src0_sel:WORD_0
	v_exp_f16_sdwa v187, v86 dst_sel:WORD_1 dst_unused:UNUSED_PRESERVE src0_sel:WORD_1
	v_exp_f16_sdwa v188, v87 dst_sel:WORD_1 dst_unused:UNUSED_PRESERVE src0_sel:WORD_1
	v_exp_f16_sdwa v189, v88 dst_sel:WORD_1 dst_unused:UNUSED_PRESERVE src0_sel:WORD_1
	v_exp_f16_sdwa v190, v89 dst_sel:WORD_1 dst_unused:UNUSED_PRESERVE src0_sel:WORD_1
	v_pk_add_f16 v107, v107, v155 neg_lo:[0,1] neg_hi:[0,1]
	v_pk_add_f16 v89, v187, 0
	v_pk_fma_f16 v49, v49, v190, 0
	v_pk_add_f16 v86, v190, 0
	v_pk_add_f16 v87, v189, 0
	v_pk_add_f16 v88, v188, 0
	v_pk_fma_f16 v48, v48, v189, 0
	v_pk_fma_f16 v47, v47, v188, 0
	v_pk_fma_f16 v46, v46, v187, 0
	v_pk_add_f16 v108, v108, v156 neg_lo:[0,1] neg_hi:[0,1]
	v_pk_add_f16 v109, v109, v157 neg_lo:[0,1] neg_hi:[0,1]
	v_exp_f16_sdwa v187, v106 dst_sel:WORD_0 dst_unused:UNUSED_PAD src0_sel:WORD_0
	v_exp_f16_sdwa v188, v107 dst_sel:WORD_0 dst_unused:UNUSED_PAD src0_sel:WORD_0
	v_exp_f16_sdwa v189, v108 dst_sel:WORD_0 dst_unused:UNUSED_PAD src0_sel:WORD_0
	v_exp_f16_sdwa v190, v109 dst_sel:WORD_0 dst_unused:UNUSED_PAD src0_sel:WORD_0
	v_exp_f16_sdwa v187, v106 dst_sel:WORD_1 dst_unused:UNUSED_PRESERVE src0_sel:WORD_1
	v_exp_f16_sdwa v188, v107 dst_sel:WORD_1 dst_unused:UNUSED_PRESERVE src0_sel:WORD_1
	v_exp_f16_sdwa v189, v108 dst_sel:WORD_1 dst_unused:UNUSED_PRESERVE src0_sel:WORD_1
	v_exp_f16_sdwa v190, v109 dst_sel:WORD_1 dst_unused:UNUSED_PRESERVE src0_sel:WORD_1
	v_pk_add_f16 v89, v89, v187
	v_pk_fma_f16 v49, v65, v190, v49
	v_pk_add_f16 v65, v81, v157 neg_lo:[0,1] neg_hi:[0,1]
	v_pk_add_f16 v88, v88, v188
	v_pk_add_f16 v87, v87, v189
	v_pk_add_f16 v86, v86, v190
	v_pk_fma_f16 v46, v62, v187, v46
	v_pk_fma_f16 v47, v63, v188, v47
	v_pk_fma_f16 v48, v64, v189, v48
	v_pk_add_f16 v62, v78, v154 neg_lo:[0,1] neg_hi:[0,1]
	v_pk_add_f16 v63, v79, v155 neg_lo:[0,1] neg_hi:[0,1]
	v_pk_add_f16 v64, v80, v156 neg_lo:[0,1] neg_hi:[0,1]
	v_exp_f16_sdwa v78, v62 dst_sel:WORD_0 dst_unused:UNUSED_PAD src0_sel:WORD_0
	v_exp_f16_sdwa v79, v63 dst_sel:WORD_0 dst_unused:UNUSED_PAD src0_sel:WORD_0
	v_exp_f16_sdwa v80, v64 dst_sel:WORD_0 dst_unused:UNUSED_PAD src0_sel:WORD_0
	v_exp_f16_sdwa v81, v65 dst_sel:WORD_0 dst_unused:UNUSED_PAD src0_sel:WORD_0
	v_exp_f16_sdwa v78, v62 dst_sel:WORD_1 dst_unused:UNUSED_PRESERVE src0_sel:WORD_1
	v_exp_f16_sdwa v79, v63 dst_sel:WORD_1 dst_unused:UNUSED_PRESERVE src0_sel:WORD_1
	v_exp_f16_sdwa v80, v64 dst_sel:WORD_1 dst_unused:UNUSED_PRESERVE src0_sel:WORD_1
	v_exp_f16_sdwa v81, v65 dst_sel:WORD_1 dst_unused:UNUSED_PRESERVE src0_sel:WORD_1
	v_pk_add_f16 v65, v89, v78
	v_pk_add_f16 v62, v86, v81
	v_pk_add_f16 v63, v87, v80
	v_pk_add_f16 v64, v88, v79
	v_pk_fma_f16 v49, v85, v81, v49
	v_pk_fma_f16 v48, v84, v80, v48
	v_pk_fma_f16 v47, v83, v79, v47
	v_pk_fma_f16 v46, v82, v78, v46
	v_pk_add_f16 v78, v125, v154 neg_lo:[0,1] neg_hi:[0,1]
	v_pk_add_f16 v79, v124, v155 neg_lo:[0,1] neg_hi:[0,1]
	v_pk_add_f16 v80, v123, v156 neg_lo:[0,1] neg_hi:[0,1]
	v_pk_add_f16 v81, v122, v157 neg_lo:[0,1] neg_hi:[0,1]
	v_exp_f16_sdwa v82, v78 dst_sel:WORD_0 dst_unused:UNUSED_PAD src0_sel:WORD_0
	v_exp_f16_sdwa v83, v79 dst_sel:WORD_0 dst_unused:UNUSED_PAD src0_sel:WORD_0
	v_exp_f16_sdwa v84, v80 dst_sel:WORD_0 dst_unused:UNUSED_PAD src0_sel:WORD_0
	v_exp_f16_sdwa v85, v81 dst_sel:WORD_0 dst_unused:UNUSED_PAD src0_sel:WORD_0
	v_exp_f16_sdwa v82, v78 dst_sel:WORD_1 dst_unused:UNUSED_PRESERVE src0_sel:WORD_1
	v_exp_f16_sdwa v83, v79 dst_sel:WORD_1 dst_unused:UNUSED_PRESERVE src0_sel:WORD_1
	v_exp_f16_sdwa v84, v80 dst_sel:WORD_1 dst_unused:UNUSED_PRESERVE src0_sel:WORD_1
	v_exp_f16_sdwa v85, v81 dst_sel:WORD_1 dst_unused:UNUSED_PRESERVE src0_sel:WORD_1
	v_pk_add_f16 v78, v129, v154 neg_lo:[0,1] neg_hi:[0,1]
	v_pk_add_f16 v65, v65, v82
	v_pk_add_f16 v64, v64, v83
	v_pk_add_f16 v63, v63, v84
	v_pk_add_f16 v62, v62, v85
	v_pk_fma_f16 v46, v22, v82, v46
	v_pk_fma_f16 v47, v23, v83, v47
	v_pk_fma_f16 v48, v24, v84, v48
	v_pk_fma_f16 v49, v25, v85, v49
	v_pk_add_f16 v79, v128, v155 neg_lo:[0,1] neg_hi:[0,1]
	v_pk_add_f16 v80, v127, v156 neg_lo:[0,1] neg_hi:[0,1]
	v_pk_add_f16 v81, v126, v157 neg_lo:[0,1] neg_hi:[0,1]
	v_exp_f16_sdwa v82, v78 dst_sel:WORD_0 dst_unused:UNUSED_PAD src0_sel:WORD_0
	v_exp_f16_sdwa v83, v79 dst_sel:WORD_0 dst_unused:UNUSED_PAD src0_sel:WORD_0
	v_exp_f16_sdwa v84, v80 dst_sel:WORD_0 dst_unused:UNUSED_PAD src0_sel:WORD_0
	v_exp_f16_sdwa v85, v81 dst_sel:WORD_0 dst_unused:UNUSED_PAD src0_sel:WORD_0
	v_exp_f16_sdwa v82, v78 dst_sel:WORD_1 dst_unused:UNUSED_PRESERVE src0_sel:WORD_1
	v_exp_f16_sdwa v83, v79 dst_sel:WORD_1 dst_unused:UNUSED_PRESERVE src0_sel:WORD_1
	v_exp_f16_sdwa v84, v80 dst_sel:WORD_1 dst_unused:UNUSED_PRESERVE src0_sel:WORD_1
	v_exp_f16_sdwa v85, v81 dst_sel:WORD_1 dst_unused:UNUSED_PRESERVE src0_sel:WORD_1
	v_pk_add_f16 v78, v102, v154 neg_lo:[0,1] neg_hi:[0,1]
	v_pk_add_f16 v65, v65, v82
	v_pk_add_f16 v62, v62, v85
	v_pk_add_f16 v63, v63, v84
	v_pk_add_f16 v64, v64, v83
	v_pk_fma_f16 v49, v37, v85, v49
	v_pk_fma_f16 v48, v36, v84, v48
	v_pk_fma_f16 v47, v35, v83, v47
	v_pk_fma_f16 v46, v34, v82, v46
	v_pk_add_f16 v79, v103, v155 neg_lo:[0,1] neg_hi:[0,1]
	v_pk_add_f16 v80, v104, v156 neg_lo:[0,1] neg_hi:[0,1]
	v_pk_add_f16 v81, v105, v157 neg_lo:[0,1] neg_hi:[0,1]
	v_exp_f16_sdwa v82, v78 dst_sel:WORD_0 dst_unused:UNUSED_PAD src0_sel:WORD_0
	v_exp_f16_sdwa v83, v79 dst_sel:WORD_0 dst_unused:UNUSED_PAD src0_sel:WORD_0
	v_exp_f16_sdwa v84, v80 dst_sel:WORD_0 dst_unused:UNUSED_PAD src0_sel:WORD_0
	v_exp_f16_sdwa v85, v81 dst_sel:WORD_0 dst_unused:UNUSED_PAD src0_sel:WORD_0
	v_exp_f16_sdwa v82, v78 dst_sel:WORD_1 dst_unused:UNUSED_PRESERVE src0_sel:WORD_1
	v_exp_f16_sdwa v83, v79 dst_sel:WORD_1 dst_unused:UNUSED_PRESERVE src0_sel:WORD_1
	v_exp_f16_sdwa v84, v80 dst_sel:WORD_1 dst_unused:UNUSED_PRESERVE src0_sel:WORD_1
	v_exp_f16_sdwa v85, v81 dst_sel:WORD_1 dst_unused:UNUSED_PRESERVE src0_sel:WORD_1
	v_pk_add_f16 v78, v141, v154 neg_lo:[0,1] neg_hi:[0,1]
	v_pk_add_f16 v65, v65, v82
	v_pk_add_f16 v64, v64, v83
	v_pk_add_f16 v63, v63, v84
	v_pk_add_f16 v62, v62, v85
	v_pk_fma_f16 v46, v42, v82, v46
	v_pk_fma_f16 v47, v43, v83, v47
	v_pk_fma_f16 v48, v44, v84, v48
	v_pk_fma_f16 v49, v45, v85, v49
	v_pk_add_f16 v79, v140, v155 neg_lo:[0,1] neg_hi:[0,1]
	v_pk_add_f16 v80, v139, v156 neg_lo:[0,1] neg_hi:[0,1]
	v_pk_add_f16 v81, v138, v157 neg_lo:[0,1] neg_hi:[0,1]
	v_exp_f16_sdwa v82, v78 dst_sel:WORD_0 dst_unused:UNUSED_PAD src0_sel:WORD_0
	v_exp_f16_sdwa v83, v79 dst_sel:WORD_0 dst_unused:UNUSED_PAD src0_sel:WORD_0
	v_exp_f16_sdwa v84, v80 dst_sel:WORD_0 dst_unused:UNUSED_PAD src0_sel:WORD_0
	v_exp_f16_sdwa v85, v81 dst_sel:WORD_0 dst_unused:UNUSED_PAD src0_sel:WORD_0
	v_exp_f16_sdwa v82, v78 dst_sel:WORD_1 dst_unused:UNUSED_PRESERVE src0_sel:WORD_1
	v_exp_f16_sdwa v83, v79 dst_sel:WORD_1 dst_unused:UNUSED_PRESERVE src0_sel:WORD_1
	v_exp_f16_sdwa v84, v80 dst_sel:WORD_1 dst_unused:UNUSED_PRESERVE src0_sel:WORD_1
	v_exp_f16_sdwa v85, v81 dst_sel:WORD_1 dst_unused:UNUSED_PRESERVE src0_sel:WORD_1
	v_pk_add_f16 v78, v186, v154 neg_lo:[0,1] neg_hi:[0,1]
	v_pk_add_f16 v65, v65, v82
	v_pk_add_f16 v62, v62, v85
	v_pk_add_f16 v63, v63, v84
	v_pk_add_f16 v64, v64, v83
	v_pk_fma_f16 v49, v9, v85, v49
	v_pk_fma_f16 v48, v8, v84, v48
	v_pk_fma_f16 v47, v7, v83, v47
	v_pk_fma_f16 v46, v6, v82, v46
	v_pk_add_f16 v79, v185, v155 neg_lo:[0,1] neg_hi:[0,1]
	v_pk_add_f16 v80, v184, v156 neg_lo:[0,1] neg_hi:[0,1]
	v_pk_add_f16 v81, v183, v157 neg_lo:[0,1] neg_hi:[0,1]
	v_exp_f16_sdwa v82, v78 dst_sel:WORD_0 dst_unused:UNUSED_PAD src0_sel:WORD_0
	v_exp_f16_sdwa v83, v79 dst_sel:WORD_0 dst_unused:UNUSED_PAD src0_sel:WORD_0
	v_exp_f16_sdwa v84, v80 dst_sel:WORD_0 dst_unused:UNUSED_PAD src0_sel:WORD_0
	v_exp_f16_sdwa v85, v81 dst_sel:WORD_0 dst_unused:UNUSED_PAD src0_sel:WORD_0
	v_exp_f16_sdwa v82, v78 dst_sel:WORD_1 dst_unused:UNUSED_PRESERVE src0_sel:WORD_1
	v_exp_f16_sdwa v83, v79 dst_sel:WORD_1 dst_unused:UNUSED_PRESERVE src0_sel:WORD_1
	v_exp_f16_sdwa v84, v80 dst_sel:WORD_1 dst_unused:UNUSED_PRESERVE src0_sel:WORD_1
	v_exp_f16_sdwa v85, v81 dst_sel:WORD_1 dst_unused:UNUSED_PRESERVE src0_sel:WORD_1
	v_pk_add_f16 v78, v118, v154 neg_lo:[0,1] neg_hi:[0,1]
	v_pk_add_f16 v65, v65, v82
	v_pk_add_f16 v64, v64, v83
	v_pk_add_f16 v63, v63, v84
	v_pk_add_f16 v62, v62, v85
	v_pk_fma_f16 v46, v10, v82, v46
	v_pk_fma_f16 v47, v11, v83, v47
	v_pk_fma_f16 v48, v12, v84, v48
	v_pk_fma_f16 v49, v13, v85, v49
	v_pk_add_f16 v79, v119, v155 neg_lo:[0,1] neg_hi:[0,1]
	v_pk_add_f16 v80, v120, v156 neg_lo:[0,1] neg_hi:[0,1]
	v_pk_add_f16 v81, v121, v157 neg_lo:[0,1] neg_hi:[0,1]
	v_exp_f16_sdwa v82, v78 dst_sel:WORD_0 dst_unused:UNUSED_PAD src0_sel:WORD_0
	v_exp_f16_sdwa v83, v79 dst_sel:WORD_0 dst_unused:UNUSED_PAD src0_sel:WORD_0
	v_exp_f16_sdwa v84, v80 dst_sel:WORD_0 dst_unused:UNUSED_PAD src0_sel:WORD_0
	v_exp_f16_sdwa v85, v81 dst_sel:WORD_0 dst_unused:UNUSED_PAD src0_sel:WORD_0
	v_exp_f16_sdwa v82, v78 dst_sel:WORD_1 dst_unused:UNUSED_PRESERVE src0_sel:WORD_1
	v_exp_f16_sdwa v83, v79 dst_sel:WORD_1 dst_unused:UNUSED_PRESERVE src0_sel:WORD_1
	v_exp_f16_sdwa v84, v80 dst_sel:WORD_1 dst_unused:UNUSED_PRESERVE src0_sel:WORD_1
	v_exp_f16_sdwa v85, v81 dst_sel:WORD_1 dst_unused:UNUSED_PRESERVE src0_sel:WORD_1
	v_pk_add_f16 v65, v65, v82
	v_pk_add_f16 v64, v64, v83
	v_rcp_f16_e32 v78, v65
	v_rcp_f16_sdwa v65, v65 dst_sel:DWORD dst_unused:UNUSED_PAD src0_sel:WORD_1
	v_pk_add_f16 v63, v63, v84
	v_rcp_f16_e32 v79, v64
	v_rcp_f16_sdwa v64, v64 dst_sel:DWORD dst_unused:UNUSED_PAD src0_sel:WORD_1
	v_pk_add_f16 v62, v62, v85
	v_rcp_f16_e32 v80, v63
	v_rcp_f16_sdwa v81, v63 dst_sel:DWORD dst_unused:UNUSED_PAD src0_sel:WORD_1
	v_pk_fma_f16 v47, v15, v83, v47
	v_pk_fma_f16 v46, v14, v82, v46
	v_rcp_f16_e32 v82, v62
	v_rcp_f16_sdwa v83, v62 dst_sel:DWORD dst_unused:UNUSED_PAD src0_sel:WORD_1
	v_pack_b32_f16 v62, v78, v65
	v_pk_mul_f16 v62, v46, v62
	v_pack_b32_f16 v46, v79, v64
	v_pk_fma_f16 v48, v16, v84, v48
	v_pk_mul_f16 v63, v47, v46
	v_pack_b32_f16 v46, v80, v81
	v_pk_fma_f16 v49, v17, v85, v49
	v_pk_mul_f16 v64, v48, v46
	v_pack_b32_f16 v46, v82, v83
	v_pk_mul_f16 v65, v49, v46
	s_waitcnt vmcnt(6)
	v_pk_mul_f16 v46, v182, v150 op_sel_hi:[0,1]
	v_pk_mul_f16 v47, v182, v151 op_sel_hi:[0,1]
	v_pk_mul_f16 v48, v182, v152 op_sel_hi:[0,1]
	v_pk_mul_f16 v49, v182, v153 op_sel_hi:[0,1]
	v_pk_mul_f16 v78, v180, v150 op_sel_hi:[0,1]
	v_pk_mul_f16 v82, v181, v150 op_sel_hi:[0,1]
	v_pk_fma_f16 v50, v50, v150, v46
	v_pk_fma_f16 v66, v66, v150, v46
	v_pk_fma_f16 v46, v94, v150, v46
	v_pk_mul_f16 v79, v180, v151 op_sel_hi:[0,1]
	v_pk_maximum3_f16 v118, v50, v66, v46
	v_pk_mul_f16 v80, v180, v152 op_sel_hi:[0,1]
	v_pk_mul_f16 v81, v180, v153 op_sel_hi:[0,1]
	v_pk_mul_f16 v83, v181, v151 op_sel_hi:[0,1]
	v_pk_mul_f16 v84, v181, v152 op_sel_hi:[0,1]
	v_pk_mul_f16 v85, v181, v153 op_sel_hi:[0,1]
	v_pk_fma_f16 v53, v53, v153, v49
	v_pk_fma_f16 v52, v52, v152, v48
	v_pk_fma_f16 v51, v51, v151, v47
	v_pk_fma_f16 v69, v69, v153, v49
	v_pk_fma_f16 v68, v68, v152, v48
	v_pk_fma_f16 v67, v67, v151, v47
	v_pk_fma_f16 v49, v97, v153, v49
	v_pk_fma_f16 v48, v96, v152, v48
	v_pk_fma_f16 v47, v95, v151, v47
	v_pk_fma_f16 v89, v18, v150, v78
	v_pk_fma_f16 v97, v30, v150, v78
	v_pk_fma_f16 v78, v54, v150, v78
	v_pk_fma_f16 v105, v74, v150, v82
	v_pk_fma_f16 v109, v98, v150, v82
	v_pk_fma_f16 v82, v114, v150, v82
	v_pk_maximum3_f16 v119, v51, v67, v47
	v_pk_maximum3_f16 v120, v52, v68, v48
	v_pk_maximum3_f16 v121, v53, v69, v49
	v_pk_maximum3_f16 v122, v89, v97, v78
	v_pk_fma_f16 v86, v21, v153, v81
	v_pk_maximum3_f16 v126, v105, v109, v82
	v_pk_fma_f16 v87, v20, v152, v80
	v_pk_maximum3_f16 v118, v118, v122, v126
	v_pk_fma_f16 v88, v19, v151, v79
	v_pk_fma_f16 v94, v33, v153, v81
	v_pk_fma_f16 v95, v32, v152, v80
	v_pk_fma_f16 v96, v31, v151, v79
	v_pk_fma_f16 v81, v57, v153, v81
	v_pk_fma_f16 v80, v56, v152, v80
	v_pk_fma_f16 v79, v55, v151, v79
	v_pk_fma_f16 v102, v77, v153, v85
	v_pk_fma_f16 v103, v76, v152, v84
	v_pk_fma_f16 v104, v75, v151, v83
	v_pk_fma_f16 v106, v101, v153, v85
	v_pk_fma_f16 v107, v100, v152, v84
	v_pk_fma_f16 v108, v99, v151, v83
	v_pk_fma_f16 v85, v117, v153, v85
	v_pk_fma_f16 v84, v116, v152, v84
	v_pk_fma_f16 v83, v115, v151, v83
	v_pk_maximum3_f16 v123, v88, v96, v79
	v_pk_maximum3_f16 v124, v87, v95, v80
	v_pk_maximum3_f16 v125, v86, v94, v81
	v_pk_maximum3_f16 v128, v103, v107, v84
	v_pk_maximum3_f16 v129, v102, v106, v85
	v_pk_maximum3_f16 v127, v104, v108, v83
	v_pk_maximum3_f16 v119, v119, v123, v127
	v_pk_maximum3_f16 v120, v120, v124, v128
	v_pk_maximum3_f16 v121, v121, v125, v129
	v_pk_add_f16 v50, v50, v118 neg_lo:[0,1] neg_hi:[0,1]
	v_pk_add_f16 v51, v51, v119 neg_lo:[0,1] neg_hi:[0,1]
	v_pk_add_f16 v52, v52, v120 neg_lo:[0,1] neg_hi:[0,1]
	v_pk_add_f16 v53, v53, v121 neg_lo:[0,1] neg_hi:[0,1]
	v_pk_add_f16 v66, v66, v118 neg_lo:[0,1] neg_hi:[0,1]
	v_exp_f16_sdwa v122, v50 dst_sel:WORD_0 dst_unused:UNUSED_PAD src0_sel:WORD_0
	v_exp_f16_sdwa v123, v51 dst_sel:WORD_0 dst_unused:UNUSED_PAD src0_sel:WORD_0
	v_exp_f16_sdwa v124, v52 dst_sel:WORD_0 dst_unused:UNUSED_PAD src0_sel:WORD_0
	v_exp_f16_sdwa v125, v53 dst_sel:WORD_0 dst_unused:UNUSED_PAD src0_sel:WORD_0
	v_exp_f16_sdwa v122, v50 dst_sel:WORD_1 dst_unused:UNUSED_PRESERVE src0_sel:WORD_1
	v_exp_f16_sdwa v123, v51 dst_sel:WORD_1 dst_unused:UNUSED_PRESERVE src0_sel:WORD_1
	v_exp_f16_sdwa v124, v52 dst_sel:WORD_1 dst_unused:UNUSED_PRESERVE src0_sel:WORD_1
	v_exp_f16_sdwa v125, v53 dst_sel:WORD_1 dst_unused:UNUSED_PRESERVE src0_sel:WORD_1
	v_pk_add_f16 v67, v67, v119 neg_lo:[0,1] neg_hi:[0,1]
	v_pk_add_f16 v50, v125, 0
	v_pk_fma_f16 v22, v22, v122, 0
	v_pk_add_f16 v51, v124, 0
	v_pk_add_f16 v52, v123, 0
	v_pk_add_f16 v53, v122, 0
	v_pk_fma_f16 v23, v23, v123, 0
	v_pk_fma_f16 v24, v24, v124, 0
	v_pk_fma_f16 v25, v25, v125, 0
	v_pk_add_f16 v68, v68, v120 neg_lo:[0,1] neg_hi:[0,1]
	v_pk_add_f16 v69, v69, v121 neg_lo:[0,1] neg_hi:[0,1]
	v_exp_f16_sdwa v122, v66 dst_sel:WORD_0 dst_unused:UNUSED_PAD src0_sel:WORD_0
	v_exp_f16_sdwa v123, v67 dst_sel:WORD_0 dst_unused:UNUSED_PAD src0_sel:WORD_0
	v_exp_f16_sdwa v124, v68 dst_sel:WORD_0 dst_unused:UNUSED_PAD src0_sel:WORD_0
	v_exp_f16_sdwa v125, v69 dst_sel:WORD_0 dst_unused:UNUSED_PAD src0_sel:WORD_0
	v_exp_f16_sdwa v122, v66 dst_sel:WORD_1 dst_unused:UNUSED_PRESERVE src0_sel:WORD_1
	v_exp_f16_sdwa v123, v67 dst_sel:WORD_1 dst_unused:UNUSED_PRESERVE src0_sel:WORD_1
	v_exp_f16_sdwa v124, v68 dst_sel:WORD_1 dst_unused:UNUSED_PRESERVE src0_sel:WORD_1
	v_exp_f16_sdwa v125, v69 dst_sel:WORD_1 dst_unused:UNUSED_PRESERVE src0_sel:WORD_1
	s_nop 0
	v_pk_add_f16 v50, v50, v125
	v_pk_fma_f16 v22, v34, v122, v22
	v_pk_add_f16 v34, v46, v118 neg_lo:[0,1] neg_hi:[0,1]
	v_pk_add_f16 v53, v53, v122
	v_pk_add_f16 v52, v52, v123
	v_pk_add_f16 v51, v51, v124
	v_pk_fma_f16 v25, v37, v125, v25
	v_pk_fma_f16 v24, v36, v124, v24
	v_pk_fma_f16 v23, v35, v123, v23
	v_pk_add_f16 v35, v47, v119 neg_lo:[0,1] neg_hi:[0,1]
	v_pk_add_f16 v36, v48, v120 neg_lo:[0,1] neg_hi:[0,1]
	v_pk_add_f16 v37, v49, v121 neg_lo:[0,1] neg_hi:[0,1]
	v_exp_f16_sdwa v46, v34 dst_sel:WORD_0 dst_unused:UNUSED_PAD src0_sel:WORD_0
	v_exp_f16_sdwa v47, v35 dst_sel:WORD_0 dst_unused:UNUSED_PAD src0_sel:WORD_0
	v_exp_f16_sdwa v48, v36 dst_sel:WORD_0 dst_unused:UNUSED_PAD src0_sel:WORD_0
	v_exp_f16_sdwa v49, v37 dst_sel:WORD_0 dst_unused:UNUSED_PAD src0_sel:WORD_0
	v_exp_f16_sdwa v46, v34 dst_sel:WORD_1 dst_unused:UNUSED_PRESERVE src0_sel:WORD_1
	v_exp_f16_sdwa v47, v35 dst_sel:WORD_1 dst_unused:UNUSED_PRESERVE src0_sel:WORD_1
	v_exp_f16_sdwa v48, v36 dst_sel:WORD_1 dst_unused:UNUSED_PRESERVE src0_sel:WORD_1
	v_exp_f16_sdwa v49, v37 dst_sel:WORD_1 dst_unused:UNUSED_PRESERVE src0_sel:WORD_1
	s_nop 0
	v_pk_add_f16 v34, v50, v49
	v_pk_add_f16 v35, v51, v48
	v_pk_add_f16 v36, v52, v47
	v_pk_add_f16 v37, v53, v46
	v_pk_fma_f16 v22, v42, v46, v22
	v_pk_fma_f16 v23, v43, v47, v23
	v_pk_fma_f16 v24, v44, v48, v24
	v_pk_fma_f16 v25, v45, v49, v25
	v_pk_add_f16 v42, v89, v118 neg_lo:[0,1] neg_hi:[0,1]
	v_pk_add_f16 v43, v88, v119 neg_lo:[0,1] neg_hi:[0,1]
	v_pk_add_f16 v44, v87, v120 neg_lo:[0,1] neg_hi:[0,1]
	v_pk_add_f16 v45, v86, v121 neg_lo:[0,1] neg_hi:[0,1]
	v_exp_f16_sdwa v46, v42 dst_sel:WORD_0 dst_unused:UNUSED_PAD src0_sel:WORD_0
	v_exp_f16_sdwa v47, v43 dst_sel:WORD_0 dst_unused:UNUSED_PAD src0_sel:WORD_0
	v_exp_f16_sdwa v48, v44 dst_sel:WORD_0 dst_unused:UNUSED_PAD src0_sel:WORD_0
	v_exp_f16_sdwa v49, v45 dst_sel:WORD_0 dst_unused:UNUSED_PAD src0_sel:WORD_0
	v_exp_f16_sdwa v46, v42 dst_sel:WORD_1 dst_unused:UNUSED_PRESERVE src0_sel:WORD_1
	v_exp_f16_sdwa v47, v43 dst_sel:WORD_1 dst_unused:UNUSED_PRESERVE src0_sel:WORD_1
	v_exp_f16_sdwa v48, v44 dst_sel:WORD_1 dst_unused:UNUSED_PRESERVE src0_sel:WORD_1
	v_exp_f16_sdwa v49, v45 dst_sel:WORD_1 dst_unused:UNUSED_PRESERVE src0_sel:WORD_1
	v_pk_add_f16 v42, v97, v118 neg_lo:[0,1] neg_hi:[0,1]
	v_pk_add_f16 v34, v34, v49
	v_pk_add_f16 v37, v37, v46
	v_pk_add_f16 v36, v36, v47
	v_pk_add_f16 v35, v35, v48
	v_pk_fma_f16 v25, v9, v49, v25
	v_pk_fma_f16 v24, v8, v48, v24
	v_pk_fma_f16 v23, v7, v47, v23
	v_pk_fma_f16 v22, v6, v46, v22
	v_pk_add_f16 v43, v96, v119 neg_lo:[0,1] neg_hi:[0,1]
	v_pk_add_f16 v44, v95, v120 neg_lo:[0,1] neg_hi:[0,1]
	v_pk_add_f16 v45, v94, v121 neg_lo:[0,1] neg_hi:[0,1]
	v_exp_f16_sdwa v46, v42 dst_sel:WORD_0 dst_unused:UNUSED_PAD src0_sel:WORD_0
	v_exp_f16_sdwa v47, v43 dst_sel:WORD_0 dst_unused:UNUSED_PAD src0_sel:WORD_0
	v_exp_f16_sdwa v48, v44 dst_sel:WORD_0 dst_unused:UNUSED_PAD src0_sel:WORD_0
	v_exp_f16_sdwa v49, v45 dst_sel:WORD_0 dst_unused:UNUSED_PAD src0_sel:WORD_0
	v_exp_f16_sdwa v46, v42 dst_sel:WORD_1 dst_unused:UNUSED_PRESERVE src0_sel:WORD_1
	v_exp_f16_sdwa v47, v43 dst_sel:WORD_1 dst_unused:UNUSED_PRESERVE src0_sel:WORD_1
	v_exp_f16_sdwa v48, v44 dst_sel:WORD_1 dst_unused:UNUSED_PRESERVE src0_sel:WORD_1
	v_exp_f16_sdwa v49, v45 dst_sel:WORD_1 dst_unused:UNUSED_PRESERVE src0_sel:WORD_1
	v_pk_add_f16 v42, v78, v118 neg_lo:[0,1] neg_hi:[0,1]
	v_pk_add_f16 v34, v34, v49
	v_pk_add_f16 v35, v35, v48
	v_pk_add_f16 v36, v36, v47
	v_pk_add_f16 v37, v37, v46
	v_pk_fma_f16 v22, v10, v46, v22
	v_pk_fma_f16 v23, v11, v47, v23
	v_pk_fma_f16 v24, v12, v48, v24
	v_pk_fma_f16 v25, v13, v49, v25
	v_pk_add_f16 v43, v79, v119 neg_lo:[0,1] neg_hi:[0,1]
	v_pk_add_f16 v44, v80, v120 neg_lo:[0,1] neg_hi:[0,1]
	v_pk_add_f16 v45, v81, v121 neg_lo:[0,1] neg_hi:[0,1]
	v_exp_f16_sdwa v46, v42 dst_sel:WORD_0 dst_unused:UNUSED_PAD src0_sel:WORD_0
	v_exp_f16_sdwa v47, v43 dst_sel:WORD_0 dst_unused:UNUSED_PAD src0_sel:WORD_0
	v_exp_f16_sdwa v48, v44 dst_sel:WORD_0 dst_unused:UNUSED_PAD src0_sel:WORD_0
	v_exp_f16_sdwa v49, v45 dst_sel:WORD_0 dst_unused:UNUSED_PAD src0_sel:WORD_0
	v_exp_f16_sdwa v46, v42 dst_sel:WORD_1 dst_unused:UNUSED_PRESERVE src0_sel:WORD_1
	v_exp_f16_sdwa v47, v43 dst_sel:WORD_1 dst_unused:UNUSED_PRESERVE src0_sel:WORD_1
	v_exp_f16_sdwa v48, v44 dst_sel:WORD_1 dst_unused:UNUSED_PRESERVE src0_sel:WORD_1
	v_exp_f16_sdwa v49, v45 dst_sel:WORD_1 dst_unused:UNUSED_PRESERVE src0_sel:WORD_1
	v_pk_add_f16 v42, v105, v118 neg_lo:[0,1] neg_hi:[0,1]
	v_pk_add_f16 v34, v34, v49
	v_pk_add_f16 v37, v37, v46
	v_pk_add_f16 v36, v36, v47
	v_pk_add_f16 v35, v35, v48
	v_pk_fma_f16 v25, v17, v49, v25
	v_pk_fma_f16 v24, v16, v48, v24
	v_pk_fma_f16 v23, v15, v47, v23
	v_pk_fma_f16 v22, v14, v46, v22
	v_pk_add_f16 v43, v104, v119 neg_lo:[0,1] neg_hi:[0,1]
	v_pk_add_f16 v44, v103, v120 neg_lo:[0,1] neg_hi:[0,1]
	v_pk_add_f16 v45, v102, v121 neg_lo:[0,1] neg_hi:[0,1]
	v_exp_f16_sdwa v46, v42 dst_sel:WORD_0 dst_unused:UNUSED_PAD src0_sel:WORD_0
	v_exp_f16_sdwa v47, v43 dst_sel:WORD_0 dst_unused:UNUSED_PAD src0_sel:WORD_0
	v_exp_f16_sdwa v48, v44 dst_sel:WORD_0 dst_unused:UNUSED_PAD src0_sel:WORD_0
	v_exp_f16_sdwa v49, v45 dst_sel:WORD_0 dst_unused:UNUSED_PAD src0_sel:WORD_0
	v_exp_f16_sdwa v46, v42 dst_sel:WORD_1 dst_unused:UNUSED_PRESERVE src0_sel:WORD_1
	v_exp_f16_sdwa v47, v43 dst_sel:WORD_1 dst_unused:UNUSED_PRESERVE src0_sel:WORD_1
	v_exp_f16_sdwa v48, v44 dst_sel:WORD_1 dst_unused:UNUSED_PRESERVE src0_sel:WORD_1
	v_exp_f16_sdwa v49, v45 dst_sel:WORD_1 dst_unused:UNUSED_PRESERVE src0_sel:WORD_1
	v_pk_add_f16 v42, v109, v118 neg_lo:[0,1] neg_hi:[0,1]
	v_pk_add_f16 v34, v34, v49
	v_pk_add_f16 v35, v35, v48
	v_pk_add_f16 v36, v36, v47
	v_pk_add_f16 v37, v37, v46
	v_pk_fma_f16 v22, v26, v46, v22
	v_pk_fma_f16 v23, v27, v47, v23
	v_pk_fma_f16 v24, v28, v48, v24
	v_pk_fma_f16 v25, v29, v49, v25
	v_pk_add_f16 v43, v108, v119 neg_lo:[0,1] neg_hi:[0,1]
	v_pk_add_f16 v44, v107, v120 neg_lo:[0,1] neg_hi:[0,1]
	v_pk_add_f16 v45, v106, v121 neg_lo:[0,1] neg_hi:[0,1]
	v_exp_f16_sdwa v46, v42 dst_sel:WORD_0 dst_unused:UNUSED_PAD src0_sel:WORD_0
	v_exp_f16_sdwa v47, v43 dst_sel:WORD_0 dst_unused:UNUSED_PAD src0_sel:WORD_0
	v_exp_f16_sdwa v48, v44 dst_sel:WORD_0 dst_unused:UNUSED_PAD src0_sel:WORD_0
	v_exp_f16_sdwa v49, v45 dst_sel:WORD_0 dst_unused:UNUSED_PAD src0_sel:WORD_0
	v_exp_f16_sdwa v46, v42 dst_sel:WORD_1 dst_unused:UNUSED_PRESERVE src0_sel:WORD_1
	v_exp_f16_sdwa v47, v43 dst_sel:WORD_1 dst_unused:UNUSED_PRESERVE src0_sel:WORD_1
	v_exp_f16_sdwa v48, v44 dst_sel:WORD_1 dst_unused:UNUSED_PRESERVE src0_sel:WORD_1
	v_exp_f16_sdwa v49, v45 dst_sel:WORD_1 dst_unused:UNUSED_PRESERVE src0_sel:WORD_1
	v_pk_add_f16 v42, v82, v118 neg_lo:[0,1] neg_hi:[0,1]
	v_pk_add_f16 v34, v34, v49
	v_pk_add_f16 v37, v37, v46
	v_pk_add_f16 v36, v36, v47
	v_pk_add_f16 v35, v35, v48
	v_pk_fma_f16 v25, v41, v49, v25
	v_pk_fma_f16 v24, v40, v48, v24
	v_pk_fma_f16 v23, v39, v47, v23
	v_pk_fma_f16 v22, v38, v46, v22
	v_pk_add_f16 v43, v83, v119 neg_lo:[0,1] neg_hi:[0,1]
	v_pk_add_f16 v44, v84, v120 neg_lo:[0,1] neg_hi:[0,1]
	v_pk_add_f16 v45, v85, v121 neg_lo:[0,1] neg_hi:[0,1]
	v_exp_f16_sdwa v46, v42 dst_sel:WORD_0 dst_unused:UNUSED_PAD src0_sel:WORD_0
	v_exp_f16_sdwa v47, v43 dst_sel:WORD_0 dst_unused:UNUSED_PAD src0_sel:WORD_0
	v_exp_f16_sdwa v48, v44 dst_sel:WORD_0 dst_unused:UNUSED_PAD src0_sel:WORD_0
	v_exp_f16_sdwa v49, v45 dst_sel:WORD_0 dst_unused:UNUSED_PAD src0_sel:WORD_0
	v_exp_f16_sdwa v46, v42 dst_sel:WORD_1 dst_unused:UNUSED_PRESERVE src0_sel:WORD_1
	v_exp_f16_sdwa v47, v43 dst_sel:WORD_1 dst_unused:UNUSED_PRESERVE src0_sel:WORD_1
	v_exp_f16_sdwa v48, v44 dst_sel:WORD_1 dst_unused:UNUSED_PRESERVE src0_sel:WORD_1
	v_exp_f16_sdwa v49, v45 dst_sel:WORD_1 dst_unused:UNUSED_PRESERVE src0_sel:WORD_1
	s_nop 0
	v_pk_add_f16 v34, v34, v49
	v_pk_add_f16 v35, v35, v48
	v_rcp_f16_e32 v44, v34
	v_rcp_f16_sdwa v34, v34 dst_sel:DWORD dst_unused:UNUSED_PAD src0_sel:WORD_1
	v_pk_add_f16 v36, v36, v47
	v_rcp_f16_e32 v45, v35
	v_rcp_f16_sdwa v35, v35 dst_sel:DWORD dst_unused:UNUSED_PAD src0_sel:WORD_1
	v_pk_add_f16 v37, v37, v46
	v_rcp_f16_e32 v43, v36
	v_rcp_f16_sdwa v36, v36 dst_sel:DWORD dst_unused:UNUSED_PAD src0_sel:WORD_1
	v_rcp_f16_e32 v42, v37
	v_rcp_f16_sdwa v37, v37 dst_sel:DWORD dst_unused:UNUSED_PAD src0_sel:WORD_1
	v_pk_fma_f16 v25, v61, v49, v25
	v_pack_b32_f16 v34, v44, v34
	v_pk_fma_f16 v24, v60, v48, v24
	v_pk_mul_f16 v25, v25, v34
	v_pack_b32_f16 v34, v45, v35
	v_pk_fma_f16 v23, v59, v47, v23
	v_pk_mul_f16 v24, v24, v34
	v_pack_b32_f16 v34, v43, v36
	v_pk_fma_f16 v22, v58, v46, v22
	v_pk_mul_f16 v23, v23, v34
	v_pack_b32_f16 v34, v42, v37
	v_pk_mul_f16 v22, v22, v34
	s_waitcnt vmcnt(0)
	v_pk_mul_f16 v34, v182, v146 op_sel_hi:[0,1]
	v_pk_mul_f16 v35, v182, v147 op_sel_hi:[0,1]
	v_pk_mul_f16 v36, v182, v148 op_sel_hi:[0,1]
	v_pk_mul_f16 v37, v182, v149 op_sel_hi:[0,1]
	v_pk_mul_f16 v42, v180, v146 op_sel_hi:[0,1]
	v_pk_mul_f16 v43, v180, v147 op_sel_hi:[0,1]
	v_pk_mul_f16 v44, v180, v148 op_sel_hi:[0,1]
	v_pk_mul_f16 v45, v180, v149 op_sel_hi:[0,1]
	v_pk_mul_f16 v46, v181, v146 op_sel_hi:[0,1]
	v_pk_mul_f16 v47, v181, v147 op_sel_hi:[0,1]
	v_pk_mul_f16 v48, v181, v148 op_sel_hi:[0,1]
	v_pk_mul_f16 v49, v181, v149 op_sel_hi:[0,1]
	v_pk_fma_f16 v21, v21, v149, v37
	v_pk_fma_f16 v20, v20, v148, v36
	v_pk_fma_f16 v19, v19, v147, v35
	v_pk_fma_f16 v18, v18, v146, v34
	v_pk_fma_f16 v33, v33, v149, v37
	v_pk_fma_f16 v32, v32, v148, v36
	v_pk_fma_f16 v31, v31, v147, v35
	v_pk_fma_f16 v30, v30, v146, v34
	v_pk_fma_f16 v37, v57, v149, v37
	v_pk_fma_f16 v36, v56, v148, v36
	v_pk_fma_f16 v35, v55, v147, v35
	v_pk_fma_f16 v34, v54, v146, v34
	v_pk_maximum3_f16 v79, v19, v31, v35
	v_pk_maximum3_f16 v80, v20, v32, v36
	v_pk_maximum3_f16 v81, v21, v33, v37
	v_pk_fma_f16 v50, v77, v149, v45
	v_pk_maximum3_f16 v78, v18, v30, v34
	v_pk_fma_f16 v51, v76, v148, v44
	v_pk_fma_f16 v52, v75, v147, v43
	v_pk_fma_f16 v53, v74, v146, v42
	v_pk_fma_f16 v54, v101, v149, v45
	v_pk_fma_f16 v55, v100, v148, v44
	v_pk_fma_f16 v56, v99, v147, v43
	v_pk_fma_f16 v57, v98, v146, v42
	v_pk_fma_f16 v45, v117, v149, v45
	v_pk_fma_f16 v44, v116, v148, v44
	v_pk_fma_f16 v43, v115, v147, v43
	v_pk_fma_f16 v42, v114, v146, v42
	v_pk_fma_f16 v66, v133, v149, v49
	v_pk_fma_f16 v67, v132, v148, v48
	v_pk_fma_f16 v68, v131, v147, v47
	v_pk_fma_f16 v69, v130, v146, v46
	v_pk_fma_f16 v74, v137, v149, v49
	v_pk_fma_f16 v75, v136, v148, v48
	v_pk_fma_f16 v76, v135, v147, v47
	v_pk_fma_f16 v77, v134, v146, v46
	v_pk_fma_f16 v49, v145, v149, v49
	v_pk_fma_f16 v48, v144, v148, v48
	v_pk_fma_f16 v47, v143, v147, v47
	v_pk_fma_f16 v46, v142, v146, v46
	v_pk_maximum3_f16 v82, v53, v57, v42
	v_pk_maximum3_f16 v83, v52, v56, v43
	v_pk_maximum3_f16 v84, v51, v55, v44
	v_pk_maximum3_f16 v85, v50, v54, v45
	v_pk_maximum3_f16 v87, v68, v76, v47
	v_pk_maximum3_f16 v86, v69, v77, v46
	v_pk_maximum3_f16 v88, v67, v75, v48
	v_pk_maximum3_f16 v89, v66, v74, v49
	v_pk_maximum3_f16 v78, v78, v82, v86
	v_pk_maximum3_f16 v79, v79, v83, v87
	v_pk_maximum3_f16 v80, v80, v84, v88
	v_pk_maximum3_f16 v81, v81, v85, v89
	s_nop 0
	v_pk_add_f16 v18, v18, v78 neg_lo:[0,1] neg_hi:[0,1]
	v_pk_add_f16 v19, v19, v79 neg_lo:[0,1] neg_hi:[0,1]
	v_pk_add_f16 v20, v20, v80 neg_lo:[0,1] neg_hi:[0,1]
	v_pk_add_f16 v21, v21, v81 neg_lo:[0,1] neg_hi:[0,1]
	v_pk_add_f16 v30, v30, v78 neg_lo:[0,1] neg_hi:[0,1]
	v_exp_f16_sdwa v82, v18 dst_sel:WORD_0 dst_unused:UNUSED_PAD src0_sel:WORD_0
	v_exp_f16_sdwa v83, v19 dst_sel:WORD_0 dst_unused:UNUSED_PAD src0_sel:WORD_0
	v_exp_f16_sdwa v84, v20 dst_sel:WORD_0 dst_unused:UNUSED_PAD src0_sel:WORD_0
	v_exp_f16_sdwa v85, v21 dst_sel:WORD_0 dst_unused:UNUSED_PAD src0_sel:WORD_0
	v_exp_f16_sdwa v82, v18 dst_sel:WORD_1 dst_unused:UNUSED_PRESERVE src0_sel:WORD_1
	v_exp_f16_sdwa v83, v19 dst_sel:WORD_1 dst_unused:UNUSED_PRESERVE src0_sel:WORD_1
	v_exp_f16_sdwa v84, v20 dst_sel:WORD_1 dst_unused:UNUSED_PRESERVE src0_sel:WORD_1
	v_exp_f16_sdwa v85, v21 dst_sel:WORD_1 dst_unused:UNUSED_PRESERVE src0_sel:WORD_1
	v_pk_add_f16 v31, v31, v79 neg_lo:[0,1] neg_hi:[0,1]
	v_pk_add_f16 v18, v82, 0
	v_pk_add_f16 v19, v83, 0
	v_pk_add_f16 v20, v84, 0
	v_pk_add_f16 v21, v85, 0
	v_pk_fma_f16 v6, v6, v82, 0
	v_pk_fma_f16 v7, v7, v83, 0
	v_pk_fma_f16 v8, v8, v84, 0
	v_pk_fma_f16 v9, v9, v85, 0
	v_pk_add_f16 v32, v32, v80 neg_lo:[0,1] neg_hi:[0,1]
	v_pk_add_f16 v33, v33, v81 neg_lo:[0,1] neg_hi:[0,1]
	v_exp_f16_sdwa v82, v30 dst_sel:WORD_0 dst_unused:UNUSED_PAD src0_sel:WORD_0
	v_exp_f16_sdwa v83, v31 dst_sel:WORD_0 dst_unused:UNUSED_PAD src0_sel:WORD_0
	v_exp_f16_sdwa v84, v32 dst_sel:WORD_0 dst_unused:UNUSED_PAD src0_sel:WORD_0
	v_exp_f16_sdwa v85, v33 dst_sel:WORD_0 dst_unused:UNUSED_PAD src0_sel:WORD_0
	v_exp_f16_sdwa v82, v30 dst_sel:WORD_1 dst_unused:UNUSED_PRESERVE src0_sel:WORD_1
	v_exp_f16_sdwa v83, v31 dst_sel:WORD_1 dst_unused:UNUSED_PRESERVE src0_sel:WORD_1
	v_exp_f16_sdwa v84, v32 dst_sel:WORD_1 dst_unused:UNUSED_PRESERVE src0_sel:WORD_1
	v_exp_f16_sdwa v85, v33 dst_sel:WORD_1 dst_unused:UNUSED_PRESERVE src0_sel:WORD_1
	s_nop 0
	v_pk_add_f16 v21, v21, v85
	v_pk_add_f16 v20, v20, v84
	v_pk_add_f16 v19, v19, v83
	v_pk_add_f16 v18, v18, v82
	v_pk_fma_f16 v9, v13, v85, v9
	v_pk_fma_f16 v8, v12, v84, v8
	v_pk_fma_f16 v7, v11, v83, v7
	v_pk_fma_f16 v6, v10, v82, v6
	v_pk_add_f16 v10, v34, v78 neg_lo:[0,1] neg_hi:[0,1]
	v_pk_add_f16 v11, v35, v79 neg_lo:[0,1] neg_hi:[0,1]
	v_pk_add_f16 v12, v36, v80 neg_lo:[0,1] neg_hi:[0,1]
	v_pk_add_f16 v13, v37, v81 neg_lo:[0,1] neg_hi:[0,1]
	v_exp_f16_sdwa v30, v10 dst_sel:WORD_0 dst_unused:UNUSED_PAD src0_sel:WORD_0
	v_exp_f16_sdwa v31, v11 dst_sel:WORD_0 dst_unused:UNUSED_PAD src0_sel:WORD_0
	v_exp_f16_sdwa v32, v12 dst_sel:WORD_0 dst_unused:UNUSED_PAD src0_sel:WORD_0
	v_exp_f16_sdwa v33, v13 dst_sel:WORD_0 dst_unused:UNUSED_PAD src0_sel:WORD_0
	v_exp_f16_sdwa v30, v10 dst_sel:WORD_1 dst_unused:UNUSED_PRESERVE src0_sel:WORD_1
	v_exp_f16_sdwa v31, v11 dst_sel:WORD_1 dst_unused:UNUSED_PRESERVE src0_sel:WORD_1
	v_exp_f16_sdwa v32, v12 dst_sel:WORD_1 dst_unused:UNUSED_PRESERVE src0_sel:WORD_1
	v_exp_f16_sdwa v33, v13 dst_sel:WORD_1 dst_unused:UNUSED_PRESERVE src0_sel:WORD_1
	v_pk_add_f16 v10, v18, v30
	v_pk_add_f16 v11, v19, v31
	v_pk_add_f16 v12, v20, v32
	v_pk_add_f16 v13, v21, v33
	v_pk_fma_f16 v6, v14, v30, v6
	v_pk_fma_f16 v7, v15, v31, v7
	v_pk_fma_f16 v8, v16, v32, v8
	v_pk_fma_f16 v9, v17, v33, v9
	v_pk_add_f16 v14, v53, v78 neg_lo:[0,1] neg_hi:[0,1]
	v_pk_add_f16 v15, v52, v79 neg_lo:[0,1] neg_hi:[0,1]
	v_pk_add_f16 v16, v51, v80 neg_lo:[0,1] neg_hi:[0,1]
	v_pk_add_f16 v17, v50, v81 neg_lo:[0,1] neg_hi:[0,1]
	v_exp_f16_sdwa v18, v14 dst_sel:WORD_0 dst_unused:UNUSED_PAD src0_sel:WORD_0
	v_exp_f16_sdwa v19, v15 dst_sel:WORD_0 dst_unused:UNUSED_PAD src0_sel:WORD_0
	v_exp_f16_sdwa v20, v16 dst_sel:WORD_0 dst_unused:UNUSED_PAD src0_sel:WORD_0
	v_exp_f16_sdwa v21, v17 dst_sel:WORD_0 dst_unused:UNUSED_PAD src0_sel:WORD_0
	v_exp_f16_sdwa v18, v14 dst_sel:WORD_1 dst_unused:UNUSED_PRESERVE src0_sel:WORD_1
	v_exp_f16_sdwa v19, v15 dst_sel:WORD_1 dst_unused:UNUSED_PRESERVE src0_sel:WORD_1
	v_exp_f16_sdwa v20, v16 dst_sel:WORD_1 dst_unused:UNUSED_PRESERVE src0_sel:WORD_1
	v_exp_f16_sdwa v21, v17 dst_sel:WORD_1 dst_unused:UNUSED_PRESERVE src0_sel:WORD_1
	v_pk_add_f16 v14, v57, v78 neg_lo:[0,1] neg_hi:[0,1]
	v_pk_add_f16 v13, v13, v21
	v_pk_add_f16 v12, v12, v20
	v_pk_add_f16 v11, v11, v19
	v_pk_add_f16 v10, v10, v18
	v_pk_fma_f16 v9, v29, v21, v9
	v_pk_fma_f16 v8, v28, v20, v8
	v_pk_fma_f16 v7, v27, v19, v7
	v_pk_fma_f16 v6, v26, v18, v6
	v_pk_add_f16 v15, v56, v79 neg_lo:[0,1] neg_hi:[0,1]
	v_pk_add_f16 v16, v55, v80 neg_lo:[0,1] neg_hi:[0,1]
	v_pk_add_f16 v17, v54, v81 neg_lo:[0,1] neg_hi:[0,1]
	v_exp_f16_sdwa v18, v14 dst_sel:WORD_0 dst_unused:UNUSED_PAD src0_sel:WORD_0
	v_exp_f16_sdwa v19, v15 dst_sel:WORD_0 dst_unused:UNUSED_PAD src0_sel:WORD_0
	v_exp_f16_sdwa v20, v16 dst_sel:WORD_0 dst_unused:UNUSED_PAD src0_sel:WORD_0
	v_exp_f16_sdwa v21, v17 dst_sel:WORD_0 dst_unused:UNUSED_PAD src0_sel:WORD_0
	v_exp_f16_sdwa v18, v14 dst_sel:WORD_1 dst_unused:UNUSED_PRESERVE src0_sel:WORD_1
	v_exp_f16_sdwa v19, v15 dst_sel:WORD_1 dst_unused:UNUSED_PRESERVE src0_sel:WORD_1
	v_exp_f16_sdwa v20, v16 dst_sel:WORD_1 dst_unused:UNUSED_PRESERVE src0_sel:WORD_1
	v_exp_f16_sdwa v21, v17 dst_sel:WORD_1 dst_unused:UNUSED_PRESERVE src0_sel:WORD_1
	v_pk_add_f16 v14, v42, v78 neg_lo:[0,1] neg_hi:[0,1]
	v_pk_add_f16 v10, v10, v18
	v_pk_add_f16 v11, v11, v19
	v_pk_add_f16 v12, v12, v20
	v_pk_add_f16 v13, v13, v21
	v_pk_fma_f16 v6, v38, v18, v6
	v_pk_fma_f16 v7, v39, v19, v7
	v_pk_fma_f16 v8, v40, v20, v8
	v_pk_fma_f16 v9, v41, v21, v9
	v_pk_add_f16 v15, v43, v79 neg_lo:[0,1] neg_hi:[0,1]
	v_pk_add_f16 v16, v44, v80 neg_lo:[0,1] neg_hi:[0,1]
	v_pk_add_f16 v17, v45, v81 neg_lo:[0,1] neg_hi:[0,1]
	v_exp_f16_sdwa v18, v14 dst_sel:WORD_0 dst_unused:UNUSED_PAD src0_sel:WORD_0
	v_exp_f16_sdwa v19, v15 dst_sel:WORD_0 dst_unused:UNUSED_PAD src0_sel:WORD_0
	v_exp_f16_sdwa v20, v16 dst_sel:WORD_0 dst_unused:UNUSED_PAD src0_sel:WORD_0
	v_exp_f16_sdwa v21, v17 dst_sel:WORD_0 dst_unused:UNUSED_PAD src0_sel:WORD_0
	v_exp_f16_sdwa v18, v14 dst_sel:WORD_1 dst_unused:UNUSED_PRESERVE src0_sel:WORD_1
	v_exp_f16_sdwa v19, v15 dst_sel:WORD_1 dst_unused:UNUSED_PRESERVE src0_sel:WORD_1
	v_exp_f16_sdwa v20, v16 dst_sel:WORD_1 dst_unused:UNUSED_PRESERVE src0_sel:WORD_1
	v_exp_f16_sdwa v21, v17 dst_sel:WORD_1 dst_unused:UNUSED_PRESERVE src0_sel:WORD_1
	v_pk_add_f16 v14, v69, v78 neg_lo:[0,1] neg_hi:[0,1]
	v_pk_add_f16 v13, v13, v21
	v_pk_add_f16 v12, v12, v20
	v_pk_add_f16 v11, v11, v19
	v_pk_add_f16 v10, v10, v18
	v_pk_fma_f16 v9, v61, v21, v9
	v_pk_fma_f16 v8, v60, v20, v8
	v_pk_fma_f16 v7, v59, v19, v7
	v_pk_fma_f16 v6, v58, v18, v6
	v_pk_add_f16 v15, v68, v79 neg_lo:[0,1] neg_hi:[0,1]
	v_pk_add_f16 v16, v67, v80 neg_lo:[0,1] neg_hi:[0,1]
	v_pk_add_f16 v17, v66, v81 neg_lo:[0,1] neg_hi:[0,1]
	v_exp_f16_sdwa v18, v14 dst_sel:WORD_0 dst_unused:UNUSED_PAD src0_sel:WORD_0
	v_exp_f16_sdwa v19, v15 dst_sel:WORD_0 dst_unused:UNUSED_PAD src0_sel:WORD_0
	v_exp_f16_sdwa v20, v16 dst_sel:WORD_0 dst_unused:UNUSED_PAD src0_sel:WORD_0
	v_exp_f16_sdwa v21, v17 dst_sel:WORD_0 dst_unused:UNUSED_PAD src0_sel:WORD_0
	v_exp_f16_sdwa v18, v14 dst_sel:WORD_1 dst_unused:UNUSED_PRESERVE src0_sel:WORD_1
	v_exp_f16_sdwa v19, v15 dst_sel:WORD_1 dst_unused:UNUSED_PRESERVE src0_sel:WORD_1
	v_exp_f16_sdwa v20, v16 dst_sel:WORD_1 dst_unused:UNUSED_PRESERVE src0_sel:WORD_1
	v_exp_f16_sdwa v21, v17 dst_sel:WORD_1 dst_unused:UNUSED_PRESERVE src0_sel:WORD_1
	v_pk_add_f16 v10, v10, v18
	v_pk_add_f16 v11, v11, v19
	v_pk_add_f16 v12, v12, v20
	v_pk_add_f16 v13, v13, v21
	v_pk_fma_f16 v14, v70, v18, v6
	v_pk_fma_f16 v15, v71, v19, v7
	v_pk_fma_f16 v16, v72, v20, v8
	v_pk_fma_f16 v17, v73, v21, v9
	v_pk_add_f16 v6, v77, v78 neg_lo:[0,1] neg_hi:[0,1]
	v_pk_add_f16 v7, v76, v79 neg_lo:[0,1] neg_hi:[0,1]
	v_pk_add_f16 v8, v75, v80 neg_lo:[0,1] neg_hi:[0,1]
	v_pk_add_f16 v9, v74, v81 neg_lo:[0,1] neg_hi:[0,1]
	v_exp_f16_sdwa v18, v6 dst_sel:WORD_0 dst_unused:UNUSED_PAD src0_sel:WORD_0
	v_exp_f16_sdwa v19, v7 dst_sel:WORD_0 dst_unused:UNUSED_PAD src0_sel:WORD_0
	v_exp_f16_sdwa v20, v8 dst_sel:WORD_0 dst_unused:UNUSED_PAD src0_sel:WORD_0
	v_exp_f16_sdwa v21, v9 dst_sel:WORD_0 dst_unused:UNUSED_PAD src0_sel:WORD_0
	v_exp_f16_sdwa v18, v6 dst_sel:WORD_1 dst_unused:UNUSED_PRESERVE src0_sel:WORD_1
	v_exp_f16_sdwa v19, v7 dst_sel:WORD_1 dst_unused:UNUSED_PRESERVE src0_sel:WORD_1
	v_exp_f16_sdwa v20, v8 dst_sel:WORD_1 dst_unused:UNUSED_PRESERVE src0_sel:WORD_1
	v_exp_f16_sdwa v21, v9 dst_sel:WORD_1 dst_unused:UNUSED_PRESERVE src0_sel:WORD_1
	s_nop 0
	v_pk_add_f16 v9, v13, v21
	v_pk_add_f16 v8, v12, v20
	v_pk_add_f16 v7, v11, v19
	v_pk_add_f16 v6, v10, v18
	v_pk_fma_f16 v13, v93, v21, v17
	v_pk_fma_f16 v12, v92, v20, v16
	v_pk_fma_f16 v11, v91, v19, v15
	v_pk_fma_f16 v10, v90, v18, v14
	v_pk_add_f16 v18, v46, v78 neg_lo:[0,1] neg_hi:[0,1]
	v_pk_add_f16 v19, v47, v79 neg_lo:[0,1] neg_hi:[0,1]
	v_pk_add_f16 v20, v48, v80 neg_lo:[0,1] neg_hi:[0,1]
	v_pk_add_f16 v21, v49, v81 neg_lo:[0,1] neg_hi:[0,1]
	v_exp_f16_sdwa v14, v18 dst_sel:WORD_0 dst_unused:UNUSED_PAD src0_sel:WORD_0
	v_exp_f16_sdwa v17, v19 dst_sel:WORD_0 dst_unused:UNUSED_PAD src0_sel:WORD_0
	v_exp_f16_sdwa v15, v20 dst_sel:WORD_0 dst_unused:UNUSED_PAD src0_sel:WORD_0
	v_exp_f16_sdwa v16, v21 dst_sel:WORD_0 dst_unused:UNUSED_PAD src0_sel:WORD_0
	v_exp_f16_sdwa v14, v18 dst_sel:WORD_1 dst_unused:UNUSED_PRESERVE src0_sel:WORD_1
	v_exp_f16_sdwa v17, v19 dst_sel:WORD_1 dst_unused:UNUSED_PRESERVE src0_sel:WORD_1
	v_exp_f16_sdwa v15, v20 dst_sel:WORD_1 dst_unused:UNUSED_PRESERVE src0_sel:WORD_1
	v_exp_f16_sdwa v16, v21 dst_sel:WORD_1 dst_unused:UNUSED_PRESERVE src0_sel:WORD_1
	s_nop 0

.LBB3_7:
	v_add_u32_e32 v182, s33, v161
	v_add_u32_e32 v181, -1, v182
	v_or_b32_e32 v2, v181, v164
	v_add_u32_e32 v180, 0x18400, v171
	v_cmp_gt_u32_e64 s[0:1], 64, v2
	s_mov_b64 s[4:5], -1
	s_and_b64 vcc, exec, s[24:25]
	s_cbranch_vccz .LBB3_45
	s_load_dwordx2 s[4:5], s[22:23], 0x20
	s_waitcnt lgkmcnt(0)
	s_load_dwordx2 s[26:27], s[4:5], 0x0
	s_load_dword s34, s[4:5], 0x8
	v_cmp_lt_u32_e64 s[64:65], 0, v182
	v_cmp_gt_u32_e64 s[66:67], 63, v182
	v_cmp_lt_u32_e64 s[68:69], 0, v162
	v_cmp_gt_u32_e64 s[70:71], 60, v162
	buffer_load_dwordx4 v[186:189], v180, s[16:19], 0 offen
	s_and_b64 s[72:73], s[68:69], s[64:65]
	s_and_b64 s[74:75], s[68:69], s[66:67]
	s_and_b64 s[76:77], s[70:71], s[64:65]
	s_and_b64 s[78:79], s[70:71], s[66:67]
	v_add_u32_e32 v249, 0xfffe7c00, v180
	v_add_u32_e32 v250, 0xfffe8000, v180
	s_mov_b64 exec, s[72:73]
	buffer_load_dwordx4 v[110:113], v249, s[16:19], 0 offen
	s_mov_b64 exec, -1
	s_mov_b64 exec, s[68:69]
	buffer_load_dwordx4 v[126:129], v250, s[16:19], 0 offen offset:512
	s_mov_b64 exec, -1
	s_mov_b64 exec, s[74:75]
	buffer_load_dwordx4 v[134:137], v250, s[16:19], 0 offen offset:2048
	s_mov_b64 exec, -1
	v_add_u32_e32 v249, 0xfffffc00, v180
	s_mov_b64 exec, s[64:65]
	buffer_load_dwordx4 v[82:85], v249, s[16:19], 0 offen
	s_mov_b64 exec, -1
	buffer_load_dwordx4 v[106:109], v180, s[16:19], 0 offen offset:512
	s_mov_b64 exec, s[66:67]
	buffer_load_dwordx4 v[122:125], v180, s[16:19], 0 offen offset:2048
	s_mov_b64 exec, -1
	v_add_u32_e32 v249, 0x17c00, v180
	v_add_u32_e32 v250, 0x18000, v180
	s_mov_b64 exec, s[64:65]
	buffer_load_dwordx4 v[50:53], v249, s[16:19], 0 offen
	s_mov_b64 exec, -1
	buffer_load_dwordx4 v[66:69], v250, s[16:19], 0 offen offset:512
	s_mov_b64 exec, s[66:67]
	buffer_load_dwordx4 v[94:97], v250, s[16:19], 0 offen offset:2048
	s_mov_b64 exec, -1
	v_add_u32_e32 v249, 0xfffe7c00, v180
	v_add_u32_e32 v250, 0xfffe8000, v180
	s_mov_b64 exec, s[72:73]
	buffer_load_dwordx4 v[70:73], v249, s[16:19], 0 offen offset:512
	s_mov_b64 exec, -1
	s_mov_b64 exec, s[68:69]
	buffer_load_dwordx4 v[98:101], v250, s[16:19], 0 offen offset:1024
	s_mov_b64 exec, -1
	s_mov_b64 exec, s[74:75]
	buffer_load_dwordx4 v[114:117], v250, s[16:19], 0 offen offset:2560
	s_mov_b64 exec, -1
	v_add_u32_e32 v249, 0xfffffc00, v180
	s_mov_b64 exec, s[64:65]
	buffer_load_dwordx4 v[42:45], v249, s[16:19], 0 offen offset:512
	s_mov_b64 exec, -1
	buffer_load_dwordx4 v[62:65], v180, s[16:19], 0 offen offset:1024
	s_mov_b64 exec, s[66:67]
	buffer_load_dwordx4 v[86:89], v180, s[16:19], 0 offen offset:2560
	s_mov_b64 exec, -1
	v_add_u32_e32 v249, 0x17c00, v180
	v_add_u32_e32 v250, 0x18000, v180
	s_mov_b64 exec, s[64:65]
	buffer_load_dwordx4 v[22:25], v249, s[16:19], 0 offen offset:512
	s_mov_b64 exec, -1
	buffer_load_dwordx4 v[30:33], v250, s[16:19], 0 offen offset:1024
	s_mov_b64 exec, s[66:67]
	buffer_load_dwordx4 v[46:49], v250, s[16:19], 0 offen offset:2560
	s_mov_b64 exec, -1
	v_add_u32_e32 v249, 0x18000, v180
	buffer_load_dwordx4 v[154:157], v249, s[16:19], 0 offen
	v_add_u32_e32 v250, 0x30000, v180
	buffer_load_dwordx4 v[150:153], v250, s[16:19], 0 offen
	v_add_u32_e32 v249, 0x48000, v180
	buffer_load_dwordx4 v[146:149], v249, s[16:19], 0 offen
	v_add_u32_e32 v249, 0x2fc00, v180
	v_add_u32_e32 v250, 0x30000, v180
	v_add_u32_e32 v251, 0x47c00, v180
	v_add_u32_e32 v252, 0x48000, v180
	v_add_u32_e32 v253, 0x5fc00, v180
	v_add_u32_e32 v254, 0x60000, v180
	s_cmp_lg_u32 s93, 0
	s_cbranch_scc1 .Lmybg_B1
	s_waitcnt vmcnt(22)
	v_cvt_pk_f16_f32 v172, v230, v231
	v_cvt_pk_f16_f32 v173, v234, v235
	v_cvt_pk_f16_f32 v174, v232, v233
	v_cvt_pk_f16_f32 v175, v236, v237
	v_cvt_pk_f16_f32 v176, v238, v239
	v_cvt_pk_f16_f32 v177, v242, v243
	v_cvt_pk_f16_f32 v178, v240, v241
	v_cvt_pk_f16_f32 v179, v244, v245
	s_mov_b32 s93, 1

.Lmyf_B1_7:
	s_mov_b64 exec, -1
	s_waitcnt lgkmcnt(0)
	v_cvt_f16_f32_e32 v183, s27
	v_cvt_f16_f32_e32 v185, s26
	v_cvt_f16_f32_e32 v184, s34
	s_mov_b64 s[4:5], 0
	s_waitcnt vmcnt(12)
	v_pk_mul_f16 v193, v185, v189 op_sel_hi:[0,1]
	v_pk_mul_f16 v197, v183, v189 op_sel_hi:[0,1]
	v_pk_mul_f16 v201, v184, v189 op_sel_hi:[0,1]
	v_pk_mul_f16 v190, v185, v186 op_sel_hi:[0,1]
	v_pk_mul_f16 v191, v185, v187 op_sel_hi:[0,1]
	v_pk_mul_f16 v192, v185, v188 op_sel_hi:[0,1]
	v_pk_mul_f16 v194, v183, v186 op_sel_hi:[0,1]
	v_pk_mul_f16 v195, v183, v187 op_sel_hi:[0,1]
	v_pk_mul_f16 v196, v183, v188 op_sel_hi:[0,1]
	v_pk_mul_f16 v198, v184, v186 op_sel_hi:[0,1]
	v_pk_mul_f16 v199, v184, v187 op_sel_hi:[0,1]
	v_pk_mul_f16 v200, v184, v188 op_sel_hi:[0,1]
	v_pk_fma_f16 v113, v113, v189, v193
	v_pk_fma_f16 v129, v129, v189, v197
	v_pk_fma_f16 v137, v137, v189, v201
	v_pk_fma_f16 v202, v85, v189, v193
	v_pk_fma_f16 v206, v109, v189, v197
	v_pk_fma_f16 v210, v125, v189, v201
	v_pk_fma_f16 v193, v53, v189, v193
	v_pk_fma_f16 v197, v69, v189, v197
	v_pk_fma_f16 v189, v97, v189, v201
	v_pk_maximum3_f16 v201, v113, v129, v137
	v_pk_fma_f16 v112, v112, v188, v192
	v_pk_fma_f16 v111, v111, v187, v191
	v_pk_fma_f16 v110, v110, v186, v190
	v_pk_fma_f16 v128, v128, v188, v196
	v_pk_fma_f16 v127, v127, v187, v195
	v_pk_fma_f16 v126, v126, v186, v194
	v_pk_fma_f16 v136, v136, v188, v200
	v_pk_fma_f16 v135, v135, v187, v199
	v_pk_fma_f16 v134, v134, v186, v198
	v_pk_fma_f16 v203, v84, v188, v192
	v_pk_fma_f16 v204, v83, v187, v191
	v_pk_fma_f16 v205, v82, v186, v190
	v_pk_fma_f16 v207, v108, v188, v196
	v_pk_fma_f16 v208, v107, v187, v195
	v_pk_fma_f16 v209, v106, v186, v194
	v_pk_fma_f16 v211, v124, v188, v200
	v_pk_fma_f16 v212, v123, v187, v199
	v_pk_fma_f16 v213, v122, v186, v198
	v_pk_fma_f16 v192, v52, v188, v192
	v_pk_fma_f16 v191, v51, v187, v191
	v_pk_fma_f16 v190, v50, v186, v190
	v_pk_fma_f16 v196, v68, v188, v196
	v_pk_fma_f16 v195, v67, v187, v195
	v_pk_fma_f16 v194, v66, v186, v194
	v_pk_fma_f16 v188, v96, v188, v200
	v_pk_fma_f16 v187, v95, v187, v199
	v_pk_fma_f16 v186, v94, v186, v198
	v_pk_maximum3_f16 v198, v110, v126, v134
	v_pk_maximum3_f16 v199, v111, v127, v135
	v_pk_maximum3_f16 v200, v112, v128, v136
	v_pk_maximum3_f16 v217, v202, v206, v210
	v_pk_maximum3_f16 v221, v193, v197, v189
	v_pk_maximum3_f16 v214, v205, v209, v213
	v_pk_maximum3_f16 v215, v204, v208, v212
	v_pk_maximum3_f16 v216, v203, v207, v211
	v_pk_maximum3_f16 v218, v190, v194, v186
	v_pk_maximum3_f16 v219, v191, v195, v187
	v_pk_maximum3_f16 v201, v201, v217, v221
	v_pk_maximum3_f16 v220, v192, v196, v188
	v_pk_maximum3_f16 v198, v198, v214, v218
	v_pk_maximum3_f16 v199, v199, v215, v219
	v_pk_maximum3_f16 v200, v200, v216, v220
	v_pk_add_f16 v113, v113, v201 neg_lo:[0,1] neg_hi:[0,1]
	v_pk_add_f16 v110, v110, v198 neg_lo:[0,1] neg_hi:[0,1]
	v_pk_add_f16 v111, v111, v199 neg_lo:[0,1] neg_hi:[0,1]
	v_pk_add_f16 v112, v112, v200 neg_lo:[0,1] neg_hi:[0,1]
	v_pk_add_f16 v126, v126, v198 neg_lo:[0,1] neg_hi:[0,1]
	v_exp_f16_sdwa v214, v110 dst_sel:WORD_0 dst_unused:UNUSED_PAD src0_sel:WORD_0
	v_exp_f16_sdwa v215, v111 dst_sel:WORD_0 dst_unused:UNUSED_PAD src0_sel:WORD_0
	v_exp_f16_sdwa v216, v112 dst_sel:WORD_0 dst_unused:UNUSED_PAD src0_sel:WORD_0
	v_exp_f16_sdwa v217, v113 dst_sel:WORD_0 dst_unused:UNUSED_PAD src0_sel:WORD_0
	v_exp_f16_sdwa v214, v110 dst_sel:WORD_1 dst_unused:UNUSED_PRESERVE src0_sel:WORD_1
	v_exp_f16_sdwa v215, v111 dst_sel:WORD_1 dst_unused:UNUSED_PRESERVE src0_sel:WORD_1
	v_exp_f16_sdwa v216, v112 dst_sel:WORD_1 dst_unused:UNUSED_PRESERVE src0_sel:WORD_1
	v_exp_f16_sdwa v217, v113 dst_sel:WORD_1 dst_unused:UNUSED_PRESERVE src0_sel:WORD_1
	v_pk_add_f16 v127, v127, v199 neg_lo:[0,1] neg_hi:[0,1]
	v_pk_add_f16 v113, v214, 0
	s_waitcnt vmcnt(3)
	v_pk_fma_f16 v73, v73, v217, 0
	v_pk_add_f16 v110, v217, 0
	v_pk_add_f16 v111, v216, 0
	v_pk_add_f16 v112, v215, 0
	v_pk_fma_f16 v72, v72, v216, 0
	v_pk_fma_f16 v71, v71, v215, 0
	s_mov_b64 exec, s[64:65]
	buffer_load_dwordx4 v[18:21], v249, s[16:19], 0 offen
	buffer_load_dwordx4 v[6:9], v249, s[16:19], 0 offen offset:512
	s_mov_b64 exec, -1
	v_pk_fma_f16 v70, v70, v214, 0
	v_pk_add_f16 v128, v128, v200 neg_lo:[0,1] neg_hi:[0,1]
	v_pk_add_f16 v129, v129, v201 neg_lo:[0,1] neg_hi:[0,1]
	v_exp_f16_sdwa v214, v126 dst_sel:WORD_0 dst_unused:UNUSED_PAD src0_sel:WORD_0
	v_exp_f16_sdwa v215, v127 dst_sel:WORD_0 dst_unused:UNUSED_PAD src0_sel:WORD_0
	v_exp_f16_sdwa v216, v128 dst_sel:WORD_0 dst_unused:UNUSED_PAD src0_sel:WORD_0
	v_exp_f16_sdwa v217, v129 dst_sel:WORD_0 dst_unused:UNUSED_PAD src0_sel:WORD_0
	v_exp_f16_sdwa v214, v126 dst_sel:WORD_1 dst_unused:UNUSED_PRESERVE src0_sel:WORD_1
	v_exp_f16_sdwa v215, v127 dst_sel:WORD_1 dst_unused:UNUSED_PRESERVE src0_sel:WORD_1
	v_exp_f16_sdwa v216, v128 dst_sel:WORD_1 dst_unused:UNUSED_PRESERVE src0_sel:WORD_1
	v_exp_f16_sdwa v217, v129 dst_sel:WORD_1 dst_unused:UNUSED_PRESERVE src0_sel:WORD_1
	v_pk_add_f16 v113, v113, v214
	v_pk_fma_f16 v73, v101, v217, v73
	v_pk_add_f16 v101, v137, v201 neg_lo:[0,1] neg_hi:[0,1]
	v_pk_add_f16 v112, v112, v215
	v_pk_add_f16 v111, v111, v216
	v_pk_add_f16 v110, v110, v217
	buffer_load_dwordx4 v[34:37], v250, s[16:19], 0 offen offset:512
	buffer_load_dwordx4 v[10:13], v250, s[16:19], 0 offen offset:1024
	v_pk_fma_f16 v70, v98, v214, v70
	v_pk_fma_f16 v71, v99, v215, v71
	v_pk_fma_f16 v72, v100, v216, v72
	v_pk_add_f16 v98, v134, v198 neg_lo:[0,1] neg_hi:[0,1]
	v_pk_add_f16 v99, v135, v199 neg_lo:[0,1] neg_hi:[0,1]
	v_pk_add_f16 v100, v136, v200 neg_lo:[0,1] neg_hi:[0,1]
	v_exp_f16_sdwa v126, v98 dst_sel:WORD_0 dst_unused:UNUSED_PAD src0_sel:WORD_0
	v_exp_f16_sdwa v127, v99 dst_sel:WORD_0 dst_unused:UNUSED_PAD src0_sel:WORD_0
	v_exp_f16_sdwa v128, v100 dst_sel:WORD_0 dst_unused:UNUSED_PAD src0_sel:WORD_0
	v_exp_f16_sdwa v129, v101 dst_sel:WORD_0 dst_unused:UNUSED_PAD src0_sel:WORD_0
	v_exp_f16_sdwa v126, v98 dst_sel:WORD_1 dst_unused:UNUSED_PRESERVE src0_sel:WORD_1
	v_exp_f16_sdwa v127, v99 dst_sel:WORD_1 dst_unused:UNUSED_PRESERVE src0_sel:WORD_1
	v_exp_f16_sdwa v128, v100 dst_sel:WORD_1 dst_unused:UNUSED_PRESERVE src0_sel:WORD_1
	v_exp_f16_sdwa v129, v101 dst_sel:WORD_1 dst_unused:UNUSED_PRESERVE src0_sel:WORD_1
	v_pk_add_f16 v101, v113, v126
	v_pk_add_f16 v98, v110, v129
	v_pk_add_f16 v99, v111, v128
	s_mov_b64 exec, s[66:67]
	buffer_load_dwordx4 v[54:57], v250, s[16:19], 0 offen offset:2048
	buffer_load_dwordx4 v[14:17], v250, s[16:19], 0 offen offset:2560
	s_mov_b64 exec, -1
	v_pk_add_f16 v100, v112, v127
	v_pk_fma_f16 v73, v117, v129, v73
	v_pk_fma_f16 v72, v116, v128, v72
	v_pk_fma_f16 v71, v115, v127, v71
	v_pk_fma_f16 v70, v114, v126, v70
	v_pk_add_f16 v110, v205, v198 neg_lo:[0,1] neg_hi:[0,1]
	v_pk_add_f16 v111, v204, v199 neg_lo:[0,1] neg_hi:[0,1]
	v_pk_add_f16 v112, v203, v200 neg_lo:[0,1] neg_hi:[0,1]
	s_mov_b64 exec, s[64:65]
	buffer_load_dwordx4 v[74:77], v251, s[16:19], 0 offen
	buffer_load_dwordx4 v[26:29], v251, s[16:19], 0 offen offset:512
	s_mov_b64 exec, -1
	v_pk_add_f16 v113, v202, v201 neg_lo:[0,1] neg_hi:[0,1]
	v_exp_f16_sdwa v114, v110 dst_sel:WORD_0 dst_unused:UNUSED_PAD src0_sel:WORD_0
	v_exp_f16_sdwa v115, v111 dst_sel:WORD_0 dst_unused:UNUSED_PAD src0_sel:WORD_0
	v_exp_f16_sdwa v116, v112 dst_sel:WORD_0 dst_unused:UNUSED_PAD src0_sel:WORD_0
	v_exp_f16_sdwa v117, v113 dst_sel:WORD_0 dst_unused:UNUSED_PAD src0_sel:WORD_0
	v_exp_f16_sdwa v114, v110 dst_sel:WORD_1 dst_unused:UNUSED_PRESERVE src0_sel:WORD_1
	v_exp_f16_sdwa v115, v111 dst_sel:WORD_1 dst_unused:UNUSED_PRESERVE src0_sel:WORD_1
	v_exp_f16_sdwa v116, v112 dst_sel:WORD_1 dst_unused:UNUSED_PRESERVE src0_sel:WORD_1
	v_exp_f16_sdwa v117, v113 dst_sel:WORD_1 dst_unused:UNUSED_PRESERVE src0_sel:WORD_1
	v_pk_add_f16 v110, v209, v198 neg_lo:[0,1] neg_hi:[0,1]
	v_pk_add_f16 v101, v101, v114
	v_pk_add_f16 v100, v100, v115
	v_pk_add_f16 v99, v99, v116
	v_pk_add_f16 v98, v98, v117
	v_pk_fma_f16 v70, v42, v114, v70
	v_pk_fma_f16 v71, v43, v115, v71
	v_pk_fma_f16 v72, v44, v116, v72
	v_pk_fma_f16 v73, v45, v117, v73
	buffer_load_dwordx4 v[102:105], v252, s[16:19], 0 offen offset:512
	buffer_load_dwordx4 v[38:41], v252, s[16:19], 0 offen offset:1024
	v_pk_add_f16 v111, v208, v199 neg_lo:[0,1] neg_hi:[0,1]
	v_pk_add_f16 v112, v207, v200 neg_lo:[0,1] neg_hi:[0,1]
	v_pk_add_f16 v113, v206, v201 neg_lo:[0,1] neg_hi:[0,1]
	v_exp_f16_sdwa v114, v110 dst_sel:WORD_0 dst_unused:UNUSED_PAD src0_sel:WORD_0
	v_exp_f16_sdwa v115, v111 dst_sel:WORD_0 dst_unused:UNUSED_PAD src0_sel:WORD_0
	v_exp_f16_sdwa v116, v112 dst_sel:WORD_0 dst_unused:UNUSED_PAD src0_sel:WORD_0
	v_exp_f16_sdwa v117, v113 dst_sel:WORD_0 dst_unused:UNUSED_PAD src0_sel:WORD_0
	v_exp_f16_sdwa v114, v110 dst_sel:WORD_1 dst_unused:UNUSED_PRESERVE src0_sel:WORD_1
	v_exp_f16_sdwa v115, v111 dst_sel:WORD_1 dst_unused:UNUSED_PRESERVE src0_sel:WORD_1
	v_exp_f16_sdwa v116, v112 dst_sel:WORD_1 dst_unused:UNUSED_PRESERVE src0_sel:WORD_1
	v_exp_f16_sdwa v117, v113 dst_sel:WORD_1 dst_unused:UNUSED_PRESERVE src0_sel:WORD_1
	v_pk_add_f16 v110, v213, v198 neg_lo:[0,1] neg_hi:[0,1]
	v_pk_add_f16 v101, v101, v114
	v_pk_add_f16 v98, v98, v117
	v_pk_add_f16 v99, v99, v116
	v_pk_add_f16 v100, v100, v115
	v_pk_fma_f16 v73, v65, v117, v73
	s_mov_b64 exec, s[66:67]
	buffer_load_dwordx4 v[118:121], v252, s[16:19], 0 offen offset:2048
	buffer_load_dwordx4 v[58:61], v252, s[16:19], 0 offen offset:2560
	s_mov_b64 exec, -1
	v_pk_fma_f16 v72, v64, v116, v72
	v_pk_fma_f16 v71, v63, v115, v71
	v_pk_fma_f16 v70, v62, v114, v70
	v_pk_add_f16 v111, v212, v199 neg_lo:[0,1] neg_hi:[0,1]
	v_pk_add_f16 v112, v211, v200 neg_lo:[0,1] neg_hi:[0,1]
	v_pk_add_f16 v113, v210, v201 neg_lo:[0,1] neg_hi:[0,1]
	v_exp_f16_sdwa v114, v110 dst_sel:WORD_0 dst_unused:UNUSED_PAD src0_sel:WORD_0
	v_exp_f16_sdwa v115, v111 dst_sel:WORD_0 dst_unused:UNUSED_PAD src0_sel:WORD_0
	v_exp_f16_sdwa v116, v112 dst_sel:WORD_0 dst_unused:UNUSED_PAD src0_sel:WORD_0
	v_exp_f16_sdwa v117, v113 dst_sel:WORD_0 dst_unused:UNUSED_PAD src0_sel:WORD_0
	v_exp_f16_sdwa v114, v110 dst_sel:WORD_1 dst_unused:UNUSED_PRESERVE src0_sel:WORD_1
	v_exp_f16_sdwa v115, v111 dst_sel:WORD_1 dst_unused:UNUSED_PRESERVE src0_sel:WORD_1
	v_exp_f16_sdwa v116, v112 dst_sel:WORD_1 dst_unused:UNUSED_PRESERVE src0_sel:WORD_1
	v_exp_f16_sdwa v117, v113 dst_sel:WORD_1 dst_unused:UNUSED_PRESERVE src0_sel:WORD_1
	v_pk_add_f16 v110, v190, v198 neg_lo:[0,1] neg_hi:[0,1]
	v_pk_add_f16 v101, v101, v114
	v_pk_add_f16 v100, v100, v115
	s_mov_b64 exec, s[76:77]
	buffer_load_dwordx4 v[130:133], v253, s[16:19], 0 offen
	buffer_load_dwordx4 v[78:81], v253, s[16:19], 0 offen offset:512
	s_mov_b64 exec, -1
	v_pk_add_f16 v99, v99, v116
	v_pk_add_f16 v98, v98, v117
	v_pk_fma_f16 v70, v86, v114, v70
	v_pk_fma_f16 v71, v87, v115, v71
	v_pk_fma_f16 v72, v88, v116, v72
	v_pk_fma_f16 v73, v89, v117, v73
	v_pk_add_f16 v111, v191, v199 neg_lo:[0,1] neg_hi:[0,1]
	v_pk_add_f16 v112, v192, v200 neg_lo:[0,1] neg_hi:[0,1]
	s_mov_b64 exec, s[70:71]
	buffer_load_dwordx4 v[138:141], v254, s[16:19], 0 offen offset:512
	buffer_load_dwordx4 v[90:93], v254, s[16:19], 0 offen offset:1024
	s_mov_b64 exec, -1
	v_pk_add_f16 v113, v193, v201 neg_lo:[0,1] neg_hi:[0,1]
	v_exp_f16_sdwa v114, v110 dst_sel:WORD_0 dst_unused:UNUSED_PAD src0_sel:WORD_0
	v_exp_f16_sdwa v115, v111 dst_sel:WORD_0 dst_unused:UNUSED_PAD src0_sel:WORD_0
	v_exp_f16_sdwa v116, v112 dst_sel:WORD_0 dst_unused:UNUSED_PAD src0_sel:WORD_0
	v_exp_f16_sdwa v117, v113 dst_sel:WORD_0 dst_unused:UNUSED_PAD src0_sel:WORD_0
	v_exp_f16_sdwa v114, v110 dst_sel:WORD_1 dst_unused:UNUSED_PRESERVE src0_sel:WORD_1
	v_exp_f16_sdwa v115, v111 dst_sel:WORD_1 dst_unused:UNUSED_PRESERVE src0_sel:WORD_1
	v_exp_f16_sdwa v116, v112 dst_sel:WORD_1 dst_unused:UNUSED_PRESERVE src0_sel:WORD_1
	v_exp_f16_sdwa v117, v113 dst_sel:WORD_1 dst_unused:UNUSED_PRESERVE src0_sel:WORD_1
	v_pk_add_f16 v110, v194, v198 neg_lo:[0,1] neg_hi:[0,1]
	v_pk_add_f16 v101, v101, v114
	v_pk_add_f16 v98, v98, v117
	v_pk_add_f16 v99, v99, v116
	v_pk_add_f16 v100, v100, v115
	v_pk_fma_f16 v73, v25, v117, v73
	v_pk_fma_f16 v72, v24, v116, v72
	v_pk_fma_f16 v71, v23, v115, v71
	s_mov_b64 exec, s[78:79]
	buffer_load_dwordx4 v[142:145], v254, s[16:19], 0 offen offset:2048
	buffer_load_dwordx4 v[2:5], v254, s[16:19], 0 offen offset:2560
	s_mov_b64 exec, -1
	v_pk_fma_f16 v70, v22, v114, v70
	v_pk_add_f16 v111, v195, v199 neg_lo:[0,1] neg_hi:[0,1]
	v_pk_add_f16 v112, v196, v200 neg_lo:[0,1] neg_hi:[0,1]
	v_pk_add_f16 v113, v197, v201 neg_lo:[0,1] neg_hi:[0,1]
	v_exp_f16_sdwa v114, v110 dst_sel:WORD_0 dst_unused:UNUSED_PAD src0_sel:WORD_0
	v_exp_f16_sdwa v115, v111 dst_sel:WORD_0 dst_unused:UNUSED_PAD src0_sel:WORD_0
	v_exp_f16_sdwa v116, v112 dst_sel:WORD_0 dst_unused:UNUSED_PAD src0_sel:WORD_0
	v_exp_f16_sdwa v117, v113 dst_sel:WORD_0 dst_unused:UNUSED_PAD src0_sel:WORD_0
	v_exp_f16_sdwa v114, v110 dst_sel:WORD_1 dst_unused:UNUSED_PRESERVE src0_sel:WORD_1
	v_exp_f16_sdwa v115, v111 dst_sel:WORD_1 dst_unused:UNUSED_PRESERVE src0_sel:WORD_1
	v_exp_f16_sdwa v116, v112 dst_sel:WORD_1 dst_unused:UNUSED_PRESERVE src0_sel:WORD_1
	v_exp_f16_sdwa v117, v113 dst_sel:WORD_1 dst_unused:UNUSED_PRESERVE src0_sel:WORD_1
	v_pk_add_f16 v110, v186, v198 neg_lo:[0,1] neg_hi:[0,1]
	v_pk_add_f16 v101, v101, v114
	v_pk_add_f16 v100, v100, v115
	v_pk_add_f16 v99, v99, v116
	v_pk_add_f16 v98, v98, v117
	v_pk_fma_f16 v70, v30, v114, v70
	v_pk_fma_f16 v71, v31, v115, v71
	v_pk_fma_f16 v72, v32, v116, v72
	v_pk_fma_f16 v73, v33, v117, v73
	v_pk_add_f16 v111, v187, v199 neg_lo:[0,1] neg_hi:[0,1]
	v_pk_add_f16 v112, v188, v200 neg_lo:[0,1] neg_hi:[0,1]
	v_pk_add_f16 v113, v189, v201 neg_lo:[0,1] neg_hi:[0,1]
	v_exp_f16_sdwa v114, v110 dst_sel:WORD_0 dst_unused:UNUSED_PAD src0_sel:WORD_0
	v_exp_f16_sdwa v115, v111 dst_sel:WORD_0 dst_unused:UNUSED_PAD src0_sel:WORD_0
	v_exp_f16_sdwa v116, v112 dst_sel:WORD_0 dst_unused:UNUSED_PAD src0_sel:WORD_0
	v_exp_f16_sdwa v117, v113 dst_sel:WORD_0 dst_unused:UNUSED_PAD src0_sel:WORD_0
	v_exp_f16_sdwa v114, v110 dst_sel:WORD_1 dst_unused:UNUSED_PRESERVE src0_sel:WORD_1
	v_exp_f16_sdwa v115, v111 dst_sel:WORD_1 dst_unused:UNUSED_PRESERVE src0_sel:WORD_1
	v_exp_f16_sdwa v116, v112 dst_sel:WORD_1 dst_unused:UNUSED_PRESERVE src0_sel:WORD_1
	v_exp_f16_sdwa v117, v113 dst_sel:WORD_1 dst_unused:UNUSED_PRESERVE src0_sel:WORD_1
	v_pk_add_f16 v101, v101, v114
	v_pk_add_f16 v100, v100, v115
	v_rcp_f16_e32 v110, v101
	v_rcp_f16_sdwa v101, v101 dst_sel:DWORD dst_unused:UNUSED_PAD src0_sel:WORD_1
	v_pk_add_f16 v99, v99, v116
	v_rcp_f16_e32 v111, v100
	v_rcp_f16_sdwa v100, v100 dst_sel:DWORD dst_unused:UNUSED_PAD src0_sel:WORD_1
	v_pk_add_f16 v98, v98, v117
	v_rcp_f16_e32 v112, v99
	v_rcp_f16_sdwa v99, v99 dst_sel:DWORD dst_unused:UNUSED_PAD src0_sel:WORD_1
	v_rcp_f16_e32 v113, v98
	v_rcp_f16_sdwa v98, v98 dst_sel:DWORD dst_unused:UNUSED_PAD src0_sel:WORD_1
	v_pk_fma_f16 v70, v46, v114, v70
	v_pack_b32_f16 v101, v110, v101
	v_pk_fma_f16 v71, v47, v115, v71
	v_pk_mul_f16 v110, v70, v101
	v_pack_b32_f16 v70, v111, v100
	v_pk_fma_f16 v72, v48, v116, v72
	v_pk_mul_f16 v111, v71, v70
	v_pack_b32_f16 v70, v112, v99
	v_pk_fma_f16 v73, v49, v117, v73
	v_pk_mul_f16 v112, v72, v70
	v_pack_b32_f16 v70, v113, v98
	v_pk_mul_f16 v113, v73, v70
	s_waitcnt vmcnt(12)
	v_pk_mul_f16 v73, v185, v157 op_sel_hi:[0,1]
	v_pk_mul_f16 v101, v183, v157 op_sel_hi:[0,1]
	v_pk_mul_f16 v117, v184, v157 op_sel_hi:[0,1]
	v_pk_mul_f16 v70, v185, v154 op_sel_hi:[0,1]
	v_pk_mul_f16 v71, v185, v155 op_sel_hi:[0,1]
	v_pk_mul_f16 v72, v185, v156 op_sel_hi:[0,1]
	v_pk_mul_f16 v98, v183, v154 op_sel_hi:[0,1]
	v_pk_mul_f16 v99, v183, v155 op_sel_hi:[0,1]
	v_pk_mul_f16 v100, v183, v156 op_sel_hi:[0,1]
	v_pk_mul_f16 v114, v184, v154 op_sel_hi:[0,1]
	v_pk_mul_f16 v115, v184, v155 op_sel_hi:[0,1]
	v_pk_mul_f16 v116, v184, v156 op_sel_hi:[0,1]
	v_pk_fma_f16 v85, v85, v157, v73
	v_pk_fma_f16 v109, v109, v157, v101
	v_pk_fma_f16 v125, v125, v157, v117
	v_pk_fma_f16 v126, v53, v157, v73
	v_pk_fma_f16 v134, v69, v157, v101
	v_pk_fma_f16 v186, v97, v157, v117
	v_pk_fma_f16 v73, v21, v157, v73
	v_pk_fma_f16 v101, v37, v157, v101
	v_pk_fma_f16 v117, v57, v157, v117
	v_pk_maximum3_f16 v157, v85, v109, v125
	v_pk_fma_f16 v84, v84, v156, v72
	v_pk_fma_f16 v83, v83, v155, v71
	v_pk_fma_f16 v82, v82, v154, v70
	v_pk_fma_f16 v108, v108, v156, v100
	v_pk_fma_f16 v107, v107, v155, v99
	v_pk_fma_f16 v106, v106, v154, v98
	v_pk_fma_f16 v124, v124, v156, v116
	v_pk_fma_f16 v123, v123, v155, v115
	v_pk_fma_f16 v122, v122, v154, v114
	v_pk_fma_f16 v127, v52, v156, v72
	v_pk_fma_f16 v128, v51, v155, v71
	v_pk_fma_f16 v129, v50, v154, v70
	v_pk_fma_f16 v135, v68, v156, v100
	v_pk_fma_f16 v136, v67, v155, v99
	v_pk_fma_f16 v137, v66, v154, v98
	v_pk_fma_f16 v187, v96, v156, v116
	v_pk_fma_f16 v188, v95, v155, v115
	v_pk_fma_f16 v189, v94, v154, v114
	v_pk_fma_f16 v72, v20, v156, v72
	v_pk_fma_f16 v71, v19, v155, v71
	v_pk_fma_f16 v70, v18, v154, v70
	v_pk_fma_f16 v100, v36, v156, v100
	v_pk_fma_f16 v99, v35, v155, v99
	v_pk_fma_f16 v98, v34, v154, v98
	v_pk_fma_f16 v116, v56, v156, v116
	v_pk_fma_f16 v115, v55, v155, v115
	v_pk_fma_f16 v114, v54, v154, v114
	v_pk_maximum3_f16 v154, v82, v106, v122
	v_pk_maximum3_f16 v155, v83, v107, v123
	v_pk_maximum3_f16 v156, v84, v108, v124
	v_pk_maximum3_f16 v193, v126, v134, v186
	v_pk_maximum3_f16 v197, v73, v101, v117
	v_pk_maximum3_f16 v190, v129, v137, v189
	v_pk_maximum3_f16 v191, v128, v136, v188
	v_pk_maximum3_f16 v192, v127, v135, v187
	v_pk_maximum3_f16 v194, v70, v98, v114
	v_pk_maximum3_f16 v195, v71, v99, v115
	v_pk_maximum3_f16 v157, v157, v193, v197
	v_pk_maximum3_f16 v196, v72, v100, v116
	v_pk_maximum3_f16 v154, v154, v190, v194
	v_pk_maximum3_f16 v155, v155, v191, v195
	v_pk_maximum3_f16 v156, v156, v192, v196
	v_pk_add_f16 v85, v85, v157 neg_lo:[0,1] neg_hi:[0,1]
	v_pk_add_f16 v82, v82, v154 neg_lo:[0,1] neg_hi:[0,1]
	v_pk_add_f16 v83, v83, v155 neg_lo:[0,1] neg_hi:[0,1]
	v_pk_add_f16 v84, v84, v156 neg_lo:[0,1] neg_hi:[0,1]
	v_pk_add_f16 v106, v106, v154 neg_lo:[0,1] neg_hi:[0,1]
	v_exp_f16_sdwa v190, v82 dst_sel:WORD_0 dst_unused:UNUSED_PAD src0_sel:WORD_0
	v_exp_f16_sdwa v191, v83 dst_sel:WORD_0 dst_unused:UNUSED_PAD src0_sel:WORD_0
	v_exp_f16_sdwa v192, v84 dst_sel:WORD_0 dst_unused:UNUSED_PAD src0_sel:WORD_0
	v_exp_f16_sdwa v193, v85 dst_sel:WORD_0 dst_unused:UNUSED_PAD src0_sel:WORD_0
	v_exp_f16_sdwa v190, v82 dst_sel:WORD_1 dst_unused:UNUSED_PRESERVE src0_sel:WORD_1
	v_exp_f16_sdwa v191, v83 dst_sel:WORD_1 dst_unused:UNUSED_PRESERVE src0_sel:WORD_1
	v_exp_f16_sdwa v192, v84 dst_sel:WORD_1 dst_unused:UNUSED_PRESERVE src0_sel:WORD_1
	v_exp_f16_sdwa v193, v85 dst_sel:WORD_1 dst_unused:UNUSED_PRESERVE src0_sel:WORD_1
	v_pk_add_f16 v107, v107, v155 neg_lo:[0,1] neg_hi:[0,1]
	v_pk_add_f16 v85, v190, 0
	v_pk_fma_f16 v45, v45, v193, 0
	v_pk_add_f16 v82, v193, 0
	v_pk_add_f16 v83, v192, 0
	v_pk_add_f16 v84, v191, 0
	v_pk_fma_f16 v44, v44, v192, 0
	v_pk_fma_f16 v43, v43, v191, 0
	v_pk_fma_f16 v42, v42, v190, 0
	v_pk_add_f16 v108, v108, v156 neg_lo:[0,1] neg_hi:[0,1]
	v_pk_add_f16 v109, v109, v157 neg_lo:[0,1] neg_hi:[0,1]
	v_pk_add_f16 v70, v70, v154 neg_lo:[0,1] neg_hi:[0,1]
	v_exp_f16_sdwa v190, v106 dst_sel:WORD_0 dst_unused:UNUSED_PAD src0_sel:WORD_0
	v_exp_f16_sdwa v191, v107 dst_sel:WORD_0 dst_unused:UNUSED_PAD src0_sel:WORD_0
	v_exp_f16_sdwa v192, v108 dst_sel:WORD_0 dst_unused:UNUSED_PAD src0_sel:WORD_0
	v_exp_f16_sdwa v193, v109 dst_sel:WORD_0 dst_unused:UNUSED_PAD src0_sel:WORD_0
	v_exp_f16_sdwa v190, v106 dst_sel:WORD_1 dst_unused:UNUSED_PRESERVE src0_sel:WORD_1
	v_exp_f16_sdwa v191, v107 dst_sel:WORD_1 dst_unused:UNUSED_PRESERVE src0_sel:WORD_1
	v_exp_f16_sdwa v192, v108 dst_sel:WORD_1 dst_unused:UNUSED_PRESERVE src0_sel:WORD_1
	v_exp_f16_sdwa v193, v109 dst_sel:WORD_1 dst_unused:UNUSED_PRESERVE src0_sel:WORD_1
	v_pk_add_f16 v71, v71, v155 neg_lo:[0,1] neg_hi:[0,1]
	v_pk_add_f16 v85, v85, v190
	v_pk_fma_f16 v45, v65, v193, v45
	v_pk_add_f16 v65, v125, v157 neg_lo:[0,1] neg_hi:[0,1]
	v_pk_add_f16 v84, v84, v191
	v_pk_add_f16 v83, v83, v192
	v_pk_add_f16 v82, v82, v193
	v_pk_fma_f16 v42, v62, v190, v42
	v_pk_fma_f16 v43, v63, v191, v43
	v_pk_fma_f16 v44, v64, v192, v44
	v_pk_add_f16 v62, v122, v154 neg_lo:[0,1] neg_hi:[0,1]
	v_pk_add_f16 v63, v123, v155 neg_lo:[0,1] neg_hi:[0,1]
	v_pk_add_f16 v64, v124, v156 neg_lo:[0,1] neg_hi:[0,1]
	v_pk_add_f16 v72, v72, v156 neg_lo:[0,1] neg_hi:[0,1]
	v_exp_f16_sdwa v106, v62 dst_sel:WORD_0 dst_unused:UNUSED_PAD src0_sel:WORD_0
	v_exp_f16_sdwa v107, v63 dst_sel:WORD_0 dst_unused:UNUSED_PAD src0_sel:WORD_0
	v_exp_f16_sdwa v108, v64 dst_sel:WORD_0 dst_unused:UNUSED_PAD src0_sel:WORD_0
	v_exp_f16_sdwa v109, v65 dst_sel:WORD_0 dst_unused:UNUSED_PAD src0_sel:WORD_0
	v_exp_f16_sdwa v106, v62 dst_sel:WORD_1 dst_unused:UNUSED_PRESERVE src0_sel:WORD_1
	v_exp_f16_sdwa v107, v63 dst_sel:WORD_1 dst_unused:UNUSED_PRESERVE src0_sel:WORD_1
	v_exp_f16_sdwa v108, v64 dst_sel:WORD_1 dst_unused:UNUSED_PRESERVE src0_sel:WORD_1
	v_exp_f16_sdwa v109, v65 dst_sel:WORD_1 dst_unused:UNUSED_PRESERVE src0_sel:WORD_1
	v_pk_add_f16 v73, v73, v157 neg_lo:[0,1] neg_hi:[0,1]
	v_pk_add_f16 v65, v85, v106
	v_pk_add_f16 v62, v82, v109
	v_pk_add_f16 v63, v83, v108
	v_pk_add_f16 v64, v84, v107
	v_pk_fma_f16 v45, v89, v109, v45
	v_pk_fma_f16 v44, v88, v108, v44
	v_pk_fma_f16 v43, v87, v107, v43
	v_pk_fma_f16 v42, v86, v106, v42
	v_pk_add_f16 v82, v129, v154 neg_lo:[0,1] neg_hi:[0,1]
	v_pk_add_f16 v83, v128, v155 neg_lo:[0,1] neg_hi:[0,1]
	v_pk_add_f16 v84, v127, v156 neg_lo:[0,1] neg_hi:[0,1]
	v_pk_add_f16 v85, v126, v157 neg_lo:[0,1] neg_hi:[0,1]
	v_exp_f16_sdwa v86, v82 dst_sel:WORD_0 dst_unused:UNUSED_PAD src0_sel:WORD_0
	v_exp_f16_sdwa v87, v83 dst_sel:WORD_0 dst_unused:UNUSED_PAD src0_sel:WORD_0
	v_exp_f16_sdwa v88, v84 dst_sel:WORD_0 dst_unused:UNUSED_PAD src0_sel:WORD_0
	v_exp_f16_sdwa v89, v85 dst_sel:WORD_0 dst_unused:UNUSED_PAD src0_sel:WORD_0
	v_exp_f16_sdwa v86, v82 dst_sel:WORD_1 dst_unused:UNUSED_PRESERVE src0_sel:WORD_1
	v_exp_f16_sdwa v87, v83 dst_sel:WORD_1 dst_unused:UNUSED_PRESERVE src0_sel:WORD_1
	v_exp_f16_sdwa v88, v84 dst_sel:WORD_1 dst_unused:UNUSED_PRESERVE src0_sel:WORD_1
	v_exp_f16_sdwa v89, v85 dst_sel:WORD_1 dst_unused:UNUSED_PRESERVE src0_sel:WORD_1
	v_pk_add_f16 v82, v137, v154 neg_lo:[0,1] neg_hi:[0,1]
	v_pk_add_f16 v65, v65, v86
	v_pk_add_f16 v64, v64, v87
	v_pk_add_f16 v63, v63, v88
	v_pk_add_f16 v62, v62, v89
	v_pk_fma_f16 v42, v22, v86, v42
	v_pk_fma_f16 v43, v23, v87, v43
	v_pk_fma_f16 v44, v24, v88, v44
	v_pk_fma_f16 v45, v25, v89, v45
	v_pk_add_f16 v83, v136, v155 neg_lo:[0,1] neg_hi:[0,1]
	v_pk_add_f16 v84, v135, v156 neg_lo:[0,1] neg_hi:[0,1]
	v_pk_add_f16 v85, v134, v157 neg_lo:[0,1] neg_hi:[0,1]
	v_exp_f16_sdwa v86, v82 dst_sel:WORD_0 dst_unused:UNUSED_PAD src0_sel:WORD_0
	v_exp_f16_sdwa v87, v83 dst_sel:WORD_0 dst_unused:UNUSED_PAD src0_sel:WORD_0
	v_exp_f16_sdwa v88, v84 dst_sel:WORD_0 dst_unused:UNUSED_PAD src0_sel:WORD_0
	v_exp_f16_sdwa v89, v85 dst_sel:WORD_0 dst_unused:UNUSED_PAD src0_sel:WORD_0
	v_exp_f16_sdwa v86, v82 dst_sel:WORD_1 dst_unused:UNUSED_PRESERVE src0_sel:WORD_1
	v_exp_f16_sdwa v87, v83 dst_sel:WORD_1 dst_unused:UNUSED_PRESERVE src0_sel:WORD_1
	v_exp_f16_sdwa v88, v84 dst_sel:WORD_1 dst_unused:UNUSED_PRESERVE src0_sel:WORD_1
	v_exp_f16_sdwa v89, v85 dst_sel:WORD_1 dst_unused:UNUSED_PRESERVE src0_sel:WORD_1
	v_pk_add_f16 v82, v189, v154 neg_lo:[0,1] neg_hi:[0,1]
	v_pk_add_f16 v65, v65, v86
	v_pk_add_f16 v62, v62, v89
	v_pk_add_f16 v63, v63, v88
	v_pk_add_f16 v64, v64, v87
	v_pk_fma_f16 v45, v33, v89, v45
	v_pk_fma_f16 v44, v32, v88, v44
	v_pk_fma_f16 v43, v31, v87, v43
	v_pk_fma_f16 v42, v30, v86, v42
	v_pk_add_f16 v83, v188, v155 neg_lo:[0,1] neg_hi:[0,1]
	v_pk_add_f16 v84, v187, v156 neg_lo:[0,1] neg_hi:[0,1]
	v_pk_add_f16 v85, v186, v157 neg_lo:[0,1] neg_hi:[0,1]
	v_exp_f16_sdwa v86, v82 dst_sel:WORD_0 dst_unused:UNUSED_PAD src0_sel:WORD_0
	v_exp_f16_sdwa v87, v83 dst_sel:WORD_0 dst_unused:UNUSED_PAD src0_sel:WORD_0
	v_exp_f16_sdwa v88, v84 dst_sel:WORD_0 dst_unused:UNUSED_PAD src0_sel:WORD_0
	v_exp_f16_sdwa v89, v85 dst_sel:WORD_0 dst_unused:UNUSED_PAD src0_sel:WORD_0
	v_exp_f16_sdwa v86, v82 dst_sel:WORD_1 dst_unused:UNUSED_PRESERVE src0_sel:WORD_1
	v_exp_f16_sdwa v87, v83 dst_sel:WORD_1 dst_unused:UNUSED_PRESERVE src0_sel:WORD_1
	v_exp_f16_sdwa v88, v84 dst_sel:WORD_1 dst_unused:UNUSED_PRESERVE src0_sel:WORD_1
	v_exp_f16_sdwa v89, v85 dst_sel:WORD_1 dst_unused:UNUSED_PRESERVE src0_sel:WORD_1
	v_exp_f16_sdwa v82, v70 dst_sel:WORD_0 dst_unused:UNUSED_PAD src0_sel:WORD_0
	v_exp_f16_sdwa v83, v71 dst_sel:WORD_0 dst_unused:UNUSED_PAD src0_sel:WORD_0
	v_exp_f16_sdwa v84, v72 dst_sel:WORD_0 dst_unused:UNUSED_PAD src0_sel:WORD_0
	v_exp_f16_sdwa v85, v73 dst_sel:WORD_0 dst_unused:UNUSED_PAD src0_sel:WORD_0
	v_exp_f16_sdwa v82, v70 dst_sel:WORD_1 dst_unused:UNUSED_PRESERVE src0_sel:WORD_1
	v_exp_f16_sdwa v83, v71 dst_sel:WORD_1 dst_unused:UNUSED_PRESERVE src0_sel:WORD_1
	v_exp_f16_sdwa v84, v72 dst_sel:WORD_1 dst_unused:UNUSED_PRESERVE src0_sel:WORD_1
	v_exp_f16_sdwa v85, v73 dst_sel:WORD_1 dst_unused:UNUSED_PRESERVE src0_sel:WORD_1
	v_pk_add_f16 v70, v98, v154 neg_lo:[0,1] neg_hi:[0,1]
	v_pk_add_f16 v65, v65, v86
	v_pk_add_f16 v64, v64, v87
	v_pk_add_f16 v63, v63, v88
	v_pk_add_f16 v62, v62, v89
	v_pk_fma_f16 v42, v46, v86, v42
	v_pk_fma_f16 v43, v47, v87, v43
	v_pk_fma_f16 v44, v48, v88, v44
	v_pk_fma_f16 v45, v49, v89, v45
	v_pk_add_f16 v65, v65, v82
	v_pk_add_f16 v62, v62, v85
	v_pk_add_f16 v63, v63, v84
	v_pk_add_f16 v64, v64, v83
	v_pk_fma_f16 v45, v9, v85, v45
	v_pk_fma_f16 v44, v8, v84, v44
	v_pk_fma_f16 v43, v7, v83, v43
	v_pk_fma_f16 v42, v6, v82, v42
	v_pk_add_f16 v71, v99, v155 neg_lo:[0,1] neg_hi:[0,1]
	v_pk_add_f16 v72, v100, v156 neg_lo:[0,1] neg_hi:[0,1]
	v_pk_add_f16 v73, v101, v157 neg_lo:[0,1] neg_hi:[0,1]
	v_exp_f16_sdwa v82, v70 dst_sel:WORD_0 dst_unused:UNUSED_PAD src0_sel:WORD_0
	v_exp_f16_sdwa v83, v71 dst_sel:WORD_0 dst_unused:UNUSED_PAD src0_sel:WORD_0
	v_exp_f16_sdwa v84, v72 dst_sel:WORD_0 dst_unused:UNUSED_PAD src0_sel:WORD_0
	v_exp_f16_sdwa v85, v73 dst_sel:WORD_0 dst_unused:UNUSED_PAD src0_sel:WORD_0
	v_exp_f16_sdwa v82, v70 dst_sel:WORD_1 dst_unused:UNUSED_PRESERVE src0_sel:WORD_1
	v_exp_f16_sdwa v83, v71 dst_sel:WORD_1 dst_unused:UNUSED_PRESERVE src0_sel:WORD_1
	v_exp_f16_sdwa v84, v72 dst_sel:WORD_1 dst_unused:UNUSED_PRESERVE src0_sel:WORD_1
	v_exp_f16_sdwa v85, v73 dst_sel:WORD_1 dst_unused:UNUSED_PRESERVE src0_sel:WORD_1
	v_pk_add_f16 v70, v114, v154 neg_lo:[0,1] neg_hi:[0,1]
	v_pk_add_f16 v65, v65, v82
	v_pk_add_f16 v64, v64, v83
	v_pk_add_f16 v63, v63, v84
	v_pk_add_f16 v62, v62, v85
	v_pk_fma_f16 v42, v10, v82, v42
	v_pk_fma_f16 v43, v11, v83, v43
	v_pk_fma_f16 v44, v12, v84, v44
	v_pk_fma_f16 v45, v13, v85, v45
	v_pk_add_f16 v71, v115, v155 neg_lo:[0,1] neg_hi:[0,1]
	v_pk_add_f16 v72, v116, v156 neg_lo:[0,1] neg_hi:[0,1]
	v_pk_add_f16 v73, v117, v157 neg_lo:[0,1] neg_hi:[0,1]
	v_exp_f16_sdwa v82, v70 dst_sel:WORD_0 dst_unused:UNUSED_PAD src0_sel:WORD_0
	v_exp_f16_sdwa v83, v71 dst_sel:WORD_0 dst_unused:UNUSED_PAD src0_sel:WORD_0
	v_exp_f16_sdwa v84, v72 dst_sel:WORD_0 dst_unused:UNUSED_PAD src0_sel:WORD_0
	v_exp_f16_sdwa v85, v73 dst_sel:WORD_0 dst_unused:UNUSED_PAD src0_sel:WORD_0
	v_exp_f16_sdwa v82, v70 dst_sel:WORD_1 dst_unused:UNUSED_PRESERVE src0_sel:WORD_1
	v_exp_f16_sdwa v83, v71 dst_sel:WORD_1 dst_unused:UNUSED_PRESERVE src0_sel:WORD_1
	v_exp_f16_sdwa v84, v72 dst_sel:WORD_1 dst_unused:UNUSED_PRESERVE src0_sel:WORD_1
	v_exp_f16_sdwa v85, v73 dst_sel:WORD_1 dst_unused:UNUSED_PRESERVE src0_sel:WORD_1
	v_pk_add_f16 v65, v65, v82
	v_pk_add_f16 v64, v64, v83
	v_rcp_f16_e32 v70, v65
	v_rcp_f16_sdwa v65, v65 dst_sel:DWORD dst_unused:UNUSED_PAD src0_sel:WORD_1
	v_pk_add_f16 v63, v63, v84
	v_rcp_f16_e32 v71, v64
	v_rcp_f16_sdwa v64, v64 dst_sel:DWORD dst_unused:UNUSED_PAD src0_sel:WORD_1
	v_pk_add_f16 v62, v62, v85
	v_rcp_f16_e32 v72, v63
	v_rcp_f16_sdwa v73, v63 dst_sel:DWORD dst_unused:UNUSED_PAD src0_sel:WORD_1
	v_pk_fma_f16 v43, v15, v83, v43
	v_pk_fma_f16 v42, v14, v82, v42
	v_rcp_f16_e32 v82, v62
	v_rcp_f16_sdwa v83, v62 dst_sel:DWORD dst_unused:UNUSED_PAD src0_sel:WORD_1
	v_pack_b32_f16 v62, v70, v65
	v_pk_mul_f16 v62, v42, v62
	v_pack_b32_f16 v42, v71, v64
	v_pk_fma_f16 v44, v16, v84, v44
	v_pk_mul_f16 v63, v43, v42
	v_pack_b32_f16 v42, v72, v73
	v_pk_fma_f16 v45, v17, v85, v45
	v_pk_mul_f16 v64, v44, v42
	v_pack_b32_f16 v42, v82, v83
	v_pk_mul_f16 v65, v45, v42
	s_waitcnt vmcnt(6)
	v_pk_mul_f16 v42, v185, v150 op_sel_hi:[0,1]
	v_pk_mul_f16 v70, v183, v150 op_sel_hi:[0,1]
	v_pk_mul_f16 v82, v184, v150 op_sel_hi:[0,1]
	v_pk_mul_f16 v43, v185, v151 op_sel_hi:[0,1]
	v_pk_mul_f16 v44, v185, v152 op_sel_hi:[0,1]
	v_pk_mul_f16 v45, v185, v153 op_sel_hi:[0,1]
	v_pk_mul_f16 v71, v183, v151 op_sel_hi:[0,1]
	v_pk_mul_f16 v72, v183, v152 op_sel_hi:[0,1]
	v_pk_mul_f16 v73, v183, v153 op_sel_hi:[0,1]
	v_pk_mul_f16 v83, v184, v151 op_sel_hi:[0,1]
	v_pk_mul_f16 v84, v184, v152 op_sel_hi:[0,1]
	v_pk_mul_f16 v85, v184, v153 op_sel_hi:[0,1]
	v_pk_fma_f16 v50, v50, v150, v42
	v_pk_fma_f16 v66, v66, v150, v70
	v_pk_fma_f16 v89, v94, v150, v82
	v_pk_fma_f16 v53, v53, v153, v45
	v_pk_maximum3_f16 v114, v50, v66, v89
	v_pk_fma_f16 v52, v52, v152, v44
	v_pk_fma_f16 v51, v51, v151, v43
	v_pk_fma_f16 v69, v69, v153, v73
	v_pk_fma_f16 v68, v68, v152, v72
	v_pk_fma_f16 v67, v67, v151, v71
	v_pk_fma_f16 v86, v97, v153, v85
	v_pk_fma_f16 v87, v96, v152, v84
	v_pk_fma_f16 v88, v95, v151, v83
	v_pk_fma_f16 v97, v18, v150, v42
	v_pk_fma_f16 v101, v34, v150, v70
	v_pk_fma_f16 v109, v54, v150, v82
	v_pk_fma_f16 v42, v74, v150, v42
	v_pk_fma_f16 v70, v102, v150, v70
	v_pk_fma_f16 v82, v118, v150, v82
	v_pk_maximum3_f16 v115, v51, v67, v88
	v_pk_maximum3_f16 v116, v52, v68, v87
	v_pk_maximum3_f16 v117, v53, v69, v86
	v_pk_maximum3_f16 v122, v97, v101, v109
	v_pk_fma_f16 v94, v21, v153, v45
	v_pk_maximum3_f16 v126, v42, v70, v82
	v_pk_fma_f16 v95, v20, v152, v44
	v_pk_maximum3_f16 v114, v114, v122, v126
	v_pk_fma_f16 v96, v19, v151, v43
	v_pk_fma_f16 v98, v37, v153, v73
	v_pk_fma_f16 v99, v36, v152, v72
	v_pk_fma_f16 v100, v35, v151, v71
	v_pk_fma_f16 v106, v57, v153, v85
	v_pk_fma_f16 v107, v56, v152, v84
	v_pk_fma_f16 v108, v55, v151, v83
	v_pk_fma_f16 v45, v77, v153, v45
	v_pk_fma_f16 v44, v76, v152, v44
	v_pk_fma_f16 v43, v75, v151, v43
	v_pk_fma_f16 v73, v105, v153, v73
	v_pk_fma_f16 v72, v104, v152, v72
	v_pk_fma_f16 v71, v103, v151, v71
	v_pk_fma_f16 v85, v121, v153, v85
	v_pk_fma_f16 v84, v120, v152, v84
	v_pk_fma_f16 v83, v119, v151, v83
	v_pk_maximum3_f16 v123, v96, v100, v108
	v_pk_maximum3_f16 v124, v95, v99, v107
	v_pk_maximum3_f16 v125, v94, v98, v106
	v_pk_maximum3_f16 v128, v44, v72, v84
	v_pk_maximum3_f16 v129, v45, v73, v85
	v_pk_maximum3_f16 v127, v43, v71, v83
	v_pk_maximum3_f16 v115, v115, v123, v127
	v_pk_maximum3_f16 v116, v116, v124, v128
	v_pk_maximum3_f16 v117, v117, v125, v129
	v_pk_add_f16 v50, v50, v114 neg_lo:[0,1] neg_hi:[0,1]
	v_pk_add_f16 v51, v51, v115 neg_lo:[0,1] neg_hi:[0,1]
	v_pk_add_f16 v52, v52, v116 neg_lo:[0,1] neg_hi:[0,1]
	v_pk_add_f16 v53, v53, v117 neg_lo:[0,1] neg_hi:[0,1]
	v_pk_add_f16 v66, v66, v114 neg_lo:[0,1] neg_hi:[0,1]
	v_exp_f16_sdwa v122, v50 dst_sel:WORD_0 dst_unused:UNUSED_PAD src0_sel:WORD_0
	v_exp_f16_sdwa v123, v51 dst_sel:WORD_0 dst_unused:UNUSED_PAD src0_sel:WORD_0
	v_exp_f16_sdwa v124, v52 dst_sel:WORD_0 dst_unused:UNUSED_PAD src0_sel:WORD_0
	v_exp_f16_sdwa v125, v53 dst_sel:WORD_0 dst_unused:UNUSED_PAD src0_sel:WORD_0
	v_exp_f16_sdwa v122, v50 dst_sel:WORD_1 dst_unused:UNUSED_PRESERVE src0_sel:WORD_1
	v_exp_f16_sdwa v123, v51 dst_sel:WORD_1 dst_unused:UNUSED_PRESERVE src0_sel:WORD_1
	v_exp_f16_sdwa v124, v52 dst_sel:WORD_1 dst_unused:UNUSED_PRESERVE src0_sel:WORD_1
	v_exp_f16_sdwa v125, v53 dst_sel:WORD_1 dst_unused:UNUSED_PRESERVE src0_sel:WORD_1
	v_pk_add_f16 v67, v67, v115 neg_lo:[0,1] neg_hi:[0,1]
	v_pk_add_f16 v50, v125, 0
	v_pk_fma_f16 v22, v22, v122, 0
	v_pk_add_f16 v51, v124, 0
	v_pk_add_f16 v52, v123, 0
	v_pk_add_f16 v53, v122, 0
	v_pk_fma_f16 v23, v23, v123, 0
	v_pk_fma_f16 v24, v24, v124, 0
	v_pk_fma_f16 v25, v25, v125, 0
	v_pk_add_f16 v68, v68, v116 neg_lo:[0,1] neg_hi:[0,1]
	v_pk_add_f16 v69, v69, v117 neg_lo:[0,1] neg_hi:[0,1]
	v_pk_add_f16 v42, v42, v114 neg_lo:[0,1] neg_hi:[0,1]
	v_exp_f16_sdwa v122, v66 dst_sel:WORD_0 dst_unused:UNUSED_PAD src0_sel:WORD_0
	v_exp_f16_sdwa v123, v67 dst_sel:WORD_0 dst_unused:UNUSED_PAD src0_sel:WORD_0
	v_exp_f16_sdwa v124, v68 dst_sel:WORD_0 dst_unused:UNUSED_PAD src0_sel:WORD_0
	v_exp_f16_sdwa v125, v69 dst_sel:WORD_0 dst_unused:UNUSED_PAD src0_sel:WORD_0
	v_exp_f16_sdwa v122, v66 dst_sel:WORD_1 dst_unused:UNUSED_PRESERVE src0_sel:WORD_1
	v_exp_f16_sdwa v123, v67 dst_sel:WORD_1 dst_unused:UNUSED_PRESERVE src0_sel:WORD_1
	v_exp_f16_sdwa v124, v68 dst_sel:WORD_1 dst_unused:UNUSED_PRESERVE src0_sel:WORD_1
	v_exp_f16_sdwa v125, v69 dst_sel:WORD_1 dst_unused:UNUSED_PRESERVE src0_sel:WORD_1
	v_pk_add_f16 v43, v43, v115 neg_lo:[0,1] neg_hi:[0,1]
	v_pk_add_f16 v50, v50, v125
	v_pk_fma_f16 v22, v30, v122, v22
	v_pk_add_f16 v30, v89, v114 neg_lo:[0,1] neg_hi:[0,1]
	v_pk_add_f16 v53, v53, v122
	v_pk_add_f16 v52, v52, v123
	v_pk_add_f16 v51, v51, v124
	v_pk_fma_f16 v25, v33, v125, v25
	v_pk_fma_f16 v24, v32, v124, v24
	v_pk_fma_f16 v23, v31, v123, v23
	v_pk_add_f16 v31, v88, v115 neg_lo:[0,1] neg_hi:[0,1]
	v_pk_add_f16 v32, v87, v116 neg_lo:[0,1] neg_hi:[0,1]
	v_pk_add_f16 v33, v86, v117 neg_lo:[0,1] neg_hi:[0,1]
	v_pk_add_f16 v44, v44, v116 neg_lo:[0,1] neg_hi:[0,1]
	v_exp_f16_sdwa v66, v30 dst_sel:WORD_0 dst_unused:UNUSED_PAD src0_sel:WORD_0
	v_exp_f16_sdwa v67, v31 dst_sel:WORD_0 dst_unused:UNUSED_PAD src0_sel:WORD_0
	v_exp_f16_sdwa v68, v32 dst_sel:WORD_0 dst_unused:UNUSED_PAD src0_sel:WORD_0
	v_exp_f16_sdwa v69, v33 dst_sel:WORD_0 dst_unused:UNUSED_PAD src0_sel:WORD_0
	v_exp_f16_sdwa v66, v30 dst_sel:WORD_1 dst_unused:UNUSED_PRESERVE src0_sel:WORD_1
	v_exp_f16_sdwa v67, v31 dst_sel:WORD_1 dst_unused:UNUSED_PRESERVE src0_sel:WORD_1
	v_exp_f16_sdwa v68, v32 dst_sel:WORD_1 dst_unused:UNUSED_PRESERVE src0_sel:WORD_1
	v_exp_f16_sdwa v69, v33 dst_sel:WORD_1 dst_unused:UNUSED_PRESERVE src0_sel:WORD_1
	v_pk_add_f16 v45, v45, v117 neg_lo:[0,1] neg_hi:[0,1]
	v_pk_add_f16 v30, v50, v69
	v_pk_add_f16 v31, v51, v68
	v_pk_add_f16 v32, v52, v67
	v_pk_add_f16 v33, v53, v66
	v_pk_fma_f16 v22, v46, v66, v22
	v_pk_fma_f16 v23, v47, v67, v23
	v_pk_fma_f16 v24, v48, v68, v24
	v_pk_fma_f16 v25, v49, v69, v25
	v_pk_add_f16 v46, v97, v114 neg_lo:[0,1] neg_hi:[0,1]
	v_pk_add_f16 v47, v96, v115 neg_lo:[0,1] neg_hi:[0,1]
	v_pk_add_f16 v48, v95, v116 neg_lo:[0,1] neg_hi:[0,1]
	v_pk_add_f16 v49, v94, v117 neg_lo:[0,1] neg_hi:[0,1]
	v_exp_f16_sdwa v50, v46 dst_sel:WORD_0 dst_unused:UNUSED_PAD src0_sel:WORD_0
	v_exp_f16_sdwa v51, v47 dst_sel:WORD_0 dst_unused:UNUSED_PAD src0_sel:WORD_0
	v_exp_f16_sdwa v52, v48 dst_sel:WORD_0 dst_unused:UNUSED_PAD src0_sel:WORD_0
	v_exp_f16_sdwa v53, v49 dst_sel:WORD_0 dst_unused:UNUSED_PAD src0_sel:WORD_0
	v_exp_f16_sdwa v50, v46 dst_sel:WORD_1 dst_unused:UNUSED_PRESERVE src0_sel:WORD_1
	v_exp_f16_sdwa v51, v47 dst_sel:WORD_1 dst_unused:UNUSED_PRESERVE src0_sel:WORD_1
	v_exp_f16_sdwa v52, v48 dst_sel:WORD_1 dst_unused:UNUSED_PRESERVE src0_sel:WORD_1
	v_exp_f16_sdwa v53, v49 dst_sel:WORD_1 dst_unused:UNUSED_PRESERVE src0_sel:WORD_1
	v_pk_add_f16 v46, v101, v114 neg_lo:[0,1] neg_hi:[0,1]
	v_pk_add_f16 v30, v30, v53
	v_pk_add_f16 v33, v33, v50
	v_pk_add_f16 v32, v32, v51
	v_pk_add_f16 v31, v31, v52
	v_pk_fma_f16 v25, v9, v53, v25
	v_pk_fma_f16 v24, v8, v52, v24
	v_pk_fma_f16 v23, v7, v51, v23
	v_pk_fma_f16 v22, v6, v50, v22
	v_pk_add_f16 v47, v100, v115 neg_lo:[0,1] neg_hi:[0,1]
	v_pk_add_f16 v48, v99, v116 neg_lo:[0,1] neg_hi:[0,1]
	v_pk_add_f16 v49, v98, v117 neg_lo:[0,1] neg_hi:[0,1]
	v_exp_f16_sdwa v50, v46 dst_sel:WORD_0 dst_unused:UNUSED_PAD src0_sel:WORD_0
	v_exp_f16_sdwa v51, v47 dst_sel:WORD_0 dst_unused:UNUSED_PAD src0_sel:WORD_0
	v_exp_f16_sdwa v52, v48 dst_sel:WORD_0 dst_unused:UNUSED_PAD src0_sel:WORD_0
	v_exp_f16_sdwa v53, v49 dst_sel:WORD_0 dst_unused:UNUSED_PAD src0_sel:WORD_0
	v_exp_f16_sdwa v50, v46 dst_sel:WORD_1 dst_unused:UNUSED_PRESERVE src0_sel:WORD_1
	v_exp_f16_sdwa v51, v47 dst_sel:WORD_1 dst_unused:UNUSED_PRESERVE src0_sel:WORD_1
	v_exp_f16_sdwa v52, v48 dst_sel:WORD_1 dst_unused:UNUSED_PRESERVE src0_sel:WORD_1
	v_exp_f16_sdwa v53, v49 dst_sel:WORD_1 dst_unused:UNUSED_PRESERVE src0_sel:WORD_1
	v_pk_add_f16 v46, v109, v114 neg_lo:[0,1] neg_hi:[0,1]
	v_pk_add_f16 v30, v30, v53
	v_pk_add_f16 v31, v31, v52
	v_pk_add_f16 v32, v32, v51
	v_pk_add_f16 v33, v33, v50
	v_pk_fma_f16 v22, v10, v50, v22
	v_pk_fma_f16 v23, v11, v51, v23
	v_pk_fma_f16 v24, v12, v52, v24
	v_pk_fma_f16 v25, v13, v53, v25
	v_pk_add_f16 v47, v108, v115 neg_lo:[0,1] neg_hi:[0,1]
	v_pk_add_f16 v48, v107, v116 neg_lo:[0,1] neg_hi:[0,1]
	v_pk_add_f16 v49, v106, v117 neg_lo:[0,1] neg_hi:[0,1]
	v_exp_f16_sdwa v50, v46 dst_sel:WORD_0 dst_unused:UNUSED_PAD src0_sel:WORD_0
	v_exp_f16_sdwa v51, v47 dst_sel:WORD_0 dst_unused:UNUSED_PAD src0_sel:WORD_0
	v_exp_f16_sdwa v52, v48 dst_sel:WORD_0 dst_unused:UNUSED_PAD src0_sel:WORD_0
	v_exp_f16_sdwa v53, v49 dst_sel:WORD_0 dst_unused:UNUSED_PAD src0_sel:WORD_0
	v_exp_f16_sdwa v50, v46 dst_sel:WORD_1 dst_unused:UNUSED_PRESERVE src0_sel:WORD_1
	v_exp_f16_sdwa v51, v47 dst_sel:WORD_1 dst_unused:UNUSED_PRESERVE src0_sel:WORD_1
	v_exp_f16_sdwa v52, v48 dst_sel:WORD_1 dst_unused:UNUSED_PRESERVE src0_sel:WORD_1
	v_exp_f16_sdwa v53, v49 dst_sel:WORD_1 dst_unused:UNUSED_PRESERVE src0_sel:WORD_1
	v_exp_f16_sdwa v46, v42 dst_sel:WORD_0 dst_unused:UNUSED_PAD src0_sel:WORD_0
	v_exp_f16_sdwa v47, v43 dst_sel:WORD_0 dst_unused:UNUSED_PAD src0_sel:WORD_0
	v_exp_f16_sdwa v48, v44 dst_sel:WORD_0 dst_unused:UNUSED_PAD src0_sel:WORD_0
	v_exp_f16_sdwa v49, v45 dst_sel:WORD_0 dst_unused:UNUSED_PAD src0_sel:WORD_0
	v_exp_f16_sdwa v46, v42 dst_sel:WORD_1 dst_unused:UNUSED_PRESERVE src0_sel:WORD_1
	v_exp_f16_sdwa v47, v43 dst_sel:WORD_1 dst_unused:UNUSED_PRESERVE src0_sel:WORD_1
	v_exp_f16_sdwa v48, v44 dst_sel:WORD_1 dst_unused:UNUSED_PRESERVE src0_sel:WORD_1
	v_exp_f16_sdwa v49, v45 dst_sel:WORD_1 dst_unused:UNUSED_PRESERVE src0_sel:WORD_1
	v_pk_add_f16 v42, v70, v114 neg_lo:[0,1] neg_hi:[0,1]
	v_pk_add_f16 v30, v30, v53
	v_pk_add_f16 v33, v33, v50
	v_pk_add_f16 v32, v32, v51
	v_pk_add_f16 v31, v31, v52
	v_pk_fma_f16 v25, v17, v53, v25
	v_pk_fma_f16 v24, v16, v52, v24
	v_pk_fma_f16 v23, v15, v51, v23
	v_pk_fma_f16 v22, v14, v50, v22
	v_pk_add_f16 v30, v30, v49
	v_pk_add_f16 v31, v31, v48
	v_pk_add_f16 v32, v32, v47
	v_pk_add_f16 v33, v33, v46
	v_pk_fma_f16 v22, v26, v46, v22
	v_pk_fma_f16 v23, v27, v47, v23
	v_pk_fma_f16 v24, v28, v48, v24
	v_pk_fma_f16 v25, v29, v49, v25
	v_pk_add_f16 v43, v71, v115 neg_lo:[0,1] neg_hi:[0,1]
	v_pk_add_f16 v44, v72, v116 neg_lo:[0,1] neg_hi:[0,1]
	v_pk_add_f16 v45, v73, v117 neg_lo:[0,1] neg_hi:[0,1]
	v_exp_f16_sdwa v46, v42 dst_sel:WORD_0 dst_unused:UNUSED_PAD src0_sel:WORD_0
	v_exp_f16_sdwa v47, v43 dst_sel:WORD_0 dst_unused:UNUSED_PAD src0_sel:WORD_0
	v_exp_f16_sdwa v48, v44 dst_sel:WORD_0 dst_unused:UNUSED_PAD src0_sel:WORD_0
	v_exp_f16_sdwa v49, v45 dst_sel:WORD_0 dst_unused:UNUSED_PAD src0_sel:WORD_0
	v_exp_f16_sdwa v46, v42 dst_sel:WORD_1 dst_unused:UNUSED_PRESERVE src0_sel:WORD_1
	v_exp_f16_sdwa v47, v43 dst_sel:WORD_1 dst_unused:UNUSED_PRESERVE src0_sel:WORD_1
	v_exp_f16_sdwa v48, v44 dst_sel:WORD_1 dst_unused:UNUSED_PRESERVE src0_sel:WORD_1
	v_exp_f16_sdwa v49, v45 dst_sel:WORD_1 dst_unused:UNUSED_PRESERVE src0_sel:WORD_1
	v_pk_add_f16 v42, v82, v114 neg_lo:[0,1] neg_hi:[0,1]
	v_pk_add_f16 v30, v30, v49
	v_pk_add_f16 v33, v33, v46
	v_pk_add_f16 v32, v32, v47
	v_pk_add_f16 v31, v31, v48
	v_pk_fma_f16 v25, v41, v49, v25
	v_pk_fma_f16 v24, v40, v48, v24
	v_pk_fma_f16 v23, v39, v47, v23
	v_pk_fma_f16 v22, v38, v46, v22
	v_pk_add_f16 v43, v83, v115 neg_lo:[0,1] neg_hi:[0,1]
	v_pk_add_f16 v44, v84, v116 neg_lo:[0,1] neg_hi:[0,1]
	v_pk_add_f16 v45, v85, v117 neg_lo:[0,1] neg_hi:[0,1]
	v_exp_f16_sdwa v46, v42 dst_sel:WORD_0 dst_unused:UNUSED_PAD src0_sel:WORD_0
	v_exp_f16_sdwa v47, v43 dst_sel:WORD_0 dst_unused:UNUSED_PAD src0_sel:WORD_0
	v_exp_f16_sdwa v48, v44 dst_sel:WORD_0 dst_unused:UNUSED_PAD src0_sel:WORD_0
	v_exp_f16_sdwa v49, v45 dst_sel:WORD_0 dst_unused:UNUSED_PAD src0_sel:WORD_0
	v_exp_f16_sdwa v46, v42 dst_sel:WORD_1 dst_unused:UNUSED_PRESERVE src0_sel:WORD_1
	v_exp_f16_sdwa v47, v43 dst_sel:WORD_1 dst_unused:UNUSED_PRESERVE src0_sel:WORD_1
	v_exp_f16_sdwa v48, v44 dst_sel:WORD_1 dst_unused:UNUSED_PRESERVE src0_sel:WORD_1
	v_exp_f16_sdwa v49, v45 dst_sel:WORD_1 dst_unused:UNUSED_PRESERVE src0_sel:WORD_1
	s_nop 0
	v_pk_add_f16 v30, v30, v49
	v_pk_add_f16 v31, v31, v48
	v_rcp_f16_e32 v44, v30
	v_rcp_f16_sdwa v30, v30 dst_sel:DWORD dst_unused:UNUSED_PAD src0_sel:WORD_1
	v_pk_add_f16 v32, v32, v47
	v_rcp_f16_e32 v45, v31
	v_rcp_f16_sdwa v31, v31 dst_sel:DWORD dst_unused:UNUSED_PAD src0_sel:WORD_1
	v_pk_add_f16 v33, v33, v46
	v_rcp_f16_e32 v43, v32
	v_rcp_f16_sdwa v32, v32 dst_sel:DWORD dst_unused:UNUSED_PAD src0_sel:WORD_1
	v_rcp_f16_e32 v42, v33
	v_rcp_f16_sdwa v33, v33 dst_sel:DWORD dst_unused:UNUSED_PAD src0_sel:WORD_1
	v_pk_fma_f16 v25, v61, v49, v25
	v_pack_b32_f16 v30, v44, v30
	v_pk_fma_f16 v24, v60, v48, v24
	v_pk_mul_f16 v25, v25, v30
	v_pack_b32_f16 v30, v45, v31
	v_pk_fma_f16 v23, v59, v47, v23
	v_pk_mul_f16 v24, v24, v30
	v_pack_b32_f16 v30, v43, v32
	v_pk_fma_f16 v22, v58, v46, v22
	v_pk_mul_f16 v23, v23, v30
	v_pack_b32_f16 v30, v42, v33
	v_pk_mul_f16 v22, v22, v30
	s_waitcnt vmcnt(0)
	v_pk_mul_f16 v30, v185, v146 op_sel_hi:[0,1]
	v_pk_mul_f16 v31, v185, v147 op_sel_hi:[0,1]
	v_pk_mul_f16 v32, v185, v148 op_sel_hi:[0,1]
	v_pk_mul_f16 v33, v185, v149 op_sel_hi:[0,1]
	v_pk_mul_f16 v42, v183, v146 op_sel_hi:[0,1]
	v_pk_mul_f16 v43, v183, v147 op_sel_hi:[0,1]
	v_pk_mul_f16 v44, v183, v148 op_sel_hi:[0,1]
	v_pk_mul_f16 v45, v183, v149 op_sel_hi:[0,1]
	v_pk_mul_f16 v46, v184, v146 op_sel_hi:[0,1]
	v_pk_mul_f16 v47, v184, v147 op_sel_hi:[0,1]
	v_pk_mul_f16 v48, v184, v148 op_sel_hi:[0,1]
	v_pk_mul_f16 v49, v184, v149 op_sel_hi:[0,1]
	v_pk_fma_f16 v21, v21, v149, v33
	v_pk_fma_f16 v20, v20, v148, v32
	v_pk_fma_f16 v19, v19, v147, v31
	v_pk_fma_f16 v18, v18, v146, v30
	v_pk_fma_f16 v37, v37, v149, v45
	v_pk_fma_f16 v36, v36, v148, v44
	v_pk_fma_f16 v35, v35, v147, v43
	v_pk_fma_f16 v34, v34, v146, v42
	v_pk_fma_f16 v50, v57, v149, v49
	v_pk_fma_f16 v51, v56, v148, v48
	v_pk_fma_f16 v52, v55, v147, v47
	v_pk_fma_f16 v53, v54, v146, v46
	v_pk_fma_f16 v54, v77, v149, v33
	v_pk_fma_f16 v55, v76, v148, v32
	v_pk_fma_f16 v56, v75, v147, v31
	v_pk_fma_f16 v57, v74, v146, v30
	v_pk_maximum3_f16 v74, v18, v34, v53
	v_pk_maximum3_f16 v75, v19, v35, v52
	v_pk_maximum3_f16 v76, v20, v36, v51
	v_pk_maximum3_f16 v77, v21, v37, v50
	v_pk_fma_f16 v66, v105, v149, v45
	v_pk_fma_f16 v67, v104, v148, v44
	v_pk_fma_f16 v68, v103, v147, v43
	v_pk_fma_f16 v69, v102, v146, v42
	v_pk_fma_f16 v70, v121, v149, v49
	v_pk_fma_f16 v71, v120, v148, v48
	v_pk_fma_f16 v72, v119, v147, v47
	v_pk_fma_f16 v73, v118, v146, v46
	v_pk_fma_f16 v33, v133, v149, v33
	v_pk_fma_f16 v32, v132, v148, v32
	v_pk_fma_f16 v31, v131, v147, v31
	v_pk_fma_f16 v30, v130, v146, v30
	v_pk_fma_f16 v45, v141, v149, v45
	v_pk_fma_f16 v44, v140, v148, v44
	v_pk_fma_f16 v43, v139, v147, v43
	v_pk_fma_f16 v42, v138, v146, v42
	v_pk_fma_f16 v49, v145, v149, v49
	v_pk_fma_f16 v48, v144, v148, v48
	v_pk_fma_f16 v47, v143, v147, v47
	v_pk_fma_f16 v46, v142, v146, v46
	v_pk_maximum3_f16 v82, v57, v69, v73
	v_pk_maximum3_f16 v83, v56, v68, v72
	v_pk_maximum3_f16 v84, v55, v67, v71
	v_pk_maximum3_f16 v85, v54, v66, v70
	v_pk_maximum3_f16 v87, v31, v43, v47
	v_pk_maximum3_f16 v86, v30, v42, v46
	v_pk_maximum3_f16 v88, v32, v44, v48
	v_pk_maximum3_f16 v89, v33, v45, v49
	v_pk_maximum3_f16 v74, v74, v82, v86
	v_pk_maximum3_f16 v75, v75, v83, v87
	v_pk_maximum3_f16 v76, v76, v84, v88
	v_pk_maximum3_f16 v77, v77, v85, v89
	s_nop 0
	v_pk_add_f16 v18, v18, v74 neg_lo:[0,1] neg_hi:[0,1]
	v_pk_add_f16 v19, v19, v75 neg_lo:[0,1] neg_hi:[0,1]
	v_pk_add_f16 v20, v20, v76 neg_lo:[0,1] neg_hi:[0,1]
	v_pk_add_f16 v21, v21, v77 neg_lo:[0,1] neg_hi:[0,1]
	v_pk_add_f16 v34, v34, v74 neg_lo:[0,1] neg_hi:[0,1]
	v_exp_f16_sdwa v82, v18 dst_sel:WORD_0 dst_unused:UNUSED_PAD src0_sel:WORD_0
	v_exp_f16_sdwa v83, v19 dst_sel:WORD_0 dst_unused:UNUSED_PAD src0_sel:WORD_0
	v_exp_f16_sdwa v84, v20 dst_sel:WORD_0 dst_unused:UNUSED_PAD src0_sel:WORD_0
	v_exp_f16_sdwa v85, v21 dst_sel:WORD_0 dst_unused:UNUSED_PAD src0_sel:WORD_0
	v_exp_f16_sdwa v82, v18 dst_sel:WORD_1 dst_unused:UNUSED_PRESERVE src0_sel:WORD_1
	v_exp_f16_sdwa v83, v19 dst_sel:WORD_1 dst_unused:UNUSED_PRESERVE src0_sel:WORD_1
	v_exp_f16_sdwa v84, v20 dst_sel:WORD_1 dst_unused:UNUSED_PRESERVE src0_sel:WORD_1
	v_exp_f16_sdwa v85, v21 dst_sel:WORD_1 dst_unused:UNUSED_PRESERVE src0_sel:WORD_1
	v_pk_add_f16 v35, v35, v75 neg_lo:[0,1] neg_hi:[0,1]
	v_pk_add_f16 v18, v82, 0
	v_pk_add_f16 v19, v83, 0
	v_pk_add_f16 v20, v84, 0
	v_pk_add_f16 v21, v85, 0
	v_pk_fma_f16 v6, v6, v82, 0
	v_pk_fma_f16 v7, v7, v83, 0
	v_pk_fma_f16 v8, v8, v84, 0
	v_pk_fma_f16 v9, v9, v85, 0
	v_pk_add_f16 v36, v36, v76 neg_lo:[0,1] neg_hi:[0,1]
	v_pk_add_f16 v37, v37, v77 neg_lo:[0,1] neg_hi:[0,1]
	v_exp_f16_sdwa v82, v34 dst_sel:WORD_0 dst_unused:UNUSED_PAD src0_sel:WORD_0
	v_exp_f16_sdwa v83, v35 dst_sel:WORD_0 dst_unused:UNUSED_PAD src0_sel:WORD_0
	v_exp_f16_sdwa v84, v36 dst_sel:WORD_0 dst_unused:UNUSED_PAD src0_sel:WORD_0
	v_exp_f16_sdwa v85, v37 dst_sel:WORD_0 dst_unused:UNUSED_PAD src0_sel:WORD_0
	v_exp_f16_sdwa v82, v34 dst_sel:WORD_1 dst_unused:UNUSED_PRESERVE src0_sel:WORD_1
	v_exp_f16_sdwa v83, v35 dst_sel:WORD_1 dst_unused:UNUSED_PRESERVE src0_sel:WORD_1
	v_exp_f16_sdwa v84, v36 dst_sel:WORD_1 dst_unused:UNUSED_PRESERVE src0_sel:WORD_1
	v_exp_f16_sdwa v85, v37 dst_sel:WORD_1 dst_unused:UNUSED_PRESERVE src0_sel:WORD_1
	s_nop 0
	v_pk_add_f16 v21, v21, v85
	v_pk_add_f16 v20, v20, v84
	v_pk_add_f16 v19, v19, v83
	v_pk_add_f16 v18, v18, v82
	v_pk_fma_f16 v9, v13, v85, v9
	v_pk_fma_f16 v8, v12, v84, v8
	v_pk_fma_f16 v7, v11, v83, v7
	v_pk_fma_f16 v6, v10, v82, v6
	v_pk_add_f16 v10, v53, v74 neg_lo:[0,1] neg_hi:[0,1]
	v_pk_add_f16 v11, v52, v75 neg_lo:[0,1] neg_hi:[0,1]
	v_pk_add_f16 v12, v51, v76 neg_lo:[0,1] neg_hi:[0,1]
	v_pk_add_f16 v13, v50, v77 neg_lo:[0,1] neg_hi:[0,1]
	v_exp_f16_sdwa v34, v10 dst_sel:WORD_0 dst_unused:UNUSED_PAD src0_sel:WORD_0
	v_exp_f16_sdwa v35, v11 dst_sel:WORD_0 dst_unused:UNUSED_PAD src0_sel:WORD_0
	v_exp_f16_sdwa v36, v12 dst_sel:WORD_0 dst_unused:UNUSED_PAD src0_sel:WORD_0
	v_exp_f16_sdwa v37, v13 dst_sel:WORD_0 dst_unused:UNUSED_PAD src0_sel:WORD_0
	v_exp_f16_sdwa v34, v10 dst_sel:WORD_1 dst_unused:UNUSED_PRESERVE src0_sel:WORD_1
	v_exp_f16_sdwa v35, v11 dst_sel:WORD_1 dst_unused:UNUSED_PRESERVE src0_sel:WORD_1
	v_exp_f16_sdwa v36, v12 dst_sel:WORD_1 dst_unused:UNUSED_PRESERVE src0_sel:WORD_1
	v_exp_f16_sdwa v37, v13 dst_sel:WORD_1 dst_unused:UNUSED_PRESERVE src0_sel:WORD_1
	v_pk_add_f16 v10, v18, v34
	v_pk_add_f16 v11, v19, v35
	v_pk_add_f16 v12, v20, v36
	v_pk_add_f16 v13, v21, v37
	v_pk_fma_f16 v6, v14, v34, v6
	v_pk_fma_f16 v7, v15, v35, v7
	v_pk_fma_f16 v8, v16, v36, v8
	v_pk_fma_f16 v9, v17, v37, v9
	v_pk_add_f16 v14, v57, v74 neg_lo:[0,1] neg_hi:[0,1]
	v_pk_add_f16 v15, v56, v75 neg_lo:[0,1] neg_hi:[0,1]
	v_pk_add_f16 v16, v55, v76 neg_lo:[0,1] neg_hi:[0,1]
	v_pk_add_f16 v17, v54, v77 neg_lo:[0,1] neg_hi:[0,1]
	v_exp_f16_sdwa v18, v14 dst_sel:WORD_0 dst_unused:UNUSED_PAD src0_sel:WORD_0
	v_exp_f16_sdwa v19, v15 dst_sel:WORD_0 dst_unused:UNUSED_PAD src0_sel:WORD_0
	v_exp_f16_sdwa v20, v16 dst_sel:WORD_0 dst_unused:UNUSED_PAD src0_sel:WORD_0
	v_exp_f16_sdwa v21, v17 dst_sel:WORD_0 dst_unused:UNUSED_PAD src0_sel:WORD_0
	v_exp_f16_sdwa v18, v14 dst_sel:WORD_1 dst_unused:UNUSED_PRESERVE src0_sel:WORD_1
	v_exp_f16_sdwa v19, v15 dst_sel:WORD_1 dst_unused:UNUSED_PRESERVE src0_sel:WORD_1
	v_exp_f16_sdwa v20, v16 dst_sel:WORD_1 dst_unused:UNUSED_PRESERVE src0_sel:WORD_1
	v_exp_f16_sdwa v21, v17 dst_sel:WORD_1 dst_unused:UNUSED_PRESERVE src0_sel:WORD_1
	v_pk_add_f16 v14, v69, v74 neg_lo:[0,1] neg_hi:[0,1]
	v_pk_add_f16 v13, v13, v21
	v_pk_add_f16 v12, v12, v20
	v_pk_add_f16 v11, v11, v19
	v_pk_add_f16 v10, v10, v18
	v_pk_fma_f16 v9, v29, v21, v9
	v_pk_fma_f16 v8, v28, v20, v8
	v_pk_fma_f16 v7, v27, v19, v7
	v_pk_fma_f16 v6, v26, v18, v6
	v_pk_add_f16 v15, v68, v75 neg_lo:[0,1] neg_hi:[0,1]
	v_pk_add_f16 v16, v67, v76 neg_lo:[0,1] neg_hi:[0,1]
	v_pk_add_f16 v17, v66, v77 neg_lo:[0,1] neg_hi:[0,1]
	v_exp_f16_sdwa v18, v14 dst_sel:WORD_0 dst_unused:UNUSED_PAD src0_sel:WORD_0
	v_exp_f16_sdwa v19, v15 dst_sel:WORD_0 dst_unused:UNUSED_PAD src0_sel:WORD_0
	v_exp_f16_sdwa v20, v16 dst_sel:WORD_0 dst_unused:UNUSED_PAD src0_sel:WORD_0
	v_exp_f16_sdwa v21, v17 dst_sel:WORD_0 dst_unused:UNUSED_PAD src0_sel:WORD_0
	v_exp_f16_sdwa v18, v14 dst_sel:WORD_1 dst_unused:UNUSED_PRESERVE src0_sel:WORD_1
	v_exp_f16_sdwa v19, v15 dst_sel:WORD_1 dst_unused:UNUSED_PRESERVE src0_sel:WORD_1
	v_exp_f16_sdwa v20, v16 dst_sel:WORD_1 dst_unused:UNUSED_PRESERVE src0_sel:WORD_1
	v_exp_f16_sdwa v21, v17 dst_sel:WORD_1 dst_unused:UNUSED_PRESERVE src0_sel:WORD_1
	v_pk_add_f16 v14, v73, v74 neg_lo:[0,1] neg_hi:[0,1]
	v_pk_add_f16 v10, v10, v18
	v_pk_add_f16 v11, v11, v19
	v_pk_add_f16 v12, v12, v20
	v_pk_add_f16 v13, v13, v21
	v_pk_fma_f16 v6, v38, v18, v6
	v_pk_fma_f16 v7, v39, v19, v7
	v_pk_fma_f16 v8, v40, v20, v8
	v_pk_fma_f16 v9, v41, v21, v9
	v_pk_add_f16 v15, v72, v75 neg_lo:[0,1] neg_hi:[0,1]
	v_pk_add_f16 v16, v71, v76 neg_lo:[0,1] neg_hi:[0,1]
	v_pk_add_f16 v17, v70, v77 neg_lo:[0,1] neg_hi:[0,1]
	v_exp_f16_sdwa v18, v14 dst_sel:WORD_0 dst_unused:UNUSED_PAD src0_sel:WORD_0
	v_exp_f16_sdwa v19, v15 dst_sel:WORD_0 dst_unused:UNUSED_PAD src0_sel:WORD_0
	v_exp_f16_sdwa v20, v16 dst_sel:WORD_0 dst_unused:UNUSED_PAD src0_sel:WORD_0
	v_exp_f16_sdwa v21, v17 dst_sel:WORD_0 dst_unused:UNUSED_PAD src0_sel:WORD_0
	v_exp_f16_sdwa v18, v14 dst_sel:WORD_1 dst_unused:UNUSED_PRESERVE src0_sel:WORD_1
	v_exp_f16_sdwa v19, v15 dst_sel:WORD_1 dst_unused:UNUSED_PRESERVE src0_sel:WORD_1
	v_exp_f16_sdwa v20, v16 dst_sel:WORD_1 dst_unused:UNUSED_PRESERVE src0_sel:WORD_1
	v_exp_f16_sdwa v21, v17 dst_sel:WORD_1 dst_unused:UNUSED_PRESERVE src0_sel:WORD_1
	v_pk_add_f16 v14, v30, v74 neg_lo:[0,1] neg_hi:[0,1]
	v_pk_add_f16 v13, v13, v21
	v_pk_add_f16 v12, v12, v20
	v_pk_add_f16 v11, v11, v19
	v_pk_add_f16 v10, v10, v18
	v_pk_fma_f16 v9, v61, v21, v9
	v_pk_fma_f16 v8, v60, v20, v8
	v_pk_fma_f16 v7, v59, v19, v7
	v_pk_fma_f16 v6, v58, v18, v6
	v_pk_add_f16 v15, v31, v75 neg_lo:[0,1] neg_hi:[0,1]
	v_pk_add_f16 v16, v32, v76 neg_lo:[0,1] neg_hi:[0,1]
	v_pk_add_f16 v17, v33, v77 neg_lo:[0,1] neg_hi:[0,1]
	v_exp_f16_sdwa v18, v14 dst_sel:WORD_0 dst_unused:UNUSED_PAD src0_sel:WORD_0
	v_exp_f16_sdwa v19, v15 dst_sel:WORD_0 dst_unused:UNUSED_PAD src0_sel:WORD_0
	v_exp_f16_sdwa v20, v16 dst_sel:WORD_0 dst_unused:UNUSED_PAD src0_sel:WORD_0
	v_exp_f16_sdwa v21, v17 dst_sel:WORD_0 dst_unused:UNUSED_PAD src0_sel:WORD_0
	v_exp_f16_sdwa v18, v14 dst_sel:WORD_1 dst_unused:UNUSED_PRESERVE src0_sel:WORD_1
	v_exp_f16_sdwa v19, v15 dst_sel:WORD_1 dst_unused:UNUSED_PRESERVE src0_sel:WORD_1
	v_exp_f16_sdwa v20, v16 dst_sel:WORD_1 dst_unused:UNUSED_PRESERVE src0_sel:WORD_1
	v_exp_f16_sdwa v21, v17 dst_sel:WORD_1 dst_unused:UNUSED_PRESERVE src0_sel:WORD_1
	v_pk_add_f16 v10, v10, v18
	v_pk_add_f16 v11, v11, v19
	v_pk_add_f16 v12, v12, v20
	v_pk_add_f16 v13, v13, v21
	v_pk_fma_f16 v14, v78, v18, v6
	v_pk_fma_f16 v15, v79, v19, v7
	v_pk_fma_f16 v16, v80, v20, v8
	v_pk_fma_f16 v17, v81, v21, v9
	v_pk_add_f16 v6, v42, v74 neg_lo:[0,1] neg_hi:[0,1]
	v_pk_add_f16 v7, v43, v75 neg_lo:[0,1] neg_hi:[0,1]
	v_pk_add_f16 v8, v44, v76 neg_lo:[0,1] neg_hi:[0,1]
	v_pk_add_f16 v9, v45, v77 neg_lo:[0,1] neg_hi:[0,1]
	v_exp_f16_sdwa v18, v6 dst_sel:WORD_0 dst_unused:UNUSED_PAD src0_sel:WORD_0
	v_exp_f16_sdwa v19, v7 dst_sel:WORD_0 dst_unused:UNUSED_PAD src0_sel:WORD_0
	v_exp_f16_sdwa v20, v8 dst_sel:WORD_0 dst_unused:UNUSED_PAD src0_sel:WORD_0
	v_exp_f16_sdwa v21, v9 dst_sel:WORD_0 dst_unused:UNUSED_PAD src0_sel:WORD_0
	v_exp_f16_sdwa v18, v6 dst_sel:WORD_1 dst_unused:UNUSED_PRESERVE src0_sel:WORD_1
	v_exp_f16_sdwa v19, v7 dst_sel:WORD_1 dst_unused:UNUSED_PRESERVE src0_sel:WORD_1
	v_exp_f16_sdwa v20, v8 dst_sel:WORD_1 dst_unused:UNUSED_PRESERVE src0_sel:WORD_1
	v_exp_f16_sdwa v21, v9 dst_sel:WORD_1 dst_unused:UNUSED_PRESERVE src0_sel:WORD_1
	s_nop 0
	v_pk_add_f16 v9, v13, v21
	v_pk_add_f16 v8, v12, v20
	v_pk_add_f16 v7, v11, v19
	v_pk_add_f16 v6, v10, v18
	v_pk_fma_f16 v13, v93, v21, v17
	v_pk_fma_f16 v12, v92, v20, v16
	v_pk_fma_f16 v11, v91, v19, v15
	v_pk_fma_f16 v10, v90, v18, v14
	v_pk_add_f16 v18, v46, v74 neg_lo:[0,1] neg_hi:[0,1]
	v_pk_add_f16 v19, v47, v75 neg_lo:[0,1] neg_hi:[0,1]
	v_pk_add_f16 v20, v48, v76 neg_lo:[0,1] neg_hi:[0,1]
	v_pk_add_f16 v21, v49, v77 neg_lo:[0,1] neg_hi:[0,1]
	v_exp_f16_sdwa v14, v18 dst_sel:WORD_0 dst_unused:UNUSED_PAD src0_sel:WORD_0
	v_exp_f16_sdwa v17, v19 dst_sel:WORD_0 dst_unused:UNUSED_PAD src0_sel:WORD_0
	v_exp_f16_sdwa v15, v20 dst_sel:WORD_0 dst_unused:UNUSED_PAD src0_sel:WORD_0
	v_exp_f16_sdwa v16, v21 dst_sel:WORD_0 dst_unused:UNUSED_PAD src0_sel:WORD_0
	v_exp_f16_sdwa v14, v18 dst_sel:WORD_1 dst_unused:UNUSED_PRESERVE src0_sel:WORD_1
	v_exp_f16_sdwa v17, v19 dst_sel:WORD_1 dst_unused:UNUSED_PRESERVE src0_sel:WORD_1
	v_exp_f16_sdwa v15, v20 dst_sel:WORD_1 dst_unused:UNUSED_PRESERVE src0_sel:WORD_1
	v_exp_f16_sdwa v16, v21 dst_sel:WORD_1 dst_unused:UNUSED_PRESERVE src0_sel:WORD_1
	s_nop 0
.LBB3_45:
	s_and_b64 vcc, exec, s[4:5]
	s_cbranch_vccz .LBB3_6
	s_load_dwordx2 s[0:1], s[22:23], 0x18
	s_waitcnt lgkmcnt(0)
	s_load_dwordx2 s[6:7], s[0:1], 0x0
	s_load_dword s28, s[0:1], 0x8
	v_cmp_lt_u32_e64 s[64:65], 0, v182
	v_cmp_gt_u32_e64 s[66:67], 63, v182
	v_cmp_lt_u32_e64 s[68:69], 0, v162
	v_cmp_gt_u32_e64 s[70:71], 60, v162
	buffer_load_dwordx4 v[184:187], v180, s[16:19], 0 offen
	s_and_b64 s[72:73], s[68:69], s[64:65]
	s_and_b64 s[74:75], s[68:69], s[66:67]
	s_and_b64 s[76:77], s[70:71], s[64:65]
	s_and_b64 s[78:79], s[70:71], s[66:67]
	v_add_u32_e32 v249, 0xfffe7c00, v180
	v_add_u32_e32 v250, 0xfffe8000, v180
	s_mov_b64 exec, s[72:73]
	buffer_load_dwordx4 v[110:113], v249, s[16:19], 0 offen
	s_mov_b64 exec, -1
	s_mov_b64 exec, s[68:69]
	buffer_load_dwordx4 v[126:129], v250, s[16:19], 0 offen offset:512
	s_mov_b64 exec, -1
	s_mov_b64 exec, s[74:75]
	buffer_load_dwordx4 v[138:141], v250, s[16:19], 0 offen offset:2048
	s_mov_b64 exec, -1
	v_add_u32_e32 v249, 0xfffffc00, v180
	s_mov_b64 exec, s[64:65]
	buffer_load_dwordx4 v[86:89], v249, s[16:19], 0 offen
	s_mov_b64 exec, -1
	buffer_load_dwordx4 v[106:109], v180, s[16:19], 0 offen offset:512
	s_mov_b64 exec, s[66:67]
	buffer_load_dwordx4 v[122:125], v180, s[16:19], 0 offen offset:2048
	s_mov_b64 exec, -1
	v_add_u32_e32 v249, 0x17c00, v180
	v_add_u32_e32 v250, 0x18000, v180
	s_mov_b64 exec, s[64:65]
	buffer_load_dwordx4 v[50:53], v249, s[16:19], 0 offen
	s_mov_b64 exec, -1
	buffer_load_dwordx4 v[66:69], v250, s[16:19], 0 offen offset:512
	s_mov_b64 exec, s[66:67]
	buffer_load_dwordx4 v[94:97], v250, s[16:19], 0 offen offset:2048
	s_mov_b64 exec, -1
	v_add_u32_e32 v249, 0xfffe7c00, v180
	v_add_u32_e32 v250, 0xfffe8000, v180
	s_mov_b64 exec, s[72:73]
	buffer_load_dwordx4 v[78:81], v249, s[16:19], 0 offen offset:512
	s_mov_b64 exec, -1
	s_mov_b64 exec, s[68:69]
	buffer_load_dwordx4 v[102:105], v250, s[16:19], 0 offen offset:1024
	s_mov_b64 exec, -1
	s_mov_b64 exec, s[74:75]
	buffer_load_dwordx4 v[118:121], v250, s[16:19], 0 offen offset:2560
	s_mov_b64 exec, -1
	v_add_u32_e32 v249, 0xfffffc00, v180
	s_mov_b64 exec, s[64:65]
	buffer_load_dwordx4 v[46:49], v249, s[16:19], 0 offen offset:512
	s_mov_b64 exec, -1
	buffer_load_dwordx4 v[62:65], v180, s[16:19], 0 offen offset:1024
	s_mov_b64 exec, s[66:67]
	buffer_load_dwordx4 v[82:85], v180, s[16:19], 0 offen offset:2560
	s_mov_b64 exec, -1
	v_add_u32_e32 v249, 0x17c00, v180
	v_add_u32_e32 v250, 0x18000, v180
	s_mov_b64 exec, s[64:65]
	buffer_load_dwordx4 v[22:25], v249, s[16:19], 0 offen offset:512
	s_mov_b64 exec, -1
	buffer_load_dwordx4 v[34:37], v250, s[16:19], 0 offen offset:1024
	s_mov_b64 exec, s[66:67]
	buffer_load_dwordx4 v[42:45], v250, s[16:19], 0 offen offset:2560
	s_mov_b64 exec, -1
	v_add_u32_e32 v249, 0x18000, v180
	buffer_load_dwordx4 v[154:157], v249, s[16:19], 0 offen
	v_add_u32_e32 v250, 0x30000, v180
	buffer_load_dwordx4 v[150:153], v250, s[16:19], 0 offen
	v_add_u32_e32 v249, 0x48000, v180
	buffer_load_dwordx4 v[146:149], v249, s[16:19], 0 offen
	v_add_u32_e32 v249, 0x2fc00, v180
	v_add_u32_e32 v250, 0x30000, v180
	v_add_u32_e32 v251, 0x47c00, v180
	v_add_u32_e32 v252, 0x48000, v180
	v_add_u32_e32 v253, 0x5fc00, v180
	v_add_u32_e32 v254, 0x60000, v180
	s_cmp_lg_u32 s93, 0
	s_cbranch_scc1 .Lmybg_B2
	s_waitcnt vmcnt(22)
	v_cvt_pk_f16_f32 v172, v230, v231
	v_cvt_pk_f16_f32 v173, v234, v235
	v_cvt_pk_f16_f32 v174, v232, v233
	v_cvt_pk_f16_f32 v175, v236, v237
	v_cvt_pk_f16_f32 v176, v238, v239
	v_cvt_pk_f16_f32 v177, v242, v243
	v_cvt_pk_f16_f32 v178, v240, v241
	v_cvt_pk_f16_f32 v179, v244, v245
	s_mov_b32 s93, 1

.LBB4_2:
	s_waitcnt vmcnt(12)
	v_pk_mul_f16 v161, v160, v162 op_sel_hi:[0,1]
	v_pk_mul_f16 v206, v160, v165 op_sel_hi:[0,1]
	v_pk_mul_f16 v210, v158, v165 op_sel_hi:[0,1]
	v_pk_mul_f16 v214, v159, v165 op_sel_hi:[0,1]
	v_pk_mul_f16 v200, v160, v163 op_sel_hi:[0,1]
	v_pk_mul_f16 v201, v160, v164 op_sel_hi:[0,1]
	v_pk_mul_f16 v207, v158, v162 op_sel_hi:[0,1]
	v_pk_mul_f16 v208, v158, v163 op_sel_hi:[0,1]
	v_pk_mul_f16 v209, v158, v164 op_sel_hi:[0,1]
	v_pk_mul_f16 v211, v159, v162 op_sel_hi:[0,1]
	v_pk_mul_f16 v212, v159, v163 op_sel_hi:[0,1]
	v_pk_mul_f16 v213, v159, v164 op_sel_hi:[0,1]
	v_pk_fma_f16 v117, v117, v165, v206
	v_pk_fma_f16 v114, v114, v162, v161
	v_pk_fma_f16 v133, v133, v165, v206
	v_pk_fma_f16 v130, v130, v162, v161
	v_pk_fma_f16 v141, v141, v165, v206
	v_pk_fma_f16 v138, v138, v162, v161
	v_pk_fma_f16 v161, v89, v165, v210
	v_pk_fma_f16 v215, v113, v165, v210
	v_pk_fma_f16 v210, v129, v165, v210
	v_pk_fma_f16 v219, v57, v165, v214
	v_pk_fma_f16 v223, v77, v165, v214
	v_pk_fma_f16 v165, v101, v165, v214
	v_pk_maximum3_f16 v214, v117, v133, v141
	v_pk_fma_f16 v116, v116, v164, v201
	v_pk_fma_f16 v115, v115, v163, v200
	v_pk_fma_f16 v132, v132, v164, v201
	v_pk_fma_f16 v131, v131, v163, v200
	v_pk_fma_f16 v140, v140, v164, v201
	v_pk_fma_f16 v139, v139, v163, v200
	v_pk_fma_f16 v200, v88, v164, v209
	v_pk_fma_f16 v201, v87, v163, v208
	v_pk_fma_f16 v206, v86, v162, v207
	v_pk_fma_f16 v216, v112, v164, v209
	v_pk_fma_f16 v217, v111, v163, v208
	v_pk_fma_f16 v218, v110, v162, v207
	v_pk_fma_f16 v209, v128, v164, v209
	v_pk_fma_f16 v208, v127, v163, v208
	v_pk_fma_f16 v207, v126, v162, v207
	v_pk_fma_f16 v220, v56, v164, v213
	v_pk_fma_f16 v221, v55, v163, v212
	v_pk_fma_f16 v222, v54, v162, v211
	v_pk_fma_f16 v224, v76, v164, v213
	v_pk_fma_f16 v225, v75, v163, v212
	v_pk_fma_f16 v226, v74, v162, v211
	v_pk_fma_f16 v164, v100, v164, v213
	v_pk_fma_f16 v163, v99, v163, v212
	v_pk_fma_f16 v162, v98, v162, v211
	v_pk_maximum3_f16 v211, v114, v130, v138
	v_pk_maximum3_f16 v212, v115, v131, v139
	v_pk_maximum3_f16 v213, v116, v132, v140
	v_pk_maximum3_f16 v230, v161, v215, v210
	v_pk_maximum3_f16 v234, v219, v223, v165
	v_pk_maximum3_f16 v227, v206, v218, v207
	v_pk_maximum3_f16 v228, v201, v217, v208
	v_pk_maximum3_f16 v229, v200, v216, v209
	v_pk_maximum3_f16 v231, v222, v226, v162
	v_pk_maximum3_f16 v232, v221, v225, v163
	v_pk_maximum3_f16 v214, v214, v230, v234
	v_pk_maximum3_f16 v233, v220, v224, v164
	v_pk_maximum3_f16 v211, v211, v227, v231
	v_pk_maximum3_f16 v212, v212, v228, v232
	v_pk_maximum3_f16 v213, v213, v229, v233
	v_pk_add_f16 v117, v117, v214 neg_lo:[0,1] neg_hi:[0,1]
	v_pk_add_f16 v114, v114, v211 neg_lo:[0,1] neg_hi:[0,1]
	v_pk_add_f16 v115, v115, v212 neg_lo:[0,1] neg_hi:[0,1]
	v_pk_add_f16 v116, v116, v213 neg_lo:[0,1] neg_hi:[0,1]
	v_pk_add_f16 v130, v130, v211 neg_lo:[0,1] neg_hi:[0,1]
	v_exp_f16_sdwa v227, v114 dst_sel:WORD_0 dst_unused:UNUSED_PAD src0_sel:WORD_0
	v_exp_f16_sdwa v228, v115 dst_sel:WORD_0 dst_unused:UNUSED_PAD src0_sel:WORD_0
	v_exp_f16_sdwa v229, v116 dst_sel:WORD_0 dst_unused:UNUSED_PAD src0_sel:WORD_0
	v_exp_f16_sdwa v230, v117 dst_sel:WORD_0 dst_unused:UNUSED_PAD src0_sel:WORD_0
	v_exp_f16_sdwa v227, v114 dst_sel:WORD_1 dst_unused:UNUSED_PRESERVE src0_sel:WORD_1
	v_exp_f16_sdwa v228, v115 dst_sel:WORD_1 dst_unused:UNUSED_PRESERVE src0_sel:WORD_1
	v_exp_f16_sdwa v229, v116 dst_sel:WORD_1 dst_unused:UNUSED_PRESERVE src0_sel:WORD_1
	v_exp_f16_sdwa v230, v117 dst_sel:WORD_1 dst_unused:UNUSED_PRESERVE src0_sel:WORD_1
	v_pk_add_f16 v131, v131, v212 neg_lo:[0,1] neg_hi:[0,1]
	v_pk_add_f16 v117, v227, 0
	s_waitcnt vmcnt(3)
	v_pk_fma_f16 v73, v73, v230, 0
	v_pk_add_f16 v114, v230, 0
	v_pk_add_f16 v115, v229, 0
	v_pk_add_f16 v116, v228, 0
	v_pk_fma_f16 v72, v72, v229, 0
	v_pk_fma_f16 v71, v71, v228, 0
	s_mov_b64 exec, s[64:65]
	buffer_load_dwordx4 v[26:29], v245, s[12:15], 0 offen
	buffer_load_dwordx4 v[10:13], v245, s[12:15], 0 offen offset:512
	s_mov_b64 exec, -1
	v_pk_fma_f16 v70, v70, v227, 0
	v_pk_add_f16 v132, v132, v213 neg_lo:[0,1] neg_hi:[0,1]
	v_pk_add_f16 v133, v133, v214 neg_lo:[0,1] neg_hi:[0,1]
	v_exp_f16_sdwa v227, v130 dst_sel:WORD_0 dst_unused:UNUSED_PAD src0_sel:WORD_0
	v_exp_f16_sdwa v228, v131 dst_sel:WORD_0 dst_unused:UNUSED_PAD src0_sel:WORD_0
	v_exp_f16_sdwa v229, v132 dst_sel:WORD_0 dst_unused:UNUSED_PAD src0_sel:WORD_0
	v_exp_f16_sdwa v230, v133 dst_sel:WORD_0 dst_unused:UNUSED_PAD src0_sel:WORD_0
	v_exp_f16_sdwa v227, v130 dst_sel:WORD_1 dst_unused:UNUSED_PRESERVE src0_sel:WORD_1
	v_exp_f16_sdwa v228, v131 dst_sel:WORD_1 dst_unused:UNUSED_PRESERVE src0_sel:WORD_1
	v_exp_f16_sdwa v229, v132 dst_sel:WORD_1 dst_unused:UNUSED_PRESERVE src0_sel:WORD_1
	v_exp_f16_sdwa v230, v133 dst_sel:WORD_1 dst_unused:UNUSED_PRESERVE src0_sel:WORD_1
	v_pk_add_f16 v117, v117, v227
	v_pk_fma_f16 v73, v97, v230, v73
	v_pk_add_f16 v97, v141, v214 neg_lo:[0,1] neg_hi:[0,1]
	v_pk_add_f16 v116, v116, v228
	v_pk_add_f16 v115, v115, v229
	v_pk_add_f16 v114, v114, v230
	buffer_load_dwordx4 v[38:41], v246, s[12:15], 0 offen offset:512
	buffer_load_dwordx4 v[14:17], v246, s[12:15], 0 offen offset:1024
	v_pk_fma_f16 v70, v94, v227, v70
	v_pk_fma_f16 v71, v95, v228, v71
	v_pk_fma_f16 v72, v96, v229, v72
	v_pk_add_f16 v94, v138, v211 neg_lo:[0,1] neg_hi:[0,1]
	v_pk_add_f16 v95, v139, v212 neg_lo:[0,1] neg_hi:[0,1]
	v_pk_add_f16 v96, v140, v213 neg_lo:[0,1] neg_hi:[0,1]
	v_exp_f16_sdwa v130, v94 dst_sel:WORD_0 dst_unused:UNUSED_PAD src0_sel:WORD_0
	v_exp_f16_sdwa v131, v95 dst_sel:WORD_0 dst_unused:UNUSED_PAD src0_sel:WORD_0
	v_exp_f16_sdwa v132, v96 dst_sel:WORD_0 dst_unused:UNUSED_PAD src0_sel:WORD_0
	v_exp_f16_sdwa v133, v97 dst_sel:WORD_0 dst_unused:UNUSED_PAD src0_sel:WORD_0
	v_exp_f16_sdwa v130, v94 dst_sel:WORD_1 dst_unused:UNUSED_PRESERVE src0_sel:WORD_1
	v_exp_f16_sdwa v131, v95 dst_sel:WORD_1 dst_unused:UNUSED_PRESERVE src0_sel:WORD_1
	v_exp_f16_sdwa v132, v96 dst_sel:WORD_1 dst_unused:UNUSED_PRESERVE src0_sel:WORD_1
	v_exp_f16_sdwa v133, v97 dst_sel:WORD_1 dst_unused:UNUSED_PRESERVE src0_sel:WORD_1
	v_pk_add_f16 v97, v117, v130
	v_pk_add_f16 v94, v114, v133
	v_pk_add_f16 v95, v115, v132
	s_mov_b64 exec, s[66:67]
	buffer_load_dwordx4 v[58:61], v246, s[12:15], 0 offen offset:2048
	buffer_load_dwordx4 v[18:21], v246, s[12:15], 0 offen offset:2560
	s_mov_b64 exec, -1
	v_pk_add_f16 v96, v116, v131
	v_pk_fma_f16 v73, v121, v133, v73
	v_pk_fma_f16 v72, v120, v132, v72
	v_pk_fma_f16 v71, v119, v131, v71
	v_pk_fma_f16 v70, v118, v130, v70
	v_pk_add_f16 v114, v206, v211 neg_lo:[0,1] neg_hi:[0,1]
	v_pk_add_f16 v115, v201, v212 neg_lo:[0,1] neg_hi:[0,1]
	v_pk_add_f16 v116, v200, v213 neg_lo:[0,1] neg_hi:[0,1]
	s_mov_b64 exec, s[64:65]
	buffer_load_dwordx4 v[78:81], v247, s[12:15], 0 offen
	buffer_load_dwordx4 v[30:33], v247, s[12:15], 0 offen offset:512
	s_mov_b64 exec, -1
	v_pk_add_f16 v117, v161, v214 neg_lo:[0,1] neg_hi:[0,1]
	v_exp_f16_sdwa v118, v114 dst_sel:WORD_0 dst_unused:UNUSED_PAD src0_sel:WORD_0
	v_exp_f16_sdwa v119, v115 dst_sel:WORD_0 dst_unused:UNUSED_PAD src0_sel:WORD_0
	v_exp_f16_sdwa v120, v116 dst_sel:WORD_0 dst_unused:UNUSED_PAD src0_sel:WORD_0
	v_exp_f16_sdwa v121, v117 dst_sel:WORD_0 dst_unused:UNUSED_PAD src0_sel:WORD_0
	v_exp_f16_sdwa v118, v114 dst_sel:WORD_1 dst_unused:UNUSED_PRESERVE src0_sel:WORD_1
	v_exp_f16_sdwa v119, v115 dst_sel:WORD_1 dst_unused:UNUSED_PRESERVE src0_sel:WORD_1
	v_exp_f16_sdwa v120, v116 dst_sel:WORD_1 dst_unused:UNUSED_PRESERVE src0_sel:WORD_1
	v_exp_f16_sdwa v121, v117 dst_sel:WORD_1 dst_unused:UNUSED_PRESERVE src0_sel:WORD_1
	v_pk_add_f16 v114, v218, v211 neg_lo:[0,1] neg_hi:[0,1]
	v_pk_add_f16 v97, v97, v118
	v_pk_add_f16 v96, v96, v119
	v_pk_add_f16 v95, v95, v120
	v_pk_add_f16 v94, v94, v121
	v_pk_fma_f16 v70, v42, v118, v70
	v_pk_fma_f16 v71, v43, v119, v71
	v_pk_fma_f16 v72, v44, v120, v72
	v_pk_fma_f16 v73, v45, v121, v73
	buffer_load_dwordx4 v[106:109], v248, s[12:15], 0 offen offset:512
	buffer_load_dwordx4 v[46:49], v248, s[12:15], 0 offen offset:1024
	v_pk_add_f16 v115, v217, v212 neg_lo:[0,1] neg_hi:[0,1]
	v_pk_add_f16 v116, v216, v213 neg_lo:[0,1] neg_hi:[0,1]
	v_pk_add_f16 v117, v215, v214 neg_lo:[0,1] neg_hi:[0,1]
	v_exp_f16_sdwa v118, v114 dst_sel:WORD_0 dst_unused:UNUSED_PAD src0_sel:WORD_0
	v_exp_f16_sdwa v119, v115 dst_sel:WORD_0 dst_unused:UNUSED_PAD src0_sel:WORD_0
	v_exp_f16_sdwa v120, v116 dst_sel:WORD_0 dst_unused:UNUSED_PAD src0_sel:WORD_0
	v_exp_f16_sdwa v121, v117 dst_sel:WORD_0 dst_unused:UNUSED_PAD src0_sel:WORD_0
	v_exp_f16_sdwa v118, v114 dst_sel:WORD_1 dst_unused:UNUSED_PRESERVE src0_sel:WORD_1
	v_exp_f16_sdwa v119, v115 dst_sel:WORD_1 dst_unused:UNUSED_PRESERVE src0_sel:WORD_1
	v_exp_f16_sdwa v120, v116 dst_sel:WORD_1 dst_unused:UNUSED_PRESERVE src0_sel:WORD_1
	v_exp_f16_sdwa v121, v117 dst_sel:WORD_1 dst_unused:UNUSED_PRESERVE src0_sel:WORD_1
	v_pk_add_f16 v114, v207, v211 neg_lo:[0,1] neg_hi:[0,1]
	v_pk_add_f16 v97, v97, v118
	v_pk_add_f16 v94, v94, v121
	v_pk_add_f16 v95, v95, v120
	v_pk_add_f16 v96, v96, v119
	v_pk_fma_f16 v73, v69, v121, v73
	s_mov_b64 exec, s[66:67]
	buffer_load_dwordx4 v[122:125], v248, s[12:15], 0 offen offset:2048
	buffer_load_dwordx4 v[62:65], v248, s[12:15], 0 offen offset:2560
	s_mov_b64 exec, -1
	v_pk_fma_f16 v72, v68, v120, v72
	v_pk_fma_f16 v71, v67, v119, v71
	v_pk_fma_f16 v70, v66, v118, v70
	v_pk_add_f16 v115, v208, v212 neg_lo:[0,1] neg_hi:[0,1]
	v_pk_add_f16 v116, v209, v213 neg_lo:[0,1] neg_hi:[0,1]
	v_pk_add_f16 v117, v210, v214 neg_lo:[0,1] neg_hi:[0,1]
	v_exp_f16_sdwa v118, v114 dst_sel:WORD_0 dst_unused:UNUSED_PAD src0_sel:WORD_0
	v_exp_f16_sdwa v119, v115 dst_sel:WORD_0 dst_unused:UNUSED_PAD src0_sel:WORD_0
	v_exp_f16_sdwa v120, v116 dst_sel:WORD_0 dst_unused:UNUSED_PAD src0_sel:WORD_0
	v_exp_f16_sdwa v121, v117 dst_sel:WORD_0 dst_unused:UNUSED_PAD src0_sel:WORD_0
	v_exp_f16_sdwa v118, v114 dst_sel:WORD_1 dst_unused:UNUSED_PRESERVE src0_sel:WORD_1
	v_exp_f16_sdwa v119, v115 dst_sel:WORD_1 dst_unused:UNUSED_PRESERVE src0_sel:WORD_1
	v_exp_f16_sdwa v120, v116 dst_sel:WORD_1 dst_unused:UNUSED_PRESERVE src0_sel:WORD_1
	v_exp_f16_sdwa v121, v117 dst_sel:WORD_1 dst_unused:UNUSED_PRESERVE src0_sel:WORD_1
	v_pk_add_f16 v114, v222, v211 neg_lo:[0,1] neg_hi:[0,1]
	v_pk_add_f16 v97, v97, v118
	v_pk_add_f16 v96, v96, v119
	s_mov_b64 exec, s[76:77]
	buffer_load_dwordx4 v[134:137], v249, s[12:15], 0 offen
	buffer_load_dwordx4 v[82:85], v249, s[12:15], 0 offen offset:512
	s_mov_b64 exec, -1
	v_pk_add_f16 v95, v95, v120
	v_pk_add_f16 v94, v94, v121
	v_pk_fma_f16 v70, v90, v118, v70
	v_pk_fma_f16 v71, v91, v119, v71
	v_pk_fma_f16 v72, v92, v120, v72
	v_pk_fma_f16 v73, v93, v121, v73
	v_pk_add_f16 v115, v221, v212 neg_lo:[0,1] neg_hi:[0,1]
	v_pk_add_f16 v116, v220, v213 neg_lo:[0,1] neg_hi:[0,1]
	s_mov_b64 exec, s[70:71]
	buffer_load_dwordx4 v[142:145], v250, s[12:15], 0 offen offset:512
	buffer_load_dwordx4 v[102:105], v250, s[12:15], 0 offen offset:1024
	s_mov_b64 exec, -1
	v_pk_add_f16 v117, v219, v214 neg_lo:[0,1] neg_hi:[0,1]
	v_exp_f16_sdwa v118, v114 dst_sel:WORD_0 dst_unused:UNUSED_PAD src0_sel:WORD_0
	v_exp_f16_sdwa v119, v115 dst_sel:WORD_0 dst_unused:UNUSED_PAD src0_sel:WORD_0
	v_exp_f16_sdwa v120, v116 dst_sel:WORD_0 dst_unused:UNUSED_PAD src0_sel:WORD_0
	v_exp_f16_sdwa v121, v117 dst_sel:WORD_0 dst_unused:UNUSED_PAD src0_sel:WORD_0
	v_exp_f16_sdwa v118, v114 dst_sel:WORD_1 dst_unused:UNUSED_PRESERVE src0_sel:WORD_1
	v_exp_f16_sdwa v119, v115 dst_sel:WORD_1 dst_unused:UNUSED_PRESERVE src0_sel:WORD_1
	v_exp_f16_sdwa v120, v116 dst_sel:WORD_1 dst_unused:UNUSED_PRESERVE src0_sel:WORD_1
	v_exp_f16_sdwa v121, v117 dst_sel:WORD_1 dst_unused:UNUSED_PRESERVE src0_sel:WORD_1
	v_pk_add_f16 v114, v226, v211 neg_lo:[0,1] neg_hi:[0,1]
	v_pk_add_f16 v97, v97, v118
	v_pk_add_f16 v94, v94, v121
	v_pk_add_f16 v95, v95, v120
	v_pk_add_f16 v96, v96, v119
	v_pk_fma_f16 v73, v25, v121, v73
	v_pk_fma_f16 v72, v24, v120, v72
	v_pk_fma_f16 v71, v23, v119, v71
	s_mov_b64 exec, s[78:79]
	buffer_load_dwordx4 v[6:9], v250, s[12:15], 0 offen offset:2048
	buffer_load_dwordx4 v[2:5], v250, s[12:15], 0 offen offset:2560
	s_mov_b64 exec, -1
	v_pk_fma_f16 v70, v22, v118, v70
	v_pk_add_f16 v115, v225, v212 neg_lo:[0,1] neg_hi:[0,1]
	v_pk_add_f16 v116, v224, v213 neg_lo:[0,1] neg_hi:[0,1]
	v_pk_add_f16 v117, v223, v214 neg_lo:[0,1] neg_hi:[0,1]
	v_exp_f16_sdwa v118, v114 dst_sel:WORD_0 dst_unused:UNUSED_PAD src0_sel:WORD_0
	v_exp_f16_sdwa v119, v115 dst_sel:WORD_0 dst_unused:UNUSED_PAD src0_sel:WORD_0
	v_exp_f16_sdwa v120, v116 dst_sel:WORD_0 dst_unused:UNUSED_PAD src0_sel:WORD_0
	v_exp_f16_sdwa v121, v117 dst_sel:WORD_0 dst_unused:UNUSED_PAD src0_sel:WORD_0
	v_exp_f16_sdwa v118, v114 dst_sel:WORD_1 dst_unused:UNUSED_PRESERVE src0_sel:WORD_1
	v_exp_f16_sdwa v119, v115 dst_sel:WORD_1 dst_unused:UNUSED_PRESERVE src0_sel:WORD_1
	v_exp_f16_sdwa v120, v116 dst_sel:WORD_1 dst_unused:UNUSED_PRESERVE src0_sel:WORD_1
	v_exp_f16_sdwa v121, v117 dst_sel:WORD_1 dst_unused:UNUSED_PRESERVE src0_sel:WORD_1
	v_pk_add_f16 v114, v162, v211 neg_lo:[0,1] neg_hi:[0,1]
	v_pk_add_f16 v97, v97, v118
	v_pk_add_f16 v96, v96, v119
	v_pk_add_f16 v95, v95, v120
	v_pk_add_f16 v94, v94, v121
	v_pk_fma_f16 v70, v34, v118, v70
	v_pk_fma_f16 v71, v35, v119, v71
	v_pk_fma_f16 v72, v36, v120, v72
	v_pk_fma_f16 v73, v37, v121, v73
	v_pk_add_f16 v115, v163, v212 neg_lo:[0,1] neg_hi:[0,1]
	v_pk_add_f16 v116, v164, v213 neg_lo:[0,1] neg_hi:[0,1]
	v_pk_add_f16 v117, v165, v214 neg_lo:[0,1] neg_hi:[0,1]
	v_exp_f16_sdwa v118, v114 dst_sel:WORD_0 dst_unused:UNUSED_PAD src0_sel:WORD_0
	v_exp_f16_sdwa v119, v115 dst_sel:WORD_0 dst_unused:UNUSED_PAD src0_sel:WORD_0
	v_exp_f16_sdwa v120, v116 dst_sel:WORD_0 dst_unused:UNUSED_PAD src0_sel:WORD_0
	v_exp_f16_sdwa v121, v117 dst_sel:WORD_0 dst_unused:UNUSED_PAD src0_sel:WORD_0
	v_exp_f16_sdwa v118, v114 dst_sel:WORD_1 dst_unused:UNUSED_PRESERVE src0_sel:WORD_1
	v_exp_f16_sdwa v119, v115 dst_sel:WORD_1 dst_unused:UNUSED_PRESERVE src0_sel:WORD_1
	v_exp_f16_sdwa v120, v116 dst_sel:WORD_1 dst_unused:UNUSED_PRESERVE src0_sel:WORD_1
	v_exp_f16_sdwa v121, v117 dst_sel:WORD_1 dst_unused:UNUSED_PRESERVE src0_sel:WORD_1
	v_pk_add_f16 v97, v97, v118
	v_pk_add_f16 v96, v96, v119
	v_rcp_f16_e32 v114, v97
	v_rcp_f16_sdwa v97, v97 dst_sel:DWORD dst_unused:UNUSED_PAD src0_sel:WORD_1
	v_pk_add_f16 v95, v95, v120
	v_rcp_f16_e32 v115, v96
	v_rcp_f16_sdwa v96, v96 dst_sel:DWORD dst_unused:UNUSED_PAD src0_sel:WORD_1
	v_pk_add_f16 v94, v94, v121
	v_rcp_f16_e32 v116, v95
	v_rcp_f16_sdwa v95, v95 dst_sel:DWORD dst_unused:UNUSED_PAD src0_sel:WORD_1
	v_rcp_f16_e32 v117, v94
	v_rcp_f16_sdwa v94, v94 dst_sel:DWORD dst_unused:UNUSED_PAD src0_sel:WORD_1
	v_pk_fma_f16 v70, v50, v118, v70
	v_pack_b32_f16 v97, v114, v97
	v_pk_fma_f16 v71, v51, v119, v71
	v_pk_mul_f16 v141, v70, v97
	v_pack_b32_f16 v70, v115, v96
	v_pk_fma_f16 v72, v52, v120, v72
	v_pk_mul_f16 v140, v71, v70
	v_pack_b32_f16 v70, v116, v95
	v_pk_fma_f16 v73, v53, v121, v73
	v_pk_mul_f16 v139, v72, v70
	v_pack_b32_f16 v70, v117, v94
	v_pk_mul_f16 v138, v73, v70
	s_waitcnt vmcnt(12)
	v_pk_mul_f16 v70, v160, v154 op_sel_hi:[0,1]
	v_pk_mul_f16 v73, v160, v157 op_sel_hi:[0,1]
	v_pk_mul_f16 v97, v158, v157 op_sel_hi:[0,1]
	v_pk_mul_f16 v117, v159, v157 op_sel_hi:[0,1]
	v_pk_mul_f16 v71, v160, v155 op_sel_hi:[0,1]
	v_pk_mul_f16 v72, v160, v156 op_sel_hi:[0,1]
	v_pk_mul_f16 v94, v158, v154 op_sel_hi:[0,1]
	v_pk_mul_f16 v95, v158, v155 op_sel_hi:[0,1]
	v_pk_mul_f16 v96, v158, v156 op_sel_hi:[0,1]
	v_pk_mul_f16 v114, v159, v154 op_sel_hi:[0,1]
	v_pk_mul_f16 v115, v159, v155 op_sel_hi:[0,1]
	v_pk_mul_f16 v116, v159, v156 op_sel_hi:[0,1]
	v_pk_fma_f16 v89, v89, v157, v73
	v_pk_fma_f16 v86, v86, v154, v70
	v_pk_fma_f16 v113, v113, v157, v73
	v_pk_fma_f16 v110, v110, v154, v70
	v_pk_fma_f16 v73, v129, v157, v73
	v_pk_fma_f16 v70, v126, v154, v70
	v_pk_fma_f16 v118, v57, v157, v97
	v_pk_fma_f16 v126, v77, v157, v97
	v_pk_fma_f16 v97, v101, v157, v97
	v_pk_fma_f16 v130, v29, v157, v117
	v_pk_fma_f16 v161, v41, v157, v117
	v_pk_fma_f16 v117, v61, v157, v117
	v_pk_maximum3_f16 v157, v89, v113, v73
	v_pk_fma_f16 v88, v88, v156, v72
	v_pk_fma_f16 v87, v87, v155, v71
	v_pk_fma_f16 v112, v112, v156, v72
	v_pk_fma_f16 v111, v111, v155, v71
	v_pk_fma_f16 v72, v128, v156, v72
	v_pk_fma_f16 v71, v127, v155, v71
	v_pk_fma_f16 v119, v56, v156, v96
	v_pk_fma_f16 v120, v55, v155, v95
	v_pk_fma_f16 v121, v54, v154, v94
	v_pk_fma_f16 v127, v76, v156, v96
	v_pk_fma_f16 v128, v75, v155, v95
	v_pk_fma_f16 v129, v74, v154, v94
	v_pk_fma_f16 v96, v100, v156, v96
	v_pk_fma_f16 v95, v99, v155, v95
	v_pk_fma_f16 v94, v98, v154, v94
	v_pk_fma_f16 v131, v28, v156, v116
	v_pk_fma_f16 v132, v27, v155, v115
	v_pk_fma_f16 v133, v26, v154, v114
	v_pk_fma_f16 v162, v40, v156, v116
	v_pk_fma_f16 v163, v39, v155, v115
	v_pk_fma_f16 v164, v38, v154, v114
	v_pk_fma_f16 v116, v60, v156, v116
	v_pk_fma_f16 v115, v59, v155, v115
	v_pk_fma_f16 v114, v58, v154, v114
	v_pk_maximum3_f16 v154, v86, v110, v70
	v_pk_maximum3_f16 v155, v87, v111, v71
	v_pk_maximum3_f16 v156, v88, v112, v72
	v_pk_maximum3_f16 v206, v118, v126, v97
	v_pk_maximum3_f16 v210, v130, v161, v117
	v_pk_maximum3_f16 v165, v121, v129, v94
	v_pk_maximum3_f16 v200, v120, v128, v95
	v_pk_maximum3_f16 v201, v119, v127, v96
	v_pk_maximum3_f16 v207, v133, v164, v114
	v_pk_maximum3_f16 v208, v132, v163, v115
	v_pk_maximum3_f16 v157, v157, v206, v210
	v_pk_maximum3_f16 v209, v131, v162, v116
	v_pk_maximum3_f16 v154, v154, v165, v207
	v_pk_maximum3_f16 v155, v155, v200, v208
	v_pk_maximum3_f16 v156, v156, v201, v209
	v_pk_add_f16 v89, v89, v157 neg_lo:[0,1] neg_hi:[0,1]
	v_pk_add_f16 v86, v86, v154 neg_lo:[0,1] neg_hi:[0,1]
	v_pk_add_f16 v87, v87, v155 neg_lo:[0,1] neg_hi:[0,1]
	v_pk_add_f16 v88, v88, v156 neg_lo:[0,1] neg_hi:[0,1]
	v_pk_add_f16 v110, v110, v154 neg_lo:[0,1] neg_hi:[0,1]
	v_exp_f16_sdwa v165, v86 dst_sel:WORD_0 dst_unused:UNUSED_PAD src0_sel:WORD_0
	v_exp_f16_sdwa v200, v87 dst_sel:WORD_0 dst_unused:UNUSED_PAD src0_sel:WORD_0
	v_exp_f16_sdwa v201, v88 dst_sel:WORD_0 dst_unused:UNUSED_PAD src0_sel:WORD_0
	v_exp_f16_sdwa v206, v89 dst_sel:WORD_0 dst_unused:UNUSED_PAD src0_sel:WORD_0
	v_exp_f16_sdwa v165, v86 dst_sel:WORD_1 dst_unused:UNUSED_PRESERVE src0_sel:WORD_1
	v_exp_f16_sdwa v200, v87 dst_sel:WORD_1 dst_unused:UNUSED_PRESERVE src0_sel:WORD_1
	v_exp_f16_sdwa v201, v88 dst_sel:WORD_1 dst_unused:UNUSED_PRESERVE src0_sel:WORD_1
	v_exp_f16_sdwa v206, v89 dst_sel:WORD_1 dst_unused:UNUSED_PRESERVE src0_sel:WORD_1
	v_pk_add_f16 v111, v111, v155 neg_lo:[0,1] neg_hi:[0,1]
	v_pk_add_f16 v89, v165, 0
	v_pk_fma_f16 v45, v45, v206, 0
	v_pk_add_f16 v86, v206, 0
	v_pk_add_f16 v87, v201, 0
	v_pk_add_f16 v88, v200, 0
	v_pk_fma_f16 v44, v44, v201, 0
	v_pk_fma_f16 v43, v43, v200, 0
	v_pk_fma_f16 v42, v42, v165, 0
	v_pk_add_f16 v112, v112, v156 neg_lo:[0,1] neg_hi:[0,1]
	v_pk_add_f16 v113, v113, v157 neg_lo:[0,1] neg_hi:[0,1]
	v_exp_f16_sdwa v165, v110 dst_sel:WORD_0 dst_unused:UNUSED_PAD src0_sel:WORD_0
	v_exp_f16_sdwa v200, v111 dst_sel:WORD_0 dst_unused:UNUSED_PAD src0_sel:WORD_0
	v_exp_f16_sdwa v201, v112 dst_sel:WORD_0 dst_unused:UNUSED_PAD src0_sel:WORD_0
	v_exp_f16_sdwa v206, v113 dst_sel:WORD_0 dst_unused:UNUSED_PAD src0_sel:WORD_0
	v_exp_f16_sdwa v165, v110 dst_sel:WORD_1 dst_unused:UNUSED_PRESERVE src0_sel:WORD_1
	v_exp_f16_sdwa v200, v111 dst_sel:WORD_1 dst_unused:UNUSED_PRESERVE src0_sel:WORD_1
	v_exp_f16_sdwa v201, v112 dst_sel:WORD_1 dst_unused:UNUSED_PRESERVE src0_sel:WORD_1
	v_exp_f16_sdwa v206, v113 dst_sel:WORD_1 dst_unused:UNUSED_PRESERVE src0_sel:WORD_1
	v_pk_add_f16 v89, v89, v165
	v_pk_fma_f16 v45, v69, v206, v45
	v_pk_add_f16 v69, v73, v157 neg_lo:[0,1] neg_hi:[0,1]
	v_pk_add_f16 v88, v88, v200
	v_pk_add_f16 v87, v87, v201
	v_pk_add_f16 v86, v86, v206
	v_pk_fma_f16 v42, v66, v165, v42
	v_pk_fma_f16 v43, v67, v200, v43
	v_pk_fma_f16 v44, v68, v201, v44
	v_pk_add_f16 v66, v70, v154 neg_lo:[0,1] neg_hi:[0,1]
	v_pk_add_f16 v67, v71, v155 neg_lo:[0,1] neg_hi:[0,1]
	v_pk_add_f16 v68, v72, v156 neg_lo:[0,1] neg_hi:[0,1]
	v_exp_f16_sdwa v70, v66 dst_sel:WORD_0 dst_unused:UNUSED_PAD src0_sel:WORD_0
	v_exp_f16_sdwa v71, v67 dst_sel:WORD_0 dst_unused:UNUSED_PAD src0_sel:WORD_0
	v_exp_f16_sdwa v72, v68 dst_sel:WORD_0 dst_unused:UNUSED_PAD src0_sel:WORD_0
	v_exp_f16_sdwa v73, v69 dst_sel:WORD_0 dst_unused:UNUSED_PAD src0_sel:WORD_0
	v_exp_f16_sdwa v70, v66 dst_sel:WORD_1 dst_unused:UNUSED_PRESERVE src0_sel:WORD_1
	v_exp_f16_sdwa v71, v67 dst_sel:WORD_1 dst_unused:UNUSED_PRESERVE src0_sel:WORD_1
	v_exp_f16_sdwa v72, v68 dst_sel:WORD_1 dst_unused:UNUSED_PRESERVE src0_sel:WORD_1
	v_exp_f16_sdwa v73, v69 dst_sel:WORD_1 dst_unused:UNUSED_PRESERVE src0_sel:WORD_1
	v_pk_add_f16 v69, v89, v70
	v_pk_add_f16 v66, v86, v73
	v_pk_add_f16 v67, v87, v72
	v_pk_add_f16 v68, v88, v71
	v_pk_fma_f16 v45, v93, v73, v45
	v_pk_fma_f16 v44, v92, v72, v44
	v_pk_fma_f16 v43, v91, v71, v43
	v_pk_fma_f16 v42, v90, v70, v42
	v_pk_add_f16 v70, v121, v154 neg_lo:[0,1] neg_hi:[0,1]
	v_pk_add_f16 v71, v120, v155 neg_lo:[0,1] neg_hi:[0,1]
	v_pk_add_f16 v72, v119, v156 neg_lo:[0,1] neg_hi:[0,1]
	v_pk_add_f16 v73, v118, v157 neg_lo:[0,1] neg_hi:[0,1]
	v_exp_f16_sdwa v86, v70 dst_sel:WORD_0 dst_unused:UNUSED_PAD src0_sel:WORD_0
	v_exp_f16_sdwa v87, v71 dst_sel:WORD_0 dst_unused:UNUSED_PAD src0_sel:WORD_0
	v_exp_f16_sdwa v88, v72 dst_sel:WORD_0 dst_unused:UNUSED_PAD src0_sel:WORD_0
	v_exp_f16_sdwa v89, v73 dst_sel:WORD_0 dst_unused:UNUSED_PAD src0_sel:WORD_0
	v_exp_f16_sdwa v86, v70 dst_sel:WORD_1 dst_unused:UNUSED_PRESERVE src0_sel:WORD_1
	v_exp_f16_sdwa v87, v71 dst_sel:WORD_1 dst_unused:UNUSED_PRESERVE src0_sel:WORD_1
	v_exp_f16_sdwa v88, v72 dst_sel:WORD_1 dst_unused:UNUSED_PRESERVE src0_sel:WORD_1
	v_exp_f16_sdwa v89, v73 dst_sel:WORD_1 dst_unused:UNUSED_PRESERVE src0_sel:WORD_1
	v_pk_add_f16 v70, v129, v154 neg_lo:[0,1] neg_hi:[0,1]
	v_pk_add_f16 v69, v69, v86
	v_pk_add_f16 v68, v68, v87
	v_pk_add_f16 v67, v67, v88
	v_pk_add_f16 v66, v66, v89
	v_pk_fma_f16 v42, v22, v86, v42
	v_pk_fma_f16 v43, v23, v87, v43
	v_pk_fma_f16 v44, v24, v88, v44
	v_pk_fma_f16 v45, v25, v89, v45
	v_pk_add_f16 v71, v128, v155 neg_lo:[0,1] neg_hi:[0,1]
	v_pk_add_f16 v72, v127, v156 neg_lo:[0,1] neg_hi:[0,1]
	v_pk_add_f16 v73, v126, v157 neg_lo:[0,1] neg_hi:[0,1]
	v_exp_f16_sdwa v86, v70 dst_sel:WORD_0 dst_unused:UNUSED_PAD src0_sel:WORD_0
	v_exp_f16_sdwa v87, v71 dst_sel:WORD_0 dst_unused:UNUSED_PAD src0_sel:WORD_0
	v_exp_f16_sdwa v88, v72 dst_sel:WORD_0 dst_unused:UNUSED_PAD src0_sel:WORD_0
	v_exp_f16_sdwa v89, v73 dst_sel:WORD_0 dst_unused:UNUSED_PAD src0_sel:WORD_0
	v_exp_f16_sdwa v86, v70 dst_sel:WORD_1 dst_unused:UNUSED_PRESERVE src0_sel:WORD_1
	v_exp_f16_sdwa v87, v71 dst_sel:WORD_1 dst_unused:UNUSED_PRESERVE src0_sel:WORD_1
	v_exp_f16_sdwa v88, v72 dst_sel:WORD_1 dst_unused:UNUSED_PRESERVE src0_sel:WORD_1
	v_exp_f16_sdwa v89, v73 dst_sel:WORD_1 dst_unused:UNUSED_PRESERVE src0_sel:WORD_1
	v_pk_add_f16 v70, v94, v154 neg_lo:[0,1] neg_hi:[0,1]
	v_pk_add_f16 v69, v69, v86
	v_pk_add_f16 v66, v66, v89
	v_pk_add_f16 v67, v67, v88
	v_pk_add_f16 v68, v68, v87
	v_pk_fma_f16 v45, v37, v89, v45
	v_pk_fma_f16 v44, v36, v88, v44
	v_pk_fma_f16 v43, v35, v87, v43
	v_pk_fma_f16 v42, v34, v86, v42
	v_pk_add_f16 v71, v95, v155 neg_lo:[0,1] neg_hi:[0,1]
	v_pk_add_f16 v72, v96, v156 neg_lo:[0,1] neg_hi:[0,1]
	v_pk_add_f16 v73, v97, v157 neg_lo:[0,1] neg_hi:[0,1]
	v_exp_f16_sdwa v86, v70 dst_sel:WORD_0 dst_unused:UNUSED_PAD src0_sel:WORD_0
	v_exp_f16_sdwa v87, v71 dst_sel:WORD_0 dst_unused:UNUSED_PAD src0_sel:WORD_0
	v_exp_f16_sdwa v88, v72 dst_sel:WORD_0 dst_unused:UNUSED_PAD src0_sel:WORD_0
	v_exp_f16_sdwa v89, v73 dst_sel:WORD_0 dst_unused:UNUSED_PAD src0_sel:WORD_0
	v_exp_f16_sdwa v86, v70 dst_sel:WORD_1 dst_unused:UNUSED_PRESERVE src0_sel:WORD_1
	v_exp_f16_sdwa v87, v71 dst_sel:WORD_1 dst_unused:UNUSED_PRESERVE src0_sel:WORD_1
	v_exp_f16_sdwa v88, v72 dst_sel:WORD_1 dst_unused:UNUSED_PRESERVE src0_sel:WORD_1
	v_exp_f16_sdwa v89, v73 dst_sel:WORD_1 dst_unused:UNUSED_PRESERVE src0_sel:WORD_1
	v_pk_add_f16 v70, v133, v154 neg_lo:[0,1] neg_hi:[0,1]
	v_pk_add_f16 v69, v69, v86
	v_pk_add_f16 v68, v68, v87
	v_pk_add_f16 v67, v67, v88
	v_pk_add_f16 v66, v66, v89
	v_pk_fma_f16 v42, v50, v86, v42
	v_pk_fma_f16 v43, v51, v87, v43
	v_pk_fma_f16 v44, v52, v88, v44
	v_pk_fma_f16 v45, v53, v89, v45
	v_pk_add_f16 v71, v132, v155 neg_lo:[0,1] neg_hi:[0,1]
	v_pk_add_f16 v72, v131, v156 neg_lo:[0,1] neg_hi:[0,1]
	v_pk_add_f16 v73, v130, v157 neg_lo:[0,1] neg_hi:[0,1]
	v_exp_f16_sdwa v86, v70 dst_sel:WORD_0 dst_unused:UNUSED_PAD src0_sel:WORD_0
	v_exp_f16_sdwa v87, v71 dst_sel:WORD_0 dst_unused:UNUSED_PAD src0_sel:WORD_0
	v_exp_f16_sdwa v88, v72 dst_sel:WORD_0 dst_unused:UNUSED_PAD src0_sel:WORD_0
	v_exp_f16_sdwa v89, v73 dst_sel:WORD_0 dst_unused:UNUSED_PAD src0_sel:WORD_0
	v_exp_f16_sdwa v86, v70 dst_sel:WORD_1 dst_unused:UNUSED_PRESERVE src0_sel:WORD_1
	v_exp_f16_sdwa v87, v71 dst_sel:WORD_1 dst_unused:UNUSED_PRESERVE src0_sel:WORD_1
	v_exp_f16_sdwa v88, v72 dst_sel:WORD_1 dst_unused:UNUSED_PRESERVE src0_sel:WORD_1
	v_exp_f16_sdwa v89, v73 dst_sel:WORD_1 dst_unused:UNUSED_PRESERVE src0_sel:WORD_1
	v_pk_add_f16 v70, v164, v154 neg_lo:[0,1] neg_hi:[0,1]
	v_pk_add_f16 v69, v69, v86
	v_pk_add_f16 v66, v66, v89
	v_pk_add_f16 v67, v67, v88
	v_pk_add_f16 v68, v68, v87
	v_pk_fma_f16 v45, v13, v89, v45
	v_pk_fma_f16 v44, v12, v88, v44
	v_pk_fma_f16 v43, v11, v87, v43
	v_pk_fma_f16 v42, v10, v86, v42
	v_pk_add_f16 v71, v163, v155 neg_lo:[0,1] neg_hi:[0,1]
	v_pk_add_f16 v72, v162, v156 neg_lo:[0,1] neg_hi:[0,1]
	v_pk_add_f16 v73, v161, v157 neg_lo:[0,1] neg_hi:[0,1]
	v_exp_f16_sdwa v86, v70 dst_sel:WORD_0 dst_unused:UNUSED_PAD src0_sel:WORD_0
	v_exp_f16_sdwa v87, v71 dst_sel:WORD_0 dst_unused:UNUSED_PAD src0_sel:WORD_0
	v_exp_f16_sdwa v88, v72 dst_sel:WORD_0 dst_unused:UNUSED_PAD src0_sel:WORD_0
	v_exp_f16_sdwa v89, v73 dst_sel:WORD_0 dst_unused:UNUSED_PAD src0_sel:WORD_0
	v_exp_f16_sdwa v86, v70 dst_sel:WORD_1 dst_unused:UNUSED_PRESERVE src0_sel:WORD_1
	v_exp_f16_sdwa v87, v71 dst_sel:WORD_1 dst_unused:UNUSED_PRESERVE src0_sel:WORD_1
	v_exp_f16_sdwa v88, v72 dst_sel:WORD_1 dst_unused:UNUSED_PRESERVE src0_sel:WORD_1
	v_exp_f16_sdwa v89, v73 dst_sel:WORD_1 dst_unused:UNUSED_PRESERVE src0_sel:WORD_1
	v_pk_add_f16 v70, v114, v154 neg_lo:[0,1] neg_hi:[0,1]
	v_pk_add_f16 v69, v69, v86
	v_pk_add_f16 v68, v68, v87
	v_pk_add_f16 v67, v67, v88
	v_pk_add_f16 v66, v66, v89
	v_pk_fma_f16 v42, v14, v86, v42
	v_pk_fma_f16 v43, v15, v87, v43
	v_pk_fma_f16 v44, v16, v88, v44
	v_pk_fma_f16 v45, v17, v89, v45
	v_pk_add_f16 v71, v115, v155 neg_lo:[0,1] neg_hi:[0,1]
	v_pk_add_f16 v72, v116, v156 neg_lo:[0,1] neg_hi:[0,1]
	v_pk_add_f16 v73, v117, v157 neg_lo:[0,1] neg_hi:[0,1]
	v_exp_f16_sdwa v86, v70 dst_sel:WORD_0 dst_unused:UNUSED_PAD src0_sel:WORD_0
	v_exp_f16_sdwa v87, v71 dst_sel:WORD_0 dst_unused:UNUSED_PAD src0_sel:WORD_0
	v_exp_f16_sdwa v88, v72 dst_sel:WORD_0 dst_unused:UNUSED_PAD src0_sel:WORD_0
	v_exp_f16_sdwa v89, v73 dst_sel:WORD_0 dst_unused:UNUSED_PAD src0_sel:WORD_0
	v_exp_f16_sdwa v86, v70 dst_sel:WORD_1 dst_unused:UNUSED_PRESERVE src0_sel:WORD_1
	v_exp_f16_sdwa v87, v71 dst_sel:WORD_1 dst_unused:UNUSED_PRESERVE src0_sel:WORD_1
	v_exp_f16_sdwa v88, v72 dst_sel:WORD_1 dst_unused:UNUSED_PRESERVE src0_sel:WORD_1
	v_exp_f16_sdwa v89, v73 dst_sel:WORD_1 dst_unused:UNUSED_PRESERVE src0_sel:WORD_1
	v_pk_add_f16 v69, v69, v86
	v_pk_add_f16 v68, v68, v87
	v_rcp_f16_e32 v70, v69
	v_rcp_f16_sdwa v69, v69 dst_sel:DWORD dst_unused:UNUSED_PAD src0_sel:WORD_1
	v_pk_add_f16 v67, v67, v88
	v_rcp_f16_e32 v71, v68
	v_rcp_f16_sdwa v68, v68 dst_sel:DWORD dst_unused:UNUSED_PAD src0_sel:WORD_1
	v_pk_add_f16 v66, v66, v89
	v_rcp_f16_e32 v72, v67
	v_rcp_f16_sdwa v67, v67 dst_sel:DWORD dst_unused:UNUSED_PAD src0_sel:WORD_1
	v_rcp_f16_e32 v73, v66
	v_rcp_f16_sdwa v66, v66 dst_sel:DWORD dst_unused:UNUSED_PAD src0_sel:WORD_1
	v_pk_fma_f16 v42, v18, v86, v42
	v_pack_b32_f16 v69, v70, v69
	v_pk_fma_f16 v43, v19, v87, v43
	v_pk_mul_f16 v97, v42, v69
	v_pack_b32_f16 v42, v71, v68
	v_pk_fma_f16 v44, v20, v88, v44
	v_pk_mul_f16 v96, v43, v42
	v_pack_b32_f16 v42, v72, v67
	v_pk_fma_f16 v45, v21, v89, v45
	v_pk_mul_f16 v95, v44, v42
	v_pack_b32_f16 v42, v73, v66
	v_pk_mul_f16 v94, v45, v42
	s_waitcnt vmcnt(6)
	v_pk_mul_f16 v45, v160, v153 op_sel_hi:[0,1]
	v_pk_mul_f16 v42, v160, v150 op_sel_hi:[0,1]
	v_pk_mul_f16 v43, v160, v151 op_sel_hi:[0,1]
	v_pk_mul_f16 v44, v160, v152 op_sel_hi:[0,1]
	v_pk_mul_f16 v69, v158, v153 op_sel_hi:[0,1]
	v_pk_mul_f16 v73, v159, v153 op_sel_hi:[0,1]
	v_pk_fma_f16 v57, v57, v153, v45
	v_pk_fma_f16 v77, v77, v153, v45
	v_pk_fma_f16 v45, v101, v153, v45
	v_pk_mul_f16 v66, v158, v150 op_sel_hi:[0,1]
	v_pk_maximum3_f16 v117, v57, v77, v45
	v_pk_mul_f16 v67, v158, v151 op_sel_hi:[0,1]
	v_pk_mul_f16 v68, v158, v152 op_sel_hi:[0,1]
	v_pk_mul_f16 v70, v159, v150 op_sel_hi:[0,1]
	v_pk_mul_f16 v71, v159, v151 op_sel_hi:[0,1]
	v_pk_mul_f16 v72, v159, v152 op_sel_hi:[0,1]
	v_pk_fma_f16 v56, v56, v152, v44
	v_pk_fma_f16 v55, v55, v151, v43
	v_pk_fma_f16 v54, v54, v150, v42
	v_pk_fma_f16 v76, v76, v152, v44
	v_pk_fma_f16 v75, v75, v151, v43
	v_pk_fma_f16 v74, v74, v150, v42
	v_pk_fma_f16 v44, v100, v152, v44
	v_pk_fma_f16 v43, v99, v151, v43
	v_pk_fma_f16 v42, v98, v150, v42
	v_pk_fma_f16 v86, v29, v153, v69
	v_pk_fma_f16 v90, v41, v153, v69
	v_pk_fma_f16 v69, v61, v153, v69
	v_pk_fma_f16 v98, v81, v153, v73
	v_pk_fma_f16 v110, v109, v153, v73
	v_pk_fma_f16 v73, v125, v153, v73
	v_pk_maximum3_f16 v114, v54, v74, v42
	v_pk_maximum3_f16 v115, v55, v75, v43
	v_pk_maximum3_f16 v116, v56, v76, v44
	v_pk_maximum3_f16 v121, v86, v90, v69
	v_pk_fma_f16 v87, v28, v152, v68
	v_pk_maximum3_f16 v129, v98, v110, v73
	v_pk_fma_f16 v88, v27, v151, v67
	v_pk_maximum3_f16 v117, v117, v121, v129
	v_pk_fma_f16 v89, v26, v150, v66
	v_pk_fma_f16 v91, v40, v152, v68
	v_pk_fma_f16 v92, v39, v151, v67
	v_pk_fma_f16 v93, v38, v150, v66
	v_pk_fma_f16 v68, v60, v152, v68
	v_pk_fma_f16 v67, v59, v151, v67
	v_pk_fma_f16 v66, v58, v150, v66
	v_pk_fma_f16 v99, v80, v152, v72
	v_pk_fma_f16 v100, v79, v151, v71
	v_pk_fma_f16 v101, v78, v150, v70
	v_pk_fma_f16 v111, v108, v152, v72
	v_pk_fma_f16 v112, v107, v151, v71
	v_pk_fma_f16 v113, v106, v150, v70
	v_pk_fma_f16 v72, v124, v152, v72
	v_pk_fma_f16 v71, v123, v151, v71
	v_pk_fma_f16 v70, v122, v150, v70
	v_pk_maximum3_f16 v118, v89, v93, v66
	v_pk_maximum3_f16 v119, v88, v92, v67
	v_pk_maximum3_f16 v120, v87, v91, v68
	v_pk_maximum3_f16 v127, v100, v112, v71
	v_pk_maximum3_f16 v128, v99, v111, v72
	v_pk_maximum3_f16 v126, v101, v113, v70
	v_pk_maximum3_f16 v114, v114, v118, v126
	v_pk_maximum3_f16 v115, v115, v119, v127
	v_pk_maximum3_f16 v116, v116, v120, v128
	v_pk_add_f16 v57, v57, v117 neg_lo:[0,1] neg_hi:[0,1]
	v_pk_add_f16 v54, v54, v114 neg_lo:[0,1] neg_hi:[0,1]
	v_pk_add_f16 v55, v55, v115 neg_lo:[0,1] neg_hi:[0,1]
	v_pk_add_f16 v56, v56, v116 neg_lo:[0,1] neg_hi:[0,1]
	v_pk_add_f16 v74, v74, v114 neg_lo:[0,1] neg_hi:[0,1]
	v_exp_f16_sdwa v118, v54 dst_sel:WORD_0 dst_unused:UNUSED_PAD src0_sel:WORD_0
	v_exp_f16_sdwa v119, v55 dst_sel:WORD_0 dst_unused:UNUSED_PAD src0_sel:WORD_0
	v_exp_f16_sdwa v120, v56 dst_sel:WORD_0 dst_unused:UNUSED_PAD src0_sel:WORD_0
	v_exp_f16_sdwa v121, v57 dst_sel:WORD_0 dst_unused:UNUSED_PAD src0_sel:WORD_0
	v_exp_f16_sdwa v118, v54 dst_sel:WORD_1 dst_unused:UNUSED_PRESERVE src0_sel:WORD_1
	v_exp_f16_sdwa v119, v55 dst_sel:WORD_1 dst_unused:UNUSED_PRESERVE src0_sel:WORD_1
	v_exp_f16_sdwa v120, v56 dst_sel:WORD_1 dst_unused:UNUSED_PRESERVE src0_sel:WORD_1
	v_exp_f16_sdwa v121, v57 dst_sel:WORD_1 dst_unused:UNUSED_PRESERVE src0_sel:WORD_1
	v_pk_add_f16 v75, v75, v115 neg_lo:[0,1] neg_hi:[0,1]
	v_pk_add_f16 v57, v118, 0
	v_pk_fma_f16 v25, v25, v121, 0
	v_pk_add_f16 v54, v121, 0
	v_pk_add_f16 v55, v120, 0
	v_pk_add_f16 v56, v119, 0
	v_pk_fma_f16 v24, v24, v120, 0
	v_pk_fma_f16 v23, v23, v119, 0
	v_pk_fma_f16 v22, v22, v118, 0
	v_pk_add_f16 v76, v76, v116 neg_lo:[0,1] neg_hi:[0,1]
	v_pk_add_f16 v77, v77, v117 neg_lo:[0,1] neg_hi:[0,1]
	v_exp_f16_sdwa v118, v74 dst_sel:WORD_0 dst_unused:UNUSED_PAD src0_sel:WORD_0
	v_exp_f16_sdwa v119, v75 dst_sel:WORD_0 dst_unused:UNUSED_PAD src0_sel:WORD_0
	v_exp_f16_sdwa v120, v76 dst_sel:WORD_0 dst_unused:UNUSED_PAD src0_sel:WORD_0
	v_exp_f16_sdwa v121, v77 dst_sel:WORD_0 dst_unused:UNUSED_PAD src0_sel:WORD_0
	v_exp_f16_sdwa v118, v74 dst_sel:WORD_1 dst_unused:UNUSED_PRESERVE src0_sel:WORD_1
	v_exp_f16_sdwa v119, v75 dst_sel:WORD_1 dst_unused:UNUSED_PRESERVE src0_sel:WORD_1
	v_exp_f16_sdwa v120, v76 dst_sel:WORD_1 dst_unused:UNUSED_PRESERVE src0_sel:WORD_1
	v_exp_f16_sdwa v121, v77 dst_sel:WORD_1 dst_unused:UNUSED_PRESERVE src0_sel:WORD_1
	v_pk_add_f16 v57, v57, v118
	v_pk_fma_f16 v25, v37, v121, v25
	v_pk_add_f16 v37, v45, v117 neg_lo:[0,1] neg_hi:[0,1]
	v_pk_add_f16 v56, v56, v119
	v_pk_add_f16 v55, v55, v120
	v_pk_add_f16 v54, v54, v121
	v_pk_fma_f16 v22, v34, v118, v22
	v_pk_fma_f16 v23, v35, v119, v23
	v_pk_fma_f16 v24, v36, v120, v24
	v_pk_add_f16 v34, v42, v114 neg_lo:[0,1] neg_hi:[0,1]
	v_pk_add_f16 v35, v43, v115 neg_lo:[0,1] neg_hi:[0,1]
	v_pk_add_f16 v36, v44, v116 neg_lo:[0,1] neg_hi:[0,1]
	v_exp_f16_sdwa v42, v34 dst_sel:WORD_0 dst_unused:UNUSED_PAD src0_sel:WORD_0
	v_exp_f16_sdwa v43, v35 dst_sel:WORD_0 dst_unused:UNUSED_PAD src0_sel:WORD_0
	v_exp_f16_sdwa v44, v36 dst_sel:WORD_0 dst_unused:UNUSED_PAD src0_sel:WORD_0
	v_exp_f16_sdwa v45, v37 dst_sel:WORD_0 dst_unused:UNUSED_PAD src0_sel:WORD_0
	v_exp_f16_sdwa v42, v34 dst_sel:WORD_1 dst_unused:UNUSED_PRESERVE src0_sel:WORD_1
	v_exp_f16_sdwa v43, v35 dst_sel:WORD_1 dst_unused:UNUSED_PRESERVE src0_sel:WORD_1
	v_exp_f16_sdwa v44, v36 dst_sel:WORD_1 dst_unused:UNUSED_PRESERVE src0_sel:WORD_1
	v_exp_f16_sdwa v45, v37 dst_sel:WORD_1 dst_unused:UNUSED_PRESERVE src0_sel:WORD_1
	v_pk_add_f16 v37, v57, v42
	v_pk_add_f16 v34, v54, v45
	v_pk_add_f16 v35, v55, v44
	v_pk_add_f16 v36, v56, v43
	v_pk_fma_f16 v25, v53, v45, v25
	v_pk_fma_f16 v24, v52, v44, v24
	v_pk_fma_f16 v23, v51, v43, v23
	v_pk_fma_f16 v22, v50, v42, v22
	v_pk_add_f16 v42, v89, v114 neg_lo:[0,1] neg_hi:[0,1]
	v_pk_add_f16 v43, v88, v115 neg_lo:[0,1] neg_hi:[0,1]
	v_pk_add_f16 v44, v87, v116 neg_lo:[0,1] neg_hi:[0,1]
	v_pk_add_f16 v45, v86, v117 neg_lo:[0,1] neg_hi:[0,1]
	v_exp_f16_sdwa v50, v42 dst_sel:WORD_0 dst_unused:UNUSED_PAD src0_sel:WORD_0
	v_exp_f16_sdwa v51, v43 dst_sel:WORD_0 dst_unused:UNUSED_PAD src0_sel:WORD_0
	v_exp_f16_sdwa v52, v44 dst_sel:WORD_0 dst_unused:UNUSED_PAD src0_sel:WORD_0
	v_exp_f16_sdwa v53, v45 dst_sel:WORD_0 dst_unused:UNUSED_PAD src0_sel:WORD_0
	v_exp_f16_sdwa v50, v42 dst_sel:WORD_1 dst_unused:UNUSED_PRESERVE src0_sel:WORD_1
	v_exp_f16_sdwa v51, v43 dst_sel:WORD_1 dst_unused:UNUSED_PRESERVE src0_sel:WORD_1
	v_exp_f16_sdwa v52, v44 dst_sel:WORD_1 dst_unused:UNUSED_PRESERVE src0_sel:WORD_1
	v_exp_f16_sdwa v53, v45 dst_sel:WORD_1 dst_unused:UNUSED_PRESERVE src0_sel:WORD_1
	v_pk_add_f16 v42, v93, v114 neg_lo:[0,1] neg_hi:[0,1]
	v_pk_add_f16 v37, v37, v50
	v_pk_add_f16 v36, v36, v51
	v_pk_add_f16 v35, v35, v52
	v_pk_add_f16 v34, v34, v53
	v_pk_fma_f16 v22, v10, v50, v22
	v_pk_fma_f16 v23, v11, v51, v23
	v_pk_fma_f16 v24, v12, v52, v24
	v_pk_fma_f16 v25, v13, v53, v25
	v_pk_add_f16 v43, v92, v115 neg_lo:[0,1] neg_hi:[0,1]
	v_pk_add_f16 v44, v91, v116 neg_lo:[0,1] neg_hi:[0,1]
	v_pk_add_f16 v45, v90, v117 neg_lo:[0,1] neg_hi:[0,1]
	v_exp_f16_sdwa v50, v42 dst_sel:WORD_0 dst_unused:UNUSED_PAD src0_sel:WORD_0
	v_exp_f16_sdwa v51, v43 dst_sel:WORD_0 dst_unused:UNUSED_PAD src0_sel:WORD_0
	v_exp_f16_sdwa v52, v44 dst_sel:WORD_0 dst_unused:UNUSED_PAD src0_sel:WORD_0
	v_exp_f16_sdwa v53, v45 dst_sel:WORD_0 dst_unused:UNUSED_PAD src0_sel:WORD_0
	v_exp_f16_sdwa v50, v42 dst_sel:WORD_1 dst_unused:UNUSED_PRESERVE src0_sel:WORD_1
	v_exp_f16_sdwa v51, v43 dst_sel:WORD_1 dst_unused:UNUSED_PRESERVE src0_sel:WORD_1
	v_exp_f16_sdwa v52, v44 dst_sel:WORD_1 dst_unused:UNUSED_PRESERVE src0_sel:WORD_1
	v_exp_f16_sdwa v53, v45 dst_sel:WORD_1 dst_unused:UNUSED_PRESERVE src0_sel:WORD_1
	v_pk_add_f16 v42, v66, v114 neg_lo:[0,1] neg_hi:[0,1]
	v_pk_add_f16 v37, v37, v50
	v_pk_add_f16 v34, v34, v53
	v_pk_add_f16 v35, v35, v52
	v_pk_add_f16 v36, v36, v51
	v_pk_fma_f16 v25, v17, v53, v25
	v_pk_fma_f16 v24, v16, v52, v24
	v_pk_fma_f16 v23, v15, v51, v23
	v_pk_fma_f16 v22, v14, v50, v22
	v_pk_add_f16 v43, v67, v115 neg_lo:[0,1] neg_hi:[0,1]
	v_pk_add_f16 v44, v68, v116 neg_lo:[0,1] neg_hi:[0,1]
	v_pk_add_f16 v45, v69, v117 neg_lo:[0,1] neg_hi:[0,1]
	v_exp_f16_sdwa v50, v42 dst_sel:WORD_0 dst_unused:UNUSED_PAD src0_sel:WORD_0
	v_exp_f16_sdwa v51, v43 dst_sel:WORD_0 dst_unused:UNUSED_PAD src0_sel:WORD_0
	v_exp_f16_sdwa v52, v44 dst_sel:WORD_0 dst_unused:UNUSED_PAD src0_sel:WORD_0
	v_exp_f16_sdwa v53, v45 dst_sel:WORD_0 dst_unused:UNUSED_PAD src0_sel:WORD_0
	v_exp_f16_sdwa v50, v42 dst_sel:WORD_1 dst_unused:UNUSED_PRESERVE src0_sel:WORD_1
	v_exp_f16_sdwa v51, v43 dst_sel:WORD_1 dst_unused:UNUSED_PRESERVE src0_sel:WORD_1
	v_exp_f16_sdwa v52, v44 dst_sel:WORD_1 dst_unused:UNUSED_PRESERVE src0_sel:WORD_1
	v_exp_f16_sdwa v53, v45 dst_sel:WORD_1 dst_unused:UNUSED_PRESERVE src0_sel:WORD_1
	v_pk_add_f16 v42, v101, v114 neg_lo:[0,1] neg_hi:[0,1]
	v_pk_add_f16 v37, v37, v50
	v_pk_add_f16 v36, v36, v51
	v_pk_add_f16 v35, v35, v52
	v_pk_add_f16 v34, v34, v53
	v_pk_fma_f16 v22, v18, v50, v22
	v_pk_fma_f16 v23, v19, v51, v23
	v_pk_fma_f16 v24, v20, v52, v24
	v_pk_fma_f16 v25, v21, v53, v25
	v_pk_add_f16 v43, v100, v115 neg_lo:[0,1] neg_hi:[0,1]
	v_pk_add_f16 v44, v99, v116 neg_lo:[0,1] neg_hi:[0,1]
	v_pk_add_f16 v45, v98, v117 neg_lo:[0,1] neg_hi:[0,1]
	v_exp_f16_sdwa v50, v42 dst_sel:WORD_0 dst_unused:UNUSED_PAD src0_sel:WORD_0
	v_exp_f16_sdwa v51, v43 dst_sel:WORD_0 dst_unused:UNUSED_PAD src0_sel:WORD_0
	v_exp_f16_sdwa v52, v44 dst_sel:WORD_0 dst_unused:UNUSED_PAD src0_sel:WORD_0
	v_exp_f16_sdwa v53, v45 dst_sel:WORD_0 dst_unused:UNUSED_PAD src0_sel:WORD_0
	v_exp_f16_sdwa v50, v42 dst_sel:WORD_1 dst_unused:UNUSED_PRESERVE src0_sel:WORD_1
	v_exp_f16_sdwa v51, v43 dst_sel:WORD_1 dst_unused:UNUSED_PRESERVE src0_sel:WORD_1
	v_exp_f16_sdwa v52, v44 dst_sel:WORD_1 dst_unused:UNUSED_PRESERVE src0_sel:WORD_1
	v_exp_f16_sdwa v53, v45 dst_sel:WORD_1 dst_unused:UNUSED_PRESERVE src0_sel:WORD_1
	v_pk_add_f16 v42, v113, v114 neg_lo:[0,1] neg_hi:[0,1]
	v_pk_add_f16 v37, v37, v50
	v_pk_add_f16 v34, v34, v53
	v_pk_add_f16 v35, v35, v52
	v_pk_add_f16 v36, v36, v51
	v_pk_fma_f16 v25, v33, v53, v25
	v_pk_fma_f16 v24, v32, v52, v24
	v_pk_fma_f16 v23, v31, v51, v23
	v_pk_fma_f16 v22, v30, v50, v22
	v_pk_add_f16 v43, v112, v115 neg_lo:[0,1] neg_hi:[0,1]
	v_pk_add_f16 v44, v111, v116 neg_lo:[0,1] neg_hi:[0,1]
	v_pk_add_f16 v45, v110, v117 neg_lo:[0,1] neg_hi:[0,1]
	v_exp_f16_sdwa v50, v42 dst_sel:WORD_0 dst_unused:UNUSED_PAD src0_sel:WORD_0
	v_exp_f16_sdwa v51, v43 dst_sel:WORD_0 dst_unused:UNUSED_PAD src0_sel:WORD_0
	v_exp_f16_sdwa v52, v44 dst_sel:WORD_0 dst_unused:UNUSED_PAD src0_sel:WORD_0
	v_exp_f16_sdwa v53, v45 dst_sel:WORD_0 dst_unused:UNUSED_PAD src0_sel:WORD_0
	v_exp_f16_sdwa v50, v42 dst_sel:WORD_1 dst_unused:UNUSED_PRESERVE src0_sel:WORD_1
	v_exp_f16_sdwa v51, v43 dst_sel:WORD_1 dst_unused:UNUSED_PRESERVE src0_sel:WORD_1
	v_exp_f16_sdwa v52, v44 dst_sel:WORD_1 dst_unused:UNUSED_PRESERVE src0_sel:WORD_1
	v_exp_f16_sdwa v53, v45 dst_sel:WORD_1 dst_unused:UNUSED_PRESERVE src0_sel:WORD_1
	v_pk_add_f16 v42, v70, v114 neg_lo:[0,1] neg_hi:[0,1]
	v_pk_add_f16 v37, v37, v50
	v_pk_add_f16 v36, v36, v51
	v_pk_add_f16 v35, v35, v52
	v_pk_add_f16 v34, v34, v53
	v_pk_fma_f16 v22, v46, v50, v22
	v_pk_fma_f16 v23, v47, v51, v23
	v_pk_fma_f16 v24, v48, v52, v24
	v_pk_fma_f16 v25, v49, v53, v25
	v_pk_add_f16 v43, v71, v115 neg_lo:[0,1] neg_hi:[0,1]
	v_pk_add_f16 v44, v72, v116 neg_lo:[0,1] neg_hi:[0,1]
	v_pk_add_f16 v45, v73, v117 neg_lo:[0,1] neg_hi:[0,1]
	v_exp_f16_sdwa v50, v42 dst_sel:WORD_0 dst_unused:UNUSED_PAD src0_sel:WORD_0
	v_exp_f16_sdwa v51, v43 dst_sel:WORD_0 dst_unused:UNUSED_PAD src0_sel:WORD_0
	v_exp_f16_sdwa v52, v44 dst_sel:WORD_0 dst_unused:UNUSED_PAD src0_sel:WORD_0
	v_exp_f16_sdwa v53, v45 dst_sel:WORD_0 dst_unused:UNUSED_PAD src0_sel:WORD_0
	v_exp_f16_sdwa v50, v42 dst_sel:WORD_1 dst_unused:UNUSED_PRESERVE src0_sel:WORD_1
	v_exp_f16_sdwa v51, v43 dst_sel:WORD_1 dst_unused:UNUSED_PRESERVE src0_sel:WORD_1
	v_exp_f16_sdwa v52, v44 dst_sel:WORD_1 dst_unused:UNUSED_PRESERVE src0_sel:WORD_1
	v_exp_f16_sdwa v53, v45 dst_sel:WORD_1 dst_unused:UNUSED_PRESERVE src0_sel:WORD_1
	v_pk_add_f16 v37, v37, v50
	v_pk_add_f16 v36, v36, v51
	v_rcp_f16_e32 v42, v37
	v_rcp_f16_sdwa v37, v37 dst_sel:DWORD dst_unused:UNUSED_PAD src0_sel:WORD_1
	v_pk_add_f16 v35, v35, v52
	v_rcp_f16_e32 v43, v36
	v_rcp_f16_sdwa v36, v36 dst_sel:DWORD dst_unused:UNUSED_PAD src0_sel:WORD_1
	v_pk_add_f16 v34, v34, v53
	v_pk_fma_f16 v22, v62, v50, v22
	v_rcp_f16_e32 v50, v35
	v_rcp_f16_sdwa v35, v35 dst_sel:DWORD dst_unused:UNUSED_PAD src0_sel:WORD_1
	v_pk_fma_f16 v23, v63, v51, v23
	v_rcp_f16_e32 v51, v34
	v_rcp_f16_sdwa v34, v34 dst_sel:DWORD dst_unused:UNUSED_PAD src0_sel:WORD_1
	v_pack_b32_f16 v37, v42, v37
	v_pk_mul_f16 v45, v22, v37
	v_pack_b32_f16 v22, v43, v36
	v_pk_fma_f16 v24, v64, v52, v24
	v_pk_mul_f16 v44, v23, v22
	v_pack_b32_f16 v22, v50, v35
	v_pk_fma_f16 v25, v65, v53, v25
	v_pk_mul_f16 v43, v24, v22
	v_pack_b32_f16 v22, v51, v34
	v_pk_mul_f16 v42, v25, v22
	s_waitcnt vmcnt(0)
	v_pk_mul_f16 v22, v160, v146 op_sel_hi:[0,1]
	v_pk_mul_f16 v23, v160, v147 op_sel_hi:[0,1]
	v_pk_mul_f16 v24, v160, v148 op_sel_hi:[0,1]
	v_pk_mul_f16 v25, v160, v149 op_sel_hi:[0,1]
	v_pk_mul_f16 v50, v159, v146 op_sel_hi:[0,1]
	v_pk_mul_f16 v51, v159, v147 op_sel_hi:[0,1]
	v_pk_mul_f16 v52, v159, v148 op_sel_hi:[0,1]
	v_pk_mul_f16 v53, v159, v149 op_sel_hi:[0,1]
	v_pk_mul_f16 v34, v158, v146 op_sel_hi:[0,1]
	v_pk_mul_f16 v35, v158, v147 op_sel_hi:[0,1]
	v_pk_mul_f16 v36, v158, v148 op_sel_hi:[0,1]
	v_pk_mul_f16 v37, v158, v149 op_sel_hi:[0,1]
	v_pk_fma_f16 v29, v29, v149, v25
	v_pk_fma_f16 v28, v28, v148, v24
	v_pk_fma_f16 v27, v27, v147, v23
	v_pk_fma_f16 v26, v26, v146, v22
	v_pk_fma_f16 v41, v41, v149, v25
	v_pk_fma_f16 v40, v40, v148, v24
	v_pk_fma_f16 v39, v39, v147, v23
	v_pk_fma_f16 v38, v38, v146, v22
	v_pk_fma_f16 v25, v61, v149, v25
	v_pk_fma_f16 v24, v60, v148, v24
	v_pk_fma_f16 v23, v59, v147, v23
	v_pk_fma_f16 v22, v58, v146, v22
	v_pk_fma_f16 v66, v137, v149, v53
	v_pk_fma_f16 v67, v136, v148, v52
	v_pk_fma_f16 v68, v135, v147, v51
	v_pk_fma_f16 v69, v134, v146, v50
	v_pk_fma_f16 v70, v145, v149, v53
	v_pk_fma_f16 v71, v144, v148, v52
	v_pk_fma_f16 v72, v143, v147, v51
	v_pk_fma_f16 v73, v142, v146, v50
	v_pk_fma_f16 v9, v9, v149, v53
	v_pk_fma_f16 v8, v8, v148, v52
	v_pk_fma_f16 v7, v7, v147, v51
	v_pk_fma_f16 v6, v6, v146, v50
	v_pk_maximum3_f16 v50, v26, v38, v22
	v_pk_maximum3_f16 v51, v27, v39, v23
	v_pk_maximum3_f16 v52, v28, v40, v24
	v_pk_maximum3_f16 v53, v29, v41, v25
	v_pk_fma_f16 v54, v81, v149, v37
	v_pk_fma_f16 v55, v80, v148, v36
	v_pk_fma_f16 v56, v79, v147, v35
	v_pk_fma_f16 v57, v78, v146, v34
	v_pk_fma_f16 v58, v109, v149, v37
	v_pk_fma_f16 v59, v108, v148, v36
	v_pk_fma_f16 v60, v107, v147, v35
	v_pk_fma_f16 v61, v106, v146, v34
	v_pk_fma_f16 v37, v125, v149, v37
	v_pk_fma_f16 v36, v124, v148, v36
	v_pk_fma_f16 v35, v123, v147, v35
	v_pk_fma_f16 v34, v122, v146, v34
	v_pk_maximum3_f16 v75, v56, v60, v35
	v_pk_maximum3_f16 v76, v55, v59, v36
	v_pk_maximum3_f16 v77, v54, v58, v37
	v_pk_maximum3_f16 v78, v69, v73, v6
	v_pk_maximum3_f16 v79, v68, v72, v7
	v_pk_maximum3_f16 v74, v57, v61, v34
	v_pk_maximum3_f16 v80, v67, v71, v8
	v_pk_maximum3_f16 v81, v66, v70, v9
	v_pk_maximum3_f16 v50, v50, v74, v78
	v_pk_maximum3_f16 v51, v51, v75, v79
	v_pk_maximum3_f16 v52, v52, v76, v80
	v_pk_maximum3_f16 v53, v53, v77, v81
	s_nop 0
	v_pk_add_f16 v26, v26, v50 neg_lo:[0,1] neg_hi:[0,1]
	v_pk_add_f16 v27, v27, v51 neg_lo:[0,1] neg_hi:[0,1]
	v_pk_add_f16 v28, v28, v52 neg_lo:[0,1] neg_hi:[0,1]
	v_pk_add_f16 v29, v29, v53 neg_lo:[0,1] neg_hi:[0,1]
	v_pk_add_f16 v38, v38, v50 neg_lo:[0,1] neg_hi:[0,1]
	v_exp_f16_sdwa v74, v26 dst_sel:WORD_0 dst_unused:UNUSED_PAD src0_sel:WORD_0
	v_exp_f16_sdwa v75, v27 dst_sel:WORD_0 dst_unused:UNUSED_PAD src0_sel:WORD_0
	v_exp_f16_sdwa v76, v28 dst_sel:WORD_0 dst_unused:UNUSED_PAD src0_sel:WORD_0
	v_exp_f16_sdwa v77, v29 dst_sel:WORD_0 dst_unused:UNUSED_PAD src0_sel:WORD_0
	v_exp_f16_sdwa v74, v26 dst_sel:WORD_1 dst_unused:UNUSED_PRESERVE src0_sel:WORD_1
	v_exp_f16_sdwa v75, v27 dst_sel:WORD_1 dst_unused:UNUSED_PRESERVE src0_sel:WORD_1
	v_exp_f16_sdwa v76, v28 dst_sel:WORD_1 dst_unused:UNUSED_PRESERVE src0_sel:WORD_1
	v_exp_f16_sdwa v77, v29 dst_sel:WORD_1 dst_unused:UNUSED_PRESERVE src0_sel:WORD_1
	v_pk_add_f16 v39, v39, v51 neg_lo:[0,1] neg_hi:[0,1]
	v_pk_add_f16 v26, v74, 0
	v_pk_add_f16 v27, v75, 0
	v_pk_add_f16 v28, v76, 0
	v_pk_add_f16 v29, v77, 0
	v_pk_fma_f16 v10, v10, v74, 0
	v_pk_fma_f16 v11, v11, v75, 0
	v_pk_fma_f16 v12, v12, v76, 0
	v_pk_fma_f16 v13, v13, v77, 0
	v_pk_add_f16 v40, v40, v52 neg_lo:[0,1] neg_hi:[0,1]
	v_pk_add_f16 v41, v41, v53 neg_lo:[0,1] neg_hi:[0,1]
	v_pk_add_f16 v6, v6, v50 neg_lo:[0,1] neg_hi:[0,1]
	v_exp_f16_sdwa v74, v38 dst_sel:WORD_0 dst_unused:UNUSED_PAD src0_sel:WORD_0
	v_exp_f16_sdwa v75, v39 dst_sel:WORD_0 dst_unused:UNUSED_PAD src0_sel:WORD_0
	v_exp_f16_sdwa v76, v40 dst_sel:WORD_0 dst_unused:UNUSED_PAD src0_sel:WORD_0
	v_exp_f16_sdwa v77, v41 dst_sel:WORD_0 dst_unused:UNUSED_PAD src0_sel:WORD_0
	v_exp_f16_sdwa v74, v38 dst_sel:WORD_1 dst_unused:UNUSED_PRESERVE src0_sel:WORD_1
	v_exp_f16_sdwa v75, v39 dst_sel:WORD_1 dst_unused:UNUSED_PRESERVE src0_sel:WORD_1
	v_exp_f16_sdwa v76, v40 dst_sel:WORD_1 dst_unused:UNUSED_PRESERVE src0_sel:WORD_1
	v_exp_f16_sdwa v77, v41 dst_sel:WORD_1 dst_unused:UNUSED_PRESERVE src0_sel:WORD_1
	v_pk_add_f16 v7, v7, v51 neg_lo:[0,1] neg_hi:[0,1]
	v_pk_add_f16 v29, v29, v77
	v_pk_add_f16 v28, v28, v76
	v_pk_add_f16 v27, v27, v75
	v_pk_add_f16 v26, v26, v74
	v_pk_fma_f16 v13, v17, v77, v13
	v_pk_fma_f16 v12, v16, v76, v12
	v_pk_fma_f16 v11, v15, v75, v11
	v_pk_fma_f16 v10, v14, v74, v10
	v_pk_add_f16 v14, v22, v50 neg_lo:[0,1] neg_hi:[0,1]
	v_pk_add_f16 v15, v23, v51 neg_lo:[0,1] neg_hi:[0,1]
	v_pk_add_f16 v16, v24, v52 neg_lo:[0,1] neg_hi:[0,1]
	v_pk_add_f16 v17, v25, v53 neg_lo:[0,1] neg_hi:[0,1]
	v_pk_add_f16 v8, v8, v52 neg_lo:[0,1] neg_hi:[0,1]
	v_exp_f16_sdwa v22, v14 dst_sel:WORD_0 dst_unused:UNUSED_PAD src0_sel:WORD_0
	v_exp_f16_sdwa v23, v15 dst_sel:WORD_0 dst_unused:UNUSED_PAD src0_sel:WORD_0
	v_exp_f16_sdwa v24, v16 dst_sel:WORD_0 dst_unused:UNUSED_PAD src0_sel:WORD_0
	v_exp_f16_sdwa v25, v17 dst_sel:WORD_0 dst_unused:UNUSED_PAD src0_sel:WORD_0
	v_exp_f16_sdwa v22, v14 dst_sel:WORD_1 dst_unused:UNUSED_PRESERVE src0_sel:WORD_1
	v_exp_f16_sdwa v23, v15 dst_sel:WORD_1 dst_unused:UNUSED_PRESERVE src0_sel:WORD_1
	v_exp_f16_sdwa v24, v16 dst_sel:WORD_1 dst_unused:UNUSED_PRESERVE src0_sel:WORD_1
	v_exp_f16_sdwa v25, v17 dst_sel:WORD_1 dst_unused:UNUSED_PRESERVE src0_sel:WORD_1
	v_pk_add_f16 v9, v9, v53 neg_lo:[0,1] neg_hi:[0,1]
	v_pk_add_f16 v14, v26, v22
	v_pk_add_f16 v15, v27, v23
	v_pk_add_f16 v16, v28, v24
	v_pk_add_f16 v17, v29, v25
	v_pk_fma_f16 v10, v18, v22, v10
	v_pk_fma_f16 v11, v19, v23, v11
	v_pk_fma_f16 v12, v20, v24, v12
	v_pk_fma_f16 v13, v21, v25, v13
	v_pk_add_f16 v18, v57, v50 neg_lo:[0,1] neg_hi:[0,1]
	v_pk_add_f16 v19, v56, v51 neg_lo:[0,1] neg_hi:[0,1]
	v_pk_add_f16 v20, v55, v52 neg_lo:[0,1] neg_hi:[0,1]
	v_pk_add_f16 v21, v54, v53 neg_lo:[0,1] neg_hi:[0,1]
	v_exp_f16_sdwa v22, v18 dst_sel:WORD_0 dst_unused:UNUSED_PAD src0_sel:WORD_0
	v_exp_f16_sdwa v23, v19 dst_sel:WORD_0 dst_unused:UNUSED_PAD src0_sel:WORD_0
	v_exp_f16_sdwa v24, v20 dst_sel:WORD_0 dst_unused:UNUSED_PAD src0_sel:WORD_0
	v_exp_f16_sdwa v25, v21 dst_sel:WORD_0 dst_unused:UNUSED_PAD src0_sel:WORD_0
	v_exp_f16_sdwa v22, v18 dst_sel:WORD_1 dst_unused:UNUSED_PRESERVE src0_sel:WORD_1
	v_exp_f16_sdwa v23, v19 dst_sel:WORD_1 dst_unused:UNUSED_PRESERVE src0_sel:WORD_1
	v_exp_f16_sdwa v24, v20 dst_sel:WORD_1 dst_unused:UNUSED_PRESERVE src0_sel:WORD_1
	v_exp_f16_sdwa v25, v21 dst_sel:WORD_1 dst_unused:UNUSED_PRESERVE src0_sel:WORD_1
	v_pk_add_f16 v18, v61, v50 neg_lo:[0,1] neg_hi:[0,1]
	v_pk_add_f16 v17, v17, v25
	v_pk_add_f16 v16, v16, v24
	v_pk_add_f16 v15, v15, v23
	v_pk_add_f16 v14, v14, v22
	v_pk_fma_f16 v13, v33, v25, v13
	v_pk_fma_f16 v12, v32, v24, v12
	v_pk_fma_f16 v11, v31, v23, v11
	v_pk_fma_f16 v10, v30, v22, v10
	v_pk_add_f16 v19, v60, v51 neg_lo:[0,1] neg_hi:[0,1]
	v_pk_add_f16 v20, v59, v52 neg_lo:[0,1] neg_hi:[0,1]
	v_pk_add_f16 v21, v58, v53 neg_lo:[0,1] neg_hi:[0,1]
	v_exp_f16_sdwa v22, v18 dst_sel:WORD_0 dst_unused:UNUSED_PAD src0_sel:WORD_0
	v_exp_f16_sdwa v23, v19 dst_sel:WORD_0 dst_unused:UNUSED_PAD src0_sel:WORD_0
	v_exp_f16_sdwa v24, v20 dst_sel:WORD_0 dst_unused:UNUSED_PAD src0_sel:WORD_0
	v_exp_f16_sdwa v25, v21 dst_sel:WORD_0 dst_unused:UNUSED_PAD src0_sel:WORD_0
	v_exp_f16_sdwa v22, v18 dst_sel:WORD_1 dst_unused:UNUSED_PRESERVE src0_sel:WORD_1
	v_exp_f16_sdwa v23, v19 dst_sel:WORD_1 dst_unused:UNUSED_PRESERVE src0_sel:WORD_1
	v_exp_f16_sdwa v24, v20 dst_sel:WORD_1 dst_unused:UNUSED_PRESERVE src0_sel:WORD_1
	v_exp_f16_sdwa v25, v21 dst_sel:WORD_1 dst_unused:UNUSED_PRESERVE src0_sel:WORD_1
	v_pk_add_f16 v18, v34, v50 neg_lo:[0,1] neg_hi:[0,1]
	v_pk_add_f16 v14, v14, v22
	v_pk_add_f16 v15, v15, v23
	v_pk_add_f16 v16, v16, v24
	v_pk_add_f16 v17, v17, v25
	v_pk_fma_f16 v10, v46, v22, v10
	v_pk_fma_f16 v11, v47, v23, v11
	v_pk_fma_f16 v12, v48, v24, v12
	v_pk_fma_f16 v13, v49, v25, v13
	v_pk_add_f16 v19, v35, v51 neg_lo:[0,1] neg_hi:[0,1]
	v_pk_add_f16 v20, v36, v52 neg_lo:[0,1] neg_hi:[0,1]
	v_pk_add_f16 v21, v37, v53 neg_lo:[0,1] neg_hi:[0,1]
	v_exp_f16_sdwa v22, v18 dst_sel:WORD_0 dst_unused:UNUSED_PAD src0_sel:WORD_0
	v_exp_f16_sdwa v23, v19 dst_sel:WORD_0 dst_unused:UNUSED_PAD src0_sel:WORD_0
	v_exp_f16_sdwa v24, v20 dst_sel:WORD_0 dst_unused:UNUSED_PAD src0_sel:WORD_0
	v_exp_f16_sdwa v25, v21 dst_sel:WORD_0 dst_unused:UNUSED_PAD src0_sel:WORD_0
	v_exp_f16_sdwa v22, v18 dst_sel:WORD_1 dst_unused:UNUSED_PRESERVE src0_sel:WORD_1
	v_exp_f16_sdwa v23, v19 dst_sel:WORD_1 dst_unused:UNUSED_PRESERVE src0_sel:WORD_1
	v_exp_f16_sdwa v24, v20 dst_sel:WORD_1 dst_unused:UNUSED_PRESERVE src0_sel:WORD_1
	v_exp_f16_sdwa v25, v21 dst_sel:WORD_1 dst_unused:UNUSED_PRESERVE src0_sel:WORD_1
	v_pk_add_f16 v18, v69, v50 neg_lo:[0,1] neg_hi:[0,1]
	v_pk_add_f16 v17, v17, v25
	v_pk_add_f16 v16, v16, v24
	v_pk_add_f16 v15, v15, v23
	v_pk_add_f16 v14, v14, v22
	v_pk_fma_f16 v13, v65, v25, v13
	v_pk_fma_f16 v12, v64, v24, v12
	v_pk_fma_f16 v11, v63, v23, v11
	v_pk_fma_f16 v10, v62, v22, v10
	v_pk_add_f16 v19, v68, v51 neg_lo:[0,1] neg_hi:[0,1]
	v_pk_add_f16 v20, v67, v52 neg_lo:[0,1] neg_hi:[0,1]
	v_pk_add_f16 v21, v66, v53 neg_lo:[0,1] neg_hi:[0,1]
	v_exp_f16_sdwa v22, v18 dst_sel:WORD_0 dst_unused:UNUSED_PAD src0_sel:WORD_0
	v_exp_f16_sdwa v23, v19 dst_sel:WORD_0 dst_unused:UNUSED_PAD src0_sel:WORD_0
	v_exp_f16_sdwa v24, v20 dst_sel:WORD_0 dst_unused:UNUSED_PAD src0_sel:WORD_0
	v_exp_f16_sdwa v25, v21 dst_sel:WORD_0 dst_unused:UNUSED_PAD src0_sel:WORD_0
	v_exp_f16_sdwa v22, v18 dst_sel:WORD_1 dst_unused:UNUSED_PRESERVE src0_sel:WORD_1
	v_exp_f16_sdwa v23, v19 dst_sel:WORD_1 dst_unused:UNUSED_PRESERVE src0_sel:WORD_1
	v_exp_f16_sdwa v24, v20 dst_sel:WORD_1 dst_unused:UNUSED_PRESERVE src0_sel:WORD_1
	v_exp_f16_sdwa v25, v21 dst_sel:WORD_1 dst_unused:UNUSED_PRESERVE src0_sel:WORD_1
	v_pk_add_f16 v18, v73, v50 neg_lo:[0,1] neg_hi:[0,1]
	v_pk_add_f16 v14, v14, v22
	v_pk_add_f16 v15, v15, v23
	v_pk_add_f16 v16, v16, v24
	v_pk_add_f16 v17, v17, v25
	v_pk_fma_f16 v10, v82, v22, v10
	v_pk_fma_f16 v11, v83, v23, v11
	v_pk_fma_f16 v12, v84, v24, v12
	v_pk_fma_f16 v13, v85, v25, v13
	v_pk_add_f16 v19, v72, v51 neg_lo:[0,1] neg_hi:[0,1]
	v_pk_add_f16 v20, v71, v52 neg_lo:[0,1] neg_hi:[0,1]
	v_pk_add_f16 v21, v70, v53 neg_lo:[0,1] neg_hi:[0,1]
	v_exp_f16_sdwa v22, v18 dst_sel:WORD_0 dst_unused:UNUSED_PAD src0_sel:WORD_0
	v_exp_f16_sdwa v23, v19 dst_sel:WORD_0 dst_unused:UNUSED_PAD src0_sel:WORD_0
	v_exp_f16_sdwa v24, v20 dst_sel:WORD_0 dst_unused:UNUSED_PAD src0_sel:WORD_0
	v_exp_f16_sdwa v25, v21 dst_sel:WORD_0 dst_unused:UNUSED_PAD src0_sel:WORD_0
	v_exp_f16_sdwa v22, v18 dst_sel:WORD_1 dst_unused:UNUSED_PRESERVE src0_sel:WORD_1
	v_exp_f16_sdwa v23, v19 dst_sel:WORD_1 dst_unused:UNUSED_PRESERVE src0_sel:WORD_1
	v_exp_f16_sdwa v24, v20 dst_sel:WORD_1 dst_unused:UNUSED_PRESERVE src0_sel:WORD_1
	v_exp_f16_sdwa v25, v21 dst_sel:WORD_1 dst_unused:UNUSED_PRESERVE src0_sel:WORD_1
	s_nop 0
	v_pk_add_f16 v17, v17, v25
	v_pk_add_f16 v16, v16, v24
	v_pk_add_f16 v15, v15, v23
	v_pk_add_f16 v14, v14, v22
	v_pk_fma_f16 v21, v105, v25, v13
	v_pk_fma_f16 v20, v104, v24, v12
	v_pk_fma_f16 v19, v103, v23, v11
	v_pk_fma_f16 v18, v102, v22, v10
	v_mov_b32_e32 v13, v5
	v_mov_b32_e32 v12, v4
	v_mov_b32_e32 v11, v3
	v_mov_b32_e32 v10, v2
	v_exp_f16_sdwa v22, v6 dst_sel:WORD_0 dst_unused:UNUSED_PAD src0_sel:WORD_0
	v_exp_f16_sdwa v23, v7 dst_sel:WORD_0 dst_unused:UNUSED_PAD src0_sel:WORD_0
	v_exp_f16_sdwa v24, v8 dst_sel:WORD_0 dst_unused:UNUSED_PAD src0_sel:WORD_0
	v_exp_f16_sdwa v25, v9 dst_sel:WORD_0 dst_unused:UNUSED_PAD src0_sel:WORD_0
	v_exp_f16_sdwa v22, v6 dst_sel:WORD_1 dst_unused:UNUSED_PRESERVE src0_sel:WORD_1
	v_exp_f16_sdwa v23, v7 dst_sel:WORD_1 dst_unused:UNUSED_PRESERVE src0_sel:WORD_1
	v_exp_f16_sdwa v24, v8 dst_sel:WORD_1 dst_unused:UNUSED_PRESERVE src0_sel:WORD_1
	v_exp_f16_sdwa v25, v9 dst_sel:WORD_1 dst_unused:UNUSED_PRESERVE src0_sel:WORD_1
	s_nop 0

.LBB4_4:
	global_load_dwordx4 v[2:5], v[170:171], off
	global_load_dwordx4 v[8:11], v[172:173], off
	global_load_dwordx4 v[210:213], v[170:171], off offset:16
	global_load_dwordx4 v[214:217], v[172:173], off offset:16
	s_lshl_b32 s48, s46, 3
	s_add_i32 s48, s48, s44
	v_or_b32_e32 v199, s48, v178
	v_add_u32_e32 v168, v199, v181
	v_add_u32_e32 v201, -1, v199
	v_mul_lo_u32 v6, v168, s47
	v_or_b32_e32 v7, v201, v182
	v_or_b32_e32 v6, v6, v166
	s_mov_b64 s[4:5], -1
	s_and_b64 vcc, exec, s[26:27]
	v_cmp_gt_u32_e64 s[2:3], 64, v7
	v_lshlrev_b32_e32 v200, 1, v6
	s_cbranch_vccz .LBB4_42
	global_load_dwordx3 v[154:156], v169, s[10:11]
	v_cmp_lt_u32_e64 s[64:65], 0, v199
	v_cmp_gt_u32_e64 s[66:67], 63, v199
	v_cmp_lt_u32_e64 s[68:69], 0, v180
	v_cmp_gt_u32_e64 s[70:71], 60, v180
	buffer_load_dwordx4 v[206:209], v200, s[36:39], 0 offen
	s_and_b64 s[72:73], s[68:69], s[64:65]
	s_and_b64 s[74:75], s[68:69], s[66:67]
	s_and_b64 s[76:77], s[70:71], s[64:65]
	s_and_b64 s[78:79], s[70:71], s[66:67]
	v_add_u32_e32 v245, 0xfffe7c00, v200
	v_add_u32_e32 v246, 0xfffe8000, v200
	s_mov_b64 exec, s[72:73]
	buffer_load_dwordx4 v[122:125], v245, s[36:39], 0 offen
	s_mov_b64 exec, -1
	s_mov_b64 exec, s[68:69]
	buffer_load_dwordx4 v[138:141], v246, s[36:39], 0 offen offset:512
	s_mov_b64 exec, -1
	s_mov_b64 exec, s[74:75]
	buffer_load_dwordx4 v[146:149], v246, s[36:39], 0 offen offset:2048
	s_mov_b64 exec, -1
	v_add_u32_e32 v245, 0xfffffc00, v200
	s_mov_b64 exec, s[64:65]
	buffer_load_dwordx4 v[94:97], v245, s[36:39], 0 offen
	s_mov_b64 exec, -1
	buffer_load_dwordx4 v[118:121], v200, s[36:39], 0 offen offset:512
	s_mov_b64 exec, s[66:67]
	buffer_load_dwordx4 v[134:137], v200, s[36:39], 0 offen offset:2048
	s_mov_b64 exec, -1
	v_add_u32_e32 v245, 0x17c00, v200
	v_add_u32_e32 v246, 0x18000, v200
	s_mov_b64 exec, s[64:65]
	buffer_load_dwordx4 v[62:65], v245, s[36:39], 0 offen
	s_mov_b64 exec, -1
	buffer_load_dwordx4 v[78:81], v246, s[36:39], 0 offen offset:512
	s_mov_b64 exec, s[66:67]
	buffer_load_dwordx4 v[102:105], v246, s[36:39], 0 offen offset:2048
	s_mov_b64 exec, -1
	v_add_u32_e32 v245, 0xfffe7c00, v200
	v_add_u32_e32 v246, 0xfffe8000, v200
	s_mov_b64 exec, s[72:73]
	buffer_load_dwordx4 v[82:85], v245, s[36:39], 0 offen offset:512
	s_mov_b64 exec, -1
	s_mov_b64 exec, s[68:69]
	buffer_load_dwordx4 v[106:109], v246, s[36:39], 0 offen offset:1024
	s_mov_b64 exec, -1
	s_mov_b64 exec, s[74:75]
	buffer_load_dwordx4 v[126:129], v246, s[36:39], 0 offen offset:2560
	s_mov_b64 exec, -1
	v_add_u32_e32 v245, 0xfffffc00, v200
	s_mov_b64 exec, s[64:65]
	buffer_load_dwordx4 v[54:57], v245, s[36:39], 0 offen offset:512
	s_mov_b64 exec, -1
	buffer_load_dwordx4 v[74:77], v200, s[36:39], 0 offen offset:1024
	s_mov_b64 exec, s[66:67]
	buffer_load_dwordx4 v[98:101], v200, s[36:39], 0 offen offset:2560
	s_mov_b64 exec, -1
	v_add_u32_e32 v245, 0x17c00, v200
	v_add_u32_e32 v246, 0x18000, v200
	s_mov_b64 exec, s[64:65]
	buffer_load_dwordx4 v[30:33], v245, s[36:39], 0 offen offset:512
	s_mov_b64 exec, -1
	buffer_load_dwordx4 v[42:45], v246, s[36:39], 0 offen offset:1024
	s_mov_b64 exec, s[66:67]
	buffer_load_dwordx4 v[58:61], v246, s[36:39], 0 offen offset:2560
	s_mov_b64 exec, -1
	v_add_u32_e32 v245, 0x18000, v200
	buffer_load_dwordx4 v[162:165], v245, s[36:39], 0 offen
	v_add_u32_e32 v246, 0x30000, v200
	buffer_load_dwordx4 v[158:161], v246, s[36:39], 0 offen
	v_add_u32_e32 v245, 0x2fc00, v200
	v_add_u32_e32 v246, 0x30000, v200
	v_add_u32_e32 v247, 0x47c00, v200
	v_add_u32_e32 v248, 0x48000, v200
	v_add_u32_e32 v249, 0x5fc00, v200
	v_add_u32_e32 v250, 0x60000, v200
	s_waitcnt vmcnt(22)
	v_cvt_pk_f16_f32 v6, v2, v3
	v_cvt_pk_f16_f32 v2, v8, v9
	v_cvt_pk_f16_f32 v7, v4, v5
	v_cvt_pk_f16_f32 v3, v10, v11
	v_cvt_pk_f16_f32 v8, v210, v211
	v_cvt_pk_f16_f32 v4, v214, v215
	v_cvt_pk_f16_f32 v9, v212, v213
	v_cvt_pk_f16_f32 v5, v216, v217
	s_not_b64 exec, s[72:73]
	s_cbranch_execz .Lmyf_C1_0
	v_mov_b32_e32 v122, v6
	v_mov_b32_e32 v123, v7
	v_mov_b32_e32 v124, v8
	v_mov_b32_e32 v125, v9
	v_mov_b32_e32 v82, v2
	v_mov_b32_e32 v83, v3
	v_mov_b32_e32 v84, v4
	v_mov_b32_e32 v85, v5

.Lmyf_C1_7:
	s_mov_b64 exec, -1
	s_waitcnt vmcnt(21)
	v_cvt_f16_f32_e32 v202, v155
	v_cvt_f16_f32_e32 v204, v154
	v_cvt_f16_f32_e32 v203, v156
	v_add_u32_e32 v251, 0x48000, v200
	buffer_load_dwordx4 v[154:157], v251, s[36:39], 0 offen
	s_mov_b64 s[4:5], 0
	s_waitcnt vmcnt(12)
	v_pk_mul_f16 v212, v204, v209 op_sel_hi:[0,1]
	v_pk_mul_f16 v216, v202, v209 op_sel_hi:[0,1]
	v_pk_mul_f16 v220, v203, v209 op_sel_hi:[0,1]
	v_pk_mul_f16 v205, v204, v206 op_sel_hi:[0,1]
	v_pk_mul_f16 v210, v204, v207 op_sel_hi:[0,1]
	v_pk_mul_f16 v211, v204, v208 op_sel_hi:[0,1]
	v_pk_mul_f16 v213, v202, v206 op_sel_hi:[0,1]
	v_pk_mul_f16 v214, v202, v207 op_sel_hi:[0,1]
	v_pk_mul_f16 v215, v202, v208 op_sel_hi:[0,1]
	v_pk_mul_f16 v217, v203, v206 op_sel_hi:[0,1]
	v_pk_mul_f16 v218, v203, v207 op_sel_hi:[0,1]
	v_pk_mul_f16 v219, v203, v208 op_sel_hi:[0,1]
	v_pk_fma_f16 v125, v125, v209, v212
	v_pk_fma_f16 v141, v141, v209, v216
	v_pk_fma_f16 v149, v149, v209, v220
	v_pk_fma_f16 v221, v97, v209, v212
	v_pk_fma_f16 v225, v121, v209, v216
	v_pk_fma_f16 v229, v137, v209, v220
	v_pk_fma_f16 v212, v65, v209, v212
	v_pk_fma_f16 v216, v81, v209, v216
	v_pk_fma_f16 v209, v105, v209, v220
	v_pk_maximum3_f16 v220, v125, v141, v149
	v_pk_fma_f16 v124, v124, v208, v211
	v_pk_fma_f16 v123, v123, v207, v210
	v_pk_fma_f16 v122, v122, v206, v205
	v_pk_fma_f16 v140, v140, v208, v215
	v_pk_fma_f16 v139, v139, v207, v214
	v_pk_fma_f16 v138, v138, v206, v213
	v_pk_fma_f16 v148, v148, v208, v219
	v_pk_fma_f16 v147, v147, v207, v218
	v_pk_fma_f16 v146, v146, v206, v217
	v_pk_fma_f16 v222, v96, v208, v211
	v_pk_fma_f16 v223, v95, v207, v210
	v_pk_fma_f16 v224, v94, v206, v205
	v_pk_fma_f16 v226, v120, v208, v215
	v_pk_fma_f16 v227, v119, v207, v214
	v_pk_fma_f16 v228, v118, v206, v213
	v_pk_fma_f16 v230, v136, v208, v219
	v_pk_fma_f16 v231, v135, v207, v218
	v_pk_fma_f16 v232, v134, v206, v217
	v_pk_fma_f16 v211, v64, v208, v211
	v_pk_fma_f16 v210, v63, v207, v210
	v_pk_fma_f16 v205, v62, v206, v205
	v_pk_fma_f16 v215, v80, v208, v215
	v_pk_fma_f16 v214, v79, v207, v214
	v_pk_fma_f16 v213, v78, v206, v213
	v_pk_fma_f16 v208, v104, v208, v219
	v_pk_fma_f16 v207, v103, v207, v218
	v_pk_fma_f16 v206, v102, v206, v217
	v_pk_maximum3_f16 v217, v122, v138, v146
	v_pk_maximum3_f16 v218, v123, v139, v147
	v_pk_maximum3_f16 v219, v124, v140, v148
	v_pk_maximum3_f16 v236, v221, v225, v229
	v_pk_maximum3_f16 v240, v212, v216, v209
	v_pk_maximum3_f16 v233, v224, v228, v232
	v_pk_maximum3_f16 v234, v223, v227, v231
	v_pk_maximum3_f16 v235, v222, v226, v230
	v_pk_maximum3_f16 v237, v205, v213, v206
	v_pk_maximum3_f16 v238, v210, v214, v207
	v_pk_maximum3_f16 v220, v220, v236, v240
	v_pk_maximum3_f16 v239, v211, v215, v208
	v_pk_maximum3_f16 v217, v217, v233, v237
	v_pk_maximum3_f16 v218, v218, v234, v238
	v_pk_maximum3_f16 v219, v219, v235, v239
	v_pk_add_f16 v125, v125, v220 neg_lo:[0,1] neg_hi:[0,1]
	v_pk_add_f16 v122, v122, v217 neg_lo:[0,1] neg_hi:[0,1]
	v_pk_add_f16 v123, v123, v218 neg_lo:[0,1] neg_hi:[0,1]
	v_pk_add_f16 v124, v124, v219 neg_lo:[0,1] neg_hi:[0,1]
	v_pk_add_f16 v138, v138, v217 neg_lo:[0,1] neg_hi:[0,1]
	v_exp_f16_sdwa v233, v122 dst_sel:WORD_0 dst_unused:UNUSED_PAD src0_sel:WORD_0
	v_exp_f16_sdwa v234, v123 dst_sel:WORD_0 dst_unused:UNUSED_PAD src0_sel:WORD_0
	v_exp_f16_sdwa v235, v124 dst_sel:WORD_0 dst_unused:UNUSED_PAD src0_sel:WORD_0
	v_exp_f16_sdwa v236, v125 dst_sel:WORD_0 dst_unused:UNUSED_PAD src0_sel:WORD_0
	v_exp_f16_sdwa v233, v122 dst_sel:WORD_1 dst_unused:UNUSED_PRESERVE src0_sel:WORD_1
	v_exp_f16_sdwa v234, v123 dst_sel:WORD_1 dst_unused:UNUSED_PRESERVE src0_sel:WORD_1
	v_exp_f16_sdwa v235, v124 dst_sel:WORD_1 dst_unused:UNUSED_PRESERVE src0_sel:WORD_1
	v_exp_f16_sdwa v236, v125 dst_sel:WORD_1 dst_unused:UNUSED_PRESERVE src0_sel:WORD_1
	v_pk_add_f16 v139, v139, v218 neg_lo:[0,1] neg_hi:[0,1]
	v_pk_add_f16 v125, v233, 0
	s_waitcnt vmcnt(3)
	v_pk_fma_f16 v85, v85, v236, 0
	v_pk_add_f16 v122, v236, 0
	v_pk_add_f16 v123, v235, 0
	v_pk_add_f16 v124, v234, 0
	v_pk_fma_f16 v84, v84, v235, 0
	v_pk_fma_f16 v83, v83, v234, 0
	s_mov_b64 exec, s[64:65]
	buffer_load_dwordx4 v[34:37], v245, s[36:39], 0 offen
	buffer_load_dwordx4 v[18:21], v245, s[36:39], 0 offen offset:512
	s_mov_b64 exec, -1
	v_pk_fma_f16 v82, v82, v233, 0
	v_pk_add_f16 v140, v140, v219 neg_lo:[0,1] neg_hi:[0,1]
	v_pk_add_f16 v141, v141, v220 neg_lo:[0,1] neg_hi:[0,1]
	v_exp_f16_sdwa v233, v138 dst_sel:WORD_0 dst_unused:UNUSED_PAD src0_sel:WORD_0
	v_exp_f16_sdwa v234, v139 dst_sel:WORD_0 dst_unused:UNUSED_PAD src0_sel:WORD_0
	v_exp_f16_sdwa v235, v140 dst_sel:WORD_0 dst_unused:UNUSED_PAD src0_sel:WORD_0
	v_exp_f16_sdwa v236, v141 dst_sel:WORD_0 dst_unused:UNUSED_PAD src0_sel:WORD_0
	v_exp_f16_sdwa v233, v138 dst_sel:WORD_1 dst_unused:UNUSED_PRESERVE src0_sel:WORD_1
	v_exp_f16_sdwa v234, v139 dst_sel:WORD_1 dst_unused:UNUSED_PRESERVE src0_sel:WORD_1
	v_exp_f16_sdwa v235, v140 dst_sel:WORD_1 dst_unused:UNUSED_PRESERVE src0_sel:WORD_1
	v_exp_f16_sdwa v236, v141 dst_sel:WORD_1 dst_unused:UNUSED_PRESERVE src0_sel:WORD_1
	v_pk_add_f16 v125, v125, v233
	v_pk_fma_f16 v85, v109, v236, v85
	v_pk_add_f16 v109, v149, v220 neg_lo:[0,1] neg_hi:[0,1]
	v_pk_add_f16 v124, v124, v234
	v_pk_add_f16 v123, v123, v235
	v_pk_add_f16 v122, v122, v236
	buffer_load_dwordx4 v[46:49], v246, s[36:39], 0 offen offset:512
	buffer_load_dwordx4 v[22:25], v246, s[36:39], 0 offen offset:1024
	v_pk_fma_f16 v82, v106, v233, v82
	v_pk_fma_f16 v83, v107, v234, v83
	v_pk_fma_f16 v84, v108, v235, v84
	v_pk_add_f16 v106, v146, v217 neg_lo:[0,1] neg_hi:[0,1]
	v_pk_add_f16 v107, v147, v218 neg_lo:[0,1] neg_hi:[0,1]
	v_pk_add_f16 v108, v148, v219 neg_lo:[0,1] neg_hi:[0,1]
	v_exp_f16_sdwa v138, v106 dst_sel:WORD_0 dst_unused:UNUSED_PAD src0_sel:WORD_0
	v_exp_f16_sdwa v139, v107 dst_sel:WORD_0 dst_unused:UNUSED_PAD src0_sel:WORD_0
	v_exp_f16_sdwa v140, v108 dst_sel:WORD_0 dst_unused:UNUSED_PAD src0_sel:WORD_0
	v_exp_f16_sdwa v141, v109 dst_sel:WORD_0 dst_unused:UNUSED_PAD src0_sel:WORD_0
	v_exp_f16_sdwa v138, v106 dst_sel:WORD_1 dst_unused:UNUSED_PRESERVE src0_sel:WORD_1
	v_exp_f16_sdwa v139, v107 dst_sel:WORD_1 dst_unused:UNUSED_PRESERVE src0_sel:WORD_1
	v_exp_f16_sdwa v140, v108 dst_sel:WORD_1 dst_unused:UNUSED_PRESERVE src0_sel:WORD_1
	v_exp_f16_sdwa v141, v109 dst_sel:WORD_1 dst_unused:UNUSED_PRESERVE src0_sel:WORD_1
	v_pk_add_f16 v109, v125, v138
	v_pk_add_f16 v106, v122, v141
	v_pk_add_f16 v107, v123, v140
	s_mov_b64 exec, s[66:67]
	buffer_load_dwordx4 v[66:69], v246, s[36:39], 0 offen offset:2048
	buffer_load_dwordx4 v[26:29], v246, s[36:39], 0 offen offset:2560
	s_mov_b64 exec, -1
	v_pk_add_f16 v108, v124, v139
	v_pk_fma_f16 v85, v129, v141, v85
	v_pk_fma_f16 v84, v128, v140, v84
	v_pk_fma_f16 v83, v127, v139, v83
	v_pk_fma_f16 v82, v126, v138, v82
	v_pk_add_f16 v122, v224, v217 neg_lo:[0,1] neg_hi:[0,1]
	v_pk_add_f16 v123, v223, v218 neg_lo:[0,1] neg_hi:[0,1]
	v_pk_add_f16 v124, v222, v219 neg_lo:[0,1] neg_hi:[0,1]
	s_mov_b64 exec, s[64:65]
	buffer_load_dwordx4 v[86:89], v247, s[36:39], 0 offen
	buffer_load_dwordx4 v[38:41], v247, s[36:39], 0 offen offset:512
	s_mov_b64 exec, -1
	v_pk_add_f16 v125, v221, v220 neg_lo:[0,1] neg_hi:[0,1]
	v_exp_f16_sdwa v126, v122 dst_sel:WORD_0 dst_unused:UNUSED_PAD src0_sel:WORD_0
	v_exp_f16_sdwa v127, v123 dst_sel:WORD_0 dst_unused:UNUSED_PAD src0_sel:WORD_0
	v_exp_f16_sdwa v128, v124 dst_sel:WORD_0 dst_unused:UNUSED_PAD src0_sel:WORD_0
	v_exp_f16_sdwa v129, v125 dst_sel:WORD_0 dst_unused:UNUSED_PAD src0_sel:WORD_0
	v_exp_f16_sdwa v126, v122 dst_sel:WORD_1 dst_unused:UNUSED_PRESERVE src0_sel:WORD_1
	v_exp_f16_sdwa v127, v123 dst_sel:WORD_1 dst_unused:UNUSED_PRESERVE src0_sel:WORD_1
	v_exp_f16_sdwa v128, v124 dst_sel:WORD_1 dst_unused:UNUSED_PRESERVE src0_sel:WORD_1
	v_exp_f16_sdwa v129, v125 dst_sel:WORD_1 dst_unused:UNUSED_PRESERVE src0_sel:WORD_1
	v_pk_add_f16 v122, v228, v217 neg_lo:[0,1] neg_hi:[0,1]
	v_pk_add_f16 v109, v109, v126
	v_pk_add_f16 v108, v108, v127
	v_pk_add_f16 v107, v107, v128
	v_pk_add_f16 v106, v106, v129
	v_pk_fma_f16 v82, v54, v126, v82
	v_pk_fma_f16 v83, v55, v127, v83
	v_pk_fma_f16 v84, v56, v128, v84
	v_pk_fma_f16 v85, v57, v129, v85
	buffer_load_dwordx4 v[114:117], v248, s[36:39], 0 offen offset:512
	buffer_load_dwordx4 v[50:53], v248, s[36:39], 0 offen offset:1024
	v_pk_add_f16 v123, v227, v218 neg_lo:[0,1] neg_hi:[0,1]
	v_pk_add_f16 v124, v226, v219 neg_lo:[0,1] neg_hi:[0,1]
	v_pk_add_f16 v125, v225, v220 neg_lo:[0,1] neg_hi:[0,1]
	v_exp_f16_sdwa v126, v122 dst_sel:WORD_0 dst_unused:UNUSED_PAD src0_sel:WORD_0
	v_exp_f16_sdwa v127, v123 dst_sel:WORD_0 dst_unused:UNUSED_PAD src0_sel:WORD_0
	v_exp_f16_sdwa v128, v124 dst_sel:WORD_0 dst_unused:UNUSED_PAD src0_sel:WORD_0
	v_exp_f16_sdwa v129, v125 dst_sel:WORD_0 dst_unused:UNUSED_PAD src0_sel:WORD_0
	v_exp_f16_sdwa v126, v122 dst_sel:WORD_1 dst_unused:UNUSED_PRESERVE src0_sel:WORD_1
	v_exp_f16_sdwa v127, v123 dst_sel:WORD_1 dst_unused:UNUSED_PRESERVE src0_sel:WORD_1
	v_exp_f16_sdwa v128, v124 dst_sel:WORD_1 dst_unused:UNUSED_PRESERVE src0_sel:WORD_1
	v_exp_f16_sdwa v129, v125 dst_sel:WORD_1 dst_unused:UNUSED_PRESERVE src0_sel:WORD_1
	v_pk_add_f16 v122, v232, v217 neg_lo:[0,1] neg_hi:[0,1]
	v_pk_add_f16 v109, v109, v126
	v_pk_add_f16 v106, v106, v129
	v_pk_add_f16 v107, v107, v128
	v_pk_add_f16 v108, v108, v127
	v_pk_fma_f16 v85, v77, v129, v85
	s_mov_b64 exec, s[66:67]
	buffer_load_dwordx4 v[130:133], v248, s[36:39], 0 offen offset:2048
	buffer_load_dwordx4 v[70:73], v248, s[36:39], 0 offen offset:2560
	s_mov_b64 exec, -1
	v_pk_fma_f16 v84, v76, v128, v84
	v_pk_fma_f16 v83, v75, v127, v83
	v_pk_fma_f16 v82, v74, v126, v82
	v_pk_add_f16 v123, v231, v218 neg_lo:[0,1] neg_hi:[0,1]
	v_pk_add_f16 v124, v230, v219 neg_lo:[0,1] neg_hi:[0,1]
	v_pk_add_f16 v125, v229, v220 neg_lo:[0,1] neg_hi:[0,1]
	v_exp_f16_sdwa v126, v122 dst_sel:WORD_0 dst_unused:UNUSED_PAD src0_sel:WORD_0
	v_exp_f16_sdwa v127, v123 dst_sel:WORD_0 dst_unused:UNUSED_PAD src0_sel:WORD_0
	v_exp_f16_sdwa v128, v124 dst_sel:WORD_0 dst_unused:UNUSED_PAD src0_sel:WORD_0
	v_exp_f16_sdwa v129, v125 dst_sel:WORD_0 dst_unused:UNUSED_PAD src0_sel:WORD_0
	v_exp_f16_sdwa v126, v122 dst_sel:WORD_1 dst_unused:UNUSED_PRESERVE src0_sel:WORD_1
	v_exp_f16_sdwa v127, v123 dst_sel:WORD_1 dst_unused:UNUSED_PRESERVE src0_sel:WORD_1
	v_exp_f16_sdwa v128, v124 dst_sel:WORD_1 dst_unused:UNUSED_PRESERVE src0_sel:WORD_1
	v_exp_f16_sdwa v129, v125 dst_sel:WORD_1 dst_unused:UNUSED_PRESERVE src0_sel:WORD_1
	v_pk_add_f16 v122, v205, v217 neg_lo:[0,1] neg_hi:[0,1]
	v_pk_add_f16 v109, v109, v126
	v_pk_add_f16 v108, v108, v127
	s_mov_b64 exec, s[76:77]
	buffer_load_dwordx4 v[142:145], v249, s[36:39], 0 offen
	buffer_load_dwordx4 v[90:93], v249, s[36:39], 0 offen offset:512
	s_mov_b64 exec, -1
	v_pk_add_f16 v107, v107, v128
	v_pk_add_f16 v106, v106, v129
	v_pk_fma_f16 v82, v98, v126, v82
	v_pk_fma_f16 v83, v99, v127, v83
	v_pk_fma_f16 v84, v100, v128, v84
	v_pk_fma_f16 v85, v101, v129, v85
	v_pk_add_f16 v123, v210, v218 neg_lo:[0,1] neg_hi:[0,1]
	v_pk_add_f16 v124, v211, v219 neg_lo:[0,1] neg_hi:[0,1]
	s_mov_b64 exec, s[70:71]
	buffer_load_dwordx4 v[150:153], v250, s[36:39], 0 offen offset:512
	buffer_load_dwordx4 v[110:113], v250, s[36:39], 0 offen offset:1024
	s_mov_b64 exec, -1
	v_pk_add_f16 v125, v212, v220 neg_lo:[0,1] neg_hi:[0,1]
	v_exp_f16_sdwa v126, v122 dst_sel:WORD_0 dst_unused:UNUSED_PAD src0_sel:WORD_0
	v_exp_f16_sdwa v127, v123 dst_sel:WORD_0 dst_unused:UNUSED_PAD src0_sel:WORD_0
	v_exp_f16_sdwa v128, v124 dst_sel:WORD_0 dst_unused:UNUSED_PAD src0_sel:WORD_0
	v_exp_f16_sdwa v129, v125 dst_sel:WORD_0 dst_unused:UNUSED_PAD src0_sel:WORD_0
	v_exp_f16_sdwa v126, v122 dst_sel:WORD_1 dst_unused:UNUSED_PRESERVE src0_sel:WORD_1
	v_exp_f16_sdwa v127, v123 dst_sel:WORD_1 dst_unused:UNUSED_PRESERVE src0_sel:WORD_1
	v_exp_f16_sdwa v128, v124 dst_sel:WORD_1 dst_unused:UNUSED_PRESERVE src0_sel:WORD_1
	v_exp_f16_sdwa v129, v125 dst_sel:WORD_1 dst_unused:UNUSED_PRESERVE src0_sel:WORD_1
	v_pk_add_f16 v122, v213, v217 neg_lo:[0,1] neg_hi:[0,1]
	v_pk_add_f16 v109, v109, v126
	v_pk_add_f16 v106, v106, v129
	v_pk_add_f16 v107, v107, v128
	v_pk_add_f16 v108, v108, v127
	v_pk_fma_f16 v85, v33, v129, v85
	v_pk_fma_f16 v84, v32, v128, v84
	v_pk_fma_f16 v83, v31, v127, v83
	s_mov_b64 exec, s[78:79]
	buffer_load_dwordx4 v[14:17], v250, s[36:39], 0 offen offset:2048
	buffer_load_dwordx4 v[10:13], v250, s[36:39], 0 offen offset:2560
	s_mov_b64 exec, -1
	v_pk_fma_f16 v82, v30, v126, v82
	v_pk_add_f16 v123, v214, v218 neg_lo:[0,1] neg_hi:[0,1]
	v_pk_add_f16 v124, v215, v219 neg_lo:[0,1] neg_hi:[0,1]
	v_pk_add_f16 v125, v216, v220 neg_lo:[0,1] neg_hi:[0,1]
	v_exp_f16_sdwa v126, v122 dst_sel:WORD_0 dst_unused:UNUSED_PAD src0_sel:WORD_0
	v_exp_f16_sdwa v127, v123 dst_sel:WORD_0 dst_unused:UNUSED_PAD src0_sel:WORD_0
	v_exp_f16_sdwa v128, v124 dst_sel:WORD_0 dst_unused:UNUSED_PAD src0_sel:WORD_0
	v_exp_f16_sdwa v129, v125 dst_sel:WORD_0 dst_unused:UNUSED_PAD src0_sel:WORD_0
	v_exp_f16_sdwa v126, v122 dst_sel:WORD_1 dst_unused:UNUSED_PRESERVE src0_sel:WORD_1
	v_exp_f16_sdwa v127, v123 dst_sel:WORD_1 dst_unused:UNUSED_PRESERVE src0_sel:WORD_1
	v_exp_f16_sdwa v128, v124 dst_sel:WORD_1 dst_unused:UNUSED_PRESERVE src0_sel:WORD_1
	v_exp_f16_sdwa v129, v125 dst_sel:WORD_1 dst_unused:UNUSED_PRESERVE src0_sel:WORD_1
	v_pk_add_f16 v122, v206, v217 neg_lo:[0,1] neg_hi:[0,1]
	v_pk_add_f16 v109, v109, v126
	v_pk_add_f16 v108, v108, v127
	v_pk_add_f16 v107, v107, v128
	v_pk_add_f16 v106, v106, v129
	v_pk_fma_f16 v82, v42, v126, v82
	v_pk_fma_f16 v83, v43, v127, v83
	v_pk_fma_f16 v84, v44, v128, v84
	v_pk_fma_f16 v85, v45, v129, v85
	v_pk_add_f16 v123, v207, v218 neg_lo:[0,1] neg_hi:[0,1]
	v_pk_add_f16 v124, v208, v219 neg_lo:[0,1] neg_hi:[0,1]
	v_pk_add_f16 v125, v209, v220 neg_lo:[0,1] neg_hi:[0,1]
	v_exp_f16_sdwa v126, v122 dst_sel:WORD_0 dst_unused:UNUSED_PAD src0_sel:WORD_0
	v_exp_f16_sdwa v127, v123 dst_sel:WORD_0 dst_unused:UNUSED_PAD src0_sel:WORD_0
	v_exp_f16_sdwa v128, v124 dst_sel:WORD_0 dst_unused:UNUSED_PAD src0_sel:WORD_0
	v_exp_f16_sdwa v129, v125 dst_sel:WORD_0 dst_unused:UNUSED_PAD src0_sel:WORD_0
	v_exp_f16_sdwa v126, v122 dst_sel:WORD_1 dst_unused:UNUSED_PRESERVE src0_sel:WORD_1
	v_exp_f16_sdwa v127, v123 dst_sel:WORD_1 dst_unused:UNUSED_PRESERVE src0_sel:WORD_1
	v_exp_f16_sdwa v128, v124 dst_sel:WORD_1 dst_unused:UNUSED_PRESERVE src0_sel:WORD_1
	v_exp_f16_sdwa v129, v125 dst_sel:WORD_1 dst_unused:UNUSED_PRESERVE src0_sel:WORD_1
	v_pk_add_f16 v109, v109, v126
	v_pk_add_f16 v108, v108, v127
	v_rcp_f16_e32 v122, v109
	v_rcp_f16_sdwa v109, v109 dst_sel:DWORD dst_unused:UNUSED_PAD src0_sel:WORD_1
	v_pk_add_f16 v107, v107, v128
	v_rcp_f16_e32 v123, v108
	v_rcp_f16_sdwa v108, v108 dst_sel:DWORD dst_unused:UNUSED_PAD src0_sel:WORD_1
	v_pk_add_f16 v106, v106, v129
	v_rcp_f16_e32 v124, v107
	v_rcp_f16_sdwa v107, v107 dst_sel:DWORD dst_unused:UNUSED_PAD src0_sel:WORD_1
	v_rcp_f16_e32 v125, v106
	v_rcp_f16_sdwa v106, v106 dst_sel:DWORD dst_unused:UNUSED_PAD src0_sel:WORD_1
	v_pk_fma_f16 v82, v58, v126, v82
	v_pack_b32_f16 v109, v122, v109
	v_pk_fma_f16 v83, v59, v127, v83
	v_pk_mul_f16 v138, v82, v109
	v_pack_b32_f16 v82, v123, v108
	v_pk_fma_f16 v84, v60, v128, v84
	v_pk_mul_f16 v139, v83, v82
	v_pack_b32_f16 v82, v124, v107
	v_pk_fma_f16 v85, v61, v129, v85
	v_pk_mul_f16 v140, v84, v82
	v_pack_b32_f16 v82, v125, v106
	v_pk_mul_f16 v141, v85, v82
	s_waitcnt vmcnt(12)
	v_pk_mul_f16 v85, v204, v165 op_sel_hi:[0,1]
	v_pk_mul_f16 v109, v202, v165 op_sel_hi:[0,1]
	v_pk_mul_f16 v122, v203, v162 op_sel_hi:[0,1]
	v_pk_mul_f16 v125, v203, v165 op_sel_hi:[0,1]
	v_pk_mul_f16 v82, v204, v162 op_sel_hi:[0,1]
	v_pk_mul_f16 v83, v204, v163 op_sel_hi:[0,1]
	v_pk_mul_f16 v84, v204, v164 op_sel_hi:[0,1]
	v_pk_mul_f16 v106, v202, v162 op_sel_hi:[0,1]
	v_pk_mul_f16 v107, v202, v163 op_sel_hi:[0,1]
	v_pk_mul_f16 v108, v202, v164 op_sel_hi:[0,1]
	v_pk_mul_f16 v123, v203, v163 op_sel_hi:[0,1]
	v_pk_mul_f16 v124, v203, v164 op_sel_hi:[0,1]
	v_pk_fma_f16 v97, v97, v165, v85
	v_pk_fma_f16 v121, v121, v165, v109
	v_pk_fma_f16 v126, v137, v165, v125
	v_pk_fma_f16 v129, v134, v162, v122
	v_pk_fma_f16 v134, v65, v165, v85
	v_pk_fma_f16 v146, v81, v165, v109
	v_pk_fma_f16 v205, v105, v165, v125
	v_pk_fma_f16 v85, v37, v165, v85
	v_pk_fma_f16 v109, v49, v165, v109
	v_pk_fma_f16 v125, v69, v165, v125
	v_pk_maximum3_f16 v165, v97, v121, v126
	v_pk_fma_f16 v96, v96, v164, v84
	v_pk_fma_f16 v95, v95, v163, v83
	v_pk_fma_f16 v94, v94, v162, v82
	v_pk_fma_f16 v120, v120, v164, v108
	v_pk_fma_f16 v119, v119, v163, v107
	v_pk_fma_f16 v118, v118, v162, v106
	v_pk_fma_f16 v127, v136, v164, v124
	v_pk_fma_f16 v128, v135, v163, v123
	v_pk_fma_f16 v135, v64, v164, v84
	v_pk_fma_f16 v136, v63, v163, v83
	v_pk_fma_f16 v137, v62, v162, v82
	v_pk_fma_f16 v147, v80, v164, v108
	v_pk_fma_f16 v148, v79, v163, v107
	v_pk_fma_f16 v149, v78, v162, v106
	v_pk_fma_f16 v206, v104, v164, v124
	v_pk_fma_f16 v207, v103, v163, v123
	v_pk_fma_f16 v208, v102, v162, v122
	v_pk_fma_f16 v84, v36, v164, v84
	v_pk_fma_f16 v83, v35, v163, v83
	v_pk_fma_f16 v82, v34, v162, v82
	v_pk_fma_f16 v108, v48, v164, v108
	v_pk_fma_f16 v107, v47, v163, v107
	v_pk_fma_f16 v106, v46, v162, v106
	v_pk_fma_f16 v124, v68, v164, v124
	v_pk_fma_f16 v123, v67, v163, v123
	v_pk_fma_f16 v122, v66, v162, v122
	v_pk_maximum3_f16 v162, v94, v118, v129
	v_pk_maximum3_f16 v163, v95, v119, v128
	v_pk_maximum3_f16 v164, v96, v120, v127
	v_pk_maximum3_f16 v212, v134, v146, v205
	v_pk_maximum3_f16 v216, v85, v109, v125
	v_pk_maximum3_f16 v209, v137, v149, v208
	v_pk_maximum3_f16 v210, v136, v148, v207
	v_pk_maximum3_f16 v211, v135, v147, v206
	v_pk_maximum3_f16 v213, v82, v106, v122
	v_pk_maximum3_f16 v214, v83, v107, v123
	v_pk_maximum3_f16 v165, v165, v212, v216
	v_pk_maximum3_f16 v215, v84, v108, v124
	v_pk_maximum3_f16 v162, v162, v209, v213
	v_pk_maximum3_f16 v163, v163, v210, v214
	v_pk_maximum3_f16 v164, v164, v211, v215
	v_pk_add_f16 v97, v97, v165 neg_lo:[0,1] neg_hi:[0,1]
	v_pk_add_f16 v94, v94, v162 neg_lo:[0,1] neg_hi:[0,1]
	v_pk_add_f16 v95, v95, v163 neg_lo:[0,1] neg_hi:[0,1]
	v_pk_add_f16 v96, v96, v164 neg_lo:[0,1] neg_hi:[0,1]
	v_pk_add_f16 v118, v118, v162 neg_lo:[0,1] neg_hi:[0,1]
	v_exp_f16_sdwa v209, v94 dst_sel:WORD_0 dst_unused:UNUSED_PAD src0_sel:WORD_0
	v_exp_f16_sdwa v210, v95 dst_sel:WORD_0 dst_unused:UNUSED_PAD src0_sel:WORD_0
	v_exp_f16_sdwa v211, v96 dst_sel:WORD_0 dst_unused:UNUSED_PAD src0_sel:WORD_0
	v_exp_f16_sdwa v212, v97 dst_sel:WORD_0 dst_unused:UNUSED_PAD src0_sel:WORD_0
	v_exp_f16_sdwa v209, v94 dst_sel:WORD_1 dst_unused:UNUSED_PRESERVE src0_sel:WORD_1
	v_exp_f16_sdwa v210, v95 dst_sel:WORD_1 dst_unused:UNUSED_PRESERVE src0_sel:WORD_1
	v_exp_f16_sdwa v211, v96 dst_sel:WORD_1 dst_unused:UNUSED_PRESERVE src0_sel:WORD_1
	v_exp_f16_sdwa v212, v97 dst_sel:WORD_1 dst_unused:UNUSED_PRESERVE src0_sel:WORD_1
	v_pk_add_f16 v119, v119, v163 neg_lo:[0,1] neg_hi:[0,1]
	v_pk_add_f16 v97, v209, 0
	v_pk_fma_f16 v57, v57, v212, 0
	v_pk_add_f16 v94, v212, 0
	v_pk_add_f16 v95, v211, 0
	v_pk_add_f16 v96, v210, 0
	v_pk_fma_f16 v56, v56, v211, 0
	v_pk_fma_f16 v55, v55, v210, 0
	v_pk_fma_f16 v54, v54, v209, 0
	v_pk_add_f16 v120, v120, v164 neg_lo:[0,1] neg_hi:[0,1]
	v_pk_add_f16 v121, v121, v165 neg_lo:[0,1] neg_hi:[0,1]
	v_pk_add_f16 v82, v82, v162 neg_lo:[0,1] neg_hi:[0,1]
	v_exp_f16_sdwa v209, v118 dst_sel:WORD_0 dst_unused:UNUSED_PAD src0_sel:WORD_0
	v_exp_f16_sdwa v210, v119 dst_sel:WORD_0 dst_unused:UNUSED_PAD src0_sel:WORD_0
	v_exp_f16_sdwa v211, v120 dst_sel:WORD_0 dst_unused:UNUSED_PAD src0_sel:WORD_0
	v_exp_f16_sdwa v212, v121 dst_sel:WORD_0 dst_unused:UNUSED_PAD src0_sel:WORD_0
	v_exp_f16_sdwa v209, v118 dst_sel:WORD_1 dst_unused:UNUSED_PRESERVE src0_sel:WORD_1
	v_exp_f16_sdwa v210, v119 dst_sel:WORD_1 dst_unused:UNUSED_PRESERVE src0_sel:WORD_1
	v_exp_f16_sdwa v211, v120 dst_sel:WORD_1 dst_unused:UNUSED_PRESERVE src0_sel:WORD_1
	v_exp_f16_sdwa v212, v121 dst_sel:WORD_1 dst_unused:UNUSED_PRESERVE src0_sel:WORD_1
	v_pk_add_f16 v83, v83, v163 neg_lo:[0,1] neg_hi:[0,1]
	v_pk_add_f16 v97, v97, v209
	v_pk_fma_f16 v57, v77, v212, v57
	v_pk_add_f16 v77, v126, v165 neg_lo:[0,1] neg_hi:[0,1]
	v_pk_add_f16 v96, v96, v210
	v_pk_add_f16 v95, v95, v211
	v_pk_add_f16 v94, v94, v212
	v_pk_fma_f16 v54, v74, v209, v54
	v_pk_fma_f16 v55, v75, v210, v55
	v_pk_fma_f16 v56, v76, v211, v56
	v_pk_add_f16 v74, v129, v162 neg_lo:[0,1] neg_hi:[0,1]
	v_pk_add_f16 v75, v128, v163 neg_lo:[0,1] neg_hi:[0,1]
	v_pk_add_f16 v76, v127, v164 neg_lo:[0,1] neg_hi:[0,1]
	v_pk_add_f16 v84, v84, v164 neg_lo:[0,1] neg_hi:[0,1]
	v_exp_f16_sdwa v118, v74 dst_sel:WORD_0 dst_unused:UNUSED_PAD src0_sel:WORD_0
	v_exp_f16_sdwa v119, v75 dst_sel:WORD_0 dst_unused:UNUSED_PAD src0_sel:WORD_0
	v_exp_f16_sdwa v120, v76 dst_sel:WORD_0 dst_unused:UNUSED_PAD src0_sel:WORD_0
	v_exp_f16_sdwa v121, v77 dst_sel:WORD_0 dst_unused:UNUSED_PAD src0_sel:WORD_0
	v_exp_f16_sdwa v118, v74 dst_sel:WORD_1 dst_unused:UNUSED_PRESERVE src0_sel:WORD_1
	v_exp_f16_sdwa v119, v75 dst_sel:WORD_1 dst_unused:UNUSED_PRESERVE src0_sel:WORD_1
	v_exp_f16_sdwa v120, v76 dst_sel:WORD_1 dst_unused:UNUSED_PRESERVE src0_sel:WORD_1
	v_exp_f16_sdwa v121, v77 dst_sel:WORD_1 dst_unused:UNUSED_PRESERVE src0_sel:WORD_1
	v_pk_add_f16 v85, v85, v165 neg_lo:[0,1] neg_hi:[0,1]
	v_pk_add_f16 v77, v97, v118
	v_pk_add_f16 v74, v94, v121
	v_pk_add_f16 v75, v95, v120
	v_pk_add_f16 v76, v96, v119
	v_pk_fma_f16 v57, v101, v121, v57
	v_pk_fma_f16 v56, v100, v120, v56
	v_pk_fma_f16 v55, v99, v119, v55
	v_pk_fma_f16 v54, v98, v118, v54
	v_pk_add_f16 v94, v137, v162 neg_lo:[0,1] neg_hi:[0,1]
	v_pk_add_f16 v95, v136, v163 neg_lo:[0,1] neg_hi:[0,1]
	v_pk_add_f16 v96, v135, v164 neg_lo:[0,1] neg_hi:[0,1]
	v_pk_add_f16 v97, v134, v165 neg_lo:[0,1] neg_hi:[0,1]
	v_exp_f16_sdwa v98, v94 dst_sel:WORD_0 dst_unused:UNUSED_PAD src0_sel:WORD_0
	v_exp_f16_sdwa v99, v95 dst_sel:WORD_0 dst_unused:UNUSED_PAD src0_sel:WORD_0
	v_exp_f16_sdwa v100, v96 dst_sel:WORD_0 dst_unused:UNUSED_PAD src0_sel:WORD_0
	v_exp_f16_sdwa v101, v97 dst_sel:WORD_0 dst_unused:UNUSED_PAD src0_sel:WORD_0
	v_exp_f16_sdwa v98, v94 dst_sel:WORD_1 dst_unused:UNUSED_PRESERVE src0_sel:WORD_1
	v_exp_f16_sdwa v99, v95 dst_sel:WORD_1 dst_unused:UNUSED_PRESERVE src0_sel:WORD_1
	v_exp_f16_sdwa v100, v96 dst_sel:WORD_1 dst_unused:UNUSED_PRESERVE src0_sel:WORD_1
	v_exp_f16_sdwa v101, v97 dst_sel:WORD_1 dst_unused:UNUSED_PRESERVE src0_sel:WORD_1
	v_pk_add_f16 v94, v149, v162 neg_lo:[0,1] neg_hi:[0,1]
	v_pk_add_f16 v77, v77, v98
	v_pk_add_f16 v76, v76, v99
	v_pk_add_f16 v75, v75, v100
	v_pk_add_f16 v74, v74, v101
	v_pk_fma_f16 v54, v30, v98, v54
	v_pk_fma_f16 v55, v31, v99, v55
	v_pk_fma_f16 v56, v32, v100, v56
	v_pk_fma_f16 v57, v33, v101, v57
	v_pk_add_f16 v95, v148, v163 neg_lo:[0,1] neg_hi:[0,1]
	v_pk_add_f16 v96, v147, v164 neg_lo:[0,1] neg_hi:[0,1]
	v_pk_add_f16 v97, v146, v165 neg_lo:[0,1] neg_hi:[0,1]
	v_exp_f16_sdwa v98, v94 dst_sel:WORD_0 dst_unused:UNUSED_PAD src0_sel:WORD_0
	v_exp_f16_sdwa v99, v95 dst_sel:WORD_0 dst_unused:UNUSED_PAD src0_sel:WORD_0
	v_exp_f16_sdwa v100, v96 dst_sel:WORD_0 dst_unused:UNUSED_PAD src0_sel:WORD_0
	v_exp_f16_sdwa v101, v97 dst_sel:WORD_0 dst_unused:UNUSED_PAD src0_sel:WORD_0
	v_exp_f16_sdwa v98, v94 dst_sel:WORD_1 dst_unused:UNUSED_PRESERVE src0_sel:WORD_1
	v_exp_f16_sdwa v99, v95 dst_sel:WORD_1 dst_unused:UNUSED_PRESERVE src0_sel:WORD_1
	v_exp_f16_sdwa v100, v96 dst_sel:WORD_1 dst_unused:UNUSED_PRESERVE src0_sel:WORD_1
	v_exp_f16_sdwa v101, v97 dst_sel:WORD_1 dst_unused:UNUSED_PRESERVE src0_sel:WORD_1
	v_pk_add_f16 v94, v208, v162 neg_lo:[0,1] neg_hi:[0,1]
	v_pk_add_f16 v77, v77, v98
	v_pk_add_f16 v74, v74, v101
	v_pk_add_f16 v75, v75, v100
	v_pk_add_f16 v76, v76, v99
	v_pk_fma_f16 v57, v45, v101, v57
	v_pk_fma_f16 v56, v44, v100, v56
	v_pk_fma_f16 v55, v43, v99, v55
	v_pk_fma_f16 v54, v42, v98, v54
	v_pk_add_f16 v95, v207, v163 neg_lo:[0,1] neg_hi:[0,1]
	v_pk_add_f16 v96, v206, v164 neg_lo:[0,1] neg_hi:[0,1]
	v_pk_add_f16 v97, v205, v165 neg_lo:[0,1] neg_hi:[0,1]
	v_exp_f16_sdwa v98, v94 dst_sel:WORD_0 dst_unused:UNUSED_PAD src0_sel:WORD_0
	v_exp_f16_sdwa v99, v95 dst_sel:WORD_0 dst_unused:UNUSED_PAD src0_sel:WORD_0
	v_exp_f16_sdwa v100, v96 dst_sel:WORD_0 dst_unused:UNUSED_PAD src0_sel:WORD_0
	v_exp_f16_sdwa v101, v97 dst_sel:WORD_0 dst_unused:UNUSED_PAD src0_sel:WORD_0
	v_exp_f16_sdwa v98, v94 dst_sel:WORD_1 dst_unused:UNUSED_PRESERVE src0_sel:WORD_1
	v_exp_f16_sdwa v99, v95 dst_sel:WORD_1 dst_unused:UNUSED_PRESERVE src0_sel:WORD_1
	v_exp_f16_sdwa v100, v96 dst_sel:WORD_1 dst_unused:UNUSED_PRESERVE src0_sel:WORD_1
	v_exp_f16_sdwa v101, v97 dst_sel:WORD_1 dst_unused:UNUSED_PRESERVE src0_sel:WORD_1
	v_exp_f16_sdwa v94, v82 dst_sel:WORD_0 dst_unused:UNUSED_PAD src0_sel:WORD_0
	v_exp_f16_sdwa v95, v83 dst_sel:WORD_0 dst_unused:UNUSED_PAD src0_sel:WORD_0
	v_exp_f16_sdwa v96, v84 dst_sel:WORD_0 dst_unused:UNUSED_PAD src0_sel:WORD_0
	v_exp_f16_sdwa v97, v85 dst_sel:WORD_0 dst_unused:UNUSED_PAD src0_sel:WORD_0
	v_exp_f16_sdwa v94, v82 dst_sel:WORD_1 dst_unused:UNUSED_PRESERVE src0_sel:WORD_1
	v_exp_f16_sdwa v95, v83 dst_sel:WORD_1 dst_unused:UNUSED_PRESERVE src0_sel:WORD_1
	v_exp_f16_sdwa v96, v84 dst_sel:WORD_1 dst_unused:UNUSED_PRESERVE src0_sel:WORD_1
	v_exp_f16_sdwa v97, v85 dst_sel:WORD_1 dst_unused:UNUSED_PRESERVE src0_sel:WORD_1
	v_pk_add_f16 v82, v106, v162 neg_lo:[0,1] neg_hi:[0,1]
	v_pk_add_f16 v77, v77, v98
	v_pk_add_f16 v76, v76, v99
	v_pk_add_f16 v75, v75, v100
	v_pk_add_f16 v74, v74, v101
	v_pk_fma_f16 v54, v58, v98, v54
	v_pk_fma_f16 v55, v59, v99, v55
	v_pk_fma_f16 v56, v60, v100, v56
	v_pk_fma_f16 v57, v61, v101, v57
	v_pk_add_f16 v77, v77, v94
	v_pk_add_f16 v74, v74, v97
	v_pk_add_f16 v75, v75, v96
	v_pk_add_f16 v76, v76, v95
	v_pk_fma_f16 v57, v21, v97, v57
	v_pk_fma_f16 v56, v20, v96, v56
	v_pk_fma_f16 v55, v19, v95, v55
	v_pk_fma_f16 v54, v18, v94, v54
	v_pk_add_f16 v83, v107, v163 neg_lo:[0,1] neg_hi:[0,1]
	v_pk_add_f16 v84, v108, v164 neg_lo:[0,1] neg_hi:[0,1]
	v_pk_add_f16 v85, v109, v165 neg_lo:[0,1] neg_hi:[0,1]
	v_exp_f16_sdwa v94, v82 dst_sel:WORD_0 dst_unused:UNUSED_PAD src0_sel:WORD_0
	v_exp_f16_sdwa v95, v83 dst_sel:WORD_0 dst_unused:UNUSED_PAD src0_sel:WORD_0
	v_exp_f16_sdwa v96, v84 dst_sel:WORD_0 dst_unused:UNUSED_PAD src0_sel:WORD_0
	v_exp_f16_sdwa v97, v85 dst_sel:WORD_0 dst_unused:UNUSED_PAD src0_sel:WORD_0
	v_exp_f16_sdwa v94, v82 dst_sel:WORD_1 dst_unused:UNUSED_PRESERVE src0_sel:WORD_1
	v_exp_f16_sdwa v95, v83 dst_sel:WORD_1 dst_unused:UNUSED_PRESERVE src0_sel:WORD_1
	v_exp_f16_sdwa v96, v84 dst_sel:WORD_1 dst_unused:UNUSED_PRESERVE src0_sel:WORD_1
	v_exp_f16_sdwa v97, v85 dst_sel:WORD_1 dst_unused:UNUSED_PRESERVE src0_sel:WORD_1
	v_pk_add_f16 v82, v122, v162 neg_lo:[0,1] neg_hi:[0,1]
	v_pk_add_f16 v77, v77, v94
	v_pk_add_f16 v76, v76, v95
	v_pk_add_f16 v75, v75, v96
	v_pk_add_f16 v74, v74, v97
	v_pk_fma_f16 v54, v22, v94, v54
	v_pk_fma_f16 v55, v23, v95, v55
	v_pk_fma_f16 v56, v24, v96, v56
	v_pk_fma_f16 v57, v25, v97, v57
	v_pk_add_f16 v83, v123, v163 neg_lo:[0,1] neg_hi:[0,1]
	v_pk_add_f16 v84, v124, v164 neg_lo:[0,1] neg_hi:[0,1]
	v_pk_add_f16 v85, v125, v165 neg_lo:[0,1] neg_hi:[0,1]
	v_exp_f16_sdwa v94, v82 dst_sel:WORD_0 dst_unused:UNUSED_PAD src0_sel:WORD_0
	v_exp_f16_sdwa v95, v83 dst_sel:WORD_0 dst_unused:UNUSED_PAD src0_sel:WORD_0
	v_exp_f16_sdwa v96, v84 dst_sel:WORD_0 dst_unused:UNUSED_PAD src0_sel:WORD_0
	v_exp_f16_sdwa v97, v85 dst_sel:WORD_0 dst_unused:UNUSED_PAD src0_sel:WORD_0
	v_exp_f16_sdwa v94, v82 dst_sel:WORD_1 dst_unused:UNUSED_PRESERVE src0_sel:WORD_1
	v_exp_f16_sdwa v95, v83 dst_sel:WORD_1 dst_unused:UNUSED_PRESERVE src0_sel:WORD_1
	v_exp_f16_sdwa v96, v84 dst_sel:WORD_1 dst_unused:UNUSED_PRESERVE src0_sel:WORD_1
	v_exp_f16_sdwa v97, v85 dst_sel:WORD_1 dst_unused:UNUSED_PRESERVE src0_sel:WORD_1
	v_pk_add_f16 v77, v77, v94
	v_pk_add_f16 v76, v76, v95
	v_rcp_f16_e32 v82, v77
	v_rcp_f16_sdwa v77, v77 dst_sel:DWORD dst_unused:UNUSED_PAD src0_sel:WORD_1
	v_pk_add_f16 v75, v75, v96
	v_rcp_f16_e32 v83, v76
	v_rcp_f16_sdwa v76, v76 dst_sel:DWORD dst_unused:UNUSED_PAD src0_sel:WORD_1
	v_pk_add_f16 v74, v74, v97
	v_rcp_f16_e32 v84, v75
	v_rcp_f16_sdwa v75, v75 dst_sel:DWORD dst_unused:UNUSED_PAD src0_sel:WORD_1
	v_rcp_f16_e32 v85, v74
	v_rcp_f16_sdwa v74, v74 dst_sel:DWORD dst_unused:UNUSED_PAD src0_sel:WORD_1
	v_pk_fma_f16 v54, v26, v94, v54
	v_pack_b32_f16 v77, v82, v77
	v_pk_fma_f16 v55, v27, v95, v55
	v_pk_mul_f16 v77, v54, v77
	v_pack_b32_f16 v54, v83, v76
	v_pk_fma_f16 v56, v28, v96, v56
	v_pk_mul_f16 v76, v55, v54
	v_pack_b32_f16 v54, v84, v75
	v_pk_fma_f16 v57, v29, v97, v57
	v_pk_mul_f16 v75, v56, v54
	v_pack_b32_f16 v54, v85, v74
	v_pk_mul_f16 v74, v57, v54
	s_waitcnt vmcnt(6)
	v_pk_mul_f16 v57, v204, v161 op_sel_hi:[0,1]
	v_pk_mul_f16 v85, v202, v161 op_sel_hi:[0,1]
	v_pk_mul_f16 v97, v203, v161 op_sel_hi:[0,1]
	v_pk_mul_f16 v54, v204, v158 op_sel_hi:[0,1]
	v_pk_mul_f16 v55, v204, v159 op_sel_hi:[0,1]
	v_pk_mul_f16 v56, v204, v160 op_sel_hi:[0,1]
	v_pk_mul_f16 v82, v202, v158 op_sel_hi:[0,1]
	v_pk_mul_f16 v83, v202, v159 op_sel_hi:[0,1]
	v_pk_mul_f16 v84, v202, v160 op_sel_hi:[0,1]
	v_pk_mul_f16 v94, v203, v158 op_sel_hi:[0,1]
	v_pk_mul_f16 v95, v203, v159 op_sel_hi:[0,1]
	v_pk_mul_f16 v96, v203, v160 op_sel_hi:[0,1]
	v_pk_fma_f16 v65, v65, v161, v57
	v_pk_fma_f16 v81, v81, v161, v85
	v_pk_fma_f16 v98, v105, v161, v97
	v_pk_fma_f16 v64, v64, v160, v56
	v_pk_maximum3_f16 v125, v65, v81, v98
	v_pk_fma_f16 v63, v63, v159, v55
	v_pk_fma_f16 v62, v62, v158, v54
	v_pk_fma_f16 v80, v80, v160, v84
	v_pk_fma_f16 v79, v79, v159, v83
	v_pk_fma_f16 v78, v78, v158, v82
	v_pk_fma_f16 v99, v104, v160, v96
	v_pk_fma_f16 v100, v103, v159, v95
	v_pk_fma_f16 v101, v102, v158, v94
	v_pk_fma_f16 v102, v37, v161, v57
	v_pk_fma_f16 v106, v49, v161, v85
	v_pk_fma_f16 v118, v69, v161, v97
	v_pk_fma_f16 v57, v89, v161, v57
	v_pk_fma_f16 v85, v117, v161, v85
	v_pk_fma_f16 v97, v133, v161, v97
	v_pk_maximum3_f16 v122, v62, v78, v101
	v_pk_maximum3_f16 v123, v63, v79, v100
	v_pk_maximum3_f16 v124, v64, v80, v99
	v_pk_maximum3_f16 v129, v102, v106, v118
	v_pk_fma_f16 v103, v36, v160, v56
	v_pk_maximum3_f16 v137, v57, v85, v97
	v_pk_fma_f16 v104, v35, v159, v55
	v_pk_maximum3_f16 v125, v125, v129, v137
	v_pk_fma_f16 v105, v34, v158, v54
	v_pk_fma_f16 v107, v48, v160, v84
	v_pk_fma_f16 v108, v47, v159, v83
	v_pk_fma_f16 v109, v46, v158, v82
	v_pk_fma_f16 v119, v68, v160, v96
	v_pk_fma_f16 v120, v67, v159, v95
	v_pk_fma_f16 v121, v66, v158, v94
	v_pk_fma_f16 v56, v88, v160, v56
	v_pk_fma_f16 v55, v87, v159, v55
	v_pk_fma_f16 v54, v86, v158, v54
	v_pk_fma_f16 v84, v116, v160, v84
	v_pk_fma_f16 v83, v115, v159, v83
	v_pk_fma_f16 v82, v114, v158, v82
	v_pk_fma_f16 v96, v132, v160, v96
	v_pk_fma_f16 v95, v131, v159, v95
	v_pk_fma_f16 v94, v130, v158, v94
	v_pk_maximum3_f16 v126, v105, v109, v121
	v_pk_maximum3_f16 v127, v104, v108, v120
	v_pk_maximum3_f16 v128, v103, v107, v119
	v_pk_maximum3_f16 v135, v55, v83, v95
	v_pk_maximum3_f16 v136, v56, v84, v96
	v_pk_maximum3_f16 v134, v54, v82, v94
	v_pk_maximum3_f16 v122, v122, v126, v134
	v_pk_maximum3_f16 v123, v123, v127, v135
	v_pk_maximum3_f16 v124, v124, v128, v136
	v_pk_add_f16 v65, v65, v125 neg_lo:[0,1] neg_hi:[0,1]
	v_pk_add_f16 v62, v62, v122 neg_lo:[0,1] neg_hi:[0,1]
	v_pk_add_f16 v63, v63, v123 neg_lo:[0,1] neg_hi:[0,1]
	v_pk_add_f16 v64, v64, v124 neg_lo:[0,1] neg_hi:[0,1]
	v_pk_add_f16 v78, v78, v122 neg_lo:[0,1] neg_hi:[0,1]
	v_exp_f16_sdwa v126, v62 dst_sel:WORD_0 dst_unused:UNUSED_PAD src0_sel:WORD_0
	v_exp_f16_sdwa v127, v63 dst_sel:WORD_0 dst_unused:UNUSED_PAD src0_sel:WORD_0
	v_exp_f16_sdwa v128, v64 dst_sel:WORD_0 dst_unused:UNUSED_PAD src0_sel:WORD_0
	v_exp_f16_sdwa v129, v65 dst_sel:WORD_0 dst_unused:UNUSED_PAD src0_sel:WORD_0
	v_exp_f16_sdwa v126, v62 dst_sel:WORD_1 dst_unused:UNUSED_PRESERVE src0_sel:WORD_1
	v_exp_f16_sdwa v127, v63 dst_sel:WORD_1 dst_unused:UNUSED_PRESERVE src0_sel:WORD_1
	v_exp_f16_sdwa v128, v64 dst_sel:WORD_1 dst_unused:UNUSED_PRESERVE src0_sel:WORD_1
	v_exp_f16_sdwa v129, v65 dst_sel:WORD_1 dst_unused:UNUSED_PRESERVE src0_sel:WORD_1
	v_pk_add_f16 v79, v79, v123 neg_lo:[0,1] neg_hi:[0,1]
	v_pk_add_f16 v65, v126, 0
	v_pk_fma_f16 v33, v33, v129, 0
	v_pk_add_f16 v62, v129, 0
	v_pk_add_f16 v63, v128, 0
	v_pk_add_f16 v64, v127, 0
	v_pk_fma_f16 v32, v32, v128, 0
	v_pk_fma_f16 v31, v31, v127, 0
	v_pk_fma_f16 v30, v30, v126, 0
	v_pk_add_f16 v80, v80, v124 neg_lo:[0,1] neg_hi:[0,1]
	v_pk_add_f16 v81, v81, v125 neg_lo:[0,1] neg_hi:[0,1]
	v_pk_add_f16 v54, v54, v122 neg_lo:[0,1] neg_hi:[0,1]
	v_exp_f16_sdwa v126, v78 dst_sel:WORD_0 dst_unused:UNUSED_PAD src0_sel:WORD_0
	v_exp_f16_sdwa v127, v79 dst_sel:WORD_0 dst_unused:UNUSED_PAD src0_sel:WORD_0
	v_exp_f16_sdwa v128, v80 dst_sel:WORD_0 dst_unused:UNUSED_PAD src0_sel:WORD_0
	v_exp_f16_sdwa v129, v81 dst_sel:WORD_0 dst_unused:UNUSED_PAD src0_sel:WORD_0
	v_exp_f16_sdwa v126, v78 dst_sel:WORD_1 dst_unused:UNUSED_PRESERVE src0_sel:WORD_1
	v_exp_f16_sdwa v127, v79 dst_sel:WORD_1 dst_unused:UNUSED_PRESERVE src0_sel:WORD_1
	v_exp_f16_sdwa v128, v80 dst_sel:WORD_1 dst_unused:UNUSED_PRESERVE src0_sel:WORD_1
	v_exp_f16_sdwa v129, v81 dst_sel:WORD_1 dst_unused:UNUSED_PRESERVE src0_sel:WORD_1
	v_pk_add_f16 v55, v55, v123 neg_lo:[0,1] neg_hi:[0,1]
	v_pk_add_f16 v65, v65, v126
	v_pk_fma_f16 v33, v45, v129, v33
	v_pk_add_f16 v45, v98, v125 neg_lo:[0,1] neg_hi:[0,1]
	v_pk_add_f16 v64, v64, v127
	v_pk_add_f16 v63, v63, v128
	v_pk_add_f16 v62, v62, v129
	v_pk_fma_f16 v30, v42, v126, v30
	v_pk_fma_f16 v31, v43, v127, v31
	v_pk_fma_f16 v32, v44, v128, v32
	v_pk_add_f16 v42, v101, v122 neg_lo:[0,1] neg_hi:[0,1]
	v_pk_add_f16 v43, v100, v123 neg_lo:[0,1] neg_hi:[0,1]
	v_pk_add_f16 v44, v99, v124 neg_lo:[0,1] neg_hi:[0,1]
	v_pk_add_f16 v56, v56, v124 neg_lo:[0,1] neg_hi:[0,1]
	v_exp_f16_sdwa v78, v42 dst_sel:WORD_0 dst_unused:UNUSED_PAD src0_sel:WORD_0
	v_exp_f16_sdwa v79, v43 dst_sel:WORD_0 dst_unused:UNUSED_PAD src0_sel:WORD_0
	v_exp_f16_sdwa v80, v44 dst_sel:WORD_0 dst_unused:UNUSED_PAD src0_sel:WORD_0
	v_exp_f16_sdwa v81, v45 dst_sel:WORD_0 dst_unused:UNUSED_PAD src0_sel:WORD_0
	v_exp_f16_sdwa v78, v42 dst_sel:WORD_1 dst_unused:UNUSED_PRESERVE src0_sel:WORD_1
	v_exp_f16_sdwa v79, v43 dst_sel:WORD_1 dst_unused:UNUSED_PRESERVE src0_sel:WORD_1
	v_exp_f16_sdwa v80, v44 dst_sel:WORD_1 dst_unused:UNUSED_PRESERVE src0_sel:WORD_1
	v_exp_f16_sdwa v81, v45 dst_sel:WORD_1 dst_unused:UNUSED_PRESERVE src0_sel:WORD_1
	v_pk_add_f16 v57, v57, v125 neg_lo:[0,1] neg_hi:[0,1]
	v_pk_add_f16 v45, v65, v78
	v_pk_add_f16 v42, v62, v81
	v_pk_add_f16 v43, v63, v80
	v_pk_add_f16 v44, v64, v79
	v_pk_fma_f16 v33, v61, v81, v33
	v_pk_fma_f16 v32, v60, v80, v32
	v_pk_fma_f16 v31, v59, v79, v31
	v_pk_fma_f16 v30, v58, v78, v30
	v_pk_add_f16 v58, v105, v122 neg_lo:[0,1] neg_hi:[0,1]
	v_pk_add_f16 v59, v104, v123 neg_lo:[0,1] neg_hi:[0,1]
	v_pk_add_f16 v60, v103, v124 neg_lo:[0,1] neg_hi:[0,1]
	v_pk_add_f16 v61, v102, v125 neg_lo:[0,1] neg_hi:[0,1]
	v_exp_f16_sdwa v62, v58 dst_sel:WORD_0 dst_unused:UNUSED_PAD src0_sel:WORD_0
	v_exp_f16_sdwa v63, v59 dst_sel:WORD_0 dst_unused:UNUSED_PAD src0_sel:WORD_0
	v_exp_f16_sdwa v64, v60 dst_sel:WORD_0 dst_unused:UNUSED_PAD src0_sel:WORD_0
	v_exp_f16_sdwa v65, v61 dst_sel:WORD_0 dst_unused:UNUSED_PAD src0_sel:WORD_0
	v_exp_f16_sdwa v62, v58 dst_sel:WORD_1 dst_unused:UNUSED_PRESERVE src0_sel:WORD_1
	v_exp_f16_sdwa v63, v59 dst_sel:WORD_1 dst_unused:UNUSED_PRESERVE src0_sel:WORD_1
	v_exp_f16_sdwa v64, v60 dst_sel:WORD_1 dst_unused:UNUSED_PRESERVE src0_sel:WORD_1
	v_exp_f16_sdwa v65, v61 dst_sel:WORD_1 dst_unused:UNUSED_PRESERVE src0_sel:WORD_1
	v_pk_add_f16 v58, v109, v122 neg_lo:[0,1] neg_hi:[0,1]
	v_pk_add_f16 v45, v45, v62
	v_pk_add_f16 v44, v44, v63
	v_pk_add_f16 v43, v43, v64
	v_pk_add_f16 v42, v42, v65
	v_pk_fma_f16 v30, v18, v62, v30
	v_pk_fma_f16 v31, v19, v63, v31
	v_pk_fma_f16 v32, v20, v64, v32
	v_pk_fma_f16 v33, v21, v65, v33
	v_pk_add_f16 v59, v108, v123 neg_lo:[0,1] neg_hi:[0,1]
	v_pk_add_f16 v60, v107, v124 neg_lo:[0,1] neg_hi:[0,1]
	v_pk_add_f16 v61, v106, v125 neg_lo:[0,1] neg_hi:[0,1]
	v_exp_f16_sdwa v62, v58 dst_sel:WORD_0 dst_unused:UNUSED_PAD src0_sel:WORD_0
	v_exp_f16_sdwa v63, v59 dst_sel:WORD_0 dst_unused:UNUSED_PAD src0_sel:WORD_0
	v_exp_f16_sdwa v64, v60 dst_sel:WORD_0 dst_unused:UNUSED_PAD src0_sel:WORD_0
	v_exp_f16_sdwa v65, v61 dst_sel:WORD_0 dst_unused:UNUSED_PAD src0_sel:WORD_0
	v_exp_f16_sdwa v62, v58 dst_sel:WORD_1 dst_unused:UNUSED_PRESERVE src0_sel:WORD_1
	v_exp_f16_sdwa v63, v59 dst_sel:WORD_1 dst_unused:UNUSED_PRESERVE src0_sel:WORD_1
	v_exp_f16_sdwa v64, v60 dst_sel:WORD_1 dst_unused:UNUSED_PRESERVE src0_sel:WORD_1
	v_exp_f16_sdwa v65, v61 dst_sel:WORD_1 dst_unused:UNUSED_PRESERVE src0_sel:WORD_1
	v_pk_add_f16 v58, v121, v122 neg_lo:[0,1] neg_hi:[0,1]
	v_pk_add_f16 v45, v45, v62
	v_pk_add_f16 v42, v42, v65
	v_pk_add_f16 v43, v43, v64
	v_pk_add_f16 v44, v44, v63
	v_pk_fma_f16 v33, v25, v65, v33
	v_pk_fma_f16 v32, v24, v64, v32
	v_pk_fma_f16 v31, v23, v63, v31
	v_pk_fma_f16 v30, v22, v62, v30
	v_pk_add_f16 v59, v120, v123 neg_lo:[0,1] neg_hi:[0,1]
	v_pk_add_f16 v60, v119, v124 neg_lo:[0,1] neg_hi:[0,1]
	v_pk_add_f16 v61, v118, v125 neg_lo:[0,1] neg_hi:[0,1]
	v_exp_f16_sdwa v62, v58 dst_sel:WORD_0 dst_unused:UNUSED_PAD src0_sel:WORD_0
	v_exp_f16_sdwa v63, v59 dst_sel:WORD_0 dst_unused:UNUSED_PAD src0_sel:WORD_0
	v_exp_f16_sdwa v64, v60 dst_sel:WORD_0 dst_unused:UNUSED_PAD src0_sel:WORD_0
	v_exp_f16_sdwa v65, v61 dst_sel:WORD_0 dst_unused:UNUSED_PAD src0_sel:WORD_0
	v_exp_f16_sdwa v62, v58 dst_sel:WORD_1 dst_unused:UNUSED_PRESERVE src0_sel:WORD_1
	v_exp_f16_sdwa v63, v59 dst_sel:WORD_1 dst_unused:UNUSED_PRESERVE src0_sel:WORD_1
	v_exp_f16_sdwa v64, v60 dst_sel:WORD_1 dst_unused:UNUSED_PRESERVE src0_sel:WORD_1
	v_exp_f16_sdwa v65, v61 dst_sel:WORD_1 dst_unused:UNUSED_PRESERVE src0_sel:WORD_1
	v_exp_f16_sdwa v58, v54 dst_sel:WORD_0 dst_unused:UNUSED_PAD src0_sel:WORD_0
	v_exp_f16_sdwa v59, v55 dst_sel:WORD_0 dst_unused:UNUSED_PAD src0_sel:WORD_0
	v_exp_f16_sdwa v60, v56 dst_sel:WORD_0 dst_unused:UNUSED_PAD src0_sel:WORD_0
	v_exp_f16_sdwa v61, v57 dst_sel:WORD_0 dst_unused:UNUSED_PAD src0_sel:WORD_0
	v_exp_f16_sdwa v58, v54 dst_sel:WORD_1 dst_unused:UNUSED_PRESERVE src0_sel:WORD_1
	v_exp_f16_sdwa v59, v55 dst_sel:WORD_1 dst_unused:UNUSED_PRESERVE src0_sel:WORD_1
	v_exp_f16_sdwa v60, v56 dst_sel:WORD_1 dst_unused:UNUSED_PRESERVE src0_sel:WORD_1
	v_exp_f16_sdwa v61, v57 dst_sel:WORD_1 dst_unused:UNUSED_PRESERVE src0_sel:WORD_1
	v_pk_add_f16 v54, v82, v122 neg_lo:[0,1] neg_hi:[0,1]
	v_pk_add_f16 v45, v45, v62
	v_pk_add_f16 v44, v44, v63
	v_pk_add_f16 v43, v43, v64
	v_pk_add_f16 v42, v42, v65
	v_pk_fma_f16 v30, v26, v62, v30
	v_pk_fma_f16 v31, v27, v63, v31
	v_pk_fma_f16 v32, v28, v64, v32
	v_pk_fma_f16 v33, v29, v65, v33
	v_pk_add_f16 v45, v45, v58
	v_pk_add_f16 v42, v42, v61
	v_pk_add_f16 v43, v43, v60
	v_pk_add_f16 v44, v44, v59
	v_pk_fma_f16 v33, v41, v61, v33
	v_pk_fma_f16 v32, v40, v60, v32
	v_pk_fma_f16 v31, v39, v59, v31
	v_pk_fma_f16 v30, v38, v58, v30
	v_pk_add_f16 v55, v83, v123 neg_lo:[0,1] neg_hi:[0,1]
	v_pk_add_f16 v56, v84, v124 neg_lo:[0,1] neg_hi:[0,1]
	v_pk_add_f16 v57, v85, v125 neg_lo:[0,1] neg_hi:[0,1]
	v_exp_f16_sdwa v58, v54 dst_sel:WORD_0 dst_unused:UNUSED_PAD src0_sel:WORD_0
	v_exp_f16_sdwa v59, v55 dst_sel:WORD_0 dst_unused:UNUSED_PAD src0_sel:WORD_0
	v_exp_f16_sdwa v60, v56 dst_sel:WORD_0 dst_unused:UNUSED_PAD src0_sel:WORD_0
	v_exp_f16_sdwa v61, v57 dst_sel:WORD_0 dst_unused:UNUSED_PAD src0_sel:WORD_0
	v_exp_f16_sdwa v58, v54 dst_sel:WORD_1 dst_unused:UNUSED_PRESERVE src0_sel:WORD_1
	v_exp_f16_sdwa v59, v55 dst_sel:WORD_1 dst_unused:UNUSED_PRESERVE src0_sel:WORD_1
	v_exp_f16_sdwa v60, v56 dst_sel:WORD_1 dst_unused:UNUSED_PRESERVE src0_sel:WORD_1
	v_exp_f16_sdwa v61, v57 dst_sel:WORD_1 dst_unused:UNUSED_PRESERVE src0_sel:WORD_1
	v_pk_add_f16 v54, v94, v122 neg_lo:[0,1] neg_hi:[0,1]
	v_pk_add_f16 v45, v45, v58
	v_pk_add_f16 v44, v44, v59
	v_pk_add_f16 v43, v43, v60
	v_pk_add_f16 v42, v42, v61
	v_pk_fma_f16 v30, v50, v58, v30
	v_pk_fma_f16 v31, v51, v59, v31
	v_pk_fma_f16 v32, v52, v60, v32
	v_pk_fma_f16 v33, v53, v61, v33
	v_pk_add_f16 v55, v95, v123 neg_lo:[0,1] neg_hi:[0,1]
	v_pk_add_f16 v56, v96, v124 neg_lo:[0,1] neg_hi:[0,1]
	v_pk_add_f16 v57, v97, v125 neg_lo:[0,1] neg_hi:[0,1]
	v_exp_f16_sdwa v58, v54 dst_sel:WORD_0 dst_unused:UNUSED_PAD src0_sel:WORD_0
	v_exp_f16_sdwa v59, v55 dst_sel:WORD_0 dst_unused:UNUSED_PAD src0_sel:WORD_0
	v_exp_f16_sdwa v60, v56 dst_sel:WORD_0 dst_unused:UNUSED_PAD src0_sel:WORD_0
	v_exp_f16_sdwa v61, v57 dst_sel:WORD_0 dst_unused:UNUSED_PAD src0_sel:WORD_0
	v_exp_f16_sdwa v58, v54 dst_sel:WORD_1 dst_unused:UNUSED_PRESERVE src0_sel:WORD_1
	v_exp_f16_sdwa v59, v55 dst_sel:WORD_1 dst_unused:UNUSED_PRESERVE src0_sel:WORD_1
	v_exp_f16_sdwa v60, v56 dst_sel:WORD_1 dst_unused:UNUSED_PRESERVE src0_sel:WORD_1
	v_exp_f16_sdwa v61, v57 dst_sel:WORD_1 dst_unused:UNUSED_PRESERVE src0_sel:WORD_1
	v_pk_add_f16 v45, v45, v58
	v_pk_add_f16 v44, v44, v59
	v_rcp_f16_e32 v54, v45
	v_rcp_f16_sdwa v45, v45 dst_sel:DWORD dst_unused:UNUSED_PAD src0_sel:WORD_1
	v_pk_add_f16 v43, v43, v60
	v_rcp_f16_e32 v55, v44
	v_rcp_f16_sdwa v44, v44 dst_sel:DWORD dst_unused:UNUSED_PAD src0_sel:WORD_1
	v_pk_add_f16 v42, v42, v61
	v_pk_fma_f16 v30, v70, v58, v30
	v_rcp_f16_e32 v58, v43
	v_rcp_f16_sdwa v43, v43 dst_sel:DWORD dst_unused:UNUSED_PAD src0_sel:WORD_1
	v_pk_fma_f16 v31, v71, v59, v31
	v_rcp_f16_e32 v59, v42
	v_rcp_f16_sdwa v42, v42 dst_sel:DWORD dst_unused:UNUSED_PAD src0_sel:WORD_1
	v_pack_b32_f16 v45, v54, v45
	v_pk_mul_f16 v57, v30, v45
	v_pack_b32_f16 v30, v55, v44
	v_pk_fma_f16 v32, v72, v60, v32
	v_pk_mul_f16 v56, v31, v30
	v_pack_b32_f16 v30, v58, v43
	v_pk_fma_f16 v33, v73, v61, v33
	v_pk_mul_f16 v55, v32, v30
	v_pack_b32_f16 v30, v59, v42
	v_pk_mul_f16 v54, v33, v30
	s_waitcnt vmcnt(0)
	v_pk_mul_f16 v30, v204, v154 op_sel_hi:[0,1]
	v_pk_mul_f16 v31, v204, v155 op_sel_hi:[0,1]
	v_pk_mul_f16 v32, v204, v156 op_sel_hi:[0,1]
	v_pk_mul_f16 v33, v204, v157 op_sel_hi:[0,1]
	v_pk_mul_f16 v42, v202, v154 op_sel_hi:[0,1]
	v_pk_mul_f16 v43, v202, v155 op_sel_hi:[0,1]
	v_pk_mul_f16 v44, v202, v156 op_sel_hi:[0,1]
	v_pk_mul_f16 v45, v202, v157 op_sel_hi:[0,1]
	v_pk_mul_f16 v58, v203, v154 op_sel_hi:[0,1]
	v_pk_mul_f16 v59, v203, v155 op_sel_hi:[0,1]
	v_pk_mul_f16 v60, v203, v156 op_sel_hi:[0,1]
	v_pk_mul_f16 v61, v203, v157 op_sel_hi:[0,1]
	v_pk_fma_f16 v37, v37, v157, v33
	v_pk_fma_f16 v36, v36, v156, v32
	v_pk_fma_f16 v35, v35, v155, v31
	v_pk_fma_f16 v34, v34, v154, v30
	v_pk_fma_f16 v49, v49, v157, v45
	v_pk_fma_f16 v48, v48, v156, v44
	v_pk_fma_f16 v47, v47, v155, v43
	v_pk_fma_f16 v46, v46, v154, v42
	v_pk_fma_f16 v62, v69, v157, v61
	v_pk_fma_f16 v63, v68, v156, v60
	v_pk_fma_f16 v64, v67, v155, v59
	v_pk_fma_f16 v65, v66, v154, v58
	v_pk_fma_f16 v66, v89, v157, v33
	v_pk_fma_f16 v67, v88, v156, v32
	v_pk_fma_f16 v68, v87, v155, v31
	v_pk_fma_f16 v69, v86, v154, v30
	v_pk_fma_f16 v78, v117, v157, v45
	v_pk_fma_f16 v79, v116, v156, v44
	v_pk_fma_f16 v80, v115, v155, v43
	v_pk_fma_f16 v81, v114, v154, v42
	v_pk_fma_f16 v82, v133, v157, v61
	v_pk_fma_f16 v83, v132, v156, v60
	v_pk_fma_f16 v84, v131, v155, v59
	v_pk_fma_f16 v85, v130, v154, v58
	v_pk_fma_f16 v61, v17, v157, v61
	v_pk_fma_f16 v60, v16, v156, v60
	v_pk_fma_f16 v59, v15, v155, v59
	v_pk_fma_f16 v58, v14, v154, v58
	v_pk_maximum3_f16 v14, v34, v46, v65
	v_pk_maximum3_f16 v15, v35, v47, v64
	v_pk_maximum3_f16 v16, v36, v48, v63
	v_pk_maximum3_f16 v17, v37, v49, v62
	v_pk_maximum3_f16 v86, v69, v81, v85
	v_pk_maximum3_f16 v87, v68, v80, v84
	v_pk_maximum3_f16 v88, v67, v79, v83
	v_pk_maximum3_f16 v89, v66, v78, v82
	v_pk_fma_f16 v33, v145, v157, v33
	v_pk_fma_f16 v32, v144, v156, v32
	v_pk_fma_f16 v31, v143, v155, v31
	v_pk_fma_f16 v30, v142, v154, v30
	v_pk_fma_f16 v45, v153, v157, v45
	v_pk_fma_f16 v44, v152, v156, v44
	v_pk_fma_f16 v43, v151, v155, v43
	v_pk_fma_f16 v42, v150, v154, v42
	v_pk_maximum3_f16 v95, v31, v43, v59
	v_pk_maximum3_f16 v96, v32, v44, v60
	v_pk_maximum3_f16 v97, v33, v45, v61
	v_pk_maximum3_f16 v94, v30, v42, v58
	v_pk_maximum3_f16 v15, v15, v87, v95
	v_pk_maximum3_f16 v16, v16, v88, v96
	v_pk_maximum3_f16 v17, v17, v89, v97
	v_pk_maximum3_f16 v14, v14, v86, v94
	v_xor_b32_e32 v86, 0x80008000, v17
	v_xor_b32_e32 v87, 0x80008000, v16
	v_xor_b32_e32 v88, 0x80008000, v15
	v_xor_b32_e32 v89, 0x80008000, v14
	v_pk_add_f16 v14, v34, v89
	v_pk_add_f16 v15, v35, v88
	v_pk_add_f16 v16, v36, v87
	v_pk_add_f16 v17, v37, v86
	v_exp_f16_sdwa v34, v14 dst_sel:WORD_0 dst_unused:UNUSED_PAD src0_sel:WORD_0
	v_exp_f16_sdwa v35, v15 dst_sel:WORD_0 dst_unused:UNUSED_PAD src0_sel:WORD_0
	v_exp_f16_sdwa v36, v16 dst_sel:WORD_0 dst_unused:UNUSED_PAD src0_sel:WORD_0
	v_exp_f16_sdwa v37, v17 dst_sel:WORD_0 dst_unused:UNUSED_PAD src0_sel:WORD_0
	v_exp_f16_sdwa v34, v14 dst_sel:WORD_1 dst_unused:UNUSED_PRESERVE src0_sel:WORD_1
	v_exp_f16_sdwa v35, v15 dst_sel:WORD_1 dst_unused:UNUSED_PRESERVE src0_sel:WORD_1
	v_exp_f16_sdwa v36, v16 dst_sel:WORD_1 dst_unused:UNUSED_PRESERVE src0_sel:WORD_1
	v_exp_f16_sdwa v37, v17 dst_sel:WORD_1 dst_unused:UNUSED_PRESERVE src0_sel:WORD_1
	v_pk_add_f16 v14, v34, 0
	v_pk_add_f16 v15, v35, 0
	v_pk_add_f16 v16, v36, 0
	v_pk_add_f16 v17, v37, 0
	v_pk_fma_f16 v18, v18, v34, 0
	v_pk_fma_f16 v19, v19, v35, 0
	v_pk_fma_f16 v20, v20, v36, 0
	v_pk_fma_f16 v21, v21, v37, 0
	v_pk_add_f16 v34, v46, v89
	v_pk_add_f16 v35, v47, v88
	v_pk_add_f16 v36, v48, v87
	v_pk_add_f16 v37, v49, v86
	v_exp_f16_sdwa v46, v34 dst_sel:WORD_0 dst_unused:UNUSED_PAD src0_sel:WORD_0
	v_exp_f16_sdwa v47, v35 dst_sel:WORD_0 dst_unused:UNUSED_PAD src0_sel:WORD_0
	v_exp_f16_sdwa v48, v36 dst_sel:WORD_0 dst_unused:UNUSED_PAD src0_sel:WORD_0
	v_exp_f16_sdwa v49, v37 dst_sel:WORD_0 dst_unused:UNUSED_PAD src0_sel:WORD_0
	v_exp_f16_sdwa v46, v34 dst_sel:WORD_1 dst_unused:UNUSED_PRESERVE src0_sel:WORD_1
	v_exp_f16_sdwa v47, v35 dst_sel:WORD_1 dst_unused:UNUSED_PRESERVE src0_sel:WORD_1
	v_exp_f16_sdwa v48, v36 dst_sel:WORD_1 dst_unused:UNUSED_PRESERVE src0_sel:WORD_1
	v_exp_f16_sdwa v49, v37 dst_sel:WORD_1 dst_unused:UNUSED_PRESERVE src0_sel:WORD_1
	s_nop 0
	v_pk_add_f16 v17, v17, v49
	v_pk_add_f16 v16, v16, v48
	v_pk_add_f16 v15, v15, v47
	v_pk_add_f16 v14, v14, v46
	v_pk_fma_f16 v21, v25, v49, v21
	v_pk_fma_f16 v20, v24, v48, v20
	v_pk_fma_f16 v19, v23, v47, v19
	v_pk_fma_f16 v18, v22, v46, v18
	v_pk_add_f16 v22, v65, v89
	v_pk_add_f16 v23, v64, v88
	v_pk_add_f16 v24, v63, v87
	v_pk_add_f16 v25, v62, v86
	v_exp_f16_sdwa v34, v22 dst_sel:WORD_0 dst_unused:UNUSED_PAD src0_sel:WORD_0
	v_exp_f16_sdwa v35, v23 dst_sel:WORD_0 dst_unused:UNUSED_PAD src0_sel:WORD_0
	v_exp_f16_sdwa v36, v24 dst_sel:WORD_0 dst_unused:UNUSED_PAD src0_sel:WORD_0
	v_exp_f16_sdwa v37, v25 dst_sel:WORD_0 dst_unused:UNUSED_PAD src0_sel:WORD_0
	v_exp_f16_sdwa v34, v22 dst_sel:WORD_1 dst_unused:UNUSED_PRESERVE src0_sel:WORD_1
	v_exp_f16_sdwa v35, v23 dst_sel:WORD_1 dst_unused:UNUSED_PRESERVE src0_sel:WORD_1
	v_exp_f16_sdwa v36, v24 dst_sel:WORD_1 dst_unused:UNUSED_PRESERVE src0_sel:WORD_1
	v_exp_f16_sdwa v37, v25 dst_sel:WORD_1 dst_unused:UNUSED_PRESERVE src0_sel:WORD_1
	v_pk_add_f16 v22, v69, v89
	v_pk_add_f16 v14, v14, v34
	v_pk_add_f16 v15, v15, v35
	v_pk_add_f16 v16, v16, v36
	v_pk_add_f16 v17, v17, v37
	v_pk_fma_f16 v18, v26, v34, v18
	v_pk_fma_f16 v19, v27, v35, v19
	v_pk_fma_f16 v20, v28, v36, v20
	v_pk_fma_f16 v21, v29, v37, v21
	v_pk_add_f16 v23, v68, v88
	v_pk_add_f16 v24, v67, v87
	v_pk_add_f16 v25, v66, v86
	v_exp_f16_sdwa v26, v22 dst_sel:WORD_0 dst_unused:UNUSED_PAD src0_sel:WORD_0
	v_exp_f16_sdwa v27, v23 dst_sel:WORD_0 dst_unused:UNUSED_PAD src0_sel:WORD_0
	v_exp_f16_sdwa v28, v24 dst_sel:WORD_0 dst_unused:UNUSED_PAD src0_sel:WORD_0
	v_exp_f16_sdwa v29, v25 dst_sel:WORD_0 dst_unused:UNUSED_PAD src0_sel:WORD_0
	v_exp_f16_sdwa v26, v22 dst_sel:WORD_1 dst_unused:UNUSED_PRESERVE src0_sel:WORD_1
	v_exp_f16_sdwa v27, v23 dst_sel:WORD_1 dst_unused:UNUSED_PRESERVE src0_sel:WORD_1
	v_exp_f16_sdwa v28, v24 dst_sel:WORD_1 dst_unused:UNUSED_PRESERVE src0_sel:WORD_1
	v_exp_f16_sdwa v29, v25 dst_sel:WORD_1 dst_unused:UNUSED_PRESERVE src0_sel:WORD_1
	v_pk_add_f16 v22, v81, v89
	v_pk_add_f16 v17, v17, v29
	v_pk_add_f16 v16, v16, v28
	v_pk_add_f16 v15, v15, v27
	v_pk_add_f16 v14, v14, v26
	v_pk_fma_f16 v21, v41, v29, v21
	v_pk_fma_f16 v20, v40, v28, v20
	v_pk_fma_f16 v19, v39, v27, v19
	v_pk_fma_f16 v18, v38, v26, v18
	v_pk_add_f16 v23, v80, v88
	v_pk_add_f16 v24, v79, v87
	v_pk_add_f16 v25, v78, v86
	v_exp_f16_sdwa v26, v22 dst_sel:WORD_0 dst_unused:UNUSED_PAD src0_sel:WORD_0
	v_exp_f16_sdwa v27, v23 dst_sel:WORD_0 dst_unused:UNUSED_PAD src0_sel:WORD_0
	v_exp_f16_sdwa v28, v24 dst_sel:WORD_0 dst_unused:UNUSED_PAD src0_sel:WORD_0
	v_exp_f16_sdwa v29, v25 dst_sel:WORD_0 dst_unused:UNUSED_PAD src0_sel:WORD_0
	v_exp_f16_sdwa v26, v22 dst_sel:WORD_1 dst_unused:UNUSED_PRESERVE src0_sel:WORD_1
	v_exp_f16_sdwa v27, v23 dst_sel:WORD_1 dst_unused:UNUSED_PRESERVE src0_sel:WORD_1
	v_exp_f16_sdwa v28, v24 dst_sel:WORD_1 dst_unused:UNUSED_PRESERVE src0_sel:WORD_1
	v_exp_f16_sdwa v29, v25 dst_sel:WORD_1 dst_unused:UNUSED_PRESERVE src0_sel:WORD_1
	v_pk_add_f16 v22, v85, v89
	v_pk_add_f16 v14, v14, v26
	v_pk_add_f16 v15, v15, v27
	v_pk_add_f16 v16, v16, v28
	v_pk_add_f16 v17, v17, v29
	v_pk_fma_f16 v18, v50, v26, v18
	v_pk_fma_f16 v19, v51, v27, v19
	v_pk_fma_f16 v20, v52, v28, v20
	v_pk_fma_f16 v21, v53, v29, v21
	v_pk_add_f16 v23, v84, v88
	v_pk_add_f16 v24, v83, v87
	v_pk_add_f16 v25, v82, v86
	v_exp_f16_sdwa v26, v22 dst_sel:WORD_0 dst_unused:UNUSED_PAD src0_sel:WORD_0
	v_exp_f16_sdwa v27, v23 dst_sel:WORD_0 dst_unused:UNUSED_PAD src0_sel:WORD_0
	v_exp_f16_sdwa v28, v24 dst_sel:WORD_0 dst_unused:UNUSED_PAD src0_sel:WORD_0
	v_exp_f16_sdwa v29, v25 dst_sel:WORD_0 dst_unused:UNUSED_PAD src0_sel:WORD_0
	v_exp_f16_sdwa v26, v22 dst_sel:WORD_1 dst_unused:UNUSED_PRESERVE src0_sel:WORD_1
	v_exp_f16_sdwa v27, v23 dst_sel:WORD_1 dst_unused:UNUSED_PRESERVE src0_sel:WORD_1
	v_exp_f16_sdwa v28, v24 dst_sel:WORD_1 dst_unused:UNUSED_PRESERVE src0_sel:WORD_1
	v_exp_f16_sdwa v29, v25 dst_sel:WORD_1 dst_unused:UNUSED_PRESERVE src0_sel:WORD_1
	v_pk_add_f16 v22, v30, v89
	v_pk_add_f16 v17, v17, v29
	v_pk_add_f16 v16, v16, v28
	v_pk_add_f16 v15, v15, v27
	v_pk_add_f16 v14, v14, v26
	v_pk_fma_f16 v21, v73, v29, v21
	v_pk_fma_f16 v20, v72, v28, v20
	v_pk_fma_f16 v19, v71, v27, v19
	v_pk_fma_f16 v18, v70, v26, v18
	v_pk_add_f16 v23, v31, v88
	v_pk_add_f16 v24, v32, v87
	v_pk_add_f16 v25, v33, v86
	v_exp_f16_sdwa v26, v22 dst_sel:WORD_0 dst_unused:UNUSED_PAD src0_sel:WORD_0
	v_exp_f16_sdwa v27, v23 dst_sel:WORD_0 dst_unused:UNUSED_PAD src0_sel:WORD_0
	v_exp_f16_sdwa v28, v24 dst_sel:WORD_0 dst_unused:UNUSED_PAD src0_sel:WORD_0
	v_exp_f16_sdwa v29, v25 dst_sel:WORD_0 dst_unused:UNUSED_PAD src0_sel:WORD_0
	v_exp_f16_sdwa v26, v22 dst_sel:WORD_1 dst_unused:UNUSED_PRESERVE src0_sel:WORD_1
	v_exp_f16_sdwa v27, v23 dst_sel:WORD_1 dst_unused:UNUSED_PRESERVE src0_sel:WORD_1
	v_exp_f16_sdwa v28, v24 dst_sel:WORD_1 dst_unused:UNUSED_PRESERVE src0_sel:WORD_1
	v_exp_f16_sdwa v29, v25 dst_sel:WORD_1 dst_unused:UNUSED_PRESERVE src0_sel:WORD_1
	v_pk_add_f16 v22, v42, v89
	v_pk_add_f16 v14, v14, v26
	v_pk_add_f16 v15, v15, v27
	v_pk_add_f16 v16, v16, v28
	v_pk_add_f16 v17, v17, v29
	v_pk_fma_f16 v18, v90, v26, v18
	v_pk_fma_f16 v19, v91, v27, v19
	v_pk_fma_f16 v20, v92, v28, v20
	v_pk_fma_f16 v21, v93, v29, v21
	v_pk_add_f16 v23, v43, v88
	v_pk_add_f16 v24, v44, v87
	v_pk_add_f16 v25, v45, v86
	v_exp_f16_sdwa v26, v22 dst_sel:WORD_0 dst_unused:UNUSED_PAD src0_sel:WORD_0
	v_exp_f16_sdwa v27, v23 dst_sel:WORD_0 dst_unused:UNUSED_PAD src0_sel:WORD_0
	v_exp_f16_sdwa v28, v24 dst_sel:WORD_0 dst_unused:UNUSED_PAD src0_sel:WORD_0
	v_exp_f16_sdwa v29, v25 dst_sel:WORD_0 dst_unused:UNUSED_PAD src0_sel:WORD_0
	v_exp_f16_sdwa v26, v22 dst_sel:WORD_1 dst_unused:UNUSED_PRESERVE src0_sel:WORD_1
	v_exp_f16_sdwa v27, v23 dst_sel:WORD_1 dst_unused:UNUSED_PRESERVE src0_sel:WORD_1
	v_exp_f16_sdwa v28, v24 dst_sel:WORD_1 dst_unused:UNUSED_PRESERVE src0_sel:WORD_1
	v_exp_f16_sdwa v29, v25 dst_sel:WORD_1 dst_unused:UNUSED_PRESERVE src0_sel:WORD_1
	v_pk_add_f16 v22, v58, v89
	v_pk_add_f16 v17, v17, v29
	v_pk_add_f16 v16, v16, v28
	v_pk_add_f16 v15, v15, v27
	v_pk_add_f16 v14, v14, v26
	v_pk_fma_f16 v21, v113, v29, v21
	v_pk_fma_f16 v20, v112, v28, v20
	v_pk_fma_f16 v19, v111, v27, v19
	v_pk_fma_f16 v18, v110, v26, v18
	v_pk_add_f16 v23, v59, v88
	v_pk_add_f16 v24, v60, v87
	v_pk_add_f16 v25, v61, v86
	v_exp_f16_sdwa v30, v22 dst_sel:WORD_0 dst_unused:UNUSED_PAD src0_sel:WORD_0
	v_exp_f16_sdwa v31, v23 dst_sel:WORD_0 dst_unused:UNUSED_PAD src0_sel:WORD_0
	v_exp_f16_sdwa v32, v24 dst_sel:WORD_0 dst_unused:UNUSED_PAD src0_sel:WORD_0
	v_exp_f16_sdwa v33, v25 dst_sel:WORD_0 dst_unused:UNUSED_PAD src0_sel:WORD_0
	v_exp_f16_sdwa v30, v22 dst_sel:WORD_1 dst_unused:UNUSED_PRESERVE src0_sel:WORD_1
	v_exp_f16_sdwa v31, v23 dst_sel:WORD_1 dst_unused:UNUSED_PRESERVE src0_sel:WORD_1
	v_exp_f16_sdwa v32, v24 dst_sel:WORD_1 dst_unused:UNUSED_PRESERVE src0_sel:WORD_1
	v_exp_f16_sdwa v33, v25 dst_sel:WORD_1 dst_unused:UNUSED_PRESERVE src0_sel:WORD_1
	s_nop 0
.LBB4_42:
	s_and_b64 vcc, exec, s[4:5]
	s_cbranch_vccz .LBB4_80
	global_load_dwordx3 v[146:148], v169, s[8:9]
	v_cmp_lt_u32_e64 s[64:65], 0, v199
	v_cmp_gt_u32_e64 s[66:67], 63, v199
	v_cmp_lt_u32_e64 s[68:69], 0, v180
	v_cmp_gt_u32_e64 s[70:71], 60, v180
	buffer_load_dwordx4 v[162:165], v200, s[36:39], 0 offen
	s_and_b64 s[72:73], s[68:69], s[64:65]
	s_and_b64 s[74:75], s[68:69], s[66:67]
	s_and_b64 s[76:77], s[70:71], s[64:65]
	s_and_b64 s[78:79], s[70:71], s[66:67]
	v_add_u32_e32 v245, 0xfffe7c00, v200
	v_add_u32_e32 v246, 0xfffe8000, v200
	s_mov_b64 exec, s[72:73]
	buffer_load_dwordx4 v[114:117], v245, s[36:39], 0 offen
	s_mov_b64 exec, -1
	s_mov_b64 exec, s[68:69]
	buffer_load_dwordx4 v[130:133], v246, s[36:39], 0 offen offset:512
	s_mov_b64 exec, -1
	s_mov_b64 exec, s[74:75]
	buffer_load_dwordx4 v[138:141], v246, s[36:39], 0 offen offset:2048
	s_mov_b64 exec, -1
	v_add_u32_e32 v245, 0xfffffc00, v200
	s_mov_b64 exec, s[64:65]
	buffer_load_dwordx4 v[86:89], v245, s[36:39], 0 offen
	s_mov_b64 exec, -1
	buffer_load_dwordx4 v[110:113], v200, s[36:39], 0 offen offset:512
	s_mov_b64 exec, s[66:67]
	buffer_load_dwordx4 v[126:129], v200, s[36:39], 0 offen offset:2048
	s_mov_b64 exec, -1
	v_add_u32_e32 v245, 0x17c00, v200
	v_add_u32_e32 v246, 0x18000, v200
	s_mov_b64 exec, s[64:65]
	buffer_load_dwordx4 v[54:57], v245, s[36:39], 0 offen
	s_mov_b64 exec, -1
	buffer_load_dwordx4 v[70:73], v246, s[36:39], 0 offen offset:512
	s_mov_b64 exec, s[66:67]
	buffer_load_dwordx4 v[94:97], v246, s[36:39], 0 offen offset:2048
	s_mov_b64 exec, -1
	v_add_u32_e32 v245, 0xfffe7c00, v200
	v_add_u32_e32 v246, 0xfffe8000, v200
	s_mov_b64 exec, s[72:73]
	buffer_load_dwordx4 v[74:77], v245, s[36:39], 0 offen offset:512
	s_mov_b64 exec, -1
	s_mov_b64 exec, s[68:69]
	buffer_load_dwordx4 v[98:101], v246, s[36:39], 0 offen offset:1024
	s_mov_b64 exec, -1
	s_mov_b64 exec, s[74:75]
	buffer_load_dwordx4 v[118:121], v246, s[36:39], 0 offen offset:2560
	s_mov_b64 exec, -1
	v_add_u32_e32 v245, 0xfffffc00, v200
	s_mov_b64 exec, s[64:65]
	buffer_load_dwordx4 v[46:49], v245, s[36:39], 0 offen offset:512
	s_mov_b64 exec, -1
	buffer_load_dwordx4 v[66:69], v200, s[36:39], 0 offen offset:1024
	s_mov_b64 exec, s[66:67]
	buffer_load_dwordx4 v[90:93], v200, s[36:39], 0 offen offset:2560
	s_mov_b64 exec, -1
	v_add_u32_e32 v245, 0x17c00, v200
	v_add_u32_e32 v246, 0x18000, v200
	s_mov_b64 exec, s[64:65]
	buffer_load_dwordx4 v[22:25], v245, s[36:39], 0 offen offset:512
	s_mov_b64 exec, -1
	buffer_load_dwordx4 v[34:37], v246, s[36:39], 0 offen offset:1024
	s_mov_b64 exec, s[66:67]
	buffer_load_dwordx4 v[50:53], v246, s[36:39], 0 offen offset:2560
	s_mov_b64 exec, -1
	v_add_u32_e32 v245, 0x18000, v200
	buffer_load_dwordx4 v[154:157], v245, s[36:39], 0 offen
	v_add_u32_e32 v246, 0x30000, v200
	buffer_load_dwordx4 v[150:153], v246, s[36:39], 0 offen
	v_add_u32_e32 v245, 0x2fc00, v200
	v_add_u32_e32 v246, 0x30000, v200
	v_add_u32_e32 v247, 0x47c00, v200
	v_add_u32_e32 v248, 0x48000, v200
	v_add_u32_e32 v249, 0x5fc00, v200
	v_add_u32_e32 v250, 0x60000, v200
	s_waitcnt vmcnt(22)
	v_cvt_pk_f16_f32 v6, v2, v3
	v_cvt_pk_f16_f32 v2, v8, v9
	v_cvt_pk_f16_f32 v7, v4, v5
	v_cvt_pk_f16_f32 v3, v10, v11
	v_cvt_pk_f16_f32 v8, v210, v211
	v_cvt_pk_f16_f32 v4, v214, v215
	v_cvt_pk_f16_f32 v9, v212, v213
	v_cvt_pk_f16_f32 v5, v216, v217
	s_not_b64 exec, s[72:73]
	s_cbranch_execz .Lmyf_C2_0
	v_mov_b32_e32 v114, v6
	v_mov_b32_e32 v115, v7
	v_mov_b32_e32 v116, v8
	v_mov_b32_e32 v117, v9
	v_mov_b32_e32 v74, v2
	v_mov_b32_e32 v75, v3
	v_mov_b32_e32 v76, v4
	v_mov_b32_e32 v77, v5

.Lmyf_C2_7:
	s_mov_b64 exec, -1
	s_waitcnt vmcnt(21)
	v_cvt_f16_f32_e32 v158, v147
	v_cvt_f16_f32_e32 v160, v146
	v_cvt_f16_f32_e32 v159, v148
	v_add_u32_e32 v251, 0x48000, v200
	buffer_load_dwordx4 v[146:149], v251, s[36:39], 0 offen
	s_waitcnt vmcnt(12)
	v_pk_mul_f16 v161, v160, v162 op_sel_hi:[0,1]
	v_pk_mul_f16 v204, v160, v165 op_sel_hi:[0,1]
	v_pk_mul_f16 v208, v158, v165 op_sel_hi:[0,1]
	v_pk_mul_f16 v212, v159, v165 op_sel_hi:[0,1]
	v_pk_mul_f16 v202, v160, v163 op_sel_hi:[0,1]
	v_pk_mul_f16 v203, v160, v164 op_sel_hi:[0,1]
	v_pk_mul_f16 v205, v158, v162 op_sel_hi:[0,1]
	v_pk_mul_f16 v206, v158, v163 op_sel_hi:[0,1]
	v_pk_mul_f16 v207, v158, v164 op_sel_hi:[0,1]
	v_pk_mul_f16 v209, v159, v162 op_sel_hi:[0,1]
	v_pk_mul_f16 v210, v159, v163 op_sel_hi:[0,1]
	v_pk_mul_f16 v211, v159, v164 op_sel_hi:[0,1]
	v_pk_fma_f16 v117, v117, v165, v204
	v_pk_fma_f16 v114, v114, v162, v161
	v_pk_fma_f16 v133, v133, v165, v204
	v_pk_fma_f16 v130, v130, v162, v161
	v_pk_fma_f16 v141, v141, v165, v204
	v_pk_fma_f16 v138, v138, v162, v161
	v_pk_fma_f16 v161, v89, v165, v208
	v_pk_fma_f16 v213, v113, v165, v208
	v_pk_fma_f16 v208, v129, v165, v208
	v_pk_fma_f16 v217, v57, v165, v212
	v_pk_fma_f16 v221, v73, v165, v212
	v_pk_fma_f16 v165, v97, v165, v212
	v_pk_maximum3_f16 v212, v117, v133, v141
	v_pk_fma_f16 v116, v116, v164, v203
	v_pk_fma_f16 v115, v115, v163, v202
	v_pk_fma_f16 v132, v132, v164, v203
	v_pk_fma_f16 v131, v131, v163, v202
	v_pk_fma_f16 v140, v140, v164, v203
	v_pk_fma_f16 v139, v139, v163, v202
	v_pk_fma_f16 v202, v88, v164, v207
	v_pk_fma_f16 v203, v87, v163, v206
	v_pk_fma_f16 v204, v86, v162, v205
	v_pk_fma_f16 v214, v112, v164, v207
	v_pk_fma_f16 v215, v111, v163, v206
	v_pk_fma_f16 v216, v110, v162, v205
	v_pk_fma_f16 v207, v128, v164, v207
	v_pk_fma_f16 v206, v127, v163, v206
	v_pk_fma_f16 v205, v126, v162, v205
	v_pk_fma_f16 v218, v56, v164, v211
	v_pk_fma_f16 v219, v55, v163, v210
	v_pk_fma_f16 v220, v54, v162, v209
	v_pk_fma_f16 v222, v72, v164, v211
	v_pk_fma_f16 v223, v71, v163, v210
	v_pk_fma_f16 v224, v70, v162, v209
	v_pk_fma_f16 v164, v96, v164, v211
	v_pk_fma_f16 v163, v95, v163, v210
	v_pk_fma_f16 v162, v94, v162, v209
	v_pk_maximum3_f16 v209, v114, v130, v138
	v_pk_maximum3_f16 v210, v115, v131, v139
	v_pk_maximum3_f16 v211, v116, v132, v140
	v_pk_maximum3_f16 v228, v161, v213, v208
	v_pk_maximum3_f16 v232, v217, v221, v165
	v_pk_maximum3_f16 v225, v204, v216, v205
	v_pk_maximum3_f16 v226, v203, v215, v206
	v_pk_maximum3_f16 v227, v202, v214, v207
	v_pk_maximum3_f16 v229, v220, v224, v162
	v_pk_maximum3_f16 v230, v219, v223, v163
	v_pk_maximum3_f16 v212, v212, v228, v232
	v_pk_maximum3_f16 v231, v218, v222, v164
	v_pk_maximum3_f16 v209, v209, v225, v229
	v_pk_maximum3_f16 v210, v210, v226, v230
	v_pk_maximum3_f16 v211, v211, v227, v231
	v_pk_add_f16 v117, v117, v212 neg_lo:[0,1] neg_hi:[0,1]
	v_pk_add_f16 v114, v114, v209 neg_lo:[0,1] neg_hi:[0,1]
	v_pk_add_f16 v115, v115, v210 neg_lo:[0,1] neg_hi:[0,1]
	v_pk_add_f16 v116, v116, v211 neg_lo:[0,1] neg_hi:[0,1]
	v_pk_add_f16 v130, v130, v209 neg_lo:[0,1] neg_hi:[0,1]
	v_exp_f16_sdwa v225, v114 dst_sel:WORD_0 dst_unused:UNUSED_PAD src0_sel:WORD_0
	v_exp_f16_sdwa v226, v115 dst_sel:WORD_0 dst_unused:UNUSED_PAD src0_sel:WORD_0
	v_exp_f16_sdwa v227, v116 dst_sel:WORD_0 dst_unused:UNUSED_PAD src0_sel:WORD_0
	v_exp_f16_sdwa v228, v117 dst_sel:WORD_0 dst_unused:UNUSED_PAD src0_sel:WORD_0
	v_exp_f16_sdwa v225, v114 dst_sel:WORD_1 dst_unused:UNUSED_PRESERVE src0_sel:WORD_1
	v_exp_f16_sdwa v226, v115 dst_sel:WORD_1 dst_unused:UNUSED_PRESERVE src0_sel:WORD_1
	v_exp_f16_sdwa v227, v116 dst_sel:WORD_1 dst_unused:UNUSED_PRESERVE src0_sel:WORD_1
	v_exp_f16_sdwa v228, v117 dst_sel:WORD_1 dst_unused:UNUSED_PRESERVE src0_sel:WORD_1
	v_pk_add_f16 v131, v131, v210 neg_lo:[0,1] neg_hi:[0,1]
	v_pk_add_f16 v117, v225, 0
	s_waitcnt vmcnt(3)
	v_pk_fma_f16 v77, v77, v228, 0
	v_pk_add_f16 v114, v228, 0
	v_pk_add_f16 v115, v227, 0
	v_pk_add_f16 v116, v226, 0
	v_pk_fma_f16 v76, v76, v227, 0
	v_pk_fma_f16 v75, v75, v226, 0
	s_mov_b64 exec, s[64:65]
	buffer_load_dwordx4 v[26:29], v245, s[36:39], 0 offen
	buffer_load_dwordx4 v[10:13], v245, s[36:39], 0 offen offset:512
	s_mov_b64 exec, -1
	v_pk_fma_f16 v74, v74, v225, 0
	v_pk_add_f16 v132, v132, v211 neg_lo:[0,1] neg_hi:[0,1]
	v_pk_add_f16 v133, v133, v212 neg_lo:[0,1] neg_hi:[0,1]
	v_exp_f16_sdwa v225, v130 dst_sel:WORD_0 dst_unused:UNUSED_PAD src0_sel:WORD_0
	v_exp_f16_sdwa v226, v131 dst_sel:WORD_0 dst_unused:UNUSED_PAD src0_sel:WORD_0
	v_exp_f16_sdwa v227, v132 dst_sel:WORD_0 dst_unused:UNUSED_PAD src0_sel:WORD_0
	v_exp_f16_sdwa v228, v133 dst_sel:WORD_0 dst_unused:UNUSED_PAD src0_sel:WORD_0
	v_exp_f16_sdwa v225, v130 dst_sel:WORD_1 dst_unused:UNUSED_PRESERVE src0_sel:WORD_1
	v_exp_f16_sdwa v226, v131 dst_sel:WORD_1 dst_unused:UNUSED_PRESERVE src0_sel:WORD_1
	v_exp_f16_sdwa v227, v132 dst_sel:WORD_1 dst_unused:UNUSED_PRESERVE src0_sel:WORD_1
	v_exp_f16_sdwa v228, v133 dst_sel:WORD_1 dst_unused:UNUSED_PRESERVE src0_sel:WORD_1
	v_pk_add_f16 v117, v117, v225
	v_pk_fma_f16 v77, v101, v228, v77
	v_pk_add_f16 v101, v141, v212 neg_lo:[0,1] neg_hi:[0,1]
	v_pk_add_f16 v116, v116, v226
	v_pk_add_f16 v115, v115, v227
	v_pk_add_f16 v114, v114, v228
	buffer_load_dwordx4 v[38:41], v246, s[36:39], 0 offen offset:512
	buffer_load_dwordx4 v[14:17], v246, s[36:39], 0 offen offset:1024
	v_pk_fma_f16 v74, v98, v225, v74
	v_pk_fma_f16 v75, v99, v226, v75
	v_pk_fma_f16 v76, v100, v227, v76
	v_pk_add_f16 v98, v138, v209 neg_lo:[0,1] neg_hi:[0,1]
	v_pk_add_f16 v99, v139, v210 neg_lo:[0,1] neg_hi:[0,1]
	v_pk_add_f16 v100, v140, v211 neg_lo:[0,1] neg_hi:[0,1]
	v_exp_f16_sdwa v130, v98 dst_sel:WORD_0 dst_unused:UNUSED_PAD src0_sel:WORD_0
	v_exp_f16_sdwa v131, v99 dst_sel:WORD_0 dst_unused:UNUSED_PAD src0_sel:WORD_0
	v_exp_f16_sdwa v132, v100 dst_sel:WORD_0 dst_unused:UNUSED_PAD src0_sel:WORD_0
	v_exp_f16_sdwa v133, v101 dst_sel:WORD_0 dst_unused:UNUSED_PAD src0_sel:WORD_0
	v_exp_f16_sdwa v130, v98 dst_sel:WORD_1 dst_unused:UNUSED_PRESERVE src0_sel:WORD_1
	v_exp_f16_sdwa v131, v99 dst_sel:WORD_1 dst_unused:UNUSED_PRESERVE src0_sel:WORD_1
	v_exp_f16_sdwa v132, v100 dst_sel:WORD_1 dst_unused:UNUSED_PRESERVE src0_sel:WORD_1
	v_exp_f16_sdwa v133, v101 dst_sel:WORD_1 dst_unused:UNUSED_PRESERVE src0_sel:WORD_1
	v_pk_add_f16 v101, v117, v130
	v_pk_add_f16 v98, v114, v133
	v_pk_add_f16 v99, v115, v132
	s_mov_b64 exec, s[66:67]
	buffer_load_dwordx4 v[58:61], v246, s[36:39], 0 offen offset:2048
	buffer_load_dwordx4 v[18:21], v246, s[36:39], 0 offen offset:2560
	s_mov_b64 exec, -1
	v_pk_add_f16 v100, v116, v131
	v_pk_fma_f16 v77, v121, v133, v77
	v_pk_fma_f16 v76, v120, v132, v76
	v_pk_fma_f16 v75, v119, v131, v75
	v_pk_fma_f16 v74, v118, v130, v74
	v_pk_add_f16 v114, v204, v209 neg_lo:[0,1] neg_hi:[0,1]
	v_pk_add_f16 v115, v203, v210 neg_lo:[0,1] neg_hi:[0,1]
	v_pk_add_f16 v116, v202, v211 neg_lo:[0,1] neg_hi:[0,1]
	s_mov_b64 exec, s[64:65]
	buffer_load_dwordx4 v[78:81], v247, s[36:39], 0 offen
	buffer_load_dwordx4 v[30:33], v247, s[36:39], 0 offen offset:512
	s_mov_b64 exec, -1
	v_pk_add_f16 v117, v161, v212 neg_lo:[0,1] neg_hi:[0,1]
	v_exp_f16_sdwa v118, v114 dst_sel:WORD_0 dst_unused:UNUSED_PAD src0_sel:WORD_0
	v_exp_f16_sdwa v119, v115 dst_sel:WORD_0 dst_unused:UNUSED_PAD src0_sel:WORD_0
	v_exp_f16_sdwa v120, v116 dst_sel:WORD_0 dst_unused:UNUSED_PAD src0_sel:WORD_0
	v_exp_f16_sdwa v121, v117 dst_sel:WORD_0 dst_unused:UNUSED_PAD src0_sel:WORD_0
	v_exp_f16_sdwa v118, v114 dst_sel:WORD_1 dst_unused:UNUSED_PRESERVE src0_sel:WORD_1
	v_exp_f16_sdwa v119, v115 dst_sel:WORD_1 dst_unused:UNUSED_PRESERVE src0_sel:WORD_1
	v_exp_f16_sdwa v120, v116 dst_sel:WORD_1 dst_unused:UNUSED_PRESERVE src0_sel:WORD_1
	v_exp_f16_sdwa v121, v117 dst_sel:WORD_1 dst_unused:UNUSED_PRESERVE src0_sel:WORD_1
	v_pk_add_f16 v114, v216, v209 neg_lo:[0,1] neg_hi:[0,1]
	v_pk_add_f16 v101, v101, v118
	v_pk_add_f16 v100, v100, v119
	v_pk_add_f16 v99, v99, v120
	v_pk_add_f16 v98, v98, v121
	v_pk_fma_f16 v74, v46, v118, v74
	v_pk_fma_f16 v75, v47, v119, v75
	v_pk_fma_f16 v76, v48, v120, v76
	v_pk_fma_f16 v77, v49, v121, v77
	buffer_load_dwordx4 v[106:109], v248, s[36:39], 0 offen offset:512
	buffer_load_dwordx4 v[42:45], v248, s[36:39], 0 offen offset:1024
	v_pk_add_f16 v115, v215, v210 neg_lo:[0,1] neg_hi:[0,1]
	v_pk_add_f16 v116, v214, v211 neg_lo:[0,1] neg_hi:[0,1]
	v_pk_add_f16 v117, v213, v212 neg_lo:[0,1] neg_hi:[0,1]
	v_exp_f16_sdwa v118, v114 dst_sel:WORD_0 dst_unused:UNUSED_PAD src0_sel:WORD_0
	v_exp_f16_sdwa v119, v115 dst_sel:WORD_0 dst_unused:UNUSED_PAD src0_sel:WORD_0
	v_exp_f16_sdwa v120, v116 dst_sel:WORD_0 dst_unused:UNUSED_PAD src0_sel:WORD_0
	v_exp_f16_sdwa v121, v117 dst_sel:WORD_0 dst_unused:UNUSED_PAD src0_sel:WORD_0
	v_exp_f16_sdwa v118, v114 dst_sel:WORD_1 dst_unused:UNUSED_PRESERVE src0_sel:WORD_1
	v_exp_f16_sdwa v119, v115 dst_sel:WORD_1 dst_unused:UNUSED_PRESERVE src0_sel:WORD_1
	v_exp_f16_sdwa v120, v116 dst_sel:WORD_1 dst_unused:UNUSED_PRESERVE src0_sel:WORD_1
	v_exp_f16_sdwa v121, v117 dst_sel:WORD_1 dst_unused:UNUSED_PRESERVE src0_sel:WORD_1
	v_pk_add_f16 v114, v205, v209 neg_lo:[0,1] neg_hi:[0,1]
	v_pk_add_f16 v101, v101, v118
	v_pk_add_f16 v98, v98, v121
	v_pk_add_f16 v99, v99, v120
	v_pk_add_f16 v100, v100, v119
	v_pk_fma_f16 v77, v69, v121, v77
	s_mov_b64 exec, s[66:67]
	buffer_load_dwordx4 v[122:125], v248, s[36:39], 0 offen offset:2048
	buffer_load_dwordx4 v[62:65], v248, s[36:39], 0 offen offset:2560
	s_mov_b64 exec, -1
	v_pk_fma_f16 v76, v68, v120, v76
	v_pk_fma_f16 v75, v67, v119, v75
	v_pk_fma_f16 v74, v66, v118, v74
	v_pk_add_f16 v115, v206, v210 neg_lo:[0,1] neg_hi:[0,1]
	v_pk_add_f16 v116, v207, v211 neg_lo:[0,1] neg_hi:[0,1]
	v_pk_add_f16 v117, v208, v212 neg_lo:[0,1] neg_hi:[0,1]
	v_exp_f16_sdwa v118, v114 dst_sel:WORD_0 dst_unused:UNUSED_PAD src0_sel:WORD_0
	v_exp_f16_sdwa v119, v115 dst_sel:WORD_0 dst_unused:UNUSED_PAD src0_sel:WORD_0
	v_exp_f16_sdwa v120, v116 dst_sel:WORD_0 dst_unused:UNUSED_PAD src0_sel:WORD_0
	v_exp_f16_sdwa v121, v117 dst_sel:WORD_0 dst_unused:UNUSED_PAD src0_sel:WORD_0
	v_exp_f16_sdwa v118, v114 dst_sel:WORD_1 dst_unused:UNUSED_PRESERVE src0_sel:WORD_1
	v_exp_f16_sdwa v119, v115 dst_sel:WORD_1 dst_unused:UNUSED_PRESERVE src0_sel:WORD_1
	v_exp_f16_sdwa v120, v116 dst_sel:WORD_1 dst_unused:UNUSED_PRESERVE src0_sel:WORD_1
	v_exp_f16_sdwa v121, v117 dst_sel:WORD_1 dst_unused:UNUSED_PRESERVE src0_sel:WORD_1
	v_pk_add_f16 v114, v220, v209 neg_lo:[0,1] neg_hi:[0,1]
	v_pk_add_f16 v101, v101, v118
	v_pk_add_f16 v100, v100, v119
	s_mov_b64 exec, s[76:77]
	buffer_load_dwordx4 v[134:137], v249, s[36:39], 0 offen
	buffer_load_dwordx4 v[82:85], v249, s[36:39], 0 offen offset:512
	s_mov_b64 exec, -1
	v_pk_add_f16 v99, v99, v120
	v_pk_add_f16 v98, v98, v121
	v_pk_fma_f16 v74, v90, v118, v74
	v_pk_fma_f16 v75, v91, v119, v75
	v_pk_fma_f16 v76, v92, v120, v76
	v_pk_fma_f16 v77, v93, v121, v77
	v_pk_add_f16 v115, v219, v210 neg_lo:[0,1] neg_hi:[0,1]
	v_pk_add_f16 v116, v218, v211 neg_lo:[0,1] neg_hi:[0,1]
	s_mov_b64 exec, s[70:71]
	buffer_load_dwordx4 v[142:145], v250, s[36:39], 0 offen offset:512
	buffer_load_dwordx4 v[102:105], v250, s[36:39], 0 offen offset:1024
	s_mov_b64 exec, -1
	v_pk_add_f16 v117, v217, v212 neg_lo:[0,1] neg_hi:[0,1]
	v_exp_f16_sdwa v118, v114 dst_sel:WORD_0 dst_unused:UNUSED_PAD src0_sel:WORD_0
	v_exp_f16_sdwa v119, v115 dst_sel:WORD_0 dst_unused:UNUSED_PAD src0_sel:WORD_0
	v_exp_f16_sdwa v120, v116 dst_sel:WORD_0 dst_unused:UNUSED_PAD src0_sel:WORD_0
	v_exp_f16_sdwa v121, v117 dst_sel:WORD_0 dst_unused:UNUSED_PAD src0_sel:WORD_0
	v_exp_f16_sdwa v118, v114 dst_sel:WORD_1 dst_unused:UNUSED_PRESERVE src0_sel:WORD_1
	v_exp_f16_sdwa v119, v115 dst_sel:WORD_1 dst_unused:UNUSED_PRESERVE src0_sel:WORD_1
	v_exp_f16_sdwa v120, v116 dst_sel:WORD_1 dst_unused:UNUSED_PRESERVE src0_sel:WORD_1
	v_exp_f16_sdwa v121, v117 dst_sel:WORD_1 dst_unused:UNUSED_PRESERVE src0_sel:WORD_1
	v_pk_add_f16 v114, v224, v209 neg_lo:[0,1] neg_hi:[0,1]
	v_pk_add_f16 v101, v101, v118
	v_pk_add_f16 v98, v98, v121
	v_pk_add_f16 v99, v99, v120
	v_pk_add_f16 v100, v100, v119
	v_pk_fma_f16 v77, v25, v121, v77
	v_pk_fma_f16 v76, v24, v120, v76
	v_pk_fma_f16 v75, v23, v119, v75
	s_mov_b64 exec, s[78:79]
	buffer_load_dwordx4 v[6:9], v250, s[36:39], 0 offen offset:2048
	buffer_load_dwordx4 v[2:5], v250, s[36:39], 0 offen offset:2560
	s_mov_b64 exec, -1
	v_pk_fma_f16 v74, v22, v118, v74
	v_pk_add_f16 v115, v223, v210 neg_lo:[0,1] neg_hi:[0,1]
	v_pk_add_f16 v116, v222, v211 neg_lo:[0,1] neg_hi:[0,1]
	v_pk_add_f16 v117, v221, v212 neg_lo:[0,1] neg_hi:[0,1]
	v_exp_f16_sdwa v118, v114 dst_sel:WORD_0 dst_unused:UNUSED_PAD src0_sel:WORD_0
	v_exp_f16_sdwa v119, v115 dst_sel:WORD_0 dst_unused:UNUSED_PAD src0_sel:WORD_0
	v_exp_f16_sdwa v120, v116 dst_sel:WORD_0 dst_unused:UNUSED_PAD src0_sel:WORD_0
	v_exp_f16_sdwa v121, v117 dst_sel:WORD_0 dst_unused:UNUSED_PAD src0_sel:WORD_0
	v_exp_f16_sdwa v118, v114 dst_sel:WORD_1 dst_unused:UNUSED_PRESERVE src0_sel:WORD_1
	v_exp_f16_sdwa v119, v115 dst_sel:WORD_1 dst_unused:UNUSED_PRESERVE src0_sel:WORD_1
	v_exp_f16_sdwa v120, v116 dst_sel:WORD_1 dst_unused:UNUSED_PRESERVE src0_sel:WORD_1
	v_exp_f16_sdwa v121, v117 dst_sel:WORD_1 dst_unused:UNUSED_PRESERVE src0_sel:WORD_1
	v_pk_add_f16 v114, v162, v209 neg_lo:[0,1] neg_hi:[0,1]
	v_pk_add_f16 v101, v101, v118
	v_pk_add_f16 v100, v100, v119
	v_pk_add_f16 v99, v99, v120
	v_pk_add_f16 v98, v98, v121
	v_pk_fma_f16 v74, v34, v118, v74
	v_pk_fma_f16 v75, v35, v119, v75
	v_pk_fma_f16 v76, v36, v120, v76
	v_pk_fma_f16 v77, v37, v121, v77
	v_pk_add_f16 v115, v163, v210 neg_lo:[0,1] neg_hi:[0,1]
	v_pk_add_f16 v116, v164, v211 neg_lo:[0,1] neg_hi:[0,1]
	v_pk_add_f16 v117, v165, v212 neg_lo:[0,1] neg_hi:[0,1]
	v_exp_f16_sdwa v118, v114 dst_sel:WORD_0 dst_unused:UNUSED_PAD src0_sel:WORD_0
	v_exp_f16_sdwa v119, v115 dst_sel:WORD_0 dst_unused:UNUSED_PAD src0_sel:WORD_0
	v_exp_f16_sdwa v120, v116 dst_sel:WORD_0 dst_unused:UNUSED_PAD src0_sel:WORD_0
	v_exp_f16_sdwa v121, v117 dst_sel:WORD_0 dst_unused:UNUSED_PAD src0_sel:WORD_0
	v_exp_f16_sdwa v118, v114 dst_sel:WORD_1 dst_unused:UNUSED_PRESERVE src0_sel:WORD_1
	v_exp_f16_sdwa v119, v115 dst_sel:WORD_1 dst_unused:UNUSED_PRESERVE src0_sel:WORD_1
	v_exp_f16_sdwa v120, v116 dst_sel:WORD_1 dst_unused:UNUSED_PRESERVE src0_sel:WORD_1
	v_exp_f16_sdwa v121, v117 dst_sel:WORD_1 dst_unused:UNUSED_PRESERVE src0_sel:WORD_1
	v_pk_add_f16 v101, v101, v118
	v_pk_add_f16 v100, v100, v119
	v_rcp_f16_e32 v114, v101
	v_rcp_f16_sdwa v101, v101 dst_sel:DWORD dst_unused:UNUSED_PAD src0_sel:WORD_1
	v_pk_add_f16 v99, v99, v120
	v_rcp_f16_e32 v115, v100
	v_rcp_f16_sdwa v100, v100 dst_sel:DWORD dst_unused:UNUSED_PAD src0_sel:WORD_1
	v_pk_add_f16 v98, v98, v121
	v_rcp_f16_e32 v116, v99
	v_rcp_f16_sdwa v99, v99 dst_sel:DWORD dst_unused:UNUSED_PAD src0_sel:WORD_1
	v_rcp_f16_e32 v117, v98
	v_rcp_f16_sdwa v98, v98 dst_sel:DWORD dst_unused:UNUSED_PAD src0_sel:WORD_1
	v_pk_fma_f16 v74, v50, v118, v74
	v_pack_b32_f16 v101, v114, v101
	v_pk_fma_f16 v75, v51, v119, v75
	v_pk_mul_f16 v138, v74, v101
	v_pack_b32_f16 v74, v115, v100
	v_pk_fma_f16 v76, v52, v120, v76
	v_pk_mul_f16 v139, v75, v74
	v_pack_b32_f16 v74, v116, v99
	v_pk_fma_f16 v77, v53, v121, v77
	v_pk_mul_f16 v140, v76, v74
	v_pack_b32_f16 v74, v117, v98
	v_pk_mul_f16 v141, v77, v74
	s_waitcnt vmcnt(12)
	v_pk_mul_f16 v74, v160, v154 op_sel_hi:[0,1]
	v_pk_mul_f16 v77, v160, v157 op_sel_hi:[0,1]
	v_pk_mul_f16 v101, v158, v157 op_sel_hi:[0,1]
	v_pk_mul_f16 v117, v159, v157 op_sel_hi:[0,1]
	v_pk_mul_f16 v75, v160, v155 op_sel_hi:[0,1]
	v_pk_mul_f16 v76, v160, v156 op_sel_hi:[0,1]
	v_pk_mul_f16 v98, v158, v154 op_sel_hi:[0,1]
	v_pk_mul_f16 v99, v158, v155 op_sel_hi:[0,1]
	v_pk_mul_f16 v100, v158, v156 op_sel_hi:[0,1]
	v_pk_mul_f16 v114, v159, v154 op_sel_hi:[0,1]
	v_pk_mul_f16 v115, v159, v155 op_sel_hi:[0,1]
	v_pk_mul_f16 v116, v159, v156 op_sel_hi:[0,1]
	v_pk_fma_f16 v89, v89, v157, v77
	v_pk_fma_f16 v86, v86, v154, v74
	v_pk_fma_f16 v113, v113, v157, v77
	v_pk_fma_f16 v110, v110, v154, v74
	v_pk_fma_f16 v77, v129, v157, v77
	v_pk_fma_f16 v74, v126, v154, v74
	v_pk_fma_f16 v118, v57, v157, v101
	v_pk_fma_f16 v126, v73, v157, v101
	v_pk_fma_f16 v101, v97, v157, v101
	v_pk_fma_f16 v130, v29, v157, v117
	v_pk_fma_f16 v161, v41, v157, v117
	v_pk_fma_f16 v117, v61, v157, v117
	v_pk_maximum3_f16 v157, v89, v113, v77
	v_pk_fma_f16 v88, v88, v156, v76
	v_pk_fma_f16 v87, v87, v155, v75
	v_pk_fma_f16 v112, v112, v156, v76
	v_pk_fma_f16 v111, v111, v155, v75
	v_pk_fma_f16 v76, v128, v156, v76
	v_pk_fma_f16 v75, v127, v155, v75
	v_pk_fma_f16 v119, v56, v156, v100
	v_pk_fma_f16 v120, v55, v155, v99
	v_pk_fma_f16 v121, v54, v154, v98
	v_pk_fma_f16 v127, v72, v156, v100
	v_pk_fma_f16 v128, v71, v155, v99
	v_pk_fma_f16 v129, v70, v154, v98
	v_pk_fma_f16 v100, v96, v156, v100
	v_pk_fma_f16 v99, v95, v155, v99
	v_pk_fma_f16 v98, v94, v154, v98
	v_pk_fma_f16 v131, v28, v156, v116
	v_pk_fma_f16 v132, v27, v155, v115
	v_pk_fma_f16 v133, v26, v154, v114
	v_pk_fma_f16 v162, v40, v156, v116
	v_pk_fma_f16 v163, v39, v155, v115
	v_pk_fma_f16 v164, v38, v154, v114
	v_pk_fma_f16 v116, v60, v156, v116
	v_pk_fma_f16 v115, v59, v155, v115
	v_pk_fma_f16 v114, v58, v154, v114
	v_pk_maximum3_f16 v154, v86, v110, v74
	v_pk_maximum3_f16 v155, v87, v111, v75
	v_pk_maximum3_f16 v156, v88, v112, v76
	v_pk_maximum3_f16 v204, v118, v126, v101
	v_pk_maximum3_f16 v208, v130, v161, v117
	v_pk_maximum3_f16 v165, v121, v129, v98
	v_pk_maximum3_f16 v202, v120, v128, v99
	v_pk_maximum3_f16 v203, v119, v127, v100
	v_pk_maximum3_f16 v205, v133, v164, v114
	v_pk_maximum3_f16 v206, v132, v163, v115
	v_pk_maximum3_f16 v157, v157, v204, v208
	v_pk_maximum3_f16 v207, v131, v162, v116
	v_pk_maximum3_f16 v154, v154, v165, v205
	v_pk_maximum3_f16 v155, v155, v202, v206
	v_pk_maximum3_f16 v156, v156, v203, v207
	v_pk_add_f16 v89, v89, v157 neg_lo:[0,1] neg_hi:[0,1]
	v_pk_add_f16 v86, v86, v154 neg_lo:[0,1] neg_hi:[0,1]
	v_pk_add_f16 v87, v87, v155 neg_lo:[0,1] neg_hi:[0,1]
	v_pk_add_f16 v88, v88, v156 neg_lo:[0,1] neg_hi:[0,1]
	v_pk_add_f16 v110, v110, v154 neg_lo:[0,1] neg_hi:[0,1]
	v_exp_f16_sdwa v165, v86 dst_sel:WORD_0 dst_unused:UNUSED_PAD src0_sel:WORD_0
	v_exp_f16_sdwa v202, v87 dst_sel:WORD_0 dst_unused:UNUSED_PAD src0_sel:WORD_0
	v_exp_f16_sdwa v203, v88 dst_sel:WORD_0 dst_unused:UNUSED_PAD src0_sel:WORD_0
	v_exp_f16_sdwa v204, v89 dst_sel:WORD_0 dst_unused:UNUSED_PAD src0_sel:WORD_0
	v_exp_f16_sdwa v165, v86 dst_sel:WORD_1 dst_unused:UNUSED_PRESERVE src0_sel:WORD_1
	v_exp_f16_sdwa v202, v87 dst_sel:WORD_1 dst_unused:UNUSED_PRESERVE src0_sel:WORD_1
	v_exp_f16_sdwa v203, v88 dst_sel:WORD_1 dst_unused:UNUSED_PRESERVE src0_sel:WORD_1
	v_exp_f16_sdwa v204, v89 dst_sel:WORD_1 dst_unused:UNUSED_PRESERVE src0_sel:WORD_1
	v_pk_add_f16 v111, v111, v155 neg_lo:[0,1] neg_hi:[0,1]
	v_pk_add_f16 v89, v165, 0
	v_pk_fma_f16 v49, v49, v204, 0
	v_pk_add_f16 v86, v204, 0
	v_pk_add_f16 v87, v203, 0
	v_pk_add_f16 v88, v202, 0
	v_pk_fma_f16 v48, v48, v203, 0
	v_pk_fma_f16 v47, v47, v202, 0
	v_pk_fma_f16 v46, v46, v165, 0
	v_pk_add_f16 v112, v112, v156 neg_lo:[0,1] neg_hi:[0,1]
	v_pk_add_f16 v113, v113, v157 neg_lo:[0,1] neg_hi:[0,1]
	v_exp_f16_sdwa v165, v110 dst_sel:WORD_0 dst_unused:UNUSED_PAD src0_sel:WORD_0
	v_exp_f16_sdwa v202, v111 dst_sel:WORD_0 dst_unused:UNUSED_PAD src0_sel:WORD_0
	v_exp_f16_sdwa v203, v112 dst_sel:WORD_0 dst_unused:UNUSED_PAD src0_sel:WORD_0
	v_exp_f16_sdwa v204, v113 dst_sel:WORD_0 dst_unused:UNUSED_PAD src0_sel:WORD_0
	v_exp_f16_sdwa v165, v110 dst_sel:WORD_1 dst_unused:UNUSED_PRESERVE src0_sel:WORD_1
	v_exp_f16_sdwa v202, v111 dst_sel:WORD_1 dst_unused:UNUSED_PRESERVE src0_sel:WORD_1
	v_exp_f16_sdwa v203, v112 dst_sel:WORD_1 dst_unused:UNUSED_PRESERVE src0_sel:WORD_1
	v_exp_f16_sdwa v204, v113 dst_sel:WORD_1 dst_unused:UNUSED_PRESERVE src0_sel:WORD_1
	v_pk_add_f16 v89, v89, v165
	v_pk_fma_f16 v49, v69, v204, v49
	v_pk_add_f16 v69, v77, v157 neg_lo:[0,1] neg_hi:[0,1]
	v_pk_add_f16 v88, v88, v202
	v_pk_add_f16 v87, v87, v203
	v_pk_add_f16 v86, v86, v204
	v_pk_fma_f16 v46, v66, v165, v46
	v_pk_fma_f16 v47, v67, v202, v47
	v_pk_fma_f16 v48, v68, v203, v48
	v_pk_add_f16 v66, v74, v154 neg_lo:[0,1] neg_hi:[0,1]
	v_pk_add_f16 v67, v75, v155 neg_lo:[0,1] neg_hi:[0,1]
	v_pk_add_f16 v68, v76, v156 neg_lo:[0,1] neg_hi:[0,1]
	v_exp_f16_sdwa v74, v66 dst_sel:WORD_0 dst_unused:UNUSED_PAD src0_sel:WORD_0
	v_exp_f16_sdwa v75, v67 dst_sel:WORD_0 dst_unused:UNUSED_PAD src0_sel:WORD_0
	v_exp_f16_sdwa v76, v68 dst_sel:WORD_0 dst_unused:UNUSED_PAD src0_sel:WORD_0
	v_exp_f16_sdwa v77, v69 dst_sel:WORD_0 dst_unused:UNUSED_PAD src0_sel:WORD_0
	v_exp_f16_sdwa v74, v66 dst_sel:WORD_1 dst_unused:UNUSED_PRESERVE src0_sel:WORD_1
	v_exp_f16_sdwa v75, v67 dst_sel:WORD_1 dst_unused:UNUSED_PRESERVE src0_sel:WORD_1
	v_exp_f16_sdwa v76, v68 dst_sel:WORD_1 dst_unused:UNUSED_PRESERVE src0_sel:WORD_1
	v_exp_f16_sdwa v77, v69 dst_sel:WORD_1 dst_unused:UNUSED_PRESERVE src0_sel:WORD_1
	v_pk_add_f16 v69, v89, v74
	v_pk_add_f16 v66, v86, v77
	v_pk_add_f16 v67, v87, v76
	v_pk_add_f16 v68, v88, v75
	v_pk_fma_f16 v49, v93, v77, v49
	v_pk_fma_f16 v48, v92, v76, v48
	v_pk_fma_f16 v47, v91, v75, v47
	v_pk_fma_f16 v46, v90, v74, v46
	v_pk_add_f16 v74, v121, v154 neg_lo:[0,1] neg_hi:[0,1]
	v_pk_add_f16 v75, v120, v155 neg_lo:[0,1] neg_hi:[0,1]
	v_pk_add_f16 v76, v119, v156 neg_lo:[0,1] neg_hi:[0,1]
	v_pk_add_f16 v77, v118, v157 neg_lo:[0,1] neg_hi:[0,1]
	v_exp_f16_sdwa v86, v74 dst_sel:WORD_0 dst_unused:UNUSED_PAD src0_sel:WORD_0
	v_exp_f16_sdwa v87, v75 dst_sel:WORD_0 dst_unused:UNUSED_PAD src0_sel:WORD_0
	v_exp_f16_sdwa v88, v76 dst_sel:WORD_0 dst_unused:UNUSED_PAD src0_sel:WORD_0
	v_exp_f16_sdwa v89, v77 dst_sel:WORD_0 dst_unused:UNUSED_PAD src0_sel:WORD_0
	v_exp_f16_sdwa v86, v74 dst_sel:WORD_1 dst_unused:UNUSED_PRESERVE src0_sel:WORD_1
	v_exp_f16_sdwa v87, v75 dst_sel:WORD_1 dst_unused:UNUSED_PRESERVE src0_sel:WORD_1
	v_exp_f16_sdwa v88, v76 dst_sel:WORD_1 dst_unused:UNUSED_PRESERVE src0_sel:WORD_1
	v_exp_f16_sdwa v89, v77 dst_sel:WORD_1 dst_unused:UNUSED_PRESERVE src0_sel:WORD_1
	v_pk_add_f16 v74, v129, v154 neg_lo:[0,1] neg_hi:[0,1]
	v_pk_add_f16 v69, v69, v86
	v_pk_add_f16 v68, v68, v87
	v_pk_add_f16 v67, v67, v88
	v_pk_add_f16 v66, v66, v89
	v_pk_fma_f16 v46, v22, v86, v46
	v_pk_fma_f16 v47, v23, v87, v47
	v_pk_fma_f16 v48, v24, v88, v48
	v_pk_fma_f16 v49, v25, v89, v49
	v_pk_add_f16 v75, v128, v155 neg_lo:[0,1] neg_hi:[0,1]
	v_pk_add_f16 v76, v127, v156 neg_lo:[0,1] neg_hi:[0,1]
	v_pk_add_f16 v77, v126, v157 neg_lo:[0,1] neg_hi:[0,1]
	v_exp_f16_sdwa v86, v74 dst_sel:WORD_0 dst_unused:UNUSED_PAD src0_sel:WORD_0
	v_exp_f16_sdwa v87, v75 dst_sel:WORD_0 dst_unused:UNUSED_PAD src0_sel:WORD_0
	v_exp_f16_sdwa v88, v76 dst_sel:WORD_0 dst_unused:UNUSED_PAD src0_sel:WORD_0
	v_exp_f16_sdwa v89, v77 dst_sel:WORD_0 dst_unused:UNUSED_PAD src0_sel:WORD_0
	v_exp_f16_sdwa v86, v74 dst_sel:WORD_1 dst_unused:UNUSED_PRESERVE src0_sel:WORD_1
	v_exp_f16_sdwa v87, v75 dst_sel:WORD_1 dst_unused:UNUSED_PRESERVE src0_sel:WORD_1
	v_exp_f16_sdwa v88, v76 dst_sel:WORD_1 dst_unused:UNUSED_PRESERVE src0_sel:WORD_1
	v_exp_f16_sdwa v89, v77 dst_sel:WORD_1 dst_unused:UNUSED_PRESERVE src0_sel:WORD_1
	v_pk_add_f16 v74, v98, v154 neg_lo:[0,1] neg_hi:[0,1]
	v_pk_add_f16 v69, v69, v86
	v_pk_add_f16 v66, v66, v89
	v_pk_add_f16 v67, v67, v88
	v_pk_add_f16 v68, v68, v87
	v_pk_fma_f16 v49, v37, v89, v49
	v_pk_fma_f16 v48, v36, v88, v48
	v_pk_fma_f16 v47, v35, v87, v47
	v_pk_fma_f16 v46, v34, v86, v46
	v_pk_add_f16 v75, v99, v155 neg_lo:[0,1] neg_hi:[0,1]
	v_pk_add_f16 v76, v100, v156 neg_lo:[0,1] neg_hi:[0,1]
	v_pk_add_f16 v77, v101, v157 neg_lo:[0,1] neg_hi:[0,1]
	v_exp_f16_sdwa v86, v74 dst_sel:WORD_0 dst_unused:UNUSED_PAD src0_sel:WORD_0
	v_exp_f16_sdwa v87, v75 dst_sel:WORD_0 dst_unused:UNUSED_PAD src0_sel:WORD_0
	v_exp_f16_sdwa v88, v76 dst_sel:WORD_0 dst_unused:UNUSED_PAD src0_sel:WORD_0
	v_exp_f16_sdwa v89, v77 dst_sel:WORD_0 dst_unused:UNUSED_PAD src0_sel:WORD_0
	v_exp_f16_sdwa v86, v74 dst_sel:WORD_1 dst_unused:UNUSED_PRESERVE src0_sel:WORD_1
	v_exp_f16_sdwa v87, v75 dst_sel:WORD_1 dst_unused:UNUSED_PRESERVE src0_sel:WORD_1
	v_exp_f16_sdwa v88, v76 dst_sel:WORD_1 dst_unused:UNUSED_PRESERVE src0_sel:WORD_1
	v_exp_f16_sdwa v89, v77 dst_sel:WORD_1 dst_unused:UNUSED_PRESERVE src0_sel:WORD_1
	v_pk_add_f16 v74, v133, v154 neg_lo:[0,1] neg_hi:[0,1]
	v_pk_add_f16 v69, v69, v86
	v_pk_add_f16 v68, v68, v87
	v_pk_add_f16 v67, v67, v88
	v_pk_add_f16 v66, v66, v89
	v_pk_fma_f16 v46, v50, v86, v46
	v_pk_fma_f16 v47, v51, v87, v47
	v_pk_fma_f16 v48, v52, v88, v48
	v_pk_fma_f16 v49, v53, v89, v49
	v_pk_add_f16 v75, v132, v155 neg_lo:[0,1] neg_hi:[0,1]
	v_pk_add_f16 v76, v131, v156 neg_lo:[0,1] neg_hi:[0,1]
	v_pk_add_f16 v77, v130, v157 neg_lo:[0,1] neg_hi:[0,1]
	v_exp_f16_sdwa v86, v74 dst_sel:WORD_0 dst_unused:UNUSED_PAD src0_sel:WORD_0
	v_exp_f16_sdwa v87, v75 dst_sel:WORD_0 dst_unused:UNUSED_PAD src0_sel:WORD_0
	v_exp_f16_sdwa v88, v76 dst_sel:WORD_0 dst_unused:UNUSED_PAD src0_sel:WORD_0
	v_exp_f16_sdwa v89, v77 dst_sel:WORD_0 dst_unused:UNUSED_PAD src0_sel:WORD_0
	v_exp_f16_sdwa v86, v74 dst_sel:WORD_1 dst_unused:UNUSED_PRESERVE src0_sel:WORD_1
	v_exp_f16_sdwa v87, v75 dst_sel:WORD_1 dst_unused:UNUSED_PRESERVE src0_sel:WORD_1
	v_exp_f16_sdwa v88, v76 dst_sel:WORD_1 dst_unused:UNUSED_PRESERVE src0_sel:WORD_1
	v_exp_f16_sdwa v89, v77 dst_sel:WORD_1 dst_unused:UNUSED_PRESERVE src0_sel:WORD_1
	v_pk_add_f16 v74, v164, v154 neg_lo:[0,1] neg_hi:[0,1]
	v_pk_add_f16 v69, v69, v86
	v_pk_add_f16 v66, v66, v89
	v_pk_add_f16 v67, v67, v88
	v_pk_add_f16 v68, v68, v87
	v_pk_fma_f16 v49, v13, v89, v49
	v_pk_fma_f16 v48, v12, v88, v48
	v_pk_fma_f16 v47, v11, v87, v47
	v_pk_fma_f16 v46, v10, v86, v46
	v_pk_add_f16 v75, v163, v155 neg_lo:[0,1] neg_hi:[0,1]
	v_pk_add_f16 v76, v162, v156 neg_lo:[0,1] neg_hi:[0,1]
	v_pk_add_f16 v77, v161, v157 neg_lo:[0,1] neg_hi:[0,1]
	v_exp_f16_sdwa v86, v74 dst_sel:WORD_0 dst_unused:UNUSED_PAD src0_sel:WORD_0
	v_exp_f16_sdwa v87, v75 dst_sel:WORD_0 dst_unused:UNUSED_PAD src0_sel:WORD_0
	v_exp_f16_sdwa v88, v76 dst_sel:WORD_0 dst_unused:UNUSED_PAD src0_sel:WORD_0
	v_exp_f16_sdwa v89, v77 dst_sel:WORD_0 dst_unused:UNUSED_PAD src0_sel:WORD_0
	v_exp_f16_sdwa v86, v74 dst_sel:WORD_1 dst_unused:UNUSED_PRESERVE src0_sel:WORD_1
	v_exp_f16_sdwa v87, v75 dst_sel:WORD_1 dst_unused:UNUSED_PRESERVE src0_sel:WORD_1
	v_exp_f16_sdwa v88, v76 dst_sel:WORD_1 dst_unused:UNUSED_PRESERVE src0_sel:WORD_1
	v_exp_f16_sdwa v89, v77 dst_sel:WORD_1 dst_unused:UNUSED_PRESERVE src0_sel:WORD_1
	v_pk_add_f16 v74, v114, v154 neg_lo:[0,1] neg_hi:[0,1]
	v_pk_add_f16 v69, v69, v86
	v_pk_add_f16 v68, v68, v87
	v_pk_add_f16 v67, v67, v88
	v_pk_add_f16 v66, v66, v89
	v_pk_fma_f16 v46, v14, v86, v46
	v_pk_fma_f16 v47, v15, v87, v47
	v_pk_fma_f16 v48, v16, v88, v48
	v_pk_fma_f16 v49, v17, v89, v49
	v_pk_add_f16 v75, v115, v155 neg_lo:[0,1] neg_hi:[0,1]
	v_pk_add_f16 v76, v116, v156 neg_lo:[0,1] neg_hi:[0,1]
	v_pk_add_f16 v77, v117, v157 neg_lo:[0,1] neg_hi:[0,1]
	v_exp_f16_sdwa v86, v74 dst_sel:WORD_0 dst_unused:UNUSED_PAD src0_sel:WORD_0
	v_exp_f16_sdwa v87, v75 dst_sel:WORD_0 dst_unused:UNUSED_PAD src0_sel:WORD_0
	v_exp_f16_sdwa v88, v76 dst_sel:WORD_0 dst_unused:UNUSED_PAD src0_sel:WORD_0
	v_exp_f16_sdwa v89, v77 dst_sel:WORD_0 dst_unused:UNUSED_PAD src0_sel:WORD_0
	v_exp_f16_sdwa v86, v74 dst_sel:WORD_1 dst_unused:UNUSED_PRESERVE src0_sel:WORD_1
	v_exp_f16_sdwa v87, v75 dst_sel:WORD_1 dst_unused:UNUSED_PRESERVE src0_sel:WORD_1
	v_exp_f16_sdwa v88, v76 dst_sel:WORD_1 dst_unused:UNUSED_PRESERVE src0_sel:WORD_1
	v_exp_f16_sdwa v89, v77 dst_sel:WORD_1 dst_unused:UNUSED_PRESERVE src0_sel:WORD_1
	v_pk_add_f16 v69, v69, v86
	v_pk_add_f16 v68, v68, v87
	v_rcp_f16_e32 v74, v69
	v_rcp_f16_sdwa v69, v69 dst_sel:DWORD dst_unused:UNUSED_PAD src0_sel:WORD_1
	v_pk_add_f16 v67, v67, v88
	v_rcp_f16_e32 v75, v68
	v_rcp_f16_sdwa v68, v68 dst_sel:DWORD dst_unused:UNUSED_PAD src0_sel:WORD_1
	v_pk_add_f16 v66, v66, v89
	v_pk_fma_f16 v46, v18, v86, v46
	v_rcp_f16_e32 v86, v67
	v_rcp_f16_sdwa v67, v67 dst_sel:DWORD dst_unused:UNUSED_PAD src0_sel:WORD_1
	v_pk_fma_f16 v47, v19, v87, v47
	v_rcp_f16_e32 v87, v66
	v_rcp_f16_sdwa v66, v66 dst_sel:DWORD dst_unused:UNUSED_PAD src0_sel:WORD_1
	v_pack_b32_f16 v69, v74, v69
	v_pk_mul_f16 v77, v46, v69
	v_pack_b32_f16 v46, v75, v68
	v_pk_fma_f16 v48, v20, v88, v48
	v_pk_mul_f16 v76, v47, v46
	v_pack_b32_f16 v46, v86, v67
	v_pk_fma_f16 v49, v21, v89, v49
	v_pk_mul_f16 v75, v48, v46
	v_pack_b32_f16 v46, v87, v66
	v_pk_mul_f16 v74, v49, v46
	s_waitcnt vmcnt(6)
	v_pk_mul_f16 v49, v160, v153 op_sel_hi:[0,1]
	v_pk_mul_f16 v46, v160, v150 op_sel_hi:[0,1]
	v_pk_mul_f16 v47, v160, v151 op_sel_hi:[0,1]
	v_pk_mul_f16 v48, v160, v152 op_sel_hi:[0,1]
	v_pk_mul_f16 v69, v158, v153 op_sel_hi:[0,1]
	v_pk_mul_f16 v89, v159, v153 op_sel_hi:[0,1]
	v_pk_fma_f16 v57, v57, v153, v49
	v_pk_fma_f16 v73, v73, v153, v49
	v_pk_fma_f16 v49, v97, v153, v49
	v_pk_mul_f16 v66, v158, v150 op_sel_hi:[0,1]
	v_pk_maximum3_f16 v117, v57, v73, v49
	v_pk_mul_f16 v67, v158, v151 op_sel_hi:[0,1]
	v_pk_mul_f16 v68, v158, v152 op_sel_hi:[0,1]
	v_pk_mul_f16 v86, v159, v150 op_sel_hi:[0,1]
	v_pk_mul_f16 v87, v159, v151 op_sel_hi:[0,1]
	v_pk_mul_f16 v88, v159, v152 op_sel_hi:[0,1]
	v_pk_fma_f16 v56, v56, v152, v48
	v_pk_fma_f16 v55, v55, v151, v47
	v_pk_fma_f16 v54, v54, v150, v46
	v_pk_fma_f16 v72, v72, v152, v48
	v_pk_fma_f16 v71, v71, v151, v47
	v_pk_fma_f16 v70, v70, v150, v46
	v_pk_fma_f16 v48, v96, v152, v48
	v_pk_fma_f16 v47, v95, v151, v47
	v_pk_fma_f16 v46, v94, v150, v46
	v_pk_fma_f16 v90, v29, v153, v69
	v_pk_fma_f16 v94, v41, v153, v69
	v_pk_fma_f16 v69, v61, v153, v69
	v_pk_fma_f16 v98, v81, v153, v89
	v_pk_fma_f16 v110, v109, v153, v89
	v_pk_fma_f16 v89, v125, v153, v89
	v_pk_maximum3_f16 v114, v54, v70, v46
	v_pk_maximum3_f16 v115, v55, v71, v47
	v_pk_maximum3_f16 v116, v56, v72, v48
	v_pk_maximum3_f16 v121, v90, v94, v69
	v_pk_fma_f16 v91, v28, v152, v68
	v_pk_maximum3_f16 v129, v98, v110, v89
	v_pk_fma_f16 v92, v27, v151, v67
	v_pk_maximum3_f16 v117, v117, v121, v129
	v_pk_fma_f16 v93, v26, v150, v66
	v_pk_fma_f16 v95, v40, v152, v68
	v_pk_fma_f16 v96, v39, v151, v67
	v_pk_fma_f16 v97, v38, v150, v66
	v_pk_fma_f16 v68, v60, v152, v68
	v_pk_fma_f16 v67, v59, v151, v67
	v_pk_fma_f16 v66, v58, v150, v66
	v_pk_fma_f16 v99, v80, v152, v88
	v_pk_fma_f16 v100, v79, v151, v87
	v_pk_fma_f16 v101, v78, v150, v86
	v_pk_fma_f16 v111, v108, v152, v88
	v_pk_fma_f16 v112, v107, v151, v87
	v_pk_fma_f16 v113, v106, v150, v86
	v_pk_fma_f16 v88, v124, v152, v88
	v_pk_fma_f16 v87, v123, v151, v87
	v_pk_fma_f16 v86, v122, v150, v86
	v_pk_maximum3_f16 v118, v93, v97, v66
	v_pk_maximum3_f16 v119, v92, v96, v67
	v_pk_maximum3_f16 v120, v91, v95, v68
	v_pk_maximum3_f16 v127, v100, v112, v87
	v_pk_maximum3_f16 v128, v99, v111, v88
	v_pk_maximum3_f16 v126, v101, v113, v86
	v_pk_maximum3_f16 v114, v114, v118, v126
	v_pk_maximum3_f16 v115, v115, v119, v127
	v_pk_maximum3_f16 v116, v116, v120, v128
	v_pk_add_f16 v57, v57, v117 neg_lo:[0,1] neg_hi:[0,1]
	v_pk_add_f16 v54, v54, v114 neg_lo:[0,1] neg_hi:[0,1]
	v_pk_add_f16 v55, v55, v115 neg_lo:[0,1] neg_hi:[0,1]
	v_pk_add_f16 v56, v56, v116 neg_lo:[0,1] neg_hi:[0,1]
	v_pk_add_f16 v70, v70, v114 neg_lo:[0,1] neg_hi:[0,1]
	v_exp_f16_sdwa v118, v54 dst_sel:WORD_0 dst_unused:UNUSED_PAD src0_sel:WORD_0
	v_exp_f16_sdwa v119, v55 dst_sel:WORD_0 dst_unused:UNUSED_PAD src0_sel:WORD_0
	v_exp_f16_sdwa v120, v56 dst_sel:WORD_0 dst_unused:UNUSED_PAD src0_sel:WORD_0
	v_exp_f16_sdwa v121, v57 dst_sel:WORD_0 dst_unused:UNUSED_PAD src0_sel:WORD_0
	v_exp_f16_sdwa v118, v54 dst_sel:WORD_1 dst_unused:UNUSED_PRESERVE src0_sel:WORD_1
	v_exp_f16_sdwa v119, v55 dst_sel:WORD_1 dst_unused:UNUSED_PRESERVE src0_sel:WORD_1
	v_exp_f16_sdwa v120, v56 dst_sel:WORD_1 dst_unused:UNUSED_PRESERVE src0_sel:WORD_1
	v_exp_f16_sdwa v121, v57 dst_sel:WORD_1 dst_unused:UNUSED_PRESERVE src0_sel:WORD_1
	v_pk_add_f16 v71, v71, v115 neg_lo:[0,1] neg_hi:[0,1]
	v_pk_add_f16 v57, v118, 0
	v_pk_fma_f16 v25, v25, v121, 0
	v_pk_add_f16 v54, v121, 0
	v_pk_add_f16 v55, v120, 0
	v_pk_add_f16 v56, v119, 0
	v_pk_fma_f16 v24, v24, v120, 0
	v_pk_fma_f16 v23, v23, v119, 0
	v_pk_fma_f16 v22, v22, v118, 0
	v_pk_add_f16 v72, v72, v116 neg_lo:[0,1] neg_hi:[0,1]
	v_pk_add_f16 v73, v73, v117 neg_lo:[0,1] neg_hi:[0,1]
	v_exp_f16_sdwa v118, v70 dst_sel:WORD_0 dst_unused:UNUSED_PAD src0_sel:WORD_0
	v_exp_f16_sdwa v119, v71 dst_sel:WORD_0 dst_unused:UNUSED_PAD src0_sel:WORD_0
	v_exp_f16_sdwa v120, v72 dst_sel:WORD_0 dst_unused:UNUSED_PAD src0_sel:WORD_0
	v_exp_f16_sdwa v121, v73 dst_sel:WORD_0 dst_unused:UNUSED_PAD src0_sel:WORD_0
	v_exp_f16_sdwa v118, v70 dst_sel:WORD_1 dst_unused:UNUSED_PRESERVE src0_sel:WORD_1
	v_exp_f16_sdwa v119, v71 dst_sel:WORD_1 dst_unused:UNUSED_PRESERVE src0_sel:WORD_1
	v_exp_f16_sdwa v120, v72 dst_sel:WORD_1 dst_unused:UNUSED_PRESERVE src0_sel:WORD_1
	v_exp_f16_sdwa v121, v73 dst_sel:WORD_1 dst_unused:UNUSED_PRESERVE src0_sel:WORD_1
	v_pk_add_f16 v57, v57, v118
	v_pk_fma_f16 v25, v37, v121, v25
	v_pk_add_f16 v37, v49, v117 neg_lo:[0,1] neg_hi:[0,1]
	v_pk_add_f16 v56, v56, v119
	v_pk_add_f16 v55, v55, v120
	v_pk_add_f16 v54, v54, v121
	v_pk_fma_f16 v22, v34, v118, v22
	v_pk_fma_f16 v23, v35, v119, v23
	v_pk_fma_f16 v24, v36, v120, v24
	v_pk_add_f16 v34, v46, v114 neg_lo:[0,1] neg_hi:[0,1]
	v_pk_add_f16 v35, v47, v115 neg_lo:[0,1] neg_hi:[0,1]
	v_pk_add_f16 v36, v48, v116 neg_lo:[0,1] neg_hi:[0,1]
	v_exp_f16_sdwa v46, v34 dst_sel:WORD_0 dst_unused:UNUSED_PAD src0_sel:WORD_0
	v_exp_f16_sdwa v47, v35 dst_sel:WORD_0 dst_unused:UNUSED_PAD src0_sel:WORD_0
	v_exp_f16_sdwa v48, v36 dst_sel:WORD_0 dst_unused:UNUSED_PAD src0_sel:WORD_0
	v_exp_f16_sdwa v49, v37 dst_sel:WORD_0 dst_unused:UNUSED_PAD src0_sel:WORD_0
	v_exp_f16_sdwa v46, v34 dst_sel:WORD_1 dst_unused:UNUSED_PRESERVE src0_sel:WORD_1
	v_exp_f16_sdwa v47, v35 dst_sel:WORD_1 dst_unused:UNUSED_PRESERVE src0_sel:WORD_1
	v_exp_f16_sdwa v48, v36 dst_sel:WORD_1 dst_unused:UNUSED_PRESERVE src0_sel:WORD_1
	v_exp_f16_sdwa v49, v37 dst_sel:WORD_1 dst_unused:UNUSED_PRESERVE src0_sel:WORD_1
	v_pk_add_f16 v37, v57, v46
	v_pk_add_f16 v34, v54, v49
	v_pk_add_f16 v35, v55, v48
	v_pk_add_f16 v36, v56, v47
	v_pk_fma_f16 v25, v53, v49, v25
	v_pk_fma_f16 v24, v52, v48, v24
	v_pk_fma_f16 v23, v51, v47, v23
	v_pk_fma_f16 v22, v50, v46, v22
	v_pk_add_f16 v46, v93, v114 neg_lo:[0,1] neg_hi:[0,1]
	v_pk_add_f16 v47, v92, v115 neg_lo:[0,1] neg_hi:[0,1]
	v_pk_add_f16 v48, v91, v116 neg_lo:[0,1] neg_hi:[0,1]
	v_pk_add_f16 v49, v90, v117 neg_lo:[0,1] neg_hi:[0,1]
	v_exp_f16_sdwa v50, v46 dst_sel:WORD_0 dst_unused:UNUSED_PAD src0_sel:WORD_0
	v_exp_f16_sdwa v51, v47 dst_sel:WORD_0 dst_unused:UNUSED_PAD src0_sel:WORD_0
	v_exp_f16_sdwa v52, v48 dst_sel:WORD_0 dst_unused:UNUSED_PAD src0_sel:WORD_0
	v_exp_f16_sdwa v53, v49 dst_sel:WORD_0 dst_unused:UNUSED_PAD src0_sel:WORD_0
	v_exp_f16_sdwa v50, v46 dst_sel:WORD_1 dst_unused:UNUSED_PRESERVE src0_sel:WORD_1
	v_exp_f16_sdwa v51, v47 dst_sel:WORD_1 dst_unused:UNUSED_PRESERVE src0_sel:WORD_1
	v_exp_f16_sdwa v52, v48 dst_sel:WORD_1 dst_unused:UNUSED_PRESERVE src0_sel:WORD_1
	v_exp_f16_sdwa v53, v49 dst_sel:WORD_1 dst_unused:UNUSED_PRESERVE src0_sel:WORD_1
	v_pk_add_f16 v46, v97, v114 neg_lo:[0,1] neg_hi:[0,1]
	v_pk_add_f16 v37, v37, v50
	v_pk_add_f16 v36, v36, v51
	v_pk_add_f16 v35, v35, v52
	v_pk_add_f16 v34, v34, v53
	v_pk_fma_f16 v22, v10, v50, v22
	v_pk_fma_f16 v23, v11, v51, v23
	v_pk_fma_f16 v24, v12, v52, v24
	v_pk_fma_f16 v25, v13, v53, v25
	v_pk_add_f16 v47, v96, v115 neg_lo:[0,1] neg_hi:[0,1]
	v_pk_add_f16 v48, v95, v116 neg_lo:[0,1] neg_hi:[0,1]
	v_pk_add_f16 v49, v94, v117 neg_lo:[0,1] neg_hi:[0,1]
	v_exp_f16_sdwa v50, v46 dst_sel:WORD_0 dst_unused:UNUSED_PAD src0_sel:WORD_0
	v_exp_f16_sdwa v51, v47 dst_sel:WORD_0 dst_unused:UNUSED_PAD src0_sel:WORD_0
	v_exp_f16_sdwa v52, v48 dst_sel:WORD_0 dst_unused:UNUSED_PAD src0_sel:WORD_0
	v_exp_f16_sdwa v53, v49 dst_sel:WORD_0 dst_unused:UNUSED_PAD src0_sel:WORD_0
	v_exp_f16_sdwa v50, v46 dst_sel:WORD_1 dst_unused:UNUSED_PRESERVE src0_sel:WORD_1
	v_exp_f16_sdwa v51, v47 dst_sel:WORD_1 dst_unused:UNUSED_PRESERVE src0_sel:WORD_1
	v_exp_f16_sdwa v52, v48 dst_sel:WORD_1 dst_unused:UNUSED_PRESERVE src0_sel:WORD_1
	v_exp_f16_sdwa v53, v49 dst_sel:WORD_1 dst_unused:UNUSED_PRESERVE src0_sel:WORD_1
	v_pk_add_f16 v46, v66, v114 neg_lo:[0,1] neg_hi:[0,1]
	v_pk_add_f16 v37, v37, v50
	v_pk_add_f16 v34, v34, v53
	v_pk_add_f16 v35, v35, v52
	v_pk_add_f16 v36, v36, v51
	v_pk_fma_f16 v25, v17, v53, v25
	v_pk_fma_f16 v24, v16, v52, v24
	v_pk_fma_f16 v23, v15, v51, v23
	v_pk_fma_f16 v22, v14, v50, v22
	v_pk_add_f16 v47, v67, v115 neg_lo:[0,1] neg_hi:[0,1]
	v_pk_add_f16 v48, v68, v116 neg_lo:[0,1] neg_hi:[0,1]
	v_pk_add_f16 v49, v69, v117 neg_lo:[0,1] neg_hi:[0,1]
	v_exp_f16_sdwa v50, v46 dst_sel:WORD_0 dst_unused:UNUSED_PAD src0_sel:WORD_0
	v_exp_f16_sdwa v51, v47 dst_sel:WORD_0 dst_unused:UNUSED_PAD src0_sel:WORD_0
	v_exp_f16_sdwa v52, v48 dst_sel:WORD_0 dst_unused:UNUSED_PAD src0_sel:WORD_0
	v_exp_f16_sdwa v53, v49 dst_sel:WORD_0 dst_unused:UNUSED_PAD src0_sel:WORD_0
	v_exp_f16_sdwa v50, v46 dst_sel:WORD_1 dst_unused:UNUSED_PRESERVE src0_sel:WORD_1
	v_exp_f16_sdwa v51, v47 dst_sel:WORD_1 dst_unused:UNUSED_PRESERVE src0_sel:WORD_1
	v_exp_f16_sdwa v52, v48 dst_sel:WORD_1 dst_unused:UNUSED_PRESERVE src0_sel:WORD_1
	v_exp_f16_sdwa v53, v49 dst_sel:WORD_1 dst_unused:UNUSED_PRESERVE src0_sel:WORD_1
	v_pk_add_f16 v46, v101, v114 neg_lo:[0,1] neg_hi:[0,1]
	v_pk_add_f16 v37, v37, v50
	v_pk_add_f16 v36, v36, v51
	v_pk_add_f16 v35, v35, v52
	v_pk_add_f16 v34, v34, v53
	v_pk_fma_f16 v22, v18, v50, v22
	v_pk_fma_f16 v23, v19, v51, v23
	v_pk_fma_f16 v24, v20, v52, v24
	v_pk_fma_f16 v25, v21, v53, v25
	v_pk_add_f16 v47, v100, v115 neg_lo:[0,1] neg_hi:[0,1]
	v_pk_add_f16 v48, v99, v116 neg_lo:[0,1] neg_hi:[0,1]
	v_pk_add_f16 v49, v98, v117 neg_lo:[0,1] neg_hi:[0,1]
	v_exp_f16_sdwa v50, v46 dst_sel:WORD_0 dst_unused:UNUSED_PAD src0_sel:WORD_0
	v_exp_f16_sdwa v51, v47 dst_sel:WORD_0 dst_unused:UNUSED_PAD src0_sel:WORD_0
	v_exp_f16_sdwa v52, v48 dst_sel:WORD_0 dst_unused:UNUSED_PAD src0_sel:WORD_0
	v_exp_f16_sdwa v53, v49 dst_sel:WORD_0 dst_unused:UNUSED_PAD src0_sel:WORD_0
	v_exp_f16_sdwa v50, v46 dst_sel:WORD_1 dst_unused:UNUSED_PRESERVE src0_sel:WORD_1
	v_exp_f16_sdwa v51, v47 dst_sel:WORD_1 dst_unused:UNUSED_PRESERVE src0_sel:WORD_1
	v_exp_f16_sdwa v52, v48 dst_sel:WORD_1 dst_unused:UNUSED_PRESERVE src0_sel:WORD_1
	v_exp_f16_sdwa v53, v49 dst_sel:WORD_1 dst_unused:UNUSED_PRESERVE src0_sel:WORD_1
	v_pk_add_f16 v46, v113, v114 neg_lo:[0,1] neg_hi:[0,1]
	v_pk_add_f16 v37, v37, v50
	v_pk_add_f16 v34, v34, v53
	v_pk_add_f16 v35, v35, v52
	v_pk_add_f16 v36, v36, v51
	v_pk_fma_f16 v25, v33, v53, v25
	v_pk_fma_f16 v24, v32, v52, v24
	v_pk_fma_f16 v23, v31, v51, v23
	v_pk_fma_f16 v22, v30, v50, v22
	v_pk_add_f16 v47, v112, v115 neg_lo:[0,1] neg_hi:[0,1]
	v_pk_add_f16 v48, v111, v116 neg_lo:[0,1] neg_hi:[0,1]
	v_pk_add_f16 v49, v110, v117 neg_lo:[0,1] neg_hi:[0,1]
	v_exp_f16_sdwa v50, v46 dst_sel:WORD_0 dst_unused:UNUSED_PAD src0_sel:WORD_0
	v_exp_f16_sdwa v51, v47 dst_sel:WORD_0 dst_unused:UNUSED_PAD src0_sel:WORD_0
	v_exp_f16_sdwa v52, v48 dst_sel:WORD_0 dst_unused:UNUSED_PAD src0_sel:WORD_0
	v_exp_f16_sdwa v53, v49 dst_sel:WORD_0 dst_unused:UNUSED_PAD src0_sel:WORD_0
	v_exp_f16_sdwa v50, v46 dst_sel:WORD_1 dst_unused:UNUSED_PRESERVE src0_sel:WORD_1
	v_exp_f16_sdwa v51, v47 dst_sel:WORD_1 dst_unused:UNUSED_PRESERVE src0_sel:WORD_1
	v_exp_f16_sdwa v52, v48 dst_sel:WORD_1 dst_unused:UNUSED_PRESERVE src0_sel:WORD_1
	v_exp_f16_sdwa v53, v49 dst_sel:WORD_1 dst_unused:UNUSED_PRESERVE src0_sel:WORD_1
	v_pk_add_f16 v46, v86, v114 neg_lo:[0,1] neg_hi:[0,1]
	v_pk_add_f16 v37, v37, v50
	v_pk_add_f16 v36, v36, v51
	v_pk_add_f16 v35, v35, v52
	v_pk_add_f16 v34, v34, v53
	v_pk_fma_f16 v22, v42, v50, v22
	v_pk_fma_f16 v23, v43, v51, v23
	v_pk_fma_f16 v24, v44, v52, v24
	v_pk_fma_f16 v25, v45, v53, v25
	v_pk_add_f16 v47, v87, v115 neg_lo:[0,1] neg_hi:[0,1]
	v_pk_add_f16 v48, v88, v116 neg_lo:[0,1] neg_hi:[0,1]
	v_pk_add_f16 v49, v89, v117 neg_lo:[0,1] neg_hi:[0,1]
	v_exp_f16_sdwa v50, v46 dst_sel:WORD_0 dst_unused:UNUSED_PAD src0_sel:WORD_0
	v_exp_f16_sdwa v51, v47 dst_sel:WORD_0 dst_unused:UNUSED_PAD src0_sel:WORD_0
	v_exp_f16_sdwa v52, v48 dst_sel:WORD_0 dst_unused:UNUSED_PAD src0_sel:WORD_0
	v_exp_f16_sdwa v53, v49 dst_sel:WORD_0 dst_unused:UNUSED_PAD src0_sel:WORD_0
	v_exp_f16_sdwa v50, v46 dst_sel:WORD_1 dst_unused:UNUSED_PRESERVE src0_sel:WORD_1
	v_exp_f16_sdwa v51, v47 dst_sel:WORD_1 dst_unused:UNUSED_PRESERVE src0_sel:WORD_1
	v_exp_f16_sdwa v52, v48 dst_sel:WORD_1 dst_unused:UNUSED_PRESERVE src0_sel:WORD_1
	v_exp_f16_sdwa v53, v49 dst_sel:WORD_1 dst_unused:UNUSED_PRESERVE src0_sel:WORD_1
	v_pk_add_f16 v37, v37, v50
	v_pk_add_f16 v36, v36, v51
	v_rcp_f16_e32 v46, v37
	v_rcp_f16_sdwa v37, v37 dst_sel:DWORD dst_unused:UNUSED_PAD src0_sel:WORD_1
	v_pk_add_f16 v35, v35, v52
	v_rcp_f16_e32 v47, v36
	v_rcp_f16_sdwa v36, v36 dst_sel:DWORD dst_unused:UNUSED_PAD src0_sel:WORD_1
	v_pk_add_f16 v34, v34, v53
	v_rcp_f16_e32 v48, v35
	v_rcp_f16_sdwa v35, v35 dst_sel:DWORD dst_unused:UNUSED_PAD src0_sel:WORD_1
	v_rcp_f16_e32 v49, v34
	v_rcp_f16_sdwa v34, v34 dst_sel:DWORD dst_unused:UNUSED_PAD src0_sel:WORD_1
	v_pk_fma_f16 v22, v62, v50, v22
	v_pack_b32_f16 v37, v46, v37
	v_pk_fma_f16 v23, v63, v51, v23
	v_pk_mul_f16 v57, v22, v37
	v_pack_b32_f16 v22, v47, v36
	v_pk_fma_f16 v24, v64, v52, v24
	v_pk_mul_f16 v56, v23, v22
	v_pack_b32_f16 v22, v48, v35
	v_pk_fma_f16 v25, v65, v53, v25
	v_pk_mul_f16 v55, v24, v22
	v_pack_b32_f16 v22, v49, v34
	v_pk_mul_f16 v54, v25, v22
	s_waitcnt vmcnt(0)
	v_pk_mul_f16 v22, v160, v146 op_sel_hi:[0,1]
	v_pk_mul_f16 v23, v160, v147 op_sel_hi:[0,1]
	v_pk_mul_f16 v24, v160, v148 op_sel_hi:[0,1]
	v_pk_mul_f16 v25, v160, v149 op_sel_hi:[0,1]
	v_pk_mul_f16 v46, v159, v146 op_sel_hi:[0,1]
	v_pk_mul_f16 v47, v159, v147 op_sel_hi:[0,1]
	v_pk_mul_f16 v48, v159, v148 op_sel_hi:[0,1]
	v_pk_mul_f16 v49, v159, v149 op_sel_hi:[0,1]
	v_pk_mul_f16 v34, v158, v146 op_sel_hi:[0,1]
	v_pk_mul_f16 v35, v158, v147 op_sel_hi:[0,1]
	v_pk_mul_f16 v36, v158, v148 op_sel_hi:[0,1]
	v_pk_mul_f16 v37, v158, v149 op_sel_hi:[0,1]
	v_pk_fma_f16 v29, v29, v149, v25
	v_pk_fma_f16 v28, v28, v148, v24
	v_pk_fma_f16 v27, v27, v147, v23
	v_pk_fma_f16 v26, v26, v146, v22
	v_pk_fma_f16 v41, v41, v149, v25
	v_pk_fma_f16 v40, v40, v148, v24
	v_pk_fma_f16 v39, v39, v147, v23
	v_pk_fma_f16 v38, v38, v146, v22
	v_pk_fma_f16 v25, v61, v149, v25
	v_pk_fma_f16 v24, v60, v148, v24
	v_pk_fma_f16 v23, v59, v147, v23
	v_pk_fma_f16 v22, v58, v146, v22
	v_pk_fma_f16 v66, v137, v149, v49
	v_pk_fma_f16 v67, v136, v148, v48
	v_pk_fma_f16 v68, v135, v147, v47
	v_pk_fma_f16 v69, v134, v146, v46
	v_pk_fma_f16 v70, v145, v149, v49
	v_pk_fma_f16 v71, v144, v148, v48
	v_pk_fma_f16 v72, v143, v147, v47
	v_pk_fma_f16 v73, v142, v146, v46
	v_pk_fma_f16 v9, v9, v149, v49
	v_pk_fma_f16 v8, v8, v148, v48
	v_pk_fma_f16 v7, v7, v147, v47
	v_pk_fma_f16 v6, v6, v146, v46
	v_pk_maximum3_f16 v46, v26, v38, v22
	v_pk_maximum3_f16 v47, v27, v39, v23
	v_pk_maximum3_f16 v48, v28, v40, v24
	v_pk_maximum3_f16 v49, v29, v41, v25
	v_pk_fma_f16 v50, v81, v149, v37
	v_pk_fma_f16 v51, v80, v148, v36
	v_pk_fma_f16 v52, v79, v147, v35
	v_pk_fma_f16 v53, v78, v146, v34
	v_pk_fma_f16 v58, v109, v149, v37
	v_pk_fma_f16 v59, v108, v148, v36
	v_pk_fma_f16 v60, v107, v147, v35
	v_pk_fma_f16 v61, v106, v146, v34
	v_pk_fma_f16 v37, v125, v149, v37
	v_pk_fma_f16 v36, v124, v148, v36
	v_pk_fma_f16 v35, v123, v147, v35
	v_pk_fma_f16 v34, v122, v146, v34
	v_pk_maximum3_f16 v79, v52, v60, v35
	v_pk_maximum3_f16 v80, v51, v59, v36
	v_pk_maximum3_f16 v81, v50, v58, v37
	v_pk_maximum3_f16 v86, v69, v73, v6
	v_pk_maximum3_f16 v87, v68, v72, v7
	v_pk_maximum3_f16 v78, v53, v61, v34
	v_pk_maximum3_f16 v88, v67, v71, v8
	v_pk_maximum3_f16 v89, v66, v70, v9
	v_pk_maximum3_f16 v46, v46, v78, v86
	v_pk_maximum3_f16 v47, v47, v79, v87
	v_pk_maximum3_f16 v48, v48, v80, v88
	v_pk_maximum3_f16 v49, v49, v81, v89
	s_nop 0
	v_pk_add_f16 v26, v26, v46 neg_lo:[0,1] neg_hi:[0,1]
	v_pk_add_f16 v27, v27, v47 neg_lo:[0,1] neg_hi:[0,1]
	v_pk_add_f16 v28, v28, v48 neg_lo:[0,1] neg_hi:[0,1]
	v_pk_add_f16 v29, v29, v49 neg_lo:[0,1] neg_hi:[0,1]
	v_pk_add_f16 v38, v38, v46 neg_lo:[0,1] neg_hi:[0,1]
	v_exp_f16_sdwa v78, v26 dst_sel:WORD_0 dst_unused:UNUSED_PAD src0_sel:WORD_0
	v_exp_f16_sdwa v79, v27 dst_sel:WORD_0 dst_unused:UNUSED_PAD src0_sel:WORD_0
	v_exp_f16_sdwa v80, v28 dst_sel:WORD_0 dst_unused:UNUSED_PAD src0_sel:WORD_0
	v_exp_f16_sdwa v81, v29 dst_sel:WORD_0 dst_unused:UNUSED_PAD src0_sel:WORD_0
	v_exp_f16_sdwa v78, v26 dst_sel:WORD_1 dst_unused:UNUSED_PRESERVE src0_sel:WORD_1
	v_exp_f16_sdwa v79, v27 dst_sel:WORD_1 dst_unused:UNUSED_PRESERVE src0_sel:WORD_1
	v_exp_f16_sdwa v80, v28 dst_sel:WORD_1 dst_unused:UNUSED_PRESERVE src0_sel:WORD_1
	v_exp_f16_sdwa v81, v29 dst_sel:WORD_1 dst_unused:UNUSED_PRESERVE src0_sel:WORD_1
	v_pk_add_f16 v39, v39, v47 neg_lo:[0,1] neg_hi:[0,1]
	v_pk_add_f16 v26, v78, 0
	v_pk_add_f16 v27, v79, 0
	v_pk_add_f16 v28, v80, 0
	v_pk_add_f16 v29, v81, 0
	v_pk_fma_f16 v10, v10, v78, 0
	v_pk_fma_f16 v11, v11, v79, 0
	v_pk_fma_f16 v12, v12, v80, 0
	v_pk_fma_f16 v13, v13, v81, 0
	v_pk_add_f16 v40, v40, v48 neg_lo:[0,1] neg_hi:[0,1]
	v_pk_add_f16 v41, v41, v49 neg_lo:[0,1] neg_hi:[0,1]
	v_pk_add_f16 v6, v6, v46 neg_lo:[0,1] neg_hi:[0,1]
	v_exp_f16_sdwa v78, v38 dst_sel:WORD_0 dst_unused:UNUSED_PAD src0_sel:WORD_0
	v_exp_f16_sdwa v79, v39 dst_sel:WORD_0 dst_unused:UNUSED_PAD src0_sel:WORD_0
	v_exp_f16_sdwa v80, v40 dst_sel:WORD_0 dst_unused:UNUSED_PAD src0_sel:WORD_0
	v_exp_f16_sdwa v81, v41 dst_sel:WORD_0 dst_unused:UNUSED_PAD src0_sel:WORD_0
	v_exp_f16_sdwa v78, v38 dst_sel:WORD_1 dst_unused:UNUSED_PRESERVE src0_sel:WORD_1
	v_exp_f16_sdwa v79, v39 dst_sel:WORD_1 dst_unused:UNUSED_PRESERVE src0_sel:WORD_1
	v_exp_f16_sdwa v80, v40 dst_sel:WORD_1 dst_unused:UNUSED_PRESERVE src0_sel:WORD_1
	v_exp_f16_sdwa v81, v41 dst_sel:WORD_1 dst_unused:UNUSED_PRESERVE src0_sel:WORD_1
	v_pk_add_f16 v7, v7, v47 neg_lo:[0,1] neg_hi:[0,1]
	v_pk_add_f16 v29, v29, v81
	v_pk_add_f16 v28, v28, v80
	v_pk_add_f16 v27, v27, v79
	v_pk_add_f16 v26, v26, v78
	v_pk_fma_f16 v13, v17, v81, v13
	v_pk_fma_f16 v12, v16, v80, v12
	v_pk_fma_f16 v11, v15, v79, v11
	v_pk_fma_f16 v10, v14, v78, v10
	v_pk_add_f16 v14, v22, v46 neg_lo:[0,1] neg_hi:[0,1]
	v_pk_add_f16 v15, v23, v47 neg_lo:[0,1] neg_hi:[0,1]
	v_pk_add_f16 v16, v24, v48 neg_lo:[0,1] neg_hi:[0,1]
	v_pk_add_f16 v17, v25, v49 neg_lo:[0,1] neg_hi:[0,1]
	v_pk_add_f16 v8, v8, v48 neg_lo:[0,1] neg_hi:[0,1]
	v_exp_f16_sdwa v22, v14 dst_sel:WORD_0 dst_unused:UNUSED_PAD src0_sel:WORD_0
	v_exp_f16_sdwa v23, v15 dst_sel:WORD_0 dst_unused:UNUSED_PAD src0_sel:WORD_0
	v_exp_f16_sdwa v24, v16 dst_sel:WORD_0 dst_unused:UNUSED_PAD src0_sel:WORD_0
	v_exp_f16_sdwa v25, v17 dst_sel:WORD_0 dst_unused:UNUSED_PAD src0_sel:WORD_0
	v_exp_f16_sdwa v22, v14 dst_sel:WORD_1 dst_unused:UNUSED_PRESERVE src0_sel:WORD_1
	v_exp_f16_sdwa v23, v15 dst_sel:WORD_1 dst_unused:UNUSED_PRESERVE src0_sel:WORD_1
	v_exp_f16_sdwa v24, v16 dst_sel:WORD_1 dst_unused:UNUSED_PRESERVE src0_sel:WORD_1
	v_exp_f16_sdwa v25, v17 dst_sel:WORD_1 dst_unused:UNUSED_PRESERVE src0_sel:WORD_1
	v_pk_add_f16 v9, v9, v49 neg_lo:[0,1] neg_hi:[0,1]
	v_pk_add_f16 v14, v26, v22
	v_pk_add_f16 v15, v27, v23
	v_pk_add_f16 v16, v28, v24
	v_pk_add_f16 v17, v29, v25
	v_pk_fma_f16 v10, v18, v22, v10
	v_pk_fma_f16 v11, v19, v23, v11
	v_pk_fma_f16 v12, v20, v24, v12
	v_pk_fma_f16 v13, v21, v25, v13
	v_pk_add_f16 v18, v53, v46 neg_lo:[0,1] neg_hi:[0,1]
	v_pk_add_f16 v19, v52, v47 neg_lo:[0,1] neg_hi:[0,1]
	v_pk_add_f16 v20, v51, v48 neg_lo:[0,1] neg_hi:[0,1]
	v_pk_add_f16 v21, v50, v49 neg_lo:[0,1] neg_hi:[0,1]
	v_exp_f16_sdwa v22, v18 dst_sel:WORD_0 dst_unused:UNUSED_PAD src0_sel:WORD_0
	v_exp_f16_sdwa v23, v19 dst_sel:WORD_0 dst_unused:UNUSED_PAD src0_sel:WORD_0
	v_exp_f16_sdwa v24, v20 dst_sel:WORD_0 dst_unused:UNUSED_PAD src0_sel:WORD_0
	v_exp_f16_sdwa v25, v21 dst_sel:WORD_0 dst_unused:UNUSED_PAD src0_sel:WORD_0
	v_exp_f16_sdwa v22, v18 dst_sel:WORD_1 dst_unused:UNUSED_PRESERVE src0_sel:WORD_1
	v_exp_f16_sdwa v23, v19 dst_sel:WORD_1 dst_unused:UNUSED_PRESERVE src0_sel:WORD_1
	v_exp_f16_sdwa v24, v20 dst_sel:WORD_1 dst_unused:UNUSED_PRESERVE src0_sel:WORD_1
	v_exp_f16_sdwa v25, v21 dst_sel:WORD_1 dst_unused:UNUSED_PRESERVE src0_sel:WORD_1
	v_pk_add_f16 v18, v61, v46 neg_lo:[0,1] neg_hi:[0,1]
	v_pk_add_f16 v17, v17, v25
	v_pk_add_f16 v16, v16, v24
	v_pk_add_f16 v15, v15, v23
	v_pk_add_f16 v14, v14, v22
	v_pk_fma_f16 v13, v33, v25, v13
	v_pk_fma_f16 v12, v32, v24, v12
	v_pk_fma_f16 v11, v31, v23, v11
	v_pk_fma_f16 v10, v30, v22, v10
	v_pk_add_f16 v19, v60, v47 neg_lo:[0,1] neg_hi:[0,1]
	v_pk_add_f16 v20, v59, v48 neg_lo:[0,1] neg_hi:[0,1]
	v_pk_add_f16 v21, v58, v49 neg_lo:[0,1] neg_hi:[0,1]
	v_exp_f16_sdwa v30, v6 dst_sel:WORD_0 dst_unused:UNUSED_PAD src0_sel:WORD_0
	v_exp_f16_sdwa v31, v7 dst_sel:WORD_0 dst_unused:UNUSED_PAD src0_sel:WORD_0
	v_exp_f16_sdwa v32, v8 dst_sel:WORD_0 dst_unused:UNUSED_PAD src0_sel:WORD_0
	v_exp_f16_sdwa v33, v9 dst_sel:WORD_0 dst_unused:UNUSED_PAD src0_sel:WORD_0
	v_exp_f16_sdwa v30, v6 dst_sel:WORD_1 dst_unused:UNUSED_PRESERVE src0_sel:WORD_1
	v_exp_f16_sdwa v31, v7 dst_sel:WORD_1 dst_unused:UNUSED_PRESERVE src0_sel:WORD_1
	v_exp_f16_sdwa v32, v8 dst_sel:WORD_1 dst_unused:UNUSED_PRESERVE src0_sel:WORD_1
	v_exp_f16_sdwa v33, v9 dst_sel:WORD_1 dst_unused:UNUSED_PRESERVE src0_sel:WORD_1
	v_exp_f16_sdwa v22, v18 dst_sel:WORD_0 dst_unused:UNUSED_PAD src0_sel:WORD_0
	v_exp_f16_sdwa v23, v19 dst_sel:WORD_0 dst_unused:UNUSED_PAD src0_sel:WORD_0
	v_exp_f16_sdwa v24, v20 dst_sel:WORD_0 dst_unused:UNUSED_PAD src0_sel:WORD_0
	v_exp_f16_sdwa v25, v21 dst_sel:WORD_0 dst_unused:UNUSED_PAD src0_sel:WORD_0
	v_exp_f16_sdwa v22, v18 dst_sel:WORD_1 dst_unused:UNUSED_PRESERVE src0_sel:WORD_1
	v_exp_f16_sdwa v23, v19 dst_sel:WORD_1 dst_unused:UNUSED_PRESERVE src0_sel:WORD_1
	v_exp_f16_sdwa v24, v20 dst_sel:WORD_1 dst_unused:UNUSED_PRESERVE src0_sel:WORD_1
	v_exp_f16_sdwa v25, v21 dst_sel:WORD_1 dst_unused:UNUSED_PRESERVE src0_sel:WORD_1
	v_pk_add_f16 v18, v34, v46 neg_lo:[0,1] neg_hi:[0,1]
	v_pk_add_f16 v14, v14, v22
	v_pk_add_f16 v15, v15, v23
	v_pk_add_f16 v16, v16, v24
	v_pk_add_f16 v17, v17, v25
	v_pk_fma_f16 v10, v42, v22, v10
	v_pk_fma_f16 v11, v43, v23, v11
	v_pk_fma_f16 v12, v44, v24, v12
	v_pk_fma_f16 v13, v45, v25, v13
	v_pk_add_f16 v19, v35, v47 neg_lo:[0,1] neg_hi:[0,1]
	v_pk_add_f16 v20, v36, v48 neg_lo:[0,1] neg_hi:[0,1]
	v_pk_add_f16 v21, v37, v49 neg_lo:[0,1] neg_hi:[0,1]
	v_exp_f16_sdwa v22, v18 dst_sel:WORD_0 dst_unused:UNUSED_PAD src0_sel:WORD_0
	v_exp_f16_sdwa v23, v19 dst_sel:WORD_0 dst_unused:UNUSED_PAD src0_sel:WORD_0
	v_exp_f16_sdwa v24, v20 dst_sel:WORD_0 dst_unused:UNUSED_PAD src0_sel:WORD_0
	v_exp_f16_sdwa v25, v21 dst_sel:WORD_0 dst_unused:UNUSED_PAD src0_sel:WORD_0
	v_exp_f16_sdwa v22, v18 dst_sel:WORD_1 dst_unused:UNUSED_PRESERVE src0_sel:WORD_1
	v_exp_f16_sdwa v23, v19 dst_sel:WORD_1 dst_unused:UNUSED_PRESERVE src0_sel:WORD_1
	v_exp_f16_sdwa v24, v20 dst_sel:WORD_1 dst_unused:UNUSED_PRESERVE src0_sel:WORD_1
	v_exp_f16_sdwa v25, v21 dst_sel:WORD_1 dst_unused:UNUSED_PRESERVE src0_sel:WORD_1
	v_pk_add_f16 v18, v69, v46 neg_lo:[0,1] neg_hi:[0,1]
	v_pk_add_f16 v17, v17, v25
	v_pk_add_f16 v16, v16, v24
	v_pk_add_f16 v15, v15, v23
	v_pk_add_f16 v14, v14, v22
	v_pk_fma_f16 v13, v65, v25, v13
	v_pk_fma_f16 v12, v64, v24, v12
	v_pk_fma_f16 v11, v63, v23, v11
	v_pk_fma_f16 v10, v62, v22, v10
	v_pk_add_f16 v19, v68, v47 neg_lo:[0,1] neg_hi:[0,1]
	v_pk_add_f16 v20, v67, v48 neg_lo:[0,1] neg_hi:[0,1]
	v_pk_add_f16 v21, v66, v49 neg_lo:[0,1] neg_hi:[0,1]
	v_exp_f16_sdwa v22, v18 dst_sel:WORD_0 dst_unused:UNUSED_PAD src0_sel:WORD_0
	v_exp_f16_sdwa v23, v19 dst_sel:WORD_0 dst_unused:UNUSED_PAD src0_sel:WORD_0
	v_exp_f16_sdwa v24, v20 dst_sel:WORD_0 dst_unused:UNUSED_PAD src0_sel:WORD_0
	v_exp_f16_sdwa v25, v21 dst_sel:WORD_0 dst_unused:UNUSED_PAD src0_sel:WORD_0
	v_exp_f16_sdwa v22, v18 dst_sel:WORD_1 dst_unused:UNUSED_PRESERVE src0_sel:WORD_1
	v_exp_f16_sdwa v23, v19 dst_sel:WORD_1 dst_unused:UNUSED_PRESERVE src0_sel:WORD_1
	v_exp_f16_sdwa v24, v20 dst_sel:WORD_1 dst_unused:UNUSED_PRESERVE src0_sel:WORD_1
	v_exp_f16_sdwa v25, v21 dst_sel:WORD_1 dst_unused:UNUSED_PRESERVE src0_sel:WORD_1
	v_pk_add_f16 v18, v73, v46 neg_lo:[0,1] neg_hi:[0,1]
	v_pk_add_f16 v14, v14, v22
	v_pk_add_f16 v15, v15, v23
	v_pk_add_f16 v16, v16, v24
	v_pk_add_f16 v17, v17, v25
	v_pk_fma_f16 v10, v82, v22, v10
	v_pk_fma_f16 v11, v83, v23, v11
	v_pk_fma_f16 v12, v84, v24, v12
	v_pk_fma_f16 v13, v85, v25, v13
	v_pk_add_f16 v19, v72, v47 neg_lo:[0,1] neg_hi:[0,1]
	v_pk_add_f16 v20, v71, v48 neg_lo:[0,1] neg_hi:[0,1]
	v_pk_add_f16 v21, v70, v49 neg_lo:[0,1] neg_hi:[0,1]
	v_exp_f16_sdwa v22, v18 dst_sel:WORD_0 dst_unused:UNUSED_PAD src0_sel:WORD_0
	v_exp_f16_sdwa v23, v19 dst_sel:WORD_0 dst_unused:UNUSED_PAD src0_sel:WORD_0
	v_exp_f16_sdwa v24, v20 dst_sel:WORD_0 dst_unused:UNUSED_PAD src0_sel:WORD_0
	v_exp_f16_sdwa v25, v21 dst_sel:WORD_0 dst_unused:UNUSED_PAD src0_sel:WORD_0
	v_exp_f16_sdwa v22, v18 dst_sel:WORD_1 dst_unused:UNUSED_PRESERVE src0_sel:WORD_1
	v_exp_f16_sdwa v23, v19 dst_sel:WORD_1 dst_unused:UNUSED_PRESERVE src0_sel:WORD_1
	v_exp_f16_sdwa v24, v20 dst_sel:WORD_1 dst_unused:UNUSED_PRESERVE src0_sel:WORD_1
	v_exp_f16_sdwa v25, v21 dst_sel:WORD_1 dst_unused:UNUSED_PRESERVE src0_sel:WORD_1
	s_nop 0
	v_pk_add_f16 v17, v17, v25
	v_pk_add_f16 v16, v16, v24
	v_pk_add_f16 v15, v15, v23
	v_pk_add_f16 v14, v14, v22
	v_pk_fma_f16 v21, v105, v25, v13
	v_pk_fma_f16 v20, v104, v24, v12
	v_pk_fma_f16 v19, v103, v23, v11
	v_pk_fma_f16 v18, v102, v22, v10
	v_mov_b32_e32 v13, v5
	v_mov_b32_e32 v12, v4
	v_mov_b32_e32 v11, v3
	v_mov_b32_e32 v10, v2
.LBB4_80:
	v_lshlrev_b64 v[6:7], 9, v[168:169]
	v_or_b32_e32 v6, v6, v198
	v_lshl_add_u64 v[2:3], s[20:21], 0, v[6:7]
	global_load_dwordx4 v[2:5], v[2:3], off nt
	v_lshl_add_u64 v[6:7], s[22:23], 0, v[6:7]
	global_load_dwordx4 v[6:9], v[6:7], off nt
	v_add_u32_e32 v168, v185, v199
	v_lshlrev_b64 v[26:27], 9, v[168:169]
	v_or_b32_e32 v26, v26, v198
	v_lshl_add_u64 v[22:23], s[20:21], 0, v[26:27]
	global_load_dwordx4 v[22:25], v[22:23], off nt
	v_lshl_add_u64 v[26:27], s[22:23], 0, v[26:27]
	global_load_dwordx4 v[26:29], v[26:27], off nt
	v_pk_add_f16 v17, v17, v33
	v_pk_add_f16 v16, v16, v32
	v_pk_add_f16 v15, v15, v31
	v_pk_add_f16 v14, v14, v30
	v_pk_fma_f16 v42, v13, v33, v21
	v_pk_fma_f16 v43, v12, v32, v20
	v_rcp_f16_e32 v12, v14
	v_rcp_f16_sdwa v13, v14 dst_sel:DWORD dst_unused:UNUSED_PAD src0_sel:WORD_1
	v_rcp_f16_e32 v14, v15
	v_rcp_f16_sdwa v15, v15 dst_sel:DWORD dst_unused:UNUSED_PAD src0_sel:WORD_1
	v_rcp_f16_e32 v46, v16
	v_rcp_f16_sdwa v16, v16 dst_sel:DWORD dst_unused:UNUSED_PAD src0_sel:WORD_1
	v_rcp_f16_e32 v47, v17
	v_rcp_f16_sdwa v17, v17 dst_sel:DWORD dst_unused:UNUSED_PAD src0_sel:WORD_1
	v_add_u32_e32 v168, v187, v199
	v_pk_fma_f16 v44, v10, v30, v18
	v_pk_fma_f16 v45, v11, v31, v19
	v_lshlrev_b64 v[10:11], 9, v[168:169]
	v_or_b32_e32 v10, v10, v198
	v_lshl_add_u64 v[38:39], s[20:21], 0, v[10:11]
	v_lshl_add_u64 v[40:41], s[22:23], 0, v[10:11]
	v_pack_b32_f16 v48, v14, v15
	v_pack_b32_f16 v49, v12, v13
	v_pack_b32_f16 v46, v46, v16
	v_pack_b32_f16 v47, v47, v17
	global_load_dwordx4 v[10:13], v[38:39], off nt
	global_load_dwordx4 v[14:17], v[40:41], off nt
	v_cvt_f32_f16_sdwa v21, v139 dst_sel:DWORD dst_unused:UNUSED_PAD src0_sel:WORD_1
	v_cvt_f32_f16_e32 v20, v139
	v_cvt_f32_f16_sdwa v19, v138 dst_sel:DWORD dst_unused:UNUSED_PAD src0_sel:WORD_1
	v_cvt_f32_f16_e32 v18, v138
	v_cvt_f32_f16_sdwa v33, v141 dst_sel:DWORD dst_unused:UNUSED_PAD src0_sel:WORD_1
	v_cvt_f32_f16_e32 v32, v141
	v_pk_mul_f16 v58, v43, v46
	v_pk_mul_f16 v59, v42, v47
	v_cvt_f32_f16_sdwa v31, v140 dst_sel:DWORD dst_unused:UNUSED_PAD src0_sel:WORD_1
	v_cvt_f32_f16_e32 v30, v140
	v_pk_mul_f16 v52, v45, v48
	v_pk_mul_f16 v53, v44, v49
	v_add_u32_e32 v168, v190, v199
	v_lshlrev_b64 v[36:37], 9, v[168:169]
	v_or_b32_e32 v36, v36, v198
	v_lshl_or_b32 v50, s46, 6, v178
	v_lshlrev_b32_e32 v51, 9, v50
	v_add_u32_e32 v203, v184, v51
	v_cvt_f32_f16_sdwa v35, v77 dst_sel:DWORD dst_unused:UNUSED_PAD src0_sel:WORD_1
	v_cvt_f32_f16_e32 v34, v77
	v_add_lshl_u32 v202, v188, v50, 9
	s_mov_b64 s[4:5], -1
	s_and_b64 vcc, exec, s[26:27]
	s_waitcnt vmcnt(5)
	v_cvt_f32_f16_e32 v38, v2
	v_cvt_f32_f16_sdwa v39, v2 dst_sel:DWORD dst_unused:UNUSED_PAD src0_sel:WORD_1
	v_cvt_f32_f16_e32 v2, v3
	v_cvt_f32_f16_sdwa v3, v3 dst_sel:DWORD dst_unused:UNUSED_PAD src0_sel:WORD_1
	s_waitcnt vmcnt(4)
	v_cvt_f32_f16_e32 v40, v6
	v_cvt_f32_f16_sdwa v41, v6 dst_sel:DWORD dst_unused:UNUSED_PAD src0_sel:WORD_1
	v_cvt_f32_f16_e32 v6, v7
	v_cvt_f32_f16_sdwa v7, v7 dst_sel:DWORD dst_unused:UNUSED_PAD src0_sel:WORD_1
	v_cvt_f32_f16_e32 v42, v4
	v_cvt_f32_f16_sdwa v43, v4 dst_sel:DWORD dst_unused:UNUSED_PAD src0_sel:WORD_1
	v_cvt_f32_f16_e32 v4, v5
	v_cvt_f32_f16_sdwa v5, v5 dst_sel:DWORD dst_unused:UNUSED_PAD src0_sel:WORD_1
	v_cvt_f32_f16_e32 v44, v8
	v_cvt_f32_f16_sdwa v45, v8 dst_sel:DWORD dst_unused:UNUSED_PAD src0_sel:WORD_1
	v_cvt_f32_f16_e32 v8, v9
	v_cvt_f32_f16_sdwa v9, v9 dst_sel:DWORD dst_unused:UNUSED_PAD src0_sel:WORD_1
	v_pk_add_f32 v[2:3], v[20:21], v[2:3]
	v_pk_add_f32 v[18:19], v[18:19], v[38:39]
	v_pk_add_f32 v[4:5], v[32:33], v[4:5]
	v_pk_add_f32 v[6:7], v[2:3], v[6:7]
	v_pk_add_f32 v[20:21], v[30:31], v[42:43]
	v_pk_add_f32 v[18:19], v[18:19], v[40:41]
	v_pk_add_f32 v[8:9], v[4:5], v[8:9]
	v_cvt_pk_f16_f32 v3, v6, v7
	v_lshl_add_u64 v[6:7], s[20:21], 0, v[36:37]
	v_pk_add_f32 v[20:21], v[20:21], v[44:45]
	v_cvt_pk_f16_f32 v2, v18, v19
	v_cvt_pk_f16_f32 v5, v8, v9
	global_load_dwordx4 v[6:9], v[6:7], off nt
	v_lshl_add_u64 v[18:19], s[22:23], 0, v[36:37]
	v_cvt_pk_f16_f32 v4, v20, v21
	global_load_dwordx4 v[18:21], v[18:19], off nt
	s_waitcnt vmcnt(5)
	v_cvt_f32_f16_e32 v46, v22
	v_cvt_f32_f16_sdwa v47, v22 dst_sel:DWORD dst_unused:UNUSED_PAD src0_sel:WORD_1
	ds_write_b128 v203, v[2:5]
	v_cvt_f32_f16_sdwa v5, v76 dst_sel:DWORD dst_unused:UNUSED_PAD src0_sel:WORD_1
	v_cvt_f32_f16_e32 v4, v76
	v_cvt_f32_f16_e32 v22, v23
	v_cvt_f32_f16_sdwa v23, v23 dst_sel:DWORD dst_unused:UNUSED_PAD src0_sel:WORD_1
	s_waitcnt vmcnt(4)
	v_cvt_f32_f16_e32 v48, v26
	v_cvt_f32_f16_sdwa v49, v26 dst_sel:DWORD dst_unused:UNUSED_PAD src0_sel:WORD_1
	v_cvt_f32_f16_e32 v26, v27
	v_cvt_f32_f16_sdwa v27, v27 dst_sel:DWORD dst_unused:UNUSED_PAD src0_sel:WORD_1
	v_cvt_f32_f16_sdwa v31, v75 dst_sel:DWORD dst_unused:UNUSED_PAD src0_sel:WORD_1
	v_cvt_f32_f16_e32 v30, v75
	v_cvt_f32_f16_e32 v32, v24
	v_cvt_f32_f16_sdwa v33, v24 dst_sel:DWORD dst_unused:UNUSED_PAD src0_sel:WORD_1
	v_pk_add_f32 v[4:5], v[4:5], v[22:23]
	v_cvt_f32_f16_e32 v22, v28
	v_pk_add_f32 v[4:5], v[4:5], v[26:27]
	v_cvt_f32_f16_sdwa v23, v28 dst_sel:DWORD dst_unused:UNUSED_PAD src0_sel:WORD_1
	v_cvt_f32_f16_sdwa v27, v74 dst_sel:DWORD dst_unused:UNUSED_PAD src0_sel:WORD_1
	v_cvt_f32_f16_e32 v26, v74
	v_cvt_f32_f16_e32 v24, v25
	v_cvt_f32_f16_sdwa v25, v25 dst_sel:DWORD dst_unused:UNUSED_PAD src0_sel:WORD_1
	v_pk_add_f32 v[2:3], v[34:35], v[46:47]
	v_cvt_f32_f16_e32 v28, v29
	v_cvt_f32_f16_sdwa v29, v29 dst_sel:DWORD dst_unused:UNUSED_PAD src0_sel:WORD_1
	v_pk_add_f32 v[2:3], v[2:3], v[48:49]
	s_nop 0
	v_cvt_pk_f16_f32 v2, v2, v3
	v_cvt_pk_f16_f32 v3, v4, v5
	v_pk_add_f32 v[4:5], v[30:31], v[32:33]
	s_nop 0
	v_pk_add_f32 v[4:5], v[4:5], v[22:23]
	v_pk_add_f32 v[22:23], v[26:27], v[24:25]
	v_cvt_pk_f16_f32 v4, v4, v5
	v_pk_add_f32 v[22:23], v[22:23], v[28:29]
	s_waitcnt vmcnt(3)
	v_cvt_f32_f16_e32 v24, v10
	v_cvt_pk_f16_f32 v5, v22, v23
	v_add_u32_e32 v22, v186, v50
	v_lshlrev_b32_e32 v204, 9, v22
	v_bitop3_b32 v22, v22, v179, 15 bitop3:0x6c
	v_lshlrev_b32_e32 v205, 4, v22
	v_cvt_f32_f16_sdwa v25, v10 dst_sel:DWORD dst_unused:UNUSED_PAD src0_sel:WORD_1
	v_or_b32_e32 v10, v205, v204
	v_cvt_f32_f16_sdwa v23, v57 dst_sel:DWORD dst_unused:UNUSED_PAD src0_sel:WORD_1
	v_cvt_f32_f16_e32 v22, v57
	ds_write_b128 v10, v[2:5]
	v_cvt_f32_f16_sdwa v5, v56 dst_sel:DWORD dst_unused:UNUSED_PAD src0_sel:WORD_1
	v_cvt_f32_f16_e32 v4, v56
	v_cvt_f32_f16_e32 v10, v11
	v_cvt_f32_f16_sdwa v11, v11 dst_sel:DWORD dst_unused:UNUSED_PAD src0_sel:WORD_1
	s_waitcnt vmcnt(2)
	v_cvt_f32_f16_e32 v26, v14
	v_cvt_f32_f16_sdwa v27, v14 dst_sel:DWORD dst_unused:UNUSED_PAD src0_sel:WORD_1
	v_cvt_f32_f16_e32 v14, v15
	v_cvt_f32_f16_sdwa v15, v15 dst_sel:DWORD dst_unused:UNUSED_PAD src0_sel:WORD_1
	v_pk_add_f32 v[2:3], v[22:23], v[24:25]
	v_cvt_f32_f16_sdwa v23, v55 dst_sel:DWORD dst_unused:UNUSED_PAD src0_sel:WORD_1
	v_cvt_f32_f16_e32 v22, v55
	v_cvt_f32_f16_e32 v24, v12
	v_cvt_f32_f16_sdwa v25, v12 dst_sel:DWORD dst_unused:UNUSED_PAD src0_sel:WORD_1
	v_pk_add_f32 v[4:5], v[4:5], v[10:11]
	v_cvt_f32_f16_e32 v10, v16
	v_pk_add_f32 v[4:5], v[4:5], v[14:15]
	v_cvt_f32_f16_sdwa v11, v16 dst_sel:DWORD dst_unused:UNUSED_PAD src0_sel:WORD_1
	v_cvt_f32_f16_sdwa v15, v54 dst_sel:DWORD dst_unused:UNUSED_PAD src0_sel:WORD_1
	v_cvt_f32_f16_e32 v14, v54
	v_cvt_f32_f16_e32 v12, v13
	v_cvt_f32_f16_sdwa v13, v13 dst_sel:DWORD dst_unused:UNUSED_PAD src0_sel:WORD_1
	v_cvt_f32_f16_e32 v16, v17
	v_cvt_f32_f16_sdwa v17, v17 dst_sel:DWORD dst_unused:UNUSED_PAD src0_sel:WORD_1
	v_pk_add_f32 v[2:3], v[2:3], v[26:27]
	s_nop 0
	v_cvt_pk_f16_f32 v2, v2, v3
	v_cvt_pk_f16_f32 v3, v4, v5
	v_pk_add_f32 v[4:5], v[22:23], v[24:25]
	s_nop 0
	v_pk_add_f32 v[4:5], v[4:5], v[10:11]
	v_pk_add_f32 v[10:11], v[14:15], v[12:13]
	v_cvt_pk_f16_f32 v4, v4, v5
	v_pk_add_f32 v[10:11], v[10:11], v[16:17]
	s_waitcnt vmcnt(1)
	v_cvt_f32_f16_e32 v12, v6
	v_cvt_pk_f16_f32 v5, v10, v11
	v_cvt_f32_f16_e32 v10, v53
	v_cvt_f32_f16_sdwa v11, v53 dst_sel:DWORD dst_unused:UNUSED_PAD src0_sel:WORD_1
	v_cvt_f32_f16_sdwa v13, v6 dst_sel:DWORD dst_unused:UNUSED_PAD src0_sel:WORD_1
	s_waitcnt vmcnt(0)
	v_cvt_f32_f16_e32 v14, v18
	v_cvt_f32_f16_sdwa v15, v18 dst_sel:DWORD dst_unused:UNUSED_PAD src0_sel:WORD_1
	v_or_b32_e32 v6, v189, v202
	ds_write_b128 v6, v[2:5]
	v_cvt_f32_f16_e32 v4, v52
	v_cvt_f32_f16_sdwa v5, v52 dst_sel:DWORD dst_unused:UNUSED_PAD src0_sel:WORD_1
	v_cvt_f32_f16_e32 v6, v7
	v_cvt_f32_f16_sdwa v7, v7 dst_sel:DWORD dst_unused:UNUSED_PAD src0_sel:WORD_1
	v_pk_add_f32 v[2:3], v[10:11], v[12:13]
	v_cvt_f32_f16_e32 v10, v19
	v_cvt_f32_f16_sdwa v11, v19 dst_sel:DWORD dst_unused:UNUSED_PAD src0_sel:WORD_1
	v_pk_add_f32 v[2:3], v[2:3], v[14:15]
	v_cvt_f32_f16_e32 v12, v58
	v_cvt_f32_f16_sdwa v13, v58 dst_sel:DWORD dst_unused:UNUSED_PAD src0_sel:WORD_1
	v_cvt_f32_f16_e32 v14, v8
	v_cvt_f32_f16_sdwa v15, v8 dst_sel:DWORD dst_unused:UNUSED_PAD src0_sel:WORD_1
	v_pk_add_f32 v[4:5], v[4:5], v[6:7]
	v_cvt_f32_f16_e32 v6, v20
	v_pk_add_f32 v[4:5], v[4:5], v[10:11]
	v_cvt_f32_f16_sdwa v7, v20 dst_sel:DWORD dst_unused:UNUSED_PAD src0_sel:WORD_1
	v_cvt_f32_f16_e32 v10, v59
	v_cvt_f32_f16_sdwa v11, v59 dst_sel:DWORD dst_unused:UNUSED_PAD src0_sel:WORD_1
	v_cvt_f32_f16_e32 v8, v9
	v_cvt_f32_f16_sdwa v9, v9 dst_sel:DWORD dst_unused:UNUSED_PAD src0_sel:WORD_1
	v_cvt_pk_f16_f32 v2, v2, v3
	v_cvt_pk_f16_f32 v3, v4, v5
	v_pk_add_f32 v[4:5], v[12:13], v[14:15]
	v_cvt_f32_f16_e32 v12, v21
	v_cvt_f32_f16_sdwa v13, v21 dst_sel:DWORD dst_unused:UNUSED_PAD src0_sel:WORD_1
	v_pk_add_f32 v[4:5], v[4:5], v[6:7]
	v_pk_add_f32 v[6:7], v[10:11], v[8:9]
	v_cvt_pk_f16_f32 v4, v4, v5
	v_pk_add_f32 v[6:7], v[6:7], v[12:13]
	s_nop 0
	v_cvt_pk_f16_f32 v5, v6, v7
	v_add_lshl_u32 v6, v191, v50, 9
	v_add_u32_e32 v168, v192, v6
	ds_write_b128 v168, v[2:5]
	global_load_dwordx4 v[2:5], v[174:175], off
	global_load_dwordx4 v[8:11], v[176:177], off
	global_load_dwordx4 v[12:15], v[174:175], off offset:16
	global_load_dwordx4 v[16:19], v[176:177], off offset:16
	s_cbranch_vccz .LBB4_118
	global_load_dwordx3 v[154:156], v169, s[18:19]
	s_mov_b32 s14, s38
	s_mov_b32 s15, s39
	v_cmp_lt_u32_e64 s[64:65], 0, v199
	v_cmp_gt_u32_e64 s[66:67], 63, v199
	v_cmp_lt_u32_e64 s[68:69], 0, v180
	v_cmp_gt_u32_e64 s[70:71], 60, v180
	buffer_load_dwordx4 v[210:213], v200, s[12:15], 0 offen
	s_and_b64 s[72:73], s[68:69], s[64:65]
	s_and_b64 s[74:75], s[68:69], s[66:67]
	s_and_b64 s[76:77], s[70:71], s[64:65]
	s_and_b64 s[78:79], s[70:71], s[66:67]
	v_add_u32_e32 v245, 0xfffe7c00, v200
	v_add_u32_e32 v246, 0xfffe8000, v200
	s_mov_b64 exec, s[72:73]
	buffer_load_dwordx4 v[122:125], v245, s[12:15], 0 offen
	s_mov_b64 exec, -1
	s_mov_b64 exec, s[68:69]
	buffer_load_dwordx4 v[138:141], v246, s[12:15], 0 offen offset:512
	s_mov_b64 exec, -1
	s_mov_b64 exec, s[74:75]
	buffer_load_dwordx4 v[146:149], v246, s[12:15], 0 offen offset:2048
	s_mov_b64 exec, -1
	v_add_u32_e32 v245, 0xfffffc00, v200
	s_mov_b64 exec, s[64:65]
	buffer_load_dwordx4 v[94:97], v245, s[12:15], 0 offen
	s_mov_b64 exec, -1
	buffer_load_dwordx4 v[118:121], v200, s[12:15], 0 offen offset:512
	s_mov_b64 exec, s[66:67]
	buffer_load_dwordx4 v[134:137], v200, s[12:15], 0 offen offset:2048
	s_mov_b64 exec, -1
	v_add_u32_e32 v245, 0x17c00, v200
	v_add_u32_e32 v246, 0x18000, v200
	s_mov_b64 exec, s[64:65]
	buffer_load_dwordx4 v[62:65], v245, s[12:15], 0 offen
	s_mov_b64 exec, -1
	buffer_load_dwordx4 v[78:81], v246, s[12:15], 0 offen offset:512
	s_mov_b64 exec, s[66:67]
	buffer_load_dwordx4 v[102:105], v246, s[12:15], 0 offen offset:2048
	s_mov_b64 exec, -1
	v_add_u32_e32 v245, 0xfffe7c00, v200
	v_add_u32_e32 v246, 0xfffe8000, v200
	s_mov_b64 exec, s[72:73]
	buffer_load_dwordx4 v[82:85], v245, s[12:15], 0 offen offset:512
	s_mov_b64 exec, -1
	s_mov_b64 exec, s[68:69]
	buffer_load_dwordx4 v[106:109], v246, s[12:15], 0 offen offset:1024
	s_mov_b64 exec, -1
	s_mov_b64 exec, s[74:75]
	buffer_load_dwordx4 v[126:129], v246, s[12:15], 0 offen offset:2560
	s_mov_b64 exec, -1
	v_add_u32_e32 v245, 0xfffffc00, v200
	s_mov_b64 exec, s[64:65]
	buffer_load_dwordx4 v[54:57], v245, s[12:15], 0 offen offset:512
	s_mov_b64 exec, -1
	buffer_load_dwordx4 v[74:77], v200, s[12:15], 0 offen offset:1024
	s_mov_b64 exec, s[66:67]
	buffer_load_dwordx4 v[98:101], v200, s[12:15], 0 offen offset:2560
	s_mov_b64 exec, -1
	v_add_u32_e32 v245, 0x17c00, v200
	v_add_u32_e32 v246, 0x18000, v200
	s_mov_b64 exec, s[64:65]
	buffer_load_dwordx4 v[30:33], v245, s[12:15], 0 offen offset:512
	s_mov_b64 exec, -1
	buffer_load_dwordx4 v[42:45], v246, s[12:15], 0 offen offset:1024
	s_mov_b64 exec, s[66:67]
	buffer_load_dwordx4 v[58:61], v246, s[12:15], 0 offen offset:2560
	s_mov_b64 exec, -1
	v_add_u32_e32 v245, 0x18000, v200
	buffer_load_dwordx4 v[162:165], v245, s[12:15], 0 offen
	v_add_u32_e32 v246, 0x30000, v200
	buffer_load_dwordx4 v[158:161], v246, s[12:15], 0 offen
	v_add_u32_e32 v245, 0x2fc00, v200
	v_add_u32_e32 v246, 0x30000, v200
	v_add_u32_e32 v247, 0x47c00, v200
	v_add_u32_e32 v248, 0x48000, v200
	v_add_u32_e32 v249, 0x5fc00, v200
	v_add_u32_e32 v250, 0x60000, v200
	s_waitcnt vmcnt(22)
	v_cvt_pk_f16_f32 v6, v2, v3
	v_cvt_pk_f16_f32 v2, v8, v9
	v_cvt_pk_f16_f32 v7, v4, v5
	v_cvt_pk_f16_f32 v3, v10, v11
	v_cvt_pk_f16_f32 v8, v12, v13
	v_cvt_pk_f16_f32 v4, v16, v17
	v_cvt_pk_f16_f32 v9, v14, v15
	v_cvt_pk_f16_f32 v5, v18, v19
	s_not_b64 exec, s[72:73]
	s_cbranch_execz .Lmyf_C3_0
	v_mov_b32_e32 v122, v6
	v_mov_b32_e32 v123, v7
	v_mov_b32_e32 v124, v8
	v_mov_b32_e32 v125, v9
	v_mov_b32_e32 v82, v2
	v_mov_b32_e32 v83, v3
	v_mov_b32_e32 v84, v4
	v_mov_b32_e32 v85, v5

.Lmyf_C3_7:
	s_mov_b64 exec, -1
	s_waitcnt vmcnt(21)
	v_cvt_f16_f32_e32 v206, v155
	v_cvt_f16_f32_e32 v208, v154
	v_cvt_f16_f32_e32 v207, v156
	v_add_u32_e32 v251, 0x48000, v200
	buffer_load_dwordx4 v[154:157], v251, s[12:15], 0 offen
	s_mov_b64 s[4:5], 0
	s_waitcnt vmcnt(12)
	v_pk_mul_f16 v216, v208, v213 op_sel_hi:[0,1]
	v_pk_mul_f16 v220, v206, v213 op_sel_hi:[0,1]
	v_pk_mul_f16 v224, v207, v213 op_sel_hi:[0,1]
	v_pk_mul_f16 v209, v208, v210 op_sel_hi:[0,1]
	v_pk_mul_f16 v214, v208, v211 op_sel_hi:[0,1]
	v_pk_mul_f16 v215, v208, v212 op_sel_hi:[0,1]
	v_pk_mul_f16 v217, v206, v210 op_sel_hi:[0,1]
	v_pk_mul_f16 v218, v206, v211 op_sel_hi:[0,1]
	v_pk_mul_f16 v219, v206, v212 op_sel_hi:[0,1]
	v_pk_mul_f16 v221, v207, v210 op_sel_hi:[0,1]
	v_pk_mul_f16 v222, v207, v211 op_sel_hi:[0,1]
	v_pk_mul_f16 v223, v207, v212 op_sel_hi:[0,1]
	v_pk_fma_f16 v125, v125, v213, v216
	v_pk_fma_f16 v141, v141, v213, v220
	v_pk_fma_f16 v149, v149, v213, v224
	v_pk_fma_f16 v225, v97, v213, v216
	v_pk_fma_f16 v229, v121, v213, v220
	v_pk_fma_f16 v233, v137, v213, v224
	v_pk_fma_f16 v216, v65, v213, v216
	v_pk_fma_f16 v220, v81, v213, v220
	v_pk_fma_f16 v213, v105, v213, v224
	v_pk_maximum3_f16 v224, v125, v141, v149
	v_pk_fma_f16 v124, v124, v212, v215
	v_pk_fma_f16 v123, v123, v211, v214
	v_pk_fma_f16 v122, v122, v210, v209
	v_pk_fma_f16 v140, v140, v212, v219
	v_pk_fma_f16 v139, v139, v211, v218
	v_pk_fma_f16 v138, v138, v210, v217
	v_pk_fma_f16 v148, v148, v212, v223
	v_pk_fma_f16 v147, v147, v211, v222
	v_pk_fma_f16 v146, v146, v210, v221
	v_pk_fma_f16 v226, v96, v212, v215
	v_pk_fma_f16 v227, v95, v211, v214
	v_pk_fma_f16 v228, v94, v210, v209
	v_pk_fma_f16 v230, v120, v212, v219
	v_pk_fma_f16 v231, v119, v211, v218
	v_pk_fma_f16 v232, v118, v210, v217
	v_pk_fma_f16 v234, v136, v212, v223
	v_pk_fma_f16 v235, v135, v211, v222
	v_pk_fma_f16 v236, v134, v210, v221
	v_pk_fma_f16 v215, v64, v212, v215
	v_pk_fma_f16 v214, v63, v211, v214
	v_pk_fma_f16 v209, v62, v210, v209
	v_pk_fma_f16 v219, v80, v212, v219
	v_pk_fma_f16 v218, v79, v211, v218
	v_pk_fma_f16 v217, v78, v210, v217
	v_pk_fma_f16 v212, v104, v212, v223
	v_pk_fma_f16 v211, v103, v211, v222
	v_pk_fma_f16 v210, v102, v210, v221
	v_pk_maximum3_f16 v221, v122, v138, v146
	v_pk_maximum3_f16 v222, v123, v139, v147
	v_pk_maximum3_f16 v223, v124, v140, v148
	v_pk_maximum3_f16 v240, v225, v229, v233
	v_pk_maximum3_f16 v244, v216, v220, v213
	v_pk_maximum3_f16 v237, v228, v232, v236
	v_pk_maximum3_f16 v238, v227, v231, v235
	v_pk_maximum3_f16 v239, v226, v230, v234
	v_pk_maximum3_f16 v241, v209, v217, v210
	v_pk_maximum3_f16 v242, v214, v218, v211
	v_pk_maximum3_f16 v224, v224, v240, v244
	v_pk_maximum3_f16 v243, v215, v219, v212
	v_pk_maximum3_f16 v221, v221, v237, v241
	v_pk_maximum3_f16 v222, v222, v238, v242
	v_pk_maximum3_f16 v223, v223, v239, v243
	v_pk_add_f16 v125, v125, v224 neg_lo:[0,1] neg_hi:[0,1]
	v_pk_add_f16 v122, v122, v221 neg_lo:[0,1] neg_hi:[0,1]
	v_pk_add_f16 v123, v123, v222 neg_lo:[0,1] neg_hi:[0,1]
	v_pk_add_f16 v124, v124, v223 neg_lo:[0,1] neg_hi:[0,1]
	v_pk_add_f16 v138, v138, v221 neg_lo:[0,1] neg_hi:[0,1]
	v_exp_f16_sdwa v237, v122 dst_sel:WORD_0 dst_unused:UNUSED_PAD src0_sel:WORD_0
	v_exp_f16_sdwa v238, v123 dst_sel:WORD_0 dst_unused:UNUSED_PAD src0_sel:WORD_0
	v_exp_f16_sdwa v239, v124 dst_sel:WORD_0 dst_unused:UNUSED_PAD src0_sel:WORD_0
	v_exp_f16_sdwa v240, v125 dst_sel:WORD_0 dst_unused:UNUSED_PAD src0_sel:WORD_0
	v_exp_f16_sdwa v237, v122 dst_sel:WORD_1 dst_unused:UNUSED_PRESERVE src0_sel:WORD_1
	v_exp_f16_sdwa v238, v123 dst_sel:WORD_1 dst_unused:UNUSED_PRESERVE src0_sel:WORD_1
	v_exp_f16_sdwa v239, v124 dst_sel:WORD_1 dst_unused:UNUSED_PRESERVE src0_sel:WORD_1
	v_exp_f16_sdwa v240, v125 dst_sel:WORD_1 dst_unused:UNUSED_PRESERVE src0_sel:WORD_1
	v_pk_add_f16 v139, v139, v222 neg_lo:[0,1] neg_hi:[0,1]
	v_pk_add_f16 v125, v237, 0
	s_waitcnt vmcnt(3)
	v_pk_fma_f16 v85, v85, v240, 0
	v_pk_add_f16 v122, v240, 0
	v_pk_add_f16 v123, v239, 0
	v_pk_add_f16 v124, v238, 0
	v_pk_fma_f16 v84, v84, v239, 0
	v_pk_fma_f16 v83, v83, v238, 0
	s_mov_b64 exec, s[64:65]
	buffer_load_dwordx4 v[34:37], v245, s[12:15], 0 offen
	buffer_load_dwordx4 v[18:21], v245, s[12:15], 0 offen offset:512
	s_mov_b64 exec, -1
	v_pk_fma_f16 v82, v82, v237, 0
	v_pk_add_f16 v140, v140, v223 neg_lo:[0,1] neg_hi:[0,1]
	v_pk_add_f16 v141, v141, v224 neg_lo:[0,1] neg_hi:[0,1]
	v_exp_f16_sdwa v237, v138 dst_sel:WORD_0 dst_unused:UNUSED_PAD src0_sel:WORD_0
	v_exp_f16_sdwa v238, v139 dst_sel:WORD_0 dst_unused:UNUSED_PAD src0_sel:WORD_0
	v_exp_f16_sdwa v239, v140 dst_sel:WORD_0 dst_unused:UNUSED_PAD src0_sel:WORD_0
	v_exp_f16_sdwa v240, v141 dst_sel:WORD_0 dst_unused:UNUSED_PAD src0_sel:WORD_0
	v_exp_f16_sdwa v237, v138 dst_sel:WORD_1 dst_unused:UNUSED_PRESERVE src0_sel:WORD_1
	v_exp_f16_sdwa v238, v139 dst_sel:WORD_1 dst_unused:UNUSED_PRESERVE src0_sel:WORD_1
	v_exp_f16_sdwa v239, v140 dst_sel:WORD_1 dst_unused:UNUSED_PRESERVE src0_sel:WORD_1
	v_exp_f16_sdwa v240, v141 dst_sel:WORD_1 dst_unused:UNUSED_PRESERVE src0_sel:WORD_1
	v_pk_add_f16 v125, v125, v237
	v_pk_fma_f16 v85, v109, v240, v85
	v_pk_add_f16 v109, v149, v224 neg_lo:[0,1] neg_hi:[0,1]
	v_pk_add_f16 v124, v124, v238
	v_pk_add_f16 v123, v123, v239
	v_pk_add_f16 v122, v122, v240
	buffer_load_dwordx4 v[46:49], v246, s[12:15], 0 offen offset:512
	buffer_load_dwordx4 v[22:25], v246, s[12:15], 0 offen offset:1024
	v_pk_fma_f16 v82, v106, v237, v82
	v_pk_fma_f16 v83, v107, v238, v83
	v_pk_fma_f16 v84, v108, v239, v84
	v_pk_add_f16 v106, v146, v221 neg_lo:[0,1] neg_hi:[0,1]
	v_pk_add_f16 v107, v147, v222 neg_lo:[0,1] neg_hi:[0,1]
	v_pk_add_f16 v108, v148, v223 neg_lo:[0,1] neg_hi:[0,1]
	v_exp_f16_sdwa v138, v106 dst_sel:WORD_0 dst_unused:UNUSED_PAD src0_sel:WORD_0
	v_exp_f16_sdwa v139, v107 dst_sel:WORD_0 dst_unused:UNUSED_PAD src0_sel:WORD_0
	v_exp_f16_sdwa v140, v108 dst_sel:WORD_0 dst_unused:UNUSED_PAD src0_sel:WORD_0
	v_exp_f16_sdwa v141, v109 dst_sel:WORD_0 dst_unused:UNUSED_PAD src0_sel:WORD_0
	v_exp_f16_sdwa v138, v106 dst_sel:WORD_1 dst_unused:UNUSED_PRESERVE src0_sel:WORD_1
	v_exp_f16_sdwa v139, v107 dst_sel:WORD_1 dst_unused:UNUSED_PRESERVE src0_sel:WORD_1
	v_exp_f16_sdwa v140, v108 dst_sel:WORD_1 dst_unused:UNUSED_PRESERVE src0_sel:WORD_1
	v_exp_f16_sdwa v141, v109 dst_sel:WORD_1 dst_unused:UNUSED_PRESERVE src0_sel:WORD_1
	v_pk_add_f16 v109, v125, v138
	v_pk_add_f16 v106, v122, v141
	v_pk_add_f16 v107, v123, v140
	s_mov_b64 exec, s[66:67]
	buffer_load_dwordx4 v[66:69], v246, s[12:15], 0 offen offset:2048
	buffer_load_dwordx4 v[26:29], v246, s[12:15], 0 offen offset:2560
	s_mov_b64 exec, -1
	v_pk_add_f16 v108, v124, v139
	v_pk_fma_f16 v85, v129, v141, v85
	v_pk_fma_f16 v84, v128, v140, v84
	v_pk_fma_f16 v83, v127, v139, v83
	v_pk_fma_f16 v82, v126, v138, v82
	v_pk_add_f16 v122, v228, v221 neg_lo:[0,1] neg_hi:[0,1]
	v_pk_add_f16 v123, v227, v222 neg_lo:[0,1] neg_hi:[0,1]
	v_pk_add_f16 v124, v226, v223 neg_lo:[0,1] neg_hi:[0,1]
	s_mov_b64 exec, s[64:65]
	buffer_load_dwordx4 v[86:89], v247, s[12:15], 0 offen
	buffer_load_dwordx4 v[38:41], v247, s[12:15], 0 offen offset:512
	s_mov_b64 exec, -1
	v_pk_add_f16 v125, v225, v224 neg_lo:[0,1] neg_hi:[0,1]
	v_exp_f16_sdwa v126, v122 dst_sel:WORD_0 dst_unused:UNUSED_PAD src0_sel:WORD_0
	v_exp_f16_sdwa v127, v123 dst_sel:WORD_0 dst_unused:UNUSED_PAD src0_sel:WORD_0
	v_exp_f16_sdwa v128, v124 dst_sel:WORD_0 dst_unused:UNUSED_PAD src0_sel:WORD_0
	v_exp_f16_sdwa v129, v125 dst_sel:WORD_0 dst_unused:UNUSED_PAD src0_sel:WORD_0
	v_exp_f16_sdwa v126, v122 dst_sel:WORD_1 dst_unused:UNUSED_PRESERVE src0_sel:WORD_1
	v_exp_f16_sdwa v127, v123 dst_sel:WORD_1 dst_unused:UNUSED_PRESERVE src0_sel:WORD_1
	v_exp_f16_sdwa v128, v124 dst_sel:WORD_1 dst_unused:UNUSED_PRESERVE src0_sel:WORD_1
	v_exp_f16_sdwa v129, v125 dst_sel:WORD_1 dst_unused:UNUSED_PRESERVE src0_sel:WORD_1
	v_pk_add_f16 v122, v232, v221 neg_lo:[0,1] neg_hi:[0,1]
	v_pk_add_f16 v109, v109, v126
	v_pk_add_f16 v108, v108, v127
	v_pk_add_f16 v107, v107, v128
	v_pk_add_f16 v106, v106, v129
	v_pk_fma_f16 v82, v54, v126, v82
	v_pk_fma_f16 v83, v55, v127, v83
	v_pk_fma_f16 v84, v56, v128, v84
	v_pk_fma_f16 v85, v57, v129, v85
	buffer_load_dwordx4 v[114:117], v248, s[12:15], 0 offen offset:512
	buffer_load_dwordx4 v[50:53], v248, s[12:15], 0 offen offset:1024
	v_pk_add_f16 v123, v231, v222 neg_lo:[0,1] neg_hi:[0,1]
	v_pk_add_f16 v124, v230, v223 neg_lo:[0,1] neg_hi:[0,1]
	v_pk_add_f16 v125, v229, v224 neg_lo:[0,1] neg_hi:[0,1]
	v_exp_f16_sdwa v126, v122 dst_sel:WORD_0 dst_unused:UNUSED_PAD src0_sel:WORD_0
	v_exp_f16_sdwa v127, v123 dst_sel:WORD_0 dst_unused:UNUSED_PAD src0_sel:WORD_0
	v_exp_f16_sdwa v128, v124 dst_sel:WORD_0 dst_unused:UNUSED_PAD src0_sel:WORD_0
	v_exp_f16_sdwa v129, v125 dst_sel:WORD_0 dst_unused:UNUSED_PAD src0_sel:WORD_0
	v_exp_f16_sdwa v126, v122 dst_sel:WORD_1 dst_unused:UNUSED_PRESERVE src0_sel:WORD_1
	v_exp_f16_sdwa v127, v123 dst_sel:WORD_1 dst_unused:UNUSED_PRESERVE src0_sel:WORD_1
	v_exp_f16_sdwa v128, v124 dst_sel:WORD_1 dst_unused:UNUSED_PRESERVE src0_sel:WORD_1
	v_exp_f16_sdwa v129, v125 dst_sel:WORD_1 dst_unused:UNUSED_PRESERVE src0_sel:WORD_1
	v_pk_add_f16 v122, v236, v221 neg_lo:[0,1] neg_hi:[0,1]
	v_pk_add_f16 v109, v109, v126
	v_pk_add_f16 v106, v106, v129
	v_pk_add_f16 v107, v107, v128
	v_pk_add_f16 v108, v108, v127
	v_pk_fma_f16 v85, v77, v129, v85
	s_mov_b64 exec, s[66:67]
	buffer_load_dwordx4 v[130:133], v248, s[12:15], 0 offen offset:2048
	buffer_load_dwordx4 v[70:73], v248, s[12:15], 0 offen offset:2560
	s_mov_b64 exec, -1
	v_pk_fma_f16 v84, v76, v128, v84
	v_pk_fma_f16 v83, v75, v127, v83
	v_pk_fma_f16 v82, v74, v126, v82
	v_pk_add_f16 v123, v235, v222 neg_lo:[0,1] neg_hi:[0,1]
	v_pk_add_f16 v124, v234, v223 neg_lo:[0,1] neg_hi:[0,1]
	v_pk_add_f16 v125, v233, v224 neg_lo:[0,1] neg_hi:[0,1]
	v_exp_f16_sdwa v126, v122 dst_sel:WORD_0 dst_unused:UNUSED_PAD src0_sel:WORD_0
	v_exp_f16_sdwa v127, v123 dst_sel:WORD_0 dst_unused:UNUSED_PAD src0_sel:WORD_0
	v_exp_f16_sdwa v128, v124 dst_sel:WORD_0 dst_unused:UNUSED_PAD src0_sel:WORD_0
	v_exp_f16_sdwa v129, v125 dst_sel:WORD_0 dst_unused:UNUSED_PAD src0_sel:WORD_0
	v_exp_f16_sdwa v126, v122 dst_sel:WORD_1 dst_unused:UNUSED_PRESERVE src0_sel:WORD_1
	v_exp_f16_sdwa v127, v123 dst_sel:WORD_1 dst_unused:UNUSED_PRESERVE src0_sel:WORD_1
	v_exp_f16_sdwa v128, v124 dst_sel:WORD_1 dst_unused:UNUSED_PRESERVE src0_sel:WORD_1
	v_exp_f16_sdwa v129, v125 dst_sel:WORD_1 dst_unused:UNUSED_PRESERVE src0_sel:WORD_1
	v_pk_add_f16 v122, v209, v221 neg_lo:[0,1] neg_hi:[0,1]
	v_pk_add_f16 v109, v109, v126
	v_pk_add_f16 v108, v108, v127
	s_mov_b64 exec, s[76:77]
	buffer_load_dwordx4 v[142:145], v249, s[12:15], 0 offen
	buffer_load_dwordx4 v[90:93], v249, s[12:15], 0 offen offset:512
	s_mov_b64 exec, -1
	v_pk_add_f16 v107, v107, v128
	v_pk_add_f16 v106, v106, v129
	v_pk_fma_f16 v82, v98, v126, v82
	v_pk_fma_f16 v83, v99, v127, v83
	v_pk_fma_f16 v84, v100, v128, v84
	v_pk_fma_f16 v85, v101, v129, v85
	v_pk_add_f16 v123, v214, v222 neg_lo:[0,1] neg_hi:[0,1]
	v_pk_add_f16 v124, v215, v223 neg_lo:[0,1] neg_hi:[0,1]
	s_mov_b64 exec, s[70:71]
	buffer_load_dwordx4 v[150:153], v250, s[12:15], 0 offen offset:512
	buffer_load_dwordx4 v[110:113], v250, s[12:15], 0 offen offset:1024
	s_mov_b64 exec, -1
	v_pk_add_f16 v125, v216, v224 neg_lo:[0,1] neg_hi:[0,1]
	v_exp_f16_sdwa v126, v122 dst_sel:WORD_0 dst_unused:UNUSED_PAD src0_sel:WORD_0
	v_exp_f16_sdwa v127, v123 dst_sel:WORD_0 dst_unused:UNUSED_PAD src0_sel:WORD_0
	v_exp_f16_sdwa v128, v124 dst_sel:WORD_0 dst_unused:UNUSED_PAD src0_sel:WORD_0
	v_exp_f16_sdwa v129, v125 dst_sel:WORD_0 dst_unused:UNUSED_PAD src0_sel:WORD_0
	v_exp_f16_sdwa v126, v122 dst_sel:WORD_1 dst_unused:UNUSED_PRESERVE src0_sel:WORD_1
	v_exp_f16_sdwa v127, v123 dst_sel:WORD_1 dst_unused:UNUSED_PRESERVE src0_sel:WORD_1
	v_exp_f16_sdwa v128, v124 dst_sel:WORD_1 dst_unused:UNUSED_PRESERVE src0_sel:WORD_1
	v_exp_f16_sdwa v129, v125 dst_sel:WORD_1 dst_unused:UNUSED_PRESERVE src0_sel:WORD_1
	v_pk_add_f16 v122, v217, v221 neg_lo:[0,1] neg_hi:[0,1]
	v_pk_add_f16 v109, v109, v126
	v_pk_add_f16 v106, v106, v129
	v_pk_add_f16 v107, v107, v128
	v_pk_add_f16 v108, v108, v127
	v_pk_fma_f16 v85, v33, v129, v85
	v_pk_fma_f16 v84, v32, v128, v84
	v_pk_fma_f16 v83, v31, v127, v83
	s_mov_b64 exec, s[78:79]
	buffer_load_dwordx4 v[14:17], v250, s[12:15], 0 offen offset:2048
	buffer_load_dwordx4 v[10:13], v250, s[12:15], 0 offen offset:2560
	s_mov_b64 exec, -1
	v_pk_fma_f16 v82, v30, v126, v82
	v_pk_add_f16 v123, v218, v222 neg_lo:[0,1] neg_hi:[0,1]
	v_pk_add_f16 v124, v219, v223 neg_lo:[0,1] neg_hi:[0,1]
	v_pk_add_f16 v125, v220, v224 neg_lo:[0,1] neg_hi:[0,1]
	v_exp_f16_sdwa v126, v122 dst_sel:WORD_0 dst_unused:UNUSED_PAD src0_sel:WORD_0
	v_exp_f16_sdwa v127, v123 dst_sel:WORD_0 dst_unused:UNUSED_PAD src0_sel:WORD_0
	v_exp_f16_sdwa v128, v124 dst_sel:WORD_0 dst_unused:UNUSED_PAD src0_sel:WORD_0
	v_exp_f16_sdwa v129, v125 dst_sel:WORD_0 dst_unused:UNUSED_PAD src0_sel:WORD_0
	v_exp_f16_sdwa v126, v122 dst_sel:WORD_1 dst_unused:UNUSED_PRESERVE src0_sel:WORD_1
	v_exp_f16_sdwa v127, v123 dst_sel:WORD_1 dst_unused:UNUSED_PRESERVE src0_sel:WORD_1
	v_exp_f16_sdwa v128, v124 dst_sel:WORD_1 dst_unused:UNUSED_PRESERVE src0_sel:WORD_1
	v_exp_f16_sdwa v129, v125 dst_sel:WORD_1 dst_unused:UNUSED_PRESERVE src0_sel:WORD_1
	v_pk_add_f16 v122, v210, v221 neg_lo:[0,1] neg_hi:[0,1]
	v_pk_add_f16 v109, v109, v126
	v_pk_add_f16 v108, v108, v127
	v_pk_add_f16 v107, v107, v128
	v_pk_add_f16 v106, v106, v129
	v_pk_fma_f16 v82, v42, v126, v82
	v_pk_fma_f16 v83, v43, v127, v83
	v_pk_fma_f16 v84, v44, v128, v84
	v_pk_fma_f16 v85, v45, v129, v85
	v_pk_add_f16 v123, v211, v222 neg_lo:[0,1] neg_hi:[0,1]
	v_pk_add_f16 v124, v212, v223 neg_lo:[0,1] neg_hi:[0,1]
	v_pk_add_f16 v125, v213, v224 neg_lo:[0,1] neg_hi:[0,1]
	v_exp_f16_sdwa v126, v122 dst_sel:WORD_0 dst_unused:UNUSED_PAD src0_sel:WORD_0
	v_exp_f16_sdwa v127, v123 dst_sel:WORD_0 dst_unused:UNUSED_PAD src0_sel:WORD_0
	v_exp_f16_sdwa v128, v124 dst_sel:WORD_0 dst_unused:UNUSED_PAD src0_sel:WORD_0
	v_exp_f16_sdwa v129, v125 dst_sel:WORD_0 dst_unused:UNUSED_PAD src0_sel:WORD_0
	v_exp_f16_sdwa v126, v122 dst_sel:WORD_1 dst_unused:UNUSED_PRESERVE src0_sel:WORD_1
	v_exp_f16_sdwa v127, v123 dst_sel:WORD_1 dst_unused:UNUSED_PRESERVE src0_sel:WORD_1
	v_exp_f16_sdwa v128, v124 dst_sel:WORD_1 dst_unused:UNUSED_PRESERVE src0_sel:WORD_1
	v_exp_f16_sdwa v129, v125 dst_sel:WORD_1 dst_unused:UNUSED_PRESERVE src0_sel:WORD_1
	v_pk_add_f16 v109, v109, v126
	v_pk_add_f16 v108, v108, v127
	v_rcp_f16_e32 v122, v109
	v_rcp_f16_sdwa v109, v109 dst_sel:DWORD dst_unused:UNUSED_PAD src0_sel:WORD_1
	v_pk_add_f16 v107, v107, v128
	v_rcp_f16_e32 v123, v108
	v_rcp_f16_sdwa v108, v108 dst_sel:DWORD dst_unused:UNUSED_PAD src0_sel:WORD_1
	v_pk_add_f16 v106, v106, v129
	v_rcp_f16_e32 v124, v107
	v_rcp_f16_sdwa v107, v107 dst_sel:DWORD dst_unused:UNUSED_PAD src0_sel:WORD_1
	v_rcp_f16_e32 v125, v106
	v_rcp_f16_sdwa v106, v106 dst_sel:DWORD dst_unused:UNUSED_PAD src0_sel:WORD_1
	v_pk_fma_f16 v82, v58, v126, v82
	v_pack_b32_f16 v109, v122, v109
	v_pk_fma_f16 v83, v59, v127, v83
	v_pk_mul_f16 v141, v82, v109
	v_pack_b32_f16 v82, v123, v108
	v_pk_fma_f16 v84, v60, v128, v84
	v_pk_mul_f16 v140, v83, v82
	v_pack_b32_f16 v82, v124, v107
	v_pk_fma_f16 v85, v61, v129, v85
	v_pk_mul_f16 v139, v84, v82
	v_pack_b32_f16 v82, v125, v106
	v_pk_mul_f16 v138, v85, v82
	s_waitcnt vmcnt(12)
	v_pk_mul_f16 v85, v208, v165 op_sel_hi:[0,1]
	v_pk_mul_f16 v109, v206, v165 op_sel_hi:[0,1]
	v_pk_mul_f16 v122, v207, v162 op_sel_hi:[0,1]
	v_pk_mul_f16 v125, v207, v165 op_sel_hi:[0,1]
	v_pk_mul_f16 v82, v208, v162 op_sel_hi:[0,1]
	v_pk_mul_f16 v83, v208, v163 op_sel_hi:[0,1]
	v_pk_mul_f16 v84, v208, v164 op_sel_hi:[0,1]
	v_pk_mul_f16 v106, v206, v162 op_sel_hi:[0,1]
	v_pk_mul_f16 v107, v206, v163 op_sel_hi:[0,1]
	v_pk_mul_f16 v108, v206, v164 op_sel_hi:[0,1]
	v_pk_mul_f16 v123, v207, v163 op_sel_hi:[0,1]
	v_pk_mul_f16 v124, v207, v164 op_sel_hi:[0,1]
	v_pk_fma_f16 v97, v97, v165, v85
	v_pk_fma_f16 v121, v121, v165, v109
	v_pk_fma_f16 v126, v137, v165, v125
	v_pk_fma_f16 v129, v134, v162, v122
	v_pk_fma_f16 v134, v65, v165, v85
	v_pk_fma_f16 v146, v81, v165, v109
	v_pk_fma_f16 v209, v105, v165, v125
	v_pk_fma_f16 v85, v37, v165, v85
	v_pk_fma_f16 v109, v49, v165, v109
	v_pk_fma_f16 v125, v69, v165, v125
	v_pk_maximum3_f16 v165, v97, v121, v126
	v_pk_fma_f16 v96, v96, v164, v84
	v_pk_fma_f16 v95, v95, v163, v83
	v_pk_fma_f16 v94, v94, v162, v82
	v_pk_fma_f16 v120, v120, v164, v108
	v_pk_fma_f16 v119, v119, v163, v107
	v_pk_fma_f16 v118, v118, v162, v106
	v_pk_fma_f16 v127, v136, v164, v124
	v_pk_fma_f16 v128, v135, v163, v123
	v_pk_fma_f16 v135, v64, v164, v84
	v_pk_fma_f16 v136, v63, v163, v83
	v_pk_fma_f16 v137, v62, v162, v82
	v_pk_fma_f16 v147, v80, v164, v108
	v_pk_fma_f16 v148, v79, v163, v107
	v_pk_fma_f16 v149, v78, v162, v106
	v_pk_fma_f16 v210, v104, v164, v124
	v_pk_fma_f16 v211, v103, v163, v123
	v_pk_fma_f16 v212, v102, v162, v122
	v_pk_fma_f16 v84, v36, v164, v84
	v_pk_fma_f16 v83, v35, v163, v83
	v_pk_fma_f16 v82, v34, v162, v82
	v_pk_fma_f16 v108, v48, v164, v108
	v_pk_fma_f16 v107, v47, v163, v107
	v_pk_fma_f16 v106, v46, v162, v106
	v_pk_fma_f16 v124, v68, v164, v124
	v_pk_fma_f16 v123, v67, v163, v123
	v_pk_fma_f16 v122, v66, v162, v122
	v_pk_maximum3_f16 v162, v94, v118, v129
	v_pk_maximum3_f16 v163, v95, v119, v128
	v_pk_maximum3_f16 v164, v96, v120, v127
	v_pk_maximum3_f16 v216, v134, v146, v209
	v_pk_maximum3_f16 v220, v85, v109, v125
	v_pk_maximum3_f16 v213, v137, v149, v212
	v_pk_maximum3_f16 v214, v136, v148, v211
	v_pk_maximum3_f16 v215, v135, v147, v210
	v_pk_maximum3_f16 v217, v82, v106, v122
	v_pk_maximum3_f16 v218, v83, v107, v123
	v_pk_maximum3_f16 v165, v165, v216, v220
	v_pk_maximum3_f16 v219, v84, v108, v124
	v_pk_maximum3_f16 v162, v162, v213, v217
	v_pk_maximum3_f16 v163, v163, v214, v218
	v_pk_maximum3_f16 v164, v164, v215, v219
	v_pk_add_f16 v97, v97, v165 neg_lo:[0,1] neg_hi:[0,1]
	v_pk_add_f16 v94, v94, v162 neg_lo:[0,1] neg_hi:[0,1]
	v_pk_add_f16 v95, v95, v163 neg_lo:[0,1] neg_hi:[0,1]
	v_pk_add_f16 v96, v96, v164 neg_lo:[0,1] neg_hi:[0,1]
	v_pk_add_f16 v118, v118, v162 neg_lo:[0,1] neg_hi:[0,1]
	v_exp_f16_sdwa v213, v94 dst_sel:WORD_0 dst_unused:UNUSED_PAD src0_sel:WORD_0
	v_exp_f16_sdwa v214, v95 dst_sel:WORD_0 dst_unused:UNUSED_PAD src0_sel:WORD_0
	v_exp_f16_sdwa v215, v96 dst_sel:WORD_0 dst_unused:UNUSED_PAD src0_sel:WORD_0
	v_exp_f16_sdwa v216, v97 dst_sel:WORD_0 dst_unused:UNUSED_PAD src0_sel:WORD_0
	v_exp_f16_sdwa v213, v94 dst_sel:WORD_1 dst_unused:UNUSED_PRESERVE src0_sel:WORD_1
	v_exp_f16_sdwa v214, v95 dst_sel:WORD_1 dst_unused:UNUSED_PRESERVE src0_sel:WORD_1
	v_exp_f16_sdwa v215, v96 dst_sel:WORD_1 dst_unused:UNUSED_PRESERVE src0_sel:WORD_1
	v_exp_f16_sdwa v216, v97 dst_sel:WORD_1 dst_unused:UNUSED_PRESERVE src0_sel:WORD_1
	v_pk_add_f16 v119, v119, v163 neg_lo:[0,1] neg_hi:[0,1]
	v_pk_add_f16 v97, v213, 0
	v_pk_fma_f16 v57, v57, v216, 0
	v_pk_add_f16 v94, v216, 0
	v_pk_add_f16 v95, v215, 0
	v_pk_add_f16 v96, v214, 0
	v_pk_fma_f16 v56, v56, v215, 0
	v_pk_fma_f16 v55, v55, v214, 0
	v_pk_fma_f16 v54, v54, v213, 0
	v_pk_add_f16 v120, v120, v164 neg_lo:[0,1] neg_hi:[0,1]
	v_pk_add_f16 v121, v121, v165 neg_lo:[0,1] neg_hi:[0,1]
	v_pk_add_f16 v82, v82, v162 neg_lo:[0,1] neg_hi:[0,1]
	v_exp_f16_sdwa v213, v118 dst_sel:WORD_0 dst_unused:UNUSED_PAD src0_sel:WORD_0
	v_exp_f16_sdwa v214, v119 dst_sel:WORD_0 dst_unused:UNUSED_PAD src0_sel:WORD_0
	v_exp_f16_sdwa v215, v120 dst_sel:WORD_0 dst_unused:UNUSED_PAD src0_sel:WORD_0
	v_exp_f16_sdwa v216, v121 dst_sel:WORD_0 dst_unused:UNUSED_PAD src0_sel:WORD_0
	v_exp_f16_sdwa v213, v118 dst_sel:WORD_1 dst_unused:UNUSED_PRESERVE src0_sel:WORD_1
	v_exp_f16_sdwa v214, v119 dst_sel:WORD_1 dst_unused:UNUSED_PRESERVE src0_sel:WORD_1
	v_exp_f16_sdwa v215, v120 dst_sel:WORD_1 dst_unused:UNUSED_PRESERVE src0_sel:WORD_1
	v_exp_f16_sdwa v216, v121 dst_sel:WORD_1 dst_unused:UNUSED_PRESERVE src0_sel:WORD_1
	v_pk_add_f16 v83, v83, v163 neg_lo:[0,1] neg_hi:[0,1]
	v_pk_add_f16 v97, v97, v213
	v_pk_fma_f16 v57, v77, v216, v57
	v_pk_add_f16 v77, v126, v165 neg_lo:[0,1] neg_hi:[0,1]
	v_pk_add_f16 v96, v96, v214
	v_pk_add_f16 v95, v95, v215
	v_pk_add_f16 v94, v94, v216
	v_pk_fma_f16 v54, v74, v213, v54
	v_pk_fma_f16 v55, v75, v214, v55
	v_pk_fma_f16 v56, v76, v215, v56
	v_pk_add_f16 v74, v129, v162 neg_lo:[0,1] neg_hi:[0,1]
	v_pk_add_f16 v75, v128, v163 neg_lo:[0,1] neg_hi:[0,1]
	v_pk_add_f16 v76, v127, v164 neg_lo:[0,1] neg_hi:[0,1]
	v_pk_add_f16 v84, v84, v164 neg_lo:[0,1] neg_hi:[0,1]
	v_exp_f16_sdwa v118, v74 dst_sel:WORD_0 dst_unused:UNUSED_PAD src0_sel:WORD_0
	v_exp_f16_sdwa v119, v75 dst_sel:WORD_0 dst_unused:UNUSED_PAD src0_sel:WORD_0
	v_exp_f16_sdwa v120, v76 dst_sel:WORD_0 dst_unused:UNUSED_PAD src0_sel:WORD_0
	v_exp_f16_sdwa v121, v77 dst_sel:WORD_0 dst_unused:UNUSED_PAD src0_sel:WORD_0
	v_exp_f16_sdwa v118, v74 dst_sel:WORD_1 dst_unused:UNUSED_PRESERVE src0_sel:WORD_1
	v_exp_f16_sdwa v119, v75 dst_sel:WORD_1 dst_unused:UNUSED_PRESERVE src0_sel:WORD_1
	v_exp_f16_sdwa v120, v76 dst_sel:WORD_1 dst_unused:UNUSED_PRESERVE src0_sel:WORD_1
	v_exp_f16_sdwa v121, v77 dst_sel:WORD_1 dst_unused:UNUSED_PRESERVE src0_sel:WORD_1
	v_pk_add_f16 v85, v85, v165 neg_lo:[0,1] neg_hi:[0,1]
	v_pk_add_f16 v77, v97, v118
	v_pk_add_f16 v74, v94, v121
	v_pk_add_f16 v75, v95, v120
	v_pk_add_f16 v76, v96, v119
	v_pk_fma_f16 v57, v101, v121, v57
	v_pk_fma_f16 v56, v100, v120, v56
	v_pk_fma_f16 v55, v99, v119, v55
	v_pk_fma_f16 v54, v98, v118, v54
	v_pk_add_f16 v94, v137, v162 neg_lo:[0,1] neg_hi:[0,1]
	v_pk_add_f16 v95, v136, v163 neg_lo:[0,1] neg_hi:[0,1]
	v_pk_add_f16 v96, v135, v164 neg_lo:[0,1] neg_hi:[0,1]
	v_pk_add_f16 v97, v134, v165 neg_lo:[0,1] neg_hi:[0,1]
	v_exp_f16_sdwa v98, v94 dst_sel:WORD_0 dst_unused:UNUSED_PAD src0_sel:WORD_0
	v_exp_f16_sdwa v99, v95 dst_sel:WORD_0 dst_unused:UNUSED_PAD src0_sel:WORD_0
	v_exp_f16_sdwa v100, v96 dst_sel:WORD_0 dst_unused:UNUSED_PAD src0_sel:WORD_0
	v_exp_f16_sdwa v101, v97 dst_sel:WORD_0 dst_unused:UNUSED_PAD src0_sel:WORD_0
	v_exp_f16_sdwa v98, v94 dst_sel:WORD_1 dst_unused:UNUSED_PRESERVE src0_sel:WORD_1
	v_exp_f16_sdwa v99, v95 dst_sel:WORD_1 dst_unused:UNUSED_PRESERVE src0_sel:WORD_1
	v_exp_f16_sdwa v100, v96 dst_sel:WORD_1 dst_unused:UNUSED_PRESERVE src0_sel:WORD_1
	v_exp_f16_sdwa v101, v97 dst_sel:WORD_1 dst_unused:UNUSED_PRESERVE src0_sel:WORD_1
	v_pk_add_f16 v94, v149, v162 neg_lo:[0,1] neg_hi:[0,1]
	v_pk_add_f16 v77, v77, v98
	v_pk_add_f16 v76, v76, v99
	v_pk_add_f16 v75, v75, v100
	v_pk_add_f16 v74, v74, v101
	v_pk_fma_f16 v54, v30, v98, v54
	v_pk_fma_f16 v55, v31, v99, v55
	v_pk_fma_f16 v56, v32, v100, v56
	v_pk_fma_f16 v57, v33, v101, v57
	v_pk_add_f16 v95, v148, v163 neg_lo:[0,1] neg_hi:[0,1]
	v_pk_add_f16 v96, v147, v164 neg_lo:[0,1] neg_hi:[0,1]
	v_pk_add_f16 v97, v146, v165 neg_lo:[0,1] neg_hi:[0,1]
	v_exp_f16_sdwa v98, v94 dst_sel:WORD_0 dst_unused:UNUSED_PAD src0_sel:WORD_0
	v_exp_f16_sdwa v99, v95 dst_sel:WORD_0 dst_unused:UNUSED_PAD src0_sel:WORD_0
	v_exp_f16_sdwa v100, v96 dst_sel:WORD_0 dst_unused:UNUSED_PAD src0_sel:WORD_0
	v_exp_f16_sdwa v101, v97 dst_sel:WORD_0 dst_unused:UNUSED_PAD src0_sel:WORD_0
	v_exp_f16_sdwa v98, v94 dst_sel:WORD_1 dst_unused:UNUSED_PRESERVE src0_sel:WORD_1
	v_exp_f16_sdwa v99, v95 dst_sel:WORD_1 dst_unused:UNUSED_PRESERVE src0_sel:WORD_1
	v_exp_f16_sdwa v100, v96 dst_sel:WORD_1 dst_unused:UNUSED_PRESERVE src0_sel:WORD_1
	v_exp_f16_sdwa v101, v97 dst_sel:WORD_1 dst_unused:UNUSED_PRESERVE src0_sel:WORD_1
	v_pk_add_f16 v94, v212, v162 neg_lo:[0,1] neg_hi:[0,1]
	v_pk_add_f16 v77, v77, v98
	v_pk_add_f16 v74, v74, v101
	v_pk_add_f16 v75, v75, v100
	v_pk_add_f16 v76, v76, v99
	v_pk_fma_f16 v57, v45, v101, v57
	v_pk_fma_f16 v56, v44, v100, v56
	v_pk_fma_f16 v55, v43, v99, v55
	v_pk_fma_f16 v54, v42, v98, v54
	v_pk_add_f16 v95, v211, v163 neg_lo:[0,1] neg_hi:[0,1]
	v_pk_add_f16 v96, v210, v164 neg_lo:[0,1] neg_hi:[0,1]
	v_pk_add_f16 v97, v209, v165 neg_lo:[0,1] neg_hi:[0,1]
	v_exp_f16_sdwa v98, v94 dst_sel:WORD_0 dst_unused:UNUSED_PAD src0_sel:WORD_0
	v_exp_f16_sdwa v99, v95 dst_sel:WORD_0 dst_unused:UNUSED_PAD src0_sel:WORD_0
	v_exp_f16_sdwa v100, v96 dst_sel:WORD_0 dst_unused:UNUSED_PAD src0_sel:WORD_0
	v_exp_f16_sdwa v101, v97 dst_sel:WORD_0 dst_unused:UNUSED_PAD src0_sel:WORD_0
	v_exp_f16_sdwa v98, v94 dst_sel:WORD_1 dst_unused:UNUSED_PRESERVE src0_sel:WORD_1
	v_exp_f16_sdwa v99, v95 dst_sel:WORD_1 dst_unused:UNUSED_PRESERVE src0_sel:WORD_1
	v_exp_f16_sdwa v100, v96 dst_sel:WORD_1 dst_unused:UNUSED_PRESERVE src0_sel:WORD_1
	v_exp_f16_sdwa v101, v97 dst_sel:WORD_1 dst_unused:UNUSED_PRESERVE src0_sel:WORD_1
	v_exp_f16_sdwa v94, v82 dst_sel:WORD_0 dst_unused:UNUSED_PAD src0_sel:WORD_0
	v_exp_f16_sdwa v95, v83 dst_sel:WORD_0 dst_unused:UNUSED_PAD src0_sel:WORD_0
	v_exp_f16_sdwa v96, v84 dst_sel:WORD_0 dst_unused:UNUSED_PAD src0_sel:WORD_0
	v_exp_f16_sdwa v97, v85 dst_sel:WORD_0 dst_unused:UNUSED_PAD src0_sel:WORD_0
	v_exp_f16_sdwa v94, v82 dst_sel:WORD_1 dst_unused:UNUSED_PRESERVE src0_sel:WORD_1
	v_exp_f16_sdwa v95, v83 dst_sel:WORD_1 dst_unused:UNUSED_PRESERVE src0_sel:WORD_1
	v_exp_f16_sdwa v96, v84 dst_sel:WORD_1 dst_unused:UNUSED_PRESERVE src0_sel:WORD_1
	v_exp_f16_sdwa v97, v85 dst_sel:WORD_1 dst_unused:UNUSED_PRESERVE src0_sel:WORD_1
	v_pk_add_f16 v82, v106, v162 neg_lo:[0,1] neg_hi:[0,1]
	v_pk_add_f16 v77, v77, v98
	v_pk_add_f16 v76, v76, v99
	v_pk_add_f16 v75, v75, v100
	v_pk_add_f16 v74, v74, v101
	v_pk_fma_f16 v54, v58, v98, v54
	v_pk_fma_f16 v55, v59, v99, v55
	v_pk_fma_f16 v56, v60, v100, v56
	v_pk_fma_f16 v57, v61, v101, v57
	v_pk_add_f16 v77, v77, v94
	v_pk_add_f16 v74, v74, v97
	v_pk_add_f16 v75, v75, v96
	v_pk_add_f16 v76, v76, v95
	v_pk_fma_f16 v57, v21, v97, v57
	v_pk_fma_f16 v56, v20, v96, v56
	v_pk_fma_f16 v55, v19, v95, v55
	v_pk_fma_f16 v54, v18, v94, v54
	v_pk_add_f16 v83, v107, v163 neg_lo:[0,1] neg_hi:[0,1]
	v_pk_add_f16 v84, v108, v164 neg_lo:[0,1] neg_hi:[0,1]
	v_pk_add_f16 v85, v109, v165 neg_lo:[0,1] neg_hi:[0,1]
	v_exp_f16_sdwa v94, v82 dst_sel:WORD_0 dst_unused:UNUSED_PAD src0_sel:WORD_0
	v_exp_f16_sdwa v95, v83 dst_sel:WORD_0 dst_unused:UNUSED_PAD src0_sel:WORD_0
	v_exp_f16_sdwa v96, v84 dst_sel:WORD_0 dst_unused:UNUSED_PAD src0_sel:WORD_0
	v_exp_f16_sdwa v97, v85 dst_sel:WORD_0 dst_unused:UNUSED_PAD src0_sel:WORD_0
	v_exp_f16_sdwa v94, v82 dst_sel:WORD_1 dst_unused:UNUSED_PRESERVE src0_sel:WORD_1
	v_exp_f16_sdwa v95, v83 dst_sel:WORD_1 dst_unused:UNUSED_PRESERVE src0_sel:WORD_1
	v_exp_f16_sdwa v96, v84 dst_sel:WORD_1 dst_unused:UNUSED_PRESERVE src0_sel:WORD_1
	v_exp_f16_sdwa v97, v85 dst_sel:WORD_1 dst_unused:UNUSED_PRESERVE src0_sel:WORD_1
	v_pk_add_f16 v82, v122, v162 neg_lo:[0,1] neg_hi:[0,1]
	v_pk_add_f16 v77, v77, v94
	v_pk_add_f16 v76, v76, v95
	v_pk_add_f16 v75, v75, v96
	v_pk_add_f16 v74, v74, v97
	v_pk_fma_f16 v54, v22, v94, v54
	v_pk_fma_f16 v55, v23, v95, v55
	v_pk_fma_f16 v56, v24, v96, v56
	v_pk_fma_f16 v57, v25, v97, v57
	v_pk_add_f16 v83, v123, v163 neg_lo:[0,1] neg_hi:[0,1]
	v_pk_add_f16 v84, v124, v164 neg_lo:[0,1] neg_hi:[0,1]
	v_pk_add_f16 v85, v125, v165 neg_lo:[0,1] neg_hi:[0,1]
	v_exp_f16_sdwa v94, v82 dst_sel:WORD_0 dst_unused:UNUSED_PAD src0_sel:WORD_0
	v_exp_f16_sdwa v95, v83 dst_sel:WORD_0 dst_unused:UNUSED_PAD src0_sel:WORD_0
	v_exp_f16_sdwa v96, v84 dst_sel:WORD_0 dst_unused:UNUSED_PAD src0_sel:WORD_0
	v_exp_f16_sdwa v97, v85 dst_sel:WORD_0 dst_unused:UNUSED_PAD src0_sel:WORD_0
	v_exp_f16_sdwa v94, v82 dst_sel:WORD_1 dst_unused:UNUSED_PRESERVE src0_sel:WORD_1
	v_exp_f16_sdwa v95, v83 dst_sel:WORD_1 dst_unused:UNUSED_PRESERVE src0_sel:WORD_1
	v_exp_f16_sdwa v96, v84 dst_sel:WORD_1 dst_unused:UNUSED_PRESERVE src0_sel:WORD_1
	v_exp_f16_sdwa v97, v85 dst_sel:WORD_1 dst_unused:UNUSED_PRESERVE src0_sel:WORD_1
	v_pk_add_f16 v77, v77, v94
	v_pk_add_f16 v76, v76, v95
	v_rcp_f16_e32 v82, v77
	v_rcp_f16_sdwa v77, v77 dst_sel:DWORD dst_unused:UNUSED_PAD src0_sel:WORD_1
	v_pk_add_f16 v75, v75, v96
	v_rcp_f16_e32 v83, v76
	v_rcp_f16_sdwa v76, v76 dst_sel:DWORD dst_unused:UNUSED_PAD src0_sel:WORD_1
	v_pk_add_f16 v74, v74, v97
	v_rcp_f16_e32 v84, v75
	v_rcp_f16_sdwa v75, v75 dst_sel:DWORD dst_unused:UNUSED_PAD src0_sel:WORD_1
	v_rcp_f16_e32 v85, v74
	v_rcp_f16_sdwa v74, v74 dst_sel:DWORD dst_unused:UNUSED_PAD src0_sel:WORD_1
	v_pk_fma_f16 v54, v26, v94, v54
	v_pack_b32_f16 v77, v82, v77
	v_pk_fma_f16 v57, v29, v97, v57
	v_pk_fma_f16 v55, v27, v95, v55
	v_pk_mul_f16 v97, v54, v77
	v_pack_b32_f16 v54, v83, v76
	v_pk_fma_f16 v56, v28, v96, v56
	v_pk_mul_f16 v96, v55, v54
	v_pack_b32_f16 v54, v84, v75
	v_pk_mul_f16 v95, v56, v54
	v_pack_b32_f16 v54, v85, v74
	v_pk_mul_f16 v94, v57, v54
	s_waitcnt vmcnt(6)
	v_pk_mul_f16 v57, v208, v161 op_sel_hi:[0,1]
	v_pk_mul_f16 v77, v206, v161 op_sel_hi:[0,1]
	v_pk_mul_f16 v85, v207, v161 op_sel_hi:[0,1]
	v_pk_mul_f16 v54, v208, v158 op_sel_hi:[0,1]
	v_pk_mul_f16 v55, v208, v159 op_sel_hi:[0,1]
	v_pk_mul_f16 v56, v208, v160 op_sel_hi:[0,1]
	v_pk_mul_f16 v74, v206, v158 op_sel_hi:[0,1]
	v_pk_mul_f16 v75, v206, v159 op_sel_hi:[0,1]
	v_pk_mul_f16 v76, v206, v160 op_sel_hi:[0,1]
	v_pk_mul_f16 v82, v207, v158 op_sel_hi:[0,1]
	v_pk_mul_f16 v83, v207, v159 op_sel_hi:[0,1]
	v_pk_mul_f16 v84, v207, v160 op_sel_hi:[0,1]
	v_pk_fma_f16 v65, v65, v161, v57
	v_pk_fma_f16 v81, v81, v161, v77
	v_pk_fma_f16 v98, v105, v161, v85
	v_pk_fma_f16 v64, v64, v160, v56
	v_pk_maximum3_f16 v125, v65, v81, v98
	v_pk_fma_f16 v63, v63, v159, v55
	v_pk_fma_f16 v62, v62, v158, v54
	v_pk_fma_f16 v80, v80, v160, v76
	v_pk_fma_f16 v79, v79, v159, v75
	v_pk_fma_f16 v78, v78, v158, v74
	v_pk_fma_f16 v99, v104, v160, v84
	v_pk_fma_f16 v100, v103, v159, v83
	v_pk_fma_f16 v101, v102, v158, v82
	v_pk_fma_f16 v102, v37, v161, v57
	v_pk_fma_f16 v106, v49, v161, v77
	v_pk_fma_f16 v118, v69, v161, v85
	v_pk_fma_f16 v57, v89, v161, v57
	v_pk_fma_f16 v77, v117, v161, v77
	v_pk_fma_f16 v85, v133, v161, v85
	v_pk_maximum3_f16 v122, v62, v78, v101
	v_pk_maximum3_f16 v123, v63, v79, v100
	v_pk_maximum3_f16 v124, v64, v80, v99
	v_pk_maximum3_f16 v129, v102, v106, v118
	v_pk_fma_f16 v103, v36, v160, v56
	v_pk_maximum3_f16 v137, v57, v77, v85
	v_pk_fma_f16 v104, v35, v159, v55
	v_pk_maximum3_f16 v125, v125, v129, v137
	v_pk_fma_f16 v105, v34, v158, v54
	v_pk_fma_f16 v107, v48, v160, v76
	v_pk_fma_f16 v108, v47, v159, v75
	v_pk_fma_f16 v109, v46, v158, v74
	v_pk_fma_f16 v119, v68, v160, v84
	v_pk_fma_f16 v120, v67, v159, v83
	v_pk_fma_f16 v121, v66, v158, v82
	v_pk_fma_f16 v56, v88, v160, v56
	v_pk_fma_f16 v55, v87, v159, v55
	v_pk_fma_f16 v54, v86, v158, v54
	v_pk_fma_f16 v76, v116, v160, v76
	v_pk_fma_f16 v75, v115, v159, v75
	v_pk_fma_f16 v74, v114, v158, v74
	v_pk_fma_f16 v84, v132, v160, v84
	v_pk_fma_f16 v83, v131, v159, v83
	v_pk_fma_f16 v82, v130, v158, v82
	v_pk_maximum3_f16 v126, v105, v109, v121
	v_pk_maximum3_f16 v127, v104, v108, v120
	v_pk_maximum3_f16 v128, v103, v107, v119
	v_pk_maximum3_f16 v135, v55, v75, v83
	v_pk_maximum3_f16 v136, v56, v76, v84
	v_pk_maximum3_f16 v134, v54, v74, v82
	v_pk_maximum3_f16 v122, v122, v126, v134
	v_pk_maximum3_f16 v123, v123, v127, v135
	v_pk_maximum3_f16 v124, v124, v128, v136
	v_pk_add_f16 v65, v65, v125 neg_lo:[0,1] neg_hi:[0,1]
	v_pk_add_f16 v62, v62, v122 neg_lo:[0,1] neg_hi:[0,1]
	v_pk_add_f16 v63, v63, v123 neg_lo:[0,1] neg_hi:[0,1]
	v_pk_add_f16 v64, v64, v124 neg_lo:[0,1] neg_hi:[0,1]
	v_pk_add_f16 v78, v78, v122 neg_lo:[0,1] neg_hi:[0,1]
	v_exp_f16_sdwa v126, v62 dst_sel:WORD_0 dst_unused:UNUSED_PAD src0_sel:WORD_0
	v_exp_f16_sdwa v127, v63 dst_sel:WORD_0 dst_unused:UNUSED_PAD src0_sel:WORD_0
	v_exp_f16_sdwa v128, v64 dst_sel:WORD_0 dst_unused:UNUSED_PAD src0_sel:WORD_0
	v_exp_f16_sdwa v129, v65 dst_sel:WORD_0 dst_unused:UNUSED_PAD src0_sel:WORD_0
	v_exp_f16_sdwa v126, v62 dst_sel:WORD_1 dst_unused:UNUSED_PRESERVE src0_sel:WORD_1
	v_exp_f16_sdwa v127, v63 dst_sel:WORD_1 dst_unused:UNUSED_PRESERVE src0_sel:WORD_1
	v_exp_f16_sdwa v128, v64 dst_sel:WORD_1 dst_unused:UNUSED_PRESERVE src0_sel:WORD_1
	v_exp_f16_sdwa v129, v65 dst_sel:WORD_1 dst_unused:UNUSED_PRESERVE src0_sel:WORD_1
	v_pk_add_f16 v79, v79, v123 neg_lo:[0,1] neg_hi:[0,1]
	v_pk_add_f16 v65, v126, 0
	v_pk_fma_f16 v33, v33, v129, 0
	v_pk_add_f16 v62, v129, 0
	v_pk_add_f16 v63, v128, 0
	v_pk_add_f16 v64, v127, 0
	v_pk_fma_f16 v32, v32, v128, 0
	v_pk_fma_f16 v31, v31, v127, 0
	v_pk_fma_f16 v30, v30, v126, 0
	v_pk_add_f16 v80, v80, v124 neg_lo:[0,1] neg_hi:[0,1]
	v_pk_add_f16 v81, v81, v125 neg_lo:[0,1] neg_hi:[0,1]
	v_pk_add_f16 v54, v54, v122 neg_lo:[0,1] neg_hi:[0,1]
	v_exp_f16_sdwa v126, v78 dst_sel:WORD_0 dst_unused:UNUSED_PAD src0_sel:WORD_0
	v_exp_f16_sdwa v127, v79 dst_sel:WORD_0 dst_unused:UNUSED_PAD src0_sel:WORD_0
	v_exp_f16_sdwa v128, v80 dst_sel:WORD_0 dst_unused:UNUSED_PAD src0_sel:WORD_0
	v_exp_f16_sdwa v129, v81 dst_sel:WORD_0 dst_unused:UNUSED_PAD src0_sel:WORD_0
	v_exp_f16_sdwa v126, v78 dst_sel:WORD_1 dst_unused:UNUSED_PRESERVE src0_sel:WORD_1
	v_exp_f16_sdwa v127, v79 dst_sel:WORD_1 dst_unused:UNUSED_PRESERVE src0_sel:WORD_1
	v_exp_f16_sdwa v128, v80 dst_sel:WORD_1 dst_unused:UNUSED_PRESERVE src0_sel:WORD_1
	v_exp_f16_sdwa v129, v81 dst_sel:WORD_1 dst_unused:UNUSED_PRESERVE src0_sel:WORD_1
	v_pk_add_f16 v55, v55, v123 neg_lo:[0,1] neg_hi:[0,1]
	v_pk_add_f16 v65, v65, v126
	v_pk_fma_f16 v33, v45, v129, v33
	v_pk_add_f16 v45, v98, v125 neg_lo:[0,1] neg_hi:[0,1]
	v_pk_add_f16 v64, v64, v127
	v_pk_add_f16 v63, v63, v128
	v_pk_add_f16 v62, v62, v129
	v_pk_fma_f16 v30, v42, v126, v30
	v_pk_fma_f16 v31, v43, v127, v31
	v_pk_fma_f16 v32, v44, v128, v32
	v_pk_add_f16 v42, v101, v122 neg_lo:[0,1] neg_hi:[0,1]
	v_pk_add_f16 v43, v100, v123 neg_lo:[0,1] neg_hi:[0,1]
	v_pk_add_f16 v44, v99, v124 neg_lo:[0,1] neg_hi:[0,1]
	v_pk_add_f16 v56, v56, v124 neg_lo:[0,1] neg_hi:[0,1]
	v_exp_f16_sdwa v78, v42 dst_sel:WORD_0 dst_unused:UNUSED_PAD src0_sel:WORD_0
	v_exp_f16_sdwa v79, v43 dst_sel:WORD_0 dst_unused:UNUSED_PAD src0_sel:WORD_0
	v_exp_f16_sdwa v80, v44 dst_sel:WORD_0 dst_unused:UNUSED_PAD src0_sel:WORD_0
	v_exp_f16_sdwa v81, v45 dst_sel:WORD_0 dst_unused:UNUSED_PAD src0_sel:WORD_0
	v_exp_f16_sdwa v78, v42 dst_sel:WORD_1 dst_unused:UNUSED_PRESERVE src0_sel:WORD_1
	v_exp_f16_sdwa v79, v43 dst_sel:WORD_1 dst_unused:UNUSED_PRESERVE src0_sel:WORD_1
	v_exp_f16_sdwa v80, v44 dst_sel:WORD_1 dst_unused:UNUSED_PRESERVE src0_sel:WORD_1
	v_exp_f16_sdwa v81, v45 dst_sel:WORD_1 dst_unused:UNUSED_PRESERVE src0_sel:WORD_1
	v_pk_add_f16 v57, v57, v125 neg_lo:[0,1] neg_hi:[0,1]
	v_pk_add_f16 v45, v65, v78
	v_pk_add_f16 v42, v62, v81
	v_pk_add_f16 v43, v63, v80
	v_pk_add_f16 v44, v64, v79
	v_pk_fma_f16 v33, v61, v81, v33
	v_pk_fma_f16 v32, v60, v80, v32
	v_pk_fma_f16 v31, v59, v79, v31
	v_pk_fma_f16 v30, v58, v78, v30
	v_pk_add_f16 v58, v105, v122 neg_lo:[0,1] neg_hi:[0,1]
	v_pk_add_f16 v59, v104, v123 neg_lo:[0,1] neg_hi:[0,1]
	v_pk_add_f16 v60, v103, v124 neg_lo:[0,1] neg_hi:[0,1]
	v_pk_add_f16 v61, v102, v125 neg_lo:[0,1] neg_hi:[0,1]
	v_exp_f16_sdwa v62, v58 dst_sel:WORD_0 dst_unused:UNUSED_PAD src0_sel:WORD_0
	v_exp_f16_sdwa v63, v59 dst_sel:WORD_0 dst_unused:UNUSED_PAD src0_sel:WORD_0
	v_exp_f16_sdwa v64, v60 dst_sel:WORD_0 dst_unused:UNUSED_PAD src0_sel:WORD_0
	v_exp_f16_sdwa v65, v61 dst_sel:WORD_0 dst_unused:UNUSED_PAD src0_sel:WORD_0
	v_exp_f16_sdwa v62, v58 dst_sel:WORD_1 dst_unused:UNUSED_PRESERVE src0_sel:WORD_1
	v_exp_f16_sdwa v63, v59 dst_sel:WORD_1 dst_unused:UNUSED_PRESERVE src0_sel:WORD_1
	v_exp_f16_sdwa v64, v60 dst_sel:WORD_1 dst_unused:UNUSED_PRESERVE src0_sel:WORD_1
	v_exp_f16_sdwa v65, v61 dst_sel:WORD_1 dst_unused:UNUSED_PRESERVE src0_sel:WORD_1
	v_pk_add_f16 v58, v109, v122 neg_lo:[0,1] neg_hi:[0,1]
	v_pk_add_f16 v45, v45, v62
	v_pk_add_f16 v44, v44, v63
	v_pk_add_f16 v43, v43, v64
	v_pk_add_f16 v42, v42, v65
	v_pk_fma_f16 v30, v18, v62, v30
	v_pk_fma_f16 v31, v19, v63, v31
	v_pk_fma_f16 v32, v20, v64, v32
	v_pk_fma_f16 v33, v21, v65, v33
	v_pk_add_f16 v59, v108, v123 neg_lo:[0,1] neg_hi:[0,1]
	v_pk_add_f16 v60, v107, v124 neg_lo:[0,1] neg_hi:[0,1]
	v_pk_add_f16 v61, v106, v125 neg_lo:[0,1] neg_hi:[0,1]
	v_exp_f16_sdwa v62, v58 dst_sel:WORD_0 dst_unused:UNUSED_PAD src0_sel:WORD_0
	v_exp_f16_sdwa v63, v59 dst_sel:WORD_0 dst_unused:UNUSED_PAD src0_sel:WORD_0
	v_exp_f16_sdwa v64, v60 dst_sel:WORD_0 dst_unused:UNUSED_PAD src0_sel:WORD_0
	v_exp_f16_sdwa v65, v61 dst_sel:WORD_0 dst_unused:UNUSED_PAD src0_sel:WORD_0
	v_exp_f16_sdwa v62, v58 dst_sel:WORD_1 dst_unused:UNUSED_PRESERVE src0_sel:WORD_1
	v_exp_f16_sdwa v63, v59 dst_sel:WORD_1 dst_unused:UNUSED_PRESERVE src0_sel:WORD_1
	v_exp_f16_sdwa v64, v60 dst_sel:WORD_1 dst_unused:UNUSED_PRESERVE src0_sel:WORD_1
	v_exp_f16_sdwa v65, v61 dst_sel:WORD_1 dst_unused:UNUSED_PRESERVE src0_sel:WORD_1
	v_pk_add_f16 v58, v121, v122 neg_lo:[0,1] neg_hi:[0,1]
	v_pk_add_f16 v45, v45, v62
	v_pk_add_f16 v42, v42, v65
	v_pk_add_f16 v43, v43, v64
	v_pk_add_f16 v44, v44, v63
	v_pk_fma_f16 v33, v25, v65, v33
	v_pk_fma_f16 v32, v24, v64, v32
	v_pk_fma_f16 v31, v23, v63, v31
	v_pk_fma_f16 v30, v22, v62, v30
	v_pk_add_f16 v59, v120, v123 neg_lo:[0,1] neg_hi:[0,1]
	v_pk_add_f16 v60, v119, v124 neg_lo:[0,1] neg_hi:[0,1]
	v_pk_add_f16 v61, v118, v125 neg_lo:[0,1] neg_hi:[0,1]
	v_exp_f16_sdwa v62, v58 dst_sel:WORD_0 dst_unused:UNUSED_PAD src0_sel:WORD_0
	v_exp_f16_sdwa v63, v59 dst_sel:WORD_0 dst_unused:UNUSED_PAD src0_sel:WORD_0
	v_exp_f16_sdwa v64, v60 dst_sel:WORD_0 dst_unused:UNUSED_PAD src0_sel:WORD_0
	v_exp_f16_sdwa v65, v61 dst_sel:WORD_0 dst_unused:UNUSED_PAD src0_sel:WORD_0
	v_exp_f16_sdwa v62, v58 dst_sel:WORD_1 dst_unused:UNUSED_PRESERVE src0_sel:WORD_1
	v_exp_f16_sdwa v63, v59 dst_sel:WORD_1 dst_unused:UNUSED_PRESERVE src0_sel:WORD_1
	v_exp_f16_sdwa v64, v60 dst_sel:WORD_1 dst_unused:UNUSED_PRESERVE src0_sel:WORD_1
	v_exp_f16_sdwa v65, v61 dst_sel:WORD_1 dst_unused:UNUSED_PRESERVE src0_sel:WORD_1
	v_exp_f16_sdwa v58, v54 dst_sel:WORD_0 dst_unused:UNUSED_PAD src0_sel:WORD_0
	v_exp_f16_sdwa v59, v55 dst_sel:WORD_0 dst_unused:UNUSED_PAD src0_sel:WORD_0
	v_exp_f16_sdwa v60, v56 dst_sel:WORD_0 dst_unused:UNUSED_PAD src0_sel:WORD_0
	v_exp_f16_sdwa v61, v57 dst_sel:WORD_0 dst_unused:UNUSED_PAD src0_sel:WORD_0
	v_exp_f16_sdwa v58, v54 dst_sel:WORD_1 dst_unused:UNUSED_PRESERVE src0_sel:WORD_1
	v_exp_f16_sdwa v59, v55 dst_sel:WORD_1 dst_unused:UNUSED_PRESERVE src0_sel:WORD_1
	v_exp_f16_sdwa v60, v56 dst_sel:WORD_1 dst_unused:UNUSED_PRESERVE src0_sel:WORD_1
	v_exp_f16_sdwa v61, v57 dst_sel:WORD_1 dst_unused:UNUSED_PRESERVE src0_sel:WORD_1
	v_pk_add_f16 v54, v74, v122 neg_lo:[0,1] neg_hi:[0,1]
	v_pk_add_f16 v45, v45, v62
	v_pk_add_f16 v44, v44, v63
	v_pk_add_f16 v43, v43, v64
	v_pk_add_f16 v42, v42, v65
	v_pk_fma_f16 v30, v26, v62, v30
	v_pk_fma_f16 v31, v27, v63, v31
	v_pk_fma_f16 v32, v28, v64, v32
	v_pk_fma_f16 v33, v29, v65, v33
	v_pk_add_f16 v45, v45, v58
	v_pk_add_f16 v42, v42, v61
	v_pk_add_f16 v43, v43, v60
	v_pk_add_f16 v44, v44, v59
	v_pk_fma_f16 v33, v41, v61, v33
	v_pk_fma_f16 v32, v40, v60, v32
	v_pk_fma_f16 v31, v39, v59, v31
	v_pk_fma_f16 v30, v38, v58, v30
	v_pk_add_f16 v55, v75, v123 neg_lo:[0,1] neg_hi:[0,1]
	v_pk_add_f16 v56, v76, v124 neg_lo:[0,1] neg_hi:[0,1]
	v_pk_add_f16 v57, v77, v125 neg_lo:[0,1] neg_hi:[0,1]
	v_exp_f16_sdwa v58, v54 dst_sel:WORD_0 dst_unused:UNUSED_PAD src0_sel:WORD_0
	v_exp_f16_sdwa v59, v55 dst_sel:WORD_0 dst_unused:UNUSED_PAD src0_sel:WORD_0
	v_exp_f16_sdwa v60, v56 dst_sel:WORD_0 dst_unused:UNUSED_PAD src0_sel:WORD_0
	v_exp_f16_sdwa v61, v57 dst_sel:WORD_0 dst_unused:UNUSED_PAD src0_sel:WORD_0
	v_exp_f16_sdwa v58, v54 dst_sel:WORD_1 dst_unused:UNUSED_PRESERVE src0_sel:WORD_1
	v_exp_f16_sdwa v59, v55 dst_sel:WORD_1 dst_unused:UNUSED_PRESERVE src0_sel:WORD_1
	v_exp_f16_sdwa v60, v56 dst_sel:WORD_1 dst_unused:UNUSED_PRESERVE src0_sel:WORD_1
	v_exp_f16_sdwa v61, v57 dst_sel:WORD_1 dst_unused:UNUSED_PRESERVE src0_sel:WORD_1
	v_pk_add_f16 v54, v82, v122 neg_lo:[0,1] neg_hi:[0,1]
	v_pk_add_f16 v45, v45, v58
	v_pk_add_f16 v44, v44, v59
	v_pk_add_f16 v43, v43, v60
	v_pk_add_f16 v42, v42, v61
	v_pk_fma_f16 v30, v50, v58, v30
	v_pk_fma_f16 v31, v51, v59, v31
	v_pk_fma_f16 v32, v52, v60, v32
	v_pk_fma_f16 v33, v53, v61, v33
	v_pk_add_f16 v55, v83, v123 neg_lo:[0,1] neg_hi:[0,1]
	v_pk_add_f16 v56, v84, v124 neg_lo:[0,1] neg_hi:[0,1]
	v_pk_add_f16 v57, v85, v125 neg_lo:[0,1] neg_hi:[0,1]
	v_exp_f16_sdwa v58, v54 dst_sel:WORD_0 dst_unused:UNUSED_PAD src0_sel:WORD_0
	v_exp_f16_sdwa v59, v55 dst_sel:WORD_0 dst_unused:UNUSED_PAD src0_sel:WORD_0
	v_exp_f16_sdwa v60, v56 dst_sel:WORD_0 dst_unused:UNUSED_PAD src0_sel:WORD_0
	v_exp_f16_sdwa v61, v57 dst_sel:WORD_0 dst_unused:UNUSED_PAD src0_sel:WORD_0
	v_exp_f16_sdwa v58, v54 dst_sel:WORD_1 dst_unused:UNUSED_PRESERVE src0_sel:WORD_1
	v_exp_f16_sdwa v59, v55 dst_sel:WORD_1 dst_unused:UNUSED_PRESERVE src0_sel:WORD_1
	v_exp_f16_sdwa v60, v56 dst_sel:WORD_1 dst_unused:UNUSED_PRESERVE src0_sel:WORD_1
	v_exp_f16_sdwa v61, v57 dst_sel:WORD_1 dst_unused:UNUSED_PRESERVE src0_sel:WORD_1
	v_pk_add_f16 v45, v45, v58
	v_pk_add_f16 v44, v44, v59
	v_rcp_f16_e32 v54, v45
	v_rcp_f16_sdwa v45, v45 dst_sel:DWORD dst_unused:UNUSED_PAD src0_sel:WORD_1
	v_pk_add_f16 v43, v43, v60
	v_rcp_f16_e32 v55, v44
	v_rcp_f16_sdwa v44, v44 dst_sel:DWORD dst_unused:UNUSED_PAD src0_sel:WORD_1
	v_pk_add_f16 v42, v42, v61
	v_rcp_f16_e32 v56, v43
	v_rcp_f16_sdwa v43, v43 dst_sel:DWORD dst_unused:UNUSED_PAD src0_sel:WORD_1
	v_rcp_f16_e32 v57, v42
	v_rcp_f16_sdwa v42, v42 dst_sel:DWORD dst_unused:UNUSED_PAD src0_sel:WORD_1
	v_pk_fma_f16 v30, v70, v58, v30
	v_pack_b32_f16 v45, v54, v45
	v_pk_fma_f16 v31, v71, v59, v31
	v_pk_mul_f16 v45, v30, v45
	v_pack_b32_f16 v30, v55, v44
	v_pk_fma_f16 v32, v72, v60, v32
	v_pk_mul_f16 v44, v31, v30
	v_pack_b32_f16 v30, v56, v43
	v_pk_fma_f16 v33, v73, v61, v33
	v_pk_mul_f16 v43, v32, v30
	v_pack_b32_f16 v30, v57, v42
	v_pk_mul_f16 v42, v33, v30
	s_waitcnt vmcnt(0)
	v_pk_mul_f16 v30, v208, v154 op_sel_hi:[0,1]
	v_pk_mul_f16 v31, v208, v155 op_sel_hi:[0,1]
	v_pk_mul_f16 v32, v208, v156 op_sel_hi:[0,1]
	v_pk_mul_f16 v33, v208, v157 op_sel_hi:[0,1]
	v_pk_mul_f16 v54, v206, v154 op_sel_hi:[0,1]
	v_pk_mul_f16 v55, v206, v155 op_sel_hi:[0,1]
	v_pk_mul_f16 v56, v206, v156 op_sel_hi:[0,1]
	v_pk_mul_f16 v57, v206, v157 op_sel_hi:[0,1]
	v_pk_mul_f16 v58, v207, v154 op_sel_hi:[0,1]
	v_pk_mul_f16 v59, v207, v155 op_sel_hi:[0,1]
	v_pk_mul_f16 v60, v207, v156 op_sel_hi:[0,1]
	v_pk_mul_f16 v61, v207, v157 op_sel_hi:[0,1]
	v_pk_fma_f16 v37, v37, v157, v33
	v_pk_fma_f16 v36, v36, v156, v32
	v_pk_fma_f16 v35, v35, v155, v31
	v_pk_fma_f16 v34, v34, v154, v30
	v_pk_fma_f16 v49, v49, v157, v57
	v_pk_fma_f16 v48, v48, v156, v56
	v_pk_fma_f16 v47, v47, v155, v55
	v_pk_fma_f16 v46, v46, v154, v54
	v_pk_fma_f16 v62, v69, v157, v61
	v_pk_fma_f16 v63, v68, v156, v60
	v_pk_fma_f16 v64, v67, v155, v59
	v_pk_fma_f16 v65, v66, v154, v58
	v_pk_fma_f16 v66, v89, v157, v33
	v_pk_fma_f16 v67, v88, v156, v32
	v_pk_fma_f16 v68, v87, v155, v31
	v_pk_fma_f16 v69, v86, v154, v30
	v_pk_fma_f16 v74, v117, v157, v57
	v_pk_fma_f16 v75, v116, v156, v56
	v_pk_fma_f16 v76, v115, v155, v55
	v_pk_fma_f16 v77, v114, v154, v54
	v_pk_fma_f16 v78, v133, v157, v61
	v_pk_fma_f16 v79, v132, v156, v60
	v_pk_fma_f16 v80, v131, v155, v59
	v_pk_fma_f16 v81, v130, v154, v58
	v_pk_fma_f16 v61, v17, v157, v61
	v_pk_fma_f16 v60, v16, v156, v60
	v_pk_fma_f16 v59, v15, v155, v59
	v_pk_fma_f16 v58, v14, v154, v58
	v_pk_maximum3_f16 v14, v34, v46, v65
	v_pk_maximum3_f16 v15, v35, v47, v64
	v_pk_maximum3_f16 v16, v36, v48, v63
	v_pk_maximum3_f16 v17, v37, v49, v62
	v_pk_maximum3_f16 v82, v69, v77, v81
	v_pk_maximum3_f16 v83, v68, v76, v80
	v_pk_maximum3_f16 v84, v67, v75, v79
	v_pk_maximum3_f16 v85, v66, v74, v78
	v_pk_fma_f16 v33, v145, v157, v33
	v_pk_fma_f16 v32, v144, v156, v32
	v_pk_fma_f16 v31, v143, v155, v31
	v_pk_fma_f16 v30, v142, v154, v30
	v_pk_fma_f16 v57, v153, v157, v57
	v_pk_fma_f16 v56, v152, v156, v56
	v_pk_fma_f16 v55, v151, v155, v55
	v_pk_fma_f16 v54, v150, v154, v54
	v_pk_maximum3_f16 v87, v31, v55, v59
	v_pk_maximum3_f16 v88, v32, v56, v60
	v_pk_maximum3_f16 v89, v33, v57, v61
	v_pk_maximum3_f16 v86, v30, v54, v58
	v_pk_maximum3_f16 v15, v15, v83, v87
	v_pk_maximum3_f16 v16, v16, v84, v88
	v_pk_maximum3_f16 v17, v17, v85, v89
	v_pk_maximum3_f16 v14, v14, v82, v86
	v_xor_b32_e32 v82, 0x80008000, v17
	v_xor_b32_e32 v83, 0x80008000, v16
	v_xor_b32_e32 v84, 0x80008000, v15
	v_xor_b32_e32 v85, 0x80008000, v14
	v_pk_add_f16 v14, v34, v85
	v_pk_add_f16 v15, v35, v84
	v_pk_add_f16 v16, v36, v83
	v_pk_add_f16 v17, v37, v82
	v_exp_f16_sdwa v34, v14 dst_sel:WORD_0 dst_unused:UNUSED_PAD src0_sel:WORD_0
	v_exp_f16_sdwa v35, v15 dst_sel:WORD_0 dst_unused:UNUSED_PAD src0_sel:WORD_0
	v_exp_f16_sdwa v36, v16 dst_sel:WORD_0 dst_unused:UNUSED_PAD src0_sel:WORD_0
	v_exp_f16_sdwa v37, v17 dst_sel:WORD_0 dst_unused:UNUSED_PAD src0_sel:WORD_0
	v_exp_f16_sdwa v34, v14 dst_sel:WORD_1 dst_unused:UNUSED_PRESERVE src0_sel:WORD_1
	v_exp_f16_sdwa v35, v15 dst_sel:WORD_1 dst_unused:UNUSED_PRESERVE src0_sel:WORD_1
	v_exp_f16_sdwa v36, v16 dst_sel:WORD_1 dst_unused:UNUSED_PRESERVE src0_sel:WORD_1
	v_exp_f16_sdwa v37, v17 dst_sel:WORD_1 dst_unused:UNUSED_PRESERVE src0_sel:WORD_1
	v_pk_add_f16 v14, v34, 0
	v_pk_add_f16 v15, v35, 0
	v_pk_add_f16 v16, v36, 0
	v_pk_add_f16 v17, v37, 0
	v_pk_fma_f16 v18, v18, v34, 0
	v_pk_fma_f16 v19, v19, v35, 0
	v_pk_fma_f16 v20, v20, v36, 0
	v_pk_fma_f16 v21, v21, v37, 0
	v_pk_add_f16 v34, v46, v85
	v_pk_add_f16 v35, v47, v84
	v_pk_add_f16 v36, v48, v83
	v_pk_add_f16 v37, v49, v82
	v_exp_f16_sdwa v46, v34 dst_sel:WORD_0 dst_unused:UNUSED_PAD src0_sel:WORD_0
	v_exp_f16_sdwa v47, v35 dst_sel:WORD_0 dst_unused:UNUSED_PAD src0_sel:WORD_0
	v_exp_f16_sdwa v48, v36 dst_sel:WORD_0 dst_unused:UNUSED_PAD src0_sel:WORD_0
	v_exp_f16_sdwa v49, v37 dst_sel:WORD_0 dst_unused:UNUSED_PAD src0_sel:WORD_0
	v_exp_f16_sdwa v46, v34 dst_sel:WORD_1 dst_unused:UNUSED_PRESERVE src0_sel:WORD_1
	v_exp_f16_sdwa v47, v35 dst_sel:WORD_1 dst_unused:UNUSED_PRESERVE src0_sel:WORD_1
	v_exp_f16_sdwa v48, v36 dst_sel:WORD_1 dst_unused:UNUSED_PRESERVE src0_sel:WORD_1
	v_exp_f16_sdwa v49, v37 dst_sel:WORD_1 dst_unused:UNUSED_PRESERVE src0_sel:WORD_1
	s_nop 0
	v_pk_add_f16 v17, v17, v49
	v_pk_add_f16 v16, v16, v48
	v_pk_add_f16 v15, v15, v47
	v_pk_add_f16 v14, v14, v46
	v_pk_fma_f16 v21, v25, v49, v21
	v_pk_fma_f16 v20, v24, v48, v20
	v_pk_fma_f16 v19, v23, v47, v19
	v_pk_fma_f16 v18, v22, v46, v18
	v_pk_add_f16 v22, v65, v85
	v_pk_add_f16 v23, v64, v84
	v_pk_add_f16 v24, v63, v83
	v_pk_add_f16 v25, v62, v82
	v_exp_f16_sdwa v34, v22 dst_sel:WORD_0 dst_unused:UNUSED_PAD src0_sel:WORD_0
	v_exp_f16_sdwa v35, v23 dst_sel:WORD_0 dst_unused:UNUSED_PAD src0_sel:WORD_0
	v_exp_f16_sdwa v36, v24 dst_sel:WORD_0 dst_unused:UNUSED_PAD src0_sel:WORD_0
	v_exp_f16_sdwa v37, v25 dst_sel:WORD_0 dst_unused:UNUSED_PAD src0_sel:WORD_0
	v_exp_f16_sdwa v34, v22 dst_sel:WORD_1 dst_unused:UNUSED_PRESERVE src0_sel:WORD_1
	v_exp_f16_sdwa v35, v23 dst_sel:WORD_1 dst_unused:UNUSED_PRESERVE src0_sel:WORD_1
	v_exp_f16_sdwa v36, v24 dst_sel:WORD_1 dst_unused:UNUSED_PRESERVE src0_sel:WORD_1
	v_exp_f16_sdwa v37, v25 dst_sel:WORD_1 dst_unused:UNUSED_PRESERVE src0_sel:WORD_1
	v_pk_add_f16 v22, v69, v85
	v_pk_add_f16 v14, v14, v34
	v_pk_add_f16 v15, v15, v35
	v_pk_add_f16 v16, v16, v36
	v_pk_add_f16 v17, v17, v37
	v_pk_fma_f16 v18, v26, v34, v18
	v_pk_fma_f16 v19, v27, v35, v19
	v_pk_fma_f16 v20, v28, v36, v20
	v_pk_fma_f16 v21, v29, v37, v21
	v_pk_add_f16 v23, v68, v84
	v_pk_add_f16 v24, v67, v83
	v_pk_add_f16 v25, v66, v82
	v_exp_f16_sdwa v26, v22 dst_sel:WORD_0 dst_unused:UNUSED_PAD src0_sel:WORD_0
	v_exp_f16_sdwa v27, v23 dst_sel:WORD_0 dst_unused:UNUSED_PAD src0_sel:WORD_0
	v_exp_f16_sdwa v28, v24 dst_sel:WORD_0 dst_unused:UNUSED_PAD src0_sel:WORD_0
	v_exp_f16_sdwa v29, v25 dst_sel:WORD_0 dst_unused:UNUSED_PAD src0_sel:WORD_0
	v_exp_f16_sdwa v26, v22 dst_sel:WORD_1 dst_unused:UNUSED_PRESERVE src0_sel:WORD_1
	v_exp_f16_sdwa v27, v23 dst_sel:WORD_1 dst_unused:UNUSED_PRESERVE src0_sel:WORD_1
	v_exp_f16_sdwa v28, v24 dst_sel:WORD_1 dst_unused:UNUSED_PRESERVE src0_sel:WORD_1
	v_exp_f16_sdwa v29, v25 dst_sel:WORD_1 dst_unused:UNUSED_PRESERVE src0_sel:WORD_1
	v_pk_add_f16 v22, v77, v85
	v_pk_add_f16 v17, v17, v29
	v_pk_add_f16 v16, v16, v28
	v_pk_add_f16 v15, v15, v27
	v_pk_add_f16 v14, v14, v26
	v_pk_fma_f16 v21, v41, v29, v21
	v_pk_fma_f16 v20, v40, v28, v20
	v_pk_fma_f16 v19, v39, v27, v19
	v_pk_fma_f16 v18, v38, v26, v18
	v_pk_add_f16 v23, v76, v84
	v_pk_add_f16 v24, v75, v83
	v_pk_add_f16 v25, v74, v82
	v_exp_f16_sdwa v26, v22 dst_sel:WORD_0 dst_unused:UNUSED_PAD src0_sel:WORD_0
	v_exp_f16_sdwa v27, v23 dst_sel:WORD_0 dst_unused:UNUSED_PAD src0_sel:WORD_0
	v_exp_f16_sdwa v28, v24 dst_sel:WORD_0 dst_unused:UNUSED_PAD src0_sel:WORD_0
	v_exp_f16_sdwa v29, v25 dst_sel:WORD_0 dst_unused:UNUSED_PAD src0_sel:WORD_0
	v_exp_f16_sdwa v26, v22 dst_sel:WORD_1 dst_unused:UNUSED_PRESERVE src0_sel:WORD_1
	v_exp_f16_sdwa v27, v23 dst_sel:WORD_1 dst_unused:UNUSED_PRESERVE src0_sel:WORD_1
	v_exp_f16_sdwa v28, v24 dst_sel:WORD_1 dst_unused:UNUSED_PRESERVE src0_sel:WORD_1
	v_exp_f16_sdwa v29, v25 dst_sel:WORD_1 dst_unused:UNUSED_PRESERVE src0_sel:WORD_1
	v_pk_add_f16 v22, v81, v85
	v_pk_add_f16 v14, v14, v26
	v_pk_add_f16 v15, v15, v27
	v_pk_add_f16 v16, v16, v28
	v_pk_add_f16 v17, v17, v29
	v_pk_fma_f16 v18, v50, v26, v18
	v_pk_fma_f16 v19, v51, v27, v19
	v_pk_fma_f16 v20, v52, v28, v20
	v_pk_fma_f16 v21, v53, v29, v21
	v_pk_add_f16 v23, v80, v84
	v_pk_add_f16 v24, v79, v83
	v_pk_add_f16 v25, v78, v82
	v_exp_f16_sdwa v26, v22 dst_sel:WORD_0 dst_unused:UNUSED_PAD src0_sel:WORD_0
	v_exp_f16_sdwa v27, v23 dst_sel:WORD_0 dst_unused:UNUSED_PAD src0_sel:WORD_0
	v_exp_f16_sdwa v28, v24 dst_sel:WORD_0 dst_unused:UNUSED_PAD src0_sel:WORD_0
	v_exp_f16_sdwa v29, v25 dst_sel:WORD_0 dst_unused:UNUSED_PAD src0_sel:WORD_0
	v_exp_f16_sdwa v26, v22 dst_sel:WORD_1 dst_unused:UNUSED_PRESERVE src0_sel:WORD_1
	v_exp_f16_sdwa v27, v23 dst_sel:WORD_1 dst_unused:UNUSED_PRESERVE src0_sel:WORD_1
	v_exp_f16_sdwa v28, v24 dst_sel:WORD_1 dst_unused:UNUSED_PRESERVE src0_sel:WORD_1
	v_exp_f16_sdwa v29, v25 dst_sel:WORD_1 dst_unused:UNUSED_PRESERVE src0_sel:WORD_1
	v_pk_add_f16 v22, v30, v85
	v_pk_add_f16 v17, v17, v29
	v_pk_add_f16 v16, v16, v28
	v_pk_add_f16 v15, v15, v27
	v_pk_add_f16 v14, v14, v26
	v_pk_fma_f16 v21, v73, v29, v21
	v_pk_fma_f16 v20, v72, v28, v20
	v_pk_fma_f16 v19, v71, v27, v19
	v_pk_fma_f16 v18, v70, v26, v18
	v_pk_add_f16 v23, v31, v84
	v_pk_add_f16 v24, v32, v83
	v_pk_add_f16 v25, v33, v82
	v_exp_f16_sdwa v26, v22 dst_sel:WORD_0 dst_unused:UNUSED_PAD src0_sel:WORD_0
	v_exp_f16_sdwa v27, v23 dst_sel:WORD_0 dst_unused:UNUSED_PAD src0_sel:WORD_0
	v_exp_f16_sdwa v28, v24 dst_sel:WORD_0 dst_unused:UNUSED_PAD src0_sel:WORD_0
	v_exp_f16_sdwa v29, v25 dst_sel:WORD_0 dst_unused:UNUSED_PAD src0_sel:WORD_0
	v_exp_f16_sdwa v26, v22 dst_sel:WORD_1 dst_unused:UNUSED_PRESERVE src0_sel:WORD_1
	v_exp_f16_sdwa v27, v23 dst_sel:WORD_1 dst_unused:UNUSED_PRESERVE src0_sel:WORD_1
	v_exp_f16_sdwa v28, v24 dst_sel:WORD_1 dst_unused:UNUSED_PRESERVE src0_sel:WORD_1
	v_exp_f16_sdwa v29, v25 dst_sel:WORD_1 dst_unused:UNUSED_PRESERVE src0_sel:WORD_1
	v_pk_add_f16 v22, v54, v85
	v_pk_add_f16 v14, v14, v26
	v_pk_add_f16 v15, v15, v27
	v_pk_add_f16 v16, v16, v28
	v_pk_add_f16 v17, v17, v29
	v_pk_fma_f16 v18, v90, v26, v18
	v_pk_fma_f16 v19, v91, v27, v19
	v_pk_fma_f16 v20, v92, v28, v20
	v_pk_fma_f16 v21, v93, v29, v21
	v_pk_add_f16 v23, v55, v84
	v_pk_add_f16 v24, v56, v83
	v_pk_add_f16 v25, v57, v82
	v_exp_f16_sdwa v26, v22 dst_sel:WORD_0 dst_unused:UNUSED_PAD src0_sel:WORD_0
	v_exp_f16_sdwa v27, v23 dst_sel:WORD_0 dst_unused:UNUSED_PAD src0_sel:WORD_0
	v_exp_f16_sdwa v28, v24 dst_sel:WORD_0 dst_unused:UNUSED_PAD src0_sel:WORD_0
	v_exp_f16_sdwa v29, v25 dst_sel:WORD_0 dst_unused:UNUSED_PAD src0_sel:WORD_0
	v_exp_f16_sdwa v26, v22 dst_sel:WORD_1 dst_unused:UNUSED_PRESERVE src0_sel:WORD_1
	v_exp_f16_sdwa v27, v23 dst_sel:WORD_1 dst_unused:UNUSED_PRESERVE src0_sel:WORD_1
	v_exp_f16_sdwa v28, v24 dst_sel:WORD_1 dst_unused:UNUSED_PRESERVE src0_sel:WORD_1
	v_exp_f16_sdwa v29, v25 dst_sel:WORD_1 dst_unused:UNUSED_PRESERVE src0_sel:WORD_1
	s_nop 0
	v_pk_add_f16 v17, v17, v29
	v_pk_add_f16 v16, v16, v28
	v_pk_add_f16 v15, v15, v27
	v_pk_add_f16 v14, v14, v26
	v_pk_fma_f16 v21, v113, v29, v21
	v_pk_fma_f16 v20, v112, v28, v20
	v_pk_fma_f16 v19, v111, v27, v19
	v_pk_fma_f16 v18, v110, v26, v18
	v_pk_add_f16 v26, v58, v85
	v_pk_add_f16 v27, v59, v84
	v_pk_add_f16 v28, v60, v83
	v_pk_add_f16 v29, v61, v82
	v_exp_f16_sdwa v22, v26 dst_sel:WORD_0 dst_unused:UNUSED_PAD src0_sel:WORD_0
	v_exp_f16_sdwa v23, v27 dst_sel:WORD_0 dst_unused:UNUSED_PAD src0_sel:WORD_0
	v_exp_f16_sdwa v24, v28 dst_sel:WORD_0 dst_unused:UNUSED_PAD src0_sel:WORD_0
	v_exp_f16_sdwa v25, v29 dst_sel:WORD_0 dst_unused:UNUSED_PAD src0_sel:WORD_0
	v_exp_f16_sdwa v22, v26 dst_sel:WORD_1 dst_unused:UNUSED_PRESERVE src0_sel:WORD_1
	v_exp_f16_sdwa v23, v27 dst_sel:WORD_1 dst_unused:UNUSED_PRESERVE src0_sel:WORD_1
	v_exp_f16_sdwa v24, v28 dst_sel:WORD_1 dst_unused:UNUSED_PRESERVE src0_sel:WORD_1
	v_exp_f16_sdwa v25, v29 dst_sel:WORD_1 dst_unused:UNUSED_PRESERVE src0_sel:WORD_1
	s_nop 0
.LBB4_118:
	s_and_b64 vcc, exec, s[4:5]
	s_cbranch_vccz .LBB4_3
	global_load_dwordx3 v[146:148], v169, s[16:17]
	s_mov_b32 s14, s38
	s_mov_b32 s15, s39
	v_cmp_lt_u32_e64 s[64:65], 0, v199
	v_cmp_gt_u32_e64 s[66:67], 63, v199
	v_cmp_lt_u32_e64 s[68:69], 0, v180
	v_cmp_gt_u32_e64 s[70:71], 60, v180
	buffer_load_dwordx4 v[162:165], v200, s[12:15], 0 offen
	s_and_b64 s[72:73], s[68:69], s[64:65]
	s_and_b64 s[74:75], s[68:69], s[66:67]
	s_and_b64 s[76:77], s[70:71], s[64:65]
	s_and_b64 s[78:79], s[70:71], s[66:67]
	v_add_u32_e32 v245, 0xfffe7c00, v200
	v_add_u32_e32 v246, 0xfffe8000, v200
	s_mov_b64 exec, s[72:73]
	buffer_load_dwordx4 v[114:117], v245, s[12:15], 0 offen
	s_mov_b64 exec, -1
	s_mov_b64 exec, s[68:69]
	buffer_load_dwordx4 v[130:133], v246, s[12:15], 0 offen offset:512
	s_mov_b64 exec, -1
	s_mov_b64 exec, s[74:75]
	buffer_load_dwordx4 v[138:141], v246, s[12:15], 0 offen offset:2048
	s_mov_b64 exec, -1
	v_add_u32_e32 v245, 0xfffffc00, v200
	s_mov_b64 exec, s[64:65]
	buffer_load_dwordx4 v[86:89], v245, s[12:15], 0 offen
	s_mov_b64 exec, -1
	buffer_load_dwordx4 v[110:113], v200, s[12:15], 0 offen offset:512
	s_mov_b64 exec, s[66:67]
	buffer_load_dwordx4 v[126:129], v200, s[12:15], 0 offen offset:2048
	s_mov_b64 exec, -1
	v_add_u32_e32 v245, 0x17c00, v200
	v_add_u32_e32 v246, 0x18000, v200
	s_mov_b64 exec, s[64:65]
	buffer_load_dwordx4 v[54:57], v245, s[12:15], 0 offen
	s_mov_b64 exec, -1
	buffer_load_dwordx4 v[74:77], v246, s[12:15], 0 offen offset:512
	s_mov_b64 exec, s[66:67]
	buffer_load_dwordx4 v[98:101], v246, s[12:15], 0 offen offset:2048
	s_mov_b64 exec, -1
	v_add_u32_e32 v245, 0xfffe7c00, v200
	v_add_u32_e32 v246, 0xfffe8000, v200
	s_mov_b64 exec, s[72:73]
	buffer_load_dwordx4 v[70:73], v245, s[12:15], 0 offen offset:512
	s_mov_b64 exec, -1
	s_mov_b64 exec, s[68:69]
	buffer_load_dwordx4 v[94:97], v246, s[12:15], 0 offen offset:1024
	s_mov_b64 exec, -1
	s_mov_b64 exec, s[74:75]
	buffer_load_dwordx4 v[118:121], v246, s[12:15], 0 offen offset:2560
	s_mov_b64 exec, -1
	v_add_u32_e32 v245, 0xfffffc00, v200
	s_mov_b64 exec, s[64:65]
	buffer_load_dwordx4 v[42:45], v245, s[12:15], 0 offen offset:512
	s_mov_b64 exec, -1
	buffer_load_dwordx4 v[66:69], v200, s[12:15], 0 offen offset:1024
	s_mov_b64 exec, s[66:67]
	buffer_load_dwordx4 v[90:93], v200, s[12:15], 0 offen offset:2560
	s_mov_b64 exec, -1
	v_add_u32_e32 v245, 0x17c00, v200
	v_add_u32_e32 v246, 0x18000, v200
	s_mov_b64 exec, s[64:65]
	buffer_load_dwordx4 v[22:25], v245, s[12:15], 0 offen offset:512
	s_mov_b64 exec, -1
	buffer_load_dwordx4 v[34:37], v246, s[12:15], 0 offen offset:1024
	s_mov_b64 exec, s[66:67]
	buffer_load_dwordx4 v[50:53], v246, s[12:15], 0 offen offset:2560
	s_mov_b64 exec, -1
	v_add_u32_e32 v245, 0x18000, v200
	buffer_load_dwordx4 v[154:157], v245, s[12:15], 0 offen
	v_add_u32_e32 v246, 0x30000, v200
	buffer_load_dwordx4 v[150:153], v246, s[12:15], 0 offen
	v_add_u32_e32 v245, 0x2fc00, v200
	v_add_u32_e32 v246, 0x30000, v200
	v_add_u32_e32 v247, 0x47c00, v200
	v_add_u32_e32 v248, 0x48000, v200
	v_add_u32_e32 v249, 0x5fc00, v200
	v_add_u32_e32 v250, 0x60000, v200
	s_waitcnt vmcnt(22)
	v_cvt_pk_f16_f32 v6, v2, v3
	v_cvt_pk_f16_f32 v2, v8, v9
	v_cvt_pk_f16_f32 v7, v4, v5
	v_cvt_pk_f16_f32 v3, v10, v11
	v_cvt_pk_f16_f32 v8, v12, v13
	v_cvt_pk_f16_f32 v4, v16, v17
	v_cvt_pk_f16_f32 v9, v14, v15
	v_cvt_pk_f16_f32 v5, v18, v19
	s_not_b64 exec, s[72:73]
	s_cbranch_execz .Lmyf_C4_0
	v_mov_b32_e32 v114, v6
	v_mov_b32_e32 v115, v7
	v_mov_b32_e32 v116, v8
	v_mov_b32_e32 v117, v9
	v_mov_b32_e32 v70, v2
	v_mov_b32_e32 v71, v3
	v_mov_b32_e32 v72, v4
	v_mov_b32_e32 v73, v5

.LBB5_2:
	s_waitcnt lgkmcnt(0)
	v_cvt_f16_f32_e32 v180, s7
	v_cvt_f16_f32_e32 v182, s6
	v_cvt_f16_f32_e32 v181, s28
	s_waitcnt vmcnt(12)
	v_pk_mul_f16 v183, v182, v184 op_sel_hi:[0,1]
	v_pk_mul_f16 v190, v182, v187 op_sel_hi:[0,1]
	v_pk_mul_f16 v194, v180, v187 op_sel_hi:[0,1]
	v_pk_mul_f16 v198, v181, v187 op_sel_hi:[0,1]
	v_pk_mul_f16 v188, v182, v185 op_sel_hi:[0,1]
	v_pk_mul_f16 v189, v182, v186 op_sel_hi:[0,1]
	v_pk_mul_f16 v191, v180, v184 op_sel_hi:[0,1]
	v_pk_mul_f16 v192, v180, v185 op_sel_hi:[0,1]
	v_pk_mul_f16 v193, v180, v186 op_sel_hi:[0,1]
	v_pk_mul_f16 v195, v181, v184 op_sel_hi:[0,1]
	v_pk_mul_f16 v196, v181, v185 op_sel_hi:[0,1]
	v_pk_mul_f16 v197, v181, v186 op_sel_hi:[0,1]
	v_pk_fma_f16 v113, v113, v187, v190
	v_pk_fma_f16 v110, v110, v184, v183
	v_pk_fma_f16 v129, v129, v187, v190
	v_pk_fma_f16 v126, v126, v184, v183
	v_pk_fma_f16 v137, v137, v187, v190
	v_pk_fma_f16 v134, v134, v184, v183
	v_pk_fma_f16 v183, v85, v187, v194
	v_pk_fma_f16 v199, v109, v187, v194
	v_pk_fma_f16 v194, v125, v187, v194
	v_pk_fma_f16 v203, v53, v187, v198
	v_pk_fma_f16 v207, v69, v187, v198
	v_pk_fma_f16 v187, v97, v187, v198
	v_pk_maximum3_f16 v198, v113, v129, v137
	v_pk_fma_f16 v112, v112, v186, v189
	v_pk_fma_f16 v111, v111, v185, v188
	v_pk_fma_f16 v128, v128, v186, v189
	v_pk_fma_f16 v127, v127, v185, v188
	v_pk_fma_f16 v136, v136, v186, v189
	v_pk_fma_f16 v135, v135, v185, v188
	v_pk_fma_f16 v188, v84, v186, v193
	v_pk_fma_f16 v189, v83, v185, v192
	v_pk_fma_f16 v190, v82, v184, v191
	v_pk_fma_f16 v200, v108, v186, v193
	v_pk_fma_f16 v201, v107, v185, v192
	v_pk_fma_f16 v202, v106, v184, v191
	v_pk_fma_f16 v193, v124, v186, v193
	v_pk_fma_f16 v192, v123, v185, v192
	v_pk_fma_f16 v191, v122, v184, v191
	v_pk_fma_f16 v204, v52, v186, v197
	v_pk_fma_f16 v205, v51, v185, v196
	v_pk_fma_f16 v206, v50, v184, v195
	v_pk_fma_f16 v208, v68, v186, v197
	v_pk_fma_f16 v209, v67, v185, v196
	v_pk_fma_f16 v210, v66, v184, v195
	v_pk_fma_f16 v186, v96, v186, v197
	v_pk_fma_f16 v185, v95, v185, v196
	v_pk_fma_f16 v184, v94, v184, v195
	v_pk_maximum3_f16 v195, v110, v126, v134
	v_pk_maximum3_f16 v196, v111, v127, v135
	v_pk_maximum3_f16 v197, v112, v128, v136
	v_pk_maximum3_f16 v214, v183, v199, v194
	v_pk_maximum3_f16 v218, v203, v207, v187
	v_pk_maximum3_f16 v211, v190, v202, v191
	v_pk_maximum3_f16 v212, v189, v201, v192
	v_pk_maximum3_f16 v213, v188, v200, v193
	v_pk_maximum3_f16 v215, v206, v210, v184
	v_pk_maximum3_f16 v216, v205, v209, v185
	v_pk_maximum3_f16 v198, v198, v214, v218
	v_pk_maximum3_f16 v217, v204, v208, v186
	v_pk_maximum3_f16 v195, v195, v211, v215
	v_pk_maximum3_f16 v196, v196, v212, v216
	v_pk_maximum3_f16 v197, v197, v213, v217
	v_pk_add_f16 v113, v113, v198 neg_lo:[0,1] neg_hi:[0,1]
	v_pk_add_f16 v110, v110, v195 neg_lo:[0,1] neg_hi:[0,1]
	v_pk_add_f16 v111, v111, v196 neg_lo:[0,1] neg_hi:[0,1]
	v_pk_add_f16 v112, v112, v197 neg_lo:[0,1] neg_hi:[0,1]
	v_pk_add_f16 v126, v126, v195 neg_lo:[0,1] neg_hi:[0,1]
	v_exp_f16_sdwa v211, v110 dst_sel:WORD_0 dst_unused:UNUSED_PAD src0_sel:WORD_0
	v_exp_f16_sdwa v212, v111 dst_sel:WORD_0 dst_unused:UNUSED_PAD src0_sel:WORD_0
	v_exp_f16_sdwa v213, v112 dst_sel:WORD_0 dst_unused:UNUSED_PAD src0_sel:WORD_0
	v_exp_f16_sdwa v214, v113 dst_sel:WORD_0 dst_unused:UNUSED_PAD src0_sel:WORD_0
	v_exp_f16_sdwa v211, v110 dst_sel:WORD_1 dst_unused:UNUSED_PRESERVE src0_sel:WORD_1
	v_exp_f16_sdwa v212, v111 dst_sel:WORD_1 dst_unused:UNUSED_PRESERVE src0_sel:WORD_1
	v_exp_f16_sdwa v213, v112 dst_sel:WORD_1 dst_unused:UNUSED_PRESERVE src0_sel:WORD_1
	v_exp_f16_sdwa v214, v113 dst_sel:WORD_1 dst_unused:UNUSED_PRESERVE src0_sel:WORD_1
	v_pk_add_f16 v127, v127, v196 neg_lo:[0,1] neg_hi:[0,1]
	v_pk_add_f16 v113, v211, 0
	s_waitcnt vmcnt(3)
	v_pk_fma_f16 v81, v81, v214, 0
	v_pk_add_f16 v110, v214, 0
	v_pk_add_f16 v111, v213, 0
	v_pk_add_f16 v112, v212, 0
	v_pk_fma_f16 v80, v80, v213, 0
	v_pk_fma_f16 v79, v79, v212, 0
	s_mov_b64 exec, s[64:65]
	buffer_load_dwordx4 v[18:21], v224, s[16:19], 0 offen
	buffer_load_dwordx4 v[6:9], v224, s[16:19], 0 offen offset:512
	s_mov_b64 exec, -1
	v_pk_fma_f16 v78, v78, v211, 0
	v_pk_add_f16 v128, v128, v197 neg_lo:[0,1] neg_hi:[0,1]
	v_pk_add_f16 v129, v129, v198 neg_lo:[0,1] neg_hi:[0,1]
	v_exp_f16_sdwa v211, v126 dst_sel:WORD_0 dst_unused:UNUSED_PAD src0_sel:WORD_0
	v_exp_f16_sdwa v212, v127 dst_sel:WORD_0 dst_unused:UNUSED_PAD src0_sel:WORD_0
	v_exp_f16_sdwa v213, v128 dst_sel:WORD_0 dst_unused:UNUSED_PAD src0_sel:WORD_0
	v_exp_f16_sdwa v214, v129 dst_sel:WORD_0 dst_unused:UNUSED_PAD src0_sel:WORD_0
	v_exp_f16_sdwa v211, v126 dst_sel:WORD_1 dst_unused:UNUSED_PRESERVE src0_sel:WORD_1
	v_exp_f16_sdwa v212, v127 dst_sel:WORD_1 dst_unused:UNUSED_PRESERVE src0_sel:WORD_1
	v_exp_f16_sdwa v213, v128 dst_sel:WORD_1 dst_unused:UNUSED_PRESERVE src0_sel:WORD_1
	v_exp_f16_sdwa v214, v129 dst_sel:WORD_1 dst_unused:UNUSED_PRESERVE src0_sel:WORD_1
	v_pk_add_f16 v113, v113, v211
	v_pk_fma_f16 v81, v105, v214, v81
	v_pk_add_f16 v105, v137, v198 neg_lo:[0,1] neg_hi:[0,1]
	v_pk_add_f16 v112, v112, v212
	v_pk_add_f16 v111, v111, v213
	v_pk_add_f16 v110, v110, v214
	buffer_load_dwordx4 v[30:33], v225, s[16:19], 0 offen offset:512
	buffer_load_dwordx4 v[10:13], v225, s[16:19], 0 offen offset:1024
	v_pk_fma_f16 v78, v102, v211, v78
	v_pk_fma_f16 v79, v103, v212, v79
	v_pk_fma_f16 v80, v104, v213, v80
	v_pk_add_f16 v102, v134, v195 neg_lo:[0,1] neg_hi:[0,1]
	v_pk_add_f16 v103, v135, v196 neg_lo:[0,1] neg_hi:[0,1]
	v_pk_add_f16 v104, v136, v197 neg_lo:[0,1] neg_hi:[0,1]
	v_exp_f16_sdwa v126, v102 dst_sel:WORD_0 dst_unused:UNUSED_PAD src0_sel:WORD_0
	v_exp_f16_sdwa v127, v103 dst_sel:WORD_0 dst_unused:UNUSED_PAD src0_sel:WORD_0
	v_exp_f16_sdwa v128, v104 dst_sel:WORD_0 dst_unused:UNUSED_PAD src0_sel:WORD_0
	v_exp_f16_sdwa v129, v105 dst_sel:WORD_0 dst_unused:UNUSED_PAD src0_sel:WORD_0
	v_exp_f16_sdwa v126, v102 dst_sel:WORD_1 dst_unused:UNUSED_PRESERVE src0_sel:WORD_1
	v_exp_f16_sdwa v127, v103 dst_sel:WORD_1 dst_unused:UNUSED_PRESERVE src0_sel:WORD_1
	v_exp_f16_sdwa v128, v104 dst_sel:WORD_1 dst_unused:UNUSED_PRESERVE src0_sel:WORD_1
	v_exp_f16_sdwa v129, v105 dst_sel:WORD_1 dst_unused:UNUSED_PRESERVE src0_sel:WORD_1
	v_pk_add_f16 v105, v113, v126
	v_pk_add_f16 v102, v110, v129
	v_pk_add_f16 v103, v111, v128
	s_mov_b64 exec, s[66:67]
	buffer_load_dwordx4 v[54:57], v225, s[16:19], 0 offen offset:2048
	buffer_load_dwordx4 v[14:17], v225, s[16:19], 0 offen offset:2560
	s_mov_b64 exec, -1
	v_pk_add_f16 v104, v112, v127
	v_pk_fma_f16 v81, v117, v129, v81
	v_pk_fma_f16 v80, v116, v128, v80
	v_pk_fma_f16 v79, v115, v127, v79
	v_pk_fma_f16 v78, v114, v126, v78
	v_pk_add_f16 v110, v190, v195 neg_lo:[0,1] neg_hi:[0,1]
	v_pk_add_f16 v111, v189, v196 neg_lo:[0,1] neg_hi:[0,1]
	v_pk_add_f16 v112, v188, v197 neg_lo:[0,1] neg_hi:[0,1]
	s_mov_b64 exec, s[64:65]
	buffer_load_dwordx4 v[74:77], v226, s[16:19], 0 offen
	buffer_load_dwordx4 v[26:29], v226, s[16:19], 0 offen offset:512
	s_mov_b64 exec, -1
	v_pk_add_f16 v113, v183, v198 neg_lo:[0,1] neg_hi:[0,1]
	v_exp_f16_sdwa v114, v110 dst_sel:WORD_0 dst_unused:UNUSED_PAD src0_sel:WORD_0
	v_exp_f16_sdwa v115, v111 dst_sel:WORD_0 dst_unused:UNUSED_PAD src0_sel:WORD_0
	v_exp_f16_sdwa v116, v112 dst_sel:WORD_0 dst_unused:UNUSED_PAD src0_sel:WORD_0
	v_exp_f16_sdwa v117, v113 dst_sel:WORD_0 dst_unused:UNUSED_PAD src0_sel:WORD_0
	v_exp_f16_sdwa v114, v110 dst_sel:WORD_1 dst_unused:UNUSED_PRESERVE src0_sel:WORD_1
	v_exp_f16_sdwa v115, v111 dst_sel:WORD_1 dst_unused:UNUSED_PRESERVE src0_sel:WORD_1
	v_exp_f16_sdwa v116, v112 dst_sel:WORD_1 dst_unused:UNUSED_PRESERVE src0_sel:WORD_1
	v_exp_f16_sdwa v117, v113 dst_sel:WORD_1 dst_unused:UNUSED_PRESERVE src0_sel:WORD_1
	v_pk_add_f16 v110, v202, v195 neg_lo:[0,1] neg_hi:[0,1]
	v_pk_add_f16 v105, v105, v114
	v_pk_add_f16 v104, v104, v115
	v_pk_add_f16 v103, v103, v116
	v_pk_add_f16 v102, v102, v117
	v_pk_fma_f16 v78, v42, v114, v78
	v_pk_fma_f16 v79, v43, v115, v79
	v_pk_fma_f16 v80, v44, v116, v80
	v_pk_fma_f16 v81, v45, v117, v81
	buffer_load_dwordx4 v[98:101], v227, s[16:19], 0 offen offset:512
	buffer_load_dwordx4 v[38:41], v227, s[16:19], 0 offen offset:1024
	v_pk_add_f16 v111, v201, v196 neg_lo:[0,1] neg_hi:[0,1]
	v_pk_add_f16 v112, v200, v197 neg_lo:[0,1] neg_hi:[0,1]
	v_pk_add_f16 v113, v199, v198 neg_lo:[0,1] neg_hi:[0,1]
	v_exp_f16_sdwa v114, v110 dst_sel:WORD_0 dst_unused:UNUSED_PAD src0_sel:WORD_0
	v_exp_f16_sdwa v115, v111 dst_sel:WORD_0 dst_unused:UNUSED_PAD src0_sel:WORD_0
	v_exp_f16_sdwa v116, v112 dst_sel:WORD_0 dst_unused:UNUSED_PAD src0_sel:WORD_0
	v_exp_f16_sdwa v117, v113 dst_sel:WORD_0 dst_unused:UNUSED_PAD src0_sel:WORD_0
	v_exp_f16_sdwa v114, v110 dst_sel:WORD_1 dst_unused:UNUSED_PRESERVE src0_sel:WORD_1
	v_exp_f16_sdwa v115, v111 dst_sel:WORD_1 dst_unused:UNUSED_PRESERVE src0_sel:WORD_1
	v_exp_f16_sdwa v116, v112 dst_sel:WORD_1 dst_unused:UNUSED_PRESERVE src0_sel:WORD_1
	v_exp_f16_sdwa v117, v113 dst_sel:WORD_1 dst_unused:UNUSED_PRESERVE src0_sel:WORD_1
	v_pk_add_f16 v110, v191, v195 neg_lo:[0,1] neg_hi:[0,1]
	v_pk_add_f16 v105, v105, v114
	v_pk_add_f16 v102, v102, v117
	v_pk_add_f16 v103, v103, v116
	v_pk_add_f16 v104, v104, v115
	v_pk_fma_f16 v81, v65, v117, v81
	s_mov_b64 exec, s[66:67]
	buffer_load_dwordx4 v[118:121], v227, s[16:19], 0 offen offset:2048
	buffer_load_dwordx4 v[58:61], v227, s[16:19], 0 offen offset:2560
	s_mov_b64 exec, -1
	v_pk_fma_f16 v80, v64, v116, v80
	v_pk_fma_f16 v79, v63, v115, v79
	v_pk_fma_f16 v78, v62, v114, v78
	v_pk_add_f16 v111, v192, v196 neg_lo:[0,1] neg_hi:[0,1]
	v_pk_add_f16 v112, v193, v197 neg_lo:[0,1] neg_hi:[0,1]
	v_pk_add_f16 v113, v194, v198 neg_lo:[0,1] neg_hi:[0,1]
	v_exp_f16_sdwa v114, v110 dst_sel:WORD_0 dst_unused:UNUSED_PAD src0_sel:WORD_0
	v_exp_f16_sdwa v115, v111 dst_sel:WORD_0 dst_unused:UNUSED_PAD src0_sel:WORD_0
	v_exp_f16_sdwa v116, v112 dst_sel:WORD_0 dst_unused:UNUSED_PAD src0_sel:WORD_0
	v_exp_f16_sdwa v117, v113 dst_sel:WORD_0 dst_unused:UNUSED_PAD src0_sel:WORD_0
	v_exp_f16_sdwa v114, v110 dst_sel:WORD_1 dst_unused:UNUSED_PRESERVE src0_sel:WORD_1
	v_exp_f16_sdwa v115, v111 dst_sel:WORD_1 dst_unused:UNUSED_PRESERVE src0_sel:WORD_1
	v_exp_f16_sdwa v116, v112 dst_sel:WORD_1 dst_unused:UNUSED_PRESERVE src0_sel:WORD_1
	v_exp_f16_sdwa v117, v113 dst_sel:WORD_1 dst_unused:UNUSED_PRESERVE src0_sel:WORD_1
	v_pk_add_f16 v110, v206, v195 neg_lo:[0,1] neg_hi:[0,1]
	v_pk_add_f16 v105, v105, v114
	v_pk_add_f16 v104, v104, v115
	s_mov_b64 exec, s[76:77]
	buffer_load_dwordx4 v[130:133], v228, s[16:19], 0 offen
	buffer_load_dwordx4 v[70:73], v228, s[16:19], 0 offen offset:512
	s_mov_b64 exec, -1
	v_pk_add_f16 v103, v103, v116
	v_pk_add_f16 v102, v102, v117
	v_pk_fma_f16 v78, v86, v114, v78
	v_pk_fma_f16 v79, v87, v115, v79
	v_pk_fma_f16 v80, v88, v116, v80
	v_pk_fma_f16 v81, v89, v117, v81
	v_pk_add_f16 v111, v205, v196 neg_lo:[0,1] neg_hi:[0,1]
	v_pk_add_f16 v112, v204, v197 neg_lo:[0,1] neg_hi:[0,1]
	s_mov_b64 exec, s[70:71]
	buffer_load_dwordx4 v[138:141], v229, s[16:19], 0 offen offset:512
	buffer_load_dwordx4 v[90:93], v229, s[16:19], 0 offen offset:1024
	s_mov_b64 exec, -1
	v_pk_add_f16 v113, v203, v198 neg_lo:[0,1] neg_hi:[0,1]
	v_exp_f16_sdwa v114, v110 dst_sel:WORD_0 dst_unused:UNUSED_PAD src0_sel:WORD_0
	v_exp_f16_sdwa v115, v111 dst_sel:WORD_0 dst_unused:UNUSED_PAD src0_sel:WORD_0
	v_exp_f16_sdwa v116, v112 dst_sel:WORD_0 dst_unused:UNUSED_PAD src0_sel:WORD_0
	v_exp_f16_sdwa v117, v113 dst_sel:WORD_0 dst_unused:UNUSED_PAD src0_sel:WORD_0
	v_exp_f16_sdwa v114, v110 dst_sel:WORD_1 dst_unused:UNUSED_PRESERVE src0_sel:WORD_1
	v_exp_f16_sdwa v115, v111 dst_sel:WORD_1 dst_unused:UNUSED_PRESERVE src0_sel:WORD_1
	v_exp_f16_sdwa v116, v112 dst_sel:WORD_1 dst_unused:UNUSED_PRESERVE src0_sel:WORD_1
	v_exp_f16_sdwa v117, v113 dst_sel:WORD_1 dst_unused:UNUSED_PRESERVE src0_sel:WORD_1
	v_pk_add_f16 v110, v210, v195 neg_lo:[0,1] neg_hi:[0,1]
	v_pk_add_f16 v105, v105, v114
	v_pk_add_f16 v102, v102, v117
	v_pk_add_f16 v103, v103, v116
	v_pk_add_f16 v104, v104, v115
	v_pk_fma_f16 v81, v25, v117, v81
	v_pk_fma_f16 v80, v24, v116, v80
	v_pk_fma_f16 v79, v23, v115, v79
	s_mov_b64 exec, s[78:79]
	buffer_load_dwordx4 v[142:145], v229, s[16:19], 0 offen offset:2048
	buffer_load_dwordx4 v[2:5], v229, s[16:19], 0 offen offset:2560
	s_mov_b64 exec, -1
	v_pk_fma_f16 v78, v22, v114, v78
	v_pk_add_f16 v111, v209, v196 neg_lo:[0,1] neg_hi:[0,1]
	v_pk_add_f16 v112, v208, v197 neg_lo:[0,1] neg_hi:[0,1]
	v_pk_add_f16 v113, v207, v198 neg_lo:[0,1] neg_hi:[0,1]
	v_exp_f16_sdwa v114, v110 dst_sel:WORD_0 dst_unused:UNUSED_PAD src0_sel:WORD_0
	v_exp_f16_sdwa v115, v111 dst_sel:WORD_0 dst_unused:UNUSED_PAD src0_sel:WORD_0
	v_exp_f16_sdwa v116, v112 dst_sel:WORD_0 dst_unused:UNUSED_PAD src0_sel:WORD_0
	v_exp_f16_sdwa v117, v113 dst_sel:WORD_0 dst_unused:UNUSED_PAD src0_sel:WORD_0
	v_exp_f16_sdwa v114, v110 dst_sel:WORD_1 dst_unused:UNUSED_PRESERVE src0_sel:WORD_1
	v_exp_f16_sdwa v115, v111 dst_sel:WORD_1 dst_unused:UNUSED_PRESERVE src0_sel:WORD_1
	v_exp_f16_sdwa v116, v112 dst_sel:WORD_1 dst_unused:UNUSED_PRESERVE src0_sel:WORD_1
	v_exp_f16_sdwa v117, v113 dst_sel:WORD_1 dst_unused:UNUSED_PRESERVE src0_sel:WORD_1
	v_pk_add_f16 v110, v184, v195 neg_lo:[0,1] neg_hi:[0,1]
	v_pk_add_f16 v105, v105, v114
	v_pk_add_f16 v104, v104, v115
	v_pk_add_f16 v103, v103, v116
	v_pk_add_f16 v102, v102, v117
	v_pk_fma_f16 v78, v34, v114, v78
	v_pk_fma_f16 v79, v35, v115, v79
	v_pk_fma_f16 v80, v36, v116, v80
	v_pk_fma_f16 v81, v37, v117, v81
	v_pk_add_f16 v111, v185, v196 neg_lo:[0,1] neg_hi:[0,1]
	v_pk_add_f16 v112, v186, v197 neg_lo:[0,1] neg_hi:[0,1]
	v_pk_add_f16 v113, v187, v198 neg_lo:[0,1] neg_hi:[0,1]
	v_exp_f16_sdwa v114, v110 dst_sel:WORD_0 dst_unused:UNUSED_PAD src0_sel:WORD_0
	v_exp_f16_sdwa v115, v111 dst_sel:WORD_0 dst_unused:UNUSED_PAD src0_sel:WORD_0
	v_exp_f16_sdwa v116, v112 dst_sel:WORD_0 dst_unused:UNUSED_PAD src0_sel:WORD_0
	v_exp_f16_sdwa v117, v113 dst_sel:WORD_0 dst_unused:UNUSED_PAD src0_sel:WORD_0
	v_exp_f16_sdwa v114, v110 dst_sel:WORD_1 dst_unused:UNUSED_PRESERVE src0_sel:WORD_1
	v_exp_f16_sdwa v115, v111 dst_sel:WORD_1 dst_unused:UNUSED_PRESERVE src0_sel:WORD_1
	v_exp_f16_sdwa v116, v112 dst_sel:WORD_1 dst_unused:UNUSED_PRESERVE src0_sel:WORD_1
	v_exp_f16_sdwa v117, v113 dst_sel:WORD_1 dst_unused:UNUSED_PRESERVE src0_sel:WORD_1
	v_pk_add_f16 v105, v105, v114
	v_pk_add_f16 v104, v104, v115
	v_rcp_f16_e32 v110, v105
	v_rcp_f16_sdwa v105, v105 dst_sel:DWORD dst_unused:UNUSED_PAD src0_sel:WORD_1
	v_pk_add_f16 v103, v103, v116
	v_rcp_f16_e32 v111, v104
	v_rcp_f16_sdwa v104, v104 dst_sel:DWORD dst_unused:UNUSED_PAD src0_sel:WORD_1
	v_pk_add_f16 v102, v102, v117
	v_rcp_f16_e32 v112, v103
	v_rcp_f16_sdwa v103, v103 dst_sel:DWORD dst_unused:UNUSED_PAD src0_sel:WORD_1
	v_rcp_f16_e32 v113, v102
	v_rcp_f16_sdwa v102, v102 dst_sel:DWORD dst_unused:UNUSED_PAD src0_sel:WORD_1
	v_pk_fma_f16 v78, v46, v114, v78
	v_pack_b32_f16 v105, v110, v105
	v_pk_fma_f16 v79, v47, v115, v79
	v_pk_mul_f16 v110, v78, v105
	v_pack_b32_f16 v78, v111, v104
	v_pk_fma_f16 v80, v48, v116, v80
	v_pk_mul_f16 v111, v79, v78
	v_pack_b32_f16 v78, v112, v103
	v_pk_fma_f16 v81, v49, v117, v81
	v_pk_mul_f16 v112, v80, v78
	v_pack_b32_f16 v78, v113, v102
	v_pk_mul_f16 v113, v81, v78
	s_waitcnt vmcnt(12)
	v_pk_mul_f16 v78, v182, v154 op_sel_hi:[0,1]
	v_pk_mul_f16 v81, v182, v157 op_sel_hi:[0,1]
	v_pk_mul_f16 v102, v180, v154 op_sel_hi:[0,1]
	v_pk_mul_f16 v114, v181, v154 op_sel_hi:[0,1]
	v_pk_mul_f16 v79, v182, v155 op_sel_hi:[0,1]
	v_pk_mul_f16 v80, v182, v156 op_sel_hi:[0,1]
	v_pk_mul_f16 v103, v180, v155 op_sel_hi:[0,1]
	v_pk_mul_f16 v104, v180, v156 op_sel_hi:[0,1]
	v_pk_mul_f16 v105, v180, v157 op_sel_hi:[0,1]
	v_pk_mul_f16 v115, v181, v155 op_sel_hi:[0,1]
	v_pk_mul_f16 v116, v181, v156 op_sel_hi:[0,1]
	v_pk_mul_f16 v117, v181, v157 op_sel_hi:[0,1]
	v_pk_fma_f16 v85, v85, v157, v81
	v_pk_fma_f16 v82, v82, v154, v78
	v_pk_fma_f16 v109, v109, v157, v81
	v_pk_fma_f16 v106, v106, v154, v78
	v_pk_fma_f16 v81, v125, v157, v81
	v_pk_fma_f16 v78, v122, v154, v78
	v_pk_fma_f16 v125, v50, v154, v102
	v_pk_fma_f16 v129, v66, v154, v102
	v_pk_fma_f16 v102, v94, v154, v102
	v_pk_fma_f16 v137, v18, v154, v114
	v_pk_fma_f16 v186, v30, v154, v114
	v_pk_fma_f16 v114, v54, v154, v114
	v_pk_maximum3_f16 v154, v82, v106, v78
	v_pk_fma_f16 v84, v84, v156, v80
	v_pk_fma_f16 v83, v83, v155, v79
	v_pk_fma_f16 v108, v108, v156, v80
	v_pk_fma_f16 v107, v107, v155, v79
	v_pk_fma_f16 v80, v124, v156, v80
	v_pk_fma_f16 v79, v123, v155, v79
	v_pk_fma_f16 v122, v53, v157, v105
	v_pk_fma_f16 v123, v52, v156, v104
	v_pk_fma_f16 v124, v51, v155, v103
	v_pk_fma_f16 v126, v69, v157, v105
	v_pk_fma_f16 v127, v68, v156, v104
	v_pk_fma_f16 v128, v67, v155, v103
	v_pk_fma_f16 v105, v97, v157, v105
	v_pk_fma_f16 v104, v96, v156, v104
	v_pk_fma_f16 v103, v95, v155, v103
	v_pk_fma_f16 v134, v21, v157, v117
	v_pk_fma_f16 v135, v20, v156, v116
	v_pk_fma_f16 v136, v19, v155, v115
	v_pk_fma_f16 v183, v33, v157, v117
	v_pk_fma_f16 v184, v32, v156, v116
	v_pk_fma_f16 v185, v31, v155, v115
	v_pk_fma_f16 v117, v57, v157, v117
	v_pk_fma_f16 v116, v56, v156, v116
	v_pk_fma_f16 v115, v55, v155, v115
	v_pk_maximum3_f16 v155, v83, v107, v79
	v_pk_maximum3_f16 v156, v84, v108, v80
	v_pk_maximum3_f16 v157, v85, v109, v81
	v_pk_maximum3_f16 v187, v125, v129, v102
	v_pk_maximum3_f16 v191, v137, v186, v114
	v_pk_maximum3_f16 v188, v124, v128, v103
	v_pk_maximum3_f16 v189, v123, v127, v104
	v_pk_maximum3_f16 v190, v122, v126, v105
	v_pk_maximum3_f16 v192, v136, v185, v115
	v_pk_maximum3_f16 v193, v135, v184, v116
	v_pk_maximum3_f16 v154, v154, v187, v191
	v_pk_maximum3_f16 v194, v134, v183, v117
	v_pk_maximum3_f16 v155, v155, v188, v192
	v_pk_maximum3_f16 v156, v156, v189, v193
	v_pk_maximum3_f16 v157, v157, v190, v194
	v_pk_add_f16 v82, v82, v154 neg_lo:[0,1] neg_hi:[0,1]
	v_pk_add_f16 v83, v83, v155 neg_lo:[0,1] neg_hi:[0,1]
	v_pk_add_f16 v84, v84, v156 neg_lo:[0,1] neg_hi:[0,1]
	v_pk_add_f16 v85, v85, v157 neg_lo:[0,1] neg_hi:[0,1]
	v_pk_add_f16 v106, v106, v154 neg_lo:[0,1] neg_hi:[0,1]
	v_exp_f16_sdwa v187, v82 dst_sel:WORD_0 dst_unused:UNUSED_PAD src0_sel:WORD_0
	v_exp_f16_sdwa v188, v83 dst_sel:WORD_0 dst_unused:UNUSED_PAD src0_sel:WORD_0
	v_exp_f16_sdwa v189, v84 dst_sel:WORD_0 dst_unused:UNUSED_PAD src0_sel:WORD_0
	v_exp_f16_sdwa v190, v85 dst_sel:WORD_0 dst_unused:UNUSED_PAD src0_sel:WORD_0
	v_exp_f16_sdwa v187, v82 dst_sel:WORD_1 dst_unused:UNUSED_PRESERVE src0_sel:WORD_1
	v_exp_f16_sdwa v188, v83 dst_sel:WORD_1 dst_unused:UNUSED_PRESERVE src0_sel:WORD_1
	v_exp_f16_sdwa v189, v84 dst_sel:WORD_1 dst_unused:UNUSED_PRESERVE src0_sel:WORD_1
	v_exp_f16_sdwa v190, v85 dst_sel:WORD_1 dst_unused:UNUSED_PRESERVE src0_sel:WORD_1
	v_pk_add_f16 v107, v107, v155 neg_lo:[0,1] neg_hi:[0,1]
	v_pk_add_f16 v82, v190, 0
	v_pk_fma_f16 v42, v42, v187, 0
	v_pk_add_f16 v83, v189, 0
	v_pk_add_f16 v84, v188, 0
	v_pk_add_f16 v85, v187, 0
	v_pk_fma_f16 v45, v45, v190, 0
	v_pk_fma_f16 v44, v44, v189, 0
	v_pk_fma_f16 v43, v43, v188, 0
	v_pk_add_f16 v108, v108, v156 neg_lo:[0,1] neg_hi:[0,1]
	v_pk_add_f16 v109, v109, v157 neg_lo:[0,1] neg_hi:[0,1]
	v_exp_f16_sdwa v187, v106 dst_sel:WORD_0 dst_unused:UNUSED_PAD src0_sel:WORD_0
	v_exp_f16_sdwa v188, v107 dst_sel:WORD_0 dst_unused:UNUSED_PAD src0_sel:WORD_0
	v_exp_f16_sdwa v189, v108 dst_sel:WORD_0 dst_unused:UNUSED_PAD src0_sel:WORD_0
	v_exp_f16_sdwa v190, v109 dst_sel:WORD_0 dst_unused:UNUSED_PAD src0_sel:WORD_0
	v_exp_f16_sdwa v187, v106 dst_sel:WORD_1 dst_unused:UNUSED_PRESERVE src0_sel:WORD_1
	v_exp_f16_sdwa v188, v107 dst_sel:WORD_1 dst_unused:UNUSED_PRESERVE src0_sel:WORD_1
	v_exp_f16_sdwa v189, v108 dst_sel:WORD_1 dst_unused:UNUSED_PRESERVE src0_sel:WORD_1
	v_exp_f16_sdwa v190, v109 dst_sel:WORD_1 dst_unused:UNUSED_PRESERVE src0_sel:WORD_1
	s_nop 0
	v_pk_add_f16 v82, v82, v190
	v_pk_fma_f16 v42, v62, v187, v42
	v_pk_add_f16 v62, v78, v154 neg_lo:[0,1] neg_hi:[0,1]
	v_pk_add_f16 v85, v85, v187
	v_pk_add_f16 v84, v84, v188
	v_pk_add_f16 v83, v83, v189
	v_pk_fma_f16 v43, v63, v188, v43
	v_pk_fma_f16 v44, v64, v189, v44
	v_pk_fma_f16 v45, v65, v190, v45
	v_pk_add_f16 v63, v79, v155 neg_lo:[0,1] neg_hi:[0,1]
	v_pk_add_f16 v64, v80, v156 neg_lo:[0,1] neg_hi:[0,1]
	v_pk_add_f16 v65, v81, v157 neg_lo:[0,1] neg_hi:[0,1]
	v_exp_f16_sdwa v78, v62 dst_sel:WORD_0 dst_unused:UNUSED_PAD src0_sel:WORD_0
	v_exp_f16_sdwa v79, v63 dst_sel:WORD_0 dst_unused:UNUSED_PAD src0_sel:WORD_0
	v_exp_f16_sdwa v80, v64 dst_sel:WORD_0 dst_unused:UNUSED_PAD src0_sel:WORD_0
	v_exp_f16_sdwa v81, v65 dst_sel:WORD_0 dst_unused:UNUSED_PAD src0_sel:WORD_0
	v_exp_f16_sdwa v78, v62 dst_sel:WORD_1 dst_unused:UNUSED_PRESERVE src0_sel:WORD_1
	v_exp_f16_sdwa v79, v63 dst_sel:WORD_1 dst_unused:UNUSED_PRESERVE src0_sel:WORD_1
	v_exp_f16_sdwa v80, v64 dst_sel:WORD_1 dst_unused:UNUSED_PRESERVE src0_sel:WORD_1
	v_exp_f16_sdwa v81, v65 dst_sel:WORD_1 dst_unused:UNUSED_PRESERVE src0_sel:WORD_1
	s_nop 0
	v_pk_add_f16 v62, v82, v81
	v_pk_add_f16 v63, v83, v80
	v_pk_add_f16 v64, v84, v79
	v_pk_add_f16 v65, v85, v78
	v_pk_fma_f16 v45, v89, v81, v45
	v_pk_fma_f16 v44, v88, v80, v44
	v_pk_fma_f16 v43, v87, v79, v43
	v_pk_fma_f16 v42, v86, v78, v42
	v_pk_add_f16 v78, v125, v154 neg_lo:[0,1] neg_hi:[0,1]
	v_pk_add_f16 v79, v124, v155 neg_lo:[0,1] neg_hi:[0,1]
	v_pk_add_f16 v80, v123, v156 neg_lo:[0,1] neg_hi:[0,1]
	v_pk_add_f16 v81, v122, v157 neg_lo:[0,1] neg_hi:[0,1]
	v_exp_f16_sdwa v82, v78 dst_sel:WORD_0 dst_unused:UNUSED_PAD src0_sel:WORD_0
	v_exp_f16_sdwa v83, v79 dst_sel:WORD_0 dst_unused:UNUSED_PAD src0_sel:WORD_0
	v_exp_f16_sdwa v84, v80 dst_sel:WORD_0 dst_unused:UNUSED_PAD src0_sel:WORD_0
	v_exp_f16_sdwa v85, v81 dst_sel:WORD_0 dst_unused:UNUSED_PAD src0_sel:WORD_0
	v_exp_f16_sdwa v82, v78 dst_sel:WORD_1 dst_unused:UNUSED_PRESERVE src0_sel:WORD_1
	v_exp_f16_sdwa v83, v79 dst_sel:WORD_1 dst_unused:UNUSED_PRESERVE src0_sel:WORD_1
	v_exp_f16_sdwa v84, v80 dst_sel:WORD_1 dst_unused:UNUSED_PRESERVE src0_sel:WORD_1
	v_exp_f16_sdwa v85, v81 dst_sel:WORD_1 dst_unused:UNUSED_PRESERVE src0_sel:WORD_1
	v_pk_add_f16 v78, v129, v154 neg_lo:[0,1] neg_hi:[0,1]
	v_pk_add_f16 v62, v62, v85
	v_pk_add_f16 v65, v65, v82
	v_pk_add_f16 v64, v64, v83
	v_pk_add_f16 v63, v63, v84
	v_pk_fma_f16 v42, v22, v82, v42
	v_pk_fma_f16 v43, v23, v83, v43
	v_pk_fma_f16 v44, v24, v84, v44
	v_pk_fma_f16 v45, v25, v85, v45
	v_pk_add_f16 v79, v128, v155 neg_lo:[0,1] neg_hi:[0,1]
	v_pk_add_f16 v80, v127, v156 neg_lo:[0,1] neg_hi:[0,1]
	v_pk_add_f16 v81, v126, v157 neg_lo:[0,1] neg_hi:[0,1]
	v_exp_f16_sdwa v82, v78 dst_sel:WORD_0 dst_unused:UNUSED_PAD src0_sel:WORD_0
	v_exp_f16_sdwa v83, v79 dst_sel:WORD_0 dst_unused:UNUSED_PAD src0_sel:WORD_0
	v_exp_f16_sdwa v84, v80 dst_sel:WORD_0 dst_unused:UNUSED_PAD src0_sel:WORD_0
	v_exp_f16_sdwa v85, v81 dst_sel:WORD_0 dst_unused:UNUSED_PAD src0_sel:WORD_0
	v_exp_f16_sdwa v82, v78 dst_sel:WORD_1 dst_unused:UNUSED_PRESERVE src0_sel:WORD_1
	v_exp_f16_sdwa v83, v79 dst_sel:WORD_1 dst_unused:UNUSED_PRESERVE src0_sel:WORD_1
	v_exp_f16_sdwa v84, v80 dst_sel:WORD_1 dst_unused:UNUSED_PRESERVE src0_sel:WORD_1
	v_exp_f16_sdwa v85, v81 dst_sel:WORD_1 dst_unused:UNUSED_PRESERVE src0_sel:WORD_1
	v_pk_add_f16 v78, v102, v154 neg_lo:[0,1] neg_hi:[0,1]
	v_pk_add_f16 v62, v62, v85
	v_pk_add_f16 v63, v63, v84
	v_pk_add_f16 v64, v64, v83
	v_pk_add_f16 v65, v65, v82
	v_pk_fma_f16 v45, v37, v85, v45
	v_pk_fma_f16 v44, v36, v84, v44
	v_pk_fma_f16 v43, v35, v83, v43
	v_pk_fma_f16 v42, v34, v82, v42
	v_pk_add_f16 v79, v103, v155 neg_lo:[0,1] neg_hi:[0,1]
	v_pk_add_f16 v80, v104, v156 neg_lo:[0,1] neg_hi:[0,1]
	v_pk_add_f16 v81, v105, v157 neg_lo:[0,1] neg_hi:[0,1]
	v_exp_f16_sdwa v82, v78 dst_sel:WORD_0 dst_unused:UNUSED_PAD src0_sel:WORD_0
	v_exp_f16_sdwa v83, v79 dst_sel:WORD_0 dst_unused:UNUSED_PAD src0_sel:WORD_0
	v_exp_f16_sdwa v84, v80 dst_sel:WORD_0 dst_unused:UNUSED_PAD src0_sel:WORD_0
	v_exp_f16_sdwa v85, v81 dst_sel:WORD_0 dst_unused:UNUSED_PAD src0_sel:WORD_0
	v_exp_f16_sdwa v82, v78 dst_sel:WORD_1 dst_unused:UNUSED_PRESERVE src0_sel:WORD_1
	v_exp_f16_sdwa v83, v79 dst_sel:WORD_1 dst_unused:UNUSED_PRESERVE src0_sel:WORD_1
	v_exp_f16_sdwa v84, v80 dst_sel:WORD_1 dst_unused:UNUSED_PRESERVE src0_sel:WORD_1
	v_exp_f16_sdwa v85, v81 dst_sel:WORD_1 dst_unused:UNUSED_PRESERVE src0_sel:WORD_1
	v_pk_add_f16 v78, v137, v154 neg_lo:[0,1] neg_hi:[0,1]
	v_pk_add_f16 v62, v62, v85
	v_pk_add_f16 v65, v65, v82
	v_pk_add_f16 v64, v64, v83
	v_pk_add_f16 v63, v63, v84
	v_pk_fma_f16 v42, v46, v82, v42
	v_pk_fma_f16 v43, v47, v83, v43
	v_pk_fma_f16 v44, v48, v84, v44
	v_pk_fma_f16 v45, v49, v85, v45
	v_pk_add_f16 v79, v136, v155 neg_lo:[0,1] neg_hi:[0,1]
	v_pk_add_f16 v80, v135, v156 neg_lo:[0,1] neg_hi:[0,1]
	v_pk_add_f16 v81, v134, v157 neg_lo:[0,1] neg_hi:[0,1]
	v_exp_f16_sdwa v82, v78 dst_sel:WORD_0 dst_unused:UNUSED_PAD src0_sel:WORD_0
	v_exp_f16_sdwa v83, v79 dst_sel:WORD_0 dst_unused:UNUSED_PAD src0_sel:WORD_0
	v_exp_f16_sdwa v84, v80 dst_sel:WORD_0 dst_unused:UNUSED_PAD src0_sel:WORD_0
	v_exp_f16_sdwa v85, v81 dst_sel:WORD_0 dst_unused:UNUSED_PAD src0_sel:WORD_0
	v_exp_f16_sdwa v82, v78 dst_sel:WORD_1 dst_unused:UNUSED_PRESERVE src0_sel:WORD_1
	v_exp_f16_sdwa v83, v79 dst_sel:WORD_1 dst_unused:UNUSED_PRESERVE src0_sel:WORD_1
	v_exp_f16_sdwa v84, v80 dst_sel:WORD_1 dst_unused:UNUSED_PRESERVE src0_sel:WORD_1
	v_exp_f16_sdwa v85, v81 dst_sel:WORD_1 dst_unused:UNUSED_PRESERVE src0_sel:WORD_1
	v_pk_add_f16 v78, v186, v154 neg_lo:[0,1] neg_hi:[0,1]
	v_pk_add_f16 v62, v62, v85
	v_pk_add_f16 v63, v63, v84
	v_pk_add_f16 v64, v64, v83
	v_pk_add_f16 v65, v65, v82
	v_pk_fma_f16 v45, v9, v85, v45
	v_pk_fma_f16 v44, v8, v84, v44
	v_pk_fma_f16 v43, v7, v83, v43
	v_pk_fma_f16 v42, v6, v82, v42
	v_pk_add_f16 v79, v185, v155 neg_lo:[0,1] neg_hi:[0,1]
	v_pk_add_f16 v80, v184, v156 neg_lo:[0,1] neg_hi:[0,1]
	v_pk_add_f16 v81, v183, v157 neg_lo:[0,1] neg_hi:[0,1]
	v_exp_f16_sdwa v82, v78 dst_sel:WORD_0 dst_unused:UNUSED_PAD src0_sel:WORD_0
	v_exp_f16_sdwa v83, v79 dst_sel:WORD_0 dst_unused:UNUSED_PAD src0_sel:WORD_0
	v_exp_f16_sdwa v84, v80 dst_sel:WORD_0 dst_unused:UNUSED_PAD src0_sel:WORD_0
	v_exp_f16_sdwa v85, v81 dst_sel:WORD_0 dst_unused:UNUSED_PAD src0_sel:WORD_0
	v_exp_f16_sdwa v82, v78 dst_sel:WORD_1 dst_unused:UNUSED_PRESERVE src0_sel:WORD_1
	v_exp_f16_sdwa v83, v79 dst_sel:WORD_1 dst_unused:UNUSED_PRESERVE src0_sel:WORD_1
	v_exp_f16_sdwa v84, v80 dst_sel:WORD_1 dst_unused:UNUSED_PRESERVE src0_sel:WORD_1
	v_exp_f16_sdwa v85, v81 dst_sel:WORD_1 dst_unused:UNUSED_PRESERVE src0_sel:WORD_1
	v_pk_add_f16 v78, v114, v154 neg_lo:[0,1] neg_hi:[0,1]
	v_pk_add_f16 v62, v62, v85
	v_pk_add_f16 v65, v65, v82
	v_pk_add_f16 v64, v64, v83
	v_pk_add_f16 v63, v63, v84
	v_pk_fma_f16 v42, v10, v82, v42
	v_pk_fma_f16 v43, v11, v83, v43
	v_pk_fma_f16 v44, v12, v84, v44
	v_pk_fma_f16 v45, v13, v85, v45
	v_pk_add_f16 v79, v115, v155 neg_lo:[0,1] neg_hi:[0,1]
	v_pk_add_f16 v80, v116, v156 neg_lo:[0,1] neg_hi:[0,1]
	v_pk_add_f16 v81, v117, v157 neg_lo:[0,1] neg_hi:[0,1]
	v_exp_f16_sdwa v82, v78 dst_sel:WORD_0 dst_unused:UNUSED_PAD src0_sel:WORD_0
	v_exp_f16_sdwa v83, v79 dst_sel:WORD_0 dst_unused:UNUSED_PAD src0_sel:WORD_0
	v_exp_f16_sdwa v84, v80 dst_sel:WORD_0 dst_unused:UNUSED_PAD src0_sel:WORD_0
	v_exp_f16_sdwa v85, v81 dst_sel:WORD_0 dst_unused:UNUSED_PAD src0_sel:WORD_0
	v_exp_f16_sdwa v82, v78 dst_sel:WORD_1 dst_unused:UNUSED_PRESERVE src0_sel:WORD_1
	v_exp_f16_sdwa v83, v79 dst_sel:WORD_1 dst_unused:UNUSED_PRESERVE src0_sel:WORD_1
	v_exp_f16_sdwa v84, v80 dst_sel:WORD_1 dst_unused:UNUSED_PRESERVE src0_sel:WORD_1
	v_exp_f16_sdwa v85, v81 dst_sel:WORD_1 dst_unused:UNUSED_PRESERVE src0_sel:WORD_1
	s_nop 0
	v_pk_add_f16 v62, v62, v85
	v_pk_add_f16 v63, v63, v84
	v_pk_add_f16 v64, v64, v83
	v_pk_add_f16 v65, v65, v82
	v_rcp_f16_e32 v81, v62
	v_rcp_f16_sdwa v62, v62 dst_sel:DWORD dst_unused:UNUSED_PAD src0_sel:WORD_1
	v_rcp_f16_e32 v78, v65
	v_rcp_f16_sdwa v65, v65 dst_sel:DWORD dst_unused:UNUSED_PAD src0_sel:WORD_1
	v_rcp_f16_e32 v79, v64
	v_rcp_f16_sdwa v64, v64 dst_sel:DWORD dst_unused:UNUSED_PAD src0_sel:WORD_1
	v_rcp_f16_e32 v80, v63
	v_rcp_f16_sdwa v63, v63 dst_sel:DWORD dst_unused:UNUSED_PAD src0_sel:WORD_1
	v_pk_fma_f16 v45, v17, v85, v45
	v_pack_b32_f16 v62, v81, v62
	v_pk_fma_f16 v44, v16, v84, v44
	v_pk_fma_f16 v43, v15, v83, v43
	v_pk_fma_f16 v42, v14, v82, v42
	v_pack_b32_f16 v65, v78, v65
	v_pack_b32_f16 v64, v79, v64
	v_pack_b32_f16 v63, v80, v63
	v_pk_mul_f16 v45, v45, v62
	s_waitcnt vmcnt(6)
	v_pk_mul_f16 v62, v182, v150 op_sel_hi:[0,1]
	v_pk_mul_f16 v42, v42, v65
	v_pk_mul_f16 v43, v43, v64
	v_pk_mul_f16 v44, v44, v63
	v_pk_mul_f16 v63, v182, v151 op_sel_hi:[0,1]
	v_pk_mul_f16 v64, v182, v152 op_sel_hi:[0,1]
	v_pk_mul_f16 v65, v182, v153 op_sel_hi:[0,1]
	v_pk_mul_f16 v78, v180, v150 op_sel_hi:[0,1]
	v_pk_mul_f16 v82, v181, v150 op_sel_hi:[0,1]
	v_pk_fma_f16 v50, v50, v150, v62
	v_pk_fma_f16 v66, v66, v150, v62
	v_pk_fma_f16 v62, v94, v150, v62
	v_pk_mul_f16 v79, v180, v151 op_sel_hi:[0,1]
	v_pk_maximum3_f16 v114, v50, v66, v62
	v_pk_mul_f16 v80, v180, v152 op_sel_hi:[0,1]
	v_pk_mul_f16 v81, v180, v153 op_sel_hi:[0,1]
	v_pk_mul_f16 v83, v181, v151 op_sel_hi:[0,1]
	v_pk_mul_f16 v84, v181, v152 op_sel_hi:[0,1]
	v_pk_mul_f16 v85, v181, v153 op_sel_hi:[0,1]
	v_pk_fma_f16 v53, v53, v153, v65
	v_pk_fma_f16 v52, v52, v152, v64
	v_pk_fma_f16 v51, v51, v151, v63
	v_pk_fma_f16 v69, v69, v153, v65
	v_pk_fma_f16 v68, v68, v152, v64
	v_pk_fma_f16 v67, v67, v151, v63
	v_pk_fma_f16 v65, v97, v153, v65
	v_pk_fma_f16 v64, v96, v152, v64
	v_pk_fma_f16 v63, v95, v151, v63
	v_pk_fma_f16 v89, v18, v150, v78
	v_pk_fma_f16 v97, v30, v150, v78
	v_pk_fma_f16 v78, v54, v150, v78
	v_pk_fma_f16 v105, v74, v150, v82
	v_pk_fma_f16 v109, v98, v150, v82
	v_pk_fma_f16 v82, v118, v150, v82
	v_pk_maximum3_f16 v115, v51, v67, v63
	v_pk_maximum3_f16 v116, v52, v68, v64
	v_pk_maximum3_f16 v117, v53, v69, v65
	v_pk_maximum3_f16 v122, v89, v97, v78
	v_pk_fma_f16 v86, v21, v153, v81
	v_pk_maximum3_f16 v126, v105, v109, v82
	v_pk_fma_f16 v87, v20, v152, v80
	v_pk_maximum3_f16 v114, v114, v122, v126
	v_pk_fma_f16 v88, v19, v151, v79
	v_pk_fma_f16 v94, v33, v153, v81
	v_pk_fma_f16 v95, v32, v152, v80
	v_pk_fma_f16 v96, v31, v151, v79
	v_pk_fma_f16 v81, v57, v153, v81
	v_pk_fma_f16 v80, v56, v152, v80
	v_pk_fma_f16 v79, v55, v151, v79
	v_pk_fma_f16 v102, v77, v153, v85
	v_pk_fma_f16 v103, v76, v152, v84
	v_pk_fma_f16 v104, v75, v151, v83
	v_pk_fma_f16 v106, v101, v153, v85
	v_pk_fma_f16 v107, v100, v152, v84
	v_pk_fma_f16 v108, v99, v151, v83
	v_pk_fma_f16 v85, v121, v153, v85
	v_pk_fma_f16 v84, v120, v152, v84
	v_pk_fma_f16 v83, v119, v151, v83
	v_pk_maximum3_f16 v123, v88, v96, v79
	v_pk_maximum3_f16 v124, v87, v95, v80
	v_pk_maximum3_f16 v125, v86, v94, v81
	v_pk_maximum3_f16 v128, v103, v107, v84
	v_pk_maximum3_f16 v129, v102, v106, v85
	v_pk_maximum3_f16 v127, v104, v108, v83
	v_pk_maximum3_f16 v115, v115, v123, v127
	v_pk_maximum3_f16 v116, v116, v124, v128
	v_pk_maximum3_f16 v117, v117, v125, v129
	v_pk_add_f16 v50, v50, v114 neg_lo:[0,1] neg_hi:[0,1]
	v_pk_add_f16 v51, v51, v115 neg_lo:[0,1] neg_hi:[0,1]
	v_pk_add_f16 v52, v52, v116 neg_lo:[0,1] neg_hi:[0,1]
	v_pk_add_f16 v53, v53, v117 neg_lo:[0,1] neg_hi:[0,1]
	v_pk_add_f16 v66, v66, v114 neg_lo:[0,1] neg_hi:[0,1]
	v_exp_f16_sdwa v122, v50 dst_sel:WORD_0 dst_unused:UNUSED_PAD src0_sel:WORD_0
	v_exp_f16_sdwa v123, v51 dst_sel:WORD_0 dst_unused:UNUSED_PAD src0_sel:WORD_0
	v_exp_f16_sdwa v124, v52 dst_sel:WORD_0 dst_unused:UNUSED_PAD src0_sel:WORD_0
	v_exp_f16_sdwa v125, v53 dst_sel:WORD_0 dst_unused:UNUSED_PAD src0_sel:WORD_0
	v_exp_f16_sdwa v122, v50 dst_sel:WORD_1 dst_unused:UNUSED_PRESERVE src0_sel:WORD_1
	v_exp_f16_sdwa v123, v51 dst_sel:WORD_1 dst_unused:UNUSED_PRESERVE src0_sel:WORD_1
	v_exp_f16_sdwa v124, v52 dst_sel:WORD_1 dst_unused:UNUSED_PRESERVE src0_sel:WORD_1
	v_exp_f16_sdwa v125, v53 dst_sel:WORD_1 dst_unused:UNUSED_PRESERVE src0_sel:WORD_1
	v_pk_add_f16 v67, v67, v115 neg_lo:[0,1] neg_hi:[0,1]
	v_pk_add_f16 v50, v125, 0
	v_pk_fma_f16 v22, v22, v122, 0
	v_pk_add_f16 v51, v124, 0
	v_pk_add_f16 v52, v123, 0
	v_pk_add_f16 v53, v122, 0
	v_pk_fma_f16 v23, v23, v123, 0
	v_pk_fma_f16 v24, v24, v124, 0
	v_pk_fma_f16 v25, v25, v125, 0
	v_pk_add_f16 v68, v68, v116 neg_lo:[0,1] neg_hi:[0,1]
	v_pk_add_f16 v69, v69, v117 neg_lo:[0,1] neg_hi:[0,1]
	v_exp_f16_sdwa v122, v66 dst_sel:WORD_0 dst_unused:UNUSED_PAD src0_sel:WORD_0
	v_exp_f16_sdwa v123, v67 dst_sel:WORD_0 dst_unused:UNUSED_PAD src0_sel:WORD_0
	v_exp_f16_sdwa v124, v68 dst_sel:WORD_0 dst_unused:UNUSED_PAD src0_sel:WORD_0
	v_exp_f16_sdwa v125, v69 dst_sel:WORD_0 dst_unused:UNUSED_PAD src0_sel:WORD_0
	v_exp_f16_sdwa v122, v66 dst_sel:WORD_1 dst_unused:UNUSED_PRESERVE src0_sel:WORD_1
	v_exp_f16_sdwa v123, v67 dst_sel:WORD_1 dst_unused:UNUSED_PRESERVE src0_sel:WORD_1
	v_exp_f16_sdwa v124, v68 dst_sel:WORD_1 dst_unused:UNUSED_PRESERVE src0_sel:WORD_1
	v_exp_f16_sdwa v125, v69 dst_sel:WORD_1 dst_unused:UNUSED_PRESERVE src0_sel:WORD_1
	s_nop 0
	v_pk_add_f16 v50, v50, v125
	v_pk_fma_f16 v22, v34, v122, v22
	v_pk_add_f16 v34, v62, v114 neg_lo:[0,1] neg_hi:[0,1]
	v_pk_add_f16 v53, v53, v122
	v_pk_add_f16 v52, v52, v123
	v_pk_add_f16 v51, v51, v124
	v_pk_fma_f16 v25, v37, v125, v25
	v_pk_fma_f16 v24, v36, v124, v24
	v_pk_fma_f16 v23, v35, v123, v23
	v_pk_add_f16 v35, v63, v115 neg_lo:[0,1] neg_hi:[0,1]
	v_pk_add_f16 v36, v64, v116 neg_lo:[0,1] neg_hi:[0,1]
	v_pk_add_f16 v37, v65, v117 neg_lo:[0,1] neg_hi:[0,1]
	v_exp_f16_sdwa v62, v34 dst_sel:WORD_0 dst_unused:UNUSED_PAD src0_sel:WORD_0
	v_exp_f16_sdwa v63, v35 dst_sel:WORD_0 dst_unused:UNUSED_PAD src0_sel:WORD_0
	v_exp_f16_sdwa v64, v36 dst_sel:WORD_0 dst_unused:UNUSED_PAD src0_sel:WORD_0
	v_exp_f16_sdwa v65, v37 dst_sel:WORD_0 dst_unused:UNUSED_PAD src0_sel:WORD_0
	v_exp_f16_sdwa v62, v34 dst_sel:WORD_1 dst_unused:UNUSED_PRESERVE src0_sel:WORD_1
	v_exp_f16_sdwa v63, v35 dst_sel:WORD_1 dst_unused:UNUSED_PRESERVE src0_sel:WORD_1
	v_exp_f16_sdwa v64, v36 dst_sel:WORD_1 dst_unused:UNUSED_PRESERVE src0_sel:WORD_1
	v_exp_f16_sdwa v65, v37 dst_sel:WORD_1 dst_unused:UNUSED_PRESERVE src0_sel:WORD_1
	s_nop 0
	v_pk_add_f16 v34, v50, v65
	v_pk_add_f16 v35, v51, v64
	v_pk_add_f16 v36, v52, v63
	v_pk_add_f16 v37, v53, v62
	v_pk_fma_f16 v22, v46, v62, v22
	v_pk_fma_f16 v23, v47, v63, v23
	v_pk_fma_f16 v24, v48, v64, v24
	v_pk_fma_f16 v25, v49, v65, v25
	v_pk_add_f16 v46, v89, v114 neg_lo:[0,1] neg_hi:[0,1]
	v_pk_add_f16 v47, v88, v115 neg_lo:[0,1] neg_hi:[0,1]
	v_pk_add_f16 v48, v87, v116 neg_lo:[0,1] neg_hi:[0,1]
	v_pk_add_f16 v49, v86, v117 neg_lo:[0,1] neg_hi:[0,1]
	v_exp_f16_sdwa v50, v46 dst_sel:WORD_0 dst_unused:UNUSED_PAD src0_sel:WORD_0
	v_exp_f16_sdwa v51, v47 dst_sel:WORD_0 dst_unused:UNUSED_PAD src0_sel:WORD_0
	v_exp_f16_sdwa v52, v48 dst_sel:WORD_0 dst_unused:UNUSED_PAD src0_sel:WORD_0
	v_exp_f16_sdwa v53, v49 dst_sel:WORD_0 dst_unused:UNUSED_PAD src0_sel:WORD_0
	v_exp_f16_sdwa v50, v46 dst_sel:WORD_1 dst_unused:UNUSED_PRESERVE src0_sel:WORD_1
	v_exp_f16_sdwa v51, v47 dst_sel:WORD_1 dst_unused:UNUSED_PRESERVE src0_sel:WORD_1
	v_exp_f16_sdwa v52, v48 dst_sel:WORD_1 dst_unused:UNUSED_PRESERVE src0_sel:WORD_1
	v_exp_f16_sdwa v53, v49 dst_sel:WORD_1 dst_unused:UNUSED_PRESERVE src0_sel:WORD_1
	v_pk_add_f16 v46, v97, v114 neg_lo:[0,1] neg_hi:[0,1]
	v_pk_add_f16 v34, v34, v53
	v_pk_add_f16 v37, v37, v50
	v_pk_add_f16 v36, v36, v51
	v_pk_add_f16 v35, v35, v52
	v_pk_fma_f16 v25, v9, v53, v25
	v_pk_fma_f16 v24, v8, v52, v24
	v_pk_fma_f16 v23, v7, v51, v23
	v_pk_fma_f16 v22, v6, v50, v22
	v_pk_add_f16 v47, v96, v115 neg_lo:[0,1] neg_hi:[0,1]
	v_pk_add_f16 v48, v95, v116 neg_lo:[0,1] neg_hi:[0,1]
	v_pk_add_f16 v49, v94, v117 neg_lo:[0,1] neg_hi:[0,1]
	v_exp_f16_sdwa v50, v46 dst_sel:WORD_0 dst_unused:UNUSED_PAD src0_sel:WORD_0
	v_exp_f16_sdwa v51, v47 dst_sel:WORD_0 dst_unused:UNUSED_PAD src0_sel:WORD_0
	v_exp_f16_sdwa v52, v48 dst_sel:WORD_0 dst_unused:UNUSED_PAD src0_sel:WORD_0
	v_exp_f16_sdwa v53, v49 dst_sel:WORD_0 dst_unused:UNUSED_PAD src0_sel:WORD_0
	v_exp_f16_sdwa v50, v46 dst_sel:WORD_1 dst_unused:UNUSED_PRESERVE src0_sel:WORD_1
	v_exp_f16_sdwa v51, v47 dst_sel:WORD_1 dst_unused:UNUSED_PRESERVE src0_sel:WORD_1
	v_exp_f16_sdwa v52, v48 dst_sel:WORD_1 dst_unused:UNUSED_PRESERVE src0_sel:WORD_1
	v_exp_f16_sdwa v53, v49 dst_sel:WORD_1 dst_unused:UNUSED_PRESERVE src0_sel:WORD_1
	v_pk_add_f16 v46, v78, v114 neg_lo:[0,1] neg_hi:[0,1]
	v_pk_add_f16 v34, v34, v53
	v_pk_add_f16 v35, v35, v52
	v_pk_add_f16 v36, v36, v51
	v_pk_add_f16 v37, v37, v50
	v_pk_fma_f16 v22, v10, v50, v22
	v_pk_fma_f16 v23, v11, v51, v23
	v_pk_fma_f16 v24, v12, v52, v24
	v_pk_fma_f16 v25, v13, v53, v25
	v_pk_add_f16 v47, v79, v115 neg_lo:[0,1] neg_hi:[0,1]
	v_pk_add_f16 v48, v80, v116 neg_lo:[0,1] neg_hi:[0,1]
	v_pk_add_f16 v49, v81, v117 neg_lo:[0,1] neg_hi:[0,1]
	v_exp_f16_sdwa v50, v46 dst_sel:WORD_0 dst_unused:UNUSED_PAD src0_sel:WORD_0
	v_exp_f16_sdwa v51, v47 dst_sel:WORD_0 dst_unused:UNUSED_PAD src0_sel:WORD_0
	v_exp_f16_sdwa v52, v48 dst_sel:WORD_0 dst_unused:UNUSED_PAD src0_sel:WORD_0
	v_exp_f16_sdwa v53, v49 dst_sel:WORD_0 dst_unused:UNUSED_PAD src0_sel:WORD_0
	v_exp_f16_sdwa v50, v46 dst_sel:WORD_1 dst_unused:UNUSED_PRESERVE src0_sel:WORD_1
	v_exp_f16_sdwa v51, v47 dst_sel:WORD_1 dst_unused:UNUSED_PRESERVE src0_sel:WORD_1
	v_exp_f16_sdwa v52, v48 dst_sel:WORD_1 dst_unused:UNUSED_PRESERVE src0_sel:WORD_1
	v_exp_f16_sdwa v53, v49 dst_sel:WORD_1 dst_unused:UNUSED_PRESERVE src0_sel:WORD_1
	v_pk_add_f16 v46, v105, v114 neg_lo:[0,1] neg_hi:[0,1]
	v_pk_add_f16 v34, v34, v53
	v_pk_add_f16 v37, v37, v50
	v_pk_add_f16 v36, v36, v51
	v_pk_add_f16 v35, v35, v52
	v_pk_fma_f16 v25, v17, v53, v25
	v_pk_fma_f16 v24, v16, v52, v24
	v_pk_fma_f16 v23, v15, v51, v23
	v_pk_fma_f16 v22, v14, v50, v22
	v_pk_add_f16 v47, v104, v115 neg_lo:[0,1] neg_hi:[0,1]
	v_pk_add_f16 v48, v103, v116 neg_lo:[0,1] neg_hi:[0,1]
	v_pk_add_f16 v49, v102, v117 neg_lo:[0,1] neg_hi:[0,1]
	v_exp_f16_sdwa v50, v46 dst_sel:WORD_0 dst_unused:UNUSED_PAD src0_sel:WORD_0
	v_exp_f16_sdwa v51, v47 dst_sel:WORD_0 dst_unused:UNUSED_PAD src0_sel:WORD_0
	v_exp_f16_sdwa v52, v48 dst_sel:WORD_0 dst_unused:UNUSED_PAD src0_sel:WORD_0
	v_exp_f16_sdwa v53, v49 dst_sel:WORD_0 dst_unused:UNUSED_PAD src0_sel:WORD_0
	v_exp_f16_sdwa v50, v46 dst_sel:WORD_1 dst_unused:UNUSED_PRESERVE src0_sel:WORD_1
	v_exp_f16_sdwa v51, v47 dst_sel:WORD_1 dst_unused:UNUSED_PRESERVE src0_sel:WORD_1
	v_exp_f16_sdwa v52, v48 dst_sel:WORD_1 dst_unused:UNUSED_PRESERVE src0_sel:WORD_1
	v_exp_f16_sdwa v53, v49 dst_sel:WORD_1 dst_unused:UNUSED_PRESERVE src0_sel:WORD_1
	v_pk_add_f16 v46, v109, v114 neg_lo:[0,1] neg_hi:[0,1]
	v_pk_add_f16 v34, v34, v53
	v_pk_add_f16 v35, v35, v52
	v_pk_add_f16 v36, v36, v51
	v_pk_add_f16 v37, v37, v50
	v_pk_fma_f16 v22, v26, v50, v22
	v_pk_fma_f16 v23, v27, v51, v23
	v_pk_fma_f16 v24, v28, v52, v24
	v_pk_fma_f16 v25, v29, v53, v25
	v_pk_add_f16 v47, v108, v115 neg_lo:[0,1] neg_hi:[0,1]
	v_pk_add_f16 v48, v107, v116 neg_lo:[0,1] neg_hi:[0,1]
	v_pk_add_f16 v49, v106, v117 neg_lo:[0,1] neg_hi:[0,1]
	v_exp_f16_sdwa v50, v46 dst_sel:WORD_0 dst_unused:UNUSED_PAD src0_sel:WORD_0
	v_exp_f16_sdwa v51, v47 dst_sel:WORD_0 dst_unused:UNUSED_PAD src0_sel:WORD_0
	v_exp_f16_sdwa v52, v48 dst_sel:WORD_0 dst_unused:UNUSED_PAD src0_sel:WORD_0
	v_exp_f16_sdwa v53, v49 dst_sel:WORD_0 dst_unused:UNUSED_PAD src0_sel:WORD_0
	v_exp_f16_sdwa v50, v46 dst_sel:WORD_1 dst_unused:UNUSED_PRESERVE src0_sel:WORD_1
	v_exp_f16_sdwa v51, v47 dst_sel:WORD_1 dst_unused:UNUSED_PRESERVE src0_sel:WORD_1
	v_exp_f16_sdwa v52, v48 dst_sel:WORD_1 dst_unused:UNUSED_PRESERVE src0_sel:WORD_1
	v_exp_f16_sdwa v53, v49 dst_sel:WORD_1 dst_unused:UNUSED_PRESERVE src0_sel:WORD_1
	v_pk_add_f16 v46, v82, v114 neg_lo:[0,1] neg_hi:[0,1]
	v_pk_add_f16 v34, v34, v53
	v_pk_add_f16 v37, v37, v50
	v_pk_add_f16 v36, v36, v51
	v_pk_add_f16 v35, v35, v52
	v_pk_fma_f16 v25, v41, v53, v25
	v_pk_fma_f16 v24, v40, v52, v24
	v_pk_fma_f16 v23, v39, v51, v23
	v_pk_fma_f16 v22, v38, v50, v22
	v_pk_add_f16 v47, v83, v115 neg_lo:[0,1] neg_hi:[0,1]
	v_pk_add_f16 v48, v84, v116 neg_lo:[0,1] neg_hi:[0,1]
	v_pk_add_f16 v49, v85, v117 neg_lo:[0,1] neg_hi:[0,1]
	v_exp_f16_sdwa v50, v46 dst_sel:WORD_0 dst_unused:UNUSED_PAD src0_sel:WORD_0
	v_exp_f16_sdwa v51, v47 dst_sel:WORD_0 dst_unused:UNUSED_PAD src0_sel:WORD_0
	v_exp_f16_sdwa v52, v48 dst_sel:WORD_0 dst_unused:UNUSED_PAD src0_sel:WORD_0
	v_exp_f16_sdwa v53, v49 dst_sel:WORD_0 dst_unused:UNUSED_PAD src0_sel:WORD_0
	v_exp_f16_sdwa v50, v46 dst_sel:WORD_1 dst_unused:UNUSED_PRESERVE src0_sel:WORD_1
	v_exp_f16_sdwa v51, v47 dst_sel:WORD_1 dst_unused:UNUSED_PRESERVE src0_sel:WORD_1
	v_exp_f16_sdwa v52, v48 dst_sel:WORD_1 dst_unused:UNUSED_PRESERVE src0_sel:WORD_1
	v_exp_f16_sdwa v53, v49 dst_sel:WORD_1 dst_unused:UNUSED_PRESERVE src0_sel:WORD_1
	s_nop 0
	v_pk_add_f16 v34, v34, v53
	v_pk_add_f16 v35, v35, v52
	v_rcp_f16_e32 v48, v34
	v_rcp_f16_sdwa v34, v34 dst_sel:DWORD dst_unused:UNUSED_PAD src0_sel:WORD_1
	v_pk_add_f16 v36, v36, v51
	v_rcp_f16_e32 v49, v35
	v_rcp_f16_sdwa v35, v35 dst_sel:DWORD dst_unused:UNUSED_PAD src0_sel:WORD_1
	v_pk_add_f16 v37, v37, v50
	v_rcp_f16_e32 v47, v36
	v_rcp_f16_sdwa v36, v36 dst_sel:DWORD dst_unused:UNUSED_PAD src0_sel:WORD_1
	v_rcp_f16_e32 v46, v37
	v_rcp_f16_sdwa v37, v37 dst_sel:DWORD dst_unused:UNUSED_PAD src0_sel:WORD_1
	v_pk_fma_f16 v25, v61, v53, v25
	v_pack_b32_f16 v34, v48, v34
	v_pk_fma_f16 v24, v60, v52, v24
	v_pk_mul_f16 v25, v25, v34
	v_pack_b32_f16 v34, v49, v35
	v_pk_fma_f16 v23, v59, v51, v23
	v_pk_mul_f16 v24, v24, v34
	v_pack_b32_f16 v34, v47, v36
	v_pk_fma_f16 v22, v58, v50, v22
	v_pk_mul_f16 v23, v23, v34
	v_pack_b32_f16 v34, v46, v37
	v_pk_mul_f16 v22, v22, v34
	s_waitcnt vmcnt(0)
	v_pk_mul_f16 v34, v182, v146 op_sel_hi:[0,1]
	v_pk_mul_f16 v35, v182, v147 op_sel_hi:[0,1]
	v_pk_mul_f16 v36, v182, v148 op_sel_hi:[0,1]
	v_pk_mul_f16 v37, v182, v149 op_sel_hi:[0,1]
	v_pk_mul_f16 v46, v180, v146 op_sel_hi:[0,1]
	v_pk_mul_f16 v47, v180, v147 op_sel_hi:[0,1]
	v_pk_mul_f16 v48, v180, v148 op_sel_hi:[0,1]
	v_pk_mul_f16 v49, v180, v149 op_sel_hi:[0,1]
	v_pk_mul_f16 v50, v181, v146 op_sel_hi:[0,1]
	v_pk_mul_f16 v51, v181, v147 op_sel_hi:[0,1]
	v_pk_mul_f16 v52, v181, v148 op_sel_hi:[0,1]
	v_pk_mul_f16 v53, v181, v149 op_sel_hi:[0,1]
	v_pk_fma_f16 v21, v21, v149, v37
	v_pk_fma_f16 v20, v20, v148, v36
	v_pk_fma_f16 v19, v19, v147, v35
	v_pk_fma_f16 v18, v18, v146, v34
	v_pk_fma_f16 v33, v33, v149, v37
	v_pk_fma_f16 v32, v32, v148, v36
	v_pk_fma_f16 v31, v31, v147, v35
	v_pk_fma_f16 v30, v30, v146, v34
	v_pk_fma_f16 v37, v57, v149, v37
	v_pk_fma_f16 v36, v56, v148, v36
	v_pk_fma_f16 v35, v55, v147, v35
	v_pk_fma_f16 v34, v54, v146, v34
	v_pk_maximum3_f16 v79, v19, v31, v35
	v_pk_maximum3_f16 v80, v20, v32, v36
	v_pk_maximum3_f16 v81, v21, v33, v37
	v_pk_fma_f16 v54, v77, v149, v49
	v_pk_maximum3_f16 v78, v18, v30, v34
	v_pk_fma_f16 v55, v76, v148, v48
	v_pk_fma_f16 v56, v75, v147, v47
	v_pk_fma_f16 v57, v74, v146, v46
	v_pk_fma_f16 v62, v101, v149, v49
	v_pk_fma_f16 v63, v100, v148, v48
	v_pk_fma_f16 v64, v99, v147, v47
	v_pk_fma_f16 v65, v98, v146, v46
	v_pk_fma_f16 v49, v121, v149, v49
	v_pk_fma_f16 v48, v120, v148, v48
	v_pk_fma_f16 v47, v119, v147, v47
	v_pk_fma_f16 v46, v118, v146, v46
	v_pk_fma_f16 v66, v133, v149, v53
	v_pk_fma_f16 v67, v132, v148, v52
	v_pk_fma_f16 v68, v131, v147, v51
	v_pk_fma_f16 v69, v130, v146, v50
	v_pk_fma_f16 v74, v141, v149, v53
	v_pk_fma_f16 v75, v140, v148, v52
	v_pk_fma_f16 v76, v139, v147, v51
	v_pk_fma_f16 v77, v138, v146, v50
	v_pk_fma_f16 v53, v145, v149, v53
	v_pk_fma_f16 v52, v144, v148, v52
	v_pk_fma_f16 v51, v143, v147, v51
	v_pk_fma_f16 v50, v142, v146, v50
	v_pk_maximum3_f16 v82, v57, v65, v46
	v_pk_maximum3_f16 v83, v56, v64, v47
	v_pk_maximum3_f16 v84, v55, v63, v48
	v_pk_maximum3_f16 v85, v54, v62, v49
	v_pk_maximum3_f16 v87, v68, v76, v51
	v_pk_maximum3_f16 v86, v69, v77, v50
	v_pk_maximum3_f16 v88, v67, v75, v52
	v_pk_maximum3_f16 v89, v66, v74, v53
	v_pk_maximum3_f16 v78, v78, v82, v86
	v_pk_maximum3_f16 v79, v79, v83, v87
	v_pk_maximum3_f16 v80, v80, v84, v88
	v_pk_maximum3_f16 v81, v81, v85, v89
	s_nop 0
	v_pk_add_f16 v18, v18, v78 neg_lo:[0,1] neg_hi:[0,1]
	v_pk_add_f16 v19, v19, v79 neg_lo:[0,1] neg_hi:[0,1]
	v_pk_add_f16 v20, v20, v80 neg_lo:[0,1] neg_hi:[0,1]
	v_pk_add_f16 v21, v21, v81 neg_lo:[0,1] neg_hi:[0,1]
	v_pk_add_f16 v30, v30, v78 neg_lo:[0,1] neg_hi:[0,1]
	v_exp_f16_sdwa v82, v18 dst_sel:WORD_0 dst_unused:UNUSED_PAD src0_sel:WORD_0
	v_exp_f16_sdwa v83, v19 dst_sel:WORD_0 dst_unused:UNUSED_PAD src0_sel:WORD_0
	v_exp_f16_sdwa v84, v20 dst_sel:WORD_0 dst_unused:UNUSED_PAD src0_sel:WORD_0
	v_exp_f16_sdwa v85, v21 dst_sel:WORD_0 dst_unused:UNUSED_PAD src0_sel:WORD_0
	v_exp_f16_sdwa v82, v18 dst_sel:WORD_1 dst_unused:UNUSED_PRESERVE src0_sel:WORD_1
	v_exp_f16_sdwa v83, v19 dst_sel:WORD_1 dst_unused:UNUSED_PRESERVE src0_sel:WORD_1
	v_exp_f16_sdwa v84, v20 dst_sel:WORD_1 dst_unused:UNUSED_PRESERVE src0_sel:WORD_1
	v_exp_f16_sdwa v85, v21 dst_sel:WORD_1 dst_unused:UNUSED_PRESERVE src0_sel:WORD_1
	v_pk_add_f16 v31, v31, v79 neg_lo:[0,1] neg_hi:[0,1]
	v_pk_add_f16 v18, v82, 0
	v_pk_add_f16 v19, v83, 0
	v_pk_add_f16 v20, v84, 0
	v_pk_add_f16 v21, v85, 0
	v_pk_fma_f16 v6, v6, v82, 0
	v_pk_fma_f16 v7, v7, v83, 0
	v_pk_fma_f16 v8, v8, v84, 0
	v_pk_fma_f16 v9, v9, v85, 0
	v_pk_add_f16 v32, v32, v80 neg_lo:[0,1] neg_hi:[0,1]
	v_pk_add_f16 v33, v33, v81 neg_lo:[0,1] neg_hi:[0,1]
	v_exp_f16_sdwa v82, v30 dst_sel:WORD_0 dst_unused:UNUSED_PAD src0_sel:WORD_0
	v_exp_f16_sdwa v83, v31 dst_sel:WORD_0 dst_unused:UNUSED_PAD src0_sel:WORD_0
	v_exp_f16_sdwa v84, v32 dst_sel:WORD_0 dst_unused:UNUSED_PAD src0_sel:WORD_0
	v_exp_f16_sdwa v85, v33 dst_sel:WORD_0 dst_unused:UNUSED_PAD src0_sel:WORD_0
	v_exp_f16_sdwa v82, v30 dst_sel:WORD_1 dst_unused:UNUSED_PRESERVE src0_sel:WORD_1
	v_exp_f16_sdwa v83, v31 dst_sel:WORD_1 dst_unused:UNUSED_PRESERVE src0_sel:WORD_1
	v_exp_f16_sdwa v84, v32 dst_sel:WORD_1 dst_unused:UNUSED_PRESERVE src0_sel:WORD_1
	v_exp_f16_sdwa v85, v33 dst_sel:WORD_1 dst_unused:UNUSED_PRESERVE src0_sel:WORD_1
	s_nop 0
	v_pk_add_f16 v21, v21, v85
	v_pk_add_f16 v20, v20, v84
	v_pk_add_f16 v19, v19, v83
	v_pk_add_f16 v18, v18, v82
	v_pk_fma_f16 v9, v13, v85, v9
	v_pk_fma_f16 v8, v12, v84, v8
	v_pk_fma_f16 v7, v11, v83, v7
	v_pk_fma_f16 v6, v10, v82, v6
	v_pk_add_f16 v10, v34, v78 neg_lo:[0,1] neg_hi:[0,1]
	v_pk_add_f16 v11, v35, v79 neg_lo:[0,1] neg_hi:[0,1]
	v_pk_add_f16 v12, v36, v80 neg_lo:[0,1] neg_hi:[0,1]
	v_pk_add_f16 v13, v37, v81 neg_lo:[0,1] neg_hi:[0,1]
	v_exp_f16_sdwa v30, v10 dst_sel:WORD_0 dst_unused:UNUSED_PAD src0_sel:WORD_0
	v_exp_f16_sdwa v31, v11 dst_sel:WORD_0 dst_unused:UNUSED_PAD src0_sel:WORD_0
	v_exp_f16_sdwa v32, v12 dst_sel:WORD_0 dst_unused:UNUSED_PAD src0_sel:WORD_0
	v_exp_f16_sdwa v33, v13 dst_sel:WORD_0 dst_unused:UNUSED_PAD src0_sel:WORD_0
	v_exp_f16_sdwa v30, v10 dst_sel:WORD_1 dst_unused:UNUSED_PRESERVE src0_sel:WORD_1
	v_exp_f16_sdwa v31, v11 dst_sel:WORD_1 dst_unused:UNUSED_PRESERVE src0_sel:WORD_1
	v_exp_f16_sdwa v32, v12 dst_sel:WORD_1 dst_unused:UNUSED_PRESERVE src0_sel:WORD_1
	v_exp_f16_sdwa v33, v13 dst_sel:WORD_1 dst_unused:UNUSED_PRESERVE src0_sel:WORD_1
	v_pk_add_f16 v10, v18, v30
	v_pk_add_f16 v11, v19, v31
	v_pk_add_f16 v12, v20, v32
	v_pk_add_f16 v13, v21, v33
	v_pk_fma_f16 v6, v14, v30, v6
	v_pk_fma_f16 v7, v15, v31, v7
	v_pk_fma_f16 v8, v16, v32, v8
	v_pk_fma_f16 v9, v17, v33, v9
	v_pk_add_f16 v14, v57, v78 neg_lo:[0,1] neg_hi:[0,1]
	v_pk_add_f16 v15, v56, v79 neg_lo:[0,1] neg_hi:[0,1]
	v_pk_add_f16 v16, v55, v80 neg_lo:[0,1] neg_hi:[0,1]
	v_pk_add_f16 v17, v54, v81 neg_lo:[0,1] neg_hi:[0,1]
	v_exp_f16_sdwa v18, v14 dst_sel:WORD_0 dst_unused:UNUSED_PAD src0_sel:WORD_0
	v_exp_f16_sdwa v19, v15 dst_sel:WORD_0 dst_unused:UNUSED_PAD src0_sel:WORD_0
	v_exp_f16_sdwa v20, v16 dst_sel:WORD_0 dst_unused:UNUSED_PAD src0_sel:WORD_0
	v_exp_f16_sdwa v21, v17 dst_sel:WORD_0 dst_unused:UNUSED_PAD src0_sel:WORD_0
	v_exp_f16_sdwa v18, v14 dst_sel:WORD_1 dst_unused:UNUSED_PRESERVE src0_sel:WORD_1
	v_exp_f16_sdwa v19, v15 dst_sel:WORD_1 dst_unused:UNUSED_PRESERVE src0_sel:WORD_1
	v_exp_f16_sdwa v20, v16 dst_sel:WORD_1 dst_unused:UNUSED_PRESERVE src0_sel:WORD_1
	v_exp_f16_sdwa v21, v17 dst_sel:WORD_1 dst_unused:UNUSED_PRESERVE src0_sel:WORD_1
	v_pk_add_f16 v14, v65, v78 neg_lo:[0,1] neg_hi:[0,1]
	v_pk_add_f16 v13, v13, v21
	v_pk_add_f16 v12, v12, v20
	v_pk_add_f16 v11, v11, v19
	v_pk_add_f16 v10, v10, v18
	v_pk_fma_f16 v9, v29, v21, v9
	v_pk_fma_f16 v8, v28, v20, v8
	v_pk_fma_f16 v7, v27, v19, v7
	v_pk_fma_f16 v6, v26, v18, v6
	v_pk_add_f16 v15, v64, v79 neg_lo:[0,1] neg_hi:[0,1]
	v_pk_add_f16 v16, v63, v80 neg_lo:[0,1] neg_hi:[0,1]
	v_pk_add_f16 v17, v62, v81 neg_lo:[0,1] neg_hi:[0,1]
	v_exp_f16_sdwa v18, v14 dst_sel:WORD_0 dst_unused:UNUSED_PAD src0_sel:WORD_0
	v_exp_f16_sdwa v19, v15 dst_sel:WORD_0 dst_unused:UNUSED_PAD src0_sel:WORD_0
	v_exp_f16_sdwa v20, v16 dst_sel:WORD_0 dst_unused:UNUSED_PAD src0_sel:WORD_0
	v_exp_f16_sdwa v21, v17 dst_sel:WORD_0 dst_unused:UNUSED_PAD src0_sel:WORD_0
	v_exp_f16_sdwa v18, v14 dst_sel:WORD_1 dst_unused:UNUSED_PRESERVE src0_sel:WORD_1
	v_exp_f16_sdwa v19, v15 dst_sel:WORD_1 dst_unused:UNUSED_PRESERVE src0_sel:WORD_1
	v_exp_f16_sdwa v20, v16 dst_sel:WORD_1 dst_unused:UNUSED_PRESERVE src0_sel:WORD_1
	v_exp_f16_sdwa v21, v17 dst_sel:WORD_1 dst_unused:UNUSED_PRESERVE src0_sel:WORD_1
	v_pk_add_f16 v14, v46, v78 neg_lo:[0,1] neg_hi:[0,1]
	v_pk_add_f16 v10, v10, v18
	v_pk_add_f16 v11, v11, v19
	v_pk_add_f16 v12, v12, v20
	v_pk_add_f16 v13, v13, v21
	v_pk_fma_f16 v6, v38, v18, v6
	v_pk_fma_f16 v7, v39, v19, v7
	v_pk_fma_f16 v8, v40, v20, v8
	v_pk_fma_f16 v9, v41, v21, v9
	v_pk_add_f16 v15, v47, v79 neg_lo:[0,1] neg_hi:[0,1]
	v_pk_add_f16 v16, v48, v80 neg_lo:[0,1] neg_hi:[0,1]
	v_pk_add_f16 v17, v49, v81 neg_lo:[0,1] neg_hi:[0,1]
	v_exp_f16_sdwa v18, v14 dst_sel:WORD_0 dst_unused:UNUSED_PAD src0_sel:WORD_0
	v_exp_f16_sdwa v19, v15 dst_sel:WORD_0 dst_unused:UNUSED_PAD src0_sel:WORD_0
	v_exp_f16_sdwa v20, v16 dst_sel:WORD_0 dst_unused:UNUSED_PAD src0_sel:WORD_0
	v_exp_f16_sdwa v21, v17 dst_sel:WORD_0 dst_unused:UNUSED_PAD src0_sel:WORD_0
	v_exp_f16_sdwa v18, v14 dst_sel:WORD_1 dst_unused:UNUSED_PRESERVE src0_sel:WORD_1
	v_exp_f16_sdwa v19, v15 dst_sel:WORD_1 dst_unused:UNUSED_PRESERVE src0_sel:WORD_1
	v_exp_f16_sdwa v20, v16 dst_sel:WORD_1 dst_unused:UNUSED_PRESERVE src0_sel:WORD_1
	v_exp_f16_sdwa v21, v17 dst_sel:WORD_1 dst_unused:UNUSED_PRESERVE src0_sel:WORD_1
	v_pk_add_f16 v14, v69, v78 neg_lo:[0,1] neg_hi:[0,1]
	v_pk_add_f16 v13, v13, v21
	v_pk_add_f16 v12, v12, v20
	v_pk_add_f16 v11, v11, v19
	v_pk_add_f16 v10, v10, v18
	v_pk_fma_f16 v9, v61, v21, v9
	v_pk_fma_f16 v8, v60, v20, v8
	v_pk_fma_f16 v7, v59, v19, v7
	v_pk_fma_f16 v6, v58, v18, v6
	v_pk_add_f16 v15, v68, v79 neg_lo:[0,1] neg_hi:[0,1]
	v_pk_add_f16 v16, v67, v80 neg_lo:[0,1] neg_hi:[0,1]
	v_pk_add_f16 v17, v66, v81 neg_lo:[0,1] neg_hi:[0,1]
	v_exp_f16_sdwa v18, v14 dst_sel:WORD_0 dst_unused:UNUSED_PAD src0_sel:WORD_0
	v_exp_f16_sdwa v19, v15 dst_sel:WORD_0 dst_unused:UNUSED_PAD src0_sel:WORD_0
	v_exp_f16_sdwa v20, v16 dst_sel:WORD_0 dst_unused:UNUSED_PAD src0_sel:WORD_0
	v_exp_f16_sdwa v21, v17 dst_sel:WORD_0 dst_unused:UNUSED_PAD src0_sel:WORD_0
	v_exp_f16_sdwa v18, v14 dst_sel:WORD_1 dst_unused:UNUSED_PRESERVE src0_sel:WORD_1
	v_exp_f16_sdwa v19, v15 dst_sel:WORD_1 dst_unused:UNUSED_PRESERVE src0_sel:WORD_1
	v_exp_f16_sdwa v20, v16 dst_sel:WORD_1 dst_unused:UNUSED_PRESERVE src0_sel:WORD_1
	v_exp_f16_sdwa v21, v17 dst_sel:WORD_1 dst_unused:UNUSED_PRESERVE src0_sel:WORD_1
	v_pk_add_f16 v10, v10, v18
	v_pk_add_f16 v11, v11, v19
	v_pk_add_f16 v12, v12, v20
	v_pk_add_f16 v13, v13, v21
	v_pk_fma_f16 v14, v70, v18, v6
	v_pk_fma_f16 v15, v71, v19, v7
	v_pk_fma_f16 v16, v72, v20, v8
	v_pk_fma_f16 v17, v73, v21, v9
	v_pk_add_f16 v6, v77, v78 neg_lo:[0,1] neg_hi:[0,1]
	v_pk_add_f16 v7, v76, v79 neg_lo:[0,1] neg_hi:[0,1]
	v_pk_add_f16 v8, v75, v80 neg_lo:[0,1] neg_hi:[0,1]
	v_pk_add_f16 v9, v74, v81 neg_lo:[0,1] neg_hi:[0,1]
	v_exp_f16_sdwa v18, v6 dst_sel:WORD_0 dst_unused:UNUSED_PAD src0_sel:WORD_0
	v_exp_f16_sdwa v19, v7 dst_sel:WORD_0 dst_unused:UNUSED_PAD src0_sel:WORD_0
	v_exp_f16_sdwa v20, v8 dst_sel:WORD_0 dst_unused:UNUSED_PAD src0_sel:WORD_0
	v_exp_f16_sdwa v21, v9 dst_sel:WORD_0 dst_unused:UNUSED_PAD src0_sel:WORD_0
	v_exp_f16_sdwa v18, v6 dst_sel:WORD_1 dst_unused:UNUSED_PRESERVE src0_sel:WORD_1
	v_exp_f16_sdwa v19, v7 dst_sel:WORD_1 dst_unused:UNUSED_PRESERVE src0_sel:WORD_1
	v_exp_f16_sdwa v20, v8 dst_sel:WORD_1 dst_unused:UNUSED_PRESERVE src0_sel:WORD_1
	v_exp_f16_sdwa v21, v9 dst_sel:WORD_1 dst_unused:UNUSED_PRESERVE src0_sel:WORD_1
	s_nop 0
	v_pk_add_f16 v9, v13, v21
	v_pk_add_f16 v8, v12, v20
	v_pk_add_f16 v7, v11, v19
	v_pk_add_f16 v6, v10, v18
	v_pk_fma_f16 v13, v93, v21, v17
	v_pk_fma_f16 v12, v92, v20, v16
	v_pk_fma_f16 v11, v91, v19, v15
	v_pk_fma_f16 v10, v90, v18, v14
	v_pk_add_f16 v18, v50, v78 neg_lo:[0,1] neg_hi:[0,1]
	v_pk_add_f16 v19, v51, v79 neg_lo:[0,1] neg_hi:[0,1]
	v_pk_add_f16 v20, v52, v80 neg_lo:[0,1] neg_hi:[0,1]
	v_pk_add_f16 v21, v53, v81 neg_lo:[0,1] neg_hi:[0,1]
	v_exp_f16_sdwa v14, v18 dst_sel:WORD_0 dst_unused:UNUSED_PAD src0_sel:WORD_0
	v_exp_f16_sdwa v17, v19 dst_sel:WORD_0 dst_unused:UNUSED_PAD src0_sel:WORD_0
	v_exp_f16_sdwa v15, v20 dst_sel:WORD_0 dst_unused:UNUSED_PAD src0_sel:WORD_0
	v_exp_f16_sdwa v16, v21 dst_sel:WORD_0 dst_unused:UNUSED_PAD src0_sel:WORD_0
	v_exp_f16_sdwa v14, v18 dst_sel:WORD_1 dst_unused:UNUSED_PRESERVE src0_sel:WORD_1
	v_exp_f16_sdwa v17, v19 dst_sel:WORD_1 dst_unused:UNUSED_PRESERVE src0_sel:WORD_1
	v_exp_f16_sdwa v15, v20 dst_sel:WORD_1 dst_unused:UNUSED_PRESERVE src0_sel:WORD_1
	v_exp_f16_sdwa v16, v21 dst_sel:WORD_1 dst_unused:UNUSED_PRESERVE src0_sel:WORD_1
	s_nop 0

.LBB5_4:
	v_add_u32_e32 v182, s30, v161
	v_add_u32_e32 v181, -1, v182
	v_or_b32_e32 v2, v181, v164
	v_add_u32_e32 v180, 0x18400, v171
	v_cmp_gt_u32_e64 s[0:1], 64, v2
	s_mov_b64 s[4:5], -1
	s_and_b64 vcc, exec, s[24:25]
	s_cbranch_vccz .LBB5_42
	s_load_dwordx2 s[4:5], s[22:23], 0x20
	s_waitcnt lgkmcnt(0)
	s_load_dwordx2 s[26:27], s[4:5], 0x0
	s_load_dword s31, s[4:5], 0x8
	v_cmp_lt_u32_e64 s[64:65], 0, v182
	v_cmp_gt_u32_e64 s[66:67], 63, v182
	v_cmp_lt_u32_e64 s[68:69], 0, v162
	v_cmp_gt_u32_e64 s[70:71], 60, v162
	buffer_load_dwordx4 v[186:189], v180, s[16:19], 0 offen
	s_and_b64 s[72:73], s[68:69], s[64:65]
	s_and_b64 s[74:75], s[68:69], s[66:67]
	s_and_b64 s[76:77], s[70:71], s[64:65]
	s_and_b64 s[78:79], s[70:71], s[66:67]
	v_add_u32_e32 v224, 0xfffe7c00, v180
	v_add_u32_e32 v225, 0xfffe8000, v180
	s_mov_b64 exec, s[72:73]
	buffer_load_dwordx4 v[110:113], v224, s[16:19], 0 offen
	s_mov_b64 exec, -1
	s_mov_b64 exec, s[68:69]
	buffer_load_dwordx4 v[126:129], v225, s[16:19], 0 offen offset:512
	s_mov_b64 exec, -1
	s_mov_b64 exec, s[74:75]
	buffer_load_dwordx4 v[134:137], v225, s[16:19], 0 offen offset:2048
	s_mov_b64 exec, -1
	v_add_u32_e32 v224, 0xfffffc00, v180
	s_mov_b64 exec, s[64:65]
	buffer_load_dwordx4 v[82:85], v224, s[16:19], 0 offen
	s_mov_b64 exec, -1
	buffer_load_dwordx4 v[106:109], v180, s[16:19], 0 offen offset:512
	s_mov_b64 exec, s[66:67]
	buffer_load_dwordx4 v[122:125], v180, s[16:19], 0 offen offset:2048
	s_mov_b64 exec, -1
	v_add_u32_e32 v224, 0x17c00, v180
	v_add_u32_e32 v225, 0x18000, v180
	s_mov_b64 exec, s[64:65]
	buffer_load_dwordx4 v[50:53], v224, s[16:19], 0 offen
	s_mov_b64 exec, -1
	buffer_load_dwordx4 v[66:69], v225, s[16:19], 0 offen offset:512
	s_mov_b64 exec, s[66:67]
	buffer_load_dwordx4 v[94:97], v225, s[16:19], 0 offen offset:2048
	s_mov_b64 exec, -1
	v_add_u32_e32 v224, 0xfffe7c00, v180
	v_add_u32_e32 v225, 0xfffe8000, v180
	s_mov_b64 exec, s[72:73]
	buffer_load_dwordx4 v[70:73], v224, s[16:19], 0 offen offset:512
	s_mov_b64 exec, -1
	s_mov_b64 exec, s[68:69]
	buffer_load_dwordx4 v[98:101], v225, s[16:19], 0 offen offset:1024
	s_mov_b64 exec, -1
	s_mov_b64 exec, s[74:75]
	buffer_load_dwordx4 v[114:117], v225, s[16:19], 0 offen offset:2560
	s_mov_b64 exec, -1
	v_add_u32_e32 v224, 0xfffffc00, v180
	s_mov_b64 exec, s[64:65]
	buffer_load_dwordx4 v[42:45], v224, s[16:19], 0 offen offset:512
	s_mov_b64 exec, -1
	buffer_load_dwordx4 v[62:65], v180, s[16:19], 0 offen offset:1024
	s_mov_b64 exec, s[66:67]
	buffer_load_dwordx4 v[86:89], v180, s[16:19], 0 offen offset:2560
	s_mov_b64 exec, -1
	v_add_u32_e32 v224, 0x17c00, v180
	v_add_u32_e32 v225, 0x18000, v180
	s_mov_b64 exec, s[64:65]
	buffer_load_dwordx4 v[22:25], v224, s[16:19], 0 offen offset:512
	s_mov_b64 exec, -1
	buffer_load_dwordx4 v[30:33], v225, s[16:19], 0 offen offset:1024
	s_mov_b64 exec, s[66:67]
	buffer_load_dwordx4 v[46:49], v225, s[16:19], 0 offen offset:2560
	s_mov_b64 exec, -1
	v_add_u32_e32 v224, 0x18000, v180
	buffer_load_dwordx4 v[154:157], v224, s[16:19], 0 offen
	v_add_u32_e32 v225, 0x30000, v180
	buffer_load_dwordx4 v[150:153], v225, s[16:19], 0 offen
	v_add_u32_e32 v224, 0x48000, v180
	buffer_load_dwordx4 v[146:149], v224, s[16:19], 0 offen
	v_add_u32_e32 v224, 0x2fc00, v180
	v_add_u32_e32 v225, 0x30000, v180
	v_add_u32_e32 v226, 0x47c00, v180
	v_add_u32_e32 v227, 0x48000, v180
	v_add_u32_e32 v228, 0x5fc00, v180
	v_add_u32_e32 v229, 0x60000, v180
	s_cmp_lg_u32 s93, 0
	s_cbranch_scc1 .Lmybg_D1
	s_waitcnt vmcnt(22)
	v_cvt_pk_f16_f32 v172, v230, v231
	v_cvt_pk_f16_f32 v173, v234, v235
	v_cvt_pk_f16_f32 v174, v232, v233
	v_cvt_pk_f16_f32 v175, v236, v237
	v_cvt_pk_f16_f32 v176, v238, v239
	v_cvt_pk_f16_f32 v177, v242, v243
	v_cvt_pk_f16_f32 v178, v240, v241
	v_cvt_pk_f16_f32 v179, v244, v245
	s_mov_b32 s93, 1

.Lmyf_D1_7:
	s_mov_b64 exec, -1
	s_waitcnt lgkmcnt(0)
	v_cvt_f16_f32_e32 v183, s27
	v_cvt_f16_f32_e32 v185, s26
	v_cvt_f16_f32_e32 v184, s31
	s_mov_b64 s[4:5], 0
	s_waitcnt vmcnt(12)
	v_pk_mul_f16 v193, v185, v189 op_sel_hi:[0,1]
	v_pk_mul_f16 v197, v183, v189 op_sel_hi:[0,1]
	v_pk_mul_f16 v201, v184, v189 op_sel_hi:[0,1]
	v_pk_mul_f16 v190, v185, v186 op_sel_hi:[0,1]
	v_pk_mul_f16 v191, v185, v187 op_sel_hi:[0,1]
	v_pk_mul_f16 v192, v185, v188 op_sel_hi:[0,1]
	v_pk_mul_f16 v194, v183, v186 op_sel_hi:[0,1]
	v_pk_mul_f16 v195, v183, v187 op_sel_hi:[0,1]
	v_pk_mul_f16 v196, v183, v188 op_sel_hi:[0,1]
	v_pk_mul_f16 v198, v184, v186 op_sel_hi:[0,1]
	v_pk_mul_f16 v199, v184, v187 op_sel_hi:[0,1]
	v_pk_mul_f16 v200, v184, v188 op_sel_hi:[0,1]
	v_pk_fma_f16 v113, v113, v189, v193
	v_pk_fma_f16 v129, v129, v189, v197
	v_pk_fma_f16 v137, v137, v189, v201
	v_pk_fma_f16 v202, v85, v189, v193
	v_pk_fma_f16 v206, v109, v189, v197
	v_pk_fma_f16 v210, v125, v189, v201
	v_pk_fma_f16 v193, v53, v189, v193
	v_pk_fma_f16 v197, v69, v189, v197
	v_pk_fma_f16 v189, v97, v189, v201
	v_pk_maximum3_f16 v201, v113, v129, v137
	v_pk_fma_f16 v112, v112, v188, v192
	v_pk_fma_f16 v111, v111, v187, v191
	v_pk_fma_f16 v110, v110, v186, v190
	v_pk_fma_f16 v128, v128, v188, v196
	v_pk_fma_f16 v127, v127, v187, v195
	v_pk_fma_f16 v126, v126, v186, v194
	v_pk_fma_f16 v136, v136, v188, v200
	v_pk_fma_f16 v135, v135, v187, v199
	v_pk_fma_f16 v134, v134, v186, v198
	v_pk_fma_f16 v203, v84, v188, v192
	v_pk_fma_f16 v204, v83, v187, v191
	v_pk_fma_f16 v205, v82, v186, v190
	v_pk_fma_f16 v207, v108, v188, v196
	v_pk_fma_f16 v208, v107, v187, v195
	v_pk_fma_f16 v209, v106, v186, v194
	v_pk_fma_f16 v211, v124, v188, v200
	v_pk_fma_f16 v212, v123, v187, v199
	v_pk_fma_f16 v213, v122, v186, v198
	v_pk_fma_f16 v192, v52, v188, v192
	v_pk_fma_f16 v191, v51, v187, v191
	v_pk_fma_f16 v190, v50, v186, v190
	v_pk_fma_f16 v196, v68, v188, v196
	v_pk_fma_f16 v195, v67, v187, v195
	v_pk_fma_f16 v194, v66, v186, v194
	v_pk_fma_f16 v188, v96, v188, v200
	v_pk_fma_f16 v187, v95, v187, v199
	v_pk_fma_f16 v186, v94, v186, v198
	v_pk_maximum3_f16 v198, v110, v126, v134
	v_pk_maximum3_f16 v199, v111, v127, v135
	v_pk_maximum3_f16 v200, v112, v128, v136
	v_pk_maximum3_f16 v217, v202, v206, v210
	v_pk_maximum3_f16 v221, v193, v197, v189
	v_pk_maximum3_f16 v214, v205, v209, v213
	v_pk_maximum3_f16 v215, v204, v208, v212
	v_pk_maximum3_f16 v216, v203, v207, v211
	v_pk_maximum3_f16 v218, v190, v194, v186
	v_pk_maximum3_f16 v219, v191, v195, v187
	v_pk_maximum3_f16 v201, v201, v217, v221
	v_pk_maximum3_f16 v220, v192, v196, v188
	v_pk_maximum3_f16 v198, v198, v214, v218
	v_pk_maximum3_f16 v199, v199, v215, v219
	v_pk_maximum3_f16 v200, v200, v216, v220
	v_pk_add_f16 v113, v113, v201 neg_lo:[0,1] neg_hi:[0,1]
	v_pk_add_f16 v110, v110, v198 neg_lo:[0,1] neg_hi:[0,1]
	v_pk_add_f16 v111, v111, v199 neg_lo:[0,1] neg_hi:[0,1]
	v_pk_add_f16 v112, v112, v200 neg_lo:[0,1] neg_hi:[0,1]
	v_pk_add_f16 v126, v126, v198 neg_lo:[0,1] neg_hi:[0,1]
	v_exp_f16_sdwa v214, v110 dst_sel:WORD_0 dst_unused:UNUSED_PAD src0_sel:WORD_0
	v_exp_f16_sdwa v215, v111 dst_sel:WORD_0 dst_unused:UNUSED_PAD src0_sel:WORD_0
	v_exp_f16_sdwa v216, v112 dst_sel:WORD_0 dst_unused:UNUSED_PAD src0_sel:WORD_0
	v_exp_f16_sdwa v217, v113 dst_sel:WORD_0 dst_unused:UNUSED_PAD src0_sel:WORD_0
	v_exp_f16_sdwa v214, v110 dst_sel:WORD_1 dst_unused:UNUSED_PRESERVE src0_sel:WORD_1
	v_exp_f16_sdwa v215, v111 dst_sel:WORD_1 dst_unused:UNUSED_PRESERVE src0_sel:WORD_1
	v_exp_f16_sdwa v216, v112 dst_sel:WORD_1 dst_unused:UNUSED_PRESERVE src0_sel:WORD_1
	v_exp_f16_sdwa v217, v113 dst_sel:WORD_1 dst_unused:UNUSED_PRESERVE src0_sel:WORD_1
	v_pk_add_f16 v127, v127, v199 neg_lo:[0,1] neg_hi:[0,1]
	v_pk_add_f16 v113, v214, 0
	s_waitcnt vmcnt(3)
	v_pk_fma_f16 v73, v73, v217, 0
	v_pk_add_f16 v110, v217, 0
	v_pk_add_f16 v111, v216, 0
	v_pk_add_f16 v112, v215, 0
	v_pk_fma_f16 v72, v72, v216, 0
	v_pk_fma_f16 v71, v71, v215, 0
	s_mov_b64 exec, s[64:65]
	buffer_load_dwordx4 v[18:21], v224, s[16:19], 0 offen
	buffer_load_dwordx4 v[6:9], v224, s[16:19], 0 offen offset:512
	s_mov_b64 exec, -1
	v_pk_fma_f16 v70, v70, v214, 0
	v_pk_add_f16 v128, v128, v200 neg_lo:[0,1] neg_hi:[0,1]
	v_pk_add_f16 v129, v129, v201 neg_lo:[0,1] neg_hi:[0,1]
	v_exp_f16_sdwa v214, v126 dst_sel:WORD_0 dst_unused:UNUSED_PAD src0_sel:WORD_0
	v_exp_f16_sdwa v215, v127 dst_sel:WORD_0 dst_unused:UNUSED_PAD src0_sel:WORD_0
	v_exp_f16_sdwa v216, v128 dst_sel:WORD_0 dst_unused:UNUSED_PAD src0_sel:WORD_0
	v_exp_f16_sdwa v217, v129 dst_sel:WORD_0 dst_unused:UNUSED_PAD src0_sel:WORD_0
	v_exp_f16_sdwa v214, v126 dst_sel:WORD_1 dst_unused:UNUSED_PRESERVE src0_sel:WORD_1
	v_exp_f16_sdwa v215, v127 dst_sel:WORD_1 dst_unused:UNUSED_PRESERVE src0_sel:WORD_1
	v_exp_f16_sdwa v216, v128 dst_sel:WORD_1 dst_unused:UNUSED_PRESERVE src0_sel:WORD_1
	v_exp_f16_sdwa v217, v129 dst_sel:WORD_1 dst_unused:UNUSED_PRESERVE src0_sel:WORD_1
	v_pk_add_f16 v113, v113, v214
	v_pk_fma_f16 v73, v101, v217, v73
	v_pk_add_f16 v101, v137, v201 neg_lo:[0,1] neg_hi:[0,1]
	v_pk_add_f16 v112, v112, v215
	v_pk_add_f16 v111, v111, v216
	v_pk_add_f16 v110, v110, v217
	buffer_load_dwordx4 v[34:37], v225, s[16:19], 0 offen offset:512
	buffer_load_dwordx4 v[10:13], v225, s[16:19], 0 offen offset:1024
	v_pk_fma_f16 v70, v98, v214, v70
	v_pk_fma_f16 v71, v99, v215, v71
	v_pk_fma_f16 v72, v100, v216, v72
	v_pk_add_f16 v98, v134, v198 neg_lo:[0,1] neg_hi:[0,1]
	v_pk_add_f16 v99, v135, v199 neg_lo:[0,1] neg_hi:[0,1]
	v_pk_add_f16 v100, v136, v200 neg_lo:[0,1] neg_hi:[0,1]
	v_exp_f16_sdwa v126, v98 dst_sel:WORD_0 dst_unused:UNUSED_PAD src0_sel:WORD_0
	v_exp_f16_sdwa v127, v99 dst_sel:WORD_0 dst_unused:UNUSED_PAD src0_sel:WORD_0
	v_exp_f16_sdwa v128, v100 dst_sel:WORD_0 dst_unused:UNUSED_PAD src0_sel:WORD_0
	v_exp_f16_sdwa v129, v101 dst_sel:WORD_0 dst_unused:UNUSED_PAD src0_sel:WORD_0
	v_exp_f16_sdwa v126, v98 dst_sel:WORD_1 dst_unused:UNUSED_PRESERVE src0_sel:WORD_1
	v_exp_f16_sdwa v127, v99 dst_sel:WORD_1 dst_unused:UNUSED_PRESERVE src0_sel:WORD_1
	v_exp_f16_sdwa v128, v100 dst_sel:WORD_1 dst_unused:UNUSED_PRESERVE src0_sel:WORD_1
	v_exp_f16_sdwa v129, v101 dst_sel:WORD_1 dst_unused:UNUSED_PRESERVE src0_sel:WORD_1
	v_pk_add_f16 v101, v113, v126
	v_pk_add_f16 v98, v110, v129
	v_pk_add_f16 v99, v111, v128
	s_mov_b64 exec, s[66:67]
	buffer_load_dwordx4 v[54:57], v225, s[16:19], 0 offen offset:2048
	buffer_load_dwordx4 v[14:17], v225, s[16:19], 0 offen offset:2560
	s_mov_b64 exec, -1
	v_pk_add_f16 v100, v112, v127
	v_pk_fma_f16 v73, v117, v129, v73
	v_pk_fma_f16 v72, v116, v128, v72
	v_pk_fma_f16 v71, v115, v127, v71
	v_pk_fma_f16 v70, v114, v126, v70
	v_pk_add_f16 v110, v205, v198 neg_lo:[0,1] neg_hi:[0,1]
	v_pk_add_f16 v111, v204, v199 neg_lo:[0,1] neg_hi:[0,1]
	v_pk_add_f16 v112, v203, v200 neg_lo:[0,1] neg_hi:[0,1]
	s_mov_b64 exec, s[64:65]
	buffer_load_dwordx4 v[74:77], v226, s[16:19], 0 offen
	buffer_load_dwordx4 v[26:29], v226, s[16:19], 0 offen offset:512
	s_mov_b64 exec, -1
	v_pk_add_f16 v113, v202, v201 neg_lo:[0,1] neg_hi:[0,1]
	v_exp_f16_sdwa v114, v110 dst_sel:WORD_0 dst_unused:UNUSED_PAD src0_sel:WORD_0
	v_exp_f16_sdwa v115, v111 dst_sel:WORD_0 dst_unused:UNUSED_PAD src0_sel:WORD_0
	v_exp_f16_sdwa v116, v112 dst_sel:WORD_0 dst_unused:UNUSED_PAD src0_sel:WORD_0
	v_exp_f16_sdwa v117, v113 dst_sel:WORD_0 dst_unused:UNUSED_PAD src0_sel:WORD_0
	v_exp_f16_sdwa v114, v110 dst_sel:WORD_1 dst_unused:UNUSED_PRESERVE src0_sel:WORD_1
	v_exp_f16_sdwa v115, v111 dst_sel:WORD_1 dst_unused:UNUSED_PRESERVE src0_sel:WORD_1
	v_exp_f16_sdwa v116, v112 dst_sel:WORD_1 dst_unused:UNUSED_PRESERVE src0_sel:WORD_1
	v_exp_f16_sdwa v117, v113 dst_sel:WORD_1 dst_unused:UNUSED_PRESERVE src0_sel:WORD_1
	v_pk_add_f16 v110, v209, v198 neg_lo:[0,1] neg_hi:[0,1]
	v_pk_add_f16 v101, v101, v114
	v_pk_add_f16 v100, v100, v115
	v_pk_add_f16 v99, v99, v116
	v_pk_add_f16 v98, v98, v117
	v_pk_fma_f16 v70, v42, v114, v70
	v_pk_fma_f16 v71, v43, v115, v71
	v_pk_fma_f16 v72, v44, v116, v72
	v_pk_fma_f16 v73, v45, v117, v73
	buffer_load_dwordx4 v[102:105], v227, s[16:19], 0 offen offset:512
	buffer_load_dwordx4 v[38:41], v227, s[16:19], 0 offen offset:1024
	v_pk_add_f16 v111, v208, v199 neg_lo:[0,1] neg_hi:[0,1]
	v_pk_add_f16 v112, v207, v200 neg_lo:[0,1] neg_hi:[0,1]
	v_pk_add_f16 v113, v206, v201 neg_lo:[0,1] neg_hi:[0,1]
	v_exp_f16_sdwa v114, v110 dst_sel:WORD_0 dst_unused:UNUSED_PAD src0_sel:WORD_0
	v_exp_f16_sdwa v115, v111 dst_sel:WORD_0 dst_unused:UNUSED_PAD src0_sel:WORD_0
	v_exp_f16_sdwa v116, v112 dst_sel:WORD_0 dst_unused:UNUSED_PAD src0_sel:WORD_0
	v_exp_f16_sdwa v117, v113 dst_sel:WORD_0 dst_unused:UNUSED_PAD src0_sel:WORD_0
	v_exp_f16_sdwa v114, v110 dst_sel:WORD_1 dst_unused:UNUSED_PRESERVE src0_sel:WORD_1
	v_exp_f16_sdwa v115, v111 dst_sel:WORD_1 dst_unused:UNUSED_PRESERVE src0_sel:WORD_1
	v_exp_f16_sdwa v116, v112 dst_sel:WORD_1 dst_unused:UNUSED_PRESERVE src0_sel:WORD_1
	v_exp_f16_sdwa v117, v113 dst_sel:WORD_1 dst_unused:UNUSED_PRESERVE src0_sel:WORD_1
	v_pk_add_f16 v110, v213, v198 neg_lo:[0,1] neg_hi:[0,1]
	v_pk_add_f16 v101, v101, v114
	v_pk_add_f16 v98, v98, v117
	v_pk_add_f16 v99, v99, v116
	v_pk_add_f16 v100, v100, v115
	v_pk_fma_f16 v73, v65, v117, v73
	s_mov_b64 exec, s[66:67]
	buffer_load_dwordx4 v[118:121], v227, s[16:19], 0 offen offset:2048
	buffer_load_dwordx4 v[58:61], v227, s[16:19], 0 offen offset:2560
	s_mov_b64 exec, -1
	v_pk_fma_f16 v72, v64, v116, v72
	v_pk_fma_f16 v71, v63, v115, v71
	v_pk_fma_f16 v70, v62, v114, v70
	v_pk_add_f16 v111, v212, v199 neg_lo:[0,1] neg_hi:[0,1]
	v_pk_add_f16 v112, v211, v200 neg_lo:[0,1] neg_hi:[0,1]
	v_pk_add_f16 v113, v210, v201 neg_lo:[0,1] neg_hi:[0,1]
	v_exp_f16_sdwa v114, v110 dst_sel:WORD_0 dst_unused:UNUSED_PAD src0_sel:WORD_0
	v_exp_f16_sdwa v115, v111 dst_sel:WORD_0 dst_unused:UNUSED_PAD src0_sel:WORD_0
	v_exp_f16_sdwa v116, v112 dst_sel:WORD_0 dst_unused:UNUSED_PAD src0_sel:WORD_0
	v_exp_f16_sdwa v117, v113 dst_sel:WORD_0 dst_unused:UNUSED_PAD src0_sel:WORD_0
	v_exp_f16_sdwa v114, v110 dst_sel:WORD_1 dst_unused:UNUSED_PRESERVE src0_sel:WORD_1
	v_exp_f16_sdwa v115, v111 dst_sel:WORD_1 dst_unused:UNUSED_PRESERVE src0_sel:WORD_1
	v_exp_f16_sdwa v116, v112 dst_sel:WORD_1 dst_unused:UNUSED_PRESERVE src0_sel:WORD_1
	v_exp_f16_sdwa v117, v113 dst_sel:WORD_1 dst_unused:UNUSED_PRESERVE src0_sel:WORD_1
	v_pk_add_f16 v110, v190, v198 neg_lo:[0,1] neg_hi:[0,1]
	v_pk_add_f16 v101, v101, v114
	v_pk_add_f16 v100, v100, v115
	s_mov_b64 exec, s[76:77]
	buffer_load_dwordx4 v[130:133], v228, s[16:19], 0 offen
	buffer_load_dwordx4 v[78:81], v228, s[16:19], 0 offen offset:512
	s_mov_b64 exec, -1
	v_pk_add_f16 v99, v99, v116
	v_pk_add_f16 v98, v98, v117
	v_pk_fma_f16 v70, v86, v114, v70
	v_pk_fma_f16 v71, v87, v115, v71
	v_pk_fma_f16 v72, v88, v116, v72
	v_pk_fma_f16 v73, v89, v117, v73
	v_pk_add_f16 v111, v191, v199 neg_lo:[0,1] neg_hi:[0,1]
	v_pk_add_f16 v112, v192, v200 neg_lo:[0,1] neg_hi:[0,1]
	s_mov_b64 exec, s[70:71]
	buffer_load_dwordx4 v[138:141], v229, s[16:19], 0 offen offset:512
	buffer_load_dwordx4 v[90:93], v229, s[16:19], 0 offen offset:1024
	s_mov_b64 exec, -1
	v_pk_add_f16 v113, v193, v201 neg_lo:[0,1] neg_hi:[0,1]
	v_exp_f16_sdwa v114, v110 dst_sel:WORD_0 dst_unused:UNUSED_PAD src0_sel:WORD_0
	v_exp_f16_sdwa v115, v111 dst_sel:WORD_0 dst_unused:UNUSED_PAD src0_sel:WORD_0
	v_exp_f16_sdwa v116, v112 dst_sel:WORD_0 dst_unused:UNUSED_PAD src0_sel:WORD_0
	v_exp_f16_sdwa v117, v113 dst_sel:WORD_0 dst_unused:UNUSED_PAD src0_sel:WORD_0
	v_exp_f16_sdwa v114, v110 dst_sel:WORD_1 dst_unused:UNUSED_PRESERVE src0_sel:WORD_1
	v_exp_f16_sdwa v115, v111 dst_sel:WORD_1 dst_unused:UNUSED_PRESERVE src0_sel:WORD_1
	v_exp_f16_sdwa v116, v112 dst_sel:WORD_1 dst_unused:UNUSED_PRESERVE src0_sel:WORD_1
	v_exp_f16_sdwa v117, v113 dst_sel:WORD_1 dst_unused:UNUSED_PRESERVE src0_sel:WORD_1
	v_pk_add_f16 v110, v194, v198 neg_lo:[0,1] neg_hi:[0,1]
	v_pk_add_f16 v101, v101, v114
	v_pk_add_f16 v98, v98, v117
	v_pk_add_f16 v99, v99, v116
	v_pk_add_f16 v100, v100, v115
	v_pk_fma_f16 v73, v25, v117, v73
	v_pk_fma_f16 v72, v24, v116, v72
	v_pk_fma_f16 v71, v23, v115, v71
	s_mov_b64 exec, s[78:79]
	buffer_load_dwordx4 v[142:145], v229, s[16:19], 0 offen offset:2048
	buffer_load_dwordx4 v[2:5], v229, s[16:19], 0 offen offset:2560
	s_mov_b64 exec, -1
	v_pk_fma_f16 v70, v22, v114, v70
	v_pk_add_f16 v111, v195, v199 neg_lo:[0,1] neg_hi:[0,1]
	v_pk_add_f16 v112, v196, v200 neg_lo:[0,1] neg_hi:[0,1]
	v_pk_add_f16 v113, v197, v201 neg_lo:[0,1] neg_hi:[0,1]
	v_exp_f16_sdwa v114, v110 dst_sel:WORD_0 dst_unused:UNUSED_PAD src0_sel:WORD_0
	v_exp_f16_sdwa v115, v111 dst_sel:WORD_0 dst_unused:UNUSED_PAD src0_sel:WORD_0
	v_exp_f16_sdwa v116, v112 dst_sel:WORD_0 dst_unused:UNUSED_PAD src0_sel:WORD_0
	v_exp_f16_sdwa v117, v113 dst_sel:WORD_0 dst_unused:UNUSED_PAD src0_sel:WORD_0
	v_exp_f16_sdwa v114, v110 dst_sel:WORD_1 dst_unused:UNUSED_PRESERVE src0_sel:WORD_1
	v_exp_f16_sdwa v115, v111 dst_sel:WORD_1 dst_unused:UNUSED_PRESERVE src0_sel:WORD_1
	v_exp_f16_sdwa v116, v112 dst_sel:WORD_1 dst_unused:UNUSED_PRESERVE src0_sel:WORD_1
	v_exp_f16_sdwa v117, v113 dst_sel:WORD_1 dst_unused:UNUSED_PRESERVE src0_sel:WORD_1
	v_pk_add_f16 v110, v186, v198 neg_lo:[0,1] neg_hi:[0,1]
	v_pk_add_f16 v101, v101, v114
	v_pk_add_f16 v100, v100, v115
	v_pk_add_f16 v99, v99, v116
	v_pk_add_f16 v98, v98, v117
	v_pk_fma_f16 v70, v30, v114, v70
	v_pk_fma_f16 v71, v31, v115, v71
	v_pk_fma_f16 v72, v32, v116, v72
	v_pk_fma_f16 v73, v33, v117, v73
	v_pk_add_f16 v111, v187, v199 neg_lo:[0,1] neg_hi:[0,1]
	v_pk_add_f16 v112, v188, v200 neg_lo:[0,1] neg_hi:[0,1]
	v_pk_add_f16 v113, v189, v201 neg_lo:[0,1] neg_hi:[0,1]
	v_exp_f16_sdwa v114, v110 dst_sel:WORD_0 dst_unused:UNUSED_PAD src0_sel:WORD_0
	v_exp_f16_sdwa v115, v111 dst_sel:WORD_0 dst_unused:UNUSED_PAD src0_sel:WORD_0
	v_exp_f16_sdwa v116, v112 dst_sel:WORD_0 dst_unused:UNUSED_PAD src0_sel:WORD_0
	v_exp_f16_sdwa v117, v113 dst_sel:WORD_0 dst_unused:UNUSED_PAD src0_sel:WORD_0
	v_exp_f16_sdwa v114, v110 dst_sel:WORD_1 dst_unused:UNUSED_PRESERVE src0_sel:WORD_1
	v_exp_f16_sdwa v115, v111 dst_sel:WORD_1 dst_unused:UNUSED_PRESERVE src0_sel:WORD_1
	v_exp_f16_sdwa v116, v112 dst_sel:WORD_1 dst_unused:UNUSED_PRESERVE src0_sel:WORD_1
	v_exp_f16_sdwa v117, v113 dst_sel:WORD_1 dst_unused:UNUSED_PRESERVE src0_sel:WORD_1
	v_pk_add_f16 v101, v101, v114
	v_pk_add_f16 v100, v100, v115
	v_rcp_f16_e32 v110, v101
	v_rcp_f16_sdwa v101, v101 dst_sel:DWORD dst_unused:UNUSED_PAD src0_sel:WORD_1
	v_pk_add_f16 v99, v99, v116
	v_rcp_f16_e32 v111, v100
	v_rcp_f16_sdwa v100, v100 dst_sel:DWORD dst_unused:UNUSED_PAD src0_sel:WORD_1
	v_pk_add_f16 v98, v98, v117
	v_rcp_f16_e32 v112, v99
	v_rcp_f16_sdwa v99, v99 dst_sel:DWORD dst_unused:UNUSED_PAD src0_sel:WORD_1
	v_rcp_f16_e32 v113, v98
	v_rcp_f16_sdwa v98, v98 dst_sel:DWORD dst_unused:UNUSED_PAD src0_sel:WORD_1
	v_pk_fma_f16 v70, v46, v114, v70
	v_pack_b32_f16 v101, v110, v101
	v_pk_fma_f16 v71, v47, v115, v71
	v_pk_mul_f16 v110, v70, v101
	v_pack_b32_f16 v70, v111, v100
	v_pk_fma_f16 v72, v48, v116, v72
	v_pk_mul_f16 v111, v71, v70
	v_pack_b32_f16 v70, v112, v99
	v_pk_fma_f16 v73, v49, v117, v73
	v_pk_mul_f16 v112, v72, v70
	v_pack_b32_f16 v70, v113, v98
	v_pk_mul_f16 v113, v73, v70
	s_waitcnt vmcnt(12)
	v_pk_mul_f16 v70, v185, v154 op_sel_hi:[0,1]
	v_pk_mul_f16 v98, v183, v154 op_sel_hi:[0,1]
	v_pk_mul_f16 v114, v184, v154 op_sel_hi:[0,1]
	v_pk_mul_f16 v71, v185, v155 op_sel_hi:[0,1]
	v_pk_mul_f16 v72, v185, v156 op_sel_hi:[0,1]
	v_pk_mul_f16 v73, v185, v157 op_sel_hi:[0,1]
	v_pk_mul_f16 v99, v183, v155 op_sel_hi:[0,1]
	v_pk_mul_f16 v100, v183, v156 op_sel_hi:[0,1]
	v_pk_mul_f16 v101, v183, v157 op_sel_hi:[0,1]
	v_pk_mul_f16 v115, v184, v155 op_sel_hi:[0,1]
	v_pk_mul_f16 v116, v184, v156 op_sel_hi:[0,1]
	v_pk_mul_f16 v117, v184, v157 op_sel_hi:[0,1]
	v_pk_fma_f16 v82, v82, v154, v70
	v_pk_fma_f16 v106, v106, v154, v98
	v_pk_fma_f16 v122, v122, v154, v114
	v_pk_fma_f16 v129, v50, v154, v70
	v_pk_fma_f16 v137, v66, v154, v98
	v_pk_fma_f16 v189, v94, v154, v114
	v_pk_fma_f16 v70, v18, v154, v70
	v_pk_fma_f16 v98, v34, v154, v98
	v_pk_fma_f16 v114, v54, v154, v114
	v_pk_maximum3_f16 v154, v82, v106, v122
	v_pk_fma_f16 v85, v85, v157, v73
	v_pk_fma_f16 v84, v84, v156, v72
	v_pk_fma_f16 v83, v83, v155, v71
	v_pk_fma_f16 v109, v109, v157, v101
	v_pk_fma_f16 v108, v108, v156, v100
	v_pk_fma_f16 v107, v107, v155, v99
	v_pk_fma_f16 v125, v125, v157, v117
	v_pk_fma_f16 v124, v124, v156, v116
	v_pk_fma_f16 v123, v123, v155, v115
	v_pk_fma_f16 v126, v53, v157, v73
	v_pk_fma_f16 v127, v52, v156, v72
	v_pk_fma_f16 v128, v51, v155, v71
	v_pk_fma_f16 v134, v69, v157, v101
	v_pk_fma_f16 v135, v68, v156, v100
	v_pk_fma_f16 v136, v67, v155, v99
	v_pk_fma_f16 v186, v97, v157, v117
	v_pk_fma_f16 v187, v96, v156, v116
	v_pk_fma_f16 v188, v95, v155, v115
	v_pk_fma_f16 v73, v21, v157, v73
	v_pk_fma_f16 v72, v20, v156, v72
	v_pk_fma_f16 v71, v19, v155, v71
	v_pk_fma_f16 v101, v37, v157, v101
	v_pk_fma_f16 v100, v36, v156, v100
	v_pk_fma_f16 v99, v35, v155, v99
	v_pk_fma_f16 v117, v57, v157, v117
	v_pk_fma_f16 v116, v56, v156, v116
	v_pk_fma_f16 v115, v55, v155, v115
	v_pk_maximum3_f16 v155, v83, v107, v123
	v_pk_maximum3_f16 v156, v84, v108, v124
	v_pk_maximum3_f16 v157, v85, v109, v125
	v_pk_maximum3_f16 v190, v129, v137, v189
	v_pk_maximum3_f16 v194, v70, v98, v114
	v_pk_maximum3_f16 v191, v128, v136, v188
	v_pk_maximum3_f16 v192, v127, v135, v187
	v_pk_maximum3_f16 v193, v126, v134, v186
	v_pk_maximum3_f16 v195, v71, v99, v115
	v_pk_maximum3_f16 v196, v72, v100, v116
	v_pk_maximum3_f16 v154, v154, v190, v194
	v_pk_maximum3_f16 v197, v73, v101, v117
	v_pk_maximum3_f16 v155, v155, v191, v195
	v_pk_maximum3_f16 v156, v156, v192, v196
	v_pk_maximum3_f16 v157, v157, v193, v197
	v_pk_add_f16 v82, v82, v154 neg_lo:[0,1] neg_hi:[0,1]
	v_pk_add_f16 v83, v83, v155 neg_lo:[0,1] neg_hi:[0,1]
	v_pk_add_f16 v84, v84, v156 neg_lo:[0,1] neg_hi:[0,1]
	v_pk_add_f16 v85, v85, v157 neg_lo:[0,1] neg_hi:[0,1]
	v_pk_add_f16 v106, v106, v154 neg_lo:[0,1] neg_hi:[0,1]
	v_exp_f16_sdwa v190, v82 dst_sel:WORD_0 dst_unused:UNUSED_PAD src0_sel:WORD_0
	v_exp_f16_sdwa v191, v83 dst_sel:WORD_0 dst_unused:UNUSED_PAD src0_sel:WORD_0
	v_exp_f16_sdwa v192, v84 dst_sel:WORD_0 dst_unused:UNUSED_PAD src0_sel:WORD_0
	v_exp_f16_sdwa v193, v85 dst_sel:WORD_0 dst_unused:UNUSED_PAD src0_sel:WORD_0
	v_exp_f16_sdwa v190, v82 dst_sel:WORD_1 dst_unused:UNUSED_PRESERVE src0_sel:WORD_1
	v_exp_f16_sdwa v191, v83 dst_sel:WORD_1 dst_unused:UNUSED_PRESERVE src0_sel:WORD_1
	v_exp_f16_sdwa v192, v84 dst_sel:WORD_1 dst_unused:UNUSED_PRESERVE src0_sel:WORD_1
	v_exp_f16_sdwa v193, v85 dst_sel:WORD_1 dst_unused:UNUSED_PRESERVE src0_sel:WORD_1
	v_pk_add_f16 v107, v107, v155 neg_lo:[0,1] neg_hi:[0,1]
	v_pk_add_f16 v82, v193, 0
	v_pk_fma_f16 v42, v42, v190, 0
	v_pk_add_f16 v83, v192, 0
	v_pk_add_f16 v84, v191, 0
	v_pk_add_f16 v85, v190, 0
	v_pk_fma_f16 v45, v45, v193, 0
	v_pk_fma_f16 v44, v44, v192, 0
	v_pk_fma_f16 v43, v43, v191, 0
	v_pk_add_f16 v108, v108, v156 neg_lo:[0,1] neg_hi:[0,1]
	v_pk_add_f16 v109, v109, v157 neg_lo:[0,1] neg_hi:[0,1]
	v_pk_add_f16 v70, v70, v154 neg_lo:[0,1] neg_hi:[0,1]
	v_exp_f16_sdwa v190, v106 dst_sel:WORD_0 dst_unused:UNUSED_PAD src0_sel:WORD_0
	v_exp_f16_sdwa v191, v107 dst_sel:WORD_0 dst_unused:UNUSED_PAD src0_sel:WORD_0
	v_exp_f16_sdwa v192, v108 dst_sel:WORD_0 dst_unused:UNUSED_PAD src0_sel:WORD_0
	v_exp_f16_sdwa v193, v109 dst_sel:WORD_0 dst_unused:UNUSED_PAD src0_sel:WORD_0
	v_exp_f16_sdwa v190, v106 dst_sel:WORD_1 dst_unused:UNUSED_PRESERVE src0_sel:WORD_1
	v_exp_f16_sdwa v191, v107 dst_sel:WORD_1 dst_unused:UNUSED_PRESERVE src0_sel:WORD_1
	v_exp_f16_sdwa v192, v108 dst_sel:WORD_1 dst_unused:UNUSED_PRESERVE src0_sel:WORD_1
	v_exp_f16_sdwa v193, v109 dst_sel:WORD_1 dst_unused:UNUSED_PRESERVE src0_sel:WORD_1
	v_pk_add_f16 v71, v71, v155 neg_lo:[0,1] neg_hi:[0,1]
	v_pk_add_f16 v82, v82, v193
	v_pk_fma_f16 v42, v62, v190, v42
	v_pk_add_f16 v62, v122, v154 neg_lo:[0,1] neg_hi:[0,1]
	v_pk_add_f16 v85, v85, v190
	v_pk_add_f16 v84, v84, v191
	v_pk_add_f16 v83, v83, v192
	v_pk_fma_f16 v43, v63, v191, v43
	v_pk_fma_f16 v44, v64, v192, v44
	v_pk_fma_f16 v45, v65, v193, v45
	v_pk_add_f16 v63, v123, v155 neg_lo:[0,1] neg_hi:[0,1]
	v_pk_add_f16 v64, v124, v156 neg_lo:[0,1] neg_hi:[0,1]
	v_pk_add_f16 v65, v125, v157 neg_lo:[0,1] neg_hi:[0,1]
	v_pk_add_f16 v72, v72, v156 neg_lo:[0,1] neg_hi:[0,1]
	v_exp_f16_sdwa v106, v62 dst_sel:WORD_0 dst_unused:UNUSED_PAD src0_sel:WORD_0
	v_exp_f16_sdwa v107, v63 dst_sel:WORD_0 dst_unused:UNUSED_PAD src0_sel:WORD_0
	v_exp_f16_sdwa v108, v64 dst_sel:WORD_0 dst_unused:UNUSED_PAD src0_sel:WORD_0
	v_exp_f16_sdwa v109, v65 dst_sel:WORD_0 dst_unused:UNUSED_PAD src0_sel:WORD_0
	v_exp_f16_sdwa v106, v62 dst_sel:WORD_1 dst_unused:UNUSED_PRESERVE src0_sel:WORD_1
	v_exp_f16_sdwa v107, v63 dst_sel:WORD_1 dst_unused:UNUSED_PRESERVE src0_sel:WORD_1
	v_exp_f16_sdwa v108, v64 dst_sel:WORD_1 dst_unused:UNUSED_PRESERVE src0_sel:WORD_1
	v_exp_f16_sdwa v109, v65 dst_sel:WORD_1 dst_unused:UNUSED_PRESERVE src0_sel:WORD_1
	v_pk_add_f16 v73, v73, v157 neg_lo:[0,1] neg_hi:[0,1]
	v_pk_add_f16 v62, v82, v109
	v_pk_add_f16 v63, v83, v108
	v_pk_add_f16 v64, v84, v107
	v_pk_add_f16 v65, v85, v106
	v_pk_fma_f16 v45, v89, v109, v45
	v_pk_fma_f16 v44, v88, v108, v44
	v_pk_fma_f16 v43, v87, v107, v43
	v_pk_fma_f16 v42, v86, v106, v42
	v_pk_add_f16 v82, v129, v154 neg_lo:[0,1] neg_hi:[0,1]
	v_pk_add_f16 v83, v128, v155 neg_lo:[0,1] neg_hi:[0,1]
	v_pk_add_f16 v84, v127, v156 neg_lo:[0,1] neg_hi:[0,1]
	v_pk_add_f16 v85, v126, v157 neg_lo:[0,1] neg_hi:[0,1]
	v_exp_f16_sdwa v86, v82 dst_sel:WORD_0 dst_unused:UNUSED_PAD src0_sel:WORD_0
	v_exp_f16_sdwa v87, v83 dst_sel:WORD_0 dst_unused:UNUSED_PAD src0_sel:WORD_0
	v_exp_f16_sdwa v88, v84 dst_sel:WORD_0 dst_unused:UNUSED_PAD src0_sel:WORD_0
	v_exp_f16_sdwa v89, v85 dst_sel:WORD_0 dst_unused:UNUSED_PAD src0_sel:WORD_0
	v_exp_f16_sdwa v86, v82 dst_sel:WORD_1 dst_unused:UNUSED_PRESERVE src0_sel:WORD_1
	v_exp_f16_sdwa v87, v83 dst_sel:WORD_1 dst_unused:UNUSED_PRESERVE src0_sel:WORD_1
	v_exp_f16_sdwa v88, v84 dst_sel:WORD_1 dst_unused:UNUSED_PRESERVE src0_sel:WORD_1
	v_exp_f16_sdwa v89, v85 dst_sel:WORD_1 dst_unused:UNUSED_PRESERVE src0_sel:WORD_1
	v_pk_add_f16 v82, v137, v154 neg_lo:[0,1] neg_hi:[0,1]
	v_pk_add_f16 v62, v62, v89
	v_pk_add_f16 v65, v65, v86
	v_pk_add_f16 v64, v64, v87
	v_pk_add_f16 v63, v63, v88
	v_pk_fma_f16 v42, v22, v86, v42
	v_pk_fma_f16 v43, v23, v87, v43
	v_pk_fma_f16 v44, v24, v88, v44
	v_pk_fma_f16 v45, v25, v89, v45
	v_pk_add_f16 v83, v136, v155 neg_lo:[0,1] neg_hi:[0,1]
	v_pk_add_f16 v84, v135, v156 neg_lo:[0,1] neg_hi:[0,1]
	v_pk_add_f16 v85, v134, v157 neg_lo:[0,1] neg_hi:[0,1]
	v_exp_f16_sdwa v86, v82 dst_sel:WORD_0 dst_unused:UNUSED_PAD src0_sel:WORD_0
	v_exp_f16_sdwa v87, v83 dst_sel:WORD_0 dst_unused:UNUSED_PAD src0_sel:WORD_0
	v_exp_f16_sdwa v88, v84 dst_sel:WORD_0 dst_unused:UNUSED_PAD src0_sel:WORD_0
	v_exp_f16_sdwa v89, v85 dst_sel:WORD_0 dst_unused:UNUSED_PAD src0_sel:WORD_0
	v_exp_f16_sdwa v86, v82 dst_sel:WORD_1 dst_unused:UNUSED_PRESERVE src0_sel:WORD_1
	v_exp_f16_sdwa v87, v83 dst_sel:WORD_1 dst_unused:UNUSED_PRESERVE src0_sel:WORD_1
	v_exp_f16_sdwa v88, v84 dst_sel:WORD_1 dst_unused:UNUSED_PRESERVE src0_sel:WORD_1
	v_exp_f16_sdwa v89, v85 dst_sel:WORD_1 dst_unused:UNUSED_PRESERVE src0_sel:WORD_1
	v_pk_add_f16 v82, v189, v154 neg_lo:[0,1] neg_hi:[0,1]
	v_pk_add_f16 v62, v62, v89
	v_pk_add_f16 v63, v63, v88
	v_pk_add_f16 v64, v64, v87
	v_pk_add_f16 v65, v65, v86
	v_pk_fma_f16 v45, v33, v89, v45
	v_pk_fma_f16 v44, v32, v88, v44
	v_pk_fma_f16 v43, v31, v87, v43
	v_pk_fma_f16 v42, v30, v86, v42
	v_pk_add_f16 v83, v188, v155 neg_lo:[0,1] neg_hi:[0,1]
	v_pk_add_f16 v84, v187, v156 neg_lo:[0,1] neg_hi:[0,1]
	v_pk_add_f16 v85, v186, v157 neg_lo:[0,1] neg_hi:[0,1]
	v_exp_f16_sdwa v86, v82 dst_sel:WORD_0 dst_unused:UNUSED_PAD src0_sel:WORD_0
	v_exp_f16_sdwa v87, v83 dst_sel:WORD_0 dst_unused:UNUSED_PAD src0_sel:WORD_0
	v_exp_f16_sdwa v88, v84 dst_sel:WORD_0 dst_unused:UNUSED_PAD src0_sel:WORD_0
	v_exp_f16_sdwa v89, v85 dst_sel:WORD_0 dst_unused:UNUSED_PAD src0_sel:WORD_0
	v_exp_f16_sdwa v86, v82 dst_sel:WORD_1 dst_unused:UNUSED_PRESERVE src0_sel:WORD_1
	v_exp_f16_sdwa v87, v83 dst_sel:WORD_1 dst_unused:UNUSED_PRESERVE src0_sel:WORD_1
	v_exp_f16_sdwa v88, v84 dst_sel:WORD_1 dst_unused:UNUSED_PRESERVE src0_sel:WORD_1
	v_exp_f16_sdwa v89, v85 dst_sel:WORD_1 dst_unused:UNUSED_PRESERVE src0_sel:WORD_1
	v_exp_f16_sdwa v82, v70 dst_sel:WORD_0 dst_unused:UNUSED_PAD src0_sel:WORD_0
	v_exp_f16_sdwa v83, v71 dst_sel:WORD_0 dst_unused:UNUSED_PAD src0_sel:WORD_0
	v_exp_f16_sdwa v84, v72 dst_sel:WORD_0 dst_unused:UNUSED_PAD src0_sel:WORD_0
	v_exp_f16_sdwa v85, v73 dst_sel:WORD_0 dst_unused:UNUSED_PAD src0_sel:WORD_0
	v_exp_f16_sdwa v82, v70 dst_sel:WORD_1 dst_unused:UNUSED_PRESERVE src0_sel:WORD_1
	v_exp_f16_sdwa v83, v71 dst_sel:WORD_1 dst_unused:UNUSED_PRESERVE src0_sel:WORD_1
	v_exp_f16_sdwa v84, v72 dst_sel:WORD_1 dst_unused:UNUSED_PRESERVE src0_sel:WORD_1
	v_exp_f16_sdwa v85, v73 dst_sel:WORD_1 dst_unused:UNUSED_PRESERVE src0_sel:WORD_1
	v_pk_add_f16 v70, v98, v154 neg_lo:[0,1] neg_hi:[0,1]
	v_pk_add_f16 v62, v62, v89
	v_pk_add_f16 v65, v65, v86
	v_pk_add_f16 v64, v64, v87
	v_pk_add_f16 v63, v63, v88
	v_pk_fma_f16 v42, v46, v86, v42
	v_pk_fma_f16 v43, v47, v87, v43
	v_pk_fma_f16 v44, v48, v88, v44
	v_pk_fma_f16 v45, v49, v89, v45
	v_pk_add_f16 v62, v62, v85
	v_pk_add_f16 v63, v63, v84
	v_pk_add_f16 v64, v64, v83
	v_pk_add_f16 v65, v65, v82
	v_pk_fma_f16 v45, v9, v85, v45
	v_pk_fma_f16 v44, v8, v84, v44
	v_pk_fma_f16 v43, v7, v83, v43
	v_pk_fma_f16 v42, v6, v82, v42
	v_pk_add_f16 v71, v99, v155 neg_lo:[0,1] neg_hi:[0,1]
	v_pk_add_f16 v72, v100, v156 neg_lo:[0,1] neg_hi:[0,1]
	v_pk_add_f16 v73, v101, v157 neg_lo:[0,1] neg_hi:[0,1]
	v_exp_f16_sdwa v82, v70 dst_sel:WORD_0 dst_unused:UNUSED_PAD src0_sel:WORD_0
	v_exp_f16_sdwa v83, v71 dst_sel:WORD_0 dst_unused:UNUSED_PAD src0_sel:WORD_0
	v_exp_f16_sdwa v84, v72 dst_sel:WORD_0 dst_unused:UNUSED_PAD src0_sel:WORD_0
	v_exp_f16_sdwa v85, v73 dst_sel:WORD_0 dst_unused:UNUSED_PAD src0_sel:WORD_0
	v_exp_f16_sdwa v82, v70 dst_sel:WORD_1 dst_unused:UNUSED_PRESERVE src0_sel:WORD_1
	v_exp_f16_sdwa v83, v71 dst_sel:WORD_1 dst_unused:UNUSED_PRESERVE src0_sel:WORD_1
	v_exp_f16_sdwa v84, v72 dst_sel:WORD_1 dst_unused:UNUSED_PRESERVE src0_sel:WORD_1
	v_exp_f16_sdwa v85, v73 dst_sel:WORD_1 dst_unused:UNUSED_PRESERVE src0_sel:WORD_1
	v_pk_add_f16 v70, v114, v154 neg_lo:[0,1] neg_hi:[0,1]
	v_pk_add_f16 v62, v62, v85
	v_pk_add_f16 v65, v65, v82
	v_pk_add_f16 v64, v64, v83
	v_pk_add_f16 v63, v63, v84
	v_pk_fma_f16 v42, v10, v82, v42
	v_pk_fma_f16 v43, v11, v83, v43
	v_pk_fma_f16 v44, v12, v84, v44
	v_pk_fma_f16 v45, v13, v85, v45
	v_pk_add_f16 v71, v115, v155 neg_lo:[0,1] neg_hi:[0,1]
	v_pk_add_f16 v72, v116, v156 neg_lo:[0,1] neg_hi:[0,1]
	v_pk_add_f16 v73, v117, v157 neg_lo:[0,1] neg_hi:[0,1]
	v_exp_f16_sdwa v82, v70 dst_sel:WORD_0 dst_unused:UNUSED_PAD src0_sel:WORD_0
	v_exp_f16_sdwa v83, v71 dst_sel:WORD_0 dst_unused:UNUSED_PAD src0_sel:WORD_0
	v_exp_f16_sdwa v84, v72 dst_sel:WORD_0 dst_unused:UNUSED_PAD src0_sel:WORD_0
	v_exp_f16_sdwa v85, v73 dst_sel:WORD_0 dst_unused:UNUSED_PAD src0_sel:WORD_0
	v_exp_f16_sdwa v82, v70 dst_sel:WORD_1 dst_unused:UNUSED_PRESERVE src0_sel:WORD_1
	v_exp_f16_sdwa v83, v71 dst_sel:WORD_1 dst_unused:UNUSED_PRESERVE src0_sel:WORD_1
	v_exp_f16_sdwa v84, v72 dst_sel:WORD_1 dst_unused:UNUSED_PRESERVE src0_sel:WORD_1
	v_exp_f16_sdwa v85, v73 dst_sel:WORD_1 dst_unused:UNUSED_PRESERVE src0_sel:WORD_1
	s_nop 0
	v_pk_add_f16 v62, v62, v85
	v_pk_add_f16 v63, v63, v84
	v_pk_add_f16 v64, v64, v83
	v_pk_add_f16 v65, v65, v82
	v_rcp_f16_e32 v73, v62
	v_rcp_f16_sdwa v62, v62 dst_sel:DWORD dst_unused:UNUSED_PAD src0_sel:WORD_1
	v_rcp_f16_e32 v70, v65
	v_rcp_f16_sdwa v65, v65 dst_sel:DWORD dst_unused:UNUSED_PAD src0_sel:WORD_1
	v_rcp_f16_e32 v71, v64
	v_rcp_f16_sdwa v64, v64 dst_sel:DWORD dst_unused:UNUSED_PAD src0_sel:WORD_1
	v_rcp_f16_e32 v72, v63
	v_rcp_f16_sdwa v63, v63 dst_sel:DWORD dst_unused:UNUSED_PAD src0_sel:WORD_1
	v_pk_fma_f16 v45, v17, v85, v45
	v_pack_b32_f16 v62, v73, v62
	v_pk_fma_f16 v44, v16, v84, v44
	v_pk_fma_f16 v43, v15, v83, v43
	v_pk_fma_f16 v42, v14, v82, v42
	v_pack_b32_f16 v65, v70, v65
	v_pack_b32_f16 v64, v71, v64
	v_pack_b32_f16 v63, v72, v63
	v_pk_mul_f16 v45, v45, v62
	s_waitcnt vmcnt(6)
	v_pk_mul_f16 v62, v185, v150 op_sel_hi:[0,1]
	v_pk_mul_f16 v70, v183, v150 op_sel_hi:[0,1]
	v_pk_mul_f16 v82, v184, v150 op_sel_hi:[0,1]
	v_pk_mul_f16 v42, v42, v65
	v_pk_mul_f16 v43, v43, v64
	v_pk_mul_f16 v44, v44, v63
	v_pk_mul_f16 v63, v185, v151 op_sel_hi:[0,1]
	v_pk_mul_f16 v64, v185, v152 op_sel_hi:[0,1]
	v_pk_mul_f16 v65, v185, v153 op_sel_hi:[0,1]
	v_pk_mul_f16 v71, v183, v151 op_sel_hi:[0,1]
	v_pk_mul_f16 v72, v183, v152 op_sel_hi:[0,1]
	v_pk_mul_f16 v73, v183, v153 op_sel_hi:[0,1]
	v_pk_mul_f16 v83, v184, v151 op_sel_hi:[0,1]
	v_pk_mul_f16 v84, v184, v152 op_sel_hi:[0,1]
	v_pk_mul_f16 v85, v184, v153 op_sel_hi:[0,1]
	v_pk_fma_f16 v50, v50, v150, v62
	v_pk_fma_f16 v66, v66, v150, v70
	v_pk_fma_f16 v89, v94, v150, v82
	v_pk_fma_f16 v53, v53, v153, v65
	v_pk_maximum3_f16 v114, v50, v66, v89
	v_pk_fma_f16 v52, v52, v152, v64
	v_pk_fma_f16 v51, v51, v151, v63
	v_pk_fma_f16 v69, v69, v153, v73
	v_pk_fma_f16 v68, v68, v152, v72
	v_pk_fma_f16 v67, v67, v151, v71
	v_pk_fma_f16 v86, v97, v153, v85
	v_pk_fma_f16 v87, v96, v152, v84
	v_pk_fma_f16 v88, v95, v151, v83
	v_pk_fma_f16 v97, v18, v150, v62
	v_pk_fma_f16 v101, v34, v150, v70
	v_pk_fma_f16 v109, v54, v150, v82
	v_pk_fma_f16 v62, v74, v150, v62
	v_pk_fma_f16 v70, v102, v150, v70
	v_pk_fma_f16 v82, v118, v150, v82
	v_pk_maximum3_f16 v115, v51, v67, v88
	v_pk_maximum3_f16 v116, v52, v68, v87
	v_pk_maximum3_f16 v117, v53, v69, v86
	v_pk_maximum3_f16 v122, v97, v101, v109
	v_pk_fma_f16 v94, v21, v153, v65
	v_pk_maximum3_f16 v126, v62, v70, v82
	v_pk_fma_f16 v95, v20, v152, v64
	v_pk_maximum3_f16 v114, v114, v122, v126
	v_pk_fma_f16 v96, v19, v151, v63
	v_pk_fma_f16 v98, v37, v153, v73
	v_pk_fma_f16 v99, v36, v152, v72
	v_pk_fma_f16 v100, v35, v151, v71
	v_pk_fma_f16 v106, v57, v153, v85
	v_pk_fma_f16 v107, v56, v152, v84
	v_pk_fma_f16 v108, v55, v151, v83
	v_pk_fma_f16 v65, v77, v153, v65
	v_pk_fma_f16 v64, v76, v152, v64
	v_pk_fma_f16 v63, v75, v151, v63
	v_pk_fma_f16 v73, v105, v153, v73
	v_pk_fma_f16 v72, v104, v152, v72
	v_pk_fma_f16 v71, v103, v151, v71
	v_pk_fma_f16 v85, v121, v153, v85
	v_pk_fma_f16 v84, v120, v152, v84
	v_pk_fma_f16 v83, v119, v151, v83
	v_pk_maximum3_f16 v123, v96, v100, v108
	v_pk_maximum3_f16 v124, v95, v99, v107
	v_pk_maximum3_f16 v125, v94, v98, v106
	v_pk_maximum3_f16 v128, v64, v72, v84
	v_pk_maximum3_f16 v129, v65, v73, v85
	v_pk_maximum3_f16 v127, v63, v71, v83
	v_pk_maximum3_f16 v115, v115, v123, v127
	v_pk_maximum3_f16 v116, v116, v124, v128
	v_pk_maximum3_f16 v117, v117, v125, v129
	v_pk_add_f16 v50, v50, v114 neg_lo:[0,1] neg_hi:[0,1]
	v_pk_add_f16 v51, v51, v115 neg_lo:[0,1] neg_hi:[0,1]
	v_pk_add_f16 v52, v52, v116 neg_lo:[0,1] neg_hi:[0,1]
	v_pk_add_f16 v53, v53, v117 neg_lo:[0,1] neg_hi:[0,1]
	v_pk_add_f16 v66, v66, v114 neg_lo:[0,1] neg_hi:[0,1]
	v_exp_f16_sdwa v122, v50 dst_sel:WORD_0 dst_unused:UNUSED_PAD src0_sel:WORD_0
	v_exp_f16_sdwa v123, v51 dst_sel:WORD_0 dst_unused:UNUSED_PAD src0_sel:WORD_0
	v_exp_f16_sdwa v124, v52 dst_sel:WORD_0 dst_unused:UNUSED_PAD src0_sel:WORD_0
	v_exp_f16_sdwa v125, v53 dst_sel:WORD_0 dst_unused:UNUSED_PAD src0_sel:WORD_0
	v_exp_f16_sdwa v122, v50 dst_sel:WORD_1 dst_unused:UNUSED_PRESERVE src0_sel:WORD_1
	v_exp_f16_sdwa v123, v51 dst_sel:WORD_1 dst_unused:UNUSED_PRESERVE src0_sel:WORD_1
	v_exp_f16_sdwa v124, v52 dst_sel:WORD_1 dst_unused:UNUSED_PRESERVE src0_sel:WORD_1
	v_exp_f16_sdwa v125, v53 dst_sel:WORD_1 dst_unused:UNUSED_PRESERVE src0_sel:WORD_1
	v_pk_add_f16 v67, v67, v115 neg_lo:[0,1] neg_hi:[0,1]
	v_pk_add_f16 v50, v125, 0
	v_pk_fma_f16 v22, v22, v122, 0
	v_pk_add_f16 v51, v124, 0
	v_pk_add_f16 v52, v123, 0
	v_pk_add_f16 v53, v122, 0
	v_pk_fma_f16 v23, v23, v123, 0
	v_pk_fma_f16 v24, v24, v124, 0
	v_pk_fma_f16 v25, v25, v125, 0
	v_pk_add_f16 v68, v68, v116 neg_lo:[0,1] neg_hi:[0,1]
	v_pk_add_f16 v69, v69, v117 neg_lo:[0,1] neg_hi:[0,1]
	v_exp_f16_sdwa v122, v66 dst_sel:WORD_0 dst_unused:UNUSED_PAD src0_sel:WORD_0
	v_exp_f16_sdwa v123, v67 dst_sel:WORD_0 dst_unused:UNUSED_PAD src0_sel:WORD_0
	v_exp_f16_sdwa v124, v68 dst_sel:WORD_0 dst_unused:UNUSED_PAD src0_sel:WORD_0
	v_exp_f16_sdwa v125, v69 dst_sel:WORD_0 dst_unused:UNUSED_PAD src0_sel:WORD_0
	v_exp_f16_sdwa v122, v66 dst_sel:WORD_1 dst_unused:UNUSED_PRESERVE src0_sel:WORD_1
	v_exp_f16_sdwa v123, v67 dst_sel:WORD_1 dst_unused:UNUSED_PRESERVE src0_sel:WORD_1
	v_exp_f16_sdwa v124, v68 dst_sel:WORD_1 dst_unused:UNUSED_PRESERVE src0_sel:WORD_1
	v_exp_f16_sdwa v125, v69 dst_sel:WORD_1 dst_unused:UNUSED_PRESERVE src0_sel:WORD_1
	s_nop 0
	v_pk_add_f16 v50, v50, v125
	v_pk_fma_f16 v22, v30, v122, v22
	v_pk_add_f16 v30, v89, v114 neg_lo:[0,1] neg_hi:[0,1]
	v_pk_add_f16 v53, v53, v122
	v_pk_add_f16 v52, v52, v123
	v_pk_add_f16 v51, v51, v124
	v_pk_fma_f16 v25, v33, v125, v25
	v_pk_fma_f16 v24, v32, v124, v24
	v_pk_fma_f16 v23, v31, v123, v23
	v_pk_add_f16 v31, v88, v115 neg_lo:[0,1] neg_hi:[0,1]
	v_pk_add_f16 v32, v87, v116 neg_lo:[0,1] neg_hi:[0,1]
	v_pk_add_f16 v33, v86, v117 neg_lo:[0,1] neg_hi:[0,1]
	v_exp_f16_sdwa v66, v30 dst_sel:WORD_0 dst_unused:UNUSED_PAD src0_sel:WORD_0
	v_exp_f16_sdwa v67, v31 dst_sel:WORD_0 dst_unused:UNUSED_PAD src0_sel:WORD_0
	v_exp_f16_sdwa v68, v32 dst_sel:WORD_0 dst_unused:UNUSED_PAD src0_sel:WORD_0
	v_exp_f16_sdwa v69, v33 dst_sel:WORD_0 dst_unused:UNUSED_PAD src0_sel:WORD_0
	v_exp_f16_sdwa v66, v30 dst_sel:WORD_1 dst_unused:UNUSED_PRESERVE src0_sel:WORD_1
	v_exp_f16_sdwa v67, v31 dst_sel:WORD_1 dst_unused:UNUSED_PRESERVE src0_sel:WORD_1
	v_exp_f16_sdwa v68, v32 dst_sel:WORD_1 dst_unused:UNUSED_PRESERVE src0_sel:WORD_1
	v_exp_f16_sdwa v69, v33 dst_sel:WORD_1 dst_unused:UNUSED_PRESERVE src0_sel:WORD_1
	s_nop 0
	v_pk_add_f16 v30, v50, v69
	v_pk_add_f16 v31, v51, v68
	v_pk_add_f16 v32, v52, v67
	v_pk_add_f16 v33, v53, v66
	v_pk_fma_f16 v22, v46, v66, v22
	v_pk_fma_f16 v23, v47, v67, v23
	v_pk_fma_f16 v24, v48, v68, v24
	v_pk_fma_f16 v25, v49, v69, v25
	v_pk_add_f16 v46, v97, v114 neg_lo:[0,1] neg_hi:[0,1]
	v_pk_add_f16 v47, v96, v115 neg_lo:[0,1] neg_hi:[0,1]
	v_pk_add_f16 v48, v95, v116 neg_lo:[0,1] neg_hi:[0,1]
	v_pk_add_f16 v49, v94, v117 neg_lo:[0,1] neg_hi:[0,1]
	v_exp_f16_sdwa v50, v46 dst_sel:WORD_0 dst_unused:UNUSED_PAD src0_sel:WORD_0
	v_exp_f16_sdwa v51, v47 dst_sel:WORD_0 dst_unused:UNUSED_PAD src0_sel:WORD_0
	v_exp_f16_sdwa v52, v48 dst_sel:WORD_0 dst_unused:UNUSED_PAD src0_sel:WORD_0
	v_exp_f16_sdwa v53, v49 dst_sel:WORD_0 dst_unused:UNUSED_PAD src0_sel:WORD_0
	v_exp_f16_sdwa v50, v46 dst_sel:WORD_1 dst_unused:UNUSED_PRESERVE src0_sel:WORD_1
	v_exp_f16_sdwa v51, v47 dst_sel:WORD_1 dst_unused:UNUSED_PRESERVE src0_sel:WORD_1
	v_exp_f16_sdwa v52, v48 dst_sel:WORD_1 dst_unused:UNUSED_PRESERVE src0_sel:WORD_1
	v_exp_f16_sdwa v53, v49 dst_sel:WORD_1 dst_unused:UNUSED_PRESERVE src0_sel:WORD_1
	v_pk_add_f16 v46, v101, v114 neg_lo:[0,1] neg_hi:[0,1]
	v_pk_add_f16 v30, v30, v53
	v_pk_add_f16 v33, v33, v50
	v_pk_add_f16 v32, v32, v51
	v_pk_add_f16 v31, v31, v52
	v_pk_fma_f16 v25, v9, v53, v25
	v_pk_fma_f16 v24, v8, v52, v24
	v_pk_fma_f16 v23, v7, v51, v23
	v_pk_fma_f16 v22, v6, v50, v22
	v_pk_add_f16 v47, v100, v115 neg_lo:[0,1] neg_hi:[0,1]
	v_pk_add_f16 v48, v99, v116 neg_lo:[0,1] neg_hi:[0,1]
	v_pk_add_f16 v49, v98, v117 neg_lo:[0,1] neg_hi:[0,1]
	v_exp_f16_sdwa v50, v46 dst_sel:WORD_0 dst_unused:UNUSED_PAD src0_sel:WORD_0
	v_exp_f16_sdwa v51, v47 dst_sel:WORD_0 dst_unused:UNUSED_PAD src0_sel:WORD_0
	v_exp_f16_sdwa v52, v48 dst_sel:WORD_0 dst_unused:UNUSED_PAD src0_sel:WORD_0
	v_exp_f16_sdwa v53, v49 dst_sel:WORD_0 dst_unused:UNUSED_PAD src0_sel:WORD_0
	v_exp_f16_sdwa v50, v46 dst_sel:WORD_1 dst_unused:UNUSED_PRESERVE src0_sel:WORD_1
	v_exp_f16_sdwa v51, v47 dst_sel:WORD_1 dst_unused:UNUSED_PRESERVE src0_sel:WORD_1
	v_exp_f16_sdwa v52, v48 dst_sel:WORD_1 dst_unused:UNUSED_PRESERVE src0_sel:WORD_1
	v_exp_f16_sdwa v53, v49 dst_sel:WORD_1 dst_unused:UNUSED_PRESERVE src0_sel:WORD_1
	v_pk_add_f16 v46, v109, v114 neg_lo:[0,1] neg_hi:[0,1]
	v_pk_add_f16 v30, v30, v53
	v_pk_add_f16 v31, v31, v52
	v_pk_add_f16 v32, v32, v51
	v_pk_add_f16 v33, v33, v50
	v_pk_fma_f16 v22, v10, v50, v22
	v_pk_fma_f16 v23, v11, v51, v23
	v_pk_fma_f16 v24, v12, v52, v24
	v_pk_fma_f16 v25, v13, v53, v25
	v_pk_add_f16 v47, v108, v115 neg_lo:[0,1] neg_hi:[0,1]
	v_pk_add_f16 v48, v107, v116 neg_lo:[0,1] neg_hi:[0,1]
	v_pk_add_f16 v49, v106, v117 neg_lo:[0,1] neg_hi:[0,1]
	v_exp_f16_sdwa v50, v46 dst_sel:WORD_0 dst_unused:UNUSED_PAD src0_sel:WORD_0
	v_exp_f16_sdwa v51, v47 dst_sel:WORD_0 dst_unused:UNUSED_PAD src0_sel:WORD_0
	v_exp_f16_sdwa v52, v48 dst_sel:WORD_0 dst_unused:UNUSED_PAD src0_sel:WORD_0
	v_exp_f16_sdwa v53, v49 dst_sel:WORD_0 dst_unused:UNUSED_PAD src0_sel:WORD_0
	v_exp_f16_sdwa v50, v46 dst_sel:WORD_1 dst_unused:UNUSED_PRESERVE src0_sel:WORD_1
	v_exp_f16_sdwa v51, v47 dst_sel:WORD_1 dst_unused:UNUSED_PRESERVE src0_sel:WORD_1
	v_exp_f16_sdwa v52, v48 dst_sel:WORD_1 dst_unused:UNUSED_PRESERVE src0_sel:WORD_1
	v_exp_f16_sdwa v53, v49 dst_sel:WORD_1 dst_unused:UNUSED_PRESERVE src0_sel:WORD_1
	v_pk_add_f16 v46, v62, v114 neg_lo:[0,1] neg_hi:[0,1]
	v_pk_add_f16 v30, v30, v53
	v_pk_add_f16 v33, v33, v50
	v_pk_add_f16 v32, v32, v51
	v_pk_add_f16 v31, v31, v52
	v_pk_fma_f16 v25, v17, v53, v25
	v_pk_fma_f16 v24, v16, v52, v24
	v_pk_fma_f16 v23, v15, v51, v23
	v_pk_fma_f16 v22, v14, v50, v22
	v_pk_add_f16 v47, v63, v115 neg_lo:[0,1] neg_hi:[0,1]
	v_pk_add_f16 v48, v64, v116 neg_lo:[0,1] neg_hi:[0,1]
	v_pk_add_f16 v49, v65, v117 neg_lo:[0,1] neg_hi:[0,1]
	v_exp_f16_sdwa v50, v46 dst_sel:WORD_0 dst_unused:UNUSED_PAD src0_sel:WORD_0
	v_exp_f16_sdwa v51, v47 dst_sel:WORD_0 dst_unused:UNUSED_PAD src0_sel:WORD_0
	v_exp_f16_sdwa v52, v48 dst_sel:WORD_0 dst_unused:UNUSED_PAD src0_sel:WORD_0
	v_exp_f16_sdwa v53, v49 dst_sel:WORD_0 dst_unused:UNUSED_PAD src0_sel:WORD_0
	v_exp_f16_sdwa v50, v46 dst_sel:WORD_1 dst_unused:UNUSED_PRESERVE src0_sel:WORD_1
	v_exp_f16_sdwa v51, v47 dst_sel:WORD_1 dst_unused:UNUSED_PRESERVE src0_sel:WORD_1
	v_exp_f16_sdwa v52, v48 dst_sel:WORD_1 dst_unused:UNUSED_PRESERVE src0_sel:WORD_1
	v_exp_f16_sdwa v53, v49 dst_sel:WORD_1 dst_unused:UNUSED_PRESERVE src0_sel:WORD_1
	v_pk_add_f16 v46, v70, v114 neg_lo:[0,1] neg_hi:[0,1]
	v_pk_add_f16 v30, v30, v53
	v_pk_add_f16 v31, v31, v52
	v_pk_add_f16 v32, v32, v51
	v_pk_add_f16 v33, v33, v50
	v_pk_fma_f16 v22, v26, v50, v22
	v_pk_fma_f16 v23, v27, v51, v23
	v_pk_fma_f16 v24, v28, v52, v24
	v_pk_fma_f16 v25, v29, v53, v25
	v_pk_add_f16 v47, v71, v115 neg_lo:[0,1] neg_hi:[0,1]
	v_pk_add_f16 v48, v72, v116 neg_lo:[0,1] neg_hi:[0,1]
	v_pk_add_f16 v49, v73, v117 neg_lo:[0,1] neg_hi:[0,1]
	v_exp_f16_sdwa v50, v46 dst_sel:WORD_0 dst_unused:UNUSED_PAD src0_sel:WORD_0
	v_exp_f16_sdwa v51, v47 dst_sel:WORD_0 dst_unused:UNUSED_PAD src0_sel:WORD_0
	v_exp_f16_sdwa v52, v48 dst_sel:WORD_0 dst_unused:UNUSED_PAD src0_sel:WORD_0
	v_exp_f16_sdwa v53, v49 dst_sel:WORD_0 dst_unused:UNUSED_PAD src0_sel:WORD_0
	v_exp_f16_sdwa v50, v46 dst_sel:WORD_1 dst_unused:UNUSED_PRESERVE src0_sel:WORD_1
	v_exp_f16_sdwa v51, v47 dst_sel:WORD_1 dst_unused:UNUSED_PRESERVE src0_sel:WORD_1
	v_exp_f16_sdwa v52, v48 dst_sel:WORD_1 dst_unused:UNUSED_PRESERVE src0_sel:WORD_1
	v_exp_f16_sdwa v53, v49 dst_sel:WORD_1 dst_unused:UNUSED_PRESERVE src0_sel:WORD_1
	v_pk_add_f16 v46, v82, v114 neg_lo:[0,1] neg_hi:[0,1]
	v_pk_add_f16 v30, v30, v53
	v_pk_add_f16 v33, v33, v50
	v_pk_add_f16 v32, v32, v51
	v_pk_add_f16 v31, v31, v52
	v_pk_fma_f16 v25, v41, v53, v25
	v_pk_fma_f16 v24, v40, v52, v24
	v_pk_fma_f16 v23, v39, v51, v23
	v_pk_fma_f16 v22, v38, v50, v22
	v_pk_add_f16 v47, v83, v115 neg_lo:[0,1] neg_hi:[0,1]
	v_pk_add_f16 v48, v84, v116 neg_lo:[0,1] neg_hi:[0,1]
	v_pk_add_f16 v49, v85, v117 neg_lo:[0,1] neg_hi:[0,1]
	v_exp_f16_sdwa v50, v46 dst_sel:WORD_0 dst_unused:UNUSED_PAD src0_sel:WORD_0
	v_exp_f16_sdwa v51, v47 dst_sel:WORD_0 dst_unused:UNUSED_PAD src0_sel:WORD_0
	v_exp_f16_sdwa v52, v48 dst_sel:WORD_0 dst_unused:UNUSED_PAD src0_sel:WORD_0
	v_exp_f16_sdwa v53, v49 dst_sel:WORD_0 dst_unused:UNUSED_PAD src0_sel:WORD_0
	v_exp_f16_sdwa v50, v46 dst_sel:WORD_1 dst_unused:UNUSED_PRESERVE src0_sel:WORD_1
	v_exp_f16_sdwa v51, v47 dst_sel:WORD_1 dst_unused:UNUSED_PRESERVE src0_sel:WORD_1
	v_exp_f16_sdwa v52, v48 dst_sel:WORD_1 dst_unused:UNUSED_PRESERVE src0_sel:WORD_1
	v_exp_f16_sdwa v53, v49 dst_sel:WORD_1 dst_unused:UNUSED_PRESERVE src0_sel:WORD_1
	s_nop 0
	v_pk_add_f16 v30, v30, v53
	v_pk_add_f16 v31, v31, v52
	v_rcp_f16_e32 v48, v30
	v_rcp_f16_sdwa v30, v30 dst_sel:DWORD dst_unused:UNUSED_PAD src0_sel:WORD_1
	v_pk_add_f16 v32, v32, v51
	v_rcp_f16_e32 v49, v31
	v_rcp_f16_sdwa v31, v31 dst_sel:DWORD dst_unused:UNUSED_PAD src0_sel:WORD_1
	v_pk_add_f16 v33, v33, v50
	v_rcp_f16_e32 v47, v32
	v_rcp_f16_sdwa v32, v32 dst_sel:DWORD dst_unused:UNUSED_PAD src0_sel:WORD_1
	v_rcp_f16_e32 v46, v33
	v_rcp_f16_sdwa v33, v33 dst_sel:DWORD dst_unused:UNUSED_PAD src0_sel:WORD_1
	v_pk_fma_f16 v25, v61, v53, v25
	v_pack_b32_f16 v30, v48, v30
	v_pk_fma_f16 v24, v60, v52, v24
	v_pk_mul_f16 v25, v25, v30
	v_pack_b32_f16 v30, v49, v31
	v_pk_fma_f16 v23, v59, v51, v23
	v_pk_mul_f16 v24, v24, v30
	v_pack_b32_f16 v30, v47, v32
	v_pk_fma_f16 v22, v58, v50, v22
	v_pk_mul_f16 v23, v23, v30
	v_pack_b32_f16 v30, v46, v33
	v_pk_mul_f16 v22, v22, v30
	s_waitcnt vmcnt(0)
	v_pk_mul_f16 v30, v185, v146 op_sel_hi:[0,1]
	v_pk_mul_f16 v31, v185, v147 op_sel_hi:[0,1]
	v_pk_mul_f16 v32, v185, v148 op_sel_hi:[0,1]
	v_pk_mul_f16 v33, v185, v149 op_sel_hi:[0,1]
	v_pk_mul_f16 v46, v183, v146 op_sel_hi:[0,1]
	v_pk_mul_f16 v47, v183, v147 op_sel_hi:[0,1]
	v_pk_mul_f16 v48, v183, v148 op_sel_hi:[0,1]
	v_pk_mul_f16 v49, v183, v149 op_sel_hi:[0,1]
	v_pk_mul_f16 v50, v184, v146 op_sel_hi:[0,1]
	v_pk_mul_f16 v51, v184, v147 op_sel_hi:[0,1]
	v_pk_mul_f16 v52, v184, v148 op_sel_hi:[0,1]
	v_pk_mul_f16 v53, v184, v149 op_sel_hi:[0,1]
	v_pk_fma_f16 v21, v21, v149, v33
	v_pk_fma_f16 v20, v20, v148, v32
	v_pk_fma_f16 v19, v19, v147, v31
	v_pk_fma_f16 v18, v18, v146, v30
	v_pk_fma_f16 v37, v37, v149, v49
	v_pk_fma_f16 v36, v36, v148, v48
	v_pk_fma_f16 v35, v35, v147, v47
	v_pk_fma_f16 v34, v34, v146, v46
	v_pk_fma_f16 v57, v57, v149, v53
	v_pk_fma_f16 v56, v56, v148, v52
	v_pk_fma_f16 v55, v55, v147, v51
	v_pk_fma_f16 v54, v54, v146, v50
	v_pk_fma_f16 v62, v77, v149, v33
	v_pk_fma_f16 v63, v76, v148, v32
	v_pk_fma_f16 v64, v75, v147, v31
	v_pk_fma_f16 v65, v74, v146, v30
	v_pk_maximum3_f16 v74, v18, v34, v54
	v_pk_maximum3_f16 v75, v19, v35, v55
	v_pk_maximum3_f16 v76, v20, v36, v56
	v_pk_maximum3_f16 v77, v21, v37, v57
	v_pk_fma_f16 v66, v105, v149, v49
	v_pk_fma_f16 v67, v104, v148, v48
	v_pk_fma_f16 v68, v103, v147, v47
	v_pk_fma_f16 v69, v102, v146, v46
	v_pk_fma_f16 v70, v121, v149, v53
	v_pk_fma_f16 v71, v120, v148, v52
	v_pk_fma_f16 v72, v119, v147, v51
	v_pk_fma_f16 v73, v118, v146, v50
	v_pk_fma_f16 v33, v133, v149, v33
	v_pk_fma_f16 v32, v132, v148, v32
	v_pk_fma_f16 v31, v131, v147, v31
	v_pk_fma_f16 v30, v130, v146, v30
	v_pk_fma_f16 v49, v141, v149, v49
	v_pk_fma_f16 v48, v140, v148, v48
	v_pk_fma_f16 v47, v139, v147, v47
	v_pk_fma_f16 v46, v138, v146, v46
	v_pk_fma_f16 v53, v145, v149, v53
	v_pk_fma_f16 v52, v144, v148, v52
	v_pk_fma_f16 v51, v143, v147, v51
	v_pk_fma_f16 v50, v142, v146, v50
	v_pk_maximum3_f16 v82, v65, v69, v73
	v_pk_maximum3_f16 v83, v64, v68, v72
	v_pk_maximum3_f16 v84, v63, v67, v71
	v_pk_maximum3_f16 v85, v62, v66, v70
	v_pk_maximum3_f16 v87, v31, v47, v51
	v_pk_maximum3_f16 v86, v30, v46, v50
	v_pk_maximum3_f16 v88, v32, v48, v52
	v_pk_maximum3_f16 v89, v33, v49, v53
	v_pk_maximum3_f16 v74, v74, v82, v86
	v_pk_maximum3_f16 v75, v75, v83, v87
	v_pk_maximum3_f16 v76, v76, v84, v88
	v_pk_maximum3_f16 v77, v77, v85, v89
	s_nop 0
	v_pk_add_f16 v18, v18, v74 neg_lo:[0,1] neg_hi:[0,1]
	v_pk_add_f16 v19, v19, v75 neg_lo:[0,1] neg_hi:[0,1]
	v_pk_add_f16 v20, v20, v76 neg_lo:[0,1] neg_hi:[0,1]
	v_pk_add_f16 v21, v21, v77 neg_lo:[0,1] neg_hi:[0,1]
	v_pk_add_f16 v34, v34, v74 neg_lo:[0,1] neg_hi:[0,1]
	v_exp_f16_sdwa v82, v18 dst_sel:WORD_0 dst_unused:UNUSED_PAD src0_sel:WORD_0
	v_exp_f16_sdwa v83, v19 dst_sel:WORD_0 dst_unused:UNUSED_PAD src0_sel:WORD_0
	v_exp_f16_sdwa v84, v20 dst_sel:WORD_0 dst_unused:UNUSED_PAD src0_sel:WORD_0
	v_exp_f16_sdwa v85, v21 dst_sel:WORD_0 dst_unused:UNUSED_PAD src0_sel:WORD_0
	v_exp_f16_sdwa v82, v18 dst_sel:WORD_1 dst_unused:UNUSED_PRESERVE src0_sel:WORD_1
	v_exp_f16_sdwa v83, v19 dst_sel:WORD_1 dst_unused:UNUSED_PRESERVE src0_sel:WORD_1
	v_exp_f16_sdwa v84, v20 dst_sel:WORD_1 dst_unused:UNUSED_PRESERVE src0_sel:WORD_1
	v_exp_f16_sdwa v85, v21 dst_sel:WORD_1 dst_unused:UNUSED_PRESERVE src0_sel:WORD_1
	v_pk_add_f16 v35, v35, v75 neg_lo:[0,1] neg_hi:[0,1]
	v_pk_add_f16 v18, v82, 0
	v_pk_add_f16 v19, v83, 0
	v_pk_add_f16 v20, v84, 0
	v_pk_add_f16 v21, v85, 0
	v_pk_fma_f16 v6, v6, v82, 0
	v_pk_fma_f16 v7, v7, v83, 0
	v_pk_fma_f16 v8, v8, v84, 0
	v_pk_fma_f16 v9, v9, v85, 0
	v_pk_add_f16 v36, v36, v76 neg_lo:[0,1] neg_hi:[0,1]
	v_pk_add_f16 v37, v37, v77 neg_lo:[0,1] neg_hi:[0,1]
	v_exp_f16_sdwa v82, v34 dst_sel:WORD_0 dst_unused:UNUSED_PAD src0_sel:WORD_0
	v_exp_f16_sdwa v83, v35 dst_sel:WORD_0 dst_unused:UNUSED_PAD src0_sel:WORD_0
	v_exp_f16_sdwa v84, v36 dst_sel:WORD_0 dst_unused:UNUSED_PAD src0_sel:WORD_0
	v_exp_f16_sdwa v85, v37 dst_sel:WORD_0 dst_unused:UNUSED_PAD src0_sel:WORD_0
	v_exp_f16_sdwa v82, v34 dst_sel:WORD_1 dst_unused:UNUSED_PRESERVE src0_sel:WORD_1
	v_exp_f16_sdwa v83, v35 dst_sel:WORD_1 dst_unused:UNUSED_PRESERVE src0_sel:WORD_1
	v_exp_f16_sdwa v84, v36 dst_sel:WORD_1 dst_unused:UNUSED_PRESERVE src0_sel:WORD_1
	v_exp_f16_sdwa v85, v37 dst_sel:WORD_1 dst_unused:UNUSED_PRESERVE src0_sel:WORD_1
	s_nop 0
	v_pk_add_f16 v21, v21, v85
	v_pk_add_f16 v20, v20, v84
	v_pk_add_f16 v19, v19, v83
	v_pk_add_f16 v18, v18, v82
	v_pk_fma_f16 v9, v13, v85, v9
	v_pk_fma_f16 v8, v12, v84, v8
	v_pk_fma_f16 v7, v11, v83, v7
	v_pk_fma_f16 v6, v10, v82, v6
	v_pk_add_f16 v10, v54, v74 neg_lo:[0,1] neg_hi:[0,1]
	v_pk_add_f16 v11, v55, v75 neg_lo:[0,1] neg_hi:[0,1]
	v_pk_add_f16 v12, v56, v76 neg_lo:[0,1] neg_hi:[0,1]
	v_pk_add_f16 v13, v57, v77 neg_lo:[0,1] neg_hi:[0,1]
	v_exp_f16_sdwa v34, v10 dst_sel:WORD_0 dst_unused:UNUSED_PAD src0_sel:WORD_0
	v_exp_f16_sdwa v35, v11 dst_sel:WORD_0 dst_unused:UNUSED_PAD src0_sel:WORD_0
	v_exp_f16_sdwa v36, v12 dst_sel:WORD_0 dst_unused:UNUSED_PAD src0_sel:WORD_0
	v_exp_f16_sdwa v37, v13 dst_sel:WORD_0 dst_unused:UNUSED_PAD src0_sel:WORD_0
	v_exp_f16_sdwa v34, v10 dst_sel:WORD_1 dst_unused:UNUSED_PRESERVE src0_sel:WORD_1
	v_exp_f16_sdwa v35, v11 dst_sel:WORD_1 dst_unused:UNUSED_PRESERVE src0_sel:WORD_1
	v_exp_f16_sdwa v36, v12 dst_sel:WORD_1 dst_unused:UNUSED_PRESERVE src0_sel:WORD_1
	v_exp_f16_sdwa v37, v13 dst_sel:WORD_1 dst_unused:UNUSED_PRESERVE src0_sel:WORD_1
	v_pk_add_f16 v10, v18, v34
	v_pk_add_f16 v11, v19, v35
	v_pk_add_f16 v12, v20, v36
	v_pk_add_f16 v13, v21, v37
	v_pk_fma_f16 v6, v14, v34, v6
	v_pk_fma_f16 v7, v15, v35, v7
	v_pk_fma_f16 v8, v16, v36, v8
	v_pk_fma_f16 v9, v17, v37, v9
	v_pk_add_f16 v14, v65, v74 neg_lo:[0,1] neg_hi:[0,1]
	v_pk_add_f16 v15, v64, v75 neg_lo:[0,1] neg_hi:[0,1]
	v_pk_add_f16 v16, v63, v76 neg_lo:[0,1] neg_hi:[0,1]
	v_pk_add_f16 v17, v62, v77 neg_lo:[0,1] neg_hi:[0,1]
	v_exp_f16_sdwa v18, v14 dst_sel:WORD_0 dst_unused:UNUSED_PAD src0_sel:WORD_0
	v_exp_f16_sdwa v19, v15 dst_sel:WORD_0 dst_unused:UNUSED_PAD src0_sel:WORD_0
	v_exp_f16_sdwa v20, v16 dst_sel:WORD_0 dst_unused:UNUSED_PAD src0_sel:WORD_0
	v_exp_f16_sdwa v21, v17 dst_sel:WORD_0 dst_unused:UNUSED_PAD src0_sel:WORD_0
	v_exp_f16_sdwa v18, v14 dst_sel:WORD_1 dst_unused:UNUSED_PRESERVE src0_sel:WORD_1
	v_exp_f16_sdwa v19, v15 dst_sel:WORD_1 dst_unused:UNUSED_PRESERVE src0_sel:WORD_1
	v_exp_f16_sdwa v20, v16 dst_sel:WORD_1 dst_unused:UNUSED_PRESERVE src0_sel:WORD_1
	v_exp_f16_sdwa v21, v17 dst_sel:WORD_1 dst_unused:UNUSED_PRESERVE src0_sel:WORD_1
	v_pk_add_f16 v14, v69, v74 neg_lo:[0,1] neg_hi:[0,1]
	v_pk_add_f16 v13, v13, v21
	v_pk_add_f16 v12, v12, v20
	v_pk_add_f16 v11, v11, v19
	v_pk_add_f16 v10, v10, v18
	v_pk_fma_f16 v9, v29, v21, v9
	v_pk_fma_f16 v8, v28, v20, v8
	v_pk_fma_f16 v7, v27, v19, v7
	v_pk_fma_f16 v6, v26, v18, v6
	v_pk_add_f16 v15, v68, v75 neg_lo:[0,1] neg_hi:[0,1]
	v_pk_add_f16 v16, v67, v76 neg_lo:[0,1] neg_hi:[0,1]
	v_pk_add_f16 v17, v66, v77 neg_lo:[0,1] neg_hi:[0,1]
	v_exp_f16_sdwa v18, v14 dst_sel:WORD_0 dst_unused:UNUSED_PAD src0_sel:WORD_0
	v_exp_f16_sdwa v19, v15 dst_sel:WORD_0 dst_unused:UNUSED_PAD src0_sel:WORD_0
	v_exp_f16_sdwa v20, v16 dst_sel:WORD_0 dst_unused:UNUSED_PAD src0_sel:WORD_0
	v_exp_f16_sdwa v21, v17 dst_sel:WORD_0 dst_unused:UNUSED_PAD src0_sel:WORD_0
	v_exp_f16_sdwa v18, v14 dst_sel:WORD_1 dst_unused:UNUSED_PRESERVE src0_sel:WORD_1
	v_exp_f16_sdwa v19, v15 dst_sel:WORD_1 dst_unused:UNUSED_PRESERVE src0_sel:WORD_1
	v_exp_f16_sdwa v20, v16 dst_sel:WORD_1 dst_unused:UNUSED_PRESERVE src0_sel:WORD_1
	v_exp_f16_sdwa v21, v17 dst_sel:WORD_1 dst_unused:UNUSED_PRESERVE src0_sel:WORD_1
	v_pk_add_f16 v14, v73, v74 neg_lo:[0,1] neg_hi:[0,1]
	v_pk_add_f16 v10, v10, v18
	v_pk_add_f16 v11, v11, v19
	v_pk_add_f16 v12, v12, v20
	v_pk_add_f16 v13, v13, v21
	v_pk_fma_f16 v6, v38, v18, v6
	v_pk_fma_f16 v7, v39, v19, v7
	v_pk_fma_f16 v8, v40, v20, v8
	v_pk_fma_f16 v9, v41, v21, v9
	v_pk_add_f16 v15, v72, v75 neg_lo:[0,1] neg_hi:[0,1]
	v_pk_add_f16 v16, v71, v76 neg_lo:[0,1] neg_hi:[0,1]
	v_pk_add_f16 v17, v70, v77 neg_lo:[0,1] neg_hi:[0,1]
	v_exp_f16_sdwa v18, v14 dst_sel:WORD_0 dst_unused:UNUSED_PAD src0_sel:WORD_0
	v_exp_f16_sdwa v19, v15 dst_sel:WORD_0 dst_unused:UNUSED_PAD src0_sel:WORD_0
	v_exp_f16_sdwa v20, v16 dst_sel:WORD_0 dst_unused:UNUSED_PAD src0_sel:WORD_0
	v_exp_f16_sdwa v21, v17 dst_sel:WORD_0 dst_unused:UNUSED_PAD src0_sel:WORD_0
	v_exp_f16_sdwa v18, v14 dst_sel:WORD_1 dst_unused:UNUSED_PRESERVE src0_sel:WORD_1
	v_exp_f16_sdwa v19, v15 dst_sel:WORD_1 dst_unused:UNUSED_PRESERVE src0_sel:WORD_1
	v_exp_f16_sdwa v20, v16 dst_sel:WORD_1 dst_unused:UNUSED_PRESERVE src0_sel:WORD_1
	v_exp_f16_sdwa v21, v17 dst_sel:WORD_1 dst_unused:UNUSED_PRESERVE src0_sel:WORD_1
	v_pk_add_f16 v14, v30, v74 neg_lo:[0,1] neg_hi:[0,1]
	v_pk_add_f16 v13, v13, v21
	v_pk_add_f16 v12, v12, v20
	v_pk_add_f16 v11, v11, v19
	v_pk_add_f16 v10, v10, v18
	v_pk_fma_f16 v9, v61, v21, v9
	v_pk_fma_f16 v8, v60, v20, v8
	v_pk_fma_f16 v7, v59, v19, v7
	v_pk_fma_f16 v6, v58, v18, v6
	v_pk_add_f16 v15, v31, v75 neg_lo:[0,1] neg_hi:[0,1]
	v_pk_add_f16 v16, v32, v76 neg_lo:[0,1] neg_hi:[0,1]
	v_pk_add_f16 v17, v33, v77 neg_lo:[0,1] neg_hi:[0,1]
	v_exp_f16_sdwa v18, v14 dst_sel:WORD_0 dst_unused:UNUSED_PAD src0_sel:WORD_0
	v_exp_f16_sdwa v19, v15 dst_sel:WORD_0 dst_unused:UNUSED_PAD src0_sel:WORD_0
	v_exp_f16_sdwa v20, v16 dst_sel:WORD_0 dst_unused:UNUSED_PAD src0_sel:WORD_0
	v_exp_f16_sdwa v21, v17 dst_sel:WORD_0 dst_unused:UNUSED_PAD src0_sel:WORD_0
	v_exp_f16_sdwa v18, v14 dst_sel:WORD_1 dst_unused:UNUSED_PRESERVE src0_sel:WORD_1
	v_exp_f16_sdwa v19, v15 dst_sel:WORD_1 dst_unused:UNUSED_PRESERVE src0_sel:WORD_1
	v_exp_f16_sdwa v20, v16 dst_sel:WORD_1 dst_unused:UNUSED_PRESERVE src0_sel:WORD_1
	v_exp_f16_sdwa v21, v17 dst_sel:WORD_1 dst_unused:UNUSED_PRESERVE src0_sel:WORD_1
	v_pk_add_f16 v10, v10, v18
	v_pk_add_f16 v11, v11, v19
	v_pk_add_f16 v12, v12, v20
	v_pk_add_f16 v13, v13, v21
	v_pk_fma_f16 v14, v78, v18, v6
	v_pk_fma_f16 v15, v79, v19, v7
	v_pk_fma_f16 v16, v80, v20, v8
	v_pk_fma_f16 v17, v81, v21, v9
	v_pk_add_f16 v6, v46, v74 neg_lo:[0,1] neg_hi:[0,1]
	v_pk_add_f16 v7, v47, v75 neg_lo:[0,1] neg_hi:[0,1]
	v_pk_add_f16 v8, v48, v76 neg_lo:[0,1] neg_hi:[0,1]
	v_pk_add_f16 v9, v49, v77 neg_lo:[0,1] neg_hi:[0,1]
	v_exp_f16_sdwa v18, v6 dst_sel:WORD_0 dst_unused:UNUSED_PAD src0_sel:WORD_0
	v_exp_f16_sdwa v19, v7 dst_sel:WORD_0 dst_unused:UNUSED_PAD src0_sel:WORD_0
	v_exp_f16_sdwa v20, v8 dst_sel:WORD_0 dst_unused:UNUSED_PAD src0_sel:WORD_0
	v_exp_f16_sdwa v21, v9 dst_sel:WORD_0 dst_unused:UNUSED_PAD src0_sel:WORD_0
	v_exp_f16_sdwa v18, v6 dst_sel:WORD_1 dst_unused:UNUSED_PRESERVE src0_sel:WORD_1
	v_exp_f16_sdwa v19, v7 dst_sel:WORD_1 dst_unused:UNUSED_PRESERVE src0_sel:WORD_1
	v_exp_f16_sdwa v20, v8 dst_sel:WORD_1 dst_unused:UNUSED_PRESERVE src0_sel:WORD_1
	v_exp_f16_sdwa v21, v9 dst_sel:WORD_1 dst_unused:UNUSED_PRESERVE src0_sel:WORD_1
	s_nop 0
	v_pk_add_f16 v9, v13, v21
	v_pk_add_f16 v8, v12, v20
	v_pk_add_f16 v7, v11, v19
	v_pk_add_f16 v6, v10, v18
	v_pk_fma_f16 v13, v93, v21, v17
	v_pk_fma_f16 v12, v92, v20, v16
	v_pk_fma_f16 v11, v91, v19, v15
	v_pk_fma_f16 v10, v90, v18, v14
	v_pk_add_f16 v18, v50, v74 neg_lo:[0,1] neg_hi:[0,1]
	v_pk_add_f16 v19, v51, v75 neg_lo:[0,1] neg_hi:[0,1]
	v_pk_add_f16 v20, v52, v76 neg_lo:[0,1] neg_hi:[0,1]
	v_pk_add_f16 v21, v53, v77 neg_lo:[0,1] neg_hi:[0,1]
	v_exp_f16_sdwa v14, v18 dst_sel:WORD_0 dst_unused:UNUSED_PAD src0_sel:WORD_0
	v_exp_f16_sdwa v17, v19 dst_sel:WORD_0 dst_unused:UNUSED_PAD src0_sel:WORD_0
	v_exp_f16_sdwa v15, v20 dst_sel:WORD_0 dst_unused:UNUSED_PAD src0_sel:WORD_0
	v_exp_f16_sdwa v16, v21 dst_sel:WORD_0 dst_unused:UNUSED_PAD src0_sel:WORD_0
	v_exp_f16_sdwa v14, v18 dst_sel:WORD_1 dst_unused:UNUSED_PRESERVE src0_sel:WORD_1
	v_exp_f16_sdwa v17, v19 dst_sel:WORD_1 dst_unused:UNUSED_PRESERVE src0_sel:WORD_1
	v_exp_f16_sdwa v15, v20 dst_sel:WORD_1 dst_unused:UNUSED_PRESERVE src0_sel:WORD_1
	v_exp_f16_sdwa v16, v21 dst_sel:WORD_1 dst_unused:UNUSED_PRESERVE src0_sel:WORD_1
	s_nop 0
.LBB5_42:
	s_and_b64 vcc, exec, s[4:5]
	s_cbranch_vccz .LBB5_3
	s_load_dwordx2 s[0:1], s[22:23], 0x18
	s_waitcnt lgkmcnt(0)
	s_load_dwordx2 s[6:7], s[0:1], 0x0
	s_load_dword s28, s[0:1], 0x8
	v_cmp_lt_u32_e64 s[64:65], 0, v182
	v_cmp_gt_u32_e64 s[66:67], 63, v182
	v_cmp_lt_u32_e64 s[68:69], 0, v162
	v_cmp_gt_u32_e64 s[70:71], 60, v162
	buffer_load_dwordx4 v[184:187], v180, s[16:19], 0 offen
	s_and_b64 s[72:73], s[68:69], s[64:65]
	s_and_b64 s[74:75], s[68:69], s[66:67]
	s_and_b64 s[76:77], s[70:71], s[64:65]
	s_and_b64 s[78:79], s[70:71], s[66:67]
	v_add_u32_e32 v224, 0xfffe7c00, v180
	v_add_u32_e32 v225, 0xfffe8000, v180
	s_mov_b64 exec, s[72:73]
	buffer_load_dwordx4 v[110:113], v224, s[16:19], 0 offen
	s_mov_b64 exec, -1
	s_mov_b64 exec, s[68:69]
	buffer_load_dwordx4 v[126:129], v225, s[16:19], 0 offen offset:512
	s_mov_b64 exec, -1
	s_mov_b64 exec, s[74:75]
	buffer_load_dwordx4 v[134:137], v225, s[16:19], 0 offen offset:2048
	s_mov_b64 exec, -1
	v_add_u32_e32 v224, 0xfffffc00, v180
	s_mov_b64 exec, s[64:65]
	buffer_load_dwordx4 v[82:85], v224, s[16:19], 0 offen
	s_mov_b64 exec, -1
	buffer_load_dwordx4 v[106:109], v180, s[16:19], 0 offen offset:512
	s_mov_b64 exec, s[66:67]
	buffer_load_dwordx4 v[122:125], v180, s[16:19], 0 offen offset:2048
	s_mov_b64 exec, -1
	v_add_u32_e32 v224, 0x17c00, v180
	v_add_u32_e32 v225, 0x18000, v180
	s_mov_b64 exec, s[64:65]
	buffer_load_dwordx4 v[50:53], v224, s[16:19], 0 offen
	s_mov_b64 exec, -1
	buffer_load_dwordx4 v[66:69], v225, s[16:19], 0 offen offset:512
	s_mov_b64 exec, s[66:67]
	buffer_load_dwordx4 v[94:97], v225, s[16:19], 0 offen offset:2048
	s_mov_b64 exec, -1
	v_add_u32_e32 v224, 0xfffe7c00, v180
	v_add_u32_e32 v225, 0xfffe8000, v180
	s_mov_b64 exec, s[72:73]
	buffer_load_dwordx4 v[78:81], v224, s[16:19], 0 offen offset:512
	s_mov_b64 exec, -1
	s_mov_b64 exec, s[68:69]
	buffer_load_dwordx4 v[102:105], v225, s[16:19], 0 offen offset:1024
	s_mov_b64 exec, -1
	s_mov_b64 exec, s[74:75]
	buffer_load_dwordx4 v[114:117], v225, s[16:19], 0 offen offset:2560
	s_mov_b64 exec, -1
	v_add_u32_e32 v224, 0xfffffc00, v180
	s_mov_b64 exec, s[64:65]
	buffer_load_dwordx4 v[42:45], v224, s[16:19], 0 offen offset:512
	s_mov_b64 exec, -1
	buffer_load_dwordx4 v[62:65], v180, s[16:19], 0 offen offset:1024
	s_mov_b64 exec, s[66:67]
	buffer_load_dwordx4 v[86:89], v180, s[16:19], 0 offen offset:2560
	s_mov_b64 exec, -1
	v_add_u32_e32 v224, 0x17c00, v180
	v_add_u32_e32 v225, 0x18000, v180
	s_mov_b64 exec, s[64:65]
	buffer_load_dwordx4 v[22:25], v224, s[16:19], 0 offen offset:512
	s_mov_b64 exec, -1
	buffer_load_dwordx4 v[34:37], v225, s[16:19], 0 offen offset:1024
	s_mov_b64 exec, s[66:67]
	buffer_load_dwordx4 v[46:49], v225, s[16:19], 0 offen offset:2560
	s_mov_b64 exec, -1
	v_add_u32_e32 v224, 0x18000, v180
	buffer_load_dwordx4 v[154:157], v224, s[16:19], 0 offen
	v_add_u32_e32 v225, 0x30000, v180
	buffer_load_dwordx4 v[150:153], v225, s[16:19], 0 offen
	v_add_u32_e32 v224, 0x48000, v180
	buffer_load_dwordx4 v[146:149], v224, s[16:19], 0 offen
	v_add_u32_e32 v224, 0x2fc00, v180
	v_add_u32_e32 v225, 0x30000, v180
	v_add_u32_e32 v226, 0x47c00, v180
	v_add_u32_e32 v227, 0x48000, v180
	v_add_u32_e32 v228, 0x5fc00, v180
	v_add_u32_e32 v229, 0x60000, v180
	s_cmp_lg_u32 s93, 0
	s_cbranch_scc1 .Lmybg_D2
	s_waitcnt vmcnt(22)
	v_cvt_pk_f16_f32 v172, v230, v231
	v_cvt_pk_f16_f32 v173, v234, v235
	v_cvt_pk_f16_f32 v174, v232, v233
	v_cvt_pk_f16_f32 v175, v236, v237
	v_cvt_pk_f16_f32 v176, v238, v239
	v_cvt_pk_f16_f32 v177, v242, v243
	v_cvt_pk_f16_f32 v178, v240, v241
	v_cvt_pk_f16_f32 v179, v244, v245
	s_mov_b32 s93, 1

_Z7k_attn2ILi2EEv8AttnArgs:
	v_readfirstlane_b32 s3, v0
	s_lshl_b32 s12, s3, 1
	v_lshlrev_b32_e32 v3, 3, v0
	s_and_b32 s12, s12, 0x80
	v_and_b32_e32 v3, 0x78, v3
	s_load_dwordx4 s[8:11], s[0:1], 0x0
	s_load_dwordx2 s[4:5], s[0:1], 0x10
	s_load_dwordx2 s[6:7], s[0:1], 0x50
	v_or_b32_e32 v180, s12, v3
	s_lshl_b32 s12, s2, 5
	v_lshrrev_b32_e32 v1, 5, v0
	v_bfe_u32 v2, v0, 4, 2
	s_and_b32 s14, s12, 0xe0
	s_lshr_b32 s12, s2, 3
	v_lshrrev_b32_e32 v0, 6, v0
	v_and_b32_e32 v1, 4, v1
	s_add_i32 s14, s14, s12
	s_and_b32 s2, s2, 56
	v_and_b32_e32 v0, 4, v0
	v_and_or_b32 v181, s14, 56, v0
	v_or3_b32 v182, v2, s2, v1
	s_and_b32 s2, s14, 0x3ffffc0
	v_or_b32_e32 v4, s2, v181
	v_lshlrev_b32_e32 v0, 1, v180
	v_mov_b32_e32 v1, 0
	s_waitcnt lgkmcnt(0)
	v_lshl_add_u64 v[2:3], s[6:7], 0, v[0:1]
	v_lshl_or_b32 v0, v4, 6, v182
	v_lshlrev_b64 v[4:5], 9, v[0:1]
	v_lshl_add_u64 v[8:9], v[2:3], 0, v[4:5]
	v_or_b32_e32 v4, 64, v0
	v_mov_b32_e32 v5, v1
	v_lshlrev_b64 v[4:5], 9, v[4:5]
	v_lshlrev_b32_e32 v20, 2, v180
	v_lshl_add_u64 v[10:11], v[2:3], 0, v[4:5]
	global_load_dwordx4 v[240:243], v20, s[10:11] offset:16
	global_load_dwordx4 v[236:239], v20, s[10:11]
	global_load_dwordx4 v[248:251], v20, s[4:5] offset:16
	global_load_dwordx4 v[244:247], v20, s[4:5]
	global_load_dwordx4 v[12:15], v[8:9], off nt
	global_load_dwordx4 v[4:7], v[10:11], off nt
	v_or_b32_e32 v8, 0x80, v0
	v_mov_b32_e32 v9, v1
	v_lshlrev_b64 v[8:9], 9, v[8:9]
	v_or_b32_e32 v0, 0xc0, v0
	v_lshl_add_u64 v[20:21], v[2:3], 0, v[8:9]
	v_lshlrev_b64 v[0:1], 9, v[0:1]
	v_lshl_add_u64 v[34:35], v[2:3], 0, v[0:1]
	global_load_dwordx4 v[8:11], v[20:21], off nt
	global_load_dwordx4 v[0:3], v[34:35], off nt
	s_bitcmp1_b32 s3, 6
	s_cselect_b64 s[4:5], -1, 0
	s_and_b32 s2, s14, 0x3ffc0
	v_or_b32_e32 v20, s2, v181
	v_lshl_or_b32 v20, v20, 6, v182
	v_add_u32_e32 v184, -1, v182
	v_add_u32_e32 v185, -1, v181
	v_mul_u32_u24_e32 v20, 0x300, v20
	v_or_b32_e32 v34, v185, v184
	v_or_b32_e32 v20, v180, v20
	s_mov_b32 s11, 0x20000
	s_mov_b32 s10, 0x1800000
	s_and_b32 s9, s9, 0xffff
	v_lshlrev_b32_e32 v183, 1, v20
	v_cmp_gt_u32_e64 s[2:3], 64, v34
	s_and_b64 vcc, exec, s[4:5]
	s_cbranch_vccz .LBB6_38
	s_load_dwordx2 s[12:13], s[0:1], 0x20
	s_waitcnt lgkmcnt(0)
	s_load_dwordx2 s[4:5], s[12:13], 0x0
	s_load_dword s12, s[12:13], 0x8
	v_cmp_lt_u32_e64 s[64:65], 0, v182
	v_cmp_gt_u32_e64 s[66:67], 63, v182
	v_cmp_lt_u32_e64 s[68:69], 0, v181
	v_cmp_gt_u32_e64 s[70:71], 60, v181
	buffer_load_dwordx4 v[190:193], v183, s[8:11], 0 offen
	s_and_b64 s[72:73], s[68:69], s[64:65]
	s_and_b64 s[74:75], s[68:69], s[66:67]
	s_and_b64 s[76:77], s[70:71], s[64:65]
	s_and_b64 s[78:79], s[70:71], s[66:67]
	v_add_u32_e32 v228, 0xfffe7c00, v183
	v_add_u32_e32 v229, 0xfffe8000, v183
	s_mov_b64 exec, s[72:73]
	buffer_load_dwordx4 v[136:139], v228, s[8:11], 0 offen
	s_mov_b64 exec, -1
	s_mov_b64 exec, s[68:69]
	buffer_load_dwordx4 v[152:155], v229, s[8:11], 0 offen offset:512
	s_mov_b64 exec, -1
	s_mov_b64 exec, s[74:75]
	buffer_load_dwordx4 v[160:163], v229, s[8:11], 0 offen offset:2048
	s_mov_b64 exec, -1
	v_add_u32_e32 v228, 0xfffffc00, v183
	s_mov_b64 exec, s[64:65]
	buffer_load_dwordx4 v[112:115], v228, s[8:11], 0 offen
	s_mov_b64 exec, -1
	buffer_load_dwordx4 v[132:135], v183, s[8:11], 0 offen offset:512
	s_mov_b64 exec, s[66:67]
	buffer_load_dwordx4 v[148:151], v183, s[8:11], 0 offen offset:2048
	s_mov_b64 exec, -1
	v_add_u32_e32 v228, 0x17c00, v183
	v_add_u32_e32 v229, 0x18000, v183
	s_mov_b64 exec, s[64:65]
	buffer_load_dwordx4 v[76:79], v228, s[8:11], 0 offen
	s_mov_b64 exec, -1
	buffer_load_dwordx4 v[92:95], v229, s[8:11], 0 offen offset:512
	s_mov_b64 exec, s[66:67]
	buffer_load_dwordx4 v[116:119], v229, s[8:11], 0 offen offset:2048
	s_mov_b64 exec, -1
	v_add_u32_e32 v228, 0xfffe7c00, v183
	v_add_u32_e32 v229, 0xfffe8000, v183
	s_mov_b64 exec, s[72:73]
	buffer_load_dwordx4 v[96:99], v228, s[8:11], 0 offen offset:512
	s_mov_b64 exec, -1
	s_mov_b64 exec, s[68:69]
	buffer_load_dwordx4 v[124:127], v229, s[8:11], 0 offen offset:1024
	s_mov_b64 exec, -1
	s_mov_b64 exec, s[74:75]
	buffer_load_dwordx4 v[140:143], v229, s[8:11], 0 offen offset:2560
	s_mov_b64 exec, -1
	v_add_u32_e32 v228, 0xfffffc00, v183
	s_mov_b64 exec, s[64:65]
	buffer_load_dwordx4 v[68:71], v228, s[8:11], 0 offen offset:512
	s_mov_b64 exec, -1
	buffer_load_dwordx4 v[88:91], v183, s[8:11], 0 offen offset:1024
	s_mov_b64 exec, s[66:67]
	buffer_load_dwordx4 v[108:111], v183, s[8:11], 0 offen offset:2560
	s_mov_b64 exec, -1
	v_add_u32_e32 v228, 0x17c00, v183
	v_add_u32_e32 v229, 0x18000, v183
	s_mov_b64 exec, s[64:65]
	buffer_load_dwordx4 v[48:51], v228, s[8:11], 0 offen offset:512
	s_mov_b64 exec, -1
	buffer_load_dwordx4 v[56:59], v229, s[8:11], 0 offen offset:1024
	s_mov_b64 exec, s[66:67]
	buffer_load_dwordx4 v[72:75], v229, s[8:11], 0 offen offset:2560
	s_mov_b64 exec, -1
	v_add_u32_e32 v228, 0x18000, v183
	buffer_load_dwordx4 v[176:179], v228, s[8:11], 0 offen
	v_add_u32_e32 v229, 0x30000, v183
	buffer_load_dwordx4 v[172:175], v229, s[8:11], 0 offen
	v_add_u32_e32 v228, 0x48000, v183
	buffer_load_dwordx4 v[168:171], v228, s[8:11], 0 offen
	v_add_u32_e32 v228, 0x2fc00, v183
	v_add_u32_e32 v229, 0x30000, v183
	v_add_u32_e32 v230, 0x47c00, v183
	v_add_u32_e32 v231, 0x48000, v183
	v_add_u32_e32 v232, 0x5fc00, v183
	v_add_u32_e32 v233, 0x60000, v183
	s_waitcnt vmcnt(26)
	v_cvt_pk_f16_f32 v22, v240, v241
	v_cvt_pk_f16_f32 v20, v236, v237
	v_cvt_pk_f16_f32 v21, v238, v239
	v_cvt_pk_f16_f32 v16, v244, v245
	v_cvt_pk_f16_f32 v17, v246, v247
	v_cvt_pk_f16_f32 v18, v248, v249
	v_cvt_pk_f16_f32 v23, v242, v243
	v_cvt_pk_f16_f32 v19, v250, v251
	s_not_b64 exec, s[72:73]
	s_cbranch_execz .Lmyf_E1_0
	v_mov_b32_e32 v136, v20
	v_mov_b32_e32 v137, v21
	v_mov_b32_e32 v138, v22
	v_mov_b32_e32 v139, v23
	v_mov_b32_e32 v96, v16
	v_mov_b32_e32 v97, v17
	v_mov_b32_e32 v98, v18
	v_mov_b32_e32 v99, v19

.Lmyf_E1_7:
	s_mov_b64 exec, -1
	s_waitcnt lgkmcnt(0)
	v_cvt_f16_f32_e32 v186, s5
	v_cvt_f16_f32_e32 v188, s4
	v_cvt_f16_f32_e32 v187, s12
	s_waitcnt vmcnt(12)
	v_pk_mul_f16 v196, v188, v193 op_sel_hi:[0,1]
	v_pk_mul_f16 v200, v186, v193 op_sel_hi:[0,1]
	v_pk_mul_f16 v204, v187, v193 op_sel_hi:[0,1]
	v_pk_mul_f16 v189, v188, v190 op_sel_hi:[0,1]
	v_pk_mul_f16 v194, v188, v191 op_sel_hi:[0,1]
	v_pk_mul_f16 v195, v188, v192 op_sel_hi:[0,1]
	v_pk_mul_f16 v197, v186, v190 op_sel_hi:[0,1]
	v_pk_mul_f16 v198, v186, v191 op_sel_hi:[0,1]
	v_pk_mul_f16 v199, v186, v192 op_sel_hi:[0,1]
	v_pk_mul_f16 v201, v187, v190 op_sel_hi:[0,1]
	v_pk_mul_f16 v202, v187, v191 op_sel_hi:[0,1]
	v_pk_mul_f16 v203, v187, v192 op_sel_hi:[0,1]
	v_pk_fma_f16 v139, v139, v193, v196
	v_pk_fma_f16 v155, v155, v193, v200
	v_pk_fma_f16 v163, v163, v193, v204
	v_pk_fma_f16 v205, v115, v193, v196
	v_pk_fma_f16 v209, v135, v193, v200
	v_pk_fma_f16 v213, v151, v193, v204
	v_pk_fma_f16 v196, v79, v193, v196
	v_pk_fma_f16 v200, v95, v193, v200
	v_pk_fma_f16 v193, v119, v193, v204
	v_pk_maximum3_f16 v204, v139, v155, v163
	v_pk_fma_f16 v138, v138, v192, v195
	v_pk_fma_f16 v137, v137, v191, v194
	v_pk_fma_f16 v136, v136, v190, v189
	v_pk_fma_f16 v154, v154, v192, v199
	v_pk_fma_f16 v153, v153, v191, v198
	v_pk_fma_f16 v152, v152, v190, v197
	v_pk_fma_f16 v162, v162, v192, v203
	v_pk_fma_f16 v161, v161, v191, v202
	v_pk_fma_f16 v160, v160, v190, v201
	v_pk_fma_f16 v206, v114, v192, v195
	v_pk_fma_f16 v207, v113, v191, v194
	v_pk_fma_f16 v208, v112, v190, v189
	v_pk_fma_f16 v210, v134, v192, v199
	v_pk_fma_f16 v211, v133, v191, v198
	v_pk_fma_f16 v212, v132, v190, v197
	v_pk_fma_f16 v214, v150, v192, v203
	v_pk_fma_f16 v215, v149, v191, v202
	v_pk_fma_f16 v216, v148, v190, v201
	v_pk_fma_f16 v195, v78, v192, v195
	v_pk_fma_f16 v194, v77, v191, v194
	v_pk_fma_f16 v189, v76, v190, v189
	v_pk_fma_f16 v199, v94, v192, v199
	v_pk_fma_f16 v198, v93, v191, v198
	v_pk_fma_f16 v197, v92, v190, v197
	v_pk_fma_f16 v192, v118, v192, v203
	v_pk_fma_f16 v191, v117, v191, v202
	v_pk_fma_f16 v190, v116, v190, v201
	v_pk_maximum3_f16 v201, v136, v152, v160
	v_pk_maximum3_f16 v202, v137, v153, v161
	v_pk_maximum3_f16 v203, v138, v154, v162
	v_pk_maximum3_f16 v220, v205, v209, v213
	v_pk_maximum3_f16 v224, v196, v200, v193
	v_pk_maximum3_f16 v217, v208, v212, v216
	v_pk_maximum3_f16 v218, v207, v211, v215
	v_pk_maximum3_f16 v219, v206, v210, v214
	v_pk_maximum3_f16 v221, v189, v197, v190
	v_pk_maximum3_f16 v222, v194, v198, v191
	v_pk_maximum3_f16 v204, v204, v220, v224
	v_pk_maximum3_f16 v223, v195, v199, v192
	v_pk_maximum3_f16 v201, v201, v217, v221
	v_pk_maximum3_f16 v202, v202, v218, v222
	v_pk_maximum3_f16 v203, v203, v219, v223
	v_pk_add_f16 v139, v139, v204 neg_lo:[0,1] neg_hi:[0,1]
	v_pk_add_f16 v136, v136, v201 neg_lo:[0,1] neg_hi:[0,1]
	v_pk_add_f16 v137, v137, v202 neg_lo:[0,1] neg_hi:[0,1]
	v_pk_add_f16 v138, v138, v203 neg_lo:[0,1] neg_hi:[0,1]
	v_pk_add_f16 v152, v152, v201 neg_lo:[0,1] neg_hi:[0,1]
	v_exp_f16_sdwa v217, v136 dst_sel:WORD_0 dst_unused:UNUSED_PAD src0_sel:WORD_0
	v_exp_f16_sdwa v218, v137 dst_sel:WORD_0 dst_unused:UNUSED_PAD src0_sel:WORD_0
	v_exp_f16_sdwa v219, v138 dst_sel:WORD_0 dst_unused:UNUSED_PAD src0_sel:WORD_0
	v_exp_f16_sdwa v220, v139 dst_sel:WORD_0 dst_unused:UNUSED_PAD src0_sel:WORD_0
	v_exp_f16_sdwa v217, v136 dst_sel:WORD_1 dst_unused:UNUSED_PRESERVE src0_sel:WORD_1
	v_exp_f16_sdwa v218, v137 dst_sel:WORD_1 dst_unused:UNUSED_PRESERVE src0_sel:WORD_1
	v_exp_f16_sdwa v219, v138 dst_sel:WORD_1 dst_unused:UNUSED_PRESERVE src0_sel:WORD_1
	v_exp_f16_sdwa v220, v139 dst_sel:WORD_1 dst_unused:UNUSED_PRESERVE src0_sel:WORD_1
	v_pk_add_f16 v153, v153, v202 neg_lo:[0,1] neg_hi:[0,1]
	v_pk_add_f16 v139, v217, 0
	s_waitcnt vmcnt(3)
	v_pk_fma_f16 v99, v99, v220, 0
	v_pk_add_f16 v136, v220, 0
	v_pk_add_f16 v137, v219, 0
	v_pk_add_f16 v138, v218, 0
	v_pk_fma_f16 v98, v98, v219, 0
	v_pk_fma_f16 v97, v97, v218, 0
	s_mov_b64 exec, s[64:65]
	buffer_load_dwordx4 v[44:47], v228, s[8:11], 0 offen
	buffer_load_dwordx4 v[32:35], v228, s[8:11], 0 offen offset:512
	s_mov_b64 exec, -1
	v_pk_fma_f16 v96, v96, v217, 0
	v_pk_add_f16 v154, v154, v203 neg_lo:[0,1] neg_hi:[0,1]
	v_pk_add_f16 v155, v155, v204 neg_lo:[0,1] neg_hi:[0,1]
	v_exp_f16_sdwa v217, v152 dst_sel:WORD_0 dst_unused:UNUSED_PAD src0_sel:WORD_0
	v_exp_f16_sdwa v218, v153 dst_sel:WORD_0 dst_unused:UNUSED_PAD src0_sel:WORD_0
	v_exp_f16_sdwa v219, v154 dst_sel:WORD_0 dst_unused:UNUSED_PAD src0_sel:WORD_0
	v_exp_f16_sdwa v220, v155 dst_sel:WORD_0 dst_unused:UNUSED_PAD src0_sel:WORD_0
	v_exp_f16_sdwa v217, v152 dst_sel:WORD_1 dst_unused:UNUSED_PRESERVE src0_sel:WORD_1
	v_exp_f16_sdwa v218, v153 dst_sel:WORD_1 dst_unused:UNUSED_PRESERVE src0_sel:WORD_1
	v_exp_f16_sdwa v219, v154 dst_sel:WORD_1 dst_unused:UNUSED_PRESERVE src0_sel:WORD_1
	v_exp_f16_sdwa v220, v155 dst_sel:WORD_1 dst_unused:UNUSED_PRESERVE src0_sel:WORD_1
	v_pk_add_f16 v139, v139, v217
	v_pk_fma_f16 v99, v127, v220, v99
	v_pk_add_f16 v127, v163, v204 neg_lo:[0,1] neg_hi:[0,1]
	v_pk_add_f16 v138, v138, v218
	v_pk_add_f16 v137, v137, v219
	v_pk_add_f16 v136, v136, v220
	buffer_load_dwordx4 v[60:63], v229, s[8:11], 0 offen offset:512
	buffer_load_dwordx4 v[36:39], v229, s[8:11], 0 offen offset:1024
	v_pk_fma_f16 v96, v124, v217, v96
	v_pk_fma_f16 v97, v125, v218, v97
	v_pk_fma_f16 v98, v126, v219, v98
	v_pk_add_f16 v124, v160, v201 neg_lo:[0,1] neg_hi:[0,1]
	v_pk_add_f16 v125, v161, v202 neg_lo:[0,1] neg_hi:[0,1]
	v_pk_add_f16 v126, v162, v203 neg_lo:[0,1] neg_hi:[0,1]
	v_exp_f16_sdwa v152, v124 dst_sel:WORD_0 dst_unused:UNUSED_PAD src0_sel:WORD_0
	v_exp_f16_sdwa v153, v125 dst_sel:WORD_0 dst_unused:UNUSED_PAD src0_sel:WORD_0
	v_exp_f16_sdwa v154, v126 dst_sel:WORD_0 dst_unused:UNUSED_PAD src0_sel:WORD_0
	v_exp_f16_sdwa v155, v127 dst_sel:WORD_0 dst_unused:UNUSED_PAD src0_sel:WORD_0
	v_exp_f16_sdwa v152, v124 dst_sel:WORD_1 dst_unused:UNUSED_PRESERVE src0_sel:WORD_1
	v_exp_f16_sdwa v153, v125 dst_sel:WORD_1 dst_unused:UNUSED_PRESERVE src0_sel:WORD_1
	v_exp_f16_sdwa v154, v126 dst_sel:WORD_1 dst_unused:UNUSED_PRESERVE src0_sel:WORD_1
	v_exp_f16_sdwa v155, v127 dst_sel:WORD_1 dst_unused:UNUSED_PRESERVE src0_sel:WORD_1
	v_pk_add_f16 v127, v139, v152
	v_pk_add_f16 v124, v136, v155
	v_pk_add_f16 v125, v137, v154
	s_mov_b64 exec, s[66:67]
	buffer_load_dwordx4 v[80:83], v229, s[8:11], 0 offen offset:2048
	buffer_load_dwordx4 v[40:43], v229, s[8:11], 0 offen offset:2560
	s_mov_b64 exec, -1
	v_pk_add_f16 v126, v138, v153
	v_pk_fma_f16 v99, v143, v155, v99
	v_pk_fma_f16 v98, v142, v154, v98
	v_pk_fma_f16 v97, v141, v153, v97
	v_pk_fma_f16 v96, v140, v152, v96
	v_pk_add_f16 v136, v208, v201 neg_lo:[0,1] neg_hi:[0,1]
	v_pk_add_f16 v137, v207, v202 neg_lo:[0,1] neg_hi:[0,1]
	v_pk_add_f16 v138, v206, v203 neg_lo:[0,1] neg_hi:[0,1]
	s_mov_b64 exec, s[64:65]
	buffer_load_dwordx4 v[100:103], v230, s[8:11], 0 offen
	buffer_load_dwordx4 v[52:55], v230, s[8:11], 0 offen offset:512
	s_mov_b64 exec, -1
	v_pk_add_f16 v139, v205, v204 neg_lo:[0,1] neg_hi:[0,1]
	v_exp_f16_sdwa v140, v136 dst_sel:WORD_0 dst_unused:UNUSED_PAD src0_sel:WORD_0
	v_exp_f16_sdwa v141, v137 dst_sel:WORD_0 dst_unused:UNUSED_PAD src0_sel:WORD_0
	v_exp_f16_sdwa v142, v138 dst_sel:WORD_0 dst_unused:UNUSED_PAD src0_sel:WORD_0
	v_exp_f16_sdwa v143, v139 dst_sel:WORD_0 dst_unused:UNUSED_PAD src0_sel:WORD_0
	v_exp_f16_sdwa v140, v136 dst_sel:WORD_1 dst_unused:UNUSED_PRESERVE src0_sel:WORD_1
	v_exp_f16_sdwa v141, v137 dst_sel:WORD_1 dst_unused:UNUSED_PRESERVE src0_sel:WORD_1
	v_exp_f16_sdwa v142, v138 dst_sel:WORD_1 dst_unused:UNUSED_PRESERVE src0_sel:WORD_1
	v_exp_f16_sdwa v143, v139 dst_sel:WORD_1 dst_unused:UNUSED_PRESERVE src0_sel:WORD_1
	v_pk_add_f16 v136, v212, v201 neg_lo:[0,1] neg_hi:[0,1]
	v_pk_add_f16 v127, v127, v140
	v_pk_add_f16 v126, v126, v141
	v_pk_add_f16 v125, v125, v142
	v_pk_add_f16 v124, v124, v143
	v_pk_fma_f16 v96, v68, v140, v96
	v_pk_fma_f16 v97, v69, v141, v97
	v_pk_fma_f16 v98, v70, v142, v98
	v_pk_fma_f16 v99, v71, v143, v99
	buffer_load_dwordx4 v[128:131], v231, s[8:11], 0 offen offset:512
	buffer_load_dwordx4 v[64:67], v231, s[8:11], 0 offen offset:1024
	v_pk_add_f16 v137, v211, v202 neg_lo:[0,1] neg_hi:[0,1]
	v_pk_add_f16 v138, v210, v203 neg_lo:[0,1] neg_hi:[0,1]
	v_pk_add_f16 v139, v209, v204 neg_lo:[0,1] neg_hi:[0,1]
	v_exp_f16_sdwa v140, v136 dst_sel:WORD_0 dst_unused:UNUSED_PAD src0_sel:WORD_0
	v_exp_f16_sdwa v141, v137 dst_sel:WORD_0 dst_unused:UNUSED_PAD src0_sel:WORD_0
	v_exp_f16_sdwa v142, v138 dst_sel:WORD_0 dst_unused:UNUSED_PAD src0_sel:WORD_0
	v_exp_f16_sdwa v143, v139 dst_sel:WORD_0 dst_unused:UNUSED_PAD src0_sel:WORD_0
	v_exp_f16_sdwa v140, v136 dst_sel:WORD_1 dst_unused:UNUSED_PRESERVE src0_sel:WORD_1
	v_exp_f16_sdwa v141, v137 dst_sel:WORD_1 dst_unused:UNUSED_PRESERVE src0_sel:WORD_1
	v_exp_f16_sdwa v142, v138 dst_sel:WORD_1 dst_unused:UNUSED_PRESERVE src0_sel:WORD_1
	v_exp_f16_sdwa v143, v139 dst_sel:WORD_1 dst_unused:UNUSED_PRESERVE src0_sel:WORD_1
	v_pk_add_f16 v136, v216, v201 neg_lo:[0,1] neg_hi:[0,1]
	v_pk_add_f16 v127, v127, v140
	v_pk_add_f16 v124, v124, v143
	v_pk_add_f16 v125, v125, v142
	v_pk_add_f16 v126, v126, v141
	v_pk_fma_f16 v99, v91, v143, v99
	s_mov_b64 exec, s[66:67]
	buffer_load_dwordx4 v[144:147], v231, s[8:11], 0 offen offset:2048
	buffer_load_dwordx4 v[84:87], v231, s[8:11], 0 offen offset:2560
	s_mov_b64 exec, -1
	v_pk_fma_f16 v98, v90, v142, v98
	v_pk_fma_f16 v97, v89, v141, v97
	v_pk_fma_f16 v96, v88, v140, v96
	v_pk_add_f16 v137, v215, v202 neg_lo:[0,1] neg_hi:[0,1]
	v_pk_add_f16 v138, v214, v203 neg_lo:[0,1] neg_hi:[0,1]
	v_pk_add_f16 v139, v213, v204 neg_lo:[0,1] neg_hi:[0,1]
	v_exp_f16_sdwa v140, v136 dst_sel:WORD_0 dst_unused:UNUSED_PAD src0_sel:WORD_0
	v_exp_f16_sdwa v141, v137 dst_sel:WORD_0 dst_unused:UNUSED_PAD src0_sel:WORD_0
	v_exp_f16_sdwa v142, v138 dst_sel:WORD_0 dst_unused:UNUSED_PAD src0_sel:WORD_0
	v_exp_f16_sdwa v143, v139 dst_sel:WORD_0 dst_unused:UNUSED_PAD src0_sel:WORD_0
	v_exp_f16_sdwa v140, v136 dst_sel:WORD_1 dst_unused:UNUSED_PRESERVE src0_sel:WORD_1
	v_exp_f16_sdwa v141, v137 dst_sel:WORD_1 dst_unused:UNUSED_PRESERVE src0_sel:WORD_1
	v_exp_f16_sdwa v142, v138 dst_sel:WORD_1 dst_unused:UNUSED_PRESERVE src0_sel:WORD_1
	v_exp_f16_sdwa v143, v139 dst_sel:WORD_1 dst_unused:UNUSED_PRESERVE src0_sel:WORD_1
	v_pk_add_f16 v136, v189, v201 neg_lo:[0,1] neg_hi:[0,1]
	v_pk_add_f16 v127, v127, v140
	v_pk_add_f16 v126, v126, v141
	s_mov_b64 exec, s[76:77]
	buffer_load_dwordx4 v[156:159], v232, s[8:11], 0 offen
	buffer_load_dwordx4 v[104:107], v232, s[8:11], 0 offen offset:512
	s_mov_b64 exec, -1
	v_pk_add_f16 v125, v125, v142
	v_pk_add_f16 v124, v124, v143
	v_pk_fma_f16 v96, v108, v140, v96
	v_pk_fma_f16 v97, v109, v141, v97
	v_pk_fma_f16 v98, v110, v142, v98
	v_pk_fma_f16 v99, v111, v143, v99
	v_pk_add_f16 v137, v194, v202 neg_lo:[0,1] neg_hi:[0,1]
	v_pk_add_f16 v138, v195, v203 neg_lo:[0,1] neg_hi:[0,1]
	s_mov_b64 exec, s[70:71]
	buffer_load_dwordx4 v[164:167], v233, s[8:11], 0 offen offset:512
	buffer_load_dwordx4 v[120:123], v233, s[8:11], 0 offen offset:1024
	s_mov_b64 exec, -1
	v_pk_add_f16 v139, v196, v204 neg_lo:[0,1] neg_hi:[0,1]
	v_exp_f16_sdwa v140, v136 dst_sel:WORD_0 dst_unused:UNUSED_PAD src0_sel:WORD_0
	v_exp_f16_sdwa v141, v137 dst_sel:WORD_0 dst_unused:UNUSED_PAD src0_sel:WORD_0
	v_exp_f16_sdwa v142, v138 dst_sel:WORD_0 dst_unused:UNUSED_PAD src0_sel:WORD_0
	v_exp_f16_sdwa v143, v139 dst_sel:WORD_0 dst_unused:UNUSED_PAD src0_sel:WORD_0
	v_exp_f16_sdwa v140, v136 dst_sel:WORD_1 dst_unused:UNUSED_PRESERVE src0_sel:WORD_1
	v_exp_f16_sdwa v141, v137 dst_sel:WORD_1 dst_unused:UNUSED_PRESERVE src0_sel:WORD_1
	v_exp_f16_sdwa v142, v138 dst_sel:WORD_1 dst_unused:UNUSED_PRESERVE src0_sel:WORD_1
	v_exp_f16_sdwa v143, v139 dst_sel:WORD_1 dst_unused:UNUSED_PRESERVE src0_sel:WORD_1
	v_pk_add_f16 v136, v197, v201 neg_lo:[0,1] neg_hi:[0,1]
	v_pk_add_f16 v127, v127, v140
	v_pk_add_f16 v124, v124, v143
	v_pk_add_f16 v125, v125, v142
	v_pk_add_f16 v126, v126, v141
	v_pk_fma_f16 v99, v51, v143, v99
	v_pk_fma_f16 v98, v50, v142, v98
	v_pk_fma_f16 v97, v49, v141, v97
	s_mov_b64 exec, s[78:79]
	buffer_load_dwordx4 v[28:31], v233, s[8:11], 0 offen offset:2048
	buffer_load_dwordx4 v[24:27], v233, s[8:11], 0 offen offset:2560
	s_mov_b64 exec, -1
	v_pk_fma_f16 v96, v48, v140, v96
	v_pk_add_f16 v137, v198, v202 neg_lo:[0,1] neg_hi:[0,1]
	v_pk_add_f16 v138, v199, v203 neg_lo:[0,1] neg_hi:[0,1]
	v_pk_add_f16 v139, v200, v204 neg_lo:[0,1] neg_hi:[0,1]
	v_exp_f16_sdwa v140, v136 dst_sel:WORD_0 dst_unused:UNUSED_PAD src0_sel:WORD_0
	v_exp_f16_sdwa v141, v137 dst_sel:WORD_0 dst_unused:UNUSED_PAD src0_sel:WORD_0
	v_exp_f16_sdwa v142, v138 dst_sel:WORD_0 dst_unused:UNUSED_PAD src0_sel:WORD_0
	v_exp_f16_sdwa v143, v139 dst_sel:WORD_0 dst_unused:UNUSED_PAD src0_sel:WORD_0
	v_exp_f16_sdwa v140, v136 dst_sel:WORD_1 dst_unused:UNUSED_PRESERVE src0_sel:WORD_1
	v_exp_f16_sdwa v141, v137 dst_sel:WORD_1 dst_unused:UNUSED_PRESERVE src0_sel:WORD_1
	v_exp_f16_sdwa v142, v138 dst_sel:WORD_1 dst_unused:UNUSED_PRESERVE src0_sel:WORD_1
	v_exp_f16_sdwa v143, v139 dst_sel:WORD_1 dst_unused:UNUSED_PRESERVE src0_sel:WORD_1
	v_pk_add_f16 v136, v190, v201 neg_lo:[0,1] neg_hi:[0,1]
	v_pk_add_f16 v127, v127, v140
	v_pk_add_f16 v126, v126, v141
	v_pk_add_f16 v125, v125, v142
	v_pk_add_f16 v124, v124, v143
	v_pk_fma_f16 v96, v56, v140, v96
	v_pk_fma_f16 v97, v57, v141, v97
	v_pk_fma_f16 v98, v58, v142, v98
	v_pk_fma_f16 v99, v59, v143, v99
	v_pk_add_f16 v137, v191, v202 neg_lo:[0,1] neg_hi:[0,1]
	v_pk_add_f16 v138, v192, v203 neg_lo:[0,1] neg_hi:[0,1]
	v_pk_add_f16 v139, v193, v204 neg_lo:[0,1] neg_hi:[0,1]
	v_exp_f16_sdwa v140, v136 dst_sel:WORD_0 dst_unused:UNUSED_PAD src0_sel:WORD_0
	v_exp_f16_sdwa v141, v137 dst_sel:WORD_0 dst_unused:UNUSED_PAD src0_sel:WORD_0
	v_exp_f16_sdwa v142, v138 dst_sel:WORD_0 dst_unused:UNUSED_PAD src0_sel:WORD_0
	v_exp_f16_sdwa v143, v139 dst_sel:WORD_0 dst_unused:UNUSED_PAD src0_sel:WORD_0
	v_exp_f16_sdwa v140, v136 dst_sel:WORD_1 dst_unused:UNUSED_PRESERVE src0_sel:WORD_1
	v_exp_f16_sdwa v141, v137 dst_sel:WORD_1 dst_unused:UNUSED_PRESERVE src0_sel:WORD_1
	v_exp_f16_sdwa v142, v138 dst_sel:WORD_1 dst_unused:UNUSED_PRESERVE src0_sel:WORD_1
	v_exp_f16_sdwa v143, v139 dst_sel:WORD_1 dst_unused:UNUSED_PRESERVE src0_sel:WORD_1
	v_pk_add_f16 v127, v127, v140
	v_pk_add_f16 v126, v126, v141
	v_rcp_f16_e32 v136, v127
	v_rcp_f16_sdwa v127, v127 dst_sel:DWORD dst_unused:UNUSED_PAD src0_sel:WORD_1
	v_pk_add_f16 v125, v125, v142
	v_rcp_f16_e32 v137, v126
	v_rcp_f16_sdwa v126, v126 dst_sel:DWORD dst_unused:UNUSED_PAD src0_sel:WORD_1
	v_pk_add_f16 v124, v124, v143
	v_rcp_f16_e32 v138, v125
	v_rcp_f16_sdwa v139, v125 dst_sel:DWORD dst_unused:UNUSED_PAD src0_sel:WORD_1
	v_pk_fma_f16 v97, v73, v141, v97
	v_pk_fma_f16 v96, v72, v140, v96
	v_rcp_f16_e32 v140, v124
	v_rcp_f16_sdwa v141, v124 dst_sel:DWORD dst_unused:UNUSED_PAD src0_sel:WORD_1
	v_pack_b32_f16 v124, v136, v127
	v_pk_mul_f16 v124, v96, v124
	v_pack_b32_f16 v96, v137, v126
	v_pk_fma_f16 v98, v74, v142, v98
	v_pk_mul_f16 v125, v97, v96
	v_pack_b32_f16 v96, v138, v139
	v_pk_fma_f16 v99, v75, v143, v99
	v_pk_mul_f16 v126, v98, v96
	v_pack_b32_f16 v96, v140, v141
	v_pk_mul_f16 v127, v99, v96
	s_waitcnt vmcnt(12)
	v_pk_mul_f16 v99, v188, v179 op_sel_hi:[0,1]
	v_pk_mul_f16 v139, v186, v179 op_sel_hi:[0,1]
	v_pk_mul_f16 v143, v187, v179 op_sel_hi:[0,1]
	v_pk_mul_f16 v96, v188, v176 op_sel_hi:[0,1]
	v_pk_mul_f16 v97, v188, v177 op_sel_hi:[0,1]
	v_pk_mul_f16 v98, v188, v178 op_sel_hi:[0,1]
	v_pk_mul_f16 v136, v186, v176 op_sel_hi:[0,1]
	v_pk_mul_f16 v137, v186, v177 op_sel_hi:[0,1]
	v_pk_mul_f16 v138, v186, v178 op_sel_hi:[0,1]
	v_pk_mul_f16 v140, v187, v176 op_sel_hi:[0,1]
	v_pk_mul_f16 v141, v187, v177 op_sel_hi:[0,1]
	v_pk_mul_f16 v142, v187, v178 op_sel_hi:[0,1]
	v_pk_fma_f16 v115, v115, v179, v99
	v_pk_fma_f16 v135, v135, v179, v139
	v_pk_fma_f16 v151, v151, v179, v143
	v_pk_fma_f16 v152, v79, v179, v99
	v_pk_fma_f16 v160, v95, v179, v139
	v_pk_fma_f16 v189, v119, v179, v143
	v_pk_fma_f16 v99, v47, v179, v99
	v_pk_fma_f16 v139, v63, v179, v139
	v_pk_fma_f16 v143, v83, v179, v143
	v_pk_maximum3_f16 v179, v115, v135, v151
	v_pk_fma_f16 v114, v114, v178, v98
	v_pk_fma_f16 v113, v113, v177, v97
	v_pk_fma_f16 v112, v112, v176, v96
	v_pk_fma_f16 v134, v134, v178, v138
	v_pk_fma_f16 v133, v133, v177, v137
	v_pk_fma_f16 v132, v132, v176, v136
	v_pk_fma_f16 v150, v150, v178, v142
	v_pk_fma_f16 v149, v149, v177, v141
	v_pk_fma_f16 v148, v148, v176, v140
	v_pk_fma_f16 v153, v78, v178, v98
	v_pk_fma_f16 v154, v77, v177, v97
	v_pk_fma_f16 v155, v76, v176, v96
	v_pk_fma_f16 v161, v94, v178, v138
	v_pk_fma_f16 v162, v93, v177, v137
	v_pk_fma_f16 v163, v92, v176, v136
	v_pk_fma_f16 v190, v118, v178, v142
	v_pk_fma_f16 v191, v117, v177, v141
	v_pk_fma_f16 v192, v116, v176, v140
	v_pk_fma_f16 v98, v46, v178, v98
	v_pk_fma_f16 v97, v45, v177, v97
	v_pk_fma_f16 v96, v44, v176, v96
	v_pk_fma_f16 v138, v62, v178, v138
	v_pk_fma_f16 v137, v61, v177, v137
	v_pk_fma_f16 v136, v60, v176, v136
	v_pk_fma_f16 v142, v82, v178, v142
	v_pk_fma_f16 v141, v81, v177, v141
	v_pk_fma_f16 v140, v80, v176, v140
	v_pk_maximum3_f16 v176, v112, v132, v148
	v_pk_maximum3_f16 v177, v113, v133, v149
	v_pk_maximum3_f16 v178, v114, v134, v150
	v_pk_maximum3_f16 v196, v152, v160, v189
	v_pk_maximum3_f16 v200, v99, v139, v143
	v_pk_maximum3_f16 v193, v155, v163, v192
	v_pk_maximum3_f16 v194, v154, v162, v191
	v_pk_maximum3_f16 v195, v153, v161, v190
	v_pk_maximum3_f16 v197, v96, v136, v140
	v_pk_maximum3_f16 v198, v97, v137, v141
	v_pk_maximum3_f16 v179, v179, v196, v200
	v_pk_maximum3_f16 v199, v98, v138, v142
	v_pk_maximum3_f16 v176, v176, v193, v197
	v_pk_maximum3_f16 v177, v177, v194, v198
	v_pk_maximum3_f16 v178, v178, v195, v199
	v_pk_add_f16 v115, v115, v179 neg_lo:[0,1] neg_hi:[0,1]
	v_pk_add_f16 v112, v112, v176 neg_lo:[0,1] neg_hi:[0,1]
	v_pk_add_f16 v113, v113, v177 neg_lo:[0,1] neg_hi:[0,1]
	v_pk_add_f16 v114, v114, v178 neg_lo:[0,1] neg_hi:[0,1]
	v_pk_add_f16 v132, v132, v176 neg_lo:[0,1] neg_hi:[0,1]
	v_exp_f16_sdwa v193, v112 dst_sel:WORD_0 dst_unused:UNUSED_PAD src0_sel:WORD_0
	v_exp_f16_sdwa v194, v113 dst_sel:WORD_0 dst_unused:UNUSED_PAD src0_sel:WORD_0
	v_exp_f16_sdwa v195, v114 dst_sel:WORD_0 dst_unused:UNUSED_PAD src0_sel:WORD_0
	v_exp_f16_sdwa v196, v115 dst_sel:WORD_0 dst_unused:UNUSED_PAD src0_sel:WORD_0
	v_exp_f16_sdwa v193, v112 dst_sel:WORD_1 dst_unused:UNUSED_PRESERVE src0_sel:WORD_1
	v_exp_f16_sdwa v194, v113 dst_sel:WORD_1 dst_unused:UNUSED_PRESERVE src0_sel:WORD_1
	v_exp_f16_sdwa v195, v114 dst_sel:WORD_1 dst_unused:UNUSED_PRESERVE src0_sel:WORD_1
	v_exp_f16_sdwa v196, v115 dst_sel:WORD_1 dst_unused:UNUSED_PRESERVE src0_sel:WORD_1
	v_pk_add_f16 v133, v133, v177 neg_lo:[0,1] neg_hi:[0,1]
	v_pk_add_f16 v115, v193, 0
	v_pk_fma_f16 v71, v71, v196, 0
	v_pk_add_f16 v112, v196, 0
	v_pk_add_f16 v113, v195, 0
	v_pk_add_f16 v114, v194, 0
	v_pk_fma_f16 v70, v70, v195, 0
	v_pk_fma_f16 v69, v69, v194, 0
	v_pk_fma_f16 v68, v68, v193, 0
	v_pk_add_f16 v134, v134, v178 neg_lo:[0,1] neg_hi:[0,1]
	v_pk_add_f16 v135, v135, v179 neg_lo:[0,1] neg_hi:[0,1]
	v_pk_add_f16 v96, v96, v176 neg_lo:[0,1] neg_hi:[0,1]
	v_exp_f16_sdwa v193, v132 dst_sel:WORD_0 dst_unused:UNUSED_PAD src0_sel:WORD_0
	v_exp_f16_sdwa v194, v133 dst_sel:WORD_0 dst_unused:UNUSED_PAD src0_sel:WORD_0
	v_exp_f16_sdwa v195, v134 dst_sel:WORD_0 dst_unused:UNUSED_PAD src0_sel:WORD_0
	v_exp_f16_sdwa v196, v135 dst_sel:WORD_0 dst_unused:UNUSED_PAD src0_sel:WORD_0
	v_exp_f16_sdwa v193, v132 dst_sel:WORD_1 dst_unused:UNUSED_PRESERVE src0_sel:WORD_1
	v_exp_f16_sdwa v194, v133 dst_sel:WORD_1 dst_unused:UNUSED_PRESERVE src0_sel:WORD_1
	v_exp_f16_sdwa v195, v134 dst_sel:WORD_1 dst_unused:UNUSED_PRESERVE src0_sel:WORD_1
	v_exp_f16_sdwa v196, v135 dst_sel:WORD_1 dst_unused:UNUSED_PRESERVE src0_sel:WORD_1
	v_pk_add_f16 v97, v97, v177 neg_lo:[0,1] neg_hi:[0,1]
	v_pk_add_f16 v115, v115, v193
	v_pk_fma_f16 v71, v91, v196, v71
	v_pk_add_f16 v91, v151, v179 neg_lo:[0,1] neg_hi:[0,1]
	v_pk_add_f16 v114, v114, v194
	v_pk_add_f16 v113, v113, v195
	v_pk_add_f16 v112, v112, v196
	v_pk_fma_f16 v68, v88, v193, v68
	v_pk_fma_f16 v69, v89, v194, v69
	v_pk_fma_f16 v70, v90, v195, v70
	v_pk_add_f16 v88, v148, v176 neg_lo:[0,1] neg_hi:[0,1]
	v_pk_add_f16 v89, v149, v177 neg_lo:[0,1] neg_hi:[0,1]
	v_pk_add_f16 v90, v150, v178 neg_lo:[0,1] neg_hi:[0,1]
	v_pk_add_f16 v98, v98, v178 neg_lo:[0,1] neg_hi:[0,1]
	v_exp_f16_sdwa v132, v88 dst_sel:WORD_0 dst_unused:UNUSED_PAD src0_sel:WORD_0
	v_exp_f16_sdwa v133, v89 dst_sel:WORD_0 dst_unused:UNUSED_PAD src0_sel:WORD_0
	v_exp_f16_sdwa v134, v90 dst_sel:WORD_0 dst_unused:UNUSED_PAD src0_sel:WORD_0
	v_exp_f16_sdwa v135, v91 dst_sel:WORD_0 dst_unused:UNUSED_PAD src0_sel:WORD_0
	v_exp_f16_sdwa v132, v88 dst_sel:WORD_1 dst_unused:UNUSED_PRESERVE src0_sel:WORD_1
	v_exp_f16_sdwa v133, v89 dst_sel:WORD_1 dst_unused:UNUSED_PRESERVE src0_sel:WORD_1
	v_exp_f16_sdwa v134, v90 dst_sel:WORD_1 dst_unused:UNUSED_PRESERVE src0_sel:WORD_1
	v_exp_f16_sdwa v135, v91 dst_sel:WORD_1 dst_unused:UNUSED_PRESERVE src0_sel:WORD_1
	v_pk_add_f16 v99, v99, v179 neg_lo:[0,1] neg_hi:[0,1]
	v_pk_add_f16 v91, v115, v132
	v_pk_add_f16 v88, v112, v135
	v_pk_add_f16 v89, v113, v134
	v_pk_add_f16 v90, v114, v133
	v_pk_fma_f16 v71, v111, v135, v71
	v_pk_fma_f16 v70, v110, v134, v70
	v_pk_fma_f16 v69, v109, v133, v69
	v_pk_fma_f16 v68, v108, v132, v68
	v_pk_add_f16 v108, v155, v176 neg_lo:[0,1] neg_hi:[0,1]
	v_pk_add_f16 v109, v154, v177 neg_lo:[0,1] neg_hi:[0,1]
	v_pk_add_f16 v110, v153, v178 neg_lo:[0,1] neg_hi:[0,1]
	v_pk_add_f16 v111, v152, v179 neg_lo:[0,1] neg_hi:[0,1]
	v_exp_f16_sdwa v112, v108 dst_sel:WORD_0 dst_unused:UNUSED_PAD src0_sel:WORD_0
	v_exp_f16_sdwa v113, v109 dst_sel:WORD_0 dst_unused:UNUSED_PAD src0_sel:WORD_0
	v_exp_f16_sdwa v114, v110 dst_sel:WORD_0 dst_unused:UNUSED_PAD src0_sel:WORD_0
	v_exp_f16_sdwa v115, v111 dst_sel:WORD_0 dst_unused:UNUSED_PAD src0_sel:WORD_0
	v_exp_f16_sdwa v112, v108 dst_sel:WORD_1 dst_unused:UNUSED_PRESERVE src0_sel:WORD_1
	v_exp_f16_sdwa v113, v109 dst_sel:WORD_1 dst_unused:UNUSED_PRESERVE src0_sel:WORD_1
	v_exp_f16_sdwa v114, v110 dst_sel:WORD_1 dst_unused:UNUSED_PRESERVE src0_sel:WORD_1
	v_exp_f16_sdwa v115, v111 dst_sel:WORD_1 dst_unused:UNUSED_PRESERVE src0_sel:WORD_1
	v_pk_add_f16 v108, v163, v176 neg_lo:[0,1] neg_hi:[0,1]
	v_pk_add_f16 v91, v91, v112
	v_pk_add_f16 v90, v90, v113
	v_pk_add_f16 v89, v89, v114
	v_pk_add_f16 v88, v88, v115
	v_pk_fma_f16 v68, v48, v112, v68
	v_pk_fma_f16 v69, v49, v113, v69
	v_pk_fma_f16 v70, v50, v114, v70
	v_pk_fma_f16 v71, v51, v115, v71
	v_pk_add_f16 v109, v162, v177 neg_lo:[0,1] neg_hi:[0,1]
	v_pk_add_f16 v110, v161, v178 neg_lo:[0,1] neg_hi:[0,1]
	v_pk_add_f16 v111, v160, v179 neg_lo:[0,1] neg_hi:[0,1]
	v_exp_f16_sdwa v112, v108 dst_sel:WORD_0 dst_unused:UNUSED_PAD src0_sel:WORD_0
	v_exp_f16_sdwa v113, v109 dst_sel:WORD_0 dst_unused:UNUSED_PAD src0_sel:WORD_0
	v_exp_f16_sdwa v114, v110 dst_sel:WORD_0 dst_unused:UNUSED_PAD src0_sel:WORD_0
	v_exp_f16_sdwa v115, v111 dst_sel:WORD_0 dst_unused:UNUSED_PAD src0_sel:WORD_0
	v_exp_f16_sdwa v112, v108 dst_sel:WORD_1 dst_unused:UNUSED_PRESERVE src0_sel:WORD_1
	v_exp_f16_sdwa v113, v109 dst_sel:WORD_1 dst_unused:UNUSED_PRESERVE src0_sel:WORD_1
	v_exp_f16_sdwa v114, v110 dst_sel:WORD_1 dst_unused:UNUSED_PRESERVE src0_sel:WORD_1
	v_exp_f16_sdwa v115, v111 dst_sel:WORD_1 dst_unused:UNUSED_PRESERVE src0_sel:WORD_1
	v_pk_add_f16 v108, v192, v176 neg_lo:[0,1] neg_hi:[0,1]
	v_pk_add_f16 v91, v91, v112
	v_pk_add_f16 v88, v88, v115
	v_pk_add_f16 v89, v89, v114
	v_pk_add_f16 v90, v90, v113
	v_pk_fma_f16 v71, v59, v115, v71
	v_pk_fma_f16 v70, v58, v114, v70
	v_pk_fma_f16 v69, v57, v113, v69
	v_pk_fma_f16 v68, v56, v112, v68
	v_pk_add_f16 v109, v191, v177 neg_lo:[0,1] neg_hi:[0,1]
	v_pk_add_f16 v110, v190, v178 neg_lo:[0,1] neg_hi:[0,1]
	v_pk_add_f16 v111, v189, v179 neg_lo:[0,1] neg_hi:[0,1]
	v_exp_f16_sdwa v112, v108 dst_sel:WORD_0 dst_unused:UNUSED_PAD src0_sel:WORD_0
	v_exp_f16_sdwa v113, v109 dst_sel:WORD_0 dst_unused:UNUSED_PAD src0_sel:WORD_0
	v_exp_f16_sdwa v114, v110 dst_sel:WORD_0 dst_unused:UNUSED_PAD src0_sel:WORD_0
	v_exp_f16_sdwa v115, v111 dst_sel:WORD_0 dst_unused:UNUSED_PAD src0_sel:WORD_0
	v_exp_f16_sdwa v112, v108 dst_sel:WORD_1 dst_unused:UNUSED_PRESERVE src0_sel:WORD_1
	v_exp_f16_sdwa v113, v109 dst_sel:WORD_1 dst_unused:UNUSED_PRESERVE src0_sel:WORD_1
	v_exp_f16_sdwa v114, v110 dst_sel:WORD_1 dst_unused:UNUSED_PRESERVE src0_sel:WORD_1
	v_exp_f16_sdwa v115, v111 dst_sel:WORD_1 dst_unused:UNUSED_PRESERVE src0_sel:WORD_1
	v_exp_f16_sdwa v108, v96 dst_sel:WORD_0 dst_unused:UNUSED_PAD src0_sel:WORD_0
	v_exp_f16_sdwa v109, v97 dst_sel:WORD_0 dst_unused:UNUSED_PAD src0_sel:WORD_0
	v_exp_f16_sdwa v110, v98 dst_sel:WORD_0 dst_unused:UNUSED_PAD src0_sel:WORD_0
	v_exp_f16_sdwa v111, v99 dst_sel:WORD_0 dst_unused:UNUSED_PAD src0_sel:WORD_0
	v_exp_f16_sdwa v108, v96 dst_sel:WORD_1 dst_unused:UNUSED_PRESERVE src0_sel:WORD_1
	v_exp_f16_sdwa v109, v97 dst_sel:WORD_1 dst_unused:UNUSED_PRESERVE src0_sel:WORD_1
	v_exp_f16_sdwa v110, v98 dst_sel:WORD_1 dst_unused:UNUSED_PRESERVE src0_sel:WORD_1
	v_exp_f16_sdwa v111, v99 dst_sel:WORD_1 dst_unused:UNUSED_PRESERVE src0_sel:WORD_1
	v_pk_add_f16 v96, v136, v176 neg_lo:[0,1] neg_hi:[0,1]
	v_pk_add_f16 v91, v91, v112
	v_pk_add_f16 v90, v90, v113
	v_pk_add_f16 v89, v89, v114
	v_pk_add_f16 v88, v88, v115
	v_pk_fma_f16 v68, v72, v112, v68
	v_pk_fma_f16 v69, v73, v113, v69
	v_pk_fma_f16 v70, v74, v114, v70
	v_pk_fma_f16 v71, v75, v115, v71
	v_pk_add_f16 v91, v91, v108
	v_pk_add_f16 v88, v88, v111
	v_pk_add_f16 v89, v89, v110
	v_pk_add_f16 v90, v90, v109
	v_pk_fma_f16 v71, v35, v111, v71
	v_pk_fma_f16 v70, v34, v110, v70
	v_pk_fma_f16 v69, v33, v109, v69
	v_pk_fma_f16 v68, v32, v108, v68
	v_pk_add_f16 v97, v137, v177 neg_lo:[0,1] neg_hi:[0,1]
	v_pk_add_f16 v98, v138, v178 neg_lo:[0,1] neg_hi:[0,1]
	v_pk_add_f16 v99, v139, v179 neg_lo:[0,1] neg_hi:[0,1]
	v_exp_f16_sdwa v108, v96 dst_sel:WORD_0 dst_unused:UNUSED_PAD src0_sel:WORD_0
	v_exp_f16_sdwa v109, v97 dst_sel:WORD_0 dst_unused:UNUSED_PAD src0_sel:WORD_0
	v_exp_f16_sdwa v110, v98 dst_sel:WORD_0 dst_unused:UNUSED_PAD src0_sel:WORD_0
	v_exp_f16_sdwa v111, v99 dst_sel:WORD_0 dst_unused:UNUSED_PAD src0_sel:WORD_0
	v_exp_f16_sdwa v108, v96 dst_sel:WORD_1 dst_unused:UNUSED_PRESERVE src0_sel:WORD_1
	v_exp_f16_sdwa v109, v97 dst_sel:WORD_1 dst_unused:UNUSED_PRESERVE src0_sel:WORD_1
	v_exp_f16_sdwa v110, v98 dst_sel:WORD_1 dst_unused:UNUSED_PRESERVE src0_sel:WORD_1
	v_exp_f16_sdwa v111, v99 dst_sel:WORD_1 dst_unused:UNUSED_PRESERVE src0_sel:WORD_1
	v_pk_add_f16 v96, v140, v176 neg_lo:[0,1] neg_hi:[0,1]
	v_pk_add_f16 v91, v91, v108
	v_pk_add_f16 v90, v90, v109
	v_pk_add_f16 v89, v89, v110
	v_pk_add_f16 v88, v88, v111
	v_pk_fma_f16 v68, v36, v108, v68
	v_pk_fma_f16 v69, v37, v109, v69
	v_pk_fma_f16 v70, v38, v110, v70
	v_pk_fma_f16 v71, v39, v111, v71
	v_pk_add_f16 v97, v141, v177 neg_lo:[0,1] neg_hi:[0,1]
	v_pk_add_f16 v98, v142, v178 neg_lo:[0,1] neg_hi:[0,1]
	v_pk_add_f16 v99, v143, v179 neg_lo:[0,1] neg_hi:[0,1]
	v_exp_f16_sdwa v108, v96 dst_sel:WORD_0 dst_unused:UNUSED_PAD src0_sel:WORD_0
	v_exp_f16_sdwa v109, v97 dst_sel:WORD_0 dst_unused:UNUSED_PAD src0_sel:WORD_0
	v_exp_f16_sdwa v110, v98 dst_sel:WORD_0 dst_unused:UNUSED_PAD src0_sel:WORD_0
	v_exp_f16_sdwa v111, v99 dst_sel:WORD_0 dst_unused:UNUSED_PAD src0_sel:WORD_0
	v_exp_f16_sdwa v108, v96 dst_sel:WORD_1 dst_unused:UNUSED_PRESERVE src0_sel:WORD_1
	v_exp_f16_sdwa v109, v97 dst_sel:WORD_1 dst_unused:UNUSED_PRESERVE src0_sel:WORD_1
	v_exp_f16_sdwa v110, v98 dst_sel:WORD_1 dst_unused:UNUSED_PRESERVE src0_sel:WORD_1
	v_exp_f16_sdwa v111, v99 dst_sel:WORD_1 dst_unused:UNUSED_PRESERVE src0_sel:WORD_1
	v_pk_add_f16 v91, v91, v108
	v_pk_add_f16 v90, v90, v109
	v_rcp_f16_e32 v96, v91
	v_rcp_f16_sdwa v91, v91 dst_sel:DWORD dst_unused:UNUSED_PAD src0_sel:WORD_1
	v_pk_add_f16 v89, v89, v110
	v_rcp_f16_e32 v97, v90
	v_rcp_f16_sdwa v90, v90 dst_sel:DWORD dst_unused:UNUSED_PAD src0_sel:WORD_1
	v_pk_add_f16 v88, v88, v111
	v_rcp_f16_e32 v98, v89
	v_rcp_f16_sdwa v99, v89 dst_sel:DWORD dst_unused:UNUSED_PAD src0_sel:WORD_1
	v_pk_fma_f16 v69, v41, v109, v69
	v_pk_fma_f16 v68, v40, v108, v68
	v_rcp_f16_e32 v108, v88
	v_rcp_f16_sdwa v109, v88 dst_sel:DWORD dst_unused:UNUSED_PAD src0_sel:WORD_1
	v_pack_b32_f16 v88, v96, v91
	v_pk_mul_f16 v88, v68, v88
	v_pack_b32_f16 v68, v97, v90
	v_pk_fma_f16 v70, v42, v110, v70
	v_pk_mul_f16 v89, v69, v68
	v_pack_b32_f16 v68, v98, v99
	v_pk_fma_f16 v71, v43, v111, v71
	v_pk_mul_f16 v90, v70, v68
	v_pack_b32_f16 v68, v108, v109
	v_pk_mul_f16 v91, v71, v68
	s_waitcnt vmcnt(6)
	v_pk_mul_f16 v68, v188, v172 op_sel_hi:[0,1]
	v_pk_mul_f16 v96, v186, v172 op_sel_hi:[0,1]
	v_pk_mul_f16 v108, v187, v172 op_sel_hi:[0,1]
	v_pk_mul_f16 v69, v188, v173 op_sel_hi:[0,1]
	v_pk_mul_f16 v70, v188, v174 op_sel_hi:[0,1]
	v_pk_mul_f16 v71, v188, v175 op_sel_hi:[0,1]
	v_pk_mul_f16 v97, v186, v173 op_sel_hi:[0,1]
	v_pk_mul_f16 v98, v186, v174 op_sel_hi:[0,1]
	v_pk_mul_f16 v99, v186, v175 op_sel_hi:[0,1]
	v_pk_mul_f16 v109, v187, v173 op_sel_hi:[0,1]
	v_pk_mul_f16 v110, v187, v174 op_sel_hi:[0,1]
	v_pk_mul_f16 v111, v187, v175 op_sel_hi:[0,1]
	v_pk_fma_f16 v76, v76, v172, v68
	v_pk_fma_f16 v92, v92, v172, v96
	v_pk_fma_f16 v115, v116, v172, v108
	v_pk_fma_f16 v79, v79, v175, v71
	v_pk_maximum3_f16 v140, v76, v92, v115
	v_pk_fma_f16 v78, v78, v174, v70
	v_pk_fma_f16 v77, v77, v173, v69
	v_pk_fma_f16 v95, v95, v175, v99
	v_pk_fma_f16 v94, v94, v174, v98
	v_pk_fma_f16 v93, v93, v173, v97
	v_pk_fma_f16 v112, v119, v175, v111
	v_pk_fma_f16 v113, v118, v174, v110
	v_pk_fma_f16 v114, v117, v173, v109
	v_pk_fma_f16 v119, v44, v172, v68
	v_pk_fma_f16 v135, v60, v172, v96
	v_pk_fma_f16 v139, v80, v172, v108
	v_pk_fma_f16 v68, v100, v172, v68
	v_pk_fma_f16 v96, v128, v172, v96
	v_pk_fma_f16 v108, v144, v172, v108
	v_pk_maximum3_f16 v141, v77, v93, v114
	v_pk_maximum3_f16 v142, v78, v94, v113
	v_pk_maximum3_f16 v143, v79, v95, v112
	v_pk_maximum3_f16 v148, v119, v135, v139
	v_pk_fma_f16 v116, v47, v175, v71
	v_pk_maximum3_f16 v152, v68, v96, v108
	v_pk_fma_f16 v117, v46, v174, v70
	v_pk_maximum3_f16 v140, v140, v148, v152
	v_pk_fma_f16 v118, v45, v173, v69
	v_pk_fma_f16 v132, v63, v175, v99
	v_pk_fma_f16 v133, v62, v174, v98
	v_pk_fma_f16 v134, v61, v173, v97
	v_pk_fma_f16 v136, v83, v175, v111
	v_pk_fma_f16 v137, v82, v174, v110
	v_pk_fma_f16 v138, v81, v173, v109
	v_pk_fma_f16 v71, v103, v175, v71
	v_pk_fma_f16 v70, v102, v174, v70
	v_pk_fma_f16 v69, v101, v173, v69
	v_pk_fma_f16 v99, v131, v175, v99
	v_pk_fma_f16 v98, v130, v174, v98
	v_pk_fma_f16 v97, v129, v173, v97
	v_pk_fma_f16 v111, v147, v175, v111
	v_pk_fma_f16 v110, v146, v174, v110
	v_pk_fma_f16 v109, v145, v173, v109
	v_pk_maximum3_f16 v149, v118, v134, v138
	v_pk_maximum3_f16 v150, v117, v133, v137
	v_pk_maximum3_f16 v151, v116, v132, v136
	v_pk_maximum3_f16 v154, v70, v98, v110
	v_pk_maximum3_f16 v155, v71, v99, v111
	v_pk_maximum3_f16 v153, v69, v97, v109
	v_pk_maximum3_f16 v141, v141, v149, v153
	v_pk_maximum3_f16 v142, v142, v150, v154
	v_pk_maximum3_f16 v143, v143, v151, v155
	v_pk_add_f16 v76, v76, v140 neg_lo:[0,1] neg_hi:[0,1]
	v_pk_add_f16 v77, v77, v141 neg_lo:[0,1] neg_hi:[0,1]
	v_pk_add_f16 v78, v78, v142 neg_lo:[0,1] neg_hi:[0,1]
	v_pk_add_f16 v79, v79, v143 neg_lo:[0,1] neg_hi:[0,1]
	v_pk_add_f16 v92, v92, v140 neg_lo:[0,1] neg_hi:[0,1]
	v_exp_f16_sdwa v148, v76 dst_sel:WORD_0 dst_unused:UNUSED_PAD src0_sel:WORD_0
	v_exp_f16_sdwa v149, v77 dst_sel:WORD_0 dst_unused:UNUSED_PAD src0_sel:WORD_0
	v_exp_f16_sdwa v150, v78 dst_sel:WORD_0 dst_unused:UNUSED_PAD src0_sel:WORD_0
	v_exp_f16_sdwa v151, v79 dst_sel:WORD_0 dst_unused:UNUSED_PAD src0_sel:WORD_0
	v_exp_f16_sdwa v148, v76 dst_sel:WORD_1 dst_unused:UNUSED_PRESERVE src0_sel:WORD_1
	v_exp_f16_sdwa v149, v77 dst_sel:WORD_1 dst_unused:UNUSED_PRESERVE src0_sel:WORD_1
	v_exp_f16_sdwa v150, v78 dst_sel:WORD_1 dst_unused:UNUSED_PRESERVE src0_sel:WORD_1
	v_exp_f16_sdwa v151, v79 dst_sel:WORD_1 dst_unused:UNUSED_PRESERVE src0_sel:WORD_1
	v_pk_add_f16 v93, v93, v141 neg_lo:[0,1] neg_hi:[0,1]
	v_pk_add_f16 v76, v151, 0
	v_pk_fma_f16 v48, v48, v148, 0
	v_pk_add_f16 v77, v150, 0
	v_pk_add_f16 v78, v149, 0
	v_pk_add_f16 v79, v148, 0
	v_pk_fma_f16 v49, v49, v149, 0
	v_pk_fma_f16 v50, v50, v150, 0
	v_pk_fma_f16 v51, v51, v151, 0
	v_pk_add_f16 v94, v94, v142 neg_lo:[0,1] neg_hi:[0,1]
	v_pk_add_f16 v95, v95, v143 neg_lo:[0,1] neg_hi:[0,1]
	v_pk_add_f16 v68, v68, v140 neg_lo:[0,1] neg_hi:[0,1]
	v_exp_f16_sdwa v148, v92 dst_sel:WORD_0 dst_unused:UNUSED_PAD src0_sel:WORD_0
	v_exp_f16_sdwa v149, v93 dst_sel:WORD_0 dst_unused:UNUSED_PAD src0_sel:WORD_0
	v_exp_f16_sdwa v150, v94 dst_sel:WORD_0 dst_unused:UNUSED_PAD src0_sel:WORD_0
	v_exp_f16_sdwa v151, v95 dst_sel:WORD_0 dst_unused:UNUSED_PAD src0_sel:WORD_0
	v_exp_f16_sdwa v148, v92 dst_sel:WORD_1 dst_unused:UNUSED_PRESERVE src0_sel:WORD_1
	v_exp_f16_sdwa v149, v93 dst_sel:WORD_1 dst_unused:UNUSED_PRESERVE src0_sel:WORD_1
	v_exp_f16_sdwa v150, v94 dst_sel:WORD_1 dst_unused:UNUSED_PRESERVE src0_sel:WORD_1
	v_exp_f16_sdwa v151, v95 dst_sel:WORD_1 dst_unused:UNUSED_PRESERVE src0_sel:WORD_1
	v_pk_add_f16 v69, v69, v141 neg_lo:[0,1] neg_hi:[0,1]
	v_pk_add_f16 v76, v76, v151
	v_pk_fma_f16 v48, v56, v148, v48
	v_pk_add_f16 v56, v115, v140 neg_lo:[0,1] neg_hi:[0,1]
	v_pk_add_f16 v79, v79, v148
	v_pk_add_f16 v78, v78, v149
	v_pk_add_f16 v77, v77, v150
	v_pk_fma_f16 v51, v59, v151, v51
	v_pk_fma_f16 v50, v58, v150, v50
	v_pk_fma_f16 v49, v57, v149, v49
	v_pk_add_f16 v57, v114, v141 neg_lo:[0,1] neg_hi:[0,1]
	v_pk_add_f16 v58, v113, v142 neg_lo:[0,1] neg_hi:[0,1]
	v_pk_add_f16 v59, v112, v143 neg_lo:[0,1] neg_hi:[0,1]
	v_pk_add_f16 v70, v70, v142 neg_lo:[0,1] neg_hi:[0,1]
	v_exp_f16_sdwa v92, v56 dst_sel:WORD_0 dst_unused:UNUSED_PAD src0_sel:WORD_0
	v_exp_f16_sdwa v93, v57 dst_sel:WORD_0 dst_unused:UNUSED_PAD src0_sel:WORD_0
	v_exp_f16_sdwa v94, v58 dst_sel:WORD_0 dst_unused:UNUSED_PAD src0_sel:WORD_0
	v_exp_f16_sdwa v95, v59 dst_sel:WORD_0 dst_unused:UNUSED_PAD src0_sel:WORD_0
	v_exp_f16_sdwa v92, v56 dst_sel:WORD_1 dst_unused:UNUSED_PRESERVE src0_sel:WORD_1
	v_exp_f16_sdwa v93, v57 dst_sel:WORD_1 dst_unused:UNUSED_PRESERVE src0_sel:WORD_1
	v_exp_f16_sdwa v94, v58 dst_sel:WORD_1 dst_unused:UNUSED_PRESERVE src0_sel:WORD_1
	v_exp_f16_sdwa v95, v59 dst_sel:WORD_1 dst_unused:UNUSED_PRESERVE src0_sel:WORD_1
	v_pk_add_f16 v71, v71, v143 neg_lo:[0,1] neg_hi:[0,1]
	v_pk_add_f16 v56, v76, v95
	v_pk_add_f16 v57, v77, v94
	v_pk_add_f16 v58, v78, v93
	v_pk_add_f16 v59, v79, v92
	v_pk_fma_f16 v48, v72, v92, v48
	v_pk_fma_f16 v49, v73, v93, v49
	v_pk_fma_f16 v50, v74, v94, v50
	v_pk_fma_f16 v51, v75, v95, v51
	v_pk_add_f16 v72, v119, v140 neg_lo:[0,1] neg_hi:[0,1]
	v_pk_add_f16 v73, v118, v141 neg_lo:[0,1] neg_hi:[0,1]
	v_pk_add_f16 v74, v117, v142 neg_lo:[0,1] neg_hi:[0,1]
	v_pk_add_f16 v75, v116, v143 neg_lo:[0,1] neg_hi:[0,1]
	v_exp_f16_sdwa v76, v72 dst_sel:WORD_0 dst_unused:UNUSED_PAD src0_sel:WORD_0
	v_exp_f16_sdwa v77, v73 dst_sel:WORD_0 dst_unused:UNUSED_PAD src0_sel:WORD_0
	v_exp_f16_sdwa v78, v74 dst_sel:WORD_0 dst_unused:UNUSED_PAD src0_sel:WORD_0
	v_exp_f16_sdwa v79, v75 dst_sel:WORD_0 dst_unused:UNUSED_PAD src0_sel:WORD_0
	v_exp_f16_sdwa v76, v72 dst_sel:WORD_1 dst_unused:UNUSED_PRESERVE src0_sel:WORD_1
	v_exp_f16_sdwa v77, v73 dst_sel:WORD_1 dst_unused:UNUSED_PRESERVE src0_sel:WORD_1
	v_exp_f16_sdwa v78, v74 dst_sel:WORD_1 dst_unused:UNUSED_PRESERVE src0_sel:WORD_1
	v_exp_f16_sdwa v79, v75 dst_sel:WORD_1 dst_unused:UNUSED_PRESERVE src0_sel:WORD_1
	v_pk_add_f16 v72, v135, v140 neg_lo:[0,1] neg_hi:[0,1]
	v_pk_add_f16 v56, v56, v79
	v_pk_add_f16 v59, v59, v76
	v_pk_add_f16 v58, v58, v77
	v_pk_add_f16 v57, v57, v78
	v_pk_fma_f16 v51, v35, v79, v51
	v_pk_fma_f16 v50, v34, v78, v50
	v_pk_fma_f16 v49, v33, v77, v49
	v_pk_fma_f16 v48, v32, v76, v48
	v_pk_add_f16 v73, v134, v141 neg_lo:[0,1] neg_hi:[0,1]
	v_pk_add_f16 v74, v133, v142 neg_lo:[0,1] neg_hi:[0,1]
	v_pk_add_f16 v75, v132, v143 neg_lo:[0,1] neg_hi:[0,1]
	v_exp_f16_sdwa v76, v72 dst_sel:WORD_0 dst_unused:UNUSED_PAD src0_sel:WORD_0
	v_exp_f16_sdwa v77, v73 dst_sel:WORD_0 dst_unused:UNUSED_PAD src0_sel:WORD_0
	v_exp_f16_sdwa v78, v74 dst_sel:WORD_0 dst_unused:UNUSED_PAD src0_sel:WORD_0
	v_exp_f16_sdwa v79, v75 dst_sel:WORD_0 dst_unused:UNUSED_PAD src0_sel:WORD_0
	v_exp_f16_sdwa v76, v72 dst_sel:WORD_1 dst_unused:UNUSED_PRESERVE src0_sel:WORD_1
	v_exp_f16_sdwa v77, v73 dst_sel:WORD_1 dst_unused:UNUSED_PRESERVE src0_sel:WORD_1
	v_exp_f16_sdwa v78, v74 dst_sel:WORD_1 dst_unused:UNUSED_PRESERVE src0_sel:WORD_1
	v_exp_f16_sdwa v79, v75 dst_sel:WORD_1 dst_unused:UNUSED_PRESERVE src0_sel:WORD_1
	v_pk_add_f16 v72, v139, v140 neg_lo:[0,1] neg_hi:[0,1]
	v_pk_add_f16 v56, v56, v79
	v_pk_add_f16 v57, v57, v78
	v_pk_add_f16 v58, v58, v77
	v_pk_add_f16 v59, v59, v76
	v_pk_fma_f16 v48, v36, v76, v48
	v_pk_fma_f16 v49, v37, v77, v49
	v_pk_fma_f16 v50, v38, v78, v50
	v_pk_fma_f16 v51, v39, v79, v51
	v_pk_add_f16 v73, v138, v141 neg_lo:[0,1] neg_hi:[0,1]
	v_pk_add_f16 v74, v137, v142 neg_lo:[0,1] neg_hi:[0,1]
	v_pk_add_f16 v75, v136, v143 neg_lo:[0,1] neg_hi:[0,1]
	v_exp_f16_sdwa v76, v72 dst_sel:WORD_0 dst_unused:UNUSED_PAD src0_sel:WORD_0
	v_exp_f16_sdwa v77, v73 dst_sel:WORD_0 dst_unused:UNUSED_PAD src0_sel:WORD_0
	v_exp_f16_sdwa v78, v74 dst_sel:WORD_0 dst_unused:UNUSED_PAD src0_sel:WORD_0
	v_exp_f16_sdwa v79, v75 dst_sel:WORD_0 dst_unused:UNUSED_PAD src0_sel:WORD_0
	v_exp_f16_sdwa v76, v72 dst_sel:WORD_1 dst_unused:UNUSED_PRESERVE src0_sel:WORD_1
	v_exp_f16_sdwa v77, v73 dst_sel:WORD_1 dst_unused:UNUSED_PRESERVE src0_sel:WORD_1
	v_exp_f16_sdwa v78, v74 dst_sel:WORD_1 dst_unused:UNUSED_PRESERVE src0_sel:WORD_1
	v_exp_f16_sdwa v79, v75 dst_sel:WORD_1 dst_unused:UNUSED_PRESERVE src0_sel:WORD_1
	v_exp_f16_sdwa v72, v68 dst_sel:WORD_0 dst_unused:UNUSED_PAD src0_sel:WORD_0
	v_exp_f16_sdwa v73, v69 dst_sel:WORD_0 dst_unused:UNUSED_PAD src0_sel:WORD_0
	v_exp_f16_sdwa v74, v70 dst_sel:WORD_0 dst_unused:UNUSED_PAD src0_sel:WORD_0
	v_exp_f16_sdwa v75, v71 dst_sel:WORD_0 dst_unused:UNUSED_PAD src0_sel:WORD_0
	v_exp_f16_sdwa v72, v68 dst_sel:WORD_1 dst_unused:UNUSED_PRESERVE src0_sel:WORD_1
	v_exp_f16_sdwa v73, v69 dst_sel:WORD_1 dst_unused:UNUSED_PRESERVE src0_sel:WORD_1
	v_exp_f16_sdwa v74, v70 dst_sel:WORD_1 dst_unused:UNUSED_PRESERVE src0_sel:WORD_1
	v_exp_f16_sdwa v75, v71 dst_sel:WORD_1 dst_unused:UNUSED_PRESERVE src0_sel:WORD_1
	v_pk_add_f16 v68, v96, v140 neg_lo:[0,1] neg_hi:[0,1]
	v_pk_add_f16 v56, v56, v79
	v_pk_add_f16 v59, v59, v76
	v_pk_add_f16 v58, v58, v77
	v_pk_add_f16 v57, v57, v78
	v_pk_fma_f16 v51, v43, v79, v51
	v_pk_fma_f16 v50, v42, v78, v50
	v_pk_fma_f16 v49, v41, v77, v49
	v_pk_fma_f16 v48, v40, v76, v48
	v_pk_add_f16 v56, v56, v75
	v_pk_add_f16 v57, v57, v74
	v_pk_add_f16 v58, v58, v73
	v_pk_add_f16 v59, v59, v72
	v_pk_fma_f16 v48, v52, v72, v48
	v_pk_fma_f16 v49, v53, v73, v49
	v_pk_fma_f16 v50, v54, v74, v50
	v_pk_fma_f16 v51, v55, v75, v51
	v_pk_add_f16 v69, v97, v141 neg_lo:[0,1] neg_hi:[0,1]
	v_pk_add_f16 v70, v98, v142 neg_lo:[0,1] neg_hi:[0,1]
	v_pk_add_f16 v71, v99, v143 neg_lo:[0,1] neg_hi:[0,1]
	v_exp_f16_sdwa v72, v68 dst_sel:WORD_0 dst_unused:UNUSED_PAD src0_sel:WORD_0
	v_exp_f16_sdwa v73, v69 dst_sel:WORD_0 dst_unused:UNUSED_PAD src0_sel:WORD_0
	v_exp_f16_sdwa v74, v70 dst_sel:WORD_0 dst_unused:UNUSED_PAD src0_sel:WORD_0
	v_exp_f16_sdwa v75, v71 dst_sel:WORD_0 dst_unused:UNUSED_PAD src0_sel:WORD_0
	v_exp_f16_sdwa v72, v68 dst_sel:WORD_1 dst_unused:UNUSED_PRESERVE src0_sel:WORD_1
	v_exp_f16_sdwa v73, v69 dst_sel:WORD_1 dst_unused:UNUSED_PRESERVE src0_sel:WORD_1
	v_exp_f16_sdwa v74, v70 dst_sel:WORD_1 dst_unused:UNUSED_PRESERVE src0_sel:WORD_1
	v_exp_f16_sdwa v75, v71 dst_sel:WORD_1 dst_unused:UNUSED_PRESERVE src0_sel:WORD_1
	v_pk_add_f16 v68, v108, v140 neg_lo:[0,1] neg_hi:[0,1]
	v_pk_add_f16 v56, v56, v75
	v_pk_add_f16 v59, v59, v72
	v_pk_add_f16 v58, v58, v73
	v_pk_add_f16 v57, v57, v74
	v_pk_fma_f16 v51, v67, v75, v51
	v_pk_fma_f16 v50, v66, v74, v50
	v_pk_fma_f16 v49, v65, v73, v49
	v_pk_fma_f16 v48, v64, v72, v48
	v_pk_add_f16 v69, v109, v141 neg_lo:[0,1] neg_hi:[0,1]
	v_pk_add_f16 v70, v110, v142 neg_lo:[0,1] neg_hi:[0,1]
	v_pk_add_f16 v71, v111, v143 neg_lo:[0,1] neg_hi:[0,1]
	v_exp_f16_sdwa v72, v68 dst_sel:WORD_0 dst_unused:UNUSED_PAD src0_sel:WORD_0
	v_exp_f16_sdwa v73, v69 dst_sel:WORD_0 dst_unused:UNUSED_PAD src0_sel:WORD_0
	v_exp_f16_sdwa v74, v70 dst_sel:WORD_0 dst_unused:UNUSED_PAD src0_sel:WORD_0
	v_exp_f16_sdwa v75, v71 dst_sel:WORD_0 dst_unused:UNUSED_PAD src0_sel:WORD_0
	v_exp_f16_sdwa v72, v68 dst_sel:WORD_1 dst_unused:UNUSED_PRESERVE src0_sel:WORD_1
	v_exp_f16_sdwa v73, v69 dst_sel:WORD_1 dst_unused:UNUSED_PRESERVE src0_sel:WORD_1
	v_exp_f16_sdwa v74, v70 dst_sel:WORD_1 dst_unused:UNUSED_PRESERVE src0_sel:WORD_1
	v_exp_f16_sdwa v75, v71 dst_sel:WORD_1 dst_unused:UNUSED_PRESERVE src0_sel:WORD_1
	s_nop 0
	v_pk_add_f16 v56, v56, v75
	v_pk_add_f16 v57, v57, v74
	v_rcp_f16_e32 v70, v56
	v_rcp_f16_sdwa v56, v56 dst_sel:DWORD dst_unused:UNUSED_PAD src0_sel:WORD_1
	v_pk_add_f16 v58, v58, v73
	v_rcp_f16_e32 v71, v57
	v_rcp_f16_sdwa v57, v57 dst_sel:DWORD dst_unused:UNUSED_PAD src0_sel:WORD_1
	v_pk_add_f16 v59, v59, v72
	v_rcp_f16_e32 v69, v58
	v_rcp_f16_sdwa v58, v58 dst_sel:DWORD dst_unused:UNUSED_PAD src0_sel:WORD_1
	v_rcp_f16_e32 v68, v59
	v_rcp_f16_sdwa v59, v59 dst_sel:DWORD dst_unused:UNUSED_PAD src0_sel:WORD_1
	v_pk_fma_f16 v51, v87, v75, v51
	v_pack_b32_f16 v56, v70, v56
	v_pk_fma_f16 v50, v86, v74, v50
	v_pk_mul_f16 v51, v51, v56
	v_pack_b32_f16 v56, v71, v57
	v_pk_fma_f16 v49, v85, v73, v49
	v_pk_mul_f16 v50, v50, v56
	v_pack_b32_f16 v56, v69, v58
	v_pk_fma_f16 v48, v84, v72, v48
	v_pk_mul_f16 v49, v49, v56
	v_pack_b32_f16 v56, v68, v59
	v_pk_mul_f16 v48, v48, v56
	s_waitcnt vmcnt(0)
	v_pk_mul_f16 v56, v188, v168 op_sel_hi:[0,1]
	v_pk_mul_f16 v57, v188, v169 op_sel_hi:[0,1]
	v_pk_mul_f16 v58, v188, v170 op_sel_hi:[0,1]
	v_pk_mul_f16 v59, v188, v171 op_sel_hi:[0,1]
	v_pk_mul_f16 v68, v186, v168 op_sel_hi:[0,1]
	v_pk_mul_f16 v69, v186, v169 op_sel_hi:[0,1]
	v_pk_mul_f16 v70, v186, v170 op_sel_hi:[0,1]
	v_pk_mul_f16 v71, v186, v171 op_sel_hi:[0,1]
	v_pk_mul_f16 v72, v187, v168 op_sel_hi:[0,1]
	v_pk_mul_f16 v73, v187, v169 op_sel_hi:[0,1]
	v_pk_mul_f16 v74, v187, v170 op_sel_hi:[0,1]
	v_pk_mul_f16 v75, v187, v171 op_sel_hi:[0,1]
	v_pk_fma_f16 v47, v47, v171, v59
	v_pk_fma_f16 v46, v46, v170, v58
	v_pk_fma_f16 v45, v45, v169, v57
	v_pk_fma_f16 v44, v44, v168, v56
	v_pk_fma_f16 v63, v63, v171, v71
	v_pk_fma_f16 v62, v62, v170, v70
	v_pk_fma_f16 v61, v61, v169, v69
	v_pk_fma_f16 v60, v60, v168, v68
	v_pk_fma_f16 v76, v83, v171, v75
	v_pk_fma_f16 v77, v82, v170, v74
	v_pk_fma_f16 v78, v81, v169, v73
	v_pk_fma_f16 v79, v80, v168, v72
	v_pk_fma_f16 v80, v103, v171, v59
	v_pk_fma_f16 v81, v102, v170, v58
	v_pk_fma_f16 v82, v101, v169, v57
	v_pk_fma_f16 v83, v100, v168, v56
	v_pk_fma_f16 v92, v131, v171, v71
	v_pk_fma_f16 v93, v130, v170, v70
	v_pk_fma_f16 v94, v129, v169, v69
	v_pk_fma_f16 v95, v128, v168, v68
	v_pk_fma_f16 v96, v147, v171, v75
	v_pk_fma_f16 v97, v146, v170, v74
	v_pk_fma_f16 v98, v145, v169, v73
	v_pk_fma_f16 v99, v144, v168, v72
	v_pk_fma_f16 v75, v31, v171, v75
	v_pk_fma_f16 v74, v30, v170, v74
	v_pk_fma_f16 v73, v29, v169, v73
	v_pk_fma_f16 v72, v28, v168, v72
	v_pk_maximum3_f16 v28, v44, v60, v79
	v_pk_maximum3_f16 v29, v45, v61, v78
	v_pk_maximum3_f16 v30, v46, v62, v77
	v_pk_maximum3_f16 v31, v47, v63, v76
	v_pk_maximum3_f16 v100, v83, v95, v99
	v_pk_maximum3_f16 v101, v82, v94, v98
	v_pk_maximum3_f16 v102, v81, v93, v97
	v_pk_maximum3_f16 v103, v80, v92, v96
	v_pk_fma_f16 v59, v159, v171, v59
	v_pk_fma_f16 v58, v158, v170, v58
	v_pk_fma_f16 v57, v157, v169, v57
	v_pk_fma_f16 v56, v156, v168, v56
	v_pk_fma_f16 v71, v167, v171, v71
	v_pk_fma_f16 v70, v166, v170, v70
	v_pk_fma_f16 v69, v165, v169, v69
	v_pk_fma_f16 v68, v164, v168, v68
	v_pk_maximum3_f16 v109, v57, v69, v73
	v_pk_maximum3_f16 v110, v58, v70, v74
	v_pk_maximum3_f16 v111, v59, v71, v75
	v_pk_maximum3_f16 v108, v56, v68, v72
	v_pk_maximum3_f16 v29, v29, v101, v109
	v_pk_maximum3_f16 v30, v30, v102, v110
	v_pk_maximum3_f16 v31, v31, v103, v111
	v_pk_maximum3_f16 v28, v28, v100, v108
	v_xor_b32_e32 v100, 0x80008000, v31
	v_xor_b32_e32 v101, 0x80008000, v30
	v_xor_b32_e32 v102, 0x80008000, v29
	v_xor_b32_e32 v103, 0x80008000, v28
	v_pk_add_f16 v28, v44, v103
	v_pk_add_f16 v29, v45, v102
	v_pk_add_f16 v30, v46, v101
	v_pk_add_f16 v31, v47, v100
	v_exp_f16_sdwa v44, v28 dst_sel:WORD_0 dst_unused:UNUSED_PAD src0_sel:WORD_0
	v_exp_f16_sdwa v45, v29 dst_sel:WORD_0 dst_unused:UNUSED_PAD src0_sel:WORD_0
	v_exp_f16_sdwa v46, v30 dst_sel:WORD_0 dst_unused:UNUSED_PAD src0_sel:WORD_0
	v_exp_f16_sdwa v47, v31 dst_sel:WORD_0 dst_unused:UNUSED_PAD src0_sel:WORD_0
	v_exp_f16_sdwa v44, v28 dst_sel:WORD_1 dst_unused:UNUSED_PRESERVE src0_sel:WORD_1
	v_exp_f16_sdwa v45, v29 dst_sel:WORD_1 dst_unused:UNUSED_PRESERVE src0_sel:WORD_1
	v_exp_f16_sdwa v46, v30 dst_sel:WORD_1 dst_unused:UNUSED_PRESERVE src0_sel:WORD_1
	v_exp_f16_sdwa v47, v31 dst_sel:WORD_1 dst_unused:UNUSED_PRESERVE src0_sel:WORD_1
	v_pk_add_f16 v28, v44, 0
	v_pk_add_f16 v29, v45, 0
	v_pk_add_f16 v30, v46, 0
	v_pk_add_f16 v31, v47, 0
	v_pk_fma_f16 v32, v32, v44, 0
	v_pk_fma_f16 v33, v33, v45, 0
	v_pk_fma_f16 v34, v34, v46, 0
	v_pk_fma_f16 v35, v35, v47, 0
	v_pk_add_f16 v44, v60, v103
	v_pk_add_f16 v45, v61, v102
	v_pk_add_f16 v46, v62, v101
	v_pk_add_f16 v47, v63, v100
	v_exp_f16_sdwa v60, v44 dst_sel:WORD_0 dst_unused:UNUSED_PAD src0_sel:WORD_0
	v_exp_f16_sdwa v61, v45 dst_sel:WORD_0 dst_unused:UNUSED_PAD src0_sel:WORD_0
	v_exp_f16_sdwa v62, v46 dst_sel:WORD_0 dst_unused:UNUSED_PAD src0_sel:WORD_0
	v_exp_f16_sdwa v63, v47 dst_sel:WORD_0 dst_unused:UNUSED_PAD src0_sel:WORD_0
	v_exp_f16_sdwa v60, v44 dst_sel:WORD_1 dst_unused:UNUSED_PRESERVE src0_sel:WORD_1
	v_exp_f16_sdwa v61, v45 dst_sel:WORD_1 dst_unused:UNUSED_PRESERVE src0_sel:WORD_1
	v_exp_f16_sdwa v62, v46 dst_sel:WORD_1 dst_unused:UNUSED_PRESERVE src0_sel:WORD_1
	v_exp_f16_sdwa v63, v47 dst_sel:WORD_1 dst_unused:UNUSED_PRESERVE src0_sel:WORD_1
	s_nop 0
	v_pk_add_f16 v31, v31, v63
	v_pk_add_f16 v30, v30, v62
	v_pk_add_f16 v29, v29, v61
	v_pk_add_f16 v28, v28, v60
	v_pk_fma_f16 v35, v39, v63, v35
	v_pk_fma_f16 v34, v38, v62, v34
	v_pk_fma_f16 v33, v37, v61, v33
	v_pk_fma_f16 v32, v36, v60, v32
	v_pk_add_f16 v36, v79, v103
	v_pk_add_f16 v37, v78, v102
	v_pk_add_f16 v38, v77, v101
	v_pk_add_f16 v39, v76, v100
	v_exp_f16_sdwa v44, v36 dst_sel:WORD_0 dst_unused:UNUSED_PAD src0_sel:WORD_0
	v_exp_f16_sdwa v45, v37 dst_sel:WORD_0 dst_unused:UNUSED_PAD src0_sel:WORD_0
	v_exp_f16_sdwa v46, v38 dst_sel:WORD_0 dst_unused:UNUSED_PAD src0_sel:WORD_0
	v_exp_f16_sdwa v47, v39 dst_sel:WORD_0 dst_unused:UNUSED_PAD src0_sel:WORD_0
	v_exp_f16_sdwa v44, v36 dst_sel:WORD_1 dst_unused:UNUSED_PRESERVE src0_sel:WORD_1
	v_exp_f16_sdwa v45, v37 dst_sel:WORD_1 dst_unused:UNUSED_PRESERVE src0_sel:WORD_1
	v_exp_f16_sdwa v46, v38 dst_sel:WORD_1 dst_unused:UNUSED_PRESERVE src0_sel:WORD_1
	v_exp_f16_sdwa v47, v39 dst_sel:WORD_1 dst_unused:UNUSED_PRESERVE src0_sel:WORD_1
	v_pk_add_f16 v36, v83, v103
	v_pk_add_f16 v28, v28, v44
	v_pk_add_f16 v29, v29, v45
	v_pk_add_f16 v30, v30, v46
	v_pk_add_f16 v31, v31, v47
	v_pk_fma_f16 v32, v40, v44, v32
	v_pk_fma_f16 v33, v41, v45, v33
	v_pk_fma_f16 v34, v42, v46, v34
	v_pk_fma_f16 v35, v43, v47, v35
	v_pk_add_f16 v37, v82, v102
	v_pk_add_f16 v38, v81, v101
	v_pk_add_f16 v39, v80, v100
	v_exp_f16_sdwa v40, v36 dst_sel:WORD_0 dst_unused:UNUSED_PAD src0_sel:WORD_0
	v_exp_f16_sdwa v41, v37 dst_sel:WORD_0 dst_unused:UNUSED_PAD src0_sel:WORD_0
	v_exp_f16_sdwa v42, v38 dst_sel:WORD_0 dst_unused:UNUSED_PAD src0_sel:WORD_0
	v_exp_f16_sdwa v43, v39 dst_sel:WORD_0 dst_unused:UNUSED_PAD src0_sel:WORD_0
	v_exp_f16_sdwa v40, v36 dst_sel:WORD_1 dst_unused:UNUSED_PRESERVE src0_sel:WORD_1
	v_exp_f16_sdwa v41, v37 dst_sel:WORD_1 dst_unused:UNUSED_PRESERVE src0_sel:WORD_1
	v_exp_f16_sdwa v42, v38 dst_sel:WORD_1 dst_unused:UNUSED_PRESERVE src0_sel:WORD_1
	v_exp_f16_sdwa v43, v39 dst_sel:WORD_1 dst_unused:UNUSED_PRESERVE src0_sel:WORD_1
	v_pk_add_f16 v36, v95, v103
	v_pk_add_f16 v31, v31, v43
	v_pk_add_f16 v30, v30, v42
	v_pk_add_f16 v29, v29, v41
	v_pk_add_f16 v28, v28, v40
	v_pk_fma_f16 v35, v55, v43, v35
	v_pk_fma_f16 v34, v54, v42, v34
	v_pk_fma_f16 v33, v53, v41, v33
	v_pk_fma_f16 v32, v52, v40, v32
	v_pk_add_f16 v37, v94, v102
	v_pk_add_f16 v38, v93, v101
	v_pk_add_f16 v39, v92, v100
	v_exp_f16_sdwa v40, v36 dst_sel:WORD_0 dst_unused:UNUSED_PAD src0_sel:WORD_0
	v_exp_f16_sdwa v41, v37 dst_sel:WORD_0 dst_unused:UNUSED_PAD src0_sel:WORD_0
	v_exp_f16_sdwa v42, v38 dst_sel:WORD_0 dst_unused:UNUSED_PAD src0_sel:WORD_0
	v_exp_f16_sdwa v43, v39 dst_sel:WORD_0 dst_unused:UNUSED_PAD src0_sel:WORD_0
	v_exp_f16_sdwa v40, v36 dst_sel:WORD_1 dst_unused:UNUSED_PRESERVE src0_sel:WORD_1
	v_exp_f16_sdwa v41, v37 dst_sel:WORD_1 dst_unused:UNUSED_PRESERVE src0_sel:WORD_1
	v_exp_f16_sdwa v42, v38 dst_sel:WORD_1 dst_unused:UNUSED_PRESERVE src0_sel:WORD_1
	v_exp_f16_sdwa v43, v39 dst_sel:WORD_1 dst_unused:UNUSED_PRESERVE src0_sel:WORD_1
	v_pk_add_f16 v36, v99, v103
	v_pk_add_f16 v28, v28, v40
	v_pk_add_f16 v29, v29, v41
	v_pk_add_f16 v30, v30, v42
	v_pk_add_f16 v31, v31, v43
	v_pk_fma_f16 v32, v64, v40, v32
	v_pk_fma_f16 v33, v65, v41, v33
	v_pk_fma_f16 v34, v66, v42, v34
	v_pk_fma_f16 v35, v67, v43, v35
	v_pk_add_f16 v37, v98, v102
	v_pk_add_f16 v38, v97, v101
	v_pk_add_f16 v39, v96, v100
	v_exp_f16_sdwa v40, v36 dst_sel:WORD_0 dst_unused:UNUSED_PAD src0_sel:WORD_0
	v_exp_f16_sdwa v41, v37 dst_sel:WORD_0 dst_unused:UNUSED_PAD src0_sel:WORD_0
	v_exp_f16_sdwa v42, v38 dst_sel:WORD_0 dst_unused:UNUSED_PAD src0_sel:WORD_0
	v_exp_f16_sdwa v43, v39 dst_sel:WORD_0 dst_unused:UNUSED_PAD src0_sel:WORD_0
	v_exp_f16_sdwa v40, v36 dst_sel:WORD_1 dst_unused:UNUSED_PRESERVE src0_sel:WORD_1
	v_exp_f16_sdwa v41, v37 dst_sel:WORD_1 dst_unused:UNUSED_PRESERVE src0_sel:WORD_1
	v_exp_f16_sdwa v42, v38 dst_sel:WORD_1 dst_unused:UNUSED_PRESERVE src0_sel:WORD_1
	v_exp_f16_sdwa v43, v39 dst_sel:WORD_1 dst_unused:UNUSED_PRESERVE src0_sel:WORD_1
	v_pk_add_f16 v36, v56, v103
	v_pk_add_f16 v31, v31, v43
	v_pk_add_f16 v30, v30, v42
	v_pk_add_f16 v29, v29, v41
	v_pk_add_f16 v28, v28, v40
	v_pk_fma_f16 v35, v87, v43, v35
	v_pk_fma_f16 v34, v86, v42, v34
	v_pk_fma_f16 v33, v85, v41, v33
	v_pk_fma_f16 v32, v84, v40, v32
	v_pk_add_f16 v37, v57, v102
	v_pk_add_f16 v38, v58, v101
	v_pk_add_f16 v39, v59, v100
	v_exp_f16_sdwa v40, v36 dst_sel:WORD_0 dst_unused:UNUSED_PAD src0_sel:WORD_0
	v_exp_f16_sdwa v41, v37 dst_sel:WORD_0 dst_unused:UNUSED_PAD src0_sel:WORD_0
	v_exp_f16_sdwa v42, v38 dst_sel:WORD_0 dst_unused:UNUSED_PAD src0_sel:WORD_0
	v_exp_f16_sdwa v43, v39 dst_sel:WORD_0 dst_unused:UNUSED_PAD src0_sel:WORD_0
	v_exp_f16_sdwa v40, v36 dst_sel:WORD_1 dst_unused:UNUSED_PRESERVE src0_sel:WORD_1
	v_exp_f16_sdwa v41, v37 dst_sel:WORD_1 dst_unused:UNUSED_PRESERVE src0_sel:WORD_1
	v_exp_f16_sdwa v42, v38 dst_sel:WORD_1 dst_unused:UNUSED_PRESERVE src0_sel:WORD_1
	v_exp_f16_sdwa v43, v39 dst_sel:WORD_1 dst_unused:UNUSED_PRESERVE src0_sel:WORD_1
	v_pk_add_f16 v36, v68, v103
	v_pk_add_f16 v28, v28, v40
	v_pk_add_f16 v29, v29, v41
	v_pk_add_f16 v30, v30, v42
	v_pk_add_f16 v31, v31, v43
	v_pk_fma_f16 v32, v104, v40, v32
	v_pk_fma_f16 v33, v105, v41, v33
	v_pk_fma_f16 v34, v106, v42, v34
	v_pk_fma_f16 v35, v107, v43, v35
	v_pk_add_f16 v37, v69, v102
	v_pk_add_f16 v38, v70, v101
	v_pk_add_f16 v39, v71, v100
	v_exp_f16_sdwa v40, v36 dst_sel:WORD_0 dst_unused:UNUSED_PAD src0_sel:WORD_0
	v_exp_f16_sdwa v41, v37 dst_sel:WORD_0 dst_unused:UNUSED_PAD src0_sel:WORD_0
	v_exp_f16_sdwa v42, v38 dst_sel:WORD_0 dst_unused:UNUSED_PAD src0_sel:WORD_0
	v_exp_f16_sdwa v43, v39 dst_sel:WORD_0 dst_unused:UNUSED_PAD src0_sel:WORD_0
	v_exp_f16_sdwa v40, v36 dst_sel:WORD_1 dst_unused:UNUSED_PRESERVE src0_sel:WORD_1
	v_exp_f16_sdwa v41, v37 dst_sel:WORD_1 dst_unused:UNUSED_PRESERVE src0_sel:WORD_1
	v_exp_f16_sdwa v42, v38 dst_sel:WORD_1 dst_unused:UNUSED_PRESERVE src0_sel:WORD_1
	v_exp_f16_sdwa v43, v39 dst_sel:WORD_1 dst_unused:UNUSED_PRESERVE src0_sel:WORD_1
	s_nop 0
	v_pk_add_f16 v31, v31, v43
	v_pk_add_f16 v30, v30, v42
	v_pk_add_f16 v29, v29, v41
	v_pk_add_f16 v28, v28, v40
	v_pk_fma_f16 v35, v123, v43, v35
	v_pk_fma_f16 v34, v122, v42, v34
	v_pk_fma_f16 v33, v121, v41, v33
	v_pk_fma_f16 v32, v120, v40, v32
	v_pk_add_f16 v40, v72, v103
	v_pk_add_f16 v41, v73, v102
	v_pk_add_f16 v42, v74, v101
	v_pk_add_f16 v43, v75, v100
	v_exp_f16_sdwa v36, v40 dst_sel:WORD_0 dst_unused:UNUSED_PAD src0_sel:WORD_0
	v_exp_f16_sdwa v37, v41 dst_sel:WORD_0 dst_unused:UNUSED_PAD src0_sel:WORD_0
	v_exp_f16_sdwa v38, v42 dst_sel:WORD_0 dst_unused:UNUSED_PAD src0_sel:WORD_0
	v_exp_f16_sdwa v39, v43 dst_sel:WORD_0 dst_unused:UNUSED_PAD src0_sel:WORD_0
	v_exp_f16_sdwa v36, v40 dst_sel:WORD_1 dst_unused:UNUSED_PRESERVE src0_sel:WORD_1
	v_exp_f16_sdwa v37, v41 dst_sel:WORD_1 dst_unused:UNUSED_PRESERVE src0_sel:WORD_1
	v_exp_f16_sdwa v38, v42 dst_sel:WORD_1 dst_unused:UNUSED_PRESERVE src0_sel:WORD_1
	v_exp_f16_sdwa v39, v43 dst_sel:WORD_1 dst_unused:UNUSED_PRESERVE src0_sel:WORD_1
	s_nop 0
	s_load_dwordx2 s[12:13], s[0:1], 0x60
	s_branch .LBB6_76
